# MoE-down unit body hand-rescheduled like MoE-up (3 A buffers, 4 B sets, counted vmcnt, half-tile stagger, own epilogue via aliased LDS staging); column blocks remapped cq+8*cbi
# speedup vs baseline: 1.0338x; 1.0107x over previous
; #define LAS __attribute__((address_space(3)))
; #define PG8_LAS __attribute__((address_space(3)))
; __device__ __forceinline__ void moe_down_stream(PG8_LAS unsigned char* lds, int e, int cb0, int slot0, int nv, const bf16_t* HIDp, const float* Wd, bf16_t* Y, const float* slot_w, const int* slot_dst) {
;     ...
;     const int tid = threadIdx.x, wid = __builtin_amdgcn_readfirstlane(tid >> 6), lane = tid & 63, wr = wid >> 1, wc = wid & 1, fr = lane & 15, fq = lane >> 4;
;     unsigned aoff[5];
; #pragma unroll
;     for (int i = 0; i < 5; ++i) { const int R = 8 * (wid + 8 * i) + (lane >> 3), C = 8 * ((lane & 7) ^ ((R >> 1) & 7)); const int w4 = R / DRW; int r = 4 * (R - DRW * w4) + w4; r = r < nv ? r : r % nv;
;         aoff[i] = ((unsigned)(slot0 + r) * (unsigned)K + (unsigned)C) * 2u; }
;     const int c0_ = 2 * lane, R0 = 64 * (c0_ >> 6) + 16 * (2 * ((c0_ >> 5) & 1) + ((c0_ >> 2) & 1)) + 4 * ((c0_ >> 3) & 3) + (c0_ & 3);
;     const char* Bb = (const char*)(Wd + (size_t)e * K * 4096 + 128 * cb0 + 2 * lane) + (size_t)(8 * wid) * RB;
;     const unsigned bw0 = (unsigned)(R0 * 128 + ((wid ^ ((R0 >> 1) & 7)) * 16)), bw1 = bw0 + 128u;
;     const int nvw = (nv - wr + 3) >> 2, mcnt = nvw <= 0 ? 0 : (((nvw + 15) >> 4) > DNM ? DNM : ((nvw + 15) >> 4));
;     unsigned amask = 0u;
; #pragma unroll
;     for (int i = 0; i < 5; ++i) { const int grp = 4 * i + (wid >> 1), w4 = grp / DNM, mf = grp % DNM, nv4 = (nv - w4 + 3) >> 2, mc4 = nv4 <= 0 ? 0 : ((nv4 + 15) >> 4); if (mf < mc4) amask |= 1u << i; }
;     LAS int* ldst = (LAS int*)(lds + MD_TAB_OFF); LAS float* lw = (LAS float*)(ldst + DR);
;     PG8_LAS unsigned char* stg = lds + MD_STG_OFF + wid * 2048;
.LBB0_784:
	s_cmp_lt_i32 s92, 10
	s_cselect_b64 s[0:1], -1, 0
	s_and_b64 s[0:1], s[0:1], s[4:5]
	s_andn2_b64 vcc, exec, s[0:1]
	s_cbranch_vccnz .LBB0_885
	v_cmp_gt_u32_e32 vcc, 64, v0
	s_waitcnt vmcnt(0) lgkmcnt(0)
	s_barrier
	s_and_saveexec_b64 s[4:5], vcc
	s_cbranch_execz .LBB0_788
	v_mov_b32_e32 v85, 0
	v_lshl_add_u64 v[2:3], s[26:27], 0, v[84:85]
	v_add_co_u32_e32 v2, vcc, 0x1000, v2
	s_add_i32 s3, 0, 0x26c00
	s_nop 0
	v_addc_co_u32_e32 v3, vcc, 0, v3, vcc
	global_load_dword v1, v[2:3], off
	v_mbcnt_lo_u32_b32 v3, -1, 0
	v_mbcnt_hi_u32_b32 v3, -1, v3
	v_and_b32_e32 v4, 64, v3
	v_add_u32_e32 v5, -1, v3
	v_cmp_lt_i32_e32 vcc, v5, v4
	v_add_u32_e32 v6, -2, v3
	v_add_u32_e32 v7, -4, v3
	v_cndmask_b32_e32 v5, v5, v3, vcc
	v_lshlrev_b32_e32 v5, 2, v5
	v_cmp_lt_i32_e32 vcc, v6, v4
	v_add_u32_e32 v8, -8, v3
	v_add_u32_e32 v9, -16, v3
	v_cndmask_b32_e32 v6, v6, v3, vcc
	v_cmp_ne_u32_e32 vcc, 0, v131
	v_lshlrev_b32_e32 v6, 2, v6
	v_subrev_u32_e32 v10, 32, v3
	v_readlane_b32 s6, v254, 5
	v_add_u32_e32 v2, 0, v84
	v_readlane_b32 s7, v254, 6
	v_add_u32_e32 v2, 0x26d40, v2
	s_waitcnt vmcnt(0)
	ds_bpermute_b32 v5, v5, v1
	s_waitcnt lgkmcnt(0)
	v_cndmask_b32_e32 v5, 0, v5, vcc
	v_add_u32_e32 v5, v5, v1
	ds_bpermute_b32 v6, v6, v5
	v_cmp_lt_i32_e32 vcc, v7, v4
	s_nop 1
	v_cndmask_b32_e32 v7, v7, v3, vcc
	v_cmp_lt_u32_e32 vcc, 1, v131
	v_lshlrev_b32_e32 v7, 2, v7
	s_waitcnt lgkmcnt(0)
	v_cndmask_b32_e32 v6, 0, v6, vcc
	v_add_u32_e32 v5, v6, v5
	ds_bpermute_b32 v6, v7, v5
	v_cmp_lt_i32_e32 vcc, v8, v4
	s_nop 1
	v_cndmask_b32_e32 v7, v8, v3, vcc
	v_cmp_lt_u32_e32 vcc, 3, v131
	v_lshlrev_b32_e32 v7, 2, v7
	s_waitcnt lgkmcnt(0)
	v_cndmask_b32_e32 v6, 0, v6, vcc
	v_add_u32_e32 v5, v6, v5
	ds_bpermute_b32 v6, v7, v5
	v_cmp_lt_i32_e32 vcc, v9, v4
	s_nop 1
	v_cndmask_b32_e32 v7, v9, v3, vcc
	v_cmp_lt_u32_e32 vcc, 7, v131
	v_lshlrev_b32_e32 v7, 2, v7
	s_waitcnt lgkmcnt(0)
	v_cndmask_b32_e32 v6, 0, v6, vcc
	v_add_u32_e32 v5, v6, v5
	ds_bpermute_b32 v6, v7, v5
	v_cmp_lt_i32_e32 vcc, v10, v4
	s_nop 1
	v_cndmask_b32_e32 v3, v10, v3, vcc
	v_cmp_lt_u32_e32 vcc, 15, v131
	v_lshlrev_b32_e32 v3, 2, v3
	s_waitcnt lgkmcnt(0)
	v_cndmask_b32_e32 v4, 0, v6, vcc
	v_add_u32_e32 v4, v4, v5
	ds_bpermute_b32 v3, v3, v4
	v_cmp_lt_u32_e32 vcc, 31, v131
	v_add_u32_e32 v5, s3, v84
	s_waitcnt lgkmcnt(0)
	v_cndmask_b32_e32 v3, 0, v3, vcc
	v_add_u32_e32 v3, v3, v4
	ds_write_b32 v5, v3 offset:4
	ds_write_b32 v2, v1
	s_and_b64 exec, exec, s[6:7]
	v_mov_b32_e32 v1, s3
	ds_write_b32 v1, v85
.LBB0_788:
	s_or_b64 exec, exec, s[4:5]
	s_and_b32 s3, s2, 7
	s_ashr_i32 s33, s2, 3
	s_add_u32 s16, s26, 0x59e00000
	s_addc_u32 s17, s27, 0
	s_add_u32 s18, s26, 0x4a200000
	v_bfe_u32 v4, v0, 1, 1
	s_addc_u32 s19, s27, 0
	v_lshlrev_b32_e32 v2, 1, v131
	v_and_b32_e32 v1, 64, v169
	v_lshrrev_b32_e32 v3, 1, v0
	v_and_or_b32 v4, v168, 2, v4
	s_add_u32 s20, s26, 0x4a600000
	v_lshl_or_b32 v1, v4, 4, v1
	v_and_b32_e32 v4, 12, v0
	v_and_b32_e32 v5, 2, v2
	v_bitop3_b32 v3, v171, v3, 7 bitop3:0x78
	s_addc_u32 s21, s27, 0
	v_or3_b32 v4, v1, v4, v5
	s_add_i32 s6, 0, 0x26e40
	v_lshlrev_b32_e32 v3, 4, v3
	s_add_i32 s7, 0, 0x14000
	s_add_i32 s8, 0, 0x18000
	v_lshlrev_b32_e32 v157, 7, v170
	v_lshlrev_b32_e32 v1, 7, v4
	v_bfe_u32 v152, v4, 1, 3
	v_add_u32_e32 v153, s6, v84
	s_add_i32 s6, 0, 0x27340
	v_bfe_u32 v4, v0, 1, 3
	v_add_u32_e32 v155, 0, v3
	v_and_b32_e32 v5, 7, v0
	v_add3_u32 v159, s7, v3, v157
	v_add3_u32 v161, s8, v3, v157
	v_bitop3_b32 v3, v171, v0, 7 bitop3:0x78
	v_add_u32_e32 v154, s6, v84
	v_bitop3_b32 v4, v171, v4, 4 bitop3:0x36
	v_lshl_add_u32 v163, v170, 4, s6
	v_lshlrev_b32_e32 v164, 4, v3
	v_bitop3_b32 v3, v171, v5, 4 bitop3:0x36
	s_lshl_b32 s6, s3, 2
	v_mov_b32_e32 v83, 0
	s_movk_i32 s4, 0x140
	v_lshlrev_b32_e32 v4, 4, v4
	v_bitop3_b32 v6, v130, v0, 7 bitop3:0x78
	v_lshlrev_b32_e32 v82, 4, v5
	v_lshlrev_b32_e32 v165, 4, v3
	v_or_b32_e32 v3, 8, v130
	s_add_i32 s73, s6, 0
	v_cmp_gt_u32_e64 s[4:5], s4, v0
	s_mov_b32 s23, 0
	v_add_u32_e32 v156, 0, v4
	v_lshlrev_b32_e32 v158, 4, v6
	v_lshl_add_u64 v[84:85], s[96:97], 0, v[82:83]
	v_add3_u32 v160, s7, v4, v157
	v_add3_u32 v162, s8, v4, v157
	v_lshlrev_b32_e32 v166, 4, v130
	v_lshlrev_b32_e32 v167, 7, v130
	v_lshlrev_b32_e32 v168, 4, v3
	v_lshlrev_b32_e32 v169, 7, v3
	s_ashr_i32 s72, s90, 3
	s_add_i32 s73, s73, 0x26d40
	v_lshlrev_b32_e32 v86, 2, v2
	s_mov_b64 s[24:25], 0x4000
	s_mov_b64 s[26:27], 0x8000
	s_mov_b64 s[28:29], 0xc000
	s_mov_b64 s[30:31], 0x10000
	s_mov_b64 s[34:35], 0x14000
	s_mov_b64 s[36:37], 0x18000
	s_mov_b64 s[38:39], 0x1c000
	s_mov_b64 s[40:41], 0x26e400
	s_mov_b64 s[42:43], 0x20c000
	s_mov_b64 s[44:45], 0x210000
	s_mov_b64 s[46:47], 0x214000
	s_mov_b64 s[48:49], 0x218000
	s_mov_b64 s[50:51], 0x21c000
	s_mov_b64 s[52:53], 0x80
	s_waitcnt lgkmcnt(0)
	s_barrier
	s_branch .LBB0_791

; #define MOE_UNIT(idx_, x_, RMAX, CBN, e_, rb_, cb_, ok_) do { int b_ = 0; ok_ = false; for (int k_ = 0; k_ < 8; ++k_) { const int ee_ = (x_) + 8 * k_, n_ = ((ecnt[ee_] + (RMAX) - 1) / (RMAX)) * (CBN); \
;         if ((idx_) < b_ + n_) { e_ = ee_; rb_ = ((idx_) - b_) / (CBN); cb_ = ((idx_) - b_) % (CBN); ok_ = true; break; } b_ += n_; } } while (0)
; __device__ __forceinline__ void moe_down_stream(PG8_LAS unsigned char* lds, int e, int cb0, int slot0, int nv, const bf16_t* HIDp, const float* Wd, bf16_t* Y, const float* slot_w, const int* slot_dst) {
;     ...
;     for (int i = 0; i < 5; ++i) { const int R = 8 * (wid + 8 * i) + (lane >> 3), C = 8 * ((lane & 7) ^ ((R >> 1) & 7)); const int w4 = R / DRW; int r = 4 * (R - DRW * w4) + w4; r = r < nv ? r : r % nv;
;         aoff[i] = ((unsigned)(slot0 + r) * (unsigned)K + (unsigned)C) * 2u; }
; __global__ void __launch_bounds__(NTHREADS, 2) hymba_fwd(Args args) {
;     ...
;         for (int j = F.bid >> 3; ; j += F.G >> 3) { int e = 0, rb = 0, cq = 0; bool ok; MOE_UNIT(j, x, mu::DR, (32 / mu::DCB), e, rb, cq, ok); if (!ok) break;
;             const int n = ecnt[e], nrb = (n + mu::DR - 1) / mu::DR, base = n / nrb, rem = n % nrb, r0 = rb * base + (rb < rem ? rb : rem), nv = base + (rb < rem ? 1 : 0);
;             const long adj = (long)e * CAPS - eo[e];
.LBB0_796:
	s_andn2_b64 vcc, exec, s[8:9]
	s_mov_b64 s[8:9], -1
	s_cbranch_vccnz .LBB0_790
	s_lshl_b32 s8, s6, 2
	s_add_i32 s13, s8, 0
	s_add_i32 s8, s13, 0x26d40
	v_mov_b32_e32 v2, s8
	ds_read_b32 v2, v2
	v_readfirstlane_b32 s15, v0
	s_mul_hi_u32 s54, s15, 0xcccccccd
	s_waitcnt lgkmcnt(0)
	v_readfirstlane_b32 s8, v2
	s_add_i32 s9, s8, 0x13f
	s_mul_hi_i32 s9, s9, 0x66666667
	s_lshr_b32 s10, s9, 31
	s_ashr_i32 s9, s9, 7
	s_add_i32 s9, s9, s10
	s_abs_i32 s10, s9
	v_cvt_f32_u32_e32 v2, s10
	s_sub_i32 s22, 0, s10
	s_abs_i32 s11, s8
	s_xor_b32 s12, s8, s9
	v_rcp_iflag_f32_e32 v2, v2
	s_ashr_i32 s12, s12, 31
	v_mul_f32_e32 v2, 0x4f7ffffe, v2
	v_cvt_u32_f32_e32 v2, v2
	s_nop 0
	v_readfirstlane_b32 s55, v2
	s_mul_i32 s22, s22, s55
	s_mul_hi_u32 s22, s55, s22
	s_add_i32 s55, s55, s22
	s_mul_hi_u32 s22, s11, s55
	s_mul_i32 s55, s22, s10
	s_sub_i32 s11, s11, s55
	s_add_i32 s56, s22, 1
	s_sub_i32 s55, s11, s10
	s_cmp_ge_u32 s11, s10
	s_cselect_b32 s22, s56, s22
	s_cselect_b32 s11, s55, s11
	s_add_i32 s55, s22, 1
	s_cmp_ge_u32 s11, s10
	s_cselect_b32 s10, s55, s22
	s_xor_b32 s10, s10, s12
	s_sub_i32 s10, s10, s12
	s_mul_i32 s9, s10, s9
	s_sub_i32 s11, s8, s9
	s_cmp_lt_i32 s7, s11
	s_cselect_b64 s[8:9], -1, 0
	s_cmp_lg_u64 s[8:9], 0
	s_addc_u32 s12, s10, 0
	s_add_i32 s8, s13, 0x26c00
	s_lshr_b32 s66, s15, 6
	v_mov_b32_e32 v2, s8
	s_lshl_b32 s22, s66, 3
	ds_read_b32 v7, v2
	s_lshr_b32 s13, s54, 9
	v_or_b32_e32 v2, s22, v130
	s_mul_i32 s8, s13, 0xffffffb0
	v_add_u32_e32 v3, s8, v2
	v_lshl_add_u32 v4, v3, 2, s13
	v_cmp_le_i32_e32 vcc, s12, v4
	s_and_saveexec_b64 s[8:9], vcc
	s_cbranch_execz .LBB0_799
	s_abs_i32 s54, s12
	v_cvt_f32_u32_e32 v3, s54
	v_sub_u32_e32 v6, 0, v4
	s_sub_i32 s55, 0, s54
	v_ashrrev_i32_e32 v5, 31, v4
	v_rcp_iflag_f32_e32 v3, v3
	v_max_i32_e32 v4, v4, v6
	v_mul_f32_e32 v3, 0x4f7ffffe, v3
	v_cvt_u32_f32_e32 v3, v3
	v_mul_lo_u32 v6, s55, v3
	v_mul_hi_u32 v6, v3, v6
	v_add_u32_e32 v3, v3, v6
	v_mul_hi_u32 v3, v4, v3
	v_mul_lo_u32 v3, v3, s54
	v_sub_u32_e32 v3, v4, v3
	v_subrev_u32_e32 v4, s54, v3
	v_cmp_le_u32_e32 vcc, s54, v3
	s_nop 1
	v_cndmask_b32_e32 v3, v3, v4, vcc
	v_subrev_u32_e32 v4, s54, v3
	v_cmp_le_u32_e32 vcc, s54, v3
	s_nop 1
	v_cndmask_b32_e32 v3, v3, v4, vcc
	v_xor_b32_e32 v3, v3, v5
	v_sub_u32_e32 v4, v3, v5

; #define LAS __attribute__((address_space(3)))
; #define PG8_LAS __attribute__((address_space(3)))
; __device__ __forceinline__ void moe_down_stream(PG8_LAS unsigned char* lds, int e, int cb0, int slot0, int nv, const bf16_t* HIDp, const float* Wd, bf16_t* Y, const float* slot_w, const int* slot_dst) {
;     ...
;     unsigned aoff[5];
; #pragma unroll
;     for (int i = 0; i < 5; ++i) { const int R = 8 * (wid + 8 * i) + (lane >> 3), C = 8 * ((lane & 7) ^ ((R >> 1) & 7)); const int w4 = R / DRW; int r = 4 * (R - DRW * w4) + w4; r = r < nv ? r : r % nv;
;         aoff[i] = ((unsigned)(slot0 + r) * (unsigned)K + (unsigned)C) * 2u; }
;     const int c0_ = 2 * lane, R0 = 64 * (c0_ >> 6) + 16 * (2 * ((c0_ >> 5) & 1) + ((c0_ >> 2) & 1)) + 4 * ((c0_ >> 3) & 3) + (c0_ & 3);
;     const char* Bb = (const char*)(Wd + (size_t)e * K * 4096 + 128 * cb0 + 2 * lane) + (size_t)(8 * wid) * RB;
;     const unsigned bw0 = (unsigned)(R0 * 128 + ((wid ^ ((R0 >> 1) & 7)) * 16)), bw1 = bw0 + 128u;
;     const int nvw = (nv - wr + 3) >> 2, mcnt = nvw <= 0 ? 0 : (((nvw + 15) >> 4) > DNM ? DNM : ((nvw + 15) >> 4));
;     unsigned amask = 0u;
; #pragma unroll
;     for (int i = 0; i < 5; ++i) { const int grp = 4 * i + (wid >> 1), w4 = grp / DNM, mf = grp % DNM, nv4 = (nv - w4 + 3) >> 2, mc4 = nv4 <= 0 ? 0 : ((nv4 + 15) >> 4); if (mf < mc4) amask |= 1u << i; }
;     LAS int* ldst = (LAS int*)(lds + MD_TAB_OFF); LAS float* lw = (LAS float*)(ldst + DR);
;     PG8_LAS unsigned char* stg = lds + MD_STG_OFF + wid * 2048;
;     __syncthreads();
;     for (int r = tid; r < DR; r += 512) { const bool ok = r < nv; ldst[r] = ok ? slot_dst[slot0 + r] : -1; lw[r] = ok ? slot_w[slot0 + r] : 0.f; }
;     asm volatile("s_waitcnt vmcnt(0)" ::: "memory");
.LBB0_811:
	s_or_b64 exec, exec, s[8:9]
	s_lshr_b32 s67, s15, 7
	s_bfe_u32 s10, s15, 0x10006
	s_lshl_b32 s74, s66, 10
	v_readfirstlane_b32 s56, v13
	s_lshl_b32 s57, s66, 2
	v_add_u32_e32 v180, s57, v171
	v_xor_b32_e32 v180, v180, v131
	v_and_b32_e32 v180, 7, v180
	v_lshlrev_b32_e32 v180, 4, v180
	v_add_u32_e32 v88, v4, v13
	v_lshl_or_b32 v88, v88, 10, v180
	v_add_u32_e32 v90, v6, v13
	v_lshl_or_b32 v90, v90, 10, v180
	v_add_u32_e32 v92, v9, v13
	v_lshl_or_b32 v92, v92, 10, v180
	v_add_u32_e32 v94, v10, v13
	v_lshl_or_b32 v94, v94, 10, v180
	v_add_u32_e32 v96, v12, v13
	v_lshl_or_b32 v96, v96, 10, v180
	s_lshl_b32 s56, s56, 10
	s_lshr_b32 s57, s66, 1
	s_add_i32 s58, s57, 0
	s_mul_i32 s59, s58, 13
	s_lshr_b32 s59, s59, 6
	s_mul_i32 s60, s59, 5
	s_sub_i32 s60, s58, s60
	s_sub_i32 s61, s12, s59
	s_add_i32 s61, s61, 3
	s_ashr_i32 s61, s61, 2
	s_add_i32 s62, s61, 15
	s_ashr_i32 s62, s62, 4
	s_cmp_gt_i32 s61, 0
	s_cselect_b32 s62, s62, 0
	s_cmp_lt_i32 s60, s62
	s_cbranch_scc1 .Lmd_used_0
	v_mov_b32_e32 v88, s56
.Lmd_used_0:
	s_add_i32 s58, s57, 4
	s_mul_i32 s59, s58, 13
	s_lshr_b32 s59, s59, 6
	s_mul_i32 s60, s59, 5
	s_sub_i32 s60, s58, s60
	s_sub_i32 s61, s12, s59
	s_add_i32 s61, s61, 3
	s_ashr_i32 s61, s61, 2
	s_add_i32 s62, s61, 15
	s_ashr_i32 s62, s62, 4
	s_cmp_gt_i32 s61, 0
	s_cselect_b32 s62, s62, 0
	s_cmp_lt_i32 s60, s62
	s_cbranch_scc1 .Lmd_used_1
	v_mov_b32_e32 v90, s56
.Lmd_used_1:
	s_add_i32 s58, s57, 8
	s_mul_i32 s59, s58, 13
	s_lshr_b32 s59, s59, 6
	s_mul_i32 s60, s59, 5
	s_sub_i32 s60, s58, s60
	s_sub_i32 s61, s12, s59
	s_add_i32 s61, s61, 3
	s_ashr_i32 s61, s61, 2
	s_add_i32 s62, s61, 15
	s_ashr_i32 s62, s62, 4
	s_cmp_gt_i32 s61, 0
	s_cselect_b32 s62, s62, 0
	s_cmp_lt_i32 s60, s62
	s_cbranch_scc1 .Lmd_used_2
	v_mov_b32_e32 v92, s56
.Lmd_used_2:
	s_add_i32 s58, s57, 12
	s_mul_i32 s59, s58, 13
	s_lshr_b32 s59, s59, 6
	s_mul_i32 s60, s59, 5
	s_sub_i32 s60, s58, s60
	s_sub_i32 s61, s12, s59
	s_add_i32 s61, s61, 3
	s_ashr_i32 s61, s61, 2
	s_add_i32 s62, s61, 15
	s_ashr_i32 s62, s62, 4
	s_cmp_gt_i32 s61, 0
	s_cselect_b32 s62, s62, 0
	s_cmp_lt_i32 s60, s62
	s_cbranch_scc1 .Lmd_used_3
	v_mov_b32_e32 v94, s56
.Lmd_used_3:
	s_add_i32 s58, s57, 16
	s_mul_i32 s59, s58, 13
	s_lshr_b32 s59, s59, 6
	s_mul_i32 s60, s59, 5
	s_sub_i32 s60, s58, s60
	s_sub_i32 s61, s12, s59
	s_add_i32 s61, s61, 3
	s_ashr_i32 s61, s61, 2
	s_add_i32 s62, s61, 15
	s_ashr_i32 s62, s62, 4
	s_cmp_gt_i32 s61, 0
	s_cselect_b32 s62, s62, 0
	s_cmp_lt_i32 s60, s62
	s_cbranch_scc1 .Lmd_used_4
	v_mov_b32_e32 v96, s56
.Lmd_used_4:
	v_bfe_u32 v180, v131, 1, 3
	v_xor_b32_e32 v180, v171, v180
	v_lshlrev_b32_e32 v180, 4, v180
	v_lshl_add_u32 v180, v170, 7, v180
	s_mul_i32 s57, s67, 0x2800
	v_add_u32_e32 v135, s57, v180
	v_xor_b32_e32 v137, 64, v135
	s_lshl_b32 s57, s10, 13
	s_add_i32 s57, s57, 0x1e000
	v_add_u32_e32 v139, s57, v180
	v_xor_b32_e32 v141, 64, v139
	v_lshrrev_b32_e32 v164, 4, v131
	v_lshlrev_b32_e32 v95, 5, v164
	v_bfe_u32 v164, v131, 1, 1
	v_lshl_or_b32 v95, v164, 4, v95
	v_bfe_u32 v164, v131, 2, 2
	v_lshl_or_b32 v95, v164, 2, v95
	v_and_b32_e32 v165, 1, v131
	v_lshl_or_b32 v95, v165, 1, v95
	v_lshl_or_b32 v164, v164, 1, v165
	v_xor_b32_e32 v164, s66, v164
	v_lshlrev_b32_e32 v95, 7, v95
	v_lshl_or_b32 v95, v164, 4, v95
	v_add_u32_e32 v95, 0x1e000, v95
	s_lshl_b32 s57, s67, 2
	v_lshl_add_u32 v82, v170, 4, s57
	v_add_u32_e32 v82, 0x27340, v82
	v_lshl_add_u32 v83, v130, 4, s57
	v_add_u32_e32 v83, 0x26e40, v83
	v_and_b32_e32 v164, 7, v170
	v_xor_b32_e32 v165, v171, v164
	v_lshlrev_b32_e32 v165, 4, v165
	v_lshl_or_b32 v84, v164, 7, v165
	v_lshrrev_b32_e32 v164, 3, v170
	v_lshl_or_b32 v84, v164, 13, v84
	v_and_b32_e32 v164, 7, v131
	v_xor_b32_e32 v165, v130, v164
	v_and_b32_e32 v165, 7, v165
	v_lshlrev_b32_e32 v165, 4, v165
	v_lshl_or_b32 v85, v130, 7, v165
	s_lshl_b32 s57, s14, 8
	s_lshl_b32 s58, s10, 7
	s_add_i32 s57, s57, s58
	s_add_u32 s58, s96, s57
	s_addc_u32 s59, s97, 0
	v_lshlrev_b32_e32 v164, 4, v164
	v_mov_b32_e32 v165, 0
	v_lshl_add_u64 v[86:87], v[164:165], 0, s[58:59]
	v_readlane_b32 s58, v254, 25
	v_readlane_b32 s59, v254, 26
	s_lshl_b64 s[60:61], s[6:7], 23
	s_add_u32 s58, s58, s60
	s_addc_u32 s59, s59, s61
	s_lshl_b32 s60, s14, 9
	s_add_u32 s58, s58, s60
	s_addc_u32 s59, s59, 0
	s_lshl_b32 s60, s66, 17
	s_add_u32 s58, s58, s60
	s_addc_u32 s59, s59, 0
	v_lshlrev_b32_e32 v164, 3, v131
	v_mov_b32_e32 v165, 0
	v_lshl_add_u64 v[132:133], v[164:165], 0, s[58:59]
	s_mov_b64 s[24:25], 0x4000
	s_mov_b64 s[26:27], 0x8000
	s_mov_b64 s[28:29], 0xc000
	s_mov_b64 s[36:37], 0x10000
	s_mov_b64 s[38:39], 0x14000
	s_mov_b64 s[40:41], 0x18000
	s_mov_b64 s[42:43], 0x1c000
	s_mov_b32 s34, 0xff901000
	s_mov_b32 s35, 0x100000
	s_mov_b32 s53, 0xfffffc80
	s_mov_b32 s32, 0x80
	v_readlane_b32 s58, v254, 31
	v_readlane_b32 s59, v254, 32
	s_add_u32 s58, s58, 0x4b000000
	s_addc_u32 s59, s59, 0
	v_lshlrev_b32_e32 v164, 4, v131
	v_mov_b32_e32 v165, 0
	v_lshl_add_u64 v[168:169], v[164:165], 0, s[58:59]
	s_mov_b64 s[30:31], s[16:17]
	s_mov_b32 s46, 0
	s_mov_b32 s47, 0xa000
	s_mov_b32 s48, 0x14000
	s_mov_b32 s51, 4
	s_mov_b32 s52, 1
	s_add_i32 m0, s74, 0x0
	s_nop 0
	global_load_lds_dwordx4 v88, s[30:31]
	s_add_i32 m0, s74, 0x2000
	s_nop 0
	global_load_lds_dwordx4 v90, s[30:31]
	s_add_i32 m0, s74, 0x4000
	s_nop 0
	global_load_lds_dwordx4 v92, s[30:31]
	s_add_i32 m0, s74, 0x6000
	s_nop 0
	global_load_lds_dwordx4 v94, s[30:31]
	s_add_i32 m0, s74, 0x8000
	s_nop 0
	global_load_lds_dwordx4 v96, s[30:31]
	s_add_u32 s30, s30, 0x80
	s_addc_u32 s31, s31, 0
	s_add_i32 m0, s74, 0xa000
	s_nop 0
	global_load_lds_dwordx4 v88, s[30:31]
	s_add_i32 m0, s74, 0xc000
	s_nop 0
	global_load_lds_dwordx4 v90, s[30:31]
; #define MD_GLDS_A(buf, tau) do { _Pragma("unroll") for (int i = 0; i < 5; ++i) if (amask & (1u << i)) \
;         __builtin_amdgcn_global_load_lds((const unsigned*)((const char*)HIDp + aoff[i] + (size_t)((tau) & 7) * 128), (PG8_LAS unsigned*)(MD_SA(buf) + wid * 1024 + i * 8192), 16, 0, 0); } while (0)
; #define MD_B_ISSUE(sb, tau) do { const char* kb_ = Bb + (size_t)((tau) >> 3) * 512 + (size_t)((tau) & 7) * (64 * (size_t)RB); _Pragma("unroll") for (int j = 0; j < 8; ++j) { const char* p_ = kb_ + (size_t)j * RB; \
;         asm volatile("global_load_dwordx2 %0, %1, off" : "=&v"(sb[j]) : "v"(p_) : "memory"); } } while (0)
; #define MD_B_WAIT(sb, N) asm volatile("s_waitcnt vmcnt(%8)" : "+v"(sb[0]), "+v"(sb[1]), "+v"(sb[2]), "+v"(sb[3]), "+v"(sb[4]), "+v"(sb[5]), "+v"(sb[6]), "+v"(sb[7]) : "n"(N) : "memory")
; __device__ __forceinline__ void moe_down_stream(PG8_LAS unsigned char* lds, int e, int cb0, int slot0, int nv, const bf16_t* HIDp, const float* Wd, bf16_t* Y, const float* slot_w, const int* slot_dst) {
;     ...
;     f32x4 acc[DNM][4];
; #pragma unroll
;     for (int m = 0; m < DNM; ++m)
; #pragma unroll
;         for (int n = 0; n < 4; ++n) acc[m][n] = (f32x4){0.f, 0.f, 0.f, 0.f};
;     f32x2 s0[8], s1[8];
;     MD_GLDS_A(0, 0); MD_B_ISSUE(s0, 0); MD_B_ISSUE(s1, 1);
;     MD_B_WAIT(s0, 8); MD_B_WRITE(s0, 0); __builtin_amdgcn_sched_barrier(0); MD_B_ISSUE(s0, 2);
;     asm volatile("s_waitcnt vmcnt(16)" ::: "memory");
;     asm volatile("s_waitcnt lgkmcnt(0)" ::: "memory"); __builtin_amdgcn_s_barrier(); asm volatile("" ::: "memory");
	s_add_i32 m0, s74, 0xe000
	s_nop 0
	global_load_lds_dwordx4 v92, s[30:31]
	s_add_i32 m0, s74, 0x10000
	s_nop 0
	global_load_lds_dwordx4 v94, s[30:31]
	s_add_i32 m0, s74, 0x12000
	s_nop 0
	global_load_lds_dwordx4 v96, s[30:31]
	s_mov_b32 s44, 0x100000
	s_mov_b32 s45, 0
	global_load_dwordx2 v[98:99], v[132:133], off
	v_lshl_add_u64 v[180:181], v[132:133], 0, s[24:25]
	global_load_dwordx2 v[100:101], v[180:181], off
	v_lshl_add_u64 v[180:181], v[132:133], 0, s[26:27]
	global_load_dwordx2 v[102:103], v[180:181], off
	v_lshl_add_u64 v[180:181], v[132:133], 0, s[28:29]
	global_load_dwordx2 v[104:105], v[180:181], off
	v_lshl_add_u64 v[180:181], v[132:133], 0, s[36:37]
	global_load_dwordx2 v[106:107], v[180:181], off
	v_lshl_add_u64 v[180:181], v[132:133], 0, s[38:39]
	global_load_dwordx2 v[108:109], v[180:181], off
	v_lshl_add_u64 v[180:181], v[132:133], 0, s[40:41]
	global_load_dwordx2 v[110:111], v[180:181], off
	v_lshl_add_u64 v[180:181], v[132:133], 0, s[42:43]
	global_load_dwordx2 v[112:113], v[180:181], off
	v_lshl_add_u64 v[132:133], v[132:133], 0, s[44:45]
	global_load_dwordx2 v[114:115], v[132:133], off
	v_lshl_add_u64 v[180:181], v[132:133], 0, s[24:25]
	global_load_dwordx2 v[116:117], v[180:181], off
	v_lshl_add_u64 v[180:181], v[132:133], 0, s[26:27]
	global_load_dwordx2 v[118:119], v[180:181], off
	v_lshl_add_u64 v[180:181], v[132:133], 0, s[28:29]
	global_load_dwordx2 v[120:121], v[180:181], off
	v_lshl_add_u64 v[180:181], v[132:133], 0, s[36:37]
	global_load_dwordx2 v[122:123], v[180:181], off
	v_lshl_add_u64 v[180:181], v[132:133], 0, s[38:39]
	global_load_dwordx2 v[124:125], v[180:181], off
	v_lshl_add_u64 v[180:181], v[132:133], 0, s[40:41]
	global_load_dwordx2 v[126:127], v[180:181], off
	v_lshl_add_u64 v[180:181], v[132:133], 0, s[42:43]
	global_load_dwordx2 v[128:129], v[180:181], off
	v_lshl_add_u64 v[132:133], v[132:133], 0, s[44:45]
	global_load_dwordx2 v[186:187], v[132:133], off
	v_lshl_add_u64 v[180:181], v[132:133], 0, s[24:25]
	global_load_dwordx2 v[188:189], v[180:181], off
	v_lshl_add_u64 v[180:181], v[132:133], 0, s[26:27]
	global_load_dwordx2 v[190:191], v[180:181], off
	v_lshl_add_u64 v[180:181], v[132:133], 0, s[28:29]
	global_load_dwordx2 v[192:193], v[180:181], off
	v_lshl_add_u64 v[180:181], v[132:133], 0, s[36:37]
	global_load_dwordx2 v[194:195], v[180:181], off
	v_lshl_add_u64 v[180:181], v[132:133], 0, s[38:39]
	global_load_dwordx2 v[196:197], v[180:181], off
	v_lshl_add_u64 v[180:181], v[132:133], 0, s[40:41]
	global_load_dwordx2 v[198:199], v[180:181], off
	v_lshl_add_u64 v[180:181], v[132:133], 0, s[42:43]
	global_load_dwordx2 v[200:201], v[180:181], off
	v_lshl_add_u64 v[132:133], v[132:133], 0, s[44:45]
	global_load_dwordx2 v[202:203], v[132:133], off
	v_lshl_add_u64 v[180:181], v[132:133], 0, s[24:25]
	global_load_dwordx2 v[204:205], v[180:181], off
	v_lshl_add_u64 v[180:181], v[132:133], 0, s[26:27]
	global_load_dwordx2 v[206:207], v[180:181], off
	v_lshl_add_u64 v[180:181], v[132:133], 0, s[28:29]
	global_load_dwordx2 v[208:209], v[180:181], off
	v_lshl_add_u64 v[180:181], v[132:133], 0, s[36:37]
	global_load_dwordx2 v[210:211], v[180:181], off
	v_lshl_add_u64 v[180:181], v[132:133], 0, s[38:39]
	global_load_dwordx2 v[212:213], v[180:181], off
	v_lshl_add_u64 v[180:181], v[132:133], 0, s[40:41]
	global_load_dwordx2 v[214:215], v[180:181], off
	v_lshl_add_u64 v[180:181], v[132:133], 0, s[42:43]
	global_load_dwordx2 v[216:217], v[180:181], off
	v_mov_b32_e32 v78, 0
	v_mov_b32_e32 v79, 0
	v_mov_b32_e32 v80, 0
	v_mov_b32_e32 v81, 0
	v_mov_b32_e32 v74, 0
	v_mov_b32_e32 v75, 0
	v_mov_b32_e32 v76, 0
	v_mov_b32_e32 v77, 0
	v_mov_b32_e32 v70, 0
	v_mov_b32_e32 v71, 0
	v_mov_b32_e32 v72, 0
	v_mov_b32_e32 v73, 0
	v_mov_b32_e32 v66, 0
	v_mov_b32_e32 v67, 0
	v_mov_b32_e32 v68, 0
	v_mov_b32_e32 v69, 0
	v_mov_b32_e32 v62, 0
	v_mov_b32_e32 v63, 0
	v_mov_b32_e32 v64, 0
	v_mov_b32_e32 v65, 0
	v_mov_b32_e32 v58, 0
	v_mov_b32_e32 v59, 0
	v_mov_b32_e32 v60, 0
	v_mov_b32_e32 v61, 0
	v_mov_b32_e32 v54, 0
	v_mov_b32_e32 v55, 0
	v_mov_b32_e32 v56, 0
	v_mov_b32_e32 v57, 0
	v_mov_b32_e32 v50, 0
	v_mov_b32_e32 v51, 0
	v_mov_b32_e32 v52, 0
	v_mov_b32_e32 v53, 0
	v_mov_b32_e32 v46, 0
	v_mov_b32_e32 v47, 0
	v_mov_b32_e32 v48, 0
	v_mov_b32_e32 v49, 0
	v_mov_b32_e32 v42, 0
	v_mov_b32_e32 v43, 0
	v_mov_b32_e32 v44, 0
	v_mov_b32_e32 v45, 0
	v_mov_b32_e32 v38, 0
	v_mov_b32_e32 v39, 0
	v_mov_b32_e32 v40, 0
	v_mov_b32_e32 v41, 0
	v_mov_b32_e32 v34, 0
	v_mov_b32_e32 v35, 0
	v_mov_b32_e32 v36, 0
	v_mov_b32_e32 v37, 0
	v_mov_b32_e32 v18, 0
	v_mov_b32_e32 v19, 0
	v_mov_b32_e32 v20, 0
	v_mov_b32_e32 v21, 0
	v_mov_b32_e32 v22, 0
	v_mov_b32_e32 v23, 0
	v_mov_b32_e32 v24, 0
	v_mov_b32_e32 v25, 0
	v_mov_b32_e32 v26, 0
	v_mov_b32_e32 v27, 0
	v_mov_b32_e32 v28, 0
	v_mov_b32_e32 v29, 0
	v_mov_b32_e32 v30, 0
	v_mov_b32_e32 v31, 0
	v_mov_b32_e32 v32, 0
	v_mov_b32_e32 v33, 0
	v_mov_b32_e32 v2, 0
	v_mov_b32_e32 v3, 0
	v_mov_b32_e32 v4, 0
	v_mov_b32_e32 v5, 0
	v_mov_b32_e32 v6, 0
	v_mov_b32_e32 v7, 0
	v_mov_b32_e32 v8, 0
	v_mov_b32_e32 v9, 0
	v_mov_b32_e32 v10, 0
	v_mov_b32_e32 v11, 0
	v_mov_b32_e32 v12, 0
	v_mov_b32_e32 v13, 0
	v_mov_b32_e32 v14, 0
	v_mov_b32_e32 v15, 0
	v_mov_b32_e32 v16, 0
	v_mov_b32_e32 v17, 0
	s_waitcnt vmcnt(24)
	v_cvt_pk_bf16_f32 v172, v98, v100
	v_cvt_pk_bf16_f32 v173, v102, v104
	v_cvt_pk_bf16_f32 v174, v106, v108
	v_cvt_pk_bf16_f32 v175, v110, v112
	v_cvt_pk_bf16_f32 v176, v99, v101
	v_cvt_pk_bf16_f32 v177, v103, v105
	v_cvt_pk_bf16_f32 v178, v107, v109
	v_cvt_pk_bf16_f32 v179, v111, v113
	ds_write_b128 v95, v[172:175] offset:0
	ds_write_b128 v95, v[176:179] offset:128
	v_lshl_add_u64 v[132:133], v[132:133], 0, s[44:45]
	global_load_dwordx2 v[98:99], v[132:133], off
	v_lshl_add_u64 v[180:181], v[132:133], 0, s[24:25]
	global_load_dwordx2 v[100:101], v[180:181], off
	v_lshl_add_u64 v[180:181], v[132:133], 0, s[26:27]
	global_load_dwordx2 v[102:103], v[180:181], off
	v_lshl_add_u64 v[180:181], v[132:133], 0, s[28:29]
	global_load_dwordx2 v[104:105], v[180:181], off
	v_lshl_add_u64 v[180:181], v[132:133], 0, s[36:37]
	global_load_dwordx2 v[106:107], v[180:181], off
	v_lshl_add_u64 v[180:181], v[132:133], 0, s[38:39]
	global_load_dwordx2 v[108:109], v[180:181], off
	v_lshl_add_u64 v[180:181], v[132:133], 0, s[40:41]
	global_load_dwordx2 v[110:111], v[180:181], off
	v_lshl_add_u64 v[180:181], v[132:133], 0, s[42:43]
	global_load_dwordx2 v[112:113], v[180:181], off
	s_waitcnt lgkmcnt(0)
	s_barrier
; #define MD_GLDS_A(buf, tau) do { _Pragma("unroll") for (int i = 0; i < 5; ++i) if (amask & (1u << i)) \
;         __builtin_amdgcn_global_load_lds((const unsigned*)((const char*)HIDp + aoff[i] + (size_t)((tau) & 7) * 128), (PG8_LAS unsigned*)(MD_SA(buf) + wid * 1024 + i * 8192), 16, 0, 0); } while (0)
; #define MD_B_ISSUE(sb, tau) do { const char* kb_ = Bb + (size_t)((tau) >> 3) * 512 + (size_t)((tau) & 7) * (64 * (size_t)RB); _Pragma("unroll") for (int j = 0; j < 8; ++j) { const char* p_ = kb_ + (size_t)j * RB; \
;         asm volatile("global_load_dwordx2 %0, %1, off" : "=&v"(sb[j]) : "v"(p_) : "memory"); } } while (0)
; #define MD_B_WAIT(sb, N) asm volatile("s_waitcnt vmcnt(%8)" : "+v"(sb[0]), "+v"(sb[1]), "+v"(sb[2]), "+v"(sb[3]), "+v"(sb[4]), "+v"(sb[5]), "+v"(sb[6]), "+v"(sb[7]) : "n"(N) : "memory")
; __device__ __forceinline__ void moe_down_stream(PG8_LAS unsigned char* lds, int e, int cb0, int slot0, int nv, const bf16_t* HIDp, const float* Wd, bf16_t* Y, const float* slot_w, const int* slot_dst) {
;     ...
;     f32x4 acc[DNM][4];
; #pragma unroll
;     for (int m = 0; m < DNM; ++m)
; #pragma unroll
;         for (int n = 0; n < 4; ++n) acc[m][n] = (f32x4){0.f, 0.f, 0.f, 0.f};
;     f32x2 s0[8], s1[8];
;     MD_GLDS_A(0, 0); MD_B_ISSUE(s0, 0); MD_B_ISSUE(s1, 1);
;     MD_B_WAIT(s0, 8); MD_B_WRITE(s0, 0); __builtin_amdgcn_sched_barrier(0); MD_B_ISSUE(s0, 2);
;     asm volatile("s_waitcnt vmcnt(16)" ::: "memory");
;     asm volatile("s_waitcnt lgkmcnt(0)" ::: "memory"); __builtin_amdgcn_s_barrier(); asm volatile("" ::: "memory");
; #pragma unroll 1
;     for (int t = 0; t < NT; t += 2) {
;         if (t + 2 < NT) MD_B_WAIT(s1, 8); else MD_B_WAIT(s1, 0);
;         MD_B_WRITE(s1, 1); __builtin_amdgcn_sched_barrier(0); MD_GLDS_A(1, t + 1); __builtin_amdgcn_sched_barrier(0);
;         if (t + 3 < NT) MD_B_ISSUE(s1, t + 3);
;         MD_COMPUTE(0);
;         MD_END(t + 3 >= NT);
;         if (t + 2 < NT) { MD_B_WAIT(s0, 8); MD_B_WRITE(s0, 0); __builtin_amdgcn_sched_barrier(0); MD_GLDS_A(0, t + 2); __builtin_amdgcn_sched_barrier(0); }
;         if (t + 4 < NT) MD_B_ISSUE(s0, t + 4);
;         MD_COMPUTE(1);
;         MD_END(t + 4 >= NT);
	s_cmp_gt_u32 s66, 3
	s_cbranch_scc1 .Lmd_grpY
	s_waitcnt vmcnt(24)
	v_cvt_pk_bf16_f32 v172, v114, v116
	v_cvt_pk_bf16_f32 v173, v118, v120
	v_cvt_pk_bf16_f32 v174, v122, v124
	v_cvt_pk_bf16_f32 v175, v126, v128
	v_cvt_pk_bf16_f32 v176, v115, v117
	v_cvt_pk_bf16_f32 v177, v119, v121
	v_cvt_pk_bf16_f32 v178, v123, v125
	v_cvt_pk_bf16_f32 v179, v127, v129
	ds_write_b128 v95, v[172:175] offset:19456
	ds_write_b128 v95, v[176:179] offset:19584
	v_add_u32_e32 v91, s46, v135
	v_add_u32_e32 v93, s46, v137
	ds_read_b128 v[238:241], v139 offset:0
	ds_read_b128 v[242:245], v139 offset:2048
	ds_read_b128 v[246:249], v139 offset:4096
	ds_read_b128 v[250:253], v139 offset:6144
	ds_read_b128 v[218:221], v91 offset:0
	ds_read_b128 v[222:225], v91 offset:2048
	ds_read_b128 v[226:229], v91 offset:4096
	ds_read_b128 v[230:233], v91 offset:6144
	ds_read_b128 v[234:237], v91 offset:8192
	s_add_i32 s49, s48, s74
	s_add_i32 s52, s52, 1
	s_and_b32 s54, s52, 7
	s_cmp_eq_u32 s54, 0
	s_cselect_b32 s54, s53, s32
	s_cselect_b32 s55, -1, 0
	s_add_u32 s30, s30, s54
	s_addc_u32 s31, s31, s55
	s_waitcnt lgkmcnt(0)
	v_mfma_f32_16x16x32_bf16 v[78:81], v[238:241], v[218:221], v[78:81]
	v_mfma_f32_16x16x32_bf16 v[74:77], v[242:245], v[218:221], v[74:77]
	v_mfma_f32_16x16x32_bf16 v[70:73], v[246:249], v[218:221], v[70:73]
	v_mfma_f32_16x16x32_bf16 v[66:69], v[250:253], v[218:221], v[66:69]
	ds_read_b128 v[218:221], v93 offset:0
	ds_read_b128 v[142:145], v141 offset:0
	s_mov_b32 m0, s49
	s_nop 0
	global_load_lds_dwordx4 v88, s[30:31]
	v_mfma_f32_16x16x32_bf16 v[62:65], v[238:241], v[222:225], v[62:65]
	v_mfma_f32_16x16x32_bf16 v[58:61], v[242:245], v[222:225], v[58:61]
	v_mfma_f32_16x16x32_bf16 v[54:57], v[246:249], v[222:225], v[54:57]
	v_mfma_f32_16x16x32_bf16 v[50:53], v[250:253], v[222:225], v[50:53]
	ds_read_b128 v[222:225], v93 offset:2048
	ds_read_b128 v[146:149], v141 offset:2048
	s_add_i32 m0, s49, 0x2000
	s_nop 0
	global_load_lds_dwordx4 v90, s[30:31]
	v_mfma_f32_16x16x32_bf16 v[46:49], v[238:241], v[226:229], v[46:49]
	v_mfma_f32_16x16x32_bf16 v[42:45], v[242:245], v[226:229], v[42:45]
	v_mfma_f32_16x16x32_bf16 v[38:41], v[246:249], v[226:229], v[38:41]
	v_mfma_f32_16x16x32_bf16 v[34:37], v[250:253], v[226:229], v[34:37]
	ds_read_b128 v[226:229], v93 offset:4096
	ds_read_b128 v[156:159], v141 offset:4096
	s_add_i32 m0, s49, 0x4000
	s_nop 0
	global_load_lds_dwordx4 v92, s[30:31]
	v_mfma_f32_16x16x32_bf16 v[18:21], v[238:241], v[230:233], v[18:21]
	v_mfma_f32_16x16x32_bf16 v[22:25], v[242:245], v[230:233], v[22:25]
	v_mfma_f32_16x16x32_bf16 v[26:29], v[246:249], v[230:233], v[26:29]
	v_mfma_f32_16x16x32_bf16 v[30:33], v[250:253], v[230:233], v[30:33]
	ds_read_b128 v[230:233], v93 offset:6144
	ds_read_b128 v[160:163], v141 offset:6144
	s_add_i32 m0, s49, 0x6000
	s_nop 0
	global_load_lds_dwordx4 v94, s[30:31]
	v_mfma_f32_16x16x32_bf16 v[2:5], v[238:241], v[234:237], v[2:5]
	v_mfma_f32_16x16x32_bf16 v[6:9], v[242:245], v[234:237], v[6:9]
	v_mfma_f32_16x16x32_bf16 v[10:13], v[246:249], v[234:237], v[10:13]
	v_mfma_f32_16x16x32_bf16 v[14:17], v[250:253], v[234:237], v[14:17]
	ds_read_b128 v[234:237], v93 offset:8192
	s_add_i32 m0, s49, 0x8000
	s_nop 0
	global_load_lds_dwordx4 v96, s[30:31]
	s_waitcnt lgkmcnt(0)
	v_mfma_f32_16x16x32_bf16 v[78:81], v[142:145], v[218:221], v[78:81]
	v_mfma_f32_16x16x32_bf16 v[74:77], v[146:149], v[218:221], v[74:77]
	v_mfma_f32_16x16x32_bf16 v[70:73], v[156:159], v[218:221], v[70:73]
	v_mfma_f32_16x16x32_bf16 v[66:69], v[160:163], v[218:221], v[66:69]
	s_add_i32 s51, s51, 1
	s_and_b32 s54, s51, 7
	s_cmp_eq_u32 s54, 0
	s_cselect_b32 s44, s34, s35
	s_cselect_b32 s45, -1, 0
	v_lshl_add_u64 v[132:133], v[132:133], 0, s[44:45]
	global_load_dwordx2 v[114:115], v[132:133], off
	v_lshl_add_u64 v[180:181], v[132:133], 0, s[24:25]
	global_load_dwordx2 v[116:117], v[180:181], off
	v_mfma_f32_16x16x32_bf16 v[62:65], v[142:145], v[222:225], v[62:65]
	v_mfma_f32_16x16x32_bf16 v[58:61], v[146:149], v[222:225], v[58:61]
	v_mfma_f32_16x16x32_bf16 v[54:57], v[156:159], v[222:225], v[54:57]
	v_mfma_f32_16x16x32_bf16 v[50:53], v[160:163], v[222:225], v[50:53]
	v_lshl_add_u64 v[180:181], v[132:133], 0, s[26:27]
	global_load_dwordx2 v[118:119], v[180:181], off
	v_lshl_add_u64 v[180:181], v[132:133], 0, s[28:29]
	global_load_dwordx2 v[120:121], v[180:181], off
	v_mfma_f32_16x16x32_bf16 v[46:49], v[142:145], v[226:229], v[46:49]
	v_mfma_f32_16x16x32_bf16 v[42:45], v[146:149], v[226:229], v[42:45]
	v_mfma_f32_16x16x32_bf16 v[38:41], v[156:159], v[226:229], v[38:41]
	v_mfma_f32_16x16x32_bf16 v[34:37], v[160:163], v[226:229], v[34:37]
	v_lshl_add_u64 v[180:181], v[132:133], 0, s[36:37]
	global_load_dwordx2 v[122:123], v[180:181], off
	v_lshl_add_u64 v[180:181], v[132:133], 0, s[38:39]
	global_load_dwordx2 v[124:125], v[180:181], off
	v_mfma_f32_16x16x32_bf16 v[18:21], v[142:145], v[230:233], v[18:21]
	v_mfma_f32_16x16x32_bf16 v[22:25], v[146:149], v[230:233], v[22:25]
	v_mfma_f32_16x16x32_bf16 v[26:29], v[156:159], v[230:233], v[26:29]
	v_mfma_f32_16x16x32_bf16 v[30:33], v[160:163], v[230:233], v[30:33]
	v_lshl_add_u64 v[180:181], v[132:133], 0, s[40:41]
	global_load_dwordx2 v[126:127], v[180:181], off
	v_lshl_add_u64 v[180:181], v[132:133], 0, s[42:43]
	global_load_dwordx2 v[128:129], v[180:181], off
	v_mfma_f32_16x16x32_bf16 v[2:5], v[142:145], v[234:237], v[2:5]
	v_mfma_f32_16x16x32_bf16 v[6:9], v[146:149], v[234:237], v[6:9]
	v_mfma_f32_16x16x32_bf16 v[10:13], v[156:159], v[234:237], v[10:13]
	v_mfma_f32_16x16x32_bf16 v[14:17], v[160:163], v[234:237], v[14:17]
	s_waitcnt lgkmcnt(0)
	s_barrier
; #define MD_GLDS_A(buf, tau) do { _Pragma("unroll") for (int i = 0; i < 5; ++i) if (amask & (1u << i)) \
;         __builtin_amdgcn_global_load_lds((const unsigned*)((const char*)HIDp + aoff[i] + (size_t)((tau) & 7) * 128), (PG8_LAS unsigned*)(MD_SA(buf) + wid * 1024 + i * 8192), 16, 0, 0); } while (0)
; #define MD_B_ISSUE(sb, tau) do { const char* kb_ = Bb + (size_t)((tau) >> 3) * 512 + (size_t)((tau) & 7) * (64 * (size_t)RB); _Pragma("unroll") for (int j = 0; j < 8; ++j) { const char* p_ = kb_ + (size_t)j * RB; \
;         asm volatile("global_load_dwordx2 %0, %1, off" : "=&v"(sb[j]) : "v"(p_) : "memory"); } } while (0)
; #define MD_B_WAIT(sb, N) asm volatile("s_waitcnt vmcnt(%8)" : "+v"(sb[0]), "+v"(sb[1]), "+v"(sb[2]), "+v"(sb[3]), "+v"(sb[4]), "+v"(sb[5]), "+v"(sb[6]), "+v"(sb[7]) : "n"(N) : "memory")
; __device__ __forceinline__ void moe_down_stream(PG8_LAS unsigned char* lds, int e, int cb0, int slot0, int nv, const bf16_t* HIDp, const float* Wd, bf16_t* Y, const float* slot_w, const int* slot_dst) {
;     ...
;     f32x4 acc[DNM][4];
; #pragma unroll
;     for (int m = 0; m < DNM; ++m)
; #pragma unroll
;         for (int n = 0; n < 4; ++n) acc[m][n] = (f32x4){0.f, 0.f, 0.f, 0.f};
;     f32x2 s0[8], s1[8];
;     MD_GLDS_A(0, 0); MD_B_ISSUE(s0, 0); MD_B_ISSUE(s1, 1);
;     MD_B_WAIT(s0, 8); MD_B_WRITE(s0, 0); __builtin_amdgcn_sched_barrier(0); MD_B_ISSUE(s0, 2);
;     asm volatile("s_waitcnt vmcnt(16)" ::: "memory");
;     asm volatile("s_waitcnt lgkmcnt(0)" ::: "memory"); __builtin_amdgcn_s_barrier(); asm volatile("" ::: "memory");
; #pragma unroll 1
;     for (int t = 0; t < NT; t += 2) {
;         if (t + 2 < NT) MD_B_WAIT(s1, 8); else MD_B_WAIT(s1, 0);
;         MD_B_WRITE(s1, 1); __builtin_amdgcn_sched_barrier(0); MD_GLDS_A(1, t + 1); __builtin_amdgcn_sched_barrier(0);
;         if (t + 3 < NT) MD_B_ISSUE(s1, t + 3);
;         MD_COMPUTE(0);
;         MD_END(t + 3 >= NT);
;         if (t + 2 < NT) { MD_B_WAIT(s0, 8); MD_B_WRITE(s0, 0); __builtin_amdgcn_sched_barrier(0); MD_GLDS_A(0, t + 2); __builtin_amdgcn_sched_barrier(0); }
;         if (t + 4 < NT) MD_B_ISSUE(s0, t + 4);
;         MD_COMPUTE(1);
;         MD_END(t + 4 >= NT);
	s_mov_b32 s49, s46
	s_mov_b32 s46, s47
	s_mov_b32 s47, s48
	s_mov_b32 s48, s49
	s_waitcnt vmcnt(29)
	v_cvt_pk_bf16_f32 v172, v186, v188
	v_cvt_pk_bf16_f32 v173, v190, v192
	v_cvt_pk_bf16_f32 v174, v194, v196
	v_cvt_pk_bf16_f32 v175, v198, v200
	v_cvt_pk_bf16_f32 v176, v187, v189
	v_cvt_pk_bf16_f32 v177, v191, v193
	v_cvt_pk_bf16_f32 v178, v195, v197
	v_cvt_pk_bf16_f32 v179, v199, v201
	ds_write_b128 v95, v[172:175] offset:0
	ds_write_b128 v95, v[176:179] offset:128
	v_add_u32_e32 v91, s46, v135
	v_add_u32_e32 v93, s46, v137
	ds_read_b128 v[238:241], v139 offset:19456
	ds_read_b128 v[242:245], v139 offset:21504
	ds_read_b128 v[246:249], v139 offset:23552
	ds_read_b128 v[250:253], v139 offset:25600
	ds_read_b128 v[218:221], v91 offset:0
	ds_read_b128 v[222:225], v91 offset:2048
	ds_read_b128 v[226:229], v91 offset:4096
	ds_read_b128 v[230:233], v91 offset:6144
	ds_read_b128 v[234:237], v91 offset:8192
	s_add_i32 s49, s48, s74
	s_add_i32 s52, s52, 1
	s_and_b32 s54, s52, 7
	s_cmp_eq_u32 s54, 0
	s_cselect_b32 s54, s53, s32
	s_cselect_b32 s55, -1, 0
	s_add_u32 s30, s30, s54
	s_addc_u32 s31, s31, s55
	s_waitcnt lgkmcnt(0)
	v_mfma_f32_16x16x32_bf16 v[78:81], v[238:241], v[218:221], v[78:81]
	v_mfma_f32_16x16x32_bf16 v[74:77], v[242:245], v[218:221], v[74:77]
	v_mfma_f32_16x16x32_bf16 v[70:73], v[246:249], v[218:221], v[70:73]
	v_mfma_f32_16x16x32_bf16 v[66:69], v[250:253], v[218:221], v[66:69]
	ds_read_b128 v[218:221], v93 offset:0
	ds_read_b128 v[142:145], v141 offset:19456
	s_mov_b32 m0, s49
	s_nop 0
	global_load_lds_dwordx4 v88, s[30:31]
	v_mfma_f32_16x16x32_bf16 v[62:65], v[238:241], v[222:225], v[62:65]
	v_mfma_f32_16x16x32_bf16 v[58:61], v[242:245], v[222:225], v[58:61]
	v_mfma_f32_16x16x32_bf16 v[54:57], v[246:249], v[222:225], v[54:57]
	v_mfma_f32_16x16x32_bf16 v[50:53], v[250:253], v[222:225], v[50:53]
	ds_read_b128 v[222:225], v93 offset:2048
	ds_read_b128 v[146:149], v141 offset:21504
	s_add_i32 m0, s49, 0x2000
	s_nop 0
	global_load_lds_dwordx4 v90, s[30:31]
	v_mfma_f32_16x16x32_bf16 v[46:49], v[238:241], v[226:229], v[46:49]
	v_mfma_f32_16x16x32_bf16 v[42:45], v[242:245], v[226:229], v[42:45]
	v_mfma_f32_16x16x32_bf16 v[38:41], v[246:249], v[226:229], v[38:41]
	v_mfma_f32_16x16x32_bf16 v[34:37], v[250:253], v[226:229], v[34:37]
	ds_read_b128 v[226:229], v93 offset:4096
	ds_read_b128 v[156:159], v141 offset:23552
	s_add_i32 m0, s49, 0x4000
	s_nop 0
	global_load_lds_dwordx4 v92, s[30:31]
	v_mfma_f32_16x16x32_bf16 v[18:21], v[238:241], v[230:233], v[18:21]
	v_mfma_f32_16x16x32_bf16 v[22:25], v[242:245], v[230:233], v[22:25]
	v_mfma_f32_16x16x32_bf16 v[26:29], v[246:249], v[230:233], v[26:29]
	v_mfma_f32_16x16x32_bf16 v[30:33], v[250:253], v[230:233], v[30:33]
	ds_read_b128 v[230:233], v93 offset:6144
	ds_read_b128 v[160:163], v141 offset:25600
	s_add_i32 m0, s49, 0x6000
	s_nop 0
	global_load_lds_dwordx4 v94, s[30:31]
	v_mfma_f32_16x16x32_bf16 v[2:5], v[238:241], v[234:237], v[2:5]
	v_mfma_f32_16x16x32_bf16 v[6:9], v[242:245], v[234:237], v[6:9]
	v_mfma_f32_16x16x32_bf16 v[10:13], v[246:249], v[234:237], v[10:13]
	v_mfma_f32_16x16x32_bf16 v[14:17], v[250:253], v[234:237], v[14:17]
	ds_read_b128 v[234:237], v93 offset:8192
	s_add_i32 m0, s49, 0x8000
	s_nop 0
	global_load_lds_dwordx4 v96, s[30:31]
	s_waitcnt lgkmcnt(0)
	v_mfma_f32_16x16x32_bf16 v[78:81], v[142:145], v[218:221], v[78:81]
	v_mfma_f32_16x16x32_bf16 v[74:77], v[146:149], v[218:221], v[74:77]
	v_mfma_f32_16x16x32_bf16 v[70:73], v[156:159], v[218:221], v[70:73]
	v_mfma_f32_16x16x32_bf16 v[66:69], v[160:163], v[218:221], v[66:69]
	s_add_i32 s51, s51, 1
	s_and_b32 s54, s51, 7
	s_cmp_eq_u32 s54, 0
	s_cselect_b32 s44, s34, s35
	s_cselect_b32 s45, -1, 0
	v_lshl_add_u64 v[132:133], v[132:133], 0, s[44:45]
	global_load_dwordx2 v[186:187], v[132:133], off
	v_lshl_add_u64 v[180:181], v[132:133], 0, s[24:25]
	global_load_dwordx2 v[188:189], v[180:181], off
	v_mfma_f32_16x16x32_bf16 v[62:65], v[142:145], v[222:225], v[62:65]
	v_mfma_f32_16x16x32_bf16 v[58:61], v[146:149], v[222:225], v[58:61]
	v_mfma_f32_16x16x32_bf16 v[54:57], v[156:159], v[222:225], v[54:57]
	v_mfma_f32_16x16x32_bf16 v[50:53], v[160:163], v[222:225], v[50:53]
	v_lshl_add_u64 v[180:181], v[132:133], 0, s[26:27]
	global_load_dwordx2 v[190:191], v[180:181], off
	v_lshl_add_u64 v[180:181], v[132:133], 0, s[28:29]
	global_load_dwordx2 v[192:193], v[180:181], off
	v_mfma_f32_16x16x32_bf16 v[46:49], v[142:145], v[226:229], v[46:49]
	v_mfma_f32_16x16x32_bf16 v[42:45], v[146:149], v[226:229], v[42:45]
	v_mfma_f32_16x16x32_bf16 v[38:41], v[156:159], v[226:229], v[38:41]
	v_mfma_f32_16x16x32_bf16 v[34:37], v[160:163], v[226:229], v[34:37]
	v_lshl_add_u64 v[180:181], v[132:133], 0, s[36:37]
	global_load_dwordx2 v[194:195], v[180:181], off
	v_lshl_add_u64 v[180:181], v[132:133], 0, s[38:39]
	global_load_dwordx2 v[196:197], v[180:181], off
	v_mfma_f32_16x16x32_bf16 v[18:21], v[142:145], v[230:233], v[18:21]
	v_mfma_f32_16x16x32_bf16 v[22:25], v[146:149], v[230:233], v[22:25]
	v_mfma_f32_16x16x32_bf16 v[26:29], v[156:159], v[230:233], v[26:29]
	v_mfma_f32_16x16x32_bf16 v[30:33], v[160:163], v[230:233], v[30:33]
	v_lshl_add_u64 v[180:181], v[132:133], 0, s[40:41]
	global_load_dwordx2 v[198:199], v[180:181], off
	v_lshl_add_u64 v[180:181], v[132:133], 0, s[42:43]
	global_load_dwordx2 v[200:201], v[180:181], off
	v_mfma_f32_16x16x32_bf16 v[2:5], v[142:145], v[234:237], v[2:5]
	v_mfma_f32_16x16x32_bf16 v[6:9], v[146:149], v[234:237], v[6:9]
	v_mfma_f32_16x16x32_bf16 v[10:13], v[156:159], v[234:237], v[10:13]
	v_mfma_f32_16x16x32_bf16 v[14:17], v[160:163], v[234:237], v[14:17]
	s_waitcnt vmcnt(21)
	s_waitcnt lgkmcnt(0)
	s_barrier
; #define MD_GLDS_A(buf, tau) do { _Pragma("unroll") for (int i = 0; i < 5; ++i) if (amask & (1u << i)) \
;         __builtin_amdgcn_global_load_lds((const unsigned*)((const char*)HIDp + aoff[i] + (size_t)((tau) & 7) * 128), (PG8_LAS unsigned*)(MD_SA(buf) + wid * 1024 + i * 8192), 16, 0, 0); } while (0)
; #define MD_B_ISSUE(sb, tau) do { const char* kb_ = Bb + (size_t)((tau) >> 3) * 512 + (size_t)((tau) & 7) * (64 * (size_t)RB); _Pragma("unroll") for (int j = 0; j < 8; ++j) { const char* p_ = kb_ + (size_t)j * RB; \
;         asm volatile("global_load_dwordx2 %0, %1, off" : "=&v"(sb[j]) : "v"(p_) : "memory"); } } while (0)
; #define MD_B_WAIT(sb, N) asm volatile("s_waitcnt vmcnt(%8)" : "+v"(sb[0]), "+v"(sb[1]), "+v"(sb[2]), "+v"(sb[3]), "+v"(sb[4]), "+v"(sb[5]), "+v"(sb[6]), "+v"(sb[7]) : "n"(N) : "memory")
; __device__ __forceinline__ void moe_down_stream(PG8_LAS unsigned char* lds, int e, int cb0, int slot0, int nv, const bf16_t* HIDp, const float* Wd, bf16_t* Y, const float* slot_w, const int* slot_dst) {
;     ...
;     f32x4 acc[DNM][4];
; #pragma unroll
;     for (int m = 0; m < DNM; ++m)
; #pragma unroll
;         for (int n = 0; n < 4; ++n) acc[m][n] = (f32x4){0.f, 0.f, 0.f, 0.f};
;     f32x2 s0[8], s1[8];
;     MD_GLDS_A(0, 0); MD_B_ISSUE(s0, 0); MD_B_ISSUE(s1, 1);
;     MD_B_WAIT(s0, 8); MD_B_WRITE(s0, 0); __builtin_amdgcn_sched_barrier(0); MD_B_ISSUE(s0, 2);
;     asm volatile("s_waitcnt vmcnt(16)" ::: "memory");
;     asm volatile("s_waitcnt lgkmcnt(0)" ::: "memory"); __builtin_amdgcn_s_barrier(); asm volatile("" ::: "memory");
; #pragma unroll 1
;     for (int t = 0; t < NT; t += 2) {
;         if (t + 2 < NT) MD_B_WAIT(s1, 8); else MD_B_WAIT(s1, 0);
;         MD_B_WRITE(s1, 1); __builtin_amdgcn_sched_barrier(0); MD_GLDS_A(1, t + 1); __builtin_amdgcn_sched_barrier(0);
;         if (t + 3 < NT) MD_B_ISSUE(s1, t + 3);
;         MD_COMPUTE(0);
;         MD_END(t + 3 >= NT);
;         if (t + 2 < NT) { MD_B_WAIT(s0, 8); MD_B_WRITE(s0, 0); __builtin_amdgcn_sched_barrier(0); MD_GLDS_A(0, t + 2); __builtin_amdgcn_sched_barrier(0); }
;         if (t + 4 < NT) MD_B_ISSUE(s0, t + 4);
;         MD_COMPUTE(1);
;         MD_END(t + 4 >= NT);
	s_mov_b32 s49, s46
	s_mov_b32 s46, s47
	s_mov_b32 s47, s48
	s_mov_b32 s48, s49
	v_cvt_pk_bf16_f32 v172, v202, v204
	v_cvt_pk_bf16_f32 v173, v206, v208
	v_cvt_pk_bf16_f32 v174, v210, v212
	v_cvt_pk_bf16_f32 v175, v214, v216
	v_cvt_pk_bf16_f32 v176, v203, v205
	v_cvt_pk_bf16_f32 v177, v207, v209
	v_cvt_pk_bf16_f32 v178, v211, v213
	v_cvt_pk_bf16_f32 v179, v215, v217
	ds_write_b128 v95, v[172:175] offset:19456
	ds_write_b128 v95, v[176:179] offset:19584
	v_add_u32_e32 v91, s46, v135
	v_add_u32_e32 v93, s46, v137
	ds_read_b128 v[238:241], v139 offset:0
	ds_read_b128 v[242:245], v139 offset:2048
	ds_read_b128 v[246:249], v139 offset:4096
	ds_read_b128 v[250:253], v139 offset:6144
	ds_read_b128 v[218:221], v91 offset:0
	ds_read_b128 v[222:225], v91 offset:2048
	ds_read_b128 v[226:229], v91 offset:4096
	ds_read_b128 v[230:233], v91 offset:6144
	ds_read_b128 v[234:237], v91 offset:8192
	s_add_i32 s49, s48, s74
	s_add_i32 s52, s52, 1
	s_and_b32 s54, s52, 7
	s_cmp_eq_u32 s54, 0
	s_cselect_b32 s54, s53, s32
	s_cselect_b32 s55, -1, 0
	s_add_u32 s30, s30, s54
	s_addc_u32 s31, s31, s55
	s_waitcnt lgkmcnt(0)
	v_mfma_f32_16x16x32_bf16 v[78:81], v[238:241], v[218:221], v[78:81]
	v_mfma_f32_16x16x32_bf16 v[74:77], v[242:245], v[218:221], v[74:77]
	v_mfma_f32_16x16x32_bf16 v[70:73], v[246:249], v[218:221], v[70:73]
	v_mfma_f32_16x16x32_bf16 v[66:69], v[250:253], v[218:221], v[66:69]
	ds_read_b128 v[218:221], v93 offset:0
	ds_read_b128 v[142:145], v141 offset:0
	s_mov_b32 m0, s49
	s_nop 0
	global_load_lds_dwordx4 v88, s[30:31]
	v_mfma_f32_16x16x32_bf16 v[62:65], v[238:241], v[222:225], v[62:65]
	v_mfma_f32_16x16x32_bf16 v[58:61], v[242:245], v[222:225], v[58:61]
	v_mfma_f32_16x16x32_bf16 v[54:57], v[246:249], v[222:225], v[54:57]
	v_mfma_f32_16x16x32_bf16 v[50:53], v[250:253], v[222:225], v[50:53]
	ds_read_b128 v[222:225], v93 offset:2048
	ds_read_b128 v[146:149], v141 offset:2048
	s_add_i32 m0, s49, 0x2000
	s_nop 0
	global_load_lds_dwordx4 v90, s[30:31]
	v_mfma_f32_16x16x32_bf16 v[46:49], v[238:241], v[226:229], v[46:49]
	v_mfma_f32_16x16x32_bf16 v[42:45], v[242:245], v[226:229], v[42:45]
	v_mfma_f32_16x16x32_bf16 v[38:41], v[246:249], v[226:229], v[38:41]
	v_mfma_f32_16x16x32_bf16 v[34:37], v[250:253], v[226:229], v[34:37]
	ds_read_b128 v[226:229], v93 offset:4096
	ds_read_b128 v[156:159], v141 offset:4096
	s_add_i32 m0, s49, 0x4000
	s_nop 0
	global_load_lds_dwordx4 v92, s[30:31]
	v_mfma_f32_16x16x32_bf16 v[18:21], v[238:241], v[230:233], v[18:21]
	v_mfma_f32_16x16x32_bf16 v[22:25], v[242:245], v[230:233], v[22:25]
	v_mfma_f32_16x16x32_bf16 v[26:29], v[246:249], v[230:233], v[26:29]
	v_mfma_f32_16x16x32_bf16 v[30:33], v[250:253], v[230:233], v[30:33]
	ds_read_b128 v[230:233], v93 offset:6144
	ds_read_b128 v[160:163], v141 offset:6144
	s_add_i32 m0, s49, 0x6000
	s_nop 0
	global_load_lds_dwordx4 v94, s[30:31]
	v_mfma_f32_16x16x32_bf16 v[2:5], v[238:241], v[234:237], v[2:5]
	v_mfma_f32_16x16x32_bf16 v[6:9], v[242:245], v[234:237], v[6:9]
	v_mfma_f32_16x16x32_bf16 v[10:13], v[246:249], v[234:237], v[10:13]
	v_mfma_f32_16x16x32_bf16 v[14:17], v[250:253], v[234:237], v[14:17]
	ds_read_b128 v[234:237], v93 offset:8192
	s_add_i32 m0, s49, 0x8000
	s_nop 0
	global_load_lds_dwordx4 v96, s[30:31]
	s_waitcnt lgkmcnt(0)
	v_mfma_f32_16x16x32_bf16 v[78:81], v[142:145], v[218:221], v[78:81]
	v_mfma_f32_16x16x32_bf16 v[74:77], v[146:149], v[218:221], v[74:77]
	v_mfma_f32_16x16x32_bf16 v[70:73], v[156:159], v[218:221], v[70:73]
	v_mfma_f32_16x16x32_bf16 v[66:69], v[160:163], v[218:221], v[66:69]
	s_add_i32 s51, s51, 1
	s_and_b32 s54, s51, 7
	s_cmp_eq_u32 s54, 0
	s_cselect_b32 s44, s34, s35
	s_cselect_b32 s45, -1, 0
	v_lshl_add_u64 v[132:133], v[132:133], 0, s[44:45]
	global_load_dwordx2 v[202:203], v[132:133], off
	v_lshl_add_u64 v[180:181], v[132:133], 0, s[24:25]
	global_load_dwordx2 v[204:205], v[180:181], off
	v_mfma_f32_16x16x32_bf16 v[62:65], v[142:145], v[222:225], v[62:65]
	v_mfma_f32_16x16x32_bf16 v[58:61], v[146:149], v[222:225], v[58:61]
	v_mfma_f32_16x16x32_bf16 v[54:57], v[156:159], v[222:225], v[54:57]
	v_mfma_f32_16x16x32_bf16 v[50:53], v[160:163], v[222:225], v[50:53]
	v_lshl_add_u64 v[180:181], v[132:133], 0, s[26:27]
	global_load_dwordx2 v[206:207], v[180:181], off
	v_lshl_add_u64 v[180:181], v[132:133], 0, s[28:29]
	global_load_dwordx2 v[208:209], v[180:181], off
	v_mfma_f32_16x16x32_bf16 v[46:49], v[142:145], v[226:229], v[46:49]
	v_mfma_f32_16x16x32_bf16 v[42:45], v[146:149], v[226:229], v[42:45]
	v_mfma_f32_16x16x32_bf16 v[38:41], v[156:159], v[226:229], v[38:41]
	v_mfma_f32_16x16x32_bf16 v[34:37], v[160:163], v[226:229], v[34:37]
	v_lshl_add_u64 v[180:181], v[132:133], 0, s[36:37]
	global_load_dwordx2 v[210:211], v[180:181], off
	v_lshl_add_u64 v[180:181], v[132:133], 0, s[38:39]
	global_load_dwordx2 v[212:213], v[180:181], off
	v_mfma_f32_16x16x32_bf16 v[18:21], v[142:145], v[230:233], v[18:21]
	v_mfma_f32_16x16x32_bf16 v[22:25], v[146:149], v[230:233], v[22:25]
	v_mfma_f32_16x16x32_bf16 v[26:29], v[156:159], v[230:233], v[26:29]
	v_mfma_f32_16x16x32_bf16 v[30:33], v[160:163], v[230:233], v[30:33]
	v_lshl_add_u64 v[180:181], v[132:133], 0, s[40:41]
	global_load_dwordx2 v[214:215], v[180:181], off
	v_lshl_add_u64 v[180:181], v[132:133], 0, s[42:43]
	global_load_dwordx2 v[216:217], v[180:181], off
	v_mfma_f32_16x16x32_bf16 v[2:5], v[142:145], v[234:237], v[2:5]
	v_mfma_f32_16x16x32_bf16 v[6:9], v[146:149], v[234:237], v[6:9]
	v_mfma_f32_16x16x32_bf16 v[10:13], v[156:159], v[234:237], v[10:13]
	v_mfma_f32_16x16x32_bf16 v[14:17], v[160:163], v[234:237], v[14:17]
	s_waitcnt vmcnt(21)
	s_waitcnt lgkmcnt(0)
	s_barrier
; #define MD_GLDS_A(buf, tau) do { _Pragma("unroll") for (int i = 0; i < 5; ++i) if (amask & (1u << i)) \
;         __builtin_amdgcn_global_load_lds((const unsigned*)((const char*)HIDp + aoff[i] + (size_t)((tau) & 7) * 128), (PG8_LAS unsigned*)(MD_SA(buf) + wid * 1024 + i * 8192), 16, 0, 0); } while (0)
; #define MD_B_ISSUE(sb, tau) do { const char* kb_ = Bb + (size_t)((tau) >> 3) * 512 + (size_t)((tau) & 7) * (64 * (size_t)RB); _Pragma("unroll") for (int j = 0; j < 8; ++j) { const char* p_ = kb_ + (size_t)j * RB; \
;         asm volatile("global_load_dwordx2 %0, %1, off" : "=&v"(sb[j]) : "v"(p_) : "memory"); } } while (0)
; #define MD_B_WAIT(sb, N) asm volatile("s_waitcnt vmcnt(%8)" : "+v"(sb[0]), "+v"(sb[1]), "+v"(sb[2]), "+v"(sb[3]), "+v"(sb[4]), "+v"(sb[5]), "+v"(sb[6]), "+v"(sb[7]) : "n"(N) : "memory")
; #define MD_END(last) do { if (last) asm volatile("s_waitcnt vmcnt(0)" ::: "memory"); else asm volatile("s_waitcnt vmcnt(8)" ::: "memory"); \
;         asm volatile("s_waitcnt lgkmcnt(0)" ::: "memory"); __builtin_amdgcn_s_barrier(); asm volatile("" ::: "memory"); } while (0)
; __device__ __forceinline__ void moe_down_stream(PG8_LAS unsigned char* lds, int e, int cb0, int slot0, int nv, const bf16_t* HIDp, const float* Wd, bf16_t* Y, const float* slot_w, const int* slot_dst) {
;     ...
;     for (int t = 0; t < NT; t += 2) {
;         if (t + 2 < NT) MD_B_WAIT(s1, 8); else MD_B_WAIT(s1, 0);
;         MD_B_WRITE(s1, 1); __builtin_amdgcn_sched_barrier(0); MD_GLDS_A(1, t + 1); __builtin_amdgcn_sched_barrier(0);
;         if (t + 3 < NT) MD_B_ISSUE(s1, t + 3);
;         MD_COMPUTE(0);
;         MD_END(t + 3 >= NT);
;         if (t + 2 < NT) { MD_B_WAIT(s0, 8); MD_B_WRITE(s0, 0); __builtin_amdgcn_sched_barrier(0); MD_GLDS_A(0, t + 2); __builtin_amdgcn_sched_barrier(0); }
;         if (t + 4 < NT) MD_B_ISSUE(s0, t + 4);
;         MD_COMPUTE(1);
;         MD_END(t + 4 >= NT);
	s_mov_b32 s49, s46
	s_mov_b32 s46, s47
	s_mov_b32 s47, s48
	s_mov_b32 s48, s49
	v_cvt_pk_bf16_f32 v172, v98, v100
	v_cvt_pk_bf16_f32 v173, v102, v104
	v_cvt_pk_bf16_f32 v174, v106, v108
	v_cvt_pk_bf16_f32 v175, v110, v112
	v_cvt_pk_bf16_f32 v176, v99, v101
	v_cvt_pk_bf16_f32 v177, v103, v105
	v_cvt_pk_bf16_f32 v178, v107, v109
	v_cvt_pk_bf16_f32 v179, v111, v113
	ds_write_b128 v95, v[172:175] offset:0
	ds_write_b128 v95, v[176:179] offset:128
	v_add_u32_e32 v91, s46, v135
	v_add_u32_e32 v93, s46, v137
	ds_read_b128 v[238:241], v139 offset:19456
	ds_read_b128 v[242:245], v139 offset:21504
	ds_read_b128 v[246:249], v139 offset:23552
	ds_read_b128 v[250:253], v139 offset:25600
	ds_read_b128 v[218:221], v91 offset:0
	ds_read_b128 v[222:225], v91 offset:2048
	ds_read_b128 v[226:229], v91 offset:4096
	ds_read_b128 v[230:233], v91 offset:6144
	ds_read_b128 v[234:237], v91 offset:8192
	s_add_i32 s49, s48, s74
	s_add_i32 s52, s52, 1
	s_and_b32 s54, s52, 7
	s_cmp_eq_u32 s54, 0
	s_cselect_b32 s54, s53, s32
	s_cselect_b32 s55, -1, 0
	s_add_u32 s30, s30, s54
	s_addc_u32 s31, s31, s55
	s_waitcnt lgkmcnt(0)
	v_mfma_f32_16x16x32_bf16 v[78:81], v[238:241], v[218:221], v[78:81]
	v_mfma_f32_16x16x32_bf16 v[74:77], v[242:245], v[218:221], v[74:77]
	v_mfma_f32_16x16x32_bf16 v[70:73], v[246:249], v[218:221], v[70:73]
	v_mfma_f32_16x16x32_bf16 v[66:69], v[250:253], v[218:221], v[66:69]
	ds_read_b128 v[218:221], v93 offset:0
	ds_read_b128 v[142:145], v141 offset:19456
	s_mov_b32 m0, s49
	s_nop 0
	global_load_lds_dwordx4 v88, s[30:31]
	v_mfma_f32_16x16x32_bf16 v[62:65], v[238:241], v[222:225], v[62:65]
	v_mfma_f32_16x16x32_bf16 v[58:61], v[242:245], v[222:225], v[58:61]
	v_mfma_f32_16x16x32_bf16 v[54:57], v[246:249], v[222:225], v[54:57]
	v_mfma_f32_16x16x32_bf16 v[50:53], v[250:253], v[222:225], v[50:53]
	ds_read_b128 v[222:225], v93 offset:2048
	ds_read_b128 v[146:149], v141 offset:21504
	s_add_i32 m0, s49, 0x2000
	s_nop 0
	global_load_lds_dwordx4 v90, s[30:31]
	v_mfma_f32_16x16x32_bf16 v[46:49], v[238:241], v[226:229], v[46:49]
	v_mfma_f32_16x16x32_bf16 v[42:45], v[242:245], v[226:229], v[42:45]
	v_mfma_f32_16x16x32_bf16 v[38:41], v[246:249], v[226:229], v[38:41]
	v_mfma_f32_16x16x32_bf16 v[34:37], v[250:253], v[226:229], v[34:37]
	ds_read_b128 v[226:229], v93 offset:4096
	ds_read_b128 v[156:159], v141 offset:23552
	s_add_i32 m0, s49, 0x4000
	s_nop 0
	global_load_lds_dwordx4 v92, s[30:31]
	v_mfma_f32_16x16x32_bf16 v[18:21], v[238:241], v[230:233], v[18:21]
	v_mfma_f32_16x16x32_bf16 v[22:25], v[242:245], v[230:233], v[22:25]
	v_mfma_f32_16x16x32_bf16 v[26:29], v[246:249], v[230:233], v[26:29]
	v_mfma_f32_16x16x32_bf16 v[30:33], v[250:253], v[230:233], v[30:33]
	ds_read_b128 v[230:233], v93 offset:6144
	ds_read_b128 v[160:163], v141 offset:25600
	s_add_i32 m0, s49, 0x6000
	s_nop 0
	global_load_lds_dwordx4 v94, s[30:31]
	v_mfma_f32_16x16x32_bf16 v[2:5], v[238:241], v[234:237], v[2:5]
	v_mfma_f32_16x16x32_bf16 v[6:9], v[242:245], v[234:237], v[6:9]
	v_mfma_f32_16x16x32_bf16 v[10:13], v[246:249], v[234:237], v[10:13]
	v_mfma_f32_16x16x32_bf16 v[14:17], v[250:253], v[234:237], v[14:17]
	ds_read_b128 v[234:237], v93 offset:8192
	s_add_i32 m0, s49, 0x8000
	s_nop 0
	global_load_lds_dwordx4 v96, s[30:31]
	s_waitcnt lgkmcnt(0)
	v_mfma_f32_16x16x32_bf16 v[78:81], v[142:145], v[218:221], v[78:81]
	v_mfma_f32_16x16x32_bf16 v[74:77], v[146:149], v[218:221], v[74:77]
	v_mfma_f32_16x16x32_bf16 v[70:73], v[156:159], v[218:221], v[70:73]
	v_mfma_f32_16x16x32_bf16 v[66:69], v[160:163], v[218:221], v[66:69]
	s_add_i32 s51, s51, 1
	s_and_b32 s54, s51, 7
	s_cmp_eq_u32 s54, 0
	s_cselect_b32 s44, s34, s35
	s_cselect_b32 s45, -1, 0
	v_lshl_add_u64 v[132:133], v[132:133], 0, s[44:45]
	global_load_dwordx2 v[98:99], v[132:133], off
	v_lshl_add_u64 v[180:181], v[132:133], 0, s[24:25]
	global_load_dwordx2 v[100:101], v[180:181], off
	v_mfma_f32_16x16x32_bf16 v[62:65], v[142:145], v[222:225], v[62:65]
	v_mfma_f32_16x16x32_bf16 v[58:61], v[146:149], v[222:225], v[58:61]
	v_mfma_f32_16x16x32_bf16 v[54:57], v[156:159], v[222:225], v[54:57]
	v_mfma_f32_16x16x32_bf16 v[50:53], v[160:163], v[222:225], v[50:53]
	v_lshl_add_u64 v[180:181], v[132:133], 0, s[26:27]
	global_load_dwordx2 v[102:103], v[180:181], off
	v_lshl_add_u64 v[180:181], v[132:133], 0, s[28:29]
	global_load_dwordx2 v[104:105], v[180:181], off
	v_mfma_f32_16x16x32_bf16 v[46:49], v[142:145], v[226:229], v[46:49]
	v_mfma_f32_16x16x32_bf16 v[42:45], v[146:149], v[226:229], v[42:45]
	v_mfma_f32_16x16x32_bf16 v[38:41], v[156:159], v[226:229], v[38:41]
	v_mfma_f32_16x16x32_bf16 v[34:37], v[160:163], v[226:229], v[34:37]
	v_lshl_add_u64 v[180:181], v[132:133], 0, s[36:37]
	global_load_dwordx2 v[106:107], v[180:181], off
	v_lshl_add_u64 v[180:181], v[132:133], 0, s[38:39]
	global_load_dwordx2 v[108:109], v[180:181], off
	v_mfma_f32_16x16x32_bf16 v[18:21], v[142:145], v[230:233], v[18:21]
	v_mfma_f32_16x16x32_bf16 v[22:25], v[146:149], v[230:233], v[22:25]
	v_mfma_f32_16x16x32_bf16 v[26:29], v[156:159], v[230:233], v[26:29]
	v_mfma_f32_16x16x32_bf16 v[30:33], v[160:163], v[230:233], v[30:33]
	v_lshl_add_u64 v[180:181], v[132:133], 0, s[40:41]
	global_load_dwordx2 v[110:111], v[180:181], off
	v_lshl_add_u64 v[180:181], v[132:133], 0, s[42:43]
	global_load_dwordx2 v[112:113], v[180:181], off
	v_mfma_f32_16x16x32_bf16 v[2:5], v[142:145], v[234:237], v[2:5]
	v_mfma_f32_16x16x32_bf16 v[6:9], v[146:149], v[234:237], v[6:9]
	v_mfma_f32_16x16x32_bf16 v[10:13], v[156:159], v[234:237], v[10:13]
	v_mfma_f32_16x16x32_bf16 v[14:17], v[160:163], v[234:237], v[14:17]
	s_waitcnt vmcnt(21)
	s_waitcnt lgkmcnt(0)
	s_barrier
; #define MD_GLDS_A(buf, tau) do { _Pragma("unroll") for (int i = 0; i < 5; ++i) if (amask & (1u << i)) \
;         __builtin_amdgcn_global_load_lds((const unsigned*)((const char*)HIDp + aoff[i] + (size_t)((tau) & 7) * 128), (PG8_LAS unsigned*)(MD_SA(buf) + wid * 1024 + i * 8192), 16, 0, 0); } while (0)
; #define MD_B_ISSUE(sb, tau) do { const char* kb_ = Bb + (size_t)((tau) >> 3) * 512 + (size_t)((tau) & 7) * (64 * (size_t)RB); _Pragma("unroll") for (int j = 0; j < 8; ++j) { const char* p_ = kb_ + (size_t)j * RB; \
;         asm volatile("global_load_dwordx2 %0, %1, off" : "=&v"(sb[j]) : "v"(p_) : "memory"); } } while (0)
; #define MD_B_WAIT(sb, N) asm volatile("s_waitcnt vmcnt(%8)" : "+v"(sb[0]), "+v"(sb[1]), "+v"(sb[2]), "+v"(sb[3]), "+v"(sb[4]), "+v"(sb[5]), "+v"(sb[6]), "+v"(sb[7]) : "n"(N) : "memory")
; #define MD_END(last) do { if (last) asm volatile("s_waitcnt vmcnt(0)" ::: "memory"); else asm volatile("s_waitcnt vmcnt(8)" ::: "memory"); \
;         asm volatile("s_waitcnt lgkmcnt(0)" ::: "memory"); __builtin_amdgcn_s_barrier(); asm volatile("" ::: "memory"); } while (0)
; __device__ __forceinline__ void moe_down_stream(PG8_LAS unsigned char* lds, int e, int cb0, int slot0, int nv, const bf16_t* HIDp, const float* Wd, bf16_t* Y, const float* slot_w, const int* slot_dst) {
;     ...
;     for (int t = 0; t < NT; t += 2) {
;         if (t + 2 < NT) MD_B_WAIT(s1, 8); else MD_B_WAIT(s1, 0);
;         MD_B_WRITE(s1, 1); __builtin_amdgcn_sched_barrier(0); MD_GLDS_A(1, t + 1); __builtin_amdgcn_sched_barrier(0);
;         if (t + 3 < NT) MD_B_ISSUE(s1, t + 3);
;         MD_COMPUTE(0);
;         MD_END(t + 3 >= NT);
;         if (t + 2 < NT) { MD_B_WAIT(s0, 8); MD_B_WRITE(s0, 0); __builtin_amdgcn_sched_barrier(0); MD_GLDS_A(0, t + 2); __builtin_amdgcn_sched_barrier(0); }
;         if (t + 4 < NT) MD_B_ISSUE(s0, t + 4);
;         MD_COMPUTE(1);
;         MD_END(t + 4 >= NT);
	s_mov_b32 s49, s46
	s_mov_b32 s46, s47
	s_mov_b32 s47, s48
	s_mov_b32 s48, s49
	v_cvt_pk_bf16_f32 v172, v114, v116
	v_cvt_pk_bf16_f32 v173, v118, v120
	v_cvt_pk_bf16_f32 v174, v122, v124
	v_cvt_pk_bf16_f32 v175, v126, v128
	v_cvt_pk_bf16_f32 v176, v115, v117
	v_cvt_pk_bf16_f32 v177, v119, v121
	v_cvt_pk_bf16_f32 v178, v123, v125
	v_cvt_pk_bf16_f32 v179, v127, v129
	ds_write_b128 v95, v[172:175] offset:19456
	ds_write_b128 v95, v[176:179] offset:19584
	v_add_u32_e32 v91, s46, v135
	v_add_u32_e32 v93, s46, v137
	ds_read_b128 v[238:241], v139 offset:0
	ds_read_b128 v[242:245], v139 offset:2048
	ds_read_b128 v[246:249], v139 offset:4096
	ds_read_b128 v[250:253], v139 offset:6144
	ds_read_b128 v[218:221], v91 offset:0
	ds_read_b128 v[222:225], v91 offset:2048
	ds_read_b128 v[226:229], v91 offset:4096
	ds_read_b128 v[230:233], v91 offset:6144
	ds_read_b128 v[234:237], v91 offset:8192
	s_add_i32 s49, s48, s74
	s_add_i32 s52, s52, 1
	s_and_b32 s54, s52, 7
	s_cmp_eq_u32 s54, 0
	s_cselect_b32 s54, s53, s32
	s_cselect_b32 s55, -1, 0
	s_add_u32 s30, s30, s54
	s_addc_u32 s31, s31, s55
	s_waitcnt lgkmcnt(0)
	v_mfma_f32_16x16x32_bf16 v[78:81], v[238:241], v[218:221], v[78:81]
	v_mfma_f32_16x16x32_bf16 v[74:77], v[242:245], v[218:221], v[74:77]
	v_mfma_f32_16x16x32_bf16 v[70:73], v[246:249], v[218:221], v[70:73]
	v_mfma_f32_16x16x32_bf16 v[66:69], v[250:253], v[218:221], v[66:69]
	ds_read_b128 v[218:221], v93 offset:0
	ds_read_b128 v[142:145], v141 offset:0
	s_mov_b32 m0, s49
	s_nop 0
	global_load_lds_dwordx4 v88, s[30:31]
	v_mfma_f32_16x16x32_bf16 v[62:65], v[238:241], v[222:225], v[62:65]
	v_mfma_f32_16x16x32_bf16 v[58:61], v[242:245], v[222:225], v[58:61]
	v_mfma_f32_16x16x32_bf16 v[54:57], v[246:249], v[222:225], v[54:57]
	v_mfma_f32_16x16x32_bf16 v[50:53], v[250:253], v[222:225], v[50:53]
	ds_read_b128 v[222:225], v93 offset:2048
	ds_read_b128 v[146:149], v141 offset:2048
	s_add_i32 m0, s49, 0x2000
	s_nop 0
	global_load_lds_dwordx4 v90, s[30:31]
	v_mfma_f32_16x16x32_bf16 v[46:49], v[238:241], v[226:229], v[46:49]
	v_mfma_f32_16x16x32_bf16 v[42:45], v[242:245], v[226:229], v[42:45]
	v_mfma_f32_16x16x32_bf16 v[38:41], v[246:249], v[226:229], v[38:41]
	v_mfma_f32_16x16x32_bf16 v[34:37], v[250:253], v[226:229], v[34:37]
	ds_read_b128 v[226:229], v93 offset:4096
	ds_read_b128 v[156:159], v141 offset:4096
	s_add_i32 m0, s49, 0x4000
	s_nop 0
	global_load_lds_dwordx4 v92, s[30:31]
	v_mfma_f32_16x16x32_bf16 v[18:21], v[238:241], v[230:233], v[18:21]
	v_mfma_f32_16x16x32_bf16 v[22:25], v[242:245], v[230:233], v[22:25]
	v_mfma_f32_16x16x32_bf16 v[26:29], v[246:249], v[230:233], v[26:29]
	v_mfma_f32_16x16x32_bf16 v[30:33], v[250:253], v[230:233], v[30:33]
	ds_read_b128 v[230:233], v93 offset:6144
	ds_read_b128 v[160:163], v141 offset:6144
	s_add_i32 m0, s49, 0x6000
	s_nop 0
	global_load_lds_dwordx4 v94, s[30:31]
	v_mfma_f32_16x16x32_bf16 v[2:5], v[238:241], v[234:237], v[2:5]
	v_mfma_f32_16x16x32_bf16 v[6:9], v[242:245], v[234:237], v[6:9]
	v_mfma_f32_16x16x32_bf16 v[10:13], v[246:249], v[234:237], v[10:13]
	v_mfma_f32_16x16x32_bf16 v[14:17], v[250:253], v[234:237], v[14:17]
	ds_read_b128 v[234:237], v93 offset:8192
	s_add_i32 m0, s49, 0x8000
	s_nop 0
	global_load_lds_dwordx4 v96, s[30:31]
	s_waitcnt lgkmcnt(0)
	v_mfma_f32_16x16x32_bf16 v[78:81], v[142:145], v[218:221], v[78:81]
	v_mfma_f32_16x16x32_bf16 v[74:77], v[146:149], v[218:221], v[74:77]
	v_mfma_f32_16x16x32_bf16 v[70:73], v[156:159], v[218:221], v[70:73]
	v_mfma_f32_16x16x32_bf16 v[66:69], v[160:163], v[218:221], v[66:69]
	s_add_i32 s51, s51, 1
	s_and_b32 s54, s51, 7
	s_cmp_eq_u32 s54, 0
	s_cselect_b32 s44, s34, s35
	s_cselect_b32 s45, -1, 0
	v_lshl_add_u64 v[132:133], v[132:133], 0, s[44:45]
	global_load_dwordx2 v[114:115], v[132:133], off
	v_lshl_add_u64 v[180:181], v[132:133], 0, s[24:25]
	global_load_dwordx2 v[116:117], v[180:181], off
	v_mfma_f32_16x16x32_bf16 v[62:65], v[142:145], v[222:225], v[62:65]
	v_mfma_f32_16x16x32_bf16 v[58:61], v[146:149], v[222:225], v[58:61]
	v_mfma_f32_16x16x32_bf16 v[54:57], v[156:159], v[222:225], v[54:57]
	v_mfma_f32_16x16x32_bf16 v[50:53], v[160:163], v[222:225], v[50:53]
	v_lshl_add_u64 v[180:181], v[132:133], 0, s[26:27]
	global_load_dwordx2 v[118:119], v[180:181], off
	v_lshl_add_u64 v[180:181], v[132:133], 0, s[28:29]
	global_load_dwordx2 v[120:121], v[180:181], off
	v_mfma_f32_16x16x32_bf16 v[46:49], v[142:145], v[226:229], v[46:49]
	v_mfma_f32_16x16x32_bf16 v[42:45], v[146:149], v[226:229], v[42:45]
	v_mfma_f32_16x16x32_bf16 v[38:41], v[156:159], v[226:229], v[38:41]
	v_mfma_f32_16x16x32_bf16 v[34:37], v[160:163], v[226:229], v[34:37]
	v_lshl_add_u64 v[180:181], v[132:133], 0, s[36:37]
	global_load_dwordx2 v[122:123], v[180:181], off
	v_lshl_add_u64 v[180:181], v[132:133], 0, s[38:39]
	global_load_dwordx2 v[124:125], v[180:181], off
	v_mfma_f32_16x16x32_bf16 v[18:21], v[142:145], v[230:233], v[18:21]
	v_mfma_f32_16x16x32_bf16 v[22:25], v[146:149], v[230:233], v[22:25]
	v_mfma_f32_16x16x32_bf16 v[26:29], v[156:159], v[230:233], v[26:29]
	v_mfma_f32_16x16x32_bf16 v[30:33], v[160:163], v[230:233], v[30:33]
	v_lshl_add_u64 v[180:181], v[132:133], 0, s[40:41]
	global_load_dwordx2 v[126:127], v[180:181], off
	v_lshl_add_u64 v[180:181], v[132:133], 0, s[42:43]
	global_load_dwordx2 v[128:129], v[180:181], off
	v_mfma_f32_16x16x32_bf16 v[2:5], v[142:145], v[234:237], v[2:5]
	v_mfma_f32_16x16x32_bf16 v[6:9], v[146:149], v[234:237], v[6:9]
	v_mfma_f32_16x16x32_bf16 v[10:13], v[156:159], v[234:237], v[10:13]
	v_mfma_f32_16x16x32_bf16 v[14:17], v[160:163], v[234:237], v[14:17]
	s_waitcnt vmcnt(21)
	s_waitcnt lgkmcnt(0)
	s_barrier
; #define MD_GLDS_A(buf, tau) do { _Pragma("unroll") for (int i = 0; i < 5; ++i) if (amask & (1u << i)) \
;         __builtin_amdgcn_global_load_lds((const unsigned*)((const char*)HIDp + aoff[i] + (size_t)((tau) & 7) * 128), (PG8_LAS unsigned*)(MD_SA(buf) + wid * 1024 + i * 8192), 16, 0, 0); } while (0)
; #define MD_B_ISSUE(sb, tau) do { const char* kb_ = Bb + (size_t)((tau) >> 3) * 512 + (size_t)((tau) & 7) * (64 * (size_t)RB); _Pragma("unroll") for (int j = 0; j < 8; ++j) { const char* p_ = kb_ + (size_t)j * RB; \
;         asm volatile("global_load_dwordx2 %0, %1, off" : "=&v"(sb[j]) : "v"(p_) : "memory"); } } while (0)
; #define MD_B_WAIT(sb, N) asm volatile("s_waitcnt vmcnt(%8)" : "+v"(sb[0]), "+v"(sb[1]), "+v"(sb[2]), "+v"(sb[3]), "+v"(sb[4]), "+v"(sb[5]), "+v"(sb[6]), "+v"(sb[7]) : "n"(N) : "memory")
; #define MD_END(last) do { if (last) asm volatile("s_waitcnt vmcnt(0)" ::: "memory"); else asm volatile("s_waitcnt vmcnt(8)" ::: "memory"); \
;         asm volatile("s_waitcnt lgkmcnt(0)" ::: "memory"); __builtin_amdgcn_s_barrier(); asm volatile("" ::: "memory"); } while (0)
; __device__ __forceinline__ void moe_down_stream(PG8_LAS unsigned char* lds, int e, int cb0, int slot0, int nv, const bf16_t* HIDp, const float* Wd, bf16_t* Y, const float* slot_w, const int* slot_dst) {
;     ...
;     for (int t = 0; t < NT; t += 2) {
;         if (t + 2 < NT) MD_B_WAIT(s1, 8); else MD_B_WAIT(s1, 0);
;         MD_B_WRITE(s1, 1); __builtin_amdgcn_sched_barrier(0); MD_GLDS_A(1, t + 1); __builtin_amdgcn_sched_barrier(0);
;         if (t + 3 < NT) MD_B_ISSUE(s1, t + 3);
;         MD_COMPUTE(0);
;         MD_END(t + 3 >= NT);
;         if (t + 2 < NT) { MD_B_WAIT(s0, 8); MD_B_WRITE(s0, 0); __builtin_amdgcn_sched_barrier(0); MD_GLDS_A(0, t + 2); __builtin_amdgcn_sched_barrier(0); }
;         if (t + 4 < NT) MD_B_ISSUE(s0, t + 4);
;         MD_COMPUTE(1);
;         MD_END(t + 4 >= NT);
	s_mov_b32 s49, s46
	s_mov_b32 s46, s47
	s_mov_b32 s47, s48
	s_mov_b32 s48, s49
	v_cvt_pk_bf16_f32 v172, v186, v188
	v_cvt_pk_bf16_f32 v173, v190, v192
	v_cvt_pk_bf16_f32 v174, v194, v196
	v_cvt_pk_bf16_f32 v175, v198, v200
	v_cvt_pk_bf16_f32 v176, v187, v189
	v_cvt_pk_bf16_f32 v177, v191, v193
	v_cvt_pk_bf16_f32 v178, v195, v197
	v_cvt_pk_bf16_f32 v179, v199, v201
	ds_write_b128 v95, v[172:175] offset:0
	ds_write_b128 v95, v[176:179] offset:128
	v_add_u32_e32 v91, s46, v135
	v_add_u32_e32 v93, s46, v137
	ds_read_b128 v[238:241], v139 offset:19456
	ds_read_b128 v[242:245], v139 offset:21504
	ds_read_b128 v[246:249], v139 offset:23552
	ds_read_b128 v[250:253], v139 offset:25600
	ds_read_b128 v[218:221], v91 offset:0
	ds_read_b128 v[222:225], v91 offset:2048
	ds_read_b128 v[226:229], v91 offset:4096
	ds_read_b128 v[230:233], v91 offset:6144
	ds_read_b128 v[234:237], v91 offset:8192
	s_add_i32 s49, s48, s74
	s_add_i32 s52, s52, 1
	s_and_b32 s54, s52, 7
	s_cmp_eq_u32 s54, 0
	s_cselect_b32 s54, s53, s32
	s_cselect_b32 s55, -1, 0
	s_add_u32 s30, s30, s54
	s_addc_u32 s31, s31, s55
	s_waitcnt lgkmcnt(0)
	v_mfma_f32_16x16x32_bf16 v[78:81], v[238:241], v[218:221], v[78:81]
	v_mfma_f32_16x16x32_bf16 v[74:77], v[242:245], v[218:221], v[74:77]
	v_mfma_f32_16x16x32_bf16 v[70:73], v[246:249], v[218:221], v[70:73]
	v_mfma_f32_16x16x32_bf16 v[66:69], v[250:253], v[218:221], v[66:69]
	ds_read_b128 v[218:221], v93 offset:0
	ds_read_b128 v[142:145], v141 offset:19456
	s_mov_b32 m0, s49
	s_nop 0
	global_load_lds_dwordx4 v88, s[30:31]
	v_mfma_f32_16x16x32_bf16 v[62:65], v[238:241], v[222:225], v[62:65]
	v_mfma_f32_16x16x32_bf16 v[58:61], v[242:245], v[222:225], v[58:61]
	v_mfma_f32_16x16x32_bf16 v[54:57], v[246:249], v[222:225], v[54:57]
	v_mfma_f32_16x16x32_bf16 v[50:53], v[250:253], v[222:225], v[50:53]
	ds_read_b128 v[222:225], v93 offset:2048
	ds_read_b128 v[146:149], v141 offset:21504
	s_add_i32 m0, s49, 0x2000
	s_nop 0
	global_load_lds_dwordx4 v90, s[30:31]
	v_mfma_f32_16x16x32_bf16 v[46:49], v[238:241], v[226:229], v[46:49]
	v_mfma_f32_16x16x32_bf16 v[42:45], v[242:245], v[226:229], v[42:45]
	v_mfma_f32_16x16x32_bf16 v[38:41], v[246:249], v[226:229], v[38:41]
	v_mfma_f32_16x16x32_bf16 v[34:37], v[250:253], v[226:229], v[34:37]
	ds_read_b128 v[226:229], v93 offset:4096
	ds_read_b128 v[156:159], v141 offset:23552
	s_add_i32 m0, s49, 0x4000
	s_nop 0
	global_load_lds_dwordx4 v92, s[30:31]
	v_mfma_f32_16x16x32_bf16 v[18:21], v[238:241], v[230:233], v[18:21]
	v_mfma_f32_16x16x32_bf16 v[22:25], v[242:245], v[230:233], v[22:25]
	v_mfma_f32_16x16x32_bf16 v[26:29], v[246:249], v[230:233], v[26:29]
	v_mfma_f32_16x16x32_bf16 v[30:33], v[250:253], v[230:233], v[30:33]
	ds_read_b128 v[230:233], v93 offset:6144
	ds_read_b128 v[160:163], v141 offset:25600
	s_add_i32 m0, s49, 0x6000
	s_nop 0
	global_load_lds_dwordx4 v94, s[30:31]
	v_mfma_f32_16x16x32_bf16 v[2:5], v[238:241], v[234:237], v[2:5]
	v_mfma_f32_16x16x32_bf16 v[6:9], v[242:245], v[234:237], v[6:9]
	v_mfma_f32_16x16x32_bf16 v[10:13], v[246:249], v[234:237], v[10:13]
	v_mfma_f32_16x16x32_bf16 v[14:17], v[250:253], v[234:237], v[14:17]
	ds_read_b128 v[234:237], v93 offset:8192
	s_add_i32 m0, s49, 0x8000
	s_nop 0
	global_load_lds_dwordx4 v96, s[30:31]
	s_waitcnt lgkmcnt(0)
	v_mfma_f32_16x16x32_bf16 v[78:81], v[142:145], v[218:221], v[78:81]
	v_mfma_f32_16x16x32_bf16 v[74:77], v[146:149], v[218:221], v[74:77]
	v_mfma_f32_16x16x32_bf16 v[70:73], v[156:159], v[218:221], v[70:73]
	v_mfma_f32_16x16x32_bf16 v[66:69], v[160:163], v[218:221], v[66:69]
	s_add_i32 s51, s51, 1
	s_and_b32 s54, s51, 7
	s_cmp_eq_u32 s54, 0
	s_cselect_b32 s44, s34, s35
	s_cselect_b32 s45, -1, 0
	v_lshl_add_u64 v[132:133], v[132:133], 0, s[44:45]
	global_load_dwordx2 v[186:187], v[132:133], off
	v_lshl_add_u64 v[180:181], v[132:133], 0, s[24:25]
	global_load_dwordx2 v[188:189], v[180:181], off
	v_mfma_f32_16x16x32_bf16 v[62:65], v[142:145], v[222:225], v[62:65]
	v_mfma_f32_16x16x32_bf16 v[58:61], v[146:149], v[222:225], v[58:61]
	v_mfma_f32_16x16x32_bf16 v[54:57], v[156:159], v[222:225], v[54:57]
	v_mfma_f32_16x16x32_bf16 v[50:53], v[160:163], v[222:225], v[50:53]
	v_lshl_add_u64 v[180:181], v[132:133], 0, s[26:27]
	global_load_dwordx2 v[190:191], v[180:181], off
	v_lshl_add_u64 v[180:181], v[132:133], 0, s[28:29]
	global_load_dwordx2 v[192:193], v[180:181], off
	v_mfma_f32_16x16x32_bf16 v[46:49], v[142:145], v[226:229], v[46:49]
	v_mfma_f32_16x16x32_bf16 v[42:45], v[146:149], v[226:229], v[42:45]
	v_mfma_f32_16x16x32_bf16 v[38:41], v[156:159], v[226:229], v[38:41]
	v_mfma_f32_16x16x32_bf16 v[34:37], v[160:163], v[226:229], v[34:37]
	v_lshl_add_u64 v[180:181], v[132:133], 0, s[36:37]
	global_load_dwordx2 v[194:195], v[180:181], off
	v_lshl_add_u64 v[180:181], v[132:133], 0, s[38:39]
	global_load_dwordx2 v[196:197], v[180:181], off
	v_mfma_f32_16x16x32_bf16 v[18:21], v[142:145], v[230:233], v[18:21]
	v_mfma_f32_16x16x32_bf16 v[22:25], v[146:149], v[230:233], v[22:25]
	v_mfma_f32_16x16x32_bf16 v[26:29], v[156:159], v[230:233], v[26:29]
	v_mfma_f32_16x16x32_bf16 v[30:33], v[160:163], v[230:233], v[30:33]
	v_lshl_add_u64 v[180:181], v[132:133], 0, s[40:41]
	global_load_dwordx2 v[198:199], v[180:181], off
	v_lshl_add_u64 v[180:181], v[132:133], 0, s[42:43]
	global_load_dwordx2 v[200:201], v[180:181], off
	v_mfma_f32_16x16x32_bf16 v[2:5], v[142:145], v[234:237], v[2:5]
	v_mfma_f32_16x16x32_bf16 v[6:9], v[146:149], v[234:237], v[6:9]
	v_mfma_f32_16x16x32_bf16 v[10:13], v[156:159], v[234:237], v[10:13]
	v_mfma_f32_16x16x32_bf16 v[14:17], v[160:163], v[234:237], v[14:17]
	s_waitcnt vmcnt(21)
	s_waitcnt lgkmcnt(0)
	s_barrier
; #define MD_GLDS_A(buf, tau) do { _Pragma("unroll") for (int i = 0; i < 5; ++i) if (amask & (1u << i)) \
;         __builtin_amdgcn_global_load_lds((const unsigned*)((const char*)HIDp + aoff[i] + (size_t)((tau) & 7) * 128), (PG8_LAS unsigned*)(MD_SA(buf) + wid * 1024 + i * 8192), 16, 0, 0); } while (0)
; #define MD_B_ISSUE(sb, tau) do { const char* kb_ = Bb + (size_t)((tau) >> 3) * 512 + (size_t)((tau) & 7) * (64 * (size_t)RB); _Pragma("unroll") for (int j = 0; j < 8; ++j) { const char* p_ = kb_ + (size_t)j * RB; \
;         asm volatile("global_load_dwordx2 %0, %1, off" : "=&v"(sb[j]) : "v"(p_) : "memory"); } } while (0)
; #define MD_B_WAIT(sb, N) asm volatile("s_waitcnt vmcnt(%8)" : "+v"(sb[0]), "+v"(sb[1]), "+v"(sb[2]), "+v"(sb[3]), "+v"(sb[4]), "+v"(sb[5]), "+v"(sb[6]), "+v"(sb[7]) : "n"(N) : "memory")
; #define MD_END(last) do { if (last) asm volatile("s_waitcnt vmcnt(0)" ::: "memory"); else asm volatile("s_waitcnt vmcnt(8)" ::: "memory"); \
;         asm volatile("s_waitcnt lgkmcnt(0)" ::: "memory"); __builtin_amdgcn_s_barrier(); asm volatile("" ::: "memory"); } while (0)
; __device__ __forceinline__ void moe_down_stream(PG8_LAS unsigned char* lds, int e, int cb0, int slot0, int nv, const bf16_t* HIDp, const float* Wd, bf16_t* Y, const float* slot_w, const int* slot_dst) {
;     ...
;     for (int t = 0; t < NT; t += 2) {
;         if (t + 2 < NT) MD_B_WAIT(s1, 8); else MD_B_WAIT(s1, 0);
;         MD_B_WRITE(s1, 1); __builtin_amdgcn_sched_barrier(0); MD_GLDS_A(1, t + 1); __builtin_amdgcn_sched_barrier(0);
;         if (t + 3 < NT) MD_B_ISSUE(s1, t + 3);
;         MD_COMPUTE(0);
;         MD_END(t + 3 >= NT);
;         if (t + 2 < NT) { MD_B_WAIT(s0, 8); MD_B_WRITE(s0, 0); __builtin_amdgcn_sched_barrier(0); MD_GLDS_A(0, t + 2); __builtin_amdgcn_sched_barrier(0); }
;         if (t + 4 < NT) MD_B_ISSUE(s0, t + 4);
;         MD_COMPUTE(1);
;         MD_END(t + 4 >= NT);
	s_mov_b32 s49, s46
	s_mov_b32 s46, s47
	s_mov_b32 s47, s48
	s_mov_b32 s48, s49
	v_cvt_pk_bf16_f32 v172, v202, v204
	v_cvt_pk_bf16_f32 v173, v206, v208
	v_cvt_pk_bf16_f32 v174, v210, v212
	v_cvt_pk_bf16_f32 v175, v214, v216
	v_cvt_pk_bf16_f32 v176, v203, v205
	v_cvt_pk_bf16_f32 v177, v207, v209
	v_cvt_pk_bf16_f32 v178, v211, v213
	v_cvt_pk_bf16_f32 v179, v215, v217
	ds_write_b128 v95, v[172:175] offset:19456
	ds_write_b128 v95, v[176:179] offset:19584
	v_add_u32_e32 v91, s46, v135
	v_add_u32_e32 v93, s46, v137
	ds_read_b128 v[238:241], v139 offset:0
	ds_read_b128 v[242:245], v139 offset:2048
	ds_read_b128 v[246:249], v139 offset:4096
	ds_read_b128 v[250:253], v139 offset:6144
	ds_read_b128 v[218:221], v91 offset:0
	ds_read_b128 v[222:225], v91 offset:2048
	ds_read_b128 v[226:229], v91 offset:4096
	ds_read_b128 v[230:233], v91 offset:6144
	ds_read_b128 v[234:237], v91 offset:8192
	s_add_i32 s49, s48, s74
	s_add_i32 s52, s52, 1
	s_and_b32 s54, s52, 7
	s_cmp_eq_u32 s54, 0
	s_cselect_b32 s54, s53, s32
	s_cselect_b32 s55, -1, 0
	s_add_u32 s30, s30, s54
	s_addc_u32 s31, s31, s55
	s_waitcnt lgkmcnt(0)
	v_mfma_f32_16x16x32_bf16 v[78:81], v[238:241], v[218:221], v[78:81]
	v_mfma_f32_16x16x32_bf16 v[74:77], v[242:245], v[218:221], v[74:77]
	v_mfma_f32_16x16x32_bf16 v[70:73], v[246:249], v[218:221], v[70:73]
	v_mfma_f32_16x16x32_bf16 v[66:69], v[250:253], v[218:221], v[66:69]
	ds_read_b128 v[218:221], v93 offset:0
	ds_read_b128 v[142:145], v141 offset:0
	s_mov_b32 m0, s49
	s_nop 0
	global_load_lds_dwordx4 v88, s[30:31]
	v_mfma_f32_16x16x32_bf16 v[62:65], v[238:241], v[222:225], v[62:65]
	v_mfma_f32_16x16x32_bf16 v[58:61], v[242:245], v[222:225], v[58:61]
	v_mfma_f32_16x16x32_bf16 v[54:57], v[246:249], v[222:225], v[54:57]
	v_mfma_f32_16x16x32_bf16 v[50:53], v[250:253], v[222:225], v[50:53]
	ds_read_b128 v[222:225], v93 offset:2048
	ds_read_b128 v[146:149], v141 offset:2048
	s_add_i32 m0, s49, 0x2000
	s_nop 0
	global_load_lds_dwordx4 v90, s[30:31]
	v_mfma_f32_16x16x32_bf16 v[46:49], v[238:241], v[226:229], v[46:49]
	v_mfma_f32_16x16x32_bf16 v[42:45], v[242:245], v[226:229], v[42:45]
	v_mfma_f32_16x16x32_bf16 v[38:41], v[246:249], v[226:229], v[38:41]
	v_mfma_f32_16x16x32_bf16 v[34:37], v[250:253], v[226:229], v[34:37]
	ds_read_b128 v[226:229], v93 offset:4096
	ds_read_b128 v[156:159], v141 offset:4096
	s_add_i32 m0, s49, 0x4000
	s_nop 0
	global_load_lds_dwordx4 v92, s[30:31]
	v_mfma_f32_16x16x32_bf16 v[18:21], v[238:241], v[230:233], v[18:21]
	v_mfma_f32_16x16x32_bf16 v[22:25], v[242:245], v[230:233], v[22:25]
	v_mfma_f32_16x16x32_bf16 v[26:29], v[246:249], v[230:233], v[26:29]
	v_mfma_f32_16x16x32_bf16 v[30:33], v[250:253], v[230:233], v[30:33]
	ds_read_b128 v[230:233], v93 offset:6144
	ds_read_b128 v[160:163], v141 offset:6144
	s_add_i32 m0, s49, 0x6000
	s_nop 0
	global_load_lds_dwordx4 v94, s[30:31]
	v_mfma_f32_16x16x32_bf16 v[2:5], v[238:241], v[234:237], v[2:5]
	v_mfma_f32_16x16x32_bf16 v[6:9], v[242:245], v[234:237], v[6:9]
	v_mfma_f32_16x16x32_bf16 v[10:13], v[246:249], v[234:237], v[10:13]
	v_mfma_f32_16x16x32_bf16 v[14:17], v[250:253], v[234:237], v[14:17]
	ds_read_b128 v[234:237], v93 offset:8192
	s_add_i32 m0, s49, 0x8000
	s_nop 0
	global_load_lds_dwordx4 v96, s[30:31]
	s_waitcnt lgkmcnt(0)
	v_mfma_f32_16x16x32_bf16 v[78:81], v[142:145], v[218:221], v[78:81]
	v_mfma_f32_16x16x32_bf16 v[74:77], v[146:149], v[218:221], v[74:77]
	v_mfma_f32_16x16x32_bf16 v[70:73], v[156:159], v[218:221], v[70:73]
	v_mfma_f32_16x16x32_bf16 v[66:69], v[160:163], v[218:221], v[66:69]
	s_add_i32 s51, s51, 1
	s_and_b32 s54, s51, 7
	s_cmp_eq_u32 s54, 0
	s_cselect_b32 s44, s34, s35
	s_cselect_b32 s45, -1, 0
	v_lshl_add_u64 v[132:133], v[132:133], 0, s[44:45]
	global_load_dwordx2 v[202:203], v[132:133], off
	v_lshl_add_u64 v[180:181], v[132:133], 0, s[24:25]
	global_load_dwordx2 v[204:205], v[180:181], off
	v_mfma_f32_16x16x32_bf16 v[62:65], v[142:145], v[222:225], v[62:65]
	v_mfma_f32_16x16x32_bf16 v[58:61], v[146:149], v[222:225], v[58:61]
	v_mfma_f32_16x16x32_bf16 v[54:57], v[156:159], v[222:225], v[54:57]
	v_mfma_f32_16x16x32_bf16 v[50:53], v[160:163], v[222:225], v[50:53]
	v_lshl_add_u64 v[180:181], v[132:133], 0, s[26:27]
	global_load_dwordx2 v[206:207], v[180:181], off
	v_lshl_add_u64 v[180:181], v[132:133], 0, s[28:29]
	global_load_dwordx2 v[208:209], v[180:181], off
	v_mfma_f32_16x16x32_bf16 v[46:49], v[142:145], v[226:229], v[46:49]
	v_mfma_f32_16x16x32_bf16 v[42:45], v[146:149], v[226:229], v[42:45]
	v_mfma_f32_16x16x32_bf16 v[38:41], v[156:159], v[226:229], v[38:41]
	v_mfma_f32_16x16x32_bf16 v[34:37], v[160:163], v[226:229], v[34:37]
	v_lshl_add_u64 v[180:181], v[132:133], 0, s[36:37]
	global_load_dwordx2 v[210:211], v[180:181], off
	v_lshl_add_u64 v[180:181], v[132:133], 0, s[38:39]
	global_load_dwordx2 v[212:213], v[180:181], off
	v_mfma_f32_16x16x32_bf16 v[18:21], v[142:145], v[230:233], v[18:21]
	v_mfma_f32_16x16x32_bf16 v[22:25], v[146:149], v[230:233], v[22:25]
	v_mfma_f32_16x16x32_bf16 v[26:29], v[156:159], v[230:233], v[26:29]
	v_mfma_f32_16x16x32_bf16 v[30:33], v[160:163], v[230:233], v[30:33]
	v_lshl_add_u64 v[180:181], v[132:133], 0, s[40:41]
	global_load_dwordx2 v[214:215], v[180:181], off
	v_lshl_add_u64 v[180:181], v[132:133], 0, s[42:43]
	global_load_dwordx2 v[216:217], v[180:181], off
	v_mfma_f32_16x16x32_bf16 v[2:5], v[142:145], v[234:237], v[2:5]
	v_mfma_f32_16x16x32_bf16 v[6:9], v[146:149], v[234:237], v[6:9]
	v_mfma_f32_16x16x32_bf16 v[10:13], v[156:159], v[234:237], v[10:13]
	v_mfma_f32_16x16x32_bf16 v[14:17], v[160:163], v[234:237], v[14:17]
	s_waitcnt vmcnt(21)
	s_waitcnt lgkmcnt(0)
	s_barrier
; #define MD_GLDS_A(buf, tau) do { _Pragma("unroll") for (int i = 0; i < 5; ++i) if (amask & (1u << i)) \
;         __builtin_amdgcn_global_load_lds((const unsigned*)((const char*)HIDp + aoff[i] + (size_t)((tau) & 7) * 128), (PG8_LAS unsigned*)(MD_SA(buf) + wid * 1024 + i * 8192), 16, 0, 0); } while (0)
; #define MD_B_ISSUE(sb, tau) do { const char* kb_ = Bb + (size_t)((tau) >> 3) * 512 + (size_t)((tau) & 7) * (64 * (size_t)RB); _Pragma("unroll") for (int j = 0; j < 8; ++j) { const char* p_ = kb_ + (size_t)j * RB; \
;         asm volatile("global_load_dwordx2 %0, %1, off" : "=&v"(sb[j]) : "v"(p_) : "memory"); } } while (0)
; #define MD_B_WAIT(sb, N) asm volatile("s_waitcnt vmcnt(%8)" : "+v"(sb[0]), "+v"(sb[1]), "+v"(sb[2]), "+v"(sb[3]), "+v"(sb[4]), "+v"(sb[5]), "+v"(sb[6]), "+v"(sb[7]) : "n"(N) : "memory")
; #define MD_END(last) do { if (last) asm volatile("s_waitcnt vmcnt(0)" ::: "memory"); else asm volatile("s_waitcnt vmcnt(8)" ::: "memory"); \
;         asm volatile("s_waitcnt lgkmcnt(0)" ::: "memory"); __builtin_amdgcn_s_barrier(); asm volatile("" ::: "memory"); } while (0)
; __device__ __forceinline__ void moe_down_stream(PG8_LAS unsigned char* lds, int e, int cb0, int slot0, int nv, const bf16_t* HIDp, const float* Wd, bf16_t* Y, const float* slot_w, const int* slot_dst) {
;     ...
;     for (int t = 0; t < NT; t += 2) {
;         if (t + 2 < NT) MD_B_WAIT(s1, 8); else MD_B_WAIT(s1, 0);
;         MD_B_WRITE(s1, 1); __builtin_amdgcn_sched_barrier(0); MD_GLDS_A(1, t + 1); __builtin_amdgcn_sched_barrier(0);
;         if (t + 3 < NT) MD_B_ISSUE(s1, t + 3);
;         MD_COMPUTE(0);
;         MD_END(t + 3 >= NT);
;         if (t + 2 < NT) { MD_B_WAIT(s0, 8); MD_B_WRITE(s0, 0); __builtin_amdgcn_sched_barrier(0); MD_GLDS_A(0, t + 2); __builtin_amdgcn_sched_barrier(0); }
;         if (t + 4 < NT) MD_B_ISSUE(s0, t + 4);
;         MD_COMPUTE(1);
;         MD_END(t + 4 >= NT);
	s_mov_b32 s49, s46
	s_mov_b32 s46, s47
	s_mov_b32 s47, s48
	s_mov_b32 s48, s49
	v_cvt_pk_bf16_f32 v172, v98, v100
	v_cvt_pk_bf16_f32 v173, v102, v104
	v_cvt_pk_bf16_f32 v174, v106, v108
	v_cvt_pk_bf16_f32 v175, v110, v112
	v_cvt_pk_bf16_f32 v176, v99, v101
	v_cvt_pk_bf16_f32 v177, v103, v105
	v_cvt_pk_bf16_f32 v178, v107, v109
	v_cvt_pk_bf16_f32 v179, v111, v113
	ds_write_b128 v95, v[172:175] offset:0
	ds_write_b128 v95, v[176:179] offset:128
	v_add_u32_e32 v91, s46, v135
	v_add_u32_e32 v93, s46, v137
	ds_read_b128 v[238:241], v139 offset:19456
	ds_read_b128 v[242:245], v139 offset:21504
	ds_read_b128 v[246:249], v139 offset:23552
	ds_read_b128 v[250:253], v139 offset:25600
	ds_read_b128 v[218:221], v91 offset:0
	ds_read_b128 v[222:225], v91 offset:2048
	ds_read_b128 v[226:229], v91 offset:4096
	ds_read_b128 v[230:233], v91 offset:6144
	ds_read_b128 v[234:237], v91 offset:8192
	s_add_i32 s49, s48, s74
	s_add_i32 s52, s52, 1
	s_and_b32 s54, s52, 7
	s_cmp_eq_u32 s54, 0
	s_cselect_b32 s54, s53, s32
	s_cselect_b32 s55, -1, 0
	s_add_u32 s30, s30, s54
	s_addc_u32 s31, s31, s55
	s_waitcnt lgkmcnt(0)
	v_mfma_f32_16x16x32_bf16 v[78:81], v[238:241], v[218:221], v[78:81]
	v_mfma_f32_16x16x32_bf16 v[74:77], v[242:245], v[218:221], v[74:77]
	v_mfma_f32_16x16x32_bf16 v[70:73], v[246:249], v[218:221], v[70:73]
	v_mfma_f32_16x16x32_bf16 v[66:69], v[250:253], v[218:221], v[66:69]
	ds_read_b128 v[218:221], v93 offset:0
	ds_read_b128 v[142:145], v141 offset:19456
	s_mov_b32 m0, s49
	s_nop 0
	global_load_lds_dwordx4 v88, s[30:31]
	v_mfma_f32_16x16x32_bf16 v[62:65], v[238:241], v[222:225], v[62:65]
	v_mfma_f32_16x16x32_bf16 v[58:61], v[242:245], v[222:225], v[58:61]
	v_mfma_f32_16x16x32_bf16 v[54:57], v[246:249], v[222:225], v[54:57]
	v_mfma_f32_16x16x32_bf16 v[50:53], v[250:253], v[222:225], v[50:53]
	ds_read_b128 v[222:225], v93 offset:2048
	ds_read_b128 v[146:149], v141 offset:21504
	s_add_i32 m0, s49, 0x2000
	s_nop 0
	global_load_lds_dwordx4 v90, s[30:31]
	v_mfma_f32_16x16x32_bf16 v[46:49], v[238:241], v[226:229], v[46:49]
	v_mfma_f32_16x16x32_bf16 v[42:45], v[242:245], v[226:229], v[42:45]
	v_mfma_f32_16x16x32_bf16 v[38:41], v[246:249], v[226:229], v[38:41]
	v_mfma_f32_16x16x32_bf16 v[34:37], v[250:253], v[226:229], v[34:37]
	ds_read_b128 v[226:229], v93 offset:4096
	ds_read_b128 v[156:159], v141 offset:23552
	s_add_i32 m0, s49, 0x4000
	s_nop 0
	global_load_lds_dwordx4 v92, s[30:31]
	v_mfma_f32_16x16x32_bf16 v[18:21], v[238:241], v[230:233], v[18:21]
	v_mfma_f32_16x16x32_bf16 v[22:25], v[242:245], v[230:233], v[22:25]
	v_mfma_f32_16x16x32_bf16 v[26:29], v[246:249], v[230:233], v[26:29]
	v_mfma_f32_16x16x32_bf16 v[30:33], v[250:253], v[230:233], v[30:33]
	ds_read_b128 v[230:233], v93 offset:6144
	ds_read_b128 v[160:163], v141 offset:25600
	s_add_i32 m0, s49, 0x6000
	s_nop 0
	global_load_lds_dwordx4 v94, s[30:31]
	v_mfma_f32_16x16x32_bf16 v[2:5], v[238:241], v[234:237], v[2:5]
	v_mfma_f32_16x16x32_bf16 v[6:9], v[242:245], v[234:237], v[6:9]
	v_mfma_f32_16x16x32_bf16 v[10:13], v[246:249], v[234:237], v[10:13]
	v_mfma_f32_16x16x32_bf16 v[14:17], v[250:253], v[234:237], v[14:17]
	ds_read_b128 v[234:237], v93 offset:8192
	s_add_i32 m0, s49, 0x8000
	s_nop 0
	global_load_lds_dwordx4 v96, s[30:31]
	s_waitcnt lgkmcnt(0)
	v_mfma_f32_16x16x32_bf16 v[78:81], v[142:145], v[218:221], v[78:81]
	v_mfma_f32_16x16x32_bf16 v[74:77], v[146:149], v[218:221], v[74:77]
	v_mfma_f32_16x16x32_bf16 v[70:73], v[156:159], v[218:221], v[70:73]
	v_mfma_f32_16x16x32_bf16 v[66:69], v[160:163], v[218:221], v[66:69]
	s_add_i32 s51, s51, 1
	s_and_b32 s54, s51, 7
	s_cmp_eq_u32 s54, 0
	s_cselect_b32 s44, s34, s35
	s_cselect_b32 s45, -1, 0
	v_lshl_add_u64 v[132:133], v[132:133], 0, s[44:45]
	global_load_dwordx2 v[98:99], v[132:133], off
	v_lshl_add_u64 v[180:181], v[132:133], 0, s[24:25]
	global_load_dwordx2 v[100:101], v[180:181], off
	v_mfma_f32_16x16x32_bf16 v[62:65], v[142:145], v[222:225], v[62:65]
	v_mfma_f32_16x16x32_bf16 v[58:61], v[146:149], v[222:225], v[58:61]
	v_mfma_f32_16x16x32_bf16 v[54:57], v[156:159], v[222:225], v[54:57]
	v_mfma_f32_16x16x32_bf16 v[50:53], v[160:163], v[222:225], v[50:53]
	v_lshl_add_u64 v[180:181], v[132:133], 0, s[26:27]
	global_load_dwordx2 v[102:103], v[180:181], off
	v_lshl_add_u64 v[180:181], v[132:133], 0, s[28:29]
	global_load_dwordx2 v[104:105], v[180:181], off
	v_mfma_f32_16x16x32_bf16 v[46:49], v[142:145], v[226:229], v[46:49]
	v_mfma_f32_16x16x32_bf16 v[42:45], v[146:149], v[226:229], v[42:45]
	v_mfma_f32_16x16x32_bf16 v[38:41], v[156:159], v[226:229], v[38:41]
	v_mfma_f32_16x16x32_bf16 v[34:37], v[160:163], v[226:229], v[34:37]
	v_lshl_add_u64 v[180:181], v[132:133], 0, s[36:37]
	global_load_dwordx2 v[106:107], v[180:181], off
	v_lshl_add_u64 v[180:181], v[132:133], 0, s[38:39]
	global_load_dwordx2 v[108:109], v[180:181], off
	v_mfma_f32_16x16x32_bf16 v[18:21], v[142:145], v[230:233], v[18:21]
	v_mfma_f32_16x16x32_bf16 v[22:25], v[146:149], v[230:233], v[22:25]
	v_mfma_f32_16x16x32_bf16 v[26:29], v[156:159], v[230:233], v[26:29]
	v_mfma_f32_16x16x32_bf16 v[30:33], v[160:163], v[230:233], v[30:33]
	v_lshl_add_u64 v[180:181], v[132:133], 0, s[40:41]
	global_load_dwordx2 v[110:111], v[180:181], off
	v_lshl_add_u64 v[180:181], v[132:133], 0, s[42:43]
	global_load_dwordx2 v[112:113], v[180:181], off
	v_mfma_f32_16x16x32_bf16 v[2:5], v[142:145], v[234:237], v[2:5]
	v_mfma_f32_16x16x32_bf16 v[6:9], v[146:149], v[234:237], v[6:9]
	v_mfma_f32_16x16x32_bf16 v[10:13], v[156:159], v[234:237], v[10:13]
	v_mfma_f32_16x16x32_bf16 v[14:17], v[160:163], v[234:237], v[14:17]
	s_waitcnt vmcnt(21)
	s_waitcnt lgkmcnt(0)
	s_barrier
; #define PG8_LAS __attribute__((address_space(3)))
; __device__ __forceinline__ unsigned cvtpk(float lo, float hi) { f32x2 v = {lo, hi}; bf16x2_t b = __builtin_convertvector(v, bf16x2_t); return __builtin_bit_cast(unsigned, b); }
; __device__ __forceinline__ void moe_down_stream(PG8_LAS unsigned char* lds, int e, int cb0, int slot0, int nv, const bf16_t* HIDp, const float* Wd, bf16_t* Y, const float* slot_w, const int* slot_dst) {
;     ...
;         if (((t + 1) & 7) == 7) {
;             const int cb = cb0 + ((t + 1) >> 3);
; #pragma unroll
;             for (int m = 0; m < DNM; ++m) {
;                 const float w_ = lw[4 * (16 * m + fr) + wr];
; #pragma unroll
;                 for (int p = 0; p < 2; ++p) { const f32x4 v0 = acc[m][2 * p] * w_, v1 = acc[m][2 * p + 1] * w_; u32x4 w; w.x = cvtpk(v0[0], v0[1]); w.y = cvtpk(v0[2], v0[3]); w.z = cvtpk(v1[0], v1[1]); w.w = cvtpk(v1[2], v1[3]);
;                     *(PG8_LAS u32x4*)(stg + fr * 128 + (((4 * p + fq) ^ (fr & 7)) * 16)) = w; }
; #pragma unroll
;                 for (int hh = 0; hh < 2; ++hh) { const int r = (lane >> 3) + 8 * hh, cc = lane & 7; const u32x4 d = *(const PG8_LAS u32x4*)(stg + r * 128 + ((cc ^ (r & 7)) * 16)); const int dst_ = ldst[4 * (16 * m + r) + wr];
;                     if (dst_ >= 0) *(u32x4*)(Y + (size_t)dst_ * D + 128 * cb + 64 * wc + 8 * cc) = d; }
; #pragma unroll
;                 for (int n = 0; n < 4; ++n) acc[m][n] = (f32x4){0.f, 0.f, 0.f, 0.f}; } }
	s_mov_b32 s49, s46
	s_mov_b32 s46, s47
	s_mov_b32 s47, s48
	s_mov_b32 s48, s49
	s_add_i32 s54, s48, s74
	v_add_u32_e32 v164, s54, v84
	v_add_u32_e32 v165, s54, v85
	ds_read_b32 v150, v82 offset:0
	ds_read_b32 v151, v83 offset:0
	ds_read_b32 v166, v83 offset:128
	s_waitcnt lgkmcnt(2)
	v_mul_f32_e32 v78, v150, v78
	v_mul_f32_e32 v79, v150, v79
	v_mul_f32_e32 v80, v150, v80
	v_mul_f32_e32 v81, v150, v81
	v_mul_f32_e32 v74, v150, v74
	v_mul_f32_e32 v75, v150, v75
	v_mul_f32_e32 v76, v150, v76
	v_mul_f32_e32 v77, v150, v77
	v_cvt_pk_bf16_f32 v182, v78, v79
	v_cvt_pk_bf16_f32 v183, v80, v81
	v_cvt_pk_bf16_f32 v184, v74, v75
	v_cvt_pk_bf16_f32 v185, v76, v77
	ds_write_b128 v164, v[182:185]
	v_mul_f32_e32 v70, v150, v70
	v_mul_f32_e32 v71, v150, v71
	v_mul_f32_e32 v72, v150, v72
	v_mul_f32_e32 v73, v150, v73
	v_mul_f32_e32 v66, v150, v66
	v_mul_f32_e32 v67, v150, v67
	v_mul_f32_e32 v68, v150, v68
	v_mul_f32_e32 v69, v150, v69
	v_cvt_pk_bf16_f32 v182, v70, v71
	v_cvt_pk_bf16_f32 v183, v72, v73
	v_cvt_pk_bf16_f32 v184, v66, v67
	v_cvt_pk_bf16_f32 v185, v68, v69
	v_xor_b32_e32 v167, 64, v164
	ds_write_b128 v167, v[182:185]
	v_mov_b32_e32 v78, 0
	v_mov_b32_e32 v74, 0
	v_mov_b32_e32 v70, 0
	v_mov_b32_e32 v66, 0
	v_mov_b32_e32 v79, 0
	v_mov_b32_e32 v75, 0
	v_mov_b32_e32 v71, 0
	v_mov_b32_e32 v67, 0
	v_mov_b32_e32 v80, 0
	v_mov_b32_e32 v76, 0
	v_mov_b32_e32 v72, 0
	v_mov_b32_e32 v68, 0
	v_mov_b32_e32 v81, 0
	v_mov_b32_e32 v77, 0
	v_mov_b32_e32 v73, 0
	v_mov_b32_e32 v69, 0
	ds_read_b128 v[182:185], v165 offset:0
	v_cmp_lt_i32_e32 vcc, -1, v151
	v_lshlrev_b32_e32 v148, 13, v151
	v_mov_b32_e32 v149, 0
	v_lshl_add_u64 v[148:149], v[148:149], 0, v[86:87]
	v_cndmask_b32_e32 v148, v168, v148, vcc
	v_cndmask_b32_e32 v149, v169, v149, vcc
	s_waitcnt lgkmcnt(0)
	global_store_dwordx4 v[148:149], v[182:185], off
	ds_read_b128 v[182:185], v165 offset:8192
	v_cmp_lt_i32_e32 vcc, -1, v166
	v_lshlrev_b32_e32 v148, 13, v166
	v_mov_b32_e32 v149, 0
	v_lshl_add_u64 v[148:149], v[148:149], 0, v[86:87]
	v_cndmask_b32_e32 v148, v168, v148, vcc
	v_cndmask_b32_e32 v149, v169, v149, vcc
	s_waitcnt lgkmcnt(0)
	global_store_dwordx4 v[148:149], v[182:185], off
	ds_read_b32 v150, v82 offset:256
	ds_read_b32 v151, v83 offset:256
	ds_read_b32 v166, v83 offset:384
	s_waitcnt lgkmcnt(2)
	v_mul_f32_e32 v62, v150, v62
	v_mul_f32_e32 v63, v150, v63
	v_mul_f32_e32 v64, v150, v64
	v_mul_f32_e32 v65, v150, v65
	v_mul_f32_e32 v58, v150, v58
	v_mul_f32_e32 v59, v150, v59
	v_mul_f32_e32 v60, v150, v60
	v_mul_f32_e32 v61, v150, v61
	v_cvt_pk_bf16_f32 v182, v62, v63
	v_cvt_pk_bf16_f32 v183, v64, v65
	v_cvt_pk_bf16_f32 v184, v58, v59
	v_cvt_pk_bf16_f32 v185, v60, v61
	ds_write_b128 v164, v[182:185]
	v_mul_f32_e32 v54, v150, v54
	v_mul_f32_e32 v55, v150, v55
	v_mul_f32_e32 v56, v150, v56
	v_mul_f32_e32 v57, v150, v57
	v_mul_f32_e32 v50, v150, v50
	v_mul_f32_e32 v51, v150, v51
	v_mul_f32_e32 v52, v150, v52
	v_mul_f32_e32 v53, v150, v53
	v_cvt_pk_bf16_f32 v182, v54, v55
	v_cvt_pk_bf16_f32 v183, v56, v57
	v_cvt_pk_bf16_f32 v184, v50, v51
	v_cvt_pk_bf16_f32 v185, v52, v53
	v_xor_b32_e32 v167, 64, v164
	ds_write_b128 v167, v[182:185]
	v_mov_b32_e32 v62, 0
	v_mov_b32_e32 v58, 0
	v_mov_b32_e32 v54, 0
	v_mov_b32_e32 v50, 0
	v_mov_b32_e32 v63, 0
	v_mov_b32_e32 v59, 0
	v_mov_b32_e32 v55, 0
	v_mov_b32_e32 v51, 0
	v_mov_b32_e32 v64, 0
	v_mov_b32_e32 v60, 0
	v_mov_b32_e32 v56, 0
	v_mov_b32_e32 v52, 0
	v_mov_b32_e32 v65, 0
	v_mov_b32_e32 v61, 0
	v_mov_b32_e32 v57, 0
	v_mov_b32_e32 v53, 0
	ds_read_b128 v[182:185], v165 offset:0
	v_cmp_lt_i32_e32 vcc, -1, v151
	v_lshlrev_b32_e32 v148, 13, v151
	v_mov_b32_e32 v149, 0
	v_lshl_add_u64 v[148:149], v[148:149], 0, v[86:87]
	v_cndmask_b32_e32 v148, v168, v148, vcc
	v_cndmask_b32_e32 v149, v169, v149, vcc
	s_waitcnt lgkmcnt(0)
	global_store_dwordx4 v[148:149], v[182:185], off
	ds_read_b128 v[182:185], v165 offset:8192
	v_cmp_lt_i32_e32 vcc, -1, v166
	v_lshlrev_b32_e32 v148, 13, v166
	v_mov_b32_e32 v149, 0
	v_lshl_add_u64 v[148:149], v[148:149], 0, v[86:87]
	v_cndmask_b32_e32 v148, v168, v148, vcc
	v_cndmask_b32_e32 v149, v169, v149, vcc
	s_waitcnt lgkmcnt(0)
	global_store_dwordx4 v[148:149], v[182:185], off
	ds_read_b32 v150, v82 offset:512
	ds_read_b32 v151, v83 offset:512
	ds_read_b32 v166, v83 offset:640
	s_waitcnt lgkmcnt(2)
	v_mul_f32_e32 v46, v150, v46
	v_mul_f32_e32 v47, v150, v47
	v_mul_f32_e32 v48, v150, v48
	v_mul_f32_e32 v49, v150, v49
	v_mul_f32_e32 v42, v150, v42
	v_mul_f32_e32 v43, v150, v43
	v_mul_f32_e32 v44, v150, v44
	v_mul_f32_e32 v45, v150, v45
	v_cvt_pk_bf16_f32 v182, v46, v47
	v_cvt_pk_bf16_f32 v183, v48, v49
	v_cvt_pk_bf16_f32 v184, v42, v43
	v_cvt_pk_bf16_f32 v185, v44, v45
	ds_write_b128 v164, v[182:185]
	v_mul_f32_e32 v38, v150, v38
	v_mul_f32_e32 v39, v150, v39
	v_mul_f32_e32 v40, v150, v40
	v_mul_f32_e32 v41, v150, v41
	v_mul_f32_e32 v34, v150, v34
	v_mul_f32_e32 v35, v150, v35
	v_mul_f32_e32 v36, v150, v36
	v_mul_f32_e32 v37, v150, v37
	v_cvt_pk_bf16_f32 v182, v38, v39
	v_cvt_pk_bf16_f32 v183, v40, v41
	v_cvt_pk_bf16_f32 v184, v34, v35
	v_cvt_pk_bf16_f32 v185, v36, v37
	v_xor_b32_e32 v167, 64, v164
	ds_write_b128 v167, v[182:185]
	v_mov_b32_e32 v46, 0
	v_mov_b32_e32 v42, 0
	v_mov_b32_e32 v38, 0
	v_mov_b32_e32 v34, 0
	v_mov_b32_e32 v47, 0
	v_mov_b32_e32 v43, 0
	v_mov_b32_e32 v39, 0
	v_mov_b32_e32 v35, 0
	v_mov_b32_e32 v48, 0
	v_mov_b32_e32 v44, 0
	v_mov_b32_e32 v40, 0
	v_mov_b32_e32 v36, 0
	v_mov_b32_e32 v49, 0
	v_mov_b32_e32 v45, 0
	v_mov_b32_e32 v41, 0
	v_mov_b32_e32 v37, 0
	ds_read_b128 v[182:185], v165 offset:0
	v_cmp_lt_i32_e32 vcc, -1, v151
	v_lshlrev_b32_e32 v148, 13, v151
	v_mov_b32_e32 v149, 0
	v_lshl_add_u64 v[148:149], v[148:149], 0, v[86:87]
	v_cndmask_b32_e32 v148, v168, v148, vcc
	v_cndmask_b32_e32 v149, v169, v149, vcc
	s_waitcnt lgkmcnt(0)
; #define PG8_LAS __attribute__((address_space(3)))
; __device__ __forceinline__ unsigned cvtpk(float lo, float hi) { f32x2 v = {lo, hi}; bf16x2_t b = __builtin_convertvector(v, bf16x2_t); return __builtin_bit_cast(unsigned, b); }
; #define MD_GLDS_A(buf, tau) do { _Pragma("unroll") for (int i = 0; i < 5; ++i) if (amask & (1u << i)) \
;         __builtin_amdgcn_global_load_lds((const unsigned*)((const char*)HIDp + aoff[i] + (size_t)((tau) & 7) * 128), (PG8_LAS unsigned*)(MD_SA(buf) + wid * 1024 + i * 8192), 16, 0, 0); } while (0)
; __device__ __forceinline__ void moe_down_stream(PG8_LAS unsigned char* lds, int e, int cb0, int slot0, int nv, const bf16_t* HIDp, const float* Wd, bf16_t* Y, const float* slot_w, const int* slot_dst) {
;     ...
;     for (int t = 0; t < NT; t += 2) {
;         if (t + 2 < NT) MD_B_WAIT(s1, 8); else MD_B_WAIT(s1, 0);
;         MD_B_WRITE(s1, 1); __builtin_amdgcn_sched_barrier(0); MD_GLDS_A(1, t + 1); __builtin_amdgcn_sched_barrier(0);
;         if (t + 3 < NT) MD_B_ISSUE(s1, t + 3);
;         MD_COMPUTE(0);
;         MD_END(t + 3 >= NT);
;         if (t + 2 < NT) { MD_B_WAIT(s0, 8); MD_B_WRITE(s0, 0); __builtin_amdgcn_sched_barrier(0); MD_GLDS_A(0, t + 2); __builtin_amdgcn_sched_barrier(0); }
;     ...
;         if (((t + 1) & 7) == 7) {
;             const int cb = cb0 + ((t + 1) >> 3);
; #pragma unroll
;             for (int m = 0; m < DNM; ++m) {
;                 const float w_ = lw[4 * (16 * m + fr) + wr];
; #pragma unroll
;                 for (int p = 0; p < 2; ++p) { const f32x4 v0 = acc[m][2 * p] * w_, v1 = acc[m][2 * p + 1] * w_; u32x4 w; w.x = cvtpk(v0[0], v0[1]); w.y = cvtpk(v0[2], v0[3]); w.z = cvtpk(v1[0], v1[1]); w.w = cvtpk(v1[2], v1[3]);
;                     *(PG8_LAS u32x4*)(stg + fr * 128 + (((4 * p + fq) ^ (fr & 7)) * 16)) = w; }
; #pragma unroll
;                 for (int hh = 0; hh < 2; ++hh) { const int r = (lane >> 3) + 8 * hh, cc = lane & 7; const u32x4 d = *(const PG8_LAS u32x4*)(stg + r * 128 + ((cc ^ (r & 7)) * 16)); const int dst_ = ldst[4 * (16 * m + r) + wr];
;                     if (dst_ >= 0) *(u32x4*)(Y + (size_t)dst_ * D + 128 * cb + 64 * wc + 8 * cc) = d; }
; #pragma unroll
;                 for (int n = 0; n < 4; ++n) acc[m][n] = (f32x4){0.f, 0.f, 0.f, 0.f}; } }
	global_store_dwordx4 v[148:149], v[182:185], off
	ds_read_b128 v[182:185], v165 offset:8192
	v_cmp_lt_i32_e32 vcc, -1, v166
	v_lshlrev_b32_e32 v148, 13, v166
	v_mov_b32_e32 v149, 0
	v_lshl_add_u64 v[148:149], v[148:149], 0, v[86:87]
	v_cndmask_b32_e32 v148, v168, v148, vcc
	v_cndmask_b32_e32 v149, v169, v149, vcc
	s_waitcnt lgkmcnt(0)
	global_store_dwordx4 v[148:149], v[182:185], off
	ds_read_b32 v150, v82 offset:768
	ds_read_b32 v151, v83 offset:768
	ds_read_b32 v166, v83 offset:896
	s_waitcnt lgkmcnt(2)
	v_mul_f32_e32 v18, v150, v18
	v_mul_f32_e32 v19, v150, v19
	v_mul_f32_e32 v20, v150, v20
	v_mul_f32_e32 v21, v150, v21
	v_mul_f32_e32 v22, v150, v22
	v_mul_f32_e32 v23, v150, v23
	v_mul_f32_e32 v24, v150, v24
	v_mul_f32_e32 v25, v150, v25
	v_cvt_pk_bf16_f32 v182, v18, v19
	v_cvt_pk_bf16_f32 v183, v20, v21
	v_cvt_pk_bf16_f32 v184, v22, v23
	v_cvt_pk_bf16_f32 v185, v24, v25
	ds_write_b128 v164, v[182:185]
	v_mul_f32_e32 v26, v150, v26
	v_mul_f32_e32 v27, v150, v27
	v_mul_f32_e32 v28, v150, v28
	v_mul_f32_e32 v29, v150, v29
	v_mul_f32_e32 v30, v150, v30
	v_mul_f32_e32 v31, v150, v31
	v_mul_f32_e32 v32, v150, v32
	v_mul_f32_e32 v33, v150, v33
	v_cvt_pk_bf16_f32 v182, v26, v27
	v_cvt_pk_bf16_f32 v183, v28, v29
	v_cvt_pk_bf16_f32 v184, v30, v31
	v_cvt_pk_bf16_f32 v185, v32, v33
	v_xor_b32_e32 v167, 64, v164
	ds_write_b128 v167, v[182:185]
	v_mov_b32_e32 v18, 0
	v_mov_b32_e32 v22, 0
	v_mov_b32_e32 v26, 0
	v_mov_b32_e32 v30, 0
	v_mov_b32_e32 v19, 0
	v_mov_b32_e32 v23, 0
	v_mov_b32_e32 v27, 0
	v_mov_b32_e32 v31, 0
	v_mov_b32_e32 v20, 0
	v_mov_b32_e32 v24, 0
	v_mov_b32_e32 v28, 0
	v_mov_b32_e32 v32, 0
	v_mov_b32_e32 v21, 0
	v_mov_b32_e32 v25, 0
	v_mov_b32_e32 v29, 0
	v_mov_b32_e32 v33, 0
	ds_read_b128 v[182:185], v165 offset:0
	v_cmp_lt_i32_e32 vcc, -1, v151
	v_lshlrev_b32_e32 v148, 13, v151
	v_mov_b32_e32 v149, 0
	v_lshl_add_u64 v[148:149], v[148:149], 0, v[86:87]
	v_cndmask_b32_e32 v148, v168, v148, vcc
	v_cndmask_b32_e32 v149, v169, v149, vcc
	s_waitcnt lgkmcnt(0)
	global_store_dwordx4 v[148:149], v[182:185], off
	ds_read_b128 v[182:185], v165 offset:8192
	v_cmp_lt_i32_e32 vcc, -1, v166
	v_lshlrev_b32_e32 v148, 13, v166
	v_mov_b32_e32 v149, 0
	v_lshl_add_u64 v[148:149], v[148:149], 0, v[86:87]
	v_cndmask_b32_e32 v148, v168, v148, vcc
	v_cndmask_b32_e32 v149, v169, v149, vcc
	s_waitcnt lgkmcnt(0)
	global_store_dwordx4 v[148:149], v[182:185], off
	ds_read_b32 v150, v82 offset:1024
	ds_read_b32 v151, v83 offset:1024
	ds_read_b32 v166, v83 offset:1152
	s_waitcnt lgkmcnt(2)
	v_mul_f32_e32 v2, v150, v2
	v_mul_f32_e32 v3, v150, v3
	v_mul_f32_e32 v4, v150, v4
	v_mul_f32_e32 v5, v150, v5
	v_mul_f32_e32 v6, v150, v6
	v_mul_f32_e32 v7, v150, v7
	v_mul_f32_e32 v8, v150, v8
	v_mul_f32_e32 v9, v150, v9
	v_cvt_pk_bf16_f32 v182, v2, v3
	v_cvt_pk_bf16_f32 v183, v4, v5
	v_cvt_pk_bf16_f32 v184, v6, v7
	v_cvt_pk_bf16_f32 v185, v8, v9
	ds_write_b128 v164, v[182:185]
	v_mul_f32_e32 v10, v150, v10
	v_mul_f32_e32 v11, v150, v11
	v_mul_f32_e32 v12, v150, v12
	v_mul_f32_e32 v13, v150, v13
	v_mul_f32_e32 v14, v150, v14
	v_mul_f32_e32 v15, v150, v15
	v_mul_f32_e32 v16, v150, v16
	v_mul_f32_e32 v17, v150, v17
	v_cvt_pk_bf16_f32 v182, v10, v11
	v_cvt_pk_bf16_f32 v183, v12, v13
	v_cvt_pk_bf16_f32 v184, v14, v15
	v_cvt_pk_bf16_f32 v185, v16, v17
	v_xor_b32_e32 v167, 64, v164
	ds_write_b128 v167, v[182:185]
	v_mov_b32_e32 v2, 0
	v_mov_b32_e32 v6, 0
	v_mov_b32_e32 v10, 0
	v_mov_b32_e32 v14, 0
	v_mov_b32_e32 v3, 0
	v_mov_b32_e32 v7, 0
	v_mov_b32_e32 v11, 0
	v_mov_b32_e32 v15, 0
	v_mov_b32_e32 v4, 0
	v_mov_b32_e32 v8, 0
	v_mov_b32_e32 v12, 0
	v_mov_b32_e32 v16, 0
	v_mov_b32_e32 v5, 0
	v_mov_b32_e32 v9, 0
	v_mov_b32_e32 v13, 0
	v_mov_b32_e32 v17, 0
	ds_read_b128 v[182:185], v165 offset:0
	v_cmp_lt_i32_e32 vcc, -1, v151
	v_lshlrev_b32_e32 v148, 13, v151
	v_mov_b32_e32 v149, 0
	v_lshl_add_u64 v[148:149], v[148:149], 0, v[86:87]
	v_cndmask_b32_e32 v148, v168, v148, vcc
	v_cndmask_b32_e32 v149, v169, v149, vcc
	s_waitcnt lgkmcnt(0)
	global_store_dwordx4 v[148:149], v[182:185], off
	ds_read_b128 v[182:185], v165 offset:8192
	v_cmp_lt_i32_e32 vcc, -1, v166
	v_lshlrev_b32_e32 v148, 13, v166
	v_mov_b32_e32 v149, 0
	v_lshl_add_u64 v[148:149], v[148:149], 0, v[86:87]
	v_cndmask_b32_e32 v148, v168, v148, vcc
	v_cndmask_b32_e32 v149, v169, v149, vcc
	s_waitcnt lgkmcnt(0)
	global_store_dwordx4 v[148:149], v[182:185], off
	v_add_co_u32_e32 v86, vcc, 0x800, v86
	s_nop 1
	v_addc_co_u32_e32 v87, vcc, 0, v87, vcc
	s_waitcnt lgkmcnt(0)
	v_cvt_pk_bf16_f32 v172, v114, v116
	v_cvt_pk_bf16_f32 v173, v118, v120
	v_cvt_pk_bf16_f32 v174, v122, v124
	v_cvt_pk_bf16_f32 v175, v126, v128
	v_cvt_pk_bf16_f32 v176, v115, v117
	v_cvt_pk_bf16_f32 v177, v119, v121
	v_cvt_pk_bf16_f32 v178, v123, v125
	v_cvt_pk_bf16_f32 v179, v127, v129
	ds_write_b128 v95, v[172:175] offset:19456
	ds_write_b128 v95, v[176:179] offset:19584
	v_add_u32_e32 v91, s46, v135
	v_add_u32_e32 v93, s46, v137
	ds_read_b128 v[238:241], v139 offset:0
	ds_read_b128 v[242:245], v139 offset:2048
	ds_read_b128 v[246:249], v139 offset:4096
	ds_read_b128 v[250:253], v139 offset:6144
	ds_read_b128 v[218:221], v91 offset:0
	ds_read_b128 v[222:225], v91 offset:2048
	ds_read_b128 v[226:229], v91 offset:4096
	ds_read_b128 v[230:233], v91 offset:6144
	ds_read_b128 v[234:237], v91 offset:8192
	s_add_i32 s49, s48, s74
	s_add_i32 s52, s52, 1
	s_and_b32 s54, s52, 7
	s_cmp_eq_u32 s54, 0
	s_cselect_b32 s54, s53, s32
	s_cselect_b32 s55, -1, 0
	s_add_u32 s30, s30, s54
	s_addc_u32 s31, s31, s55
	s_waitcnt lgkmcnt(0)
; #define MD_GLDS_A(buf, tau) do { _Pragma("unroll") for (int i = 0; i < 5; ++i) if (amask & (1u << i)) \
;         __builtin_amdgcn_global_load_lds((const unsigned*)((const char*)HIDp + aoff[i] + (size_t)((tau) & 7) * 128), (PG8_LAS unsigned*)(MD_SA(buf) + wid * 1024 + i * 8192), 16, 0, 0); } while (0)
; #define MD_B_ISSUE(sb, tau) do { const char* kb_ = Bb + (size_t)((tau) >> 3) * 512 + (size_t)((tau) & 7) * (64 * (size_t)RB); _Pragma("unroll") for (int j = 0; j < 8; ++j) { const char* p_ = kb_ + (size_t)j * RB; \
;         asm volatile("global_load_dwordx2 %0, %1, off" : "=&v"(sb[j]) : "v"(p_) : "memory"); } } while (0)
; #define MD_B_WAIT(sb, N) asm volatile("s_waitcnt vmcnt(%8)" : "+v"(sb[0]), "+v"(sb[1]), "+v"(sb[2]), "+v"(sb[3]), "+v"(sb[4]), "+v"(sb[5]), "+v"(sb[6]), "+v"(sb[7]) : "n"(N) : "memory")
; #define MD_END(last) do { if (last) asm volatile("s_waitcnt vmcnt(0)" ::: "memory"); else asm volatile("s_waitcnt vmcnt(8)" ::: "memory"); \
;         asm volatile("s_waitcnt lgkmcnt(0)" ::: "memory"); __builtin_amdgcn_s_barrier(); asm volatile("" ::: "memory"); } while (0)
; __device__ __forceinline__ void moe_down_stream(PG8_LAS unsigned char* lds, int e, int cb0, int slot0, int nv, const bf16_t* HIDp, const float* Wd, bf16_t* Y, const float* slot_w, const int* slot_dst) {
;     ...
;         if (t + 3 < NT) MD_B_ISSUE(s1, t + 3);
;         MD_COMPUTE(0);
;         MD_END(t + 3 >= NT);
;         if (t + 2 < NT) { MD_B_WAIT(s0, 8); MD_B_WRITE(s0, 0); __builtin_amdgcn_sched_barrier(0); MD_GLDS_A(0, t + 2); __builtin_amdgcn_sched_barrier(0); }
;         if (t + 4 < NT) MD_B_ISSUE(s0, t + 4);
;         MD_COMPUTE(1);
;         MD_END(t + 4 >= NT);
	v_mfma_f32_16x16x32_bf16 v[78:81], v[238:241], v[218:221], v[78:81]
	v_mfma_f32_16x16x32_bf16 v[74:77], v[242:245], v[218:221], v[74:77]
	v_mfma_f32_16x16x32_bf16 v[70:73], v[246:249], v[218:221], v[70:73]
	v_mfma_f32_16x16x32_bf16 v[66:69], v[250:253], v[218:221], v[66:69]
	ds_read_b128 v[218:221], v93 offset:0
	ds_read_b128 v[142:145], v141 offset:0
	s_mov_b32 m0, s49
	s_nop 0
	global_load_lds_dwordx4 v88, s[30:31]
	v_mfma_f32_16x16x32_bf16 v[62:65], v[238:241], v[222:225], v[62:65]
	v_mfma_f32_16x16x32_bf16 v[58:61], v[242:245], v[222:225], v[58:61]
	v_mfma_f32_16x16x32_bf16 v[54:57], v[246:249], v[222:225], v[54:57]
	v_mfma_f32_16x16x32_bf16 v[50:53], v[250:253], v[222:225], v[50:53]
	ds_read_b128 v[222:225], v93 offset:2048
	ds_read_b128 v[146:149], v141 offset:2048
	s_add_i32 m0, s49, 0x2000
	s_nop 0
	global_load_lds_dwordx4 v90, s[30:31]
	v_mfma_f32_16x16x32_bf16 v[46:49], v[238:241], v[226:229], v[46:49]
	v_mfma_f32_16x16x32_bf16 v[42:45], v[242:245], v[226:229], v[42:45]
	v_mfma_f32_16x16x32_bf16 v[38:41], v[246:249], v[226:229], v[38:41]
	v_mfma_f32_16x16x32_bf16 v[34:37], v[250:253], v[226:229], v[34:37]
	ds_read_b128 v[226:229], v93 offset:4096
	ds_read_b128 v[156:159], v141 offset:4096
	s_add_i32 m0, s49, 0x4000
	s_nop 0
	global_load_lds_dwordx4 v92, s[30:31]
	v_mfma_f32_16x16x32_bf16 v[18:21], v[238:241], v[230:233], v[18:21]
	v_mfma_f32_16x16x32_bf16 v[22:25], v[242:245], v[230:233], v[22:25]
	v_mfma_f32_16x16x32_bf16 v[26:29], v[246:249], v[230:233], v[26:29]
	v_mfma_f32_16x16x32_bf16 v[30:33], v[250:253], v[230:233], v[30:33]
	ds_read_b128 v[230:233], v93 offset:6144
	ds_read_b128 v[160:163], v141 offset:6144
	s_add_i32 m0, s49, 0x6000
	s_nop 0
	global_load_lds_dwordx4 v94, s[30:31]
	v_mfma_f32_16x16x32_bf16 v[2:5], v[238:241], v[234:237], v[2:5]
	v_mfma_f32_16x16x32_bf16 v[6:9], v[242:245], v[234:237], v[6:9]
	v_mfma_f32_16x16x32_bf16 v[10:13], v[246:249], v[234:237], v[10:13]
	v_mfma_f32_16x16x32_bf16 v[14:17], v[250:253], v[234:237], v[14:17]
	ds_read_b128 v[234:237], v93 offset:8192
	s_add_i32 m0, s49, 0x8000
	s_nop 0
	global_load_lds_dwordx4 v96, s[30:31]
	s_waitcnt lgkmcnt(0)
	v_mfma_f32_16x16x32_bf16 v[78:81], v[142:145], v[218:221], v[78:81]
	v_mfma_f32_16x16x32_bf16 v[74:77], v[146:149], v[218:221], v[74:77]
	v_mfma_f32_16x16x32_bf16 v[70:73], v[156:159], v[218:221], v[70:73]
	v_mfma_f32_16x16x32_bf16 v[66:69], v[160:163], v[218:221], v[66:69]
	s_add_i32 s51, s51, 1
	s_and_b32 s54, s51, 7
	s_cmp_eq_u32 s54, 0
	s_cselect_b32 s44, s34, s35
	s_cselect_b32 s45, -1, 0
	v_lshl_add_u64 v[132:133], v[132:133], 0, s[44:45]
	global_load_dwordx2 v[114:115], v[132:133], off
	v_lshl_add_u64 v[180:181], v[132:133], 0, s[24:25]
	global_load_dwordx2 v[116:117], v[180:181], off
	v_mfma_f32_16x16x32_bf16 v[62:65], v[142:145], v[222:225], v[62:65]
	v_mfma_f32_16x16x32_bf16 v[58:61], v[146:149], v[222:225], v[58:61]
	v_mfma_f32_16x16x32_bf16 v[54:57], v[156:159], v[222:225], v[54:57]
	v_mfma_f32_16x16x32_bf16 v[50:53], v[160:163], v[222:225], v[50:53]
	v_lshl_add_u64 v[180:181], v[132:133], 0, s[26:27]
	global_load_dwordx2 v[118:119], v[180:181], off
	v_lshl_add_u64 v[180:181], v[132:133], 0, s[28:29]
	global_load_dwordx2 v[120:121], v[180:181], off
	v_mfma_f32_16x16x32_bf16 v[46:49], v[142:145], v[226:229], v[46:49]
	v_mfma_f32_16x16x32_bf16 v[42:45], v[146:149], v[226:229], v[42:45]
	v_mfma_f32_16x16x32_bf16 v[38:41], v[156:159], v[226:229], v[38:41]
	v_mfma_f32_16x16x32_bf16 v[34:37], v[160:163], v[226:229], v[34:37]
	v_lshl_add_u64 v[180:181], v[132:133], 0, s[36:37]
	global_load_dwordx2 v[122:123], v[180:181], off
	v_lshl_add_u64 v[180:181], v[132:133], 0, s[38:39]
	global_load_dwordx2 v[124:125], v[180:181], off
	v_mfma_f32_16x16x32_bf16 v[18:21], v[142:145], v[230:233], v[18:21]
	v_mfma_f32_16x16x32_bf16 v[22:25], v[146:149], v[230:233], v[22:25]
	v_mfma_f32_16x16x32_bf16 v[26:29], v[156:159], v[230:233], v[26:29]
	v_mfma_f32_16x16x32_bf16 v[30:33], v[160:163], v[230:233], v[30:33]
	v_lshl_add_u64 v[180:181], v[132:133], 0, s[40:41]
	global_load_dwordx2 v[126:127], v[180:181], off
	v_lshl_add_u64 v[180:181], v[132:133], 0, s[42:43]
	global_load_dwordx2 v[128:129], v[180:181], off
	v_mfma_f32_16x16x32_bf16 v[2:5], v[142:145], v[234:237], v[2:5]
	v_mfma_f32_16x16x32_bf16 v[6:9], v[146:149], v[234:237], v[6:9]
	v_mfma_f32_16x16x32_bf16 v[10:13], v[156:159], v[234:237], v[10:13]
	v_mfma_f32_16x16x32_bf16 v[14:17], v[160:163], v[234:237], v[14:17]
	s_waitcnt vmcnt(31)
	s_waitcnt lgkmcnt(0)
	s_barrier
; #define MD_GLDS_A(buf, tau) do { _Pragma("unroll") for (int i = 0; i < 5; ++i) if (amask & (1u << i)) \
;         __builtin_amdgcn_global_load_lds((const unsigned*)((const char*)HIDp + aoff[i] + (size_t)((tau) & 7) * 128), (PG8_LAS unsigned*)(MD_SA(buf) + wid * 1024 + i * 8192), 16, 0, 0); } while (0)
; #define MD_B_ISSUE(sb, tau) do { const char* kb_ = Bb + (size_t)((tau) >> 3) * 512 + (size_t)((tau) & 7) * (64 * (size_t)RB); _Pragma("unroll") for (int j = 0; j < 8; ++j) { const char* p_ = kb_ + (size_t)j * RB; \
;         asm volatile("global_load_dwordx2 %0, %1, off" : "=&v"(sb[j]) : "v"(p_) : "memory"); } } while (0)
; #define MD_B_WAIT(sb, N) asm volatile("s_waitcnt vmcnt(%8)" : "+v"(sb[0]), "+v"(sb[1]), "+v"(sb[2]), "+v"(sb[3]), "+v"(sb[4]), "+v"(sb[5]), "+v"(sb[6]), "+v"(sb[7]) : "n"(N) : "memory")
; #define MD_END(last) do { if (last) asm volatile("s_waitcnt vmcnt(0)" ::: "memory"); else asm volatile("s_waitcnt vmcnt(8)" ::: "memory"); \
;         asm volatile("s_waitcnt lgkmcnt(0)" ::: "memory"); __builtin_amdgcn_s_barrier(); asm volatile("" ::: "memory"); } while (0)
; __device__ __forceinline__ void moe_down_stream(PG8_LAS unsigned char* lds, int e, int cb0, int slot0, int nv, const bf16_t* HIDp, const float* Wd, bf16_t* Y, const float* slot_w, const int* slot_dst) {
;     ...
;     for (int t = 0; t < NT; t += 2) {
;         if (t + 2 < NT) MD_B_WAIT(s1, 8); else MD_B_WAIT(s1, 0);
;         MD_B_WRITE(s1, 1); __builtin_amdgcn_sched_barrier(0); MD_GLDS_A(1, t + 1); __builtin_amdgcn_sched_barrier(0);
;         if (t + 3 < NT) MD_B_ISSUE(s1, t + 3);
;         MD_COMPUTE(0);
;         MD_END(t + 3 >= NT);
;         if (t + 2 < NT) { MD_B_WAIT(s0, 8); MD_B_WRITE(s0, 0); __builtin_amdgcn_sched_barrier(0); MD_GLDS_A(0, t + 2); __builtin_amdgcn_sched_barrier(0); }
;         if (t + 4 < NT) MD_B_ISSUE(s0, t + 4);
;         MD_COMPUTE(1);
;         MD_END(t + 4 >= NT);
	s_mov_b32 s49, s46
	s_mov_b32 s46, s47
	s_mov_b32 s47, s48
	s_mov_b32 s48, s49
	v_cvt_pk_bf16_f32 v172, v186, v188
	v_cvt_pk_bf16_f32 v173, v190, v192
	v_cvt_pk_bf16_f32 v174, v194, v196
	v_cvt_pk_bf16_f32 v175, v198, v200
	v_cvt_pk_bf16_f32 v176, v187, v189
	v_cvt_pk_bf16_f32 v177, v191, v193
	v_cvt_pk_bf16_f32 v178, v195, v197
	v_cvt_pk_bf16_f32 v179, v199, v201
	ds_write_b128 v95, v[172:175] offset:0
	ds_write_b128 v95, v[176:179] offset:128
	v_add_u32_e32 v91, s46, v135
	v_add_u32_e32 v93, s46, v137
	ds_read_b128 v[238:241], v139 offset:19456
	ds_read_b128 v[242:245], v139 offset:21504
	ds_read_b128 v[246:249], v139 offset:23552
	ds_read_b128 v[250:253], v139 offset:25600
	ds_read_b128 v[218:221], v91 offset:0
	ds_read_b128 v[222:225], v91 offset:2048
	ds_read_b128 v[226:229], v91 offset:4096
	ds_read_b128 v[230:233], v91 offset:6144
	ds_read_b128 v[234:237], v91 offset:8192
	s_add_i32 s49, s48, s74
	s_add_i32 s52, s52, 1
	s_and_b32 s54, s52, 7
	s_cmp_eq_u32 s54, 0
	s_cselect_b32 s54, s53, s32
	s_cselect_b32 s55, -1, 0
	s_add_u32 s30, s30, s54
	s_addc_u32 s31, s31, s55
	s_waitcnt lgkmcnt(0)
	v_mfma_f32_16x16x32_bf16 v[78:81], v[238:241], v[218:221], v[78:81]
	v_mfma_f32_16x16x32_bf16 v[74:77], v[242:245], v[218:221], v[74:77]
	v_mfma_f32_16x16x32_bf16 v[70:73], v[246:249], v[218:221], v[70:73]
	v_mfma_f32_16x16x32_bf16 v[66:69], v[250:253], v[218:221], v[66:69]
	ds_read_b128 v[218:221], v93 offset:0
	ds_read_b128 v[142:145], v141 offset:19456
	s_mov_b32 m0, s49
	s_nop 0
	global_load_lds_dwordx4 v88, s[30:31]
	v_mfma_f32_16x16x32_bf16 v[62:65], v[238:241], v[222:225], v[62:65]
	v_mfma_f32_16x16x32_bf16 v[58:61], v[242:245], v[222:225], v[58:61]
	v_mfma_f32_16x16x32_bf16 v[54:57], v[246:249], v[222:225], v[54:57]
	v_mfma_f32_16x16x32_bf16 v[50:53], v[250:253], v[222:225], v[50:53]
	ds_read_b128 v[222:225], v93 offset:2048
	ds_read_b128 v[146:149], v141 offset:21504
	s_add_i32 m0, s49, 0x2000
	s_nop 0
	global_load_lds_dwordx4 v90, s[30:31]
	v_mfma_f32_16x16x32_bf16 v[46:49], v[238:241], v[226:229], v[46:49]
	v_mfma_f32_16x16x32_bf16 v[42:45], v[242:245], v[226:229], v[42:45]
	v_mfma_f32_16x16x32_bf16 v[38:41], v[246:249], v[226:229], v[38:41]
	v_mfma_f32_16x16x32_bf16 v[34:37], v[250:253], v[226:229], v[34:37]
	ds_read_b128 v[226:229], v93 offset:4096
	ds_read_b128 v[156:159], v141 offset:23552
	s_add_i32 m0, s49, 0x4000
	s_nop 0
	global_load_lds_dwordx4 v92, s[30:31]
	v_mfma_f32_16x16x32_bf16 v[18:21], v[238:241], v[230:233], v[18:21]
	v_mfma_f32_16x16x32_bf16 v[22:25], v[242:245], v[230:233], v[22:25]
	v_mfma_f32_16x16x32_bf16 v[26:29], v[246:249], v[230:233], v[26:29]
	v_mfma_f32_16x16x32_bf16 v[30:33], v[250:253], v[230:233], v[30:33]
	ds_read_b128 v[230:233], v93 offset:6144
	ds_read_b128 v[160:163], v141 offset:25600
	s_add_i32 m0, s49, 0x6000
	s_nop 0
	global_load_lds_dwordx4 v94, s[30:31]
	v_mfma_f32_16x16x32_bf16 v[2:5], v[238:241], v[234:237], v[2:5]
	v_mfma_f32_16x16x32_bf16 v[6:9], v[242:245], v[234:237], v[6:9]
	v_mfma_f32_16x16x32_bf16 v[10:13], v[246:249], v[234:237], v[10:13]
	v_mfma_f32_16x16x32_bf16 v[14:17], v[250:253], v[234:237], v[14:17]
	ds_read_b128 v[234:237], v93 offset:8192
	s_add_i32 m0, s49, 0x8000
	s_nop 0
	global_load_lds_dwordx4 v96, s[30:31]
	s_waitcnt lgkmcnt(0)
	v_mfma_f32_16x16x32_bf16 v[78:81], v[142:145], v[218:221], v[78:81]
	v_mfma_f32_16x16x32_bf16 v[74:77], v[146:149], v[218:221], v[74:77]
	v_mfma_f32_16x16x32_bf16 v[70:73], v[156:159], v[218:221], v[70:73]
	v_mfma_f32_16x16x32_bf16 v[66:69], v[160:163], v[218:221], v[66:69]
	s_add_i32 s51, s51, 1
	s_and_b32 s54, s51, 7
	s_cmp_eq_u32 s54, 0
	s_cselect_b32 s44, s34, s35
	s_cselect_b32 s45, -1, 0
	v_lshl_add_u64 v[132:133], v[132:133], 0, s[44:45]
	global_load_dwordx2 v[186:187], v[132:133], off
	v_lshl_add_u64 v[180:181], v[132:133], 0, s[24:25]
	global_load_dwordx2 v[188:189], v[180:181], off
	v_mfma_f32_16x16x32_bf16 v[62:65], v[142:145], v[222:225], v[62:65]
	v_mfma_f32_16x16x32_bf16 v[58:61], v[146:149], v[222:225], v[58:61]
	v_mfma_f32_16x16x32_bf16 v[54:57], v[156:159], v[222:225], v[54:57]
	v_mfma_f32_16x16x32_bf16 v[50:53], v[160:163], v[222:225], v[50:53]
	v_lshl_add_u64 v[180:181], v[132:133], 0, s[26:27]
	global_load_dwordx2 v[190:191], v[180:181], off
	v_lshl_add_u64 v[180:181], v[132:133], 0, s[28:29]
	global_load_dwordx2 v[192:193], v[180:181], off
	v_mfma_f32_16x16x32_bf16 v[46:49], v[142:145], v[226:229], v[46:49]
	v_mfma_f32_16x16x32_bf16 v[42:45], v[146:149], v[226:229], v[42:45]
	v_mfma_f32_16x16x32_bf16 v[38:41], v[156:159], v[226:229], v[38:41]
	v_mfma_f32_16x16x32_bf16 v[34:37], v[160:163], v[226:229], v[34:37]
	v_lshl_add_u64 v[180:181], v[132:133], 0, s[36:37]
	global_load_dwordx2 v[194:195], v[180:181], off
	v_lshl_add_u64 v[180:181], v[132:133], 0, s[38:39]
	global_load_dwordx2 v[196:197], v[180:181], off
	v_mfma_f32_16x16x32_bf16 v[18:21], v[142:145], v[230:233], v[18:21]
	v_mfma_f32_16x16x32_bf16 v[22:25], v[146:149], v[230:233], v[22:25]
	v_mfma_f32_16x16x32_bf16 v[26:29], v[156:159], v[230:233], v[26:29]
	v_mfma_f32_16x16x32_bf16 v[30:33], v[160:163], v[230:233], v[30:33]
	v_lshl_add_u64 v[180:181], v[132:133], 0, s[40:41]
	global_load_dwordx2 v[198:199], v[180:181], off
	v_lshl_add_u64 v[180:181], v[132:133], 0, s[42:43]
	global_load_dwordx2 v[200:201], v[180:181], off
	v_mfma_f32_16x16x32_bf16 v[2:5], v[142:145], v[234:237], v[2:5]
	v_mfma_f32_16x16x32_bf16 v[6:9], v[146:149], v[234:237], v[6:9]
	v_mfma_f32_16x16x32_bf16 v[10:13], v[156:159], v[234:237], v[10:13]
	v_mfma_f32_16x16x32_bf16 v[14:17], v[160:163], v[234:237], v[14:17]
	s_waitcnt vmcnt(21)
	s_waitcnt lgkmcnt(0)
	s_barrier
; #define MD_GLDS_A(buf, tau) do { _Pragma("unroll") for (int i = 0; i < 5; ++i) if (amask & (1u << i)) \
;         __builtin_amdgcn_global_load_lds((const unsigned*)((const char*)HIDp + aoff[i] + (size_t)((tau) & 7) * 128), (PG8_LAS unsigned*)(MD_SA(buf) + wid * 1024 + i * 8192), 16, 0, 0); } while (0)
; #define MD_B_ISSUE(sb, tau) do { const char* kb_ = Bb + (size_t)((tau) >> 3) * 512 + (size_t)((tau) & 7) * (64 * (size_t)RB); _Pragma("unroll") for (int j = 0; j < 8; ++j) { const char* p_ = kb_ + (size_t)j * RB; \
;         asm volatile("global_load_dwordx2 %0, %1, off" : "=&v"(sb[j]) : "v"(p_) : "memory"); } } while (0)
; #define MD_B_WAIT(sb, N) asm volatile("s_waitcnt vmcnt(%8)" : "+v"(sb[0]), "+v"(sb[1]), "+v"(sb[2]), "+v"(sb[3]), "+v"(sb[4]), "+v"(sb[5]), "+v"(sb[6]), "+v"(sb[7]) : "n"(N) : "memory")
; #define MD_END(last) do { if (last) asm volatile("s_waitcnt vmcnt(0)" ::: "memory"); else asm volatile("s_waitcnt vmcnt(8)" ::: "memory"); \
;         asm volatile("s_waitcnt lgkmcnt(0)" ::: "memory"); __builtin_amdgcn_s_barrier(); asm volatile("" ::: "memory"); } while (0)
; __device__ __forceinline__ void moe_down_stream(PG8_LAS unsigned char* lds, int e, int cb0, int slot0, int nv, const bf16_t* HIDp, const float* Wd, bf16_t* Y, const float* slot_w, const int* slot_dst) {
;     ...
;     for (int t = 0; t < NT; t += 2) {
;         if (t + 2 < NT) MD_B_WAIT(s1, 8); else MD_B_WAIT(s1, 0);
;         MD_B_WRITE(s1, 1); __builtin_amdgcn_sched_barrier(0); MD_GLDS_A(1, t + 1); __builtin_amdgcn_sched_barrier(0);
;         if (t + 3 < NT) MD_B_ISSUE(s1, t + 3);
;         MD_COMPUTE(0);
;         MD_END(t + 3 >= NT);
;         if (t + 2 < NT) { MD_B_WAIT(s0, 8); MD_B_WRITE(s0, 0); __builtin_amdgcn_sched_barrier(0); MD_GLDS_A(0, t + 2); __builtin_amdgcn_sched_barrier(0); }
;         if (t + 4 < NT) MD_B_ISSUE(s0, t + 4);
;         MD_COMPUTE(1);
;         MD_END(t + 4 >= NT);
	s_mov_b32 s49, s46
	s_mov_b32 s46, s47
	s_mov_b32 s47, s48
	s_mov_b32 s48, s49
	v_cvt_pk_bf16_f32 v172, v202, v204
	v_cvt_pk_bf16_f32 v173, v206, v208
	v_cvt_pk_bf16_f32 v174, v210, v212
	v_cvt_pk_bf16_f32 v175, v214, v216
	v_cvt_pk_bf16_f32 v176, v203, v205
	v_cvt_pk_bf16_f32 v177, v207, v209
	v_cvt_pk_bf16_f32 v178, v211, v213
	v_cvt_pk_bf16_f32 v179, v215, v217
	ds_write_b128 v95, v[172:175] offset:19456
	ds_write_b128 v95, v[176:179] offset:19584
	v_add_u32_e32 v91, s46, v135
	v_add_u32_e32 v93, s46, v137
	ds_read_b128 v[238:241], v139 offset:0
	ds_read_b128 v[242:245], v139 offset:2048
	ds_read_b128 v[246:249], v139 offset:4096
	ds_read_b128 v[250:253], v139 offset:6144
	ds_read_b128 v[218:221], v91 offset:0
	ds_read_b128 v[222:225], v91 offset:2048
	ds_read_b128 v[226:229], v91 offset:4096
	ds_read_b128 v[230:233], v91 offset:6144
	ds_read_b128 v[234:237], v91 offset:8192
	s_add_i32 s49, s48, s74
	s_add_i32 s52, s52, 1
	s_and_b32 s54, s52, 7
	s_cmp_eq_u32 s54, 0
	s_cselect_b32 s54, s53, s32
	s_cselect_b32 s55, -1, 0
	s_add_u32 s30, s30, s54
	s_addc_u32 s31, s31, s55
	s_waitcnt lgkmcnt(0)
	v_mfma_f32_16x16x32_bf16 v[78:81], v[238:241], v[218:221], v[78:81]
	v_mfma_f32_16x16x32_bf16 v[74:77], v[242:245], v[218:221], v[74:77]
	v_mfma_f32_16x16x32_bf16 v[70:73], v[246:249], v[218:221], v[70:73]
	v_mfma_f32_16x16x32_bf16 v[66:69], v[250:253], v[218:221], v[66:69]
	ds_read_b128 v[218:221], v93 offset:0
	ds_read_b128 v[142:145], v141 offset:0
	s_mov_b32 m0, s49
	s_nop 0
	global_load_lds_dwordx4 v88, s[30:31]
	v_mfma_f32_16x16x32_bf16 v[62:65], v[238:241], v[222:225], v[62:65]
	v_mfma_f32_16x16x32_bf16 v[58:61], v[242:245], v[222:225], v[58:61]
	v_mfma_f32_16x16x32_bf16 v[54:57], v[246:249], v[222:225], v[54:57]
	v_mfma_f32_16x16x32_bf16 v[50:53], v[250:253], v[222:225], v[50:53]
	ds_read_b128 v[222:225], v93 offset:2048
	ds_read_b128 v[146:149], v141 offset:2048
	s_add_i32 m0, s49, 0x2000
	s_nop 0
	global_load_lds_dwordx4 v90, s[30:31]
	v_mfma_f32_16x16x32_bf16 v[46:49], v[238:241], v[226:229], v[46:49]
	v_mfma_f32_16x16x32_bf16 v[42:45], v[242:245], v[226:229], v[42:45]
	v_mfma_f32_16x16x32_bf16 v[38:41], v[246:249], v[226:229], v[38:41]
	v_mfma_f32_16x16x32_bf16 v[34:37], v[250:253], v[226:229], v[34:37]
	ds_read_b128 v[226:229], v93 offset:4096
	ds_read_b128 v[156:159], v141 offset:4096
	s_add_i32 m0, s49, 0x4000
	s_nop 0
	global_load_lds_dwordx4 v92, s[30:31]
	v_mfma_f32_16x16x32_bf16 v[18:21], v[238:241], v[230:233], v[18:21]
	v_mfma_f32_16x16x32_bf16 v[22:25], v[242:245], v[230:233], v[22:25]
	v_mfma_f32_16x16x32_bf16 v[26:29], v[246:249], v[230:233], v[26:29]
	v_mfma_f32_16x16x32_bf16 v[30:33], v[250:253], v[230:233], v[30:33]
	ds_read_b128 v[230:233], v93 offset:6144
	ds_read_b128 v[160:163], v141 offset:6144
	s_add_i32 m0, s49, 0x6000
	s_nop 0
	global_load_lds_dwordx4 v94, s[30:31]
	v_mfma_f32_16x16x32_bf16 v[2:5], v[238:241], v[234:237], v[2:5]
	v_mfma_f32_16x16x32_bf16 v[6:9], v[242:245], v[234:237], v[6:9]
	v_mfma_f32_16x16x32_bf16 v[10:13], v[246:249], v[234:237], v[10:13]
	v_mfma_f32_16x16x32_bf16 v[14:17], v[250:253], v[234:237], v[14:17]
	ds_read_b128 v[234:237], v93 offset:8192
	s_add_i32 m0, s49, 0x8000
	s_nop 0
	global_load_lds_dwordx4 v96, s[30:31]
	s_waitcnt lgkmcnt(0)
	v_mfma_f32_16x16x32_bf16 v[78:81], v[142:145], v[218:221], v[78:81]
	v_mfma_f32_16x16x32_bf16 v[74:77], v[146:149], v[218:221], v[74:77]
	v_mfma_f32_16x16x32_bf16 v[70:73], v[156:159], v[218:221], v[70:73]
	v_mfma_f32_16x16x32_bf16 v[66:69], v[160:163], v[218:221], v[66:69]
	s_add_i32 s51, s51, 1
	s_and_b32 s54, s51, 7
	s_cmp_eq_u32 s54, 0
	s_cselect_b32 s44, s34, s35
	s_cselect_b32 s45, -1, 0
	v_lshl_add_u64 v[132:133], v[132:133], 0, s[44:45]
	global_load_dwordx2 v[202:203], v[132:133], off
	v_lshl_add_u64 v[180:181], v[132:133], 0, s[24:25]
	global_load_dwordx2 v[204:205], v[180:181], off
	v_mfma_f32_16x16x32_bf16 v[62:65], v[142:145], v[222:225], v[62:65]
	v_mfma_f32_16x16x32_bf16 v[58:61], v[146:149], v[222:225], v[58:61]
	v_mfma_f32_16x16x32_bf16 v[54:57], v[156:159], v[222:225], v[54:57]
	v_mfma_f32_16x16x32_bf16 v[50:53], v[160:163], v[222:225], v[50:53]
	v_lshl_add_u64 v[180:181], v[132:133], 0, s[26:27]
	global_load_dwordx2 v[206:207], v[180:181], off
	v_lshl_add_u64 v[180:181], v[132:133], 0, s[28:29]
	global_load_dwordx2 v[208:209], v[180:181], off
	v_mfma_f32_16x16x32_bf16 v[46:49], v[142:145], v[226:229], v[46:49]
	v_mfma_f32_16x16x32_bf16 v[42:45], v[146:149], v[226:229], v[42:45]
	v_mfma_f32_16x16x32_bf16 v[38:41], v[156:159], v[226:229], v[38:41]
	v_mfma_f32_16x16x32_bf16 v[34:37], v[160:163], v[226:229], v[34:37]
	v_lshl_add_u64 v[180:181], v[132:133], 0, s[36:37]
	global_load_dwordx2 v[210:211], v[180:181], off
	v_lshl_add_u64 v[180:181], v[132:133], 0, s[38:39]
	global_load_dwordx2 v[212:213], v[180:181], off
	v_mfma_f32_16x16x32_bf16 v[18:21], v[142:145], v[230:233], v[18:21]
	v_mfma_f32_16x16x32_bf16 v[22:25], v[146:149], v[230:233], v[22:25]
	v_mfma_f32_16x16x32_bf16 v[26:29], v[156:159], v[230:233], v[26:29]
	v_mfma_f32_16x16x32_bf16 v[30:33], v[160:163], v[230:233], v[30:33]
	v_lshl_add_u64 v[180:181], v[132:133], 0, s[40:41]
	global_load_dwordx2 v[214:215], v[180:181], off
	v_lshl_add_u64 v[180:181], v[132:133], 0, s[42:43]
	global_load_dwordx2 v[216:217], v[180:181], off
	v_mfma_f32_16x16x32_bf16 v[2:5], v[142:145], v[234:237], v[2:5]
	v_mfma_f32_16x16x32_bf16 v[6:9], v[146:149], v[234:237], v[6:9]
	v_mfma_f32_16x16x32_bf16 v[10:13], v[156:159], v[234:237], v[10:13]
	v_mfma_f32_16x16x32_bf16 v[14:17], v[160:163], v[234:237], v[14:17]
	s_waitcnt vmcnt(21)
	s_waitcnt lgkmcnt(0)
	s_barrier
; #define MD_GLDS_A(buf, tau) do { _Pragma("unroll") for (int i = 0; i < 5; ++i) if (amask & (1u << i)) \
;         __builtin_amdgcn_global_load_lds((const unsigned*)((const char*)HIDp + aoff[i] + (size_t)((tau) & 7) * 128), (PG8_LAS unsigned*)(MD_SA(buf) + wid * 1024 + i * 8192), 16, 0, 0); } while (0)
; #define MD_B_ISSUE(sb, tau) do { const char* kb_ = Bb + (size_t)((tau) >> 3) * 512 + (size_t)((tau) & 7) * (64 * (size_t)RB); _Pragma("unroll") for (int j = 0; j < 8; ++j) { const char* p_ = kb_ + (size_t)j * RB; \
;         asm volatile("global_load_dwordx2 %0, %1, off" : "=&v"(sb[j]) : "v"(p_) : "memory"); } } while (0)
; #define MD_B_WAIT(sb, N) asm volatile("s_waitcnt vmcnt(%8)" : "+v"(sb[0]), "+v"(sb[1]), "+v"(sb[2]), "+v"(sb[3]), "+v"(sb[4]), "+v"(sb[5]), "+v"(sb[6]), "+v"(sb[7]) : "n"(N) : "memory")
; #define MD_END(last) do { if (last) asm volatile("s_waitcnt vmcnt(0)" ::: "memory"); else asm volatile("s_waitcnt vmcnt(8)" ::: "memory"); \
;         asm volatile("s_waitcnt lgkmcnt(0)" ::: "memory"); __builtin_amdgcn_s_barrier(); asm volatile("" ::: "memory"); } while (0)
; __device__ __forceinline__ void moe_down_stream(PG8_LAS unsigned char* lds, int e, int cb0, int slot0, int nv, const bf16_t* HIDp, const float* Wd, bf16_t* Y, const float* slot_w, const int* slot_dst) {
;     ...
;     for (int t = 0; t < NT; t += 2) {
;         if (t + 2 < NT) MD_B_WAIT(s1, 8); else MD_B_WAIT(s1, 0);
;         MD_B_WRITE(s1, 1); __builtin_amdgcn_sched_barrier(0); MD_GLDS_A(1, t + 1); __builtin_amdgcn_sched_barrier(0);
;         if (t + 3 < NT) MD_B_ISSUE(s1, t + 3);
;         MD_COMPUTE(0);
;         MD_END(t + 3 >= NT);
;         if (t + 2 < NT) { MD_B_WAIT(s0, 8); MD_B_WRITE(s0, 0); __builtin_amdgcn_sched_barrier(0); MD_GLDS_A(0, t + 2); __builtin_amdgcn_sched_barrier(0); }
;         if (t + 4 < NT) MD_B_ISSUE(s0, t + 4);
;         MD_COMPUTE(1);
;         MD_END(t + 4 >= NT);
	s_mov_b32 s49, s46
	s_mov_b32 s46, s47
	s_mov_b32 s47, s48
	s_mov_b32 s48, s49
	v_cvt_pk_bf16_f32 v172, v98, v100
	v_cvt_pk_bf16_f32 v173, v102, v104
	v_cvt_pk_bf16_f32 v174, v106, v108
	v_cvt_pk_bf16_f32 v175, v110, v112
	v_cvt_pk_bf16_f32 v176, v99, v101
	v_cvt_pk_bf16_f32 v177, v103, v105
	v_cvt_pk_bf16_f32 v178, v107, v109
	v_cvt_pk_bf16_f32 v179, v111, v113
	ds_write_b128 v95, v[172:175] offset:0
	ds_write_b128 v95, v[176:179] offset:128
	v_add_u32_e32 v91, s46, v135
	v_add_u32_e32 v93, s46, v137
	ds_read_b128 v[238:241], v139 offset:19456
	ds_read_b128 v[242:245], v139 offset:21504
	ds_read_b128 v[246:249], v139 offset:23552
	ds_read_b128 v[250:253], v139 offset:25600
	ds_read_b128 v[218:221], v91 offset:0
	ds_read_b128 v[222:225], v91 offset:2048
	ds_read_b128 v[226:229], v91 offset:4096
	ds_read_b128 v[230:233], v91 offset:6144
	ds_read_b128 v[234:237], v91 offset:8192
	s_add_i32 s49, s48, s74
	s_add_i32 s52, s52, 1
	s_and_b32 s54, s52, 7
	s_cmp_eq_u32 s54, 0
	s_cselect_b32 s54, s53, s32
	s_cselect_b32 s55, -1, 0
	s_add_u32 s30, s30, s54
	s_addc_u32 s31, s31, s55
	s_waitcnt lgkmcnt(0)
	v_mfma_f32_16x16x32_bf16 v[78:81], v[238:241], v[218:221], v[78:81]
	v_mfma_f32_16x16x32_bf16 v[74:77], v[242:245], v[218:221], v[74:77]
	v_mfma_f32_16x16x32_bf16 v[70:73], v[246:249], v[218:221], v[70:73]
	v_mfma_f32_16x16x32_bf16 v[66:69], v[250:253], v[218:221], v[66:69]
	ds_read_b128 v[218:221], v93 offset:0
	ds_read_b128 v[142:145], v141 offset:19456
	s_mov_b32 m0, s49
	s_nop 0
	global_load_lds_dwordx4 v88, s[30:31]
	v_mfma_f32_16x16x32_bf16 v[62:65], v[238:241], v[222:225], v[62:65]
	v_mfma_f32_16x16x32_bf16 v[58:61], v[242:245], v[222:225], v[58:61]
	v_mfma_f32_16x16x32_bf16 v[54:57], v[246:249], v[222:225], v[54:57]
	v_mfma_f32_16x16x32_bf16 v[50:53], v[250:253], v[222:225], v[50:53]
	ds_read_b128 v[222:225], v93 offset:2048
	ds_read_b128 v[146:149], v141 offset:21504
	s_add_i32 m0, s49, 0x2000
	s_nop 0
	global_load_lds_dwordx4 v90, s[30:31]
	v_mfma_f32_16x16x32_bf16 v[46:49], v[238:241], v[226:229], v[46:49]
	v_mfma_f32_16x16x32_bf16 v[42:45], v[242:245], v[226:229], v[42:45]
	v_mfma_f32_16x16x32_bf16 v[38:41], v[246:249], v[226:229], v[38:41]
	v_mfma_f32_16x16x32_bf16 v[34:37], v[250:253], v[226:229], v[34:37]
	ds_read_b128 v[226:229], v93 offset:4096
	ds_read_b128 v[156:159], v141 offset:23552
	s_add_i32 m0, s49, 0x4000
	s_nop 0
	global_load_lds_dwordx4 v92, s[30:31]
	v_mfma_f32_16x16x32_bf16 v[18:21], v[238:241], v[230:233], v[18:21]
	v_mfma_f32_16x16x32_bf16 v[22:25], v[242:245], v[230:233], v[22:25]
	v_mfma_f32_16x16x32_bf16 v[26:29], v[246:249], v[230:233], v[26:29]
	v_mfma_f32_16x16x32_bf16 v[30:33], v[250:253], v[230:233], v[30:33]
	ds_read_b128 v[230:233], v93 offset:6144
	ds_read_b128 v[160:163], v141 offset:25600
	s_add_i32 m0, s49, 0x6000
	s_nop 0
	global_load_lds_dwordx4 v94, s[30:31]
	v_mfma_f32_16x16x32_bf16 v[2:5], v[238:241], v[234:237], v[2:5]
	v_mfma_f32_16x16x32_bf16 v[6:9], v[242:245], v[234:237], v[6:9]
	v_mfma_f32_16x16x32_bf16 v[10:13], v[246:249], v[234:237], v[10:13]
	v_mfma_f32_16x16x32_bf16 v[14:17], v[250:253], v[234:237], v[14:17]
	ds_read_b128 v[234:237], v93 offset:8192
	s_add_i32 m0, s49, 0x8000
	s_nop 0
	global_load_lds_dwordx4 v96, s[30:31]
	s_waitcnt lgkmcnt(0)
	v_mfma_f32_16x16x32_bf16 v[78:81], v[142:145], v[218:221], v[78:81]
	v_mfma_f32_16x16x32_bf16 v[74:77], v[146:149], v[218:221], v[74:77]
	v_mfma_f32_16x16x32_bf16 v[70:73], v[156:159], v[218:221], v[70:73]
	v_mfma_f32_16x16x32_bf16 v[66:69], v[160:163], v[218:221], v[66:69]
	s_add_i32 s51, s51, 1
	s_and_b32 s54, s51, 7
	s_cmp_eq_u32 s54, 0
	s_cselect_b32 s44, s34, s35
	s_cselect_b32 s45, -1, 0
	v_lshl_add_u64 v[132:133], v[132:133], 0, s[44:45]
	global_load_dwordx2 v[98:99], v[132:133], off
	v_lshl_add_u64 v[180:181], v[132:133], 0, s[24:25]
	global_load_dwordx2 v[100:101], v[180:181], off
	v_mfma_f32_16x16x32_bf16 v[62:65], v[142:145], v[222:225], v[62:65]
	v_mfma_f32_16x16x32_bf16 v[58:61], v[146:149], v[222:225], v[58:61]
	v_mfma_f32_16x16x32_bf16 v[54:57], v[156:159], v[222:225], v[54:57]
	v_mfma_f32_16x16x32_bf16 v[50:53], v[160:163], v[222:225], v[50:53]
	v_lshl_add_u64 v[180:181], v[132:133], 0, s[26:27]
	global_load_dwordx2 v[102:103], v[180:181], off
	v_lshl_add_u64 v[180:181], v[132:133], 0, s[28:29]
	global_load_dwordx2 v[104:105], v[180:181], off
	v_mfma_f32_16x16x32_bf16 v[46:49], v[142:145], v[226:229], v[46:49]
	v_mfma_f32_16x16x32_bf16 v[42:45], v[146:149], v[226:229], v[42:45]
	v_mfma_f32_16x16x32_bf16 v[38:41], v[156:159], v[226:229], v[38:41]
	v_mfma_f32_16x16x32_bf16 v[34:37], v[160:163], v[226:229], v[34:37]
	v_lshl_add_u64 v[180:181], v[132:133], 0, s[36:37]
	global_load_dwordx2 v[106:107], v[180:181], off
	v_lshl_add_u64 v[180:181], v[132:133], 0, s[38:39]
	global_load_dwordx2 v[108:109], v[180:181], off
	v_mfma_f32_16x16x32_bf16 v[18:21], v[142:145], v[230:233], v[18:21]
	v_mfma_f32_16x16x32_bf16 v[22:25], v[146:149], v[230:233], v[22:25]
	v_mfma_f32_16x16x32_bf16 v[26:29], v[156:159], v[230:233], v[26:29]
	v_mfma_f32_16x16x32_bf16 v[30:33], v[160:163], v[230:233], v[30:33]
	v_lshl_add_u64 v[180:181], v[132:133], 0, s[40:41]
	global_load_dwordx2 v[110:111], v[180:181], off
	v_lshl_add_u64 v[180:181], v[132:133], 0, s[42:43]
	global_load_dwordx2 v[112:113], v[180:181], off
	v_mfma_f32_16x16x32_bf16 v[2:5], v[142:145], v[234:237], v[2:5]
	v_mfma_f32_16x16x32_bf16 v[6:9], v[146:149], v[234:237], v[6:9]
	v_mfma_f32_16x16x32_bf16 v[10:13], v[156:159], v[234:237], v[10:13]
	v_mfma_f32_16x16x32_bf16 v[14:17], v[160:163], v[234:237], v[14:17]
	s_waitcnt vmcnt(21)
	s_waitcnt lgkmcnt(0)
	s_barrier
; #define MD_GLDS_A(buf, tau) do { _Pragma("unroll") for (int i = 0; i < 5; ++i) if (amask & (1u << i)) \
;         __builtin_amdgcn_global_load_lds((const unsigned*)((const char*)HIDp + aoff[i] + (size_t)((tau) & 7) * 128), (PG8_LAS unsigned*)(MD_SA(buf) + wid * 1024 + i * 8192), 16, 0, 0); } while (0)
; #define MD_B_ISSUE(sb, tau) do { const char* kb_ = Bb + (size_t)((tau) >> 3) * 512 + (size_t)((tau) & 7) * (64 * (size_t)RB); _Pragma("unroll") for (int j = 0; j < 8; ++j) { const char* p_ = kb_ + (size_t)j * RB; \
;         asm volatile("global_load_dwordx2 %0, %1, off" : "=&v"(sb[j]) : "v"(p_) : "memory"); } } while (0)
; #define MD_B_WAIT(sb, N) asm volatile("s_waitcnt vmcnt(%8)" : "+v"(sb[0]), "+v"(sb[1]), "+v"(sb[2]), "+v"(sb[3]), "+v"(sb[4]), "+v"(sb[5]), "+v"(sb[6]), "+v"(sb[7]) : "n"(N) : "memory")
; #define MD_END(last) do { if (last) asm volatile("s_waitcnt vmcnt(0)" ::: "memory"); else asm volatile("s_waitcnt vmcnt(8)" ::: "memory"); \
;         asm volatile("s_waitcnt lgkmcnt(0)" ::: "memory"); __builtin_amdgcn_s_barrier(); asm volatile("" ::: "memory"); } while (0)
; __device__ __forceinline__ void moe_down_stream(PG8_LAS unsigned char* lds, int e, int cb0, int slot0, int nv, const bf16_t* HIDp, const float* Wd, bf16_t* Y, const float* slot_w, const int* slot_dst) {
;     ...
;     for (int t = 0; t < NT; t += 2) {
;         if (t + 2 < NT) MD_B_WAIT(s1, 8); else MD_B_WAIT(s1, 0);
;         MD_B_WRITE(s1, 1); __builtin_amdgcn_sched_barrier(0); MD_GLDS_A(1, t + 1); __builtin_amdgcn_sched_barrier(0);
;         if (t + 3 < NT) MD_B_ISSUE(s1, t + 3);
;         MD_COMPUTE(0);
;         MD_END(t + 3 >= NT);
;         if (t + 2 < NT) { MD_B_WAIT(s0, 8); MD_B_WRITE(s0, 0); __builtin_amdgcn_sched_barrier(0); MD_GLDS_A(0, t + 2); __builtin_amdgcn_sched_barrier(0); }
;         if (t + 4 < NT) MD_B_ISSUE(s0, t + 4);
;         MD_COMPUTE(1);
;         MD_END(t + 4 >= NT);
	s_mov_b32 s49, s46
	s_mov_b32 s46, s47
	s_mov_b32 s47, s48
	s_mov_b32 s48, s49
	v_cvt_pk_bf16_f32 v172, v114, v116
	v_cvt_pk_bf16_f32 v173, v118, v120
	v_cvt_pk_bf16_f32 v174, v122, v124
	v_cvt_pk_bf16_f32 v175, v126, v128
	v_cvt_pk_bf16_f32 v176, v115, v117
	v_cvt_pk_bf16_f32 v177, v119, v121
	v_cvt_pk_bf16_f32 v178, v123, v125
	v_cvt_pk_bf16_f32 v179, v127, v129
	ds_write_b128 v95, v[172:175] offset:19456
	ds_write_b128 v95, v[176:179] offset:19584
	v_add_u32_e32 v91, s46, v135
	v_add_u32_e32 v93, s46, v137
	ds_read_b128 v[238:241], v139 offset:0
	ds_read_b128 v[242:245], v139 offset:2048
	ds_read_b128 v[246:249], v139 offset:4096
	ds_read_b128 v[250:253], v139 offset:6144
	ds_read_b128 v[218:221], v91 offset:0
	ds_read_b128 v[222:225], v91 offset:2048
	ds_read_b128 v[226:229], v91 offset:4096
	ds_read_b128 v[230:233], v91 offset:6144
	ds_read_b128 v[234:237], v91 offset:8192
	s_add_i32 s49, s48, s74
	s_add_i32 s52, s52, 1
	s_and_b32 s54, s52, 7
	s_cmp_eq_u32 s54, 0
	s_cselect_b32 s54, s53, s32
	s_cselect_b32 s55, -1, 0
	s_add_u32 s30, s30, s54
	s_addc_u32 s31, s31, s55
	s_waitcnt lgkmcnt(0)
	v_mfma_f32_16x16x32_bf16 v[78:81], v[238:241], v[218:221], v[78:81]
	v_mfma_f32_16x16x32_bf16 v[74:77], v[242:245], v[218:221], v[74:77]
	v_mfma_f32_16x16x32_bf16 v[70:73], v[246:249], v[218:221], v[70:73]
	v_mfma_f32_16x16x32_bf16 v[66:69], v[250:253], v[218:221], v[66:69]
	ds_read_b128 v[218:221], v93 offset:0
	ds_read_b128 v[142:145], v141 offset:0
	s_mov_b32 m0, s49
	s_nop 0
	global_load_lds_dwordx4 v88, s[30:31]
	v_mfma_f32_16x16x32_bf16 v[62:65], v[238:241], v[222:225], v[62:65]
	v_mfma_f32_16x16x32_bf16 v[58:61], v[242:245], v[222:225], v[58:61]
	v_mfma_f32_16x16x32_bf16 v[54:57], v[246:249], v[222:225], v[54:57]
	v_mfma_f32_16x16x32_bf16 v[50:53], v[250:253], v[222:225], v[50:53]
	ds_read_b128 v[222:225], v93 offset:2048
	ds_read_b128 v[146:149], v141 offset:2048
	s_add_i32 m0, s49, 0x2000
	s_nop 0
	global_load_lds_dwordx4 v90, s[30:31]
	v_mfma_f32_16x16x32_bf16 v[46:49], v[238:241], v[226:229], v[46:49]
	v_mfma_f32_16x16x32_bf16 v[42:45], v[242:245], v[226:229], v[42:45]
	v_mfma_f32_16x16x32_bf16 v[38:41], v[246:249], v[226:229], v[38:41]
	v_mfma_f32_16x16x32_bf16 v[34:37], v[250:253], v[226:229], v[34:37]
	ds_read_b128 v[226:229], v93 offset:4096
	ds_read_b128 v[156:159], v141 offset:4096
	s_add_i32 m0, s49, 0x4000
	s_nop 0
	global_load_lds_dwordx4 v92, s[30:31]
	v_mfma_f32_16x16x32_bf16 v[18:21], v[238:241], v[230:233], v[18:21]
	v_mfma_f32_16x16x32_bf16 v[22:25], v[242:245], v[230:233], v[22:25]
	v_mfma_f32_16x16x32_bf16 v[26:29], v[246:249], v[230:233], v[26:29]
	v_mfma_f32_16x16x32_bf16 v[30:33], v[250:253], v[230:233], v[30:33]
	ds_read_b128 v[230:233], v93 offset:6144
	ds_read_b128 v[160:163], v141 offset:6144
	s_add_i32 m0, s49, 0x6000
	s_nop 0
	global_load_lds_dwordx4 v94, s[30:31]
	v_mfma_f32_16x16x32_bf16 v[2:5], v[238:241], v[234:237], v[2:5]
	v_mfma_f32_16x16x32_bf16 v[6:9], v[242:245], v[234:237], v[6:9]
	v_mfma_f32_16x16x32_bf16 v[10:13], v[246:249], v[234:237], v[10:13]
	v_mfma_f32_16x16x32_bf16 v[14:17], v[250:253], v[234:237], v[14:17]
	ds_read_b128 v[234:237], v93 offset:8192
	s_add_i32 m0, s49, 0x8000
	s_nop 0
	global_load_lds_dwordx4 v96, s[30:31]
	s_waitcnt lgkmcnt(0)
	v_mfma_f32_16x16x32_bf16 v[78:81], v[142:145], v[218:221], v[78:81]
	v_mfma_f32_16x16x32_bf16 v[74:77], v[146:149], v[218:221], v[74:77]
	v_mfma_f32_16x16x32_bf16 v[70:73], v[156:159], v[218:221], v[70:73]
	v_mfma_f32_16x16x32_bf16 v[66:69], v[160:163], v[218:221], v[66:69]
	s_add_i32 s51, s51, 1
	s_and_b32 s54, s51, 7
	s_cmp_eq_u32 s54, 0
	s_cselect_b32 s44, s34, s35
	s_cselect_b32 s45, -1, 0
	v_lshl_add_u64 v[132:133], v[132:133], 0, s[44:45]
	global_load_dwordx2 v[114:115], v[132:133], off
	v_lshl_add_u64 v[180:181], v[132:133], 0, s[24:25]
	global_load_dwordx2 v[116:117], v[180:181], off
	v_mfma_f32_16x16x32_bf16 v[62:65], v[142:145], v[222:225], v[62:65]
	v_mfma_f32_16x16x32_bf16 v[58:61], v[146:149], v[222:225], v[58:61]
	v_mfma_f32_16x16x32_bf16 v[54:57], v[156:159], v[222:225], v[54:57]
	v_mfma_f32_16x16x32_bf16 v[50:53], v[160:163], v[222:225], v[50:53]
	v_lshl_add_u64 v[180:181], v[132:133], 0, s[26:27]
	global_load_dwordx2 v[118:119], v[180:181], off
	v_lshl_add_u64 v[180:181], v[132:133], 0, s[28:29]
	global_load_dwordx2 v[120:121], v[180:181], off
	v_mfma_f32_16x16x32_bf16 v[46:49], v[142:145], v[226:229], v[46:49]
	v_mfma_f32_16x16x32_bf16 v[42:45], v[146:149], v[226:229], v[42:45]
	v_mfma_f32_16x16x32_bf16 v[38:41], v[156:159], v[226:229], v[38:41]
	v_mfma_f32_16x16x32_bf16 v[34:37], v[160:163], v[226:229], v[34:37]
	v_lshl_add_u64 v[180:181], v[132:133], 0, s[36:37]
	global_load_dwordx2 v[122:123], v[180:181], off
	v_lshl_add_u64 v[180:181], v[132:133], 0, s[38:39]
	global_load_dwordx2 v[124:125], v[180:181], off
	v_mfma_f32_16x16x32_bf16 v[18:21], v[142:145], v[230:233], v[18:21]
	v_mfma_f32_16x16x32_bf16 v[22:25], v[146:149], v[230:233], v[22:25]
	v_mfma_f32_16x16x32_bf16 v[26:29], v[156:159], v[230:233], v[26:29]
	v_mfma_f32_16x16x32_bf16 v[30:33], v[160:163], v[230:233], v[30:33]
	v_lshl_add_u64 v[180:181], v[132:133], 0, s[40:41]
	global_load_dwordx2 v[126:127], v[180:181], off
	v_lshl_add_u64 v[180:181], v[132:133], 0, s[42:43]
	global_load_dwordx2 v[128:129], v[180:181], off
	v_mfma_f32_16x16x32_bf16 v[2:5], v[142:145], v[234:237], v[2:5]
	v_mfma_f32_16x16x32_bf16 v[6:9], v[146:149], v[234:237], v[6:9]
	v_mfma_f32_16x16x32_bf16 v[10:13], v[156:159], v[234:237], v[10:13]
	v_mfma_f32_16x16x32_bf16 v[14:17], v[160:163], v[234:237], v[14:17]
	s_waitcnt vmcnt(21)
	s_waitcnt lgkmcnt(0)
	s_barrier
; #define MD_GLDS_A(buf, tau) do { _Pragma("unroll") for (int i = 0; i < 5; ++i) if (amask & (1u << i)) \
;         __builtin_amdgcn_global_load_lds((const unsigned*)((const char*)HIDp + aoff[i] + (size_t)((tau) & 7) * 128), (PG8_LAS unsigned*)(MD_SA(buf) + wid * 1024 + i * 8192), 16, 0, 0); } while (0)
; #define MD_B_ISSUE(sb, tau) do { const char* kb_ = Bb + (size_t)((tau) >> 3) * 512 + (size_t)((tau) & 7) * (64 * (size_t)RB); _Pragma("unroll") for (int j = 0; j < 8; ++j) { const char* p_ = kb_ + (size_t)j * RB; \
;         asm volatile("global_load_dwordx2 %0, %1, off" : "=&v"(sb[j]) : "v"(p_) : "memory"); } } while (0)
; #define MD_B_WAIT(sb, N) asm volatile("s_waitcnt vmcnt(%8)" : "+v"(sb[0]), "+v"(sb[1]), "+v"(sb[2]), "+v"(sb[3]), "+v"(sb[4]), "+v"(sb[5]), "+v"(sb[6]), "+v"(sb[7]) : "n"(N) : "memory")
; #define MD_END(last) do { if (last) asm volatile("s_waitcnt vmcnt(0)" ::: "memory"); else asm volatile("s_waitcnt vmcnt(8)" ::: "memory"); \
;         asm volatile("s_waitcnt lgkmcnt(0)" ::: "memory"); __builtin_amdgcn_s_barrier(); asm volatile("" ::: "memory"); } while (0)
; __device__ __forceinline__ void moe_down_stream(PG8_LAS unsigned char* lds, int e, int cb0, int slot0, int nv, const bf16_t* HIDp, const float* Wd, bf16_t* Y, const float* slot_w, const int* slot_dst) {
;     ...
;     for (int t = 0; t < NT; t += 2) {
;         if (t + 2 < NT) MD_B_WAIT(s1, 8); else MD_B_WAIT(s1, 0);
;         MD_B_WRITE(s1, 1); __builtin_amdgcn_sched_barrier(0); MD_GLDS_A(1, t + 1); __builtin_amdgcn_sched_barrier(0);
;         if (t + 3 < NT) MD_B_ISSUE(s1, t + 3);
;         MD_COMPUTE(0);
;         MD_END(t + 3 >= NT);
;         if (t + 2 < NT) { MD_B_WAIT(s0, 8); MD_B_WRITE(s0, 0); __builtin_amdgcn_sched_barrier(0); MD_GLDS_A(0, t + 2); __builtin_amdgcn_sched_barrier(0); }
;         if (t + 4 < NT) MD_B_ISSUE(s0, t + 4);
;         MD_COMPUTE(1);
;         MD_END(t + 4 >= NT);
	s_mov_b32 s49, s46
	s_mov_b32 s46, s47
	s_mov_b32 s47, s48
	s_mov_b32 s48, s49
	v_cvt_pk_bf16_f32 v172, v186, v188
	v_cvt_pk_bf16_f32 v173, v190, v192
	v_cvt_pk_bf16_f32 v174, v194, v196
	v_cvt_pk_bf16_f32 v175, v198, v200
	v_cvt_pk_bf16_f32 v176, v187, v189
	v_cvt_pk_bf16_f32 v177, v191, v193
	v_cvt_pk_bf16_f32 v178, v195, v197
	v_cvt_pk_bf16_f32 v179, v199, v201
	ds_write_b128 v95, v[172:175] offset:0
	ds_write_b128 v95, v[176:179] offset:128
	v_add_u32_e32 v91, s46, v135
	v_add_u32_e32 v93, s46, v137
	ds_read_b128 v[238:241], v139 offset:19456
	ds_read_b128 v[242:245], v139 offset:21504
	ds_read_b128 v[246:249], v139 offset:23552
	ds_read_b128 v[250:253], v139 offset:25600
	ds_read_b128 v[218:221], v91 offset:0
	ds_read_b128 v[222:225], v91 offset:2048
	ds_read_b128 v[226:229], v91 offset:4096
	ds_read_b128 v[230:233], v91 offset:6144
	ds_read_b128 v[234:237], v91 offset:8192
	s_add_i32 s49, s48, s74
	s_add_i32 s52, s52, 1
	s_and_b32 s54, s52, 7
	s_cmp_eq_u32 s54, 0
	s_cselect_b32 s54, s53, s32
	s_cselect_b32 s55, -1, 0
	s_add_u32 s30, s30, s54
	s_addc_u32 s31, s31, s55
	s_waitcnt lgkmcnt(0)
	v_mfma_f32_16x16x32_bf16 v[78:81], v[238:241], v[218:221], v[78:81]
	v_mfma_f32_16x16x32_bf16 v[74:77], v[242:245], v[218:221], v[74:77]
	v_mfma_f32_16x16x32_bf16 v[70:73], v[246:249], v[218:221], v[70:73]
	v_mfma_f32_16x16x32_bf16 v[66:69], v[250:253], v[218:221], v[66:69]
	ds_read_b128 v[218:221], v93 offset:0
	ds_read_b128 v[142:145], v141 offset:19456
	s_mov_b32 m0, s49
	s_nop 0
	global_load_lds_dwordx4 v88, s[30:31]
	v_mfma_f32_16x16x32_bf16 v[62:65], v[238:241], v[222:225], v[62:65]
	v_mfma_f32_16x16x32_bf16 v[58:61], v[242:245], v[222:225], v[58:61]
	v_mfma_f32_16x16x32_bf16 v[54:57], v[246:249], v[222:225], v[54:57]
	v_mfma_f32_16x16x32_bf16 v[50:53], v[250:253], v[222:225], v[50:53]
	ds_read_b128 v[222:225], v93 offset:2048
	ds_read_b128 v[146:149], v141 offset:21504
	s_add_i32 m0, s49, 0x2000
	s_nop 0
	global_load_lds_dwordx4 v90, s[30:31]
	v_mfma_f32_16x16x32_bf16 v[46:49], v[238:241], v[226:229], v[46:49]
	v_mfma_f32_16x16x32_bf16 v[42:45], v[242:245], v[226:229], v[42:45]
	v_mfma_f32_16x16x32_bf16 v[38:41], v[246:249], v[226:229], v[38:41]
	v_mfma_f32_16x16x32_bf16 v[34:37], v[250:253], v[226:229], v[34:37]
	ds_read_b128 v[226:229], v93 offset:4096
	ds_read_b128 v[156:159], v141 offset:23552
	s_add_i32 m0, s49, 0x4000
	s_nop 0
	global_load_lds_dwordx4 v92, s[30:31]
	v_mfma_f32_16x16x32_bf16 v[18:21], v[238:241], v[230:233], v[18:21]
	v_mfma_f32_16x16x32_bf16 v[22:25], v[242:245], v[230:233], v[22:25]
	v_mfma_f32_16x16x32_bf16 v[26:29], v[246:249], v[230:233], v[26:29]
	v_mfma_f32_16x16x32_bf16 v[30:33], v[250:253], v[230:233], v[30:33]
	ds_read_b128 v[230:233], v93 offset:6144
	ds_read_b128 v[160:163], v141 offset:25600
	s_add_i32 m0, s49, 0x6000
	s_nop 0
	global_load_lds_dwordx4 v94, s[30:31]
	v_mfma_f32_16x16x32_bf16 v[2:5], v[238:241], v[234:237], v[2:5]
	v_mfma_f32_16x16x32_bf16 v[6:9], v[242:245], v[234:237], v[6:9]
	v_mfma_f32_16x16x32_bf16 v[10:13], v[246:249], v[234:237], v[10:13]
	v_mfma_f32_16x16x32_bf16 v[14:17], v[250:253], v[234:237], v[14:17]
	ds_read_b128 v[234:237], v93 offset:8192
	s_add_i32 m0, s49, 0x8000
	s_nop 0
	global_load_lds_dwordx4 v96, s[30:31]
	s_waitcnt lgkmcnt(0)
	v_mfma_f32_16x16x32_bf16 v[78:81], v[142:145], v[218:221], v[78:81]
	v_mfma_f32_16x16x32_bf16 v[74:77], v[146:149], v[218:221], v[74:77]
	v_mfma_f32_16x16x32_bf16 v[70:73], v[156:159], v[218:221], v[70:73]
	v_mfma_f32_16x16x32_bf16 v[66:69], v[160:163], v[218:221], v[66:69]
	s_add_i32 s51, s51, 1
	s_and_b32 s54, s51, 7
	s_cmp_eq_u32 s54, 0
	s_cselect_b32 s44, s34, s35
	s_cselect_b32 s45, -1, 0
	v_lshl_add_u64 v[132:133], v[132:133], 0, s[44:45]
	global_load_dwordx2 v[186:187], v[132:133], off
	v_lshl_add_u64 v[180:181], v[132:133], 0, s[24:25]
	global_load_dwordx2 v[188:189], v[180:181], off
	v_mfma_f32_16x16x32_bf16 v[62:65], v[142:145], v[222:225], v[62:65]
	v_mfma_f32_16x16x32_bf16 v[58:61], v[146:149], v[222:225], v[58:61]
	v_mfma_f32_16x16x32_bf16 v[54:57], v[156:159], v[222:225], v[54:57]
	v_mfma_f32_16x16x32_bf16 v[50:53], v[160:163], v[222:225], v[50:53]
	v_lshl_add_u64 v[180:181], v[132:133], 0, s[26:27]
	global_load_dwordx2 v[190:191], v[180:181], off
	v_lshl_add_u64 v[180:181], v[132:133], 0, s[28:29]
	global_load_dwordx2 v[192:193], v[180:181], off
	v_mfma_f32_16x16x32_bf16 v[46:49], v[142:145], v[226:229], v[46:49]
	v_mfma_f32_16x16x32_bf16 v[42:45], v[146:149], v[226:229], v[42:45]
	v_mfma_f32_16x16x32_bf16 v[38:41], v[156:159], v[226:229], v[38:41]
	v_mfma_f32_16x16x32_bf16 v[34:37], v[160:163], v[226:229], v[34:37]
	v_lshl_add_u64 v[180:181], v[132:133], 0, s[36:37]
	global_load_dwordx2 v[194:195], v[180:181], off
	v_lshl_add_u64 v[180:181], v[132:133], 0, s[38:39]
	global_load_dwordx2 v[196:197], v[180:181], off
	v_mfma_f32_16x16x32_bf16 v[18:21], v[142:145], v[230:233], v[18:21]
	v_mfma_f32_16x16x32_bf16 v[22:25], v[146:149], v[230:233], v[22:25]
	v_mfma_f32_16x16x32_bf16 v[26:29], v[156:159], v[230:233], v[26:29]
	v_mfma_f32_16x16x32_bf16 v[30:33], v[160:163], v[230:233], v[30:33]
	v_lshl_add_u64 v[180:181], v[132:133], 0, s[40:41]
	global_load_dwordx2 v[198:199], v[180:181], off
	v_lshl_add_u64 v[180:181], v[132:133], 0, s[42:43]
	global_load_dwordx2 v[200:201], v[180:181], off
	v_mfma_f32_16x16x32_bf16 v[2:5], v[142:145], v[234:237], v[2:5]
	v_mfma_f32_16x16x32_bf16 v[6:9], v[146:149], v[234:237], v[6:9]
	v_mfma_f32_16x16x32_bf16 v[10:13], v[156:159], v[234:237], v[10:13]
	v_mfma_f32_16x16x32_bf16 v[14:17], v[160:163], v[234:237], v[14:17]
	s_waitcnt vmcnt(21)
	s_waitcnt lgkmcnt(0)
	s_barrier
; #define MD_GLDS_A(buf, tau) do { _Pragma("unroll") for (int i = 0; i < 5; ++i) if (amask & (1u << i)) \
;         __builtin_amdgcn_global_load_lds((const unsigned*)((const char*)HIDp + aoff[i] + (size_t)((tau) & 7) * 128), (PG8_LAS unsigned*)(MD_SA(buf) + wid * 1024 + i * 8192), 16, 0, 0); } while (0)
; #define MD_B_ISSUE(sb, tau) do { const char* kb_ = Bb + (size_t)((tau) >> 3) * 512 + (size_t)((tau) & 7) * (64 * (size_t)RB); _Pragma("unroll") for (int j = 0; j < 8; ++j) { const char* p_ = kb_ + (size_t)j * RB; \
;         asm volatile("global_load_dwordx2 %0, %1, off" : "=&v"(sb[j]) : "v"(p_) : "memory"); } } while (0)
; #define MD_B_WAIT(sb, N) asm volatile("s_waitcnt vmcnt(%8)" : "+v"(sb[0]), "+v"(sb[1]), "+v"(sb[2]), "+v"(sb[3]), "+v"(sb[4]), "+v"(sb[5]), "+v"(sb[6]), "+v"(sb[7]) : "n"(N) : "memory")
; #define MD_END(last) do { if (last) asm volatile("s_waitcnt vmcnt(0)" ::: "memory"); else asm volatile("s_waitcnt vmcnt(8)" ::: "memory"); \
;         asm volatile("s_waitcnt lgkmcnt(0)" ::: "memory"); __builtin_amdgcn_s_barrier(); asm volatile("" ::: "memory"); } while (0)
; __device__ __forceinline__ void moe_down_stream(PG8_LAS unsigned char* lds, int e, int cb0, int slot0, int nv, const bf16_t* HIDp, const float* Wd, bf16_t* Y, const float* slot_w, const int* slot_dst) {
;     ...
;     for (int t = 0; t < NT; t += 2) {
;         if (t + 2 < NT) MD_B_WAIT(s1, 8); else MD_B_WAIT(s1, 0);
;         MD_B_WRITE(s1, 1); __builtin_amdgcn_sched_barrier(0); MD_GLDS_A(1, t + 1); __builtin_amdgcn_sched_barrier(0);
;         if (t + 3 < NT) MD_B_ISSUE(s1, t + 3);
;         MD_COMPUTE(0);
;         MD_END(t + 3 >= NT);
;         if (t + 2 < NT) { MD_B_WAIT(s0, 8); MD_B_WRITE(s0, 0); __builtin_amdgcn_sched_barrier(0); MD_GLDS_A(0, t + 2); __builtin_amdgcn_sched_barrier(0); }
;         if (t + 4 < NT) MD_B_ISSUE(s0, t + 4);
;         MD_COMPUTE(1);
;         MD_END(t + 4 >= NT);
	s_mov_b32 s49, s46
	s_mov_b32 s46, s47
	s_mov_b32 s47, s48
	s_mov_b32 s48, s49
	v_cvt_pk_bf16_f32 v172, v202, v204
	v_cvt_pk_bf16_f32 v173, v206, v208
	v_cvt_pk_bf16_f32 v174, v210, v212
	v_cvt_pk_bf16_f32 v175, v214, v216
	v_cvt_pk_bf16_f32 v176, v203, v205
	v_cvt_pk_bf16_f32 v177, v207, v209
	v_cvt_pk_bf16_f32 v178, v211, v213
	v_cvt_pk_bf16_f32 v179, v215, v217
	ds_write_b128 v95, v[172:175] offset:19456
	ds_write_b128 v95, v[176:179] offset:19584
	v_add_u32_e32 v91, s46, v135
	v_add_u32_e32 v93, s46, v137
	ds_read_b128 v[238:241], v139 offset:0
	ds_read_b128 v[242:245], v139 offset:2048
	ds_read_b128 v[246:249], v139 offset:4096
	ds_read_b128 v[250:253], v139 offset:6144
	ds_read_b128 v[218:221], v91 offset:0
	ds_read_b128 v[222:225], v91 offset:2048
	ds_read_b128 v[226:229], v91 offset:4096
	ds_read_b128 v[230:233], v91 offset:6144
	ds_read_b128 v[234:237], v91 offset:8192
	s_add_i32 s49, s48, s74
	s_add_i32 s52, s52, 1
	s_and_b32 s54, s52, 7
	s_cmp_eq_u32 s54, 0
	s_cselect_b32 s54, s53, s32
	s_cselect_b32 s55, -1, 0
	s_add_u32 s30, s30, s54
	s_addc_u32 s31, s31, s55
	s_waitcnt lgkmcnt(0)
	v_mfma_f32_16x16x32_bf16 v[78:81], v[238:241], v[218:221], v[78:81]
	v_mfma_f32_16x16x32_bf16 v[74:77], v[242:245], v[218:221], v[74:77]
	v_mfma_f32_16x16x32_bf16 v[70:73], v[246:249], v[218:221], v[70:73]
	v_mfma_f32_16x16x32_bf16 v[66:69], v[250:253], v[218:221], v[66:69]
	ds_read_b128 v[218:221], v93 offset:0
	ds_read_b128 v[142:145], v141 offset:0
	s_mov_b32 m0, s49
	s_nop 0
	global_load_lds_dwordx4 v88, s[30:31]
	v_mfma_f32_16x16x32_bf16 v[62:65], v[238:241], v[222:225], v[62:65]
	v_mfma_f32_16x16x32_bf16 v[58:61], v[242:245], v[222:225], v[58:61]
	v_mfma_f32_16x16x32_bf16 v[54:57], v[246:249], v[222:225], v[54:57]
	v_mfma_f32_16x16x32_bf16 v[50:53], v[250:253], v[222:225], v[50:53]
	ds_read_b128 v[222:225], v93 offset:2048
	ds_read_b128 v[146:149], v141 offset:2048
	s_add_i32 m0, s49, 0x2000
	s_nop 0
	global_load_lds_dwordx4 v90, s[30:31]
	v_mfma_f32_16x16x32_bf16 v[46:49], v[238:241], v[226:229], v[46:49]
	v_mfma_f32_16x16x32_bf16 v[42:45], v[242:245], v[226:229], v[42:45]
	v_mfma_f32_16x16x32_bf16 v[38:41], v[246:249], v[226:229], v[38:41]
	v_mfma_f32_16x16x32_bf16 v[34:37], v[250:253], v[226:229], v[34:37]
	ds_read_b128 v[226:229], v93 offset:4096
	ds_read_b128 v[156:159], v141 offset:4096
	s_add_i32 m0, s49, 0x4000
	s_nop 0
	global_load_lds_dwordx4 v92, s[30:31]
	v_mfma_f32_16x16x32_bf16 v[18:21], v[238:241], v[230:233], v[18:21]
	v_mfma_f32_16x16x32_bf16 v[22:25], v[242:245], v[230:233], v[22:25]
	v_mfma_f32_16x16x32_bf16 v[26:29], v[246:249], v[230:233], v[26:29]
	v_mfma_f32_16x16x32_bf16 v[30:33], v[250:253], v[230:233], v[30:33]
	ds_read_b128 v[230:233], v93 offset:6144
	ds_read_b128 v[160:163], v141 offset:6144
	s_add_i32 m0, s49, 0x6000
	s_nop 0
	global_load_lds_dwordx4 v94, s[30:31]
	v_mfma_f32_16x16x32_bf16 v[2:5], v[238:241], v[234:237], v[2:5]
	v_mfma_f32_16x16x32_bf16 v[6:9], v[242:245], v[234:237], v[6:9]
	v_mfma_f32_16x16x32_bf16 v[10:13], v[246:249], v[234:237], v[10:13]
	v_mfma_f32_16x16x32_bf16 v[14:17], v[250:253], v[234:237], v[14:17]
	ds_read_b128 v[234:237], v93 offset:8192
	s_add_i32 m0, s49, 0x8000
	s_nop 0
	global_load_lds_dwordx4 v96, s[30:31]
	s_waitcnt lgkmcnt(0)
	v_mfma_f32_16x16x32_bf16 v[78:81], v[142:145], v[218:221], v[78:81]
	v_mfma_f32_16x16x32_bf16 v[74:77], v[146:149], v[218:221], v[74:77]
	v_mfma_f32_16x16x32_bf16 v[70:73], v[156:159], v[218:221], v[70:73]
	v_mfma_f32_16x16x32_bf16 v[66:69], v[160:163], v[218:221], v[66:69]
	s_add_i32 s51, s51, 1
	s_and_b32 s54, s51, 7
	s_cmp_eq_u32 s54, 0
	s_cselect_b32 s44, s34, s35
	s_cselect_b32 s45, -1, 0
	v_lshl_add_u64 v[132:133], v[132:133], 0, s[44:45]
	global_load_dwordx2 v[202:203], v[132:133], off
	v_lshl_add_u64 v[180:181], v[132:133], 0, s[24:25]
	global_load_dwordx2 v[204:205], v[180:181], off
	v_mfma_f32_16x16x32_bf16 v[62:65], v[142:145], v[222:225], v[62:65]
	v_mfma_f32_16x16x32_bf16 v[58:61], v[146:149], v[222:225], v[58:61]
	v_mfma_f32_16x16x32_bf16 v[54:57], v[156:159], v[222:225], v[54:57]
	v_mfma_f32_16x16x32_bf16 v[50:53], v[160:163], v[222:225], v[50:53]
	v_lshl_add_u64 v[180:181], v[132:133], 0, s[26:27]
	global_load_dwordx2 v[206:207], v[180:181], off
	v_lshl_add_u64 v[180:181], v[132:133], 0, s[28:29]
	global_load_dwordx2 v[208:209], v[180:181], off
	v_mfma_f32_16x16x32_bf16 v[46:49], v[142:145], v[226:229], v[46:49]
	v_mfma_f32_16x16x32_bf16 v[42:45], v[146:149], v[226:229], v[42:45]
	v_mfma_f32_16x16x32_bf16 v[38:41], v[156:159], v[226:229], v[38:41]
	v_mfma_f32_16x16x32_bf16 v[34:37], v[160:163], v[226:229], v[34:37]
	v_lshl_add_u64 v[180:181], v[132:133], 0, s[36:37]
	global_load_dwordx2 v[210:211], v[180:181], off
	v_lshl_add_u64 v[180:181], v[132:133], 0, s[38:39]
	global_load_dwordx2 v[212:213], v[180:181], off
	v_mfma_f32_16x16x32_bf16 v[18:21], v[142:145], v[230:233], v[18:21]
	v_mfma_f32_16x16x32_bf16 v[22:25], v[146:149], v[230:233], v[22:25]
	v_mfma_f32_16x16x32_bf16 v[26:29], v[156:159], v[230:233], v[26:29]
	v_mfma_f32_16x16x32_bf16 v[30:33], v[160:163], v[230:233], v[30:33]
	v_lshl_add_u64 v[180:181], v[132:133], 0, s[40:41]
	global_load_dwordx2 v[214:215], v[180:181], off
	v_lshl_add_u64 v[180:181], v[132:133], 0, s[42:43]
	global_load_dwordx2 v[216:217], v[180:181], off
	v_mfma_f32_16x16x32_bf16 v[2:5], v[142:145], v[234:237], v[2:5]
	v_mfma_f32_16x16x32_bf16 v[6:9], v[146:149], v[234:237], v[6:9]
	v_mfma_f32_16x16x32_bf16 v[10:13], v[156:159], v[234:237], v[10:13]
	v_mfma_f32_16x16x32_bf16 v[14:17], v[160:163], v[234:237], v[14:17]
	s_waitcnt vmcnt(21)
	s_waitcnt lgkmcnt(0)
	s_barrier
; #define MD_GLDS_A(buf, tau) do { _Pragma("unroll") for (int i = 0; i < 5; ++i) if (amask & (1u << i)) \
;         __builtin_amdgcn_global_load_lds((const unsigned*)((const char*)HIDp + aoff[i] + (size_t)((tau) & 7) * 128), (PG8_LAS unsigned*)(MD_SA(buf) + wid * 1024 + i * 8192), 16, 0, 0); } while (0)
; #define MD_B_ISSUE(sb, tau) do { const char* kb_ = Bb + (size_t)((tau) >> 3) * 512 + (size_t)((tau) & 7) * (64 * (size_t)RB); _Pragma("unroll") for (int j = 0; j < 8; ++j) { const char* p_ = kb_ + (size_t)j * RB; \
;         asm volatile("global_load_dwordx2 %0, %1, off" : "=&v"(sb[j]) : "v"(p_) : "memory"); } } while (0)
; #define MD_B_WAIT(sb, N) asm volatile("s_waitcnt vmcnt(%8)" : "+v"(sb[0]), "+v"(sb[1]), "+v"(sb[2]), "+v"(sb[3]), "+v"(sb[4]), "+v"(sb[5]), "+v"(sb[6]), "+v"(sb[7]) : "n"(N) : "memory")
; #define MD_END(last) do { if (last) asm volatile("s_waitcnt vmcnt(0)" ::: "memory"); else asm volatile("s_waitcnt vmcnt(8)" ::: "memory"); \
;         asm volatile("s_waitcnt lgkmcnt(0)" ::: "memory"); __builtin_amdgcn_s_barrier(); asm volatile("" ::: "memory"); } while (0)
; __device__ __forceinline__ void moe_down_stream(PG8_LAS unsigned char* lds, int e, int cb0, int slot0, int nv, const bf16_t* HIDp, const float* Wd, bf16_t* Y, const float* slot_w, const int* slot_dst) {
;     ...
;     for (int t = 0; t < NT; t += 2) {
;         if (t + 2 < NT) MD_B_WAIT(s1, 8); else MD_B_WAIT(s1, 0);
;         MD_B_WRITE(s1, 1); __builtin_amdgcn_sched_barrier(0); MD_GLDS_A(1, t + 1); __builtin_amdgcn_sched_barrier(0);
;         if (t + 3 < NT) MD_B_ISSUE(s1, t + 3);
;         MD_COMPUTE(0);
;         MD_END(t + 3 >= NT);
;         if (t + 2 < NT) { MD_B_WAIT(s0, 8); MD_B_WRITE(s0, 0); __builtin_amdgcn_sched_barrier(0); MD_GLDS_A(0, t + 2); __builtin_amdgcn_sched_barrier(0); }
;         if (t + 4 < NT) MD_B_ISSUE(s0, t + 4);
;         MD_COMPUTE(1);
;         MD_END(t + 4 >= NT);
	s_mov_b32 s49, s46
	s_mov_b32 s46, s47
	s_mov_b32 s47, s48
	s_mov_b32 s48, s49
	v_cvt_pk_bf16_f32 v172, v98, v100
	v_cvt_pk_bf16_f32 v173, v102, v104
	v_cvt_pk_bf16_f32 v174, v106, v108
	v_cvt_pk_bf16_f32 v175, v110, v112
	v_cvt_pk_bf16_f32 v176, v99, v101
	v_cvt_pk_bf16_f32 v177, v103, v105
	v_cvt_pk_bf16_f32 v178, v107, v109
	v_cvt_pk_bf16_f32 v179, v111, v113
	ds_write_b128 v95, v[172:175] offset:0
	ds_write_b128 v95, v[176:179] offset:128
	v_add_u32_e32 v91, s46, v135
	v_add_u32_e32 v93, s46, v137
	ds_read_b128 v[238:241], v139 offset:19456
	ds_read_b128 v[242:245], v139 offset:21504
	ds_read_b128 v[246:249], v139 offset:23552
	ds_read_b128 v[250:253], v139 offset:25600
	ds_read_b128 v[218:221], v91 offset:0
	ds_read_b128 v[222:225], v91 offset:2048
	ds_read_b128 v[226:229], v91 offset:4096
	ds_read_b128 v[230:233], v91 offset:6144
	ds_read_b128 v[234:237], v91 offset:8192
	s_add_i32 s49, s48, s74
	s_add_i32 s52, s52, 1
	s_and_b32 s54, s52, 7
	s_cmp_eq_u32 s54, 0
	s_cselect_b32 s54, s53, s32
	s_cselect_b32 s55, -1, 0
	s_add_u32 s30, s30, s54
	s_addc_u32 s31, s31, s55
	s_waitcnt lgkmcnt(0)
	v_mfma_f32_16x16x32_bf16 v[78:81], v[238:241], v[218:221], v[78:81]
	v_mfma_f32_16x16x32_bf16 v[74:77], v[242:245], v[218:221], v[74:77]
	v_mfma_f32_16x16x32_bf16 v[70:73], v[246:249], v[218:221], v[70:73]
	v_mfma_f32_16x16x32_bf16 v[66:69], v[250:253], v[218:221], v[66:69]
	ds_read_b128 v[218:221], v93 offset:0
	ds_read_b128 v[142:145], v141 offset:19456
	s_mov_b32 m0, s49
	s_nop 0
	global_load_lds_dwordx4 v88, s[30:31]
	v_mfma_f32_16x16x32_bf16 v[62:65], v[238:241], v[222:225], v[62:65]
	v_mfma_f32_16x16x32_bf16 v[58:61], v[242:245], v[222:225], v[58:61]
	v_mfma_f32_16x16x32_bf16 v[54:57], v[246:249], v[222:225], v[54:57]
	v_mfma_f32_16x16x32_bf16 v[50:53], v[250:253], v[222:225], v[50:53]
	ds_read_b128 v[222:225], v93 offset:2048
	ds_read_b128 v[146:149], v141 offset:21504
	s_add_i32 m0, s49, 0x2000
	s_nop 0
	global_load_lds_dwordx4 v90, s[30:31]
	v_mfma_f32_16x16x32_bf16 v[46:49], v[238:241], v[226:229], v[46:49]
	v_mfma_f32_16x16x32_bf16 v[42:45], v[242:245], v[226:229], v[42:45]
	v_mfma_f32_16x16x32_bf16 v[38:41], v[246:249], v[226:229], v[38:41]
	v_mfma_f32_16x16x32_bf16 v[34:37], v[250:253], v[226:229], v[34:37]
	ds_read_b128 v[226:229], v93 offset:4096
	ds_read_b128 v[156:159], v141 offset:23552
	s_add_i32 m0, s49, 0x4000
	s_nop 0
	global_load_lds_dwordx4 v92, s[30:31]
	v_mfma_f32_16x16x32_bf16 v[18:21], v[238:241], v[230:233], v[18:21]
	v_mfma_f32_16x16x32_bf16 v[22:25], v[242:245], v[230:233], v[22:25]
	v_mfma_f32_16x16x32_bf16 v[26:29], v[246:249], v[230:233], v[26:29]
	v_mfma_f32_16x16x32_bf16 v[30:33], v[250:253], v[230:233], v[30:33]
	ds_read_b128 v[230:233], v93 offset:6144
	ds_read_b128 v[160:163], v141 offset:25600
	s_add_i32 m0, s49, 0x6000
	s_nop 0
	global_load_lds_dwordx4 v94, s[30:31]
	v_mfma_f32_16x16x32_bf16 v[2:5], v[238:241], v[234:237], v[2:5]
	v_mfma_f32_16x16x32_bf16 v[6:9], v[242:245], v[234:237], v[6:9]
	v_mfma_f32_16x16x32_bf16 v[10:13], v[246:249], v[234:237], v[10:13]
	v_mfma_f32_16x16x32_bf16 v[14:17], v[250:253], v[234:237], v[14:17]
	ds_read_b128 v[234:237], v93 offset:8192
	s_add_i32 m0, s49, 0x8000
	s_nop 0
	global_load_lds_dwordx4 v96, s[30:31]
	s_waitcnt lgkmcnt(0)
	v_mfma_f32_16x16x32_bf16 v[78:81], v[142:145], v[218:221], v[78:81]
	v_mfma_f32_16x16x32_bf16 v[74:77], v[146:149], v[218:221], v[74:77]
	v_mfma_f32_16x16x32_bf16 v[70:73], v[156:159], v[218:221], v[70:73]
	v_mfma_f32_16x16x32_bf16 v[66:69], v[160:163], v[218:221], v[66:69]
	s_add_i32 s51, s51, 1
	s_and_b32 s54, s51, 7
	s_cmp_eq_u32 s54, 0
	s_cselect_b32 s44, s34, s35
	s_cselect_b32 s45, -1, 0
	v_lshl_add_u64 v[132:133], v[132:133], 0, s[44:45]
	global_load_dwordx2 v[98:99], v[132:133], off
	v_lshl_add_u64 v[180:181], v[132:133], 0, s[24:25]
	global_load_dwordx2 v[100:101], v[180:181], off
	v_mfma_f32_16x16x32_bf16 v[62:65], v[142:145], v[222:225], v[62:65]
	v_mfma_f32_16x16x32_bf16 v[58:61], v[146:149], v[222:225], v[58:61]
	v_mfma_f32_16x16x32_bf16 v[54:57], v[156:159], v[222:225], v[54:57]
	v_mfma_f32_16x16x32_bf16 v[50:53], v[160:163], v[222:225], v[50:53]
	v_lshl_add_u64 v[180:181], v[132:133], 0, s[26:27]
	global_load_dwordx2 v[102:103], v[180:181], off
	v_lshl_add_u64 v[180:181], v[132:133], 0, s[28:29]
	global_load_dwordx2 v[104:105], v[180:181], off
	v_mfma_f32_16x16x32_bf16 v[46:49], v[142:145], v[226:229], v[46:49]
	v_mfma_f32_16x16x32_bf16 v[42:45], v[146:149], v[226:229], v[42:45]
	v_mfma_f32_16x16x32_bf16 v[38:41], v[156:159], v[226:229], v[38:41]
	v_mfma_f32_16x16x32_bf16 v[34:37], v[160:163], v[226:229], v[34:37]
	v_lshl_add_u64 v[180:181], v[132:133], 0, s[36:37]
	global_load_dwordx2 v[106:107], v[180:181], off
	v_lshl_add_u64 v[180:181], v[132:133], 0, s[38:39]
	global_load_dwordx2 v[108:109], v[180:181], off
	v_mfma_f32_16x16x32_bf16 v[18:21], v[142:145], v[230:233], v[18:21]
	v_mfma_f32_16x16x32_bf16 v[22:25], v[146:149], v[230:233], v[22:25]
	v_mfma_f32_16x16x32_bf16 v[26:29], v[156:159], v[230:233], v[26:29]
	v_mfma_f32_16x16x32_bf16 v[30:33], v[160:163], v[230:233], v[30:33]
	v_lshl_add_u64 v[180:181], v[132:133], 0, s[40:41]
	global_load_dwordx2 v[110:111], v[180:181], off
	v_lshl_add_u64 v[180:181], v[132:133], 0, s[42:43]
	global_load_dwordx2 v[112:113], v[180:181], off
	v_mfma_f32_16x16x32_bf16 v[2:5], v[142:145], v[234:237], v[2:5]
	v_mfma_f32_16x16x32_bf16 v[6:9], v[146:149], v[234:237], v[6:9]
	v_mfma_f32_16x16x32_bf16 v[10:13], v[156:159], v[234:237], v[10:13]
	v_mfma_f32_16x16x32_bf16 v[14:17], v[160:163], v[234:237], v[14:17]
	s_waitcnt vmcnt(21)
	s_waitcnt lgkmcnt(0)
	s_barrier
; #define PG8_LAS __attribute__((address_space(3)))
; __device__ __forceinline__ unsigned cvtpk(float lo, float hi) { f32x2 v = {lo, hi}; bf16x2_t b = __builtin_convertvector(v, bf16x2_t); return __builtin_bit_cast(unsigned, b); }
; __device__ __forceinline__ void moe_down_stream(PG8_LAS unsigned char* lds, int e, int cb0, int slot0, int nv, const bf16_t* HIDp, const float* Wd, bf16_t* Y, const float* slot_w, const int* slot_dst) {
;     ...
;         if (((t + 1) & 7) == 7) {
;             const int cb = cb0 + ((t + 1) >> 3);
; #pragma unroll
;             for (int m = 0; m < DNM; ++m) {
;                 const float w_ = lw[4 * (16 * m + fr) + wr];
; #pragma unroll
;                 for (int p = 0; p < 2; ++p) { const f32x4 v0 = acc[m][2 * p] * w_, v1 = acc[m][2 * p + 1] * w_; u32x4 w; w.x = cvtpk(v0[0], v0[1]); w.y = cvtpk(v0[2], v0[3]); w.z = cvtpk(v1[0], v1[1]); w.w = cvtpk(v1[2], v1[3]);
;                     *(PG8_LAS u32x4*)(stg + fr * 128 + (((4 * p + fq) ^ (fr & 7)) * 16)) = w; }
; #pragma unroll
;                 for (int hh = 0; hh < 2; ++hh) { const int r = (lane >> 3) + 8 * hh, cc = lane & 7; const u32x4 d = *(const PG8_LAS u32x4*)(stg + r * 128 + ((cc ^ (r & 7)) * 16)); const int dst_ = ldst[4 * (16 * m + r) + wr];
;                     if (dst_ >= 0) *(u32x4*)(Y + (size_t)dst_ * D + 128 * cb + 64 * wc + 8 * cc) = d; }
; #pragma unroll
;                 for (int n = 0; n < 4; ++n) acc[m][n] = (f32x4){0.f, 0.f, 0.f, 0.f}; } }
	s_mov_b32 s49, s46
	s_mov_b32 s46, s47
	s_mov_b32 s47, s48
	s_mov_b32 s48, s49
	s_add_i32 s54, s48, s74
	v_add_u32_e32 v164, s54, v84
	v_add_u32_e32 v165, s54, v85
	ds_read_b32 v150, v82 offset:0
	ds_read_b32 v151, v83 offset:0
	ds_read_b32 v166, v83 offset:128
	s_waitcnt lgkmcnt(2)
	v_mul_f32_e32 v78, v150, v78
	v_mul_f32_e32 v79, v150, v79
	v_mul_f32_e32 v80, v150, v80
	v_mul_f32_e32 v81, v150, v81
	v_mul_f32_e32 v74, v150, v74
	v_mul_f32_e32 v75, v150, v75
	v_mul_f32_e32 v76, v150, v76
	v_mul_f32_e32 v77, v150, v77
	v_cvt_pk_bf16_f32 v182, v78, v79
	v_cvt_pk_bf16_f32 v183, v80, v81
	v_cvt_pk_bf16_f32 v184, v74, v75
	v_cvt_pk_bf16_f32 v185, v76, v77
	ds_write_b128 v164, v[182:185]
	v_mul_f32_e32 v70, v150, v70
	v_mul_f32_e32 v71, v150, v71
	v_mul_f32_e32 v72, v150, v72
	v_mul_f32_e32 v73, v150, v73
	v_mul_f32_e32 v66, v150, v66
	v_mul_f32_e32 v67, v150, v67
	v_mul_f32_e32 v68, v150, v68
	v_mul_f32_e32 v69, v150, v69
	v_cvt_pk_bf16_f32 v182, v70, v71
	v_cvt_pk_bf16_f32 v183, v72, v73
	v_cvt_pk_bf16_f32 v184, v66, v67
	v_cvt_pk_bf16_f32 v185, v68, v69
	v_xor_b32_e32 v167, 64, v164
	ds_write_b128 v167, v[182:185]
	v_mov_b32_e32 v78, 0
	v_mov_b32_e32 v74, 0
	v_mov_b32_e32 v70, 0
	v_mov_b32_e32 v66, 0
	v_mov_b32_e32 v79, 0
	v_mov_b32_e32 v75, 0
	v_mov_b32_e32 v71, 0
	v_mov_b32_e32 v67, 0
	v_mov_b32_e32 v80, 0
	v_mov_b32_e32 v76, 0
	v_mov_b32_e32 v72, 0
	v_mov_b32_e32 v68, 0
	v_mov_b32_e32 v81, 0
	v_mov_b32_e32 v77, 0
	v_mov_b32_e32 v73, 0
	v_mov_b32_e32 v69, 0
	ds_read_b128 v[182:185], v165 offset:0
	v_cmp_lt_i32_e32 vcc, -1, v151
	v_lshlrev_b32_e32 v148, 13, v151
	v_mov_b32_e32 v149, 0
	v_lshl_add_u64 v[148:149], v[148:149], 0, v[86:87]
	v_cndmask_b32_e32 v148, v168, v148, vcc
	v_cndmask_b32_e32 v149, v169, v149, vcc
	s_waitcnt lgkmcnt(0)
	global_store_dwordx4 v[148:149], v[182:185], off
	ds_read_b128 v[182:185], v165 offset:8192
	v_cmp_lt_i32_e32 vcc, -1, v166
	v_lshlrev_b32_e32 v148, 13, v166
	v_mov_b32_e32 v149, 0
	v_lshl_add_u64 v[148:149], v[148:149], 0, v[86:87]
	v_cndmask_b32_e32 v148, v168, v148, vcc
	v_cndmask_b32_e32 v149, v169, v149, vcc
	s_waitcnt lgkmcnt(0)
	global_store_dwordx4 v[148:149], v[182:185], off
	ds_read_b32 v150, v82 offset:256
	ds_read_b32 v151, v83 offset:256
	ds_read_b32 v166, v83 offset:384
	s_waitcnt lgkmcnt(2)
	v_mul_f32_e32 v62, v150, v62
	v_mul_f32_e32 v63, v150, v63
	v_mul_f32_e32 v64, v150, v64
	v_mul_f32_e32 v65, v150, v65
	v_mul_f32_e32 v58, v150, v58
	v_mul_f32_e32 v59, v150, v59
	v_mul_f32_e32 v60, v150, v60
	v_mul_f32_e32 v61, v150, v61
	v_cvt_pk_bf16_f32 v182, v62, v63
	v_cvt_pk_bf16_f32 v183, v64, v65
	v_cvt_pk_bf16_f32 v184, v58, v59
	v_cvt_pk_bf16_f32 v185, v60, v61
	ds_write_b128 v164, v[182:185]
	v_mul_f32_e32 v54, v150, v54
	v_mul_f32_e32 v55, v150, v55
	v_mul_f32_e32 v56, v150, v56
	v_mul_f32_e32 v57, v150, v57
	v_mul_f32_e32 v50, v150, v50
	v_mul_f32_e32 v51, v150, v51
	v_mul_f32_e32 v52, v150, v52
	v_mul_f32_e32 v53, v150, v53
	v_cvt_pk_bf16_f32 v182, v54, v55
	v_cvt_pk_bf16_f32 v183, v56, v57
	v_cvt_pk_bf16_f32 v184, v50, v51
	v_cvt_pk_bf16_f32 v185, v52, v53
	v_xor_b32_e32 v167, 64, v164
	ds_write_b128 v167, v[182:185]
	v_mov_b32_e32 v62, 0
	v_mov_b32_e32 v58, 0
	v_mov_b32_e32 v54, 0
	v_mov_b32_e32 v50, 0
	v_mov_b32_e32 v63, 0
	v_mov_b32_e32 v59, 0
	v_mov_b32_e32 v55, 0
	v_mov_b32_e32 v51, 0
	v_mov_b32_e32 v64, 0
	v_mov_b32_e32 v60, 0
	v_mov_b32_e32 v56, 0
	v_mov_b32_e32 v52, 0
	v_mov_b32_e32 v65, 0
	v_mov_b32_e32 v61, 0
	v_mov_b32_e32 v57, 0
	v_mov_b32_e32 v53, 0
	ds_read_b128 v[182:185], v165 offset:0
	v_cmp_lt_i32_e32 vcc, -1, v151
	v_lshlrev_b32_e32 v148, 13, v151
	v_mov_b32_e32 v149, 0
	v_lshl_add_u64 v[148:149], v[148:149], 0, v[86:87]
	v_cndmask_b32_e32 v148, v168, v148, vcc
	v_cndmask_b32_e32 v149, v169, v149, vcc
	s_waitcnt lgkmcnt(0)
	global_store_dwordx4 v[148:149], v[182:185], off
	ds_read_b128 v[182:185], v165 offset:8192
	v_cmp_lt_i32_e32 vcc, -1, v166
	v_lshlrev_b32_e32 v148, 13, v166
	v_mov_b32_e32 v149, 0
	v_lshl_add_u64 v[148:149], v[148:149], 0, v[86:87]
	v_cndmask_b32_e32 v148, v168, v148, vcc
	v_cndmask_b32_e32 v149, v169, v149, vcc
	s_waitcnt lgkmcnt(0)
	global_store_dwordx4 v[148:149], v[182:185], off
	ds_read_b32 v150, v82 offset:512
	ds_read_b32 v151, v83 offset:512
	ds_read_b32 v166, v83 offset:640
	s_waitcnt lgkmcnt(2)
	v_mul_f32_e32 v46, v150, v46
	v_mul_f32_e32 v47, v150, v47
	v_mul_f32_e32 v48, v150, v48
	v_mul_f32_e32 v49, v150, v49
	v_mul_f32_e32 v42, v150, v42
	v_mul_f32_e32 v43, v150, v43
	v_mul_f32_e32 v44, v150, v44
	v_mul_f32_e32 v45, v150, v45
	v_cvt_pk_bf16_f32 v182, v46, v47
	v_cvt_pk_bf16_f32 v183, v48, v49
	v_cvt_pk_bf16_f32 v184, v42, v43
	v_cvt_pk_bf16_f32 v185, v44, v45
	ds_write_b128 v164, v[182:185]
	v_mul_f32_e32 v38, v150, v38
	v_mul_f32_e32 v39, v150, v39
	v_mul_f32_e32 v40, v150, v40
	v_mul_f32_e32 v41, v150, v41
	v_mul_f32_e32 v34, v150, v34
	v_mul_f32_e32 v35, v150, v35
	v_mul_f32_e32 v36, v150, v36
	v_mul_f32_e32 v37, v150, v37
	v_cvt_pk_bf16_f32 v182, v38, v39
	v_cvt_pk_bf16_f32 v183, v40, v41
	v_cvt_pk_bf16_f32 v184, v34, v35
	v_cvt_pk_bf16_f32 v185, v36, v37
	v_xor_b32_e32 v167, 64, v164
	ds_write_b128 v167, v[182:185]
	v_mov_b32_e32 v46, 0
	v_mov_b32_e32 v42, 0
	v_mov_b32_e32 v38, 0
	v_mov_b32_e32 v34, 0
	v_mov_b32_e32 v47, 0
	v_mov_b32_e32 v43, 0
	v_mov_b32_e32 v39, 0
	v_mov_b32_e32 v35, 0
	v_mov_b32_e32 v48, 0
	v_mov_b32_e32 v44, 0
	v_mov_b32_e32 v40, 0
	v_mov_b32_e32 v36, 0
	v_mov_b32_e32 v49, 0
	v_mov_b32_e32 v45, 0
	v_mov_b32_e32 v41, 0
	v_mov_b32_e32 v37, 0
	ds_read_b128 v[182:185], v165 offset:0
	v_cmp_lt_i32_e32 vcc, -1, v151
	v_lshlrev_b32_e32 v148, 13, v151
	v_mov_b32_e32 v149, 0
	v_lshl_add_u64 v[148:149], v[148:149], 0, v[86:87]
	v_cndmask_b32_e32 v148, v168, v148, vcc
	v_cndmask_b32_e32 v149, v169, v149, vcc
	s_waitcnt lgkmcnt(0)
; #define PG8_LAS __attribute__((address_space(3)))
; __device__ __forceinline__ unsigned cvtpk(float lo, float hi) { f32x2 v = {lo, hi}; bf16x2_t b = __builtin_convertvector(v, bf16x2_t); return __builtin_bit_cast(unsigned, b); }
; #define MD_GLDS_A(buf, tau) do { _Pragma("unroll") for (int i = 0; i < 5; ++i) if (amask & (1u << i)) \
;         __builtin_amdgcn_global_load_lds((const unsigned*)((const char*)HIDp + aoff[i] + (size_t)((tau) & 7) * 128), (PG8_LAS unsigned*)(MD_SA(buf) + wid * 1024 + i * 8192), 16, 0, 0); } while (0)
; __device__ __forceinline__ void moe_down_stream(PG8_LAS unsigned char* lds, int e, int cb0, int slot0, int nv, const bf16_t* HIDp, const float* Wd, bf16_t* Y, const float* slot_w, const int* slot_dst) {
;     ...
;     for (int t = 0; t < NT; t += 2) {
;         if (t + 2 < NT) MD_B_WAIT(s1, 8); else MD_B_WAIT(s1, 0);
;         MD_B_WRITE(s1, 1); __builtin_amdgcn_sched_barrier(0); MD_GLDS_A(1, t + 1); __builtin_amdgcn_sched_barrier(0);
;         if (t + 3 < NT) MD_B_ISSUE(s1, t + 3);
;         MD_COMPUTE(0);
;         MD_END(t + 3 >= NT);
;         if (t + 2 < NT) { MD_B_WAIT(s0, 8); MD_B_WRITE(s0, 0); __builtin_amdgcn_sched_barrier(0); MD_GLDS_A(0, t + 2); __builtin_amdgcn_sched_barrier(0); }
;     ...
;         if (((t + 1) & 7) == 7) {
;             const int cb = cb0 + ((t + 1) >> 3);
; #pragma unroll
;             for (int m = 0; m < DNM; ++m) {
;                 const float w_ = lw[4 * (16 * m + fr) + wr];
; #pragma unroll
;                 for (int p = 0; p < 2; ++p) { const f32x4 v0 = acc[m][2 * p] * w_, v1 = acc[m][2 * p + 1] * w_; u32x4 w; w.x = cvtpk(v0[0], v0[1]); w.y = cvtpk(v0[2], v0[3]); w.z = cvtpk(v1[0], v1[1]); w.w = cvtpk(v1[2], v1[3]);
;                     *(PG8_LAS u32x4*)(stg + fr * 128 + (((4 * p + fq) ^ (fr & 7)) * 16)) = w; }
; #pragma unroll
;                 for (int hh = 0; hh < 2; ++hh) { const int r = (lane >> 3) + 8 * hh, cc = lane & 7; const u32x4 d = *(const PG8_LAS u32x4*)(stg + r * 128 + ((cc ^ (r & 7)) * 16)); const int dst_ = ldst[4 * (16 * m + r) + wr];
;                     if (dst_ >= 0) *(u32x4*)(Y + (size_t)dst_ * D + 128 * cb + 64 * wc + 8 * cc) = d; }
; #pragma unroll
;                 for (int n = 0; n < 4; ++n) acc[m][n] = (f32x4){0.f, 0.f, 0.f, 0.f}; } }
	global_store_dwordx4 v[148:149], v[182:185], off
	ds_read_b128 v[182:185], v165 offset:8192
	v_cmp_lt_i32_e32 vcc, -1, v166
	v_lshlrev_b32_e32 v148, 13, v166
	v_mov_b32_e32 v149, 0
	v_lshl_add_u64 v[148:149], v[148:149], 0, v[86:87]
	v_cndmask_b32_e32 v148, v168, v148, vcc
	v_cndmask_b32_e32 v149, v169, v149, vcc
	s_waitcnt lgkmcnt(0)
	global_store_dwordx4 v[148:149], v[182:185], off
	ds_read_b32 v150, v82 offset:768
	ds_read_b32 v151, v83 offset:768
	ds_read_b32 v166, v83 offset:896
	s_waitcnt lgkmcnt(2)
	v_mul_f32_e32 v18, v150, v18
	v_mul_f32_e32 v19, v150, v19
	v_mul_f32_e32 v20, v150, v20
	v_mul_f32_e32 v21, v150, v21
	v_mul_f32_e32 v22, v150, v22
	v_mul_f32_e32 v23, v150, v23
	v_mul_f32_e32 v24, v150, v24
	v_mul_f32_e32 v25, v150, v25
	v_cvt_pk_bf16_f32 v182, v18, v19
	v_cvt_pk_bf16_f32 v183, v20, v21
	v_cvt_pk_bf16_f32 v184, v22, v23
	v_cvt_pk_bf16_f32 v185, v24, v25
	ds_write_b128 v164, v[182:185]
	v_mul_f32_e32 v26, v150, v26
	v_mul_f32_e32 v27, v150, v27
	v_mul_f32_e32 v28, v150, v28
	v_mul_f32_e32 v29, v150, v29
	v_mul_f32_e32 v30, v150, v30
	v_mul_f32_e32 v31, v150, v31
	v_mul_f32_e32 v32, v150, v32
	v_mul_f32_e32 v33, v150, v33
	v_cvt_pk_bf16_f32 v182, v26, v27
	v_cvt_pk_bf16_f32 v183, v28, v29
	v_cvt_pk_bf16_f32 v184, v30, v31
	v_cvt_pk_bf16_f32 v185, v32, v33
	v_xor_b32_e32 v167, 64, v164
	ds_write_b128 v167, v[182:185]
	v_mov_b32_e32 v18, 0
	v_mov_b32_e32 v22, 0
	v_mov_b32_e32 v26, 0
	v_mov_b32_e32 v30, 0
	v_mov_b32_e32 v19, 0
	v_mov_b32_e32 v23, 0
	v_mov_b32_e32 v27, 0
	v_mov_b32_e32 v31, 0
	v_mov_b32_e32 v20, 0
	v_mov_b32_e32 v24, 0
	v_mov_b32_e32 v28, 0
	v_mov_b32_e32 v32, 0
	v_mov_b32_e32 v21, 0
	v_mov_b32_e32 v25, 0
	v_mov_b32_e32 v29, 0
	v_mov_b32_e32 v33, 0
	ds_read_b128 v[182:185], v165 offset:0
	v_cmp_lt_i32_e32 vcc, -1, v151
	v_lshlrev_b32_e32 v148, 13, v151
	v_mov_b32_e32 v149, 0
	v_lshl_add_u64 v[148:149], v[148:149], 0, v[86:87]
	v_cndmask_b32_e32 v148, v168, v148, vcc
	v_cndmask_b32_e32 v149, v169, v149, vcc
	s_waitcnt lgkmcnt(0)
	global_store_dwordx4 v[148:149], v[182:185], off
	ds_read_b128 v[182:185], v165 offset:8192
	v_cmp_lt_i32_e32 vcc, -1, v166
	v_lshlrev_b32_e32 v148, 13, v166
	v_mov_b32_e32 v149, 0
	v_lshl_add_u64 v[148:149], v[148:149], 0, v[86:87]
	v_cndmask_b32_e32 v148, v168, v148, vcc
	v_cndmask_b32_e32 v149, v169, v149, vcc
	s_waitcnt lgkmcnt(0)
	global_store_dwordx4 v[148:149], v[182:185], off
	ds_read_b32 v150, v82 offset:1024
	ds_read_b32 v151, v83 offset:1024
	ds_read_b32 v166, v83 offset:1152
	s_waitcnt lgkmcnt(2)
	v_mul_f32_e32 v2, v150, v2
	v_mul_f32_e32 v3, v150, v3
	v_mul_f32_e32 v4, v150, v4
	v_mul_f32_e32 v5, v150, v5
	v_mul_f32_e32 v6, v150, v6
	v_mul_f32_e32 v7, v150, v7
	v_mul_f32_e32 v8, v150, v8
	v_mul_f32_e32 v9, v150, v9
	v_cvt_pk_bf16_f32 v182, v2, v3
	v_cvt_pk_bf16_f32 v183, v4, v5
	v_cvt_pk_bf16_f32 v184, v6, v7
	v_cvt_pk_bf16_f32 v185, v8, v9
	ds_write_b128 v164, v[182:185]
	v_mul_f32_e32 v10, v150, v10
	v_mul_f32_e32 v11, v150, v11
	v_mul_f32_e32 v12, v150, v12
	v_mul_f32_e32 v13, v150, v13
	v_mul_f32_e32 v14, v150, v14
	v_mul_f32_e32 v15, v150, v15
	v_mul_f32_e32 v16, v150, v16
	v_mul_f32_e32 v17, v150, v17
	v_cvt_pk_bf16_f32 v182, v10, v11
	v_cvt_pk_bf16_f32 v183, v12, v13
	v_cvt_pk_bf16_f32 v184, v14, v15
	v_cvt_pk_bf16_f32 v185, v16, v17
	v_xor_b32_e32 v167, 64, v164
	ds_write_b128 v167, v[182:185]
	v_mov_b32_e32 v2, 0
	v_mov_b32_e32 v6, 0
	v_mov_b32_e32 v10, 0
	v_mov_b32_e32 v14, 0
	v_mov_b32_e32 v3, 0
	v_mov_b32_e32 v7, 0
	v_mov_b32_e32 v11, 0
	v_mov_b32_e32 v15, 0
	v_mov_b32_e32 v4, 0
	v_mov_b32_e32 v8, 0
	v_mov_b32_e32 v12, 0
	v_mov_b32_e32 v16, 0
	v_mov_b32_e32 v5, 0
	v_mov_b32_e32 v9, 0
	v_mov_b32_e32 v13, 0
	v_mov_b32_e32 v17, 0
	ds_read_b128 v[182:185], v165 offset:0
	v_cmp_lt_i32_e32 vcc, -1, v151
	v_lshlrev_b32_e32 v148, 13, v151
	v_mov_b32_e32 v149, 0
	v_lshl_add_u64 v[148:149], v[148:149], 0, v[86:87]
	v_cndmask_b32_e32 v148, v168, v148, vcc
	v_cndmask_b32_e32 v149, v169, v149, vcc
	s_waitcnt lgkmcnt(0)
	global_store_dwordx4 v[148:149], v[182:185], off
	ds_read_b128 v[182:185], v165 offset:8192
	v_cmp_lt_i32_e32 vcc, -1, v166
	v_lshlrev_b32_e32 v148, 13, v166
	v_mov_b32_e32 v149, 0
	v_lshl_add_u64 v[148:149], v[148:149], 0, v[86:87]
	v_cndmask_b32_e32 v148, v168, v148, vcc
	v_cndmask_b32_e32 v149, v169, v149, vcc
	s_waitcnt lgkmcnt(0)
	global_store_dwordx4 v[148:149], v[182:185], off
	v_add_co_u32_e32 v86, vcc, 0x800, v86
	s_nop 1
	v_addc_co_u32_e32 v87, vcc, 0, v87, vcc
	s_waitcnt lgkmcnt(0)
	v_cvt_pk_bf16_f32 v172, v114, v116
	v_cvt_pk_bf16_f32 v173, v118, v120
	v_cvt_pk_bf16_f32 v174, v122, v124
	v_cvt_pk_bf16_f32 v175, v126, v128
	v_cvt_pk_bf16_f32 v176, v115, v117
	v_cvt_pk_bf16_f32 v177, v119, v121
	v_cvt_pk_bf16_f32 v178, v123, v125
	v_cvt_pk_bf16_f32 v179, v127, v129
	ds_write_b128 v95, v[172:175] offset:19456
	ds_write_b128 v95, v[176:179] offset:19584
	v_add_u32_e32 v91, s46, v135
	v_add_u32_e32 v93, s46, v137
	ds_read_b128 v[238:241], v139 offset:0
	ds_read_b128 v[242:245], v139 offset:2048
	ds_read_b128 v[246:249], v139 offset:4096
	ds_read_b128 v[250:253], v139 offset:6144
	ds_read_b128 v[218:221], v91 offset:0
	ds_read_b128 v[222:225], v91 offset:2048
	ds_read_b128 v[226:229], v91 offset:4096
	ds_read_b128 v[230:233], v91 offset:6144
	ds_read_b128 v[234:237], v91 offset:8192
	s_add_i32 s49, s48, s74
	s_add_i32 s52, s52, 1
	s_and_b32 s54, s52, 7
	s_cmp_eq_u32 s54, 0
	s_cselect_b32 s54, s53, s32
	s_cselect_b32 s55, -1, 0
	s_add_u32 s30, s30, s54
	s_addc_u32 s31, s31, s55
	s_waitcnt lgkmcnt(0)
; #define MD_GLDS_A(buf, tau) do { _Pragma("unroll") for (int i = 0; i < 5; ++i) if (amask & (1u << i)) \
;         __builtin_amdgcn_global_load_lds((const unsigned*)((const char*)HIDp + aoff[i] + (size_t)((tau) & 7) * 128), (PG8_LAS unsigned*)(MD_SA(buf) + wid * 1024 + i * 8192), 16, 0, 0); } while (0)
; #define MD_B_ISSUE(sb, tau) do { const char* kb_ = Bb + (size_t)((tau) >> 3) * 512 + (size_t)((tau) & 7) * (64 * (size_t)RB); _Pragma("unroll") for (int j = 0; j < 8; ++j) { const char* p_ = kb_ + (size_t)j * RB; \
;         asm volatile("global_load_dwordx2 %0, %1, off" : "=&v"(sb[j]) : "v"(p_) : "memory"); } } while (0)
; #define MD_B_WAIT(sb, N) asm volatile("s_waitcnt vmcnt(%8)" : "+v"(sb[0]), "+v"(sb[1]), "+v"(sb[2]), "+v"(sb[3]), "+v"(sb[4]), "+v"(sb[5]), "+v"(sb[6]), "+v"(sb[7]) : "n"(N) : "memory")
; #define MD_END(last) do { if (last) asm volatile("s_waitcnt vmcnt(0)" ::: "memory"); else asm volatile("s_waitcnt vmcnt(8)" ::: "memory"); \
;         asm volatile("s_waitcnt lgkmcnt(0)" ::: "memory"); __builtin_amdgcn_s_barrier(); asm volatile("" ::: "memory"); } while (0)
; __device__ __forceinline__ void moe_down_stream(PG8_LAS unsigned char* lds, int e, int cb0, int slot0, int nv, const bf16_t* HIDp, const float* Wd, bf16_t* Y, const float* slot_w, const int* slot_dst) {
;     ...
;         if (t + 3 < NT) MD_B_ISSUE(s1, t + 3);
;         MD_COMPUTE(0);
;         MD_END(t + 3 >= NT);
;         if (t + 2 < NT) { MD_B_WAIT(s0, 8); MD_B_WRITE(s0, 0); __builtin_amdgcn_sched_barrier(0); MD_GLDS_A(0, t + 2); __builtin_amdgcn_sched_barrier(0); }
;         if (t + 4 < NT) MD_B_ISSUE(s0, t + 4);
;         MD_COMPUTE(1);
;         MD_END(t + 4 >= NT);
	v_mfma_f32_16x16x32_bf16 v[78:81], v[238:241], v[218:221], v[78:81]
	v_mfma_f32_16x16x32_bf16 v[74:77], v[242:245], v[218:221], v[74:77]
	v_mfma_f32_16x16x32_bf16 v[70:73], v[246:249], v[218:221], v[70:73]
	v_mfma_f32_16x16x32_bf16 v[66:69], v[250:253], v[218:221], v[66:69]
	ds_read_b128 v[218:221], v93 offset:0
	ds_read_b128 v[142:145], v141 offset:0
	s_mov_b32 m0, s49
	s_nop 0
	global_load_lds_dwordx4 v88, s[30:31]
	v_mfma_f32_16x16x32_bf16 v[62:65], v[238:241], v[222:225], v[62:65]
	v_mfma_f32_16x16x32_bf16 v[58:61], v[242:245], v[222:225], v[58:61]
	v_mfma_f32_16x16x32_bf16 v[54:57], v[246:249], v[222:225], v[54:57]
	v_mfma_f32_16x16x32_bf16 v[50:53], v[250:253], v[222:225], v[50:53]
	ds_read_b128 v[222:225], v93 offset:2048
	ds_read_b128 v[146:149], v141 offset:2048
	s_add_i32 m0, s49, 0x2000
	s_nop 0
	global_load_lds_dwordx4 v90, s[30:31]
	v_mfma_f32_16x16x32_bf16 v[46:49], v[238:241], v[226:229], v[46:49]
	v_mfma_f32_16x16x32_bf16 v[42:45], v[242:245], v[226:229], v[42:45]
	v_mfma_f32_16x16x32_bf16 v[38:41], v[246:249], v[226:229], v[38:41]
	v_mfma_f32_16x16x32_bf16 v[34:37], v[250:253], v[226:229], v[34:37]
	ds_read_b128 v[226:229], v93 offset:4096
	ds_read_b128 v[156:159], v141 offset:4096
	s_add_i32 m0, s49, 0x4000
	s_nop 0
	global_load_lds_dwordx4 v92, s[30:31]
	v_mfma_f32_16x16x32_bf16 v[18:21], v[238:241], v[230:233], v[18:21]
	v_mfma_f32_16x16x32_bf16 v[22:25], v[242:245], v[230:233], v[22:25]
	v_mfma_f32_16x16x32_bf16 v[26:29], v[246:249], v[230:233], v[26:29]
	v_mfma_f32_16x16x32_bf16 v[30:33], v[250:253], v[230:233], v[30:33]
	ds_read_b128 v[230:233], v93 offset:6144
	ds_read_b128 v[160:163], v141 offset:6144
	s_add_i32 m0, s49, 0x6000
	s_nop 0
	global_load_lds_dwordx4 v94, s[30:31]
	v_mfma_f32_16x16x32_bf16 v[2:5], v[238:241], v[234:237], v[2:5]
	v_mfma_f32_16x16x32_bf16 v[6:9], v[242:245], v[234:237], v[6:9]
	v_mfma_f32_16x16x32_bf16 v[10:13], v[246:249], v[234:237], v[10:13]
	v_mfma_f32_16x16x32_bf16 v[14:17], v[250:253], v[234:237], v[14:17]
	ds_read_b128 v[234:237], v93 offset:8192
	s_add_i32 m0, s49, 0x8000
	s_nop 0
	global_load_lds_dwordx4 v96, s[30:31]
	s_waitcnt lgkmcnt(0)
	v_mfma_f32_16x16x32_bf16 v[78:81], v[142:145], v[218:221], v[78:81]
	v_mfma_f32_16x16x32_bf16 v[74:77], v[146:149], v[218:221], v[74:77]
	v_mfma_f32_16x16x32_bf16 v[70:73], v[156:159], v[218:221], v[70:73]
	v_mfma_f32_16x16x32_bf16 v[66:69], v[160:163], v[218:221], v[66:69]
	s_add_i32 s51, s51, 1
	s_and_b32 s54, s51, 7
	s_cmp_eq_u32 s54, 0
	s_cselect_b32 s44, s34, s35
	s_cselect_b32 s45, -1, 0
	v_lshl_add_u64 v[132:133], v[132:133], 0, s[44:45]
	global_load_dwordx2 v[114:115], v[132:133], off
	v_lshl_add_u64 v[180:181], v[132:133], 0, s[24:25]
	global_load_dwordx2 v[116:117], v[180:181], off
	v_mfma_f32_16x16x32_bf16 v[62:65], v[142:145], v[222:225], v[62:65]
	v_mfma_f32_16x16x32_bf16 v[58:61], v[146:149], v[222:225], v[58:61]
	v_mfma_f32_16x16x32_bf16 v[54:57], v[156:159], v[222:225], v[54:57]
	v_mfma_f32_16x16x32_bf16 v[50:53], v[160:163], v[222:225], v[50:53]
	v_lshl_add_u64 v[180:181], v[132:133], 0, s[26:27]
	global_load_dwordx2 v[118:119], v[180:181], off
	v_lshl_add_u64 v[180:181], v[132:133], 0, s[28:29]
	global_load_dwordx2 v[120:121], v[180:181], off
	v_mfma_f32_16x16x32_bf16 v[46:49], v[142:145], v[226:229], v[46:49]
	v_mfma_f32_16x16x32_bf16 v[42:45], v[146:149], v[226:229], v[42:45]
	v_mfma_f32_16x16x32_bf16 v[38:41], v[156:159], v[226:229], v[38:41]
	v_mfma_f32_16x16x32_bf16 v[34:37], v[160:163], v[226:229], v[34:37]
	v_lshl_add_u64 v[180:181], v[132:133], 0, s[36:37]
	global_load_dwordx2 v[122:123], v[180:181], off
	v_lshl_add_u64 v[180:181], v[132:133], 0, s[38:39]
	global_load_dwordx2 v[124:125], v[180:181], off
	v_mfma_f32_16x16x32_bf16 v[18:21], v[142:145], v[230:233], v[18:21]
	v_mfma_f32_16x16x32_bf16 v[22:25], v[146:149], v[230:233], v[22:25]
	v_mfma_f32_16x16x32_bf16 v[26:29], v[156:159], v[230:233], v[26:29]
	v_mfma_f32_16x16x32_bf16 v[30:33], v[160:163], v[230:233], v[30:33]
	v_lshl_add_u64 v[180:181], v[132:133], 0, s[40:41]
	global_load_dwordx2 v[126:127], v[180:181], off
	v_lshl_add_u64 v[180:181], v[132:133], 0, s[42:43]
	global_load_dwordx2 v[128:129], v[180:181], off
	v_mfma_f32_16x16x32_bf16 v[2:5], v[142:145], v[234:237], v[2:5]
	v_mfma_f32_16x16x32_bf16 v[6:9], v[146:149], v[234:237], v[6:9]
	v_mfma_f32_16x16x32_bf16 v[10:13], v[156:159], v[234:237], v[10:13]
	v_mfma_f32_16x16x32_bf16 v[14:17], v[160:163], v[234:237], v[14:17]
	s_waitcnt vmcnt(31)
	s_waitcnt lgkmcnt(0)
	s_barrier
; #define MD_GLDS_A(buf, tau) do { _Pragma("unroll") for (int i = 0; i < 5; ++i) if (amask & (1u << i)) \
;         __builtin_amdgcn_global_load_lds((const unsigned*)((const char*)HIDp + aoff[i] + (size_t)((tau) & 7) * 128), (PG8_LAS unsigned*)(MD_SA(buf) + wid * 1024 + i * 8192), 16, 0, 0); } while (0)
; #define MD_B_ISSUE(sb, tau) do { const char* kb_ = Bb + (size_t)((tau) >> 3) * 512 + (size_t)((tau) & 7) * (64 * (size_t)RB); _Pragma("unroll") for (int j = 0; j < 8; ++j) { const char* p_ = kb_ + (size_t)j * RB; \
;         asm volatile("global_load_dwordx2 %0, %1, off" : "=&v"(sb[j]) : "v"(p_) : "memory"); } } while (0)
; #define MD_B_WAIT(sb, N) asm volatile("s_waitcnt vmcnt(%8)" : "+v"(sb[0]), "+v"(sb[1]), "+v"(sb[2]), "+v"(sb[3]), "+v"(sb[4]), "+v"(sb[5]), "+v"(sb[6]), "+v"(sb[7]) : "n"(N) : "memory")
; #define MD_END(last) do { if (last) asm volatile("s_waitcnt vmcnt(0)" ::: "memory"); else asm volatile("s_waitcnt vmcnt(8)" ::: "memory"); \
;         asm volatile("s_waitcnt lgkmcnt(0)" ::: "memory"); __builtin_amdgcn_s_barrier(); asm volatile("" ::: "memory"); } while (0)
; __device__ __forceinline__ void moe_down_stream(PG8_LAS unsigned char* lds, int e, int cb0, int slot0, int nv, const bf16_t* HIDp, const float* Wd, bf16_t* Y, const float* slot_w, const int* slot_dst) {
;     ...
;     for (int t = 0; t < NT; t += 2) {
;         if (t + 2 < NT) MD_B_WAIT(s1, 8); else MD_B_WAIT(s1, 0);
;         MD_B_WRITE(s1, 1); __builtin_amdgcn_sched_barrier(0); MD_GLDS_A(1, t + 1); __builtin_amdgcn_sched_barrier(0);
;         if (t + 3 < NT) MD_B_ISSUE(s1, t + 3);
;         MD_COMPUTE(0);
;         MD_END(t + 3 >= NT);
;         if (t + 2 < NT) { MD_B_WAIT(s0, 8); MD_B_WRITE(s0, 0); __builtin_amdgcn_sched_barrier(0); MD_GLDS_A(0, t + 2); __builtin_amdgcn_sched_barrier(0); }
;         if (t + 4 < NT) MD_B_ISSUE(s0, t + 4);
;         MD_COMPUTE(1);
;         MD_END(t + 4 >= NT);
	s_mov_b32 s49, s46
	s_mov_b32 s46, s47
	s_mov_b32 s47, s48
	s_mov_b32 s48, s49
	v_cvt_pk_bf16_f32 v172, v186, v188
	v_cvt_pk_bf16_f32 v173, v190, v192
	v_cvt_pk_bf16_f32 v174, v194, v196
	v_cvt_pk_bf16_f32 v175, v198, v200
	v_cvt_pk_bf16_f32 v176, v187, v189
	v_cvt_pk_bf16_f32 v177, v191, v193
	v_cvt_pk_bf16_f32 v178, v195, v197
	v_cvt_pk_bf16_f32 v179, v199, v201
	ds_write_b128 v95, v[172:175] offset:0
	ds_write_b128 v95, v[176:179] offset:128
	v_add_u32_e32 v91, s46, v135
	v_add_u32_e32 v93, s46, v137
	ds_read_b128 v[238:241], v139 offset:19456
	ds_read_b128 v[242:245], v139 offset:21504
	ds_read_b128 v[246:249], v139 offset:23552
	ds_read_b128 v[250:253], v139 offset:25600
	ds_read_b128 v[218:221], v91 offset:0
	ds_read_b128 v[222:225], v91 offset:2048
	ds_read_b128 v[226:229], v91 offset:4096
	ds_read_b128 v[230:233], v91 offset:6144
	ds_read_b128 v[234:237], v91 offset:8192
	s_add_i32 s49, s48, s74
	s_add_i32 s52, s52, 1
	s_and_b32 s54, s52, 7
	s_cmp_eq_u32 s54, 0
	s_cselect_b32 s54, s53, s32
	s_cselect_b32 s55, -1, 0
	s_add_u32 s30, s30, s54
	s_addc_u32 s31, s31, s55
	s_waitcnt lgkmcnt(0)
	v_mfma_f32_16x16x32_bf16 v[78:81], v[238:241], v[218:221], v[78:81]
	v_mfma_f32_16x16x32_bf16 v[74:77], v[242:245], v[218:221], v[74:77]
	v_mfma_f32_16x16x32_bf16 v[70:73], v[246:249], v[218:221], v[70:73]
	v_mfma_f32_16x16x32_bf16 v[66:69], v[250:253], v[218:221], v[66:69]
	ds_read_b128 v[218:221], v93 offset:0
	ds_read_b128 v[142:145], v141 offset:19456
	s_mov_b32 m0, s49
	s_nop 0
	global_load_lds_dwordx4 v88, s[30:31]
	v_mfma_f32_16x16x32_bf16 v[62:65], v[238:241], v[222:225], v[62:65]
	v_mfma_f32_16x16x32_bf16 v[58:61], v[242:245], v[222:225], v[58:61]
	v_mfma_f32_16x16x32_bf16 v[54:57], v[246:249], v[222:225], v[54:57]
	v_mfma_f32_16x16x32_bf16 v[50:53], v[250:253], v[222:225], v[50:53]
	ds_read_b128 v[222:225], v93 offset:2048
	ds_read_b128 v[146:149], v141 offset:21504
	s_add_i32 m0, s49, 0x2000
	s_nop 0
	global_load_lds_dwordx4 v90, s[30:31]
	v_mfma_f32_16x16x32_bf16 v[46:49], v[238:241], v[226:229], v[46:49]
	v_mfma_f32_16x16x32_bf16 v[42:45], v[242:245], v[226:229], v[42:45]
	v_mfma_f32_16x16x32_bf16 v[38:41], v[246:249], v[226:229], v[38:41]
	v_mfma_f32_16x16x32_bf16 v[34:37], v[250:253], v[226:229], v[34:37]
	ds_read_b128 v[226:229], v93 offset:4096
	ds_read_b128 v[156:159], v141 offset:23552
	s_add_i32 m0, s49, 0x4000
	s_nop 0
	global_load_lds_dwordx4 v92, s[30:31]
	v_mfma_f32_16x16x32_bf16 v[18:21], v[238:241], v[230:233], v[18:21]
	v_mfma_f32_16x16x32_bf16 v[22:25], v[242:245], v[230:233], v[22:25]
	v_mfma_f32_16x16x32_bf16 v[26:29], v[246:249], v[230:233], v[26:29]
	v_mfma_f32_16x16x32_bf16 v[30:33], v[250:253], v[230:233], v[30:33]
	ds_read_b128 v[230:233], v93 offset:6144
	ds_read_b128 v[160:163], v141 offset:25600
	s_add_i32 m0, s49, 0x6000
	s_nop 0
	global_load_lds_dwordx4 v94, s[30:31]
	v_mfma_f32_16x16x32_bf16 v[2:5], v[238:241], v[234:237], v[2:5]
	v_mfma_f32_16x16x32_bf16 v[6:9], v[242:245], v[234:237], v[6:9]
	v_mfma_f32_16x16x32_bf16 v[10:13], v[246:249], v[234:237], v[10:13]
	v_mfma_f32_16x16x32_bf16 v[14:17], v[250:253], v[234:237], v[14:17]
	ds_read_b128 v[234:237], v93 offset:8192
	s_add_i32 m0, s49, 0x8000
	s_nop 0
	global_load_lds_dwordx4 v96, s[30:31]
	s_waitcnt lgkmcnt(0)
	v_mfma_f32_16x16x32_bf16 v[78:81], v[142:145], v[218:221], v[78:81]
	v_mfma_f32_16x16x32_bf16 v[74:77], v[146:149], v[218:221], v[74:77]
	v_mfma_f32_16x16x32_bf16 v[70:73], v[156:159], v[218:221], v[70:73]
	v_mfma_f32_16x16x32_bf16 v[66:69], v[160:163], v[218:221], v[66:69]
	s_add_i32 s51, s51, 1
	s_and_b32 s54, s51, 7
	s_cmp_eq_u32 s54, 0
	s_cselect_b32 s44, s34, s35
	s_cselect_b32 s45, -1, 0
	v_lshl_add_u64 v[132:133], v[132:133], 0, s[44:45]
	global_load_dwordx2 v[186:187], v[132:133], off
	v_lshl_add_u64 v[180:181], v[132:133], 0, s[24:25]
	global_load_dwordx2 v[188:189], v[180:181], off
	v_mfma_f32_16x16x32_bf16 v[62:65], v[142:145], v[222:225], v[62:65]
	v_mfma_f32_16x16x32_bf16 v[58:61], v[146:149], v[222:225], v[58:61]
	v_mfma_f32_16x16x32_bf16 v[54:57], v[156:159], v[222:225], v[54:57]
	v_mfma_f32_16x16x32_bf16 v[50:53], v[160:163], v[222:225], v[50:53]
	v_lshl_add_u64 v[180:181], v[132:133], 0, s[26:27]
	global_load_dwordx2 v[190:191], v[180:181], off
	v_lshl_add_u64 v[180:181], v[132:133], 0, s[28:29]
	global_load_dwordx2 v[192:193], v[180:181], off
	v_mfma_f32_16x16x32_bf16 v[46:49], v[142:145], v[226:229], v[46:49]
	v_mfma_f32_16x16x32_bf16 v[42:45], v[146:149], v[226:229], v[42:45]
	v_mfma_f32_16x16x32_bf16 v[38:41], v[156:159], v[226:229], v[38:41]
	v_mfma_f32_16x16x32_bf16 v[34:37], v[160:163], v[226:229], v[34:37]
	v_lshl_add_u64 v[180:181], v[132:133], 0, s[36:37]
	global_load_dwordx2 v[194:195], v[180:181], off
	v_lshl_add_u64 v[180:181], v[132:133], 0, s[38:39]
	global_load_dwordx2 v[196:197], v[180:181], off
	v_mfma_f32_16x16x32_bf16 v[18:21], v[142:145], v[230:233], v[18:21]
	v_mfma_f32_16x16x32_bf16 v[22:25], v[146:149], v[230:233], v[22:25]
	v_mfma_f32_16x16x32_bf16 v[26:29], v[156:159], v[230:233], v[26:29]
	v_mfma_f32_16x16x32_bf16 v[30:33], v[160:163], v[230:233], v[30:33]
	v_lshl_add_u64 v[180:181], v[132:133], 0, s[40:41]
	global_load_dwordx2 v[198:199], v[180:181], off
	v_lshl_add_u64 v[180:181], v[132:133], 0, s[42:43]
	global_load_dwordx2 v[200:201], v[180:181], off
	v_mfma_f32_16x16x32_bf16 v[2:5], v[142:145], v[234:237], v[2:5]
	v_mfma_f32_16x16x32_bf16 v[6:9], v[146:149], v[234:237], v[6:9]
	v_mfma_f32_16x16x32_bf16 v[10:13], v[156:159], v[234:237], v[10:13]
	v_mfma_f32_16x16x32_bf16 v[14:17], v[160:163], v[234:237], v[14:17]
	s_waitcnt vmcnt(21)
	s_waitcnt lgkmcnt(0)
	s_barrier
; #define MD_GLDS_A(buf, tau) do { _Pragma("unroll") for (int i = 0; i < 5; ++i) if (amask & (1u << i)) \
;         __builtin_amdgcn_global_load_lds((const unsigned*)((const char*)HIDp + aoff[i] + (size_t)((tau) & 7) * 128), (PG8_LAS unsigned*)(MD_SA(buf) + wid * 1024 + i * 8192), 16, 0, 0); } while (0)
; #define MD_B_ISSUE(sb, tau) do { const char* kb_ = Bb + (size_t)((tau) >> 3) * 512 + (size_t)((tau) & 7) * (64 * (size_t)RB); _Pragma("unroll") for (int j = 0; j < 8; ++j) { const char* p_ = kb_ + (size_t)j * RB; \
;         asm volatile("global_load_dwordx2 %0, %1, off" : "=&v"(sb[j]) : "v"(p_) : "memory"); } } while (0)
; #define MD_B_WAIT(sb, N) asm volatile("s_waitcnt vmcnt(%8)" : "+v"(sb[0]), "+v"(sb[1]), "+v"(sb[2]), "+v"(sb[3]), "+v"(sb[4]), "+v"(sb[5]), "+v"(sb[6]), "+v"(sb[7]) : "n"(N) : "memory")
; #define MD_END(last) do { if (last) asm volatile("s_waitcnt vmcnt(0)" ::: "memory"); else asm volatile("s_waitcnt vmcnt(8)" ::: "memory"); \
;         asm volatile("s_waitcnt lgkmcnt(0)" ::: "memory"); __builtin_amdgcn_s_barrier(); asm volatile("" ::: "memory"); } while (0)
; __device__ __forceinline__ void moe_down_stream(PG8_LAS unsigned char* lds, int e, int cb0, int slot0, int nv, const bf16_t* HIDp, const float* Wd, bf16_t* Y, const float* slot_w, const int* slot_dst) {
;     ...
;     for (int t = 0; t < NT; t += 2) {
;         if (t + 2 < NT) MD_B_WAIT(s1, 8); else MD_B_WAIT(s1, 0);
;         MD_B_WRITE(s1, 1); __builtin_amdgcn_sched_barrier(0); MD_GLDS_A(1, t + 1); __builtin_amdgcn_sched_barrier(0);
;         if (t + 3 < NT) MD_B_ISSUE(s1, t + 3);
;         MD_COMPUTE(0);
;         MD_END(t + 3 >= NT);
;         if (t + 2 < NT) { MD_B_WAIT(s0, 8); MD_B_WRITE(s0, 0); __builtin_amdgcn_sched_barrier(0); MD_GLDS_A(0, t + 2); __builtin_amdgcn_sched_barrier(0); }
;         if (t + 4 < NT) MD_B_ISSUE(s0, t + 4);
;         MD_COMPUTE(1);
;         MD_END(t + 4 >= NT);
	s_mov_b32 s49, s46
	s_mov_b32 s46, s47
	s_mov_b32 s47, s48
	s_mov_b32 s48, s49
	v_cvt_pk_bf16_f32 v172, v202, v204
	v_cvt_pk_bf16_f32 v173, v206, v208
	v_cvt_pk_bf16_f32 v174, v210, v212
	v_cvt_pk_bf16_f32 v175, v214, v216
	v_cvt_pk_bf16_f32 v176, v203, v205
	v_cvt_pk_bf16_f32 v177, v207, v209
	v_cvt_pk_bf16_f32 v178, v211, v213
	v_cvt_pk_bf16_f32 v179, v215, v217
	ds_write_b128 v95, v[172:175] offset:19456
	ds_write_b128 v95, v[176:179] offset:19584
	v_add_u32_e32 v91, s46, v135
	v_add_u32_e32 v93, s46, v137
	ds_read_b128 v[238:241], v139 offset:0
	ds_read_b128 v[242:245], v139 offset:2048
	ds_read_b128 v[246:249], v139 offset:4096
	ds_read_b128 v[250:253], v139 offset:6144
	ds_read_b128 v[218:221], v91 offset:0
	ds_read_b128 v[222:225], v91 offset:2048
	ds_read_b128 v[226:229], v91 offset:4096
	ds_read_b128 v[230:233], v91 offset:6144
	ds_read_b128 v[234:237], v91 offset:8192
	s_add_i32 s49, s48, s74
	s_add_i32 s52, s52, 1
	s_and_b32 s54, s52, 7
	s_cmp_eq_u32 s54, 0
	s_cselect_b32 s54, s53, s32
	s_cselect_b32 s55, -1, 0
	s_add_u32 s30, s30, s54
	s_addc_u32 s31, s31, s55
	s_waitcnt lgkmcnt(0)
	v_mfma_f32_16x16x32_bf16 v[78:81], v[238:241], v[218:221], v[78:81]
	v_mfma_f32_16x16x32_bf16 v[74:77], v[242:245], v[218:221], v[74:77]
	v_mfma_f32_16x16x32_bf16 v[70:73], v[246:249], v[218:221], v[70:73]
	v_mfma_f32_16x16x32_bf16 v[66:69], v[250:253], v[218:221], v[66:69]
	ds_read_b128 v[218:221], v93 offset:0
	ds_read_b128 v[142:145], v141 offset:0
	s_mov_b32 m0, s49
	s_nop 0
	global_load_lds_dwordx4 v88, s[30:31]
	v_mfma_f32_16x16x32_bf16 v[62:65], v[238:241], v[222:225], v[62:65]
	v_mfma_f32_16x16x32_bf16 v[58:61], v[242:245], v[222:225], v[58:61]
	v_mfma_f32_16x16x32_bf16 v[54:57], v[246:249], v[222:225], v[54:57]
	v_mfma_f32_16x16x32_bf16 v[50:53], v[250:253], v[222:225], v[50:53]
	ds_read_b128 v[222:225], v93 offset:2048
	ds_read_b128 v[146:149], v141 offset:2048
	s_add_i32 m0, s49, 0x2000
	s_nop 0
	global_load_lds_dwordx4 v90, s[30:31]
	v_mfma_f32_16x16x32_bf16 v[46:49], v[238:241], v[226:229], v[46:49]
	v_mfma_f32_16x16x32_bf16 v[42:45], v[242:245], v[226:229], v[42:45]
	v_mfma_f32_16x16x32_bf16 v[38:41], v[246:249], v[226:229], v[38:41]
	v_mfma_f32_16x16x32_bf16 v[34:37], v[250:253], v[226:229], v[34:37]
	ds_read_b128 v[226:229], v93 offset:4096
	ds_read_b128 v[156:159], v141 offset:4096
	s_add_i32 m0, s49, 0x4000
	s_nop 0
	global_load_lds_dwordx4 v92, s[30:31]
	v_mfma_f32_16x16x32_bf16 v[18:21], v[238:241], v[230:233], v[18:21]
	v_mfma_f32_16x16x32_bf16 v[22:25], v[242:245], v[230:233], v[22:25]
	v_mfma_f32_16x16x32_bf16 v[26:29], v[246:249], v[230:233], v[26:29]
	v_mfma_f32_16x16x32_bf16 v[30:33], v[250:253], v[230:233], v[30:33]
	ds_read_b128 v[230:233], v93 offset:6144
	ds_read_b128 v[160:163], v141 offset:6144
	s_add_i32 m0, s49, 0x6000
	s_nop 0
	global_load_lds_dwordx4 v94, s[30:31]
	v_mfma_f32_16x16x32_bf16 v[2:5], v[238:241], v[234:237], v[2:5]
	v_mfma_f32_16x16x32_bf16 v[6:9], v[242:245], v[234:237], v[6:9]
	v_mfma_f32_16x16x32_bf16 v[10:13], v[246:249], v[234:237], v[10:13]
	v_mfma_f32_16x16x32_bf16 v[14:17], v[250:253], v[234:237], v[14:17]
	ds_read_b128 v[234:237], v93 offset:8192
	s_add_i32 m0, s49, 0x8000
	s_nop 0
	global_load_lds_dwordx4 v96, s[30:31]
	s_waitcnt lgkmcnt(0)
	v_mfma_f32_16x16x32_bf16 v[78:81], v[142:145], v[218:221], v[78:81]
	v_mfma_f32_16x16x32_bf16 v[74:77], v[146:149], v[218:221], v[74:77]
	v_mfma_f32_16x16x32_bf16 v[70:73], v[156:159], v[218:221], v[70:73]
	v_mfma_f32_16x16x32_bf16 v[66:69], v[160:163], v[218:221], v[66:69]
	s_add_i32 s51, s51, 1
	s_and_b32 s54, s51, 7
	s_cmp_eq_u32 s54, 0
	s_cselect_b32 s44, s34, s35
	s_cselect_b32 s45, -1, 0
	v_lshl_add_u64 v[132:133], v[132:133], 0, s[44:45]
	global_load_dwordx2 v[202:203], v[132:133], off
	v_lshl_add_u64 v[180:181], v[132:133], 0, s[24:25]
	global_load_dwordx2 v[204:205], v[180:181], off
	v_mfma_f32_16x16x32_bf16 v[62:65], v[142:145], v[222:225], v[62:65]
	v_mfma_f32_16x16x32_bf16 v[58:61], v[146:149], v[222:225], v[58:61]
	v_mfma_f32_16x16x32_bf16 v[54:57], v[156:159], v[222:225], v[54:57]
	v_mfma_f32_16x16x32_bf16 v[50:53], v[160:163], v[222:225], v[50:53]
	v_lshl_add_u64 v[180:181], v[132:133], 0, s[26:27]
	global_load_dwordx2 v[206:207], v[180:181], off
	v_lshl_add_u64 v[180:181], v[132:133], 0, s[28:29]
	global_load_dwordx2 v[208:209], v[180:181], off
	v_mfma_f32_16x16x32_bf16 v[46:49], v[142:145], v[226:229], v[46:49]
	v_mfma_f32_16x16x32_bf16 v[42:45], v[146:149], v[226:229], v[42:45]
	v_mfma_f32_16x16x32_bf16 v[38:41], v[156:159], v[226:229], v[38:41]
	v_mfma_f32_16x16x32_bf16 v[34:37], v[160:163], v[226:229], v[34:37]
	v_lshl_add_u64 v[180:181], v[132:133], 0, s[36:37]
	global_load_dwordx2 v[210:211], v[180:181], off
	v_lshl_add_u64 v[180:181], v[132:133], 0, s[38:39]
	global_load_dwordx2 v[212:213], v[180:181], off
	v_mfma_f32_16x16x32_bf16 v[18:21], v[142:145], v[230:233], v[18:21]
	v_mfma_f32_16x16x32_bf16 v[22:25], v[146:149], v[230:233], v[22:25]
	v_mfma_f32_16x16x32_bf16 v[26:29], v[156:159], v[230:233], v[26:29]
	v_mfma_f32_16x16x32_bf16 v[30:33], v[160:163], v[230:233], v[30:33]
	v_lshl_add_u64 v[180:181], v[132:133], 0, s[40:41]
	global_load_dwordx2 v[214:215], v[180:181], off
	v_lshl_add_u64 v[180:181], v[132:133], 0, s[42:43]
	global_load_dwordx2 v[216:217], v[180:181], off
	v_mfma_f32_16x16x32_bf16 v[2:5], v[142:145], v[234:237], v[2:5]
	v_mfma_f32_16x16x32_bf16 v[6:9], v[146:149], v[234:237], v[6:9]
	v_mfma_f32_16x16x32_bf16 v[10:13], v[156:159], v[234:237], v[10:13]
	v_mfma_f32_16x16x32_bf16 v[14:17], v[160:163], v[234:237], v[14:17]
	s_waitcnt vmcnt(21)
	s_waitcnt lgkmcnt(0)
	s_barrier
; #define MD_GLDS_A(buf, tau) do { _Pragma("unroll") for (int i = 0; i < 5; ++i) if (amask & (1u << i)) \
;         __builtin_amdgcn_global_load_lds((const unsigned*)((const char*)HIDp + aoff[i] + (size_t)((tau) & 7) * 128), (PG8_LAS unsigned*)(MD_SA(buf) + wid * 1024 + i * 8192), 16, 0, 0); } while (0)
; #define MD_B_ISSUE(sb, tau) do { const char* kb_ = Bb + (size_t)((tau) >> 3) * 512 + (size_t)((tau) & 7) * (64 * (size_t)RB); _Pragma("unroll") for (int j = 0; j < 8; ++j) { const char* p_ = kb_ + (size_t)j * RB; \
;         asm volatile("global_load_dwordx2 %0, %1, off" : "=&v"(sb[j]) : "v"(p_) : "memory"); } } while (0)
; #define MD_B_WAIT(sb, N) asm volatile("s_waitcnt vmcnt(%8)" : "+v"(sb[0]), "+v"(sb[1]), "+v"(sb[2]), "+v"(sb[3]), "+v"(sb[4]), "+v"(sb[5]), "+v"(sb[6]), "+v"(sb[7]) : "n"(N) : "memory")
; #define MD_END(last) do { if (last) asm volatile("s_waitcnt vmcnt(0)" ::: "memory"); else asm volatile("s_waitcnt vmcnt(8)" ::: "memory"); \
;         asm volatile("s_waitcnt lgkmcnt(0)" ::: "memory"); __builtin_amdgcn_s_barrier(); asm volatile("" ::: "memory"); } while (0)
; __device__ __forceinline__ void moe_down_stream(PG8_LAS unsigned char* lds, int e, int cb0, int slot0, int nv, const bf16_t* HIDp, const float* Wd, bf16_t* Y, const float* slot_w, const int* slot_dst) {
;     ...
;     for (int t = 0; t < NT; t += 2) {
;         if (t + 2 < NT) MD_B_WAIT(s1, 8); else MD_B_WAIT(s1, 0);
;         MD_B_WRITE(s1, 1); __builtin_amdgcn_sched_barrier(0); MD_GLDS_A(1, t + 1); __builtin_amdgcn_sched_barrier(0);
;         if (t + 3 < NT) MD_B_ISSUE(s1, t + 3);
;         MD_COMPUTE(0);
;         MD_END(t + 3 >= NT);
;         if (t + 2 < NT) { MD_B_WAIT(s0, 8); MD_B_WRITE(s0, 0); __builtin_amdgcn_sched_barrier(0); MD_GLDS_A(0, t + 2); __builtin_amdgcn_sched_barrier(0); }
;         if (t + 4 < NT) MD_B_ISSUE(s0, t + 4);
;         MD_COMPUTE(1);
;         MD_END(t + 4 >= NT);
	s_mov_b32 s49, s46
	s_mov_b32 s46, s47
	s_mov_b32 s47, s48
	s_mov_b32 s48, s49
	v_cvt_pk_bf16_f32 v172, v98, v100
	v_cvt_pk_bf16_f32 v173, v102, v104
	v_cvt_pk_bf16_f32 v174, v106, v108
	v_cvt_pk_bf16_f32 v175, v110, v112
	v_cvt_pk_bf16_f32 v176, v99, v101
	v_cvt_pk_bf16_f32 v177, v103, v105
	v_cvt_pk_bf16_f32 v178, v107, v109
	v_cvt_pk_bf16_f32 v179, v111, v113
	ds_write_b128 v95, v[172:175] offset:0
	ds_write_b128 v95, v[176:179] offset:128
	v_add_u32_e32 v91, s46, v135
	v_add_u32_e32 v93, s46, v137
	ds_read_b128 v[238:241], v139 offset:19456
	ds_read_b128 v[242:245], v139 offset:21504
	ds_read_b128 v[246:249], v139 offset:23552
	ds_read_b128 v[250:253], v139 offset:25600
	ds_read_b128 v[218:221], v91 offset:0
	ds_read_b128 v[222:225], v91 offset:2048
	ds_read_b128 v[226:229], v91 offset:4096
	ds_read_b128 v[230:233], v91 offset:6144
	ds_read_b128 v[234:237], v91 offset:8192
	s_add_i32 s49, s48, s74
	s_add_i32 s52, s52, 1
	s_and_b32 s54, s52, 7
	s_cmp_eq_u32 s54, 0
	s_cselect_b32 s54, s53, s32
	s_cselect_b32 s55, -1, 0
	s_add_u32 s30, s30, s54
	s_addc_u32 s31, s31, s55
	s_waitcnt lgkmcnt(0)
	v_mfma_f32_16x16x32_bf16 v[78:81], v[238:241], v[218:221], v[78:81]
	v_mfma_f32_16x16x32_bf16 v[74:77], v[242:245], v[218:221], v[74:77]
	v_mfma_f32_16x16x32_bf16 v[70:73], v[246:249], v[218:221], v[70:73]
	v_mfma_f32_16x16x32_bf16 v[66:69], v[250:253], v[218:221], v[66:69]
	ds_read_b128 v[218:221], v93 offset:0
	ds_read_b128 v[142:145], v141 offset:19456
	s_mov_b32 m0, s49
	s_nop 0
	global_load_lds_dwordx4 v88, s[30:31]
	v_mfma_f32_16x16x32_bf16 v[62:65], v[238:241], v[222:225], v[62:65]
	v_mfma_f32_16x16x32_bf16 v[58:61], v[242:245], v[222:225], v[58:61]
	v_mfma_f32_16x16x32_bf16 v[54:57], v[246:249], v[222:225], v[54:57]
	v_mfma_f32_16x16x32_bf16 v[50:53], v[250:253], v[222:225], v[50:53]
	ds_read_b128 v[222:225], v93 offset:2048
	ds_read_b128 v[146:149], v141 offset:21504
	s_add_i32 m0, s49, 0x2000
	s_nop 0
	global_load_lds_dwordx4 v90, s[30:31]
	v_mfma_f32_16x16x32_bf16 v[46:49], v[238:241], v[226:229], v[46:49]
	v_mfma_f32_16x16x32_bf16 v[42:45], v[242:245], v[226:229], v[42:45]
	v_mfma_f32_16x16x32_bf16 v[38:41], v[246:249], v[226:229], v[38:41]
	v_mfma_f32_16x16x32_bf16 v[34:37], v[250:253], v[226:229], v[34:37]
	ds_read_b128 v[226:229], v93 offset:4096
	ds_read_b128 v[156:159], v141 offset:23552
	s_add_i32 m0, s49, 0x4000
	s_nop 0
	global_load_lds_dwordx4 v92, s[30:31]
	v_mfma_f32_16x16x32_bf16 v[18:21], v[238:241], v[230:233], v[18:21]
	v_mfma_f32_16x16x32_bf16 v[22:25], v[242:245], v[230:233], v[22:25]
	v_mfma_f32_16x16x32_bf16 v[26:29], v[246:249], v[230:233], v[26:29]
	v_mfma_f32_16x16x32_bf16 v[30:33], v[250:253], v[230:233], v[30:33]
	ds_read_b128 v[230:233], v93 offset:6144
	ds_read_b128 v[160:163], v141 offset:25600
	s_add_i32 m0, s49, 0x6000
	s_nop 0
	global_load_lds_dwordx4 v94, s[30:31]
	v_mfma_f32_16x16x32_bf16 v[2:5], v[238:241], v[234:237], v[2:5]
	v_mfma_f32_16x16x32_bf16 v[6:9], v[242:245], v[234:237], v[6:9]
	v_mfma_f32_16x16x32_bf16 v[10:13], v[246:249], v[234:237], v[10:13]
	v_mfma_f32_16x16x32_bf16 v[14:17], v[250:253], v[234:237], v[14:17]
	ds_read_b128 v[234:237], v93 offset:8192
	s_add_i32 m0, s49, 0x8000
	s_nop 0
	global_load_lds_dwordx4 v96, s[30:31]
	s_waitcnt lgkmcnt(0)
	v_mfma_f32_16x16x32_bf16 v[78:81], v[142:145], v[218:221], v[78:81]
	v_mfma_f32_16x16x32_bf16 v[74:77], v[146:149], v[218:221], v[74:77]
	v_mfma_f32_16x16x32_bf16 v[70:73], v[156:159], v[218:221], v[70:73]
	v_mfma_f32_16x16x32_bf16 v[66:69], v[160:163], v[218:221], v[66:69]
	s_add_i32 s51, s51, 1
	s_and_b32 s54, s51, 7
	s_cmp_eq_u32 s54, 0
	s_cselect_b32 s44, s34, s35
	s_cselect_b32 s45, -1, 0
	v_lshl_add_u64 v[132:133], v[132:133], 0, s[44:45]
	global_load_dwordx2 v[98:99], v[132:133], off
	v_lshl_add_u64 v[180:181], v[132:133], 0, s[24:25]
	global_load_dwordx2 v[100:101], v[180:181], off
	v_mfma_f32_16x16x32_bf16 v[62:65], v[142:145], v[222:225], v[62:65]
	v_mfma_f32_16x16x32_bf16 v[58:61], v[146:149], v[222:225], v[58:61]
	v_mfma_f32_16x16x32_bf16 v[54:57], v[156:159], v[222:225], v[54:57]
	v_mfma_f32_16x16x32_bf16 v[50:53], v[160:163], v[222:225], v[50:53]
	v_lshl_add_u64 v[180:181], v[132:133], 0, s[26:27]
	global_load_dwordx2 v[102:103], v[180:181], off
	v_lshl_add_u64 v[180:181], v[132:133], 0, s[28:29]
	global_load_dwordx2 v[104:105], v[180:181], off
	v_mfma_f32_16x16x32_bf16 v[46:49], v[142:145], v[226:229], v[46:49]
	v_mfma_f32_16x16x32_bf16 v[42:45], v[146:149], v[226:229], v[42:45]
	v_mfma_f32_16x16x32_bf16 v[38:41], v[156:159], v[226:229], v[38:41]
	v_mfma_f32_16x16x32_bf16 v[34:37], v[160:163], v[226:229], v[34:37]
	v_lshl_add_u64 v[180:181], v[132:133], 0, s[36:37]
	global_load_dwordx2 v[106:107], v[180:181], off
	v_lshl_add_u64 v[180:181], v[132:133], 0, s[38:39]
	global_load_dwordx2 v[108:109], v[180:181], off
	v_mfma_f32_16x16x32_bf16 v[18:21], v[142:145], v[230:233], v[18:21]
	v_mfma_f32_16x16x32_bf16 v[22:25], v[146:149], v[230:233], v[22:25]
	v_mfma_f32_16x16x32_bf16 v[26:29], v[156:159], v[230:233], v[26:29]
	v_mfma_f32_16x16x32_bf16 v[30:33], v[160:163], v[230:233], v[30:33]
	v_lshl_add_u64 v[180:181], v[132:133], 0, s[40:41]
	global_load_dwordx2 v[110:111], v[180:181], off
	v_lshl_add_u64 v[180:181], v[132:133], 0, s[42:43]
	global_load_dwordx2 v[112:113], v[180:181], off
	v_mfma_f32_16x16x32_bf16 v[2:5], v[142:145], v[234:237], v[2:5]
	v_mfma_f32_16x16x32_bf16 v[6:9], v[146:149], v[234:237], v[6:9]
	v_mfma_f32_16x16x32_bf16 v[10:13], v[156:159], v[234:237], v[10:13]
	v_mfma_f32_16x16x32_bf16 v[14:17], v[160:163], v[234:237], v[14:17]
	s_waitcnt vmcnt(21)
	s_waitcnt lgkmcnt(0)
	s_barrier
; #define MD_GLDS_A(buf, tau) do { _Pragma("unroll") for (int i = 0; i < 5; ++i) if (amask & (1u << i)) \
;         __builtin_amdgcn_global_load_lds((const unsigned*)((const char*)HIDp + aoff[i] + (size_t)((tau) & 7) * 128), (PG8_LAS unsigned*)(MD_SA(buf) + wid * 1024 + i * 8192), 16, 0, 0); } while (0)
; #define MD_B_ISSUE(sb, tau) do { const char* kb_ = Bb + (size_t)((tau) >> 3) * 512 + (size_t)((tau) & 7) * (64 * (size_t)RB); _Pragma("unroll") for (int j = 0; j < 8; ++j) { const char* p_ = kb_ + (size_t)j * RB; \
;         asm volatile("global_load_dwordx2 %0, %1, off" : "=&v"(sb[j]) : "v"(p_) : "memory"); } } while (0)
; #define MD_B_WAIT(sb, N) asm volatile("s_waitcnt vmcnt(%8)" : "+v"(sb[0]), "+v"(sb[1]), "+v"(sb[2]), "+v"(sb[3]), "+v"(sb[4]), "+v"(sb[5]), "+v"(sb[6]), "+v"(sb[7]) : "n"(N) : "memory")
; #define MD_END(last) do { if (last) asm volatile("s_waitcnt vmcnt(0)" ::: "memory"); else asm volatile("s_waitcnt vmcnt(8)" ::: "memory"); \
;         asm volatile("s_waitcnt lgkmcnt(0)" ::: "memory"); __builtin_amdgcn_s_barrier(); asm volatile("" ::: "memory"); } while (0)
; __device__ __forceinline__ void moe_down_stream(PG8_LAS unsigned char* lds, int e, int cb0, int slot0, int nv, const bf16_t* HIDp, const float* Wd, bf16_t* Y, const float* slot_w, const int* slot_dst) {
;     ...
;     for (int t = 0; t < NT; t += 2) {
;         if (t + 2 < NT) MD_B_WAIT(s1, 8); else MD_B_WAIT(s1, 0);
;         MD_B_WRITE(s1, 1); __builtin_amdgcn_sched_barrier(0); MD_GLDS_A(1, t + 1); __builtin_amdgcn_sched_barrier(0);
;         if (t + 3 < NT) MD_B_ISSUE(s1, t + 3);
;         MD_COMPUTE(0);
;         MD_END(t + 3 >= NT);
;         if (t + 2 < NT) { MD_B_WAIT(s0, 8); MD_B_WRITE(s0, 0); __builtin_amdgcn_sched_barrier(0); MD_GLDS_A(0, t + 2); __builtin_amdgcn_sched_barrier(0); }
;         if (t + 4 < NT) MD_B_ISSUE(s0, t + 4);
;         MD_COMPUTE(1);
;         MD_END(t + 4 >= NT);
	s_mov_b32 s49, s46
	s_mov_b32 s46, s47
	s_mov_b32 s47, s48
	s_mov_b32 s48, s49
	v_cvt_pk_bf16_f32 v172, v114, v116
	v_cvt_pk_bf16_f32 v173, v118, v120
	v_cvt_pk_bf16_f32 v174, v122, v124
	v_cvt_pk_bf16_f32 v175, v126, v128
	v_cvt_pk_bf16_f32 v176, v115, v117
	v_cvt_pk_bf16_f32 v177, v119, v121
	v_cvt_pk_bf16_f32 v178, v123, v125
	v_cvt_pk_bf16_f32 v179, v127, v129
	ds_write_b128 v95, v[172:175] offset:19456
	ds_write_b128 v95, v[176:179] offset:19584
	v_add_u32_e32 v91, s46, v135
	v_add_u32_e32 v93, s46, v137
	ds_read_b128 v[238:241], v139 offset:0
	ds_read_b128 v[242:245], v139 offset:2048
	ds_read_b128 v[246:249], v139 offset:4096
	ds_read_b128 v[250:253], v139 offset:6144
	ds_read_b128 v[218:221], v91 offset:0
	ds_read_b128 v[222:225], v91 offset:2048
	ds_read_b128 v[226:229], v91 offset:4096
	ds_read_b128 v[230:233], v91 offset:6144
	ds_read_b128 v[234:237], v91 offset:8192
	s_add_i32 s49, s48, s74
	s_add_i32 s52, s52, 1
	s_and_b32 s54, s52, 7
	s_cmp_eq_u32 s54, 0
	s_cselect_b32 s54, s53, s32
	s_cselect_b32 s55, -1, 0
	s_add_u32 s30, s30, s54
	s_addc_u32 s31, s31, s55
	s_waitcnt lgkmcnt(0)
	v_mfma_f32_16x16x32_bf16 v[78:81], v[238:241], v[218:221], v[78:81]
	v_mfma_f32_16x16x32_bf16 v[74:77], v[242:245], v[218:221], v[74:77]
	v_mfma_f32_16x16x32_bf16 v[70:73], v[246:249], v[218:221], v[70:73]
	v_mfma_f32_16x16x32_bf16 v[66:69], v[250:253], v[218:221], v[66:69]
	ds_read_b128 v[218:221], v93 offset:0
	ds_read_b128 v[142:145], v141 offset:0
	s_mov_b32 m0, s49
	s_nop 0
	global_load_lds_dwordx4 v88, s[30:31]
	v_mfma_f32_16x16x32_bf16 v[62:65], v[238:241], v[222:225], v[62:65]
	v_mfma_f32_16x16x32_bf16 v[58:61], v[242:245], v[222:225], v[58:61]
	v_mfma_f32_16x16x32_bf16 v[54:57], v[246:249], v[222:225], v[54:57]
	v_mfma_f32_16x16x32_bf16 v[50:53], v[250:253], v[222:225], v[50:53]
	ds_read_b128 v[222:225], v93 offset:2048
	ds_read_b128 v[146:149], v141 offset:2048
	s_add_i32 m0, s49, 0x2000
	s_nop 0
	global_load_lds_dwordx4 v90, s[30:31]
	v_mfma_f32_16x16x32_bf16 v[46:49], v[238:241], v[226:229], v[46:49]
	v_mfma_f32_16x16x32_bf16 v[42:45], v[242:245], v[226:229], v[42:45]
	v_mfma_f32_16x16x32_bf16 v[38:41], v[246:249], v[226:229], v[38:41]
	v_mfma_f32_16x16x32_bf16 v[34:37], v[250:253], v[226:229], v[34:37]
	ds_read_b128 v[226:229], v93 offset:4096
	ds_read_b128 v[156:159], v141 offset:4096
	s_add_i32 m0, s49, 0x4000
	s_nop 0
	global_load_lds_dwordx4 v92, s[30:31]
	v_mfma_f32_16x16x32_bf16 v[18:21], v[238:241], v[230:233], v[18:21]
	v_mfma_f32_16x16x32_bf16 v[22:25], v[242:245], v[230:233], v[22:25]
	v_mfma_f32_16x16x32_bf16 v[26:29], v[246:249], v[230:233], v[26:29]
	v_mfma_f32_16x16x32_bf16 v[30:33], v[250:253], v[230:233], v[30:33]
	ds_read_b128 v[230:233], v93 offset:6144
	ds_read_b128 v[160:163], v141 offset:6144
	s_add_i32 m0, s49, 0x6000
	s_nop 0
	global_load_lds_dwordx4 v94, s[30:31]
	v_mfma_f32_16x16x32_bf16 v[2:5], v[238:241], v[234:237], v[2:5]
	v_mfma_f32_16x16x32_bf16 v[6:9], v[242:245], v[234:237], v[6:9]
	v_mfma_f32_16x16x32_bf16 v[10:13], v[246:249], v[234:237], v[10:13]
	v_mfma_f32_16x16x32_bf16 v[14:17], v[250:253], v[234:237], v[14:17]
	ds_read_b128 v[234:237], v93 offset:8192
	s_add_i32 m0, s49, 0x8000
	s_nop 0
	global_load_lds_dwordx4 v96, s[30:31]
	s_waitcnt lgkmcnt(0)
	v_mfma_f32_16x16x32_bf16 v[78:81], v[142:145], v[218:221], v[78:81]
	v_mfma_f32_16x16x32_bf16 v[74:77], v[146:149], v[218:221], v[74:77]
	v_mfma_f32_16x16x32_bf16 v[70:73], v[156:159], v[218:221], v[70:73]
	v_mfma_f32_16x16x32_bf16 v[66:69], v[160:163], v[218:221], v[66:69]
	s_add_i32 s51, s51, 1
	s_and_b32 s54, s51, 7
	s_cmp_eq_u32 s54, 0
	s_cselect_b32 s44, s34, s35
	s_cselect_b32 s45, -1, 0
	v_lshl_add_u64 v[132:133], v[132:133], 0, s[44:45]
	global_load_dwordx2 v[114:115], v[132:133], off
	v_lshl_add_u64 v[180:181], v[132:133], 0, s[24:25]
	global_load_dwordx2 v[116:117], v[180:181], off
	v_mfma_f32_16x16x32_bf16 v[62:65], v[142:145], v[222:225], v[62:65]
	v_mfma_f32_16x16x32_bf16 v[58:61], v[146:149], v[222:225], v[58:61]
	v_mfma_f32_16x16x32_bf16 v[54:57], v[156:159], v[222:225], v[54:57]
	v_mfma_f32_16x16x32_bf16 v[50:53], v[160:163], v[222:225], v[50:53]
	v_lshl_add_u64 v[180:181], v[132:133], 0, s[26:27]
	global_load_dwordx2 v[118:119], v[180:181], off
	v_lshl_add_u64 v[180:181], v[132:133], 0, s[28:29]
	global_load_dwordx2 v[120:121], v[180:181], off
	v_mfma_f32_16x16x32_bf16 v[46:49], v[142:145], v[226:229], v[46:49]
	v_mfma_f32_16x16x32_bf16 v[42:45], v[146:149], v[226:229], v[42:45]
	v_mfma_f32_16x16x32_bf16 v[38:41], v[156:159], v[226:229], v[38:41]
	v_mfma_f32_16x16x32_bf16 v[34:37], v[160:163], v[226:229], v[34:37]
	v_lshl_add_u64 v[180:181], v[132:133], 0, s[36:37]
	global_load_dwordx2 v[122:123], v[180:181], off
	v_lshl_add_u64 v[180:181], v[132:133], 0, s[38:39]
	global_load_dwordx2 v[124:125], v[180:181], off
	v_mfma_f32_16x16x32_bf16 v[18:21], v[142:145], v[230:233], v[18:21]
	v_mfma_f32_16x16x32_bf16 v[22:25], v[146:149], v[230:233], v[22:25]
	v_mfma_f32_16x16x32_bf16 v[26:29], v[156:159], v[230:233], v[26:29]
	v_mfma_f32_16x16x32_bf16 v[30:33], v[160:163], v[230:233], v[30:33]
	v_lshl_add_u64 v[180:181], v[132:133], 0, s[40:41]
	global_load_dwordx2 v[126:127], v[180:181], off
	v_lshl_add_u64 v[180:181], v[132:133], 0, s[42:43]
	global_load_dwordx2 v[128:129], v[180:181], off
	v_mfma_f32_16x16x32_bf16 v[2:5], v[142:145], v[234:237], v[2:5]
	v_mfma_f32_16x16x32_bf16 v[6:9], v[146:149], v[234:237], v[6:9]
	v_mfma_f32_16x16x32_bf16 v[10:13], v[156:159], v[234:237], v[10:13]
	v_mfma_f32_16x16x32_bf16 v[14:17], v[160:163], v[234:237], v[14:17]
	s_waitcnt vmcnt(21)
	s_waitcnt lgkmcnt(0)
	s_barrier
; #define MD_GLDS_A(buf, tau) do { _Pragma("unroll") for (int i = 0; i < 5; ++i) if (amask & (1u << i)) \
;         __builtin_amdgcn_global_load_lds((const unsigned*)((const char*)HIDp + aoff[i] + (size_t)((tau) & 7) * 128), (PG8_LAS unsigned*)(MD_SA(buf) + wid * 1024 + i * 8192), 16, 0, 0); } while (0)
; #define MD_B_ISSUE(sb, tau) do { const char* kb_ = Bb + (size_t)((tau) >> 3) * 512 + (size_t)((tau) & 7) * (64 * (size_t)RB); _Pragma("unroll") for (int j = 0; j < 8; ++j) { const char* p_ = kb_ + (size_t)j * RB; \
;         asm volatile("global_load_dwordx2 %0, %1, off" : "=&v"(sb[j]) : "v"(p_) : "memory"); } } while (0)
; #define MD_B_WAIT(sb, N) asm volatile("s_waitcnt vmcnt(%8)" : "+v"(sb[0]), "+v"(sb[1]), "+v"(sb[2]), "+v"(sb[3]), "+v"(sb[4]), "+v"(sb[5]), "+v"(sb[6]), "+v"(sb[7]) : "n"(N) : "memory")
; #define MD_END(last) do { if (last) asm volatile("s_waitcnt vmcnt(0)" ::: "memory"); else asm volatile("s_waitcnt vmcnt(8)" ::: "memory"); \
;         asm volatile("s_waitcnt lgkmcnt(0)" ::: "memory"); __builtin_amdgcn_s_barrier(); asm volatile("" ::: "memory"); } while (0)
; __device__ __forceinline__ void moe_down_stream(PG8_LAS unsigned char* lds, int e, int cb0, int slot0, int nv, const bf16_t* HIDp, const float* Wd, bf16_t* Y, const float* slot_w, const int* slot_dst) {
;     ...
;     for (int t = 0; t < NT; t += 2) {
;         if (t + 2 < NT) MD_B_WAIT(s1, 8); else MD_B_WAIT(s1, 0);
;         MD_B_WRITE(s1, 1); __builtin_amdgcn_sched_barrier(0); MD_GLDS_A(1, t + 1); __builtin_amdgcn_sched_barrier(0);
;         if (t + 3 < NT) MD_B_ISSUE(s1, t + 3);
;         MD_COMPUTE(0);
;         MD_END(t + 3 >= NT);
;         if (t + 2 < NT) { MD_B_WAIT(s0, 8); MD_B_WRITE(s0, 0); __builtin_amdgcn_sched_barrier(0); MD_GLDS_A(0, t + 2); __builtin_amdgcn_sched_barrier(0); }
;         if (t + 4 < NT) MD_B_ISSUE(s0, t + 4);
;         MD_COMPUTE(1);
;         MD_END(t + 4 >= NT);
	s_mov_b32 s49, s46
	s_mov_b32 s46, s47
	s_mov_b32 s47, s48
	s_mov_b32 s48, s49
	v_cvt_pk_bf16_f32 v172, v186, v188
	v_cvt_pk_bf16_f32 v173, v190, v192
	v_cvt_pk_bf16_f32 v174, v194, v196
	v_cvt_pk_bf16_f32 v175, v198, v200
	v_cvt_pk_bf16_f32 v176, v187, v189
	v_cvt_pk_bf16_f32 v177, v191, v193
	v_cvt_pk_bf16_f32 v178, v195, v197
	v_cvt_pk_bf16_f32 v179, v199, v201
	ds_write_b128 v95, v[172:175] offset:0
	ds_write_b128 v95, v[176:179] offset:128
	v_add_u32_e32 v91, s46, v135
	v_add_u32_e32 v93, s46, v137
	ds_read_b128 v[238:241], v139 offset:19456
	ds_read_b128 v[242:245], v139 offset:21504
	ds_read_b128 v[246:249], v139 offset:23552
	ds_read_b128 v[250:253], v139 offset:25600
	ds_read_b128 v[218:221], v91 offset:0
	ds_read_b128 v[222:225], v91 offset:2048
	ds_read_b128 v[226:229], v91 offset:4096
	ds_read_b128 v[230:233], v91 offset:6144
	ds_read_b128 v[234:237], v91 offset:8192
	s_add_i32 s49, s48, s74
	s_add_i32 s52, s52, 1
	s_and_b32 s54, s52, 7
	s_cmp_eq_u32 s54, 0
	s_cselect_b32 s54, s53, s32
	s_cselect_b32 s55, -1, 0
	s_add_u32 s30, s30, s54
	s_addc_u32 s31, s31, s55
	s_waitcnt lgkmcnt(0)
	v_mfma_f32_16x16x32_bf16 v[78:81], v[238:241], v[218:221], v[78:81]
	v_mfma_f32_16x16x32_bf16 v[74:77], v[242:245], v[218:221], v[74:77]
	v_mfma_f32_16x16x32_bf16 v[70:73], v[246:249], v[218:221], v[70:73]
	v_mfma_f32_16x16x32_bf16 v[66:69], v[250:253], v[218:221], v[66:69]
	ds_read_b128 v[218:221], v93 offset:0
	ds_read_b128 v[142:145], v141 offset:19456
	s_mov_b32 m0, s49
	s_nop 0
	global_load_lds_dwordx4 v88, s[30:31]
	v_mfma_f32_16x16x32_bf16 v[62:65], v[238:241], v[222:225], v[62:65]
	v_mfma_f32_16x16x32_bf16 v[58:61], v[242:245], v[222:225], v[58:61]
	v_mfma_f32_16x16x32_bf16 v[54:57], v[246:249], v[222:225], v[54:57]
	v_mfma_f32_16x16x32_bf16 v[50:53], v[250:253], v[222:225], v[50:53]
	ds_read_b128 v[222:225], v93 offset:2048
	ds_read_b128 v[146:149], v141 offset:21504
	s_add_i32 m0, s49, 0x2000
	s_nop 0
	global_load_lds_dwordx4 v90, s[30:31]
	v_mfma_f32_16x16x32_bf16 v[46:49], v[238:241], v[226:229], v[46:49]
	v_mfma_f32_16x16x32_bf16 v[42:45], v[242:245], v[226:229], v[42:45]
	v_mfma_f32_16x16x32_bf16 v[38:41], v[246:249], v[226:229], v[38:41]
	v_mfma_f32_16x16x32_bf16 v[34:37], v[250:253], v[226:229], v[34:37]
	ds_read_b128 v[226:229], v93 offset:4096
	ds_read_b128 v[156:159], v141 offset:23552
	s_add_i32 m0, s49, 0x4000
	s_nop 0
	global_load_lds_dwordx4 v92, s[30:31]
	v_mfma_f32_16x16x32_bf16 v[18:21], v[238:241], v[230:233], v[18:21]
	v_mfma_f32_16x16x32_bf16 v[22:25], v[242:245], v[230:233], v[22:25]
	v_mfma_f32_16x16x32_bf16 v[26:29], v[246:249], v[230:233], v[26:29]
	v_mfma_f32_16x16x32_bf16 v[30:33], v[250:253], v[230:233], v[30:33]
	ds_read_b128 v[230:233], v93 offset:6144
	ds_read_b128 v[160:163], v141 offset:25600
	s_add_i32 m0, s49, 0x6000
	s_nop 0
	global_load_lds_dwordx4 v94, s[30:31]
	v_mfma_f32_16x16x32_bf16 v[2:5], v[238:241], v[234:237], v[2:5]
	v_mfma_f32_16x16x32_bf16 v[6:9], v[242:245], v[234:237], v[6:9]
	v_mfma_f32_16x16x32_bf16 v[10:13], v[246:249], v[234:237], v[10:13]
	v_mfma_f32_16x16x32_bf16 v[14:17], v[250:253], v[234:237], v[14:17]
	ds_read_b128 v[234:237], v93 offset:8192
	s_add_i32 m0, s49, 0x8000
	s_nop 0
	global_load_lds_dwordx4 v96, s[30:31]
	s_waitcnt lgkmcnt(0)
	v_mfma_f32_16x16x32_bf16 v[78:81], v[142:145], v[218:221], v[78:81]
	v_mfma_f32_16x16x32_bf16 v[74:77], v[146:149], v[218:221], v[74:77]
	v_mfma_f32_16x16x32_bf16 v[70:73], v[156:159], v[218:221], v[70:73]
	v_mfma_f32_16x16x32_bf16 v[66:69], v[160:163], v[218:221], v[66:69]
	s_add_i32 s51, s51, 1
	s_and_b32 s54, s51, 7
	s_cmp_eq_u32 s54, 0
	s_cselect_b32 s44, s34, s35
	s_cselect_b32 s45, -1, 0
	v_lshl_add_u64 v[132:133], v[132:133], 0, s[44:45]
	global_load_dwordx2 v[186:187], v[132:133], off
	v_lshl_add_u64 v[180:181], v[132:133], 0, s[24:25]
	global_load_dwordx2 v[188:189], v[180:181], off
	v_mfma_f32_16x16x32_bf16 v[62:65], v[142:145], v[222:225], v[62:65]
	v_mfma_f32_16x16x32_bf16 v[58:61], v[146:149], v[222:225], v[58:61]
	v_mfma_f32_16x16x32_bf16 v[54:57], v[156:159], v[222:225], v[54:57]
	v_mfma_f32_16x16x32_bf16 v[50:53], v[160:163], v[222:225], v[50:53]
	v_lshl_add_u64 v[180:181], v[132:133], 0, s[26:27]
	global_load_dwordx2 v[190:191], v[180:181], off
	v_lshl_add_u64 v[180:181], v[132:133], 0, s[28:29]
	global_load_dwordx2 v[192:193], v[180:181], off
	v_mfma_f32_16x16x32_bf16 v[46:49], v[142:145], v[226:229], v[46:49]
	v_mfma_f32_16x16x32_bf16 v[42:45], v[146:149], v[226:229], v[42:45]
	v_mfma_f32_16x16x32_bf16 v[38:41], v[156:159], v[226:229], v[38:41]
	v_mfma_f32_16x16x32_bf16 v[34:37], v[160:163], v[226:229], v[34:37]
	v_lshl_add_u64 v[180:181], v[132:133], 0, s[36:37]
	global_load_dwordx2 v[194:195], v[180:181], off
	v_lshl_add_u64 v[180:181], v[132:133], 0, s[38:39]
	global_load_dwordx2 v[196:197], v[180:181], off
	v_mfma_f32_16x16x32_bf16 v[18:21], v[142:145], v[230:233], v[18:21]
	v_mfma_f32_16x16x32_bf16 v[22:25], v[146:149], v[230:233], v[22:25]
	v_mfma_f32_16x16x32_bf16 v[26:29], v[156:159], v[230:233], v[26:29]
	v_mfma_f32_16x16x32_bf16 v[30:33], v[160:163], v[230:233], v[30:33]
	v_lshl_add_u64 v[180:181], v[132:133], 0, s[40:41]
	global_load_dwordx2 v[198:199], v[180:181], off
	v_lshl_add_u64 v[180:181], v[132:133], 0, s[42:43]
	global_load_dwordx2 v[200:201], v[180:181], off
	v_mfma_f32_16x16x32_bf16 v[2:5], v[142:145], v[234:237], v[2:5]
	v_mfma_f32_16x16x32_bf16 v[6:9], v[146:149], v[234:237], v[6:9]
	v_mfma_f32_16x16x32_bf16 v[10:13], v[156:159], v[234:237], v[10:13]
	v_mfma_f32_16x16x32_bf16 v[14:17], v[160:163], v[234:237], v[14:17]
	s_waitcnt vmcnt(21)
	s_waitcnt lgkmcnt(0)
	s_barrier
; #define MD_GLDS_A(buf, tau) do { _Pragma("unroll") for (int i = 0; i < 5; ++i) if (amask & (1u << i)) \
;         __builtin_amdgcn_global_load_lds((const unsigned*)((const char*)HIDp + aoff[i] + (size_t)((tau) & 7) * 128), (PG8_LAS unsigned*)(MD_SA(buf) + wid * 1024 + i * 8192), 16, 0, 0); } while (0)
; #define MD_B_ISSUE(sb, tau) do { const char* kb_ = Bb + (size_t)((tau) >> 3) * 512 + (size_t)((tau) & 7) * (64 * (size_t)RB); _Pragma("unroll") for (int j = 0; j < 8; ++j) { const char* p_ = kb_ + (size_t)j * RB; \
;         asm volatile("global_load_dwordx2 %0, %1, off" : "=&v"(sb[j]) : "v"(p_) : "memory"); } } while (0)
; #define MD_B_WAIT(sb, N) asm volatile("s_waitcnt vmcnt(%8)" : "+v"(sb[0]), "+v"(sb[1]), "+v"(sb[2]), "+v"(sb[3]), "+v"(sb[4]), "+v"(sb[5]), "+v"(sb[6]), "+v"(sb[7]) : "n"(N) : "memory")
; #define MD_END(last) do { if (last) asm volatile("s_waitcnt vmcnt(0)" ::: "memory"); else asm volatile("s_waitcnt vmcnt(8)" ::: "memory"); \
;         asm volatile("s_waitcnt lgkmcnt(0)" ::: "memory"); __builtin_amdgcn_s_barrier(); asm volatile("" ::: "memory"); } while (0)
; __device__ __forceinline__ void moe_down_stream(PG8_LAS unsigned char* lds, int e, int cb0, int slot0, int nv, const bf16_t* HIDp, const float* Wd, bf16_t* Y, const float* slot_w, const int* slot_dst) {
;     ...
;     for (int t = 0; t < NT; t += 2) {
;         if (t + 2 < NT) MD_B_WAIT(s1, 8); else MD_B_WAIT(s1, 0);
;         MD_B_WRITE(s1, 1); __builtin_amdgcn_sched_barrier(0); MD_GLDS_A(1, t + 1); __builtin_amdgcn_sched_barrier(0);
;         if (t + 3 < NT) MD_B_ISSUE(s1, t + 3);
;         MD_COMPUTE(0);
;         MD_END(t + 3 >= NT);
;         if (t + 2 < NT) { MD_B_WAIT(s0, 8); MD_B_WRITE(s0, 0); __builtin_amdgcn_sched_barrier(0); MD_GLDS_A(0, t + 2); __builtin_amdgcn_sched_barrier(0); }
;         if (t + 4 < NT) MD_B_ISSUE(s0, t + 4);
;         MD_COMPUTE(1);
;         MD_END(t + 4 >= NT);
	s_mov_b32 s49, s46
	s_mov_b32 s46, s47
	s_mov_b32 s47, s48
	s_mov_b32 s48, s49
	v_cvt_pk_bf16_f32 v172, v202, v204
	v_cvt_pk_bf16_f32 v173, v206, v208
	v_cvt_pk_bf16_f32 v174, v210, v212
	v_cvt_pk_bf16_f32 v175, v214, v216
	v_cvt_pk_bf16_f32 v176, v203, v205
	v_cvt_pk_bf16_f32 v177, v207, v209
	v_cvt_pk_bf16_f32 v178, v211, v213
	v_cvt_pk_bf16_f32 v179, v215, v217
	ds_write_b128 v95, v[172:175] offset:19456
	ds_write_b128 v95, v[176:179] offset:19584
	v_add_u32_e32 v91, s46, v135
	v_add_u32_e32 v93, s46, v137
	ds_read_b128 v[238:241], v139 offset:0
	ds_read_b128 v[242:245], v139 offset:2048
	ds_read_b128 v[246:249], v139 offset:4096
	ds_read_b128 v[250:253], v139 offset:6144
	ds_read_b128 v[218:221], v91 offset:0
	ds_read_b128 v[222:225], v91 offset:2048
	ds_read_b128 v[226:229], v91 offset:4096
	ds_read_b128 v[230:233], v91 offset:6144
	ds_read_b128 v[234:237], v91 offset:8192
	s_add_i32 s49, s48, s74
	s_add_i32 s52, s52, 1
	s_and_b32 s54, s52, 7
	s_cmp_eq_u32 s54, 0
	s_cselect_b32 s54, s53, s32
	s_cselect_b32 s55, -1, 0
	s_add_u32 s30, s30, s54
	s_addc_u32 s31, s31, s55
	s_waitcnt lgkmcnt(0)
	v_mfma_f32_16x16x32_bf16 v[78:81], v[238:241], v[218:221], v[78:81]
	v_mfma_f32_16x16x32_bf16 v[74:77], v[242:245], v[218:221], v[74:77]
	v_mfma_f32_16x16x32_bf16 v[70:73], v[246:249], v[218:221], v[70:73]
	v_mfma_f32_16x16x32_bf16 v[66:69], v[250:253], v[218:221], v[66:69]
	ds_read_b128 v[218:221], v93 offset:0
	ds_read_b128 v[142:145], v141 offset:0
	s_mov_b32 m0, s49
	s_nop 0
	global_load_lds_dwordx4 v88, s[30:31]
	v_mfma_f32_16x16x32_bf16 v[62:65], v[238:241], v[222:225], v[62:65]
	v_mfma_f32_16x16x32_bf16 v[58:61], v[242:245], v[222:225], v[58:61]
	v_mfma_f32_16x16x32_bf16 v[54:57], v[246:249], v[222:225], v[54:57]
	v_mfma_f32_16x16x32_bf16 v[50:53], v[250:253], v[222:225], v[50:53]
	ds_read_b128 v[222:225], v93 offset:2048
	ds_read_b128 v[146:149], v141 offset:2048
	s_add_i32 m0, s49, 0x2000
	s_nop 0
	global_load_lds_dwordx4 v90, s[30:31]
	v_mfma_f32_16x16x32_bf16 v[46:49], v[238:241], v[226:229], v[46:49]
	v_mfma_f32_16x16x32_bf16 v[42:45], v[242:245], v[226:229], v[42:45]
	v_mfma_f32_16x16x32_bf16 v[38:41], v[246:249], v[226:229], v[38:41]
	v_mfma_f32_16x16x32_bf16 v[34:37], v[250:253], v[226:229], v[34:37]
	ds_read_b128 v[226:229], v93 offset:4096
	ds_read_b128 v[156:159], v141 offset:4096
	s_add_i32 m0, s49, 0x4000
	s_nop 0
	global_load_lds_dwordx4 v92, s[30:31]
	v_mfma_f32_16x16x32_bf16 v[18:21], v[238:241], v[230:233], v[18:21]
	v_mfma_f32_16x16x32_bf16 v[22:25], v[242:245], v[230:233], v[22:25]
	v_mfma_f32_16x16x32_bf16 v[26:29], v[246:249], v[230:233], v[26:29]
	v_mfma_f32_16x16x32_bf16 v[30:33], v[250:253], v[230:233], v[30:33]
	ds_read_b128 v[230:233], v93 offset:6144
	ds_read_b128 v[160:163], v141 offset:6144
	s_add_i32 m0, s49, 0x6000
	s_nop 0
	global_load_lds_dwordx4 v94, s[30:31]
	v_mfma_f32_16x16x32_bf16 v[2:5], v[238:241], v[234:237], v[2:5]
	v_mfma_f32_16x16x32_bf16 v[6:9], v[242:245], v[234:237], v[6:9]
	v_mfma_f32_16x16x32_bf16 v[10:13], v[246:249], v[234:237], v[10:13]
	v_mfma_f32_16x16x32_bf16 v[14:17], v[250:253], v[234:237], v[14:17]
	ds_read_b128 v[234:237], v93 offset:8192
	s_add_i32 m0, s49, 0x8000
	s_nop 0
	global_load_lds_dwordx4 v96, s[30:31]
	s_waitcnt lgkmcnt(0)
	v_mfma_f32_16x16x32_bf16 v[78:81], v[142:145], v[218:221], v[78:81]
	v_mfma_f32_16x16x32_bf16 v[74:77], v[146:149], v[218:221], v[74:77]
	v_mfma_f32_16x16x32_bf16 v[70:73], v[156:159], v[218:221], v[70:73]
	v_mfma_f32_16x16x32_bf16 v[66:69], v[160:163], v[218:221], v[66:69]
	s_add_i32 s51, s51, 1
	s_and_b32 s54, s51, 7
	s_cmp_eq_u32 s54, 0
	s_cselect_b32 s44, s34, s35
	s_cselect_b32 s45, -1, 0
	v_lshl_add_u64 v[132:133], v[132:133], 0, s[44:45]
	global_load_dwordx2 v[202:203], v[132:133], off
	v_lshl_add_u64 v[180:181], v[132:133], 0, s[24:25]
	global_load_dwordx2 v[204:205], v[180:181], off
	v_mfma_f32_16x16x32_bf16 v[62:65], v[142:145], v[222:225], v[62:65]
	v_mfma_f32_16x16x32_bf16 v[58:61], v[146:149], v[222:225], v[58:61]
	v_mfma_f32_16x16x32_bf16 v[54:57], v[156:159], v[222:225], v[54:57]
	v_mfma_f32_16x16x32_bf16 v[50:53], v[160:163], v[222:225], v[50:53]
	v_lshl_add_u64 v[180:181], v[132:133], 0, s[26:27]
	global_load_dwordx2 v[206:207], v[180:181], off
	v_lshl_add_u64 v[180:181], v[132:133], 0, s[28:29]
	global_load_dwordx2 v[208:209], v[180:181], off
	v_mfma_f32_16x16x32_bf16 v[46:49], v[142:145], v[226:229], v[46:49]
	v_mfma_f32_16x16x32_bf16 v[42:45], v[146:149], v[226:229], v[42:45]
	v_mfma_f32_16x16x32_bf16 v[38:41], v[156:159], v[226:229], v[38:41]
	v_mfma_f32_16x16x32_bf16 v[34:37], v[160:163], v[226:229], v[34:37]
	v_lshl_add_u64 v[180:181], v[132:133], 0, s[36:37]
	global_load_dwordx2 v[210:211], v[180:181], off
	v_lshl_add_u64 v[180:181], v[132:133], 0, s[38:39]
	global_load_dwordx2 v[212:213], v[180:181], off
	v_mfma_f32_16x16x32_bf16 v[18:21], v[142:145], v[230:233], v[18:21]
	v_mfma_f32_16x16x32_bf16 v[22:25], v[146:149], v[230:233], v[22:25]
	v_mfma_f32_16x16x32_bf16 v[26:29], v[156:159], v[230:233], v[26:29]
	v_mfma_f32_16x16x32_bf16 v[30:33], v[160:163], v[230:233], v[30:33]
	v_lshl_add_u64 v[180:181], v[132:133], 0, s[40:41]
	global_load_dwordx2 v[214:215], v[180:181], off
	v_lshl_add_u64 v[180:181], v[132:133], 0, s[42:43]
	global_load_dwordx2 v[216:217], v[180:181], off
	v_mfma_f32_16x16x32_bf16 v[2:5], v[142:145], v[234:237], v[2:5]
	v_mfma_f32_16x16x32_bf16 v[6:9], v[146:149], v[234:237], v[6:9]
	v_mfma_f32_16x16x32_bf16 v[10:13], v[156:159], v[234:237], v[10:13]
	v_mfma_f32_16x16x32_bf16 v[14:17], v[160:163], v[234:237], v[14:17]
	s_waitcnt vmcnt(21)
	s_waitcnt lgkmcnt(0)
	s_barrier
; #define MD_GLDS_A(buf, tau) do { _Pragma("unroll") for (int i = 0; i < 5; ++i) if (amask & (1u << i)) \
;         __builtin_amdgcn_global_load_lds((const unsigned*)((const char*)HIDp + aoff[i] + (size_t)((tau) & 7) * 128), (PG8_LAS unsigned*)(MD_SA(buf) + wid * 1024 + i * 8192), 16, 0, 0); } while (0)
; #define MD_B_ISSUE(sb, tau) do { const char* kb_ = Bb + (size_t)((tau) >> 3) * 512 + (size_t)((tau) & 7) * (64 * (size_t)RB); _Pragma("unroll") for (int j = 0; j < 8; ++j) { const char* p_ = kb_ + (size_t)j * RB; \
;         asm volatile("global_load_dwordx2 %0, %1, off" : "=&v"(sb[j]) : "v"(p_) : "memory"); } } while (0)
; #define MD_B_WAIT(sb, N) asm volatile("s_waitcnt vmcnt(%8)" : "+v"(sb[0]), "+v"(sb[1]), "+v"(sb[2]), "+v"(sb[3]), "+v"(sb[4]), "+v"(sb[5]), "+v"(sb[6]), "+v"(sb[7]) : "n"(N) : "memory")
; #define MD_END(last) do { if (last) asm volatile("s_waitcnt vmcnt(0)" ::: "memory"); else asm volatile("s_waitcnt vmcnt(8)" ::: "memory"); \
;         asm volatile("s_waitcnt lgkmcnt(0)" ::: "memory"); __builtin_amdgcn_s_barrier(); asm volatile("" ::: "memory"); } while (0)
; __device__ __forceinline__ void moe_down_stream(PG8_LAS unsigned char* lds, int e, int cb0, int slot0, int nv, const bf16_t* HIDp, const float* Wd, bf16_t* Y, const float* slot_w, const int* slot_dst) {
;     ...
;     for (int t = 0; t < NT; t += 2) {
;         if (t + 2 < NT) MD_B_WAIT(s1, 8); else MD_B_WAIT(s1, 0);
;         MD_B_WRITE(s1, 1); __builtin_amdgcn_sched_barrier(0); MD_GLDS_A(1, t + 1); __builtin_amdgcn_sched_barrier(0);
;         if (t + 3 < NT) MD_B_ISSUE(s1, t + 3);
;         MD_COMPUTE(0);
;         MD_END(t + 3 >= NT);
;         if (t + 2 < NT) { MD_B_WAIT(s0, 8); MD_B_WRITE(s0, 0); __builtin_amdgcn_sched_barrier(0); MD_GLDS_A(0, t + 2); __builtin_amdgcn_sched_barrier(0); }
;         if (t + 4 < NT) MD_B_ISSUE(s0, t + 4);
;         MD_COMPUTE(1);
;         MD_END(t + 4 >= NT);
	s_mov_b32 s49, s46
	s_mov_b32 s46, s47
	s_mov_b32 s47, s48
	s_mov_b32 s48, s49
	v_cvt_pk_bf16_f32 v172, v98, v100
	v_cvt_pk_bf16_f32 v173, v102, v104
	v_cvt_pk_bf16_f32 v174, v106, v108
	v_cvt_pk_bf16_f32 v175, v110, v112
	v_cvt_pk_bf16_f32 v176, v99, v101
	v_cvt_pk_bf16_f32 v177, v103, v105
	v_cvt_pk_bf16_f32 v178, v107, v109
	v_cvt_pk_bf16_f32 v179, v111, v113
	ds_write_b128 v95, v[172:175] offset:0
	ds_write_b128 v95, v[176:179] offset:128
	v_add_u32_e32 v91, s46, v135
	v_add_u32_e32 v93, s46, v137
	ds_read_b128 v[238:241], v139 offset:19456
	ds_read_b128 v[242:245], v139 offset:21504
	ds_read_b128 v[246:249], v139 offset:23552
	ds_read_b128 v[250:253], v139 offset:25600
	ds_read_b128 v[218:221], v91 offset:0
	ds_read_b128 v[222:225], v91 offset:2048
	ds_read_b128 v[226:229], v91 offset:4096
	ds_read_b128 v[230:233], v91 offset:6144
	ds_read_b128 v[234:237], v91 offset:8192
	s_add_i32 s49, s48, s74
	s_add_i32 s52, s52, 1
	s_and_b32 s54, s52, 7
	s_cmp_eq_u32 s54, 0
	s_cselect_b32 s54, s53, s32
	s_cselect_b32 s55, -1, 0
	s_add_u32 s30, s30, s54
	s_addc_u32 s31, s31, s55
	s_waitcnt lgkmcnt(0)
	v_mfma_f32_16x16x32_bf16 v[78:81], v[238:241], v[218:221], v[78:81]
	v_mfma_f32_16x16x32_bf16 v[74:77], v[242:245], v[218:221], v[74:77]
	v_mfma_f32_16x16x32_bf16 v[70:73], v[246:249], v[218:221], v[70:73]
	v_mfma_f32_16x16x32_bf16 v[66:69], v[250:253], v[218:221], v[66:69]
	ds_read_b128 v[218:221], v93 offset:0
	ds_read_b128 v[142:145], v141 offset:19456
	s_mov_b32 m0, s49
	s_nop 0
	global_load_lds_dwordx4 v88, s[30:31]
	v_mfma_f32_16x16x32_bf16 v[62:65], v[238:241], v[222:225], v[62:65]
	v_mfma_f32_16x16x32_bf16 v[58:61], v[242:245], v[222:225], v[58:61]
	v_mfma_f32_16x16x32_bf16 v[54:57], v[246:249], v[222:225], v[54:57]
	v_mfma_f32_16x16x32_bf16 v[50:53], v[250:253], v[222:225], v[50:53]
	ds_read_b128 v[222:225], v93 offset:2048
	ds_read_b128 v[146:149], v141 offset:21504
	s_add_i32 m0, s49, 0x2000
	s_nop 0
	global_load_lds_dwordx4 v90, s[30:31]
	v_mfma_f32_16x16x32_bf16 v[46:49], v[238:241], v[226:229], v[46:49]
	v_mfma_f32_16x16x32_bf16 v[42:45], v[242:245], v[226:229], v[42:45]
	v_mfma_f32_16x16x32_bf16 v[38:41], v[246:249], v[226:229], v[38:41]
	v_mfma_f32_16x16x32_bf16 v[34:37], v[250:253], v[226:229], v[34:37]
	ds_read_b128 v[226:229], v93 offset:4096
	ds_read_b128 v[156:159], v141 offset:23552
	s_add_i32 m0, s49, 0x4000
	s_nop 0
	global_load_lds_dwordx4 v92, s[30:31]
	v_mfma_f32_16x16x32_bf16 v[18:21], v[238:241], v[230:233], v[18:21]
	v_mfma_f32_16x16x32_bf16 v[22:25], v[242:245], v[230:233], v[22:25]
	v_mfma_f32_16x16x32_bf16 v[26:29], v[246:249], v[230:233], v[26:29]
	v_mfma_f32_16x16x32_bf16 v[30:33], v[250:253], v[230:233], v[30:33]
	ds_read_b128 v[230:233], v93 offset:6144
	ds_read_b128 v[160:163], v141 offset:25600
	s_add_i32 m0, s49, 0x6000
	s_nop 0
	global_load_lds_dwordx4 v94, s[30:31]
	v_mfma_f32_16x16x32_bf16 v[2:5], v[238:241], v[234:237], v[2:5]
	v_mfma_f32_16x16x32_bf16 v[6:9], v[242:245], v[234:237], v[6:9]
	v_mfma_f32_16x16x32_bf16 v[10:13], v[246:249], v[234:237], v[10:13]
	v_mfma_f32_16x16x32_bf16 v[14:17], v[250:253], v[234:237], v[14:17]
	ds_read_b128 v[234:237], v93 offset:8192
	s_add_i32 m0, s49, 0x8000
	s_nop 0
	global_load_lds_dwordx4 v96, s[30:31]
	s_waitcnt lgkmcnt(0)
	v_mfma_f32_16x16x32_bf16 v[78:81], v[142:145], v[218:221], v[78:81]
	v_mfma_f32_16x16x32_bf16 v[74:77], v[146:149], v[218:221], v[74:77]
	v_mfma_f32_16x16x32_bf16 v[70:73], v[156:159], v[218:221], v[70:73]
	v_mfma_f32_16x16x32_bf16 v[66:69], v[160:163], v[218:221], v[66:69]
	s_add_i32 s51, s51, 1
	s_and_b32 s54, s51, 7
	s_cmp_eq_u32 s54, 0
	s_cselect_b32 s44, s34, s35
	s_cselect_b32 s45, -1, 0
	v_lshl_add_u64 v[132:133], v[132:133], 0, s[44:45]
	global_load_dwordx2 v[98:99], v[132:133], off
	v_lshl_add_u64 v[180:181], v[132:133], 0, s[24:25]
	global_load_dwordx2 v[100:101], v[180:181], off
	v_mfma_f32_16x16x32_bf16 v[62:65], v[142:145], v[222:225], v[62:65]
	v_mfma_f32_16x16x32_bf16 v[58:61], v[146:149], v[222:225], v[58:61]
	v_mfma_f32_16x16x32_bf16 v[54:57], v[156:159], v[222:225], v[54:57]
	v_mfma_f32_16x16x32_bf16 v[50:53], v[160:163], v[222:225], v[50:53]
	v_lshl_add_u64 v[180:181], v[132:133], 0, s[26:27]
	global_load_dwordx2 v[102:103], v[180:181], off
	v_lshl_add_u64 v[180:181], v[132:133], 0, s[28:29]
	global_load_dwordx2 v[104:105], v[180:181], off
	v_mfma_f32_16x16x32_bf16 v[46:49], v[142:145], v[226:229], v[46:49]
	v_mfma_f32_16x16x32_bf16 v[42:45], v[146:149], v[226:229], v[42:45]
	v_mfma_f32_16x16x32_bf16 v[38:41], v[156:159], v[226:229], v[38:41]
	v_mfma_f32_16x16x32_bf16 v[34:37], v[160:163], v[226:229], v[34:37]
	v_lshl_add_u64 v[180:181], v[132:133], 0, s[36:37]
	global_load_dwordx2 v[106:107], v[180:181], off
	v_lshl_add_u64 v[180:181], v[132:133], 0, s[38:39]
	global_load_dwordx2 v[108:109], v[180:181], off
	v_mfma_f32_16x16x32_bf16 v[18:21], v[142:145], v[230:233], v[18:21]
	v_mfma_f32_16x16x32_bf16 v[22:25], v[146:149], v[230:233], v[22:25]
	v_mfma_f32_16x16x32_bf16 v[26:29], v[156:159], v[230:233], v[26:29]
	v_mfma_f32_16x16x32_bf16 v[30:33], v[160:163], v[230:233], v[30:33]
	v_lshl_add_u64 v[180:181], v[132:133], 0, s[40:41]
	global_load_dwordx2 v[110:111], v[180:181], off
	v_lshl_add_u64 v[180:181], v[132:133], 0, s[42:43]
	global_load_dwordx2 v[112:113], v[180:181], off
	v_mfma_f32_16x16x32_bf16 v[2:5], v[142:145], v[234:237], v[2:5]
	v_mfma_f32_16x16x32_bf16 v[6:9], v[146:149], v[234:237], v[6:9]
	v_mfma_f32_16x16x32_bf16 v[10:13], v[156:159], v[234:237], v[10:13]
	v_mfma_f32_16x16x32_bf16 v[14:17], v[160:163], v[234:237], v[14:17]
	s_waitcnt vmcnt(21)
	s_waitcnt lgkmcnt(0)
	s_barrier
; #define PG8_LAS __attribute__((address_space(3)))
; __device__ __forceinline__ unsigned cvtpk(float lo, float hi) { f32x2 v = {lo, hi}; bf16x2_t b = __builtin_convertvector(v, bf16x2_t); return __builtin_bit_cast(unsigned, b); }
; __device__ __forceinline__ void moe_down_stream(PG8_LAS unsigned char* lds, int e, int cb0, int slot0, int nv, const bf16_t* HIDp, const float* Wd, bf16_t* Y, const float* slot_w, const int* slot_dst) {
;     ...
;         if (((t + 1) & 7) == 7) {
;             const int cb = cb0 + ((t + 1) >> 3);
; #pragma unroll
;             for (int m = 0; m < DNM; ++m) {
;                 const float w_ = lw[4 * (16 * m + fr) + wr];
; #pragma unroll
;                 for (int p = 0; p < 2; ++p) { const f32x4 v0 = acc[m][2 * p] * w_, v1 = acc[m][2 * p + 1] * w_; u32x4 w; w.x = cvtpk(v0[0], v0[1]); w.y = cvtpk(v0[2], v0[3]); w.z = cvtpk(v1[0], v1[1]); w.w = cvtpk(v1[2], v1[3]);
;                     *(PG8_LAS u32x4*)(stg + fr * 128 + (((4 * p + fq) ^ (fr & 7)) * 16)) = w; }
; #pragma unroll
;                 for (int hh = 0; hh < 2; ++hh) { const int r = (lane >> 3) + 8 * hh, cc = lane & 7; const u32x4 d = *(const PG8_LAS u32x4*)(stg + r * 128 + ((cc ^ (r & 7)) * 16)); const int dst_ = ldst[4 * (16 * m + r) + wr];
;                     if (dst_ >= 0) *(u32x4*)(Y + (size_t)dst_ * D + 128 * cb + 64 * wc + 8 * cc) = d; }
; #pragma unroll
;                 for (int n = 0; n < 4; ++n) acc[m][n] = (f32x4){0.f, 0.f, 0.f, 0.f}; } }
	s_mov_b32 s49, s46
	s_mov_b32 s46, s47
	s_mov_b32 s47, s48
	s_mov_b32 s48, s49
	s_add_i32 s54, s48, s74
	v_add_u32_e32 v164, s54, v84
	v_add_u32_e32 v165, s54, v85
	ds_read_b32 v150, v82 offset:0
	ds_read_b32 v151, v83 offset:0
	ds_read_b32 v166, v83 offset:128
	s_waitcnt lgkmcnt(2)
	v_mul_f32_e32 v78, v150, v78
	v_mul_f32_e32 v79, v150, v79
	v_mul_f32_e32 v80, v150, v80
	v_mul_f32_e32 v81, v150, v81
	v_mul_f32_e32 v74, v150, v74
	v_mul_f32_e32 v75, v150, v75
	v_mul_f32_e32 v76, v150, v76
	v_mul_f32_e32 v77, v150, v77
	v_cvt_pk_bf16_f32 v182, v78, v79
	v_cvt_pk_bf16_f32 v183, v80, v81
	v_cvt_pk_bf16_f32 v184, v74, v75
	v_cvt_pk_bf16_f32 v185, v76, v77
	ds_write_b128 v164, v[182:185]
	v_mul_f32_e32 v70, v150, v70
	v_mul_f32_e32 v71, v150, v71
	v_mul_f32_e32 v72, v150, v72
	v_mul_f32_e32 v73, v150, v73
	v_mul_f32_e32 v66, v150, v66
	v_mul_f32_e32 v67, v150, v67
	v_mul_f32_e32 v68, v150, v68
	v_mul_f32_e32 v69, v150, v69
	v_cvt_pk_bf16_f32 v182, v70, v71
	v_cvt_pk_bf16_f32 v183, v72, v73
	v_cvt_pk_bf16_f32 v184, v66, v67
	v_cvt_pk_bf16_f32 v185, v68, v69
	v_xor_b32_e32 v167, 64, v164
	ds_write_b128 v167, v[182:185]
	v_mov_b32_e32 v78, 0
	v_mov_b32_e32 v74, 0
	v_mov_b32_e32 v70, 0
	v_mov_b32_e32 v66, 0
	v_mov_b32_e32 v79, 0
	v_mov_b32_e32 v75, 0
	v_mov_b32_e32 v71, 0
	v_mov_b32_e32 v67, 0
	v_mov_b32_e32 v80, 0
	v_mov_b32_e32 v76, 0
	v_mov_b32_e32 v72, 0
	v_mov_b32_e32 v68, 0
	v_mov_b32_e32 v81, 0
	v_mov_b32_e32 v77, 0
	v_mov_b32_e32 v73, 0
	v_mov_b32_e32 v69, 0
	ds_read_b128 v[182:185], v165 offset:0
	v_cmp_lt_i32_e32 vcc, -1, v151
	v_lshlrev_b32_e32 v148, 13, v151
	v_mov_b32_e32 v149, 0
	v_lshl_add_u64 v[148:149], v[148:149], 0, v[86:87]
	v_cndmask_b32_e32 v148, v168, v148, vcc
	v_cndmask_b32_e32 v149, v169, v149, vcc
	s_waitcnt lgkmcnt(0)
	global_store_dwordx4 v[148:149], v[182:185], off
	ds_read_b128 v[182:185], v165 offset:8192
	v_cmp_lt_i32_e32 vcc, -1, v166
	v_lshlrev_b32_e32 v148, 13, v166
	v_mov_b32_e32 v149, 0
	v_lshl_add_u64 v[148:149], v[148:149], 0, v[86:87]
	v_cndmask_b32_e32 v148, v168, v148, vcc
	v_cndmask_b32_e32 v149, v169, v149, vcc
	s_waitcnt lgkmcnt(0)
	global_store_dwordx4 v[148:149], v[182:185], off
	ds_read_b32 v150, v82 offset:256
	ds_read_b32 v151, v83 offset:256
	ds_read_b32 v166, v83 offset:384
	s_waitcnt lgkmcnt(2)
	v_mul_f32_e32 v62, v150, v62
	v_mul_f32_e32 v63, v150, v63
	v_mul_f32_e32 v64, v150, v64
	v_mul_f32_e32 v65, v150, v65
	v_mul_f32_e32 v58, v150, v58
	v_mul_f32_e32 v59, v150, v59
	v_mul_f32_e32 v60, v150, v60
	v_mul_f32_e32 v61, v150, v61
	v_cvt_pk_bf16_f32 v182, v62, v63
	v_cvt_pk_bf16_f32 v183, v64, v65
	v_cvt_pk_bf16_f32 v184, v58, v59
	v_cvt_pk_bf16_f32 v185, v60, v61
	ds_write_b128 v164, v[182:185]
	v_mul_f32_e32 v54, v150, v54
	v_mul_f32_e32 v55, v150, v55
	v_mul_f32_e32 v56, v150, v56
	v_mul_f32_e32 v57, v150, v57
	v_mul_f32_e32 v50, v150, v50
	v_mul_f32_e32 v51, v150, v51
	v_mul_f32_e32 v52, v150, v52
	v_mul_f32_e32 v53, v150, v53
	v_cvt_pk_bf16_f32 v182, v54, v55
	v_cvt_pk_bf16_f32 v183, v56, v57
	v_cvt_pk_bf16_f32 v184, v50, v51
	v_cvt_pk_bf16_f32 v185, v52, v53
	v_xor_b32_e32 v167, 64, v164
	ds_write_b128 v167, v[182:185]
	v_mov_b32_e32 v62, 0
	v_mov_b32_e32 v58, 0
	v_mov_b32_e32 v54, 0
	v_mov_b32_e32 v50, 0
	v_mov_b32_e32 v63, 0
	v_mov_b32_e32 v59, 0
	v_mov_b32_e32 v55, 0
	v_mov_b32_e32 v51, 0
	v_mov_b32_e32 v64, 0
	v_mov_b32_e32 v60, 0
	v_mov_b32_e32 v56, 0
	v_mov_b32_e32 v52, 0
	v_mov_b32_e32 v65, 0
	v_mov_b32_e32 v61, 0
	v_mov_b32_e32 v57, 0
	v_mov_b32_e32 v53, 0
	ds_read_b128 v[182:185], v165 offset:0
	v_cmp_lt_i32_e32 vcc, -1, v151
	v_lshlrev_b32_e32 v148, 13, v151
	v_mov_b32_e32 v149, 0
	v_lshl_add_u64 v[148:149], v[148:149], 0, v[86:87]
	v_cndmask_b32_e32 v148, v168, v148, vcc
	v_cndmask_b32_e32 v149, v169, v149, vcc
	s_waitcnt lgkmcnt(0)
	global_store_dwordx4 v[148:149], v[182:185], off
	ds_read_b128 v[182:185], v165 offset:8192
	v_cmp_lt_i32_e32 vcc, -1, v166
	v_lshlrev_b32_e32 v148, 13, v166
	v_mov_b32_e32 v149, 0
	v_lshl_add_u64 v[148:149], v[148:149], 0, v[86:87]
	v_cndmask_b32_e32 v148, v168, v148, vcc
	v_cndmask_b32_e32 v149, v169, v149, vcc
	s_waitcnt lgkmcnt(0)
	global_store_dwordx4 v[148:149], v[182:185], off
	ds_read_b32 v150, v82 offset:512
	ds_read_b32 v151, v83 offset:512
	ds_read_b32 v166, v83 offset:640
	s_waitcnt lgkmcnt(2)
	v_mul_f32_e32 v46, v150, v46
	v_mul_f32_e32 v47, v150, v47
	v_mul_f32_e32 v48, v150, v48
	v_mul_f32_e32 v49, v150, v49
	v_mul_f32_e32 v42, v150, v42
	v_mul_f32_e32 v43, v150, v43
	v_mul_f32_e32 v44, v150, v44
	v_mul_f32_e32 v45, v150, v45
	v_cvt_pk_bf16_f32 v182, v46, v47
	v_cvt_pk_bf16_f32 v183, v48, v49
	v_cvt_pk_bf16_f32 v184, v42, v43
	v_cvt_pk_bf16_f32 v185, v44, v45
	ds_write_b128 v164, v[182:185]
	v_mul_f32_e32 v38, v150, v38
	v_mul_f32_e32 v39, v150, v39
	v_mul_f32_e32 v40, v150, v40
	v_mul_f32_e32 v41, v150, v41
	v_mul_f32_e32 v34, v150, v34
	v_mul_f32_e32 v35, v150, v35
	v_mul_f32_e32 v36, v150, v36
	v_mul_f32_e32 v37, v150, v37
	v_cvt_pk_bf16_f32 v182, v38, v39
	v_cvt_pk_bf16_f32 v183, v40, v41
	v_cvt_pk_bf16_f32 v184, v34, v35
	v_cvt_pk_bf16_f32 v185, v36, v37
	v_xor_b32_e32 v167, 64, v164
	ds_write_b128 v167, v[182:185]
	v_mov_b32_e32 v46, 0
	v_mov_b32_e32 v42, 0
	v_mov_b32_e32 v38, 0
	v_mov_b32_e32 v34, 0
	v_mov_b32_e32 v47, 0
	v_mov_b32_e32 v43, 0
	v_mov_b32_e32 v39, 0
	v_mov_b32_e32 v35, 0
	v_mov_b32_e32 v48, 0
	v_mov_b32_e32 v44, 0
	v_mov_b32_e32 v40, 0
	v_mov_b32_e32 v36, 0
	v_mov_b32_e32 v49, 0
	v_mov_b32_e32 v45, 0
	v_mov_b32_e32 v41, 0
	v_mov_b32_e32 v37, 0
	ds_read_b128 v[182:185], v165 offset:0
	v_cmp_lt_i32_e32 vcc, -1, v151
	v_lshlrev_b32_e32 v148, 13, v151
	v_mov_b32_e32 v149, 0
	v_lshl_add_u64 v[148:149], v[148:149], 0, v[86:87]
	v_cndmask_b32_e32 v148, v168, v148, vcc
	v_cndmask_b32_e32 v149, v169, v149, vcc
	s_waitcnt lgkmcnt(0)
; #define PG8_LAS __attribute__((address_space(3)))
; __device__ __forceinline__ unsigned cvtpk(float lo, float hi) { f32x2 v = {lo, hi}; bf16x2_t b = __builtin_convertvector(v, bf16x2_t); return __builtin_bit_cast(unsigned, b); }
; __device__ __forceinline__ void moe_down_stream(PG8_LAS unsigned char* lds, int e, int cb0, int slot0, int nv, const bf16_t* HIDp, const float* Wd, bf16_t* Y, const float* slot_w, const int* slot_dst) {
;     ...
;         if (((t + 1) & 7) == 7) {
;             const int cb = cb0 + ((t + 1) >> 3);
; #pragma unroll
;             for (int m = 0; m < DNM; ++m) {
;                 const float w_ = lw[4 * (16 * m + fr) + wr];
; #pragma unroll
;                 for (int p = 0; p < 2; ++p) { const f32x4 v0 = acc[m][2 * p] * w_, v1 = acc[m][2 * p + 1] * w_; u32x4 w; w.x = cvtpk(v0[0], v0[1]); w.y = cvtpk(v0[2], v0[3]); w.z = cvtpk(v1[0], v1[1]); w.w = cvtpk(v1[2], v1[3]);
;                     *(PG8_LAS u32x4*)(stg + fr * 128 + (((4 * p + fq) ^ (fr & 7)) * 16)) = w; }
; #pragma unroll
;                 for (int hh = 0; hh < 2; ++hh) { const int r = (lane >> 3) + 8 * hh, cc = lane & 7; const u32x4 d = *(const PG8_LAS u32x4*)(stg + r * 128 + ((cc ^ (r & 7)) * 16)); const int dst_ = ldst[4 * (16 * m + r) + wr];
;                     if (dst_ >= 0) *(u32x4*)(Y + (size_t)dst_ * D + 128 * cb + 64 * wc + 8 * cc) = d; }
; #pragma unroll
;                 for (int n = 0; n < 4; ++n) acc[m][n] = (f32x4){0.f, 0.f, 0.f, 0.f}; } }
	global_store_dwordx4 v[148:149], v[182:185], off
	ds_read_b128 v[182:185], v165 offset:8192
	v_cmp_lt_i32_e32 vcc, -1, v166
	v_lshlrev_b32_e32 v148, 13, v166
	v_mov_b32_e32 v149, 0
	v_lshl_add_u64 v[148:149], v[148:149], 0, v[86:87]
	v_cndmask_b32_e32 v148, v168, v148, vcc
	v_cndmask_b32_e32 v149, v169, v149, vcc
	s_waitcnt lgkmcnt(0)
	global_store_dwordx4 v[148:149], v[182:185], off
	ds_read_b32 v150, v82 offset:768
	ds_read_b32 v151, v83 offset:768
	ds_read_b32 v166, v83 offset:896
	s_waitcnt lgkmcnt(2)
	v_mul_f32_e32 v18, v150, v18
	v_mul_f32_e32 v19, v150, v19
	v_mul_f32_e32 v20, v150, v20
	v_mul_f32_e32 v21, v150, v21
	v_mul_f32_e32 v22, v150, v22
	v_mul_f32_e32 v23, v150, v23
	v_mul_f32_e32 v24, v150, v24
	v_mul_f32_e32 v25, v150, v25
	v_cvt_pk_bf16_f32 v182, v18, v19
	v_cvt_pk_bf16_f32 v183, v20, v21
	v_cvt_pk_bf16_f32 v184, v22, v23
	v_cvt_pk_bf16_f32 v185, v24, v25
	ds_write_b128 v164, v[182:185]
	v_mul_f32_e32 v26, v150, v26
	v_mul_f32_e32 v27, v150, v27
	v_mul_f32_e32 v28, v150, v28
	v_mul_f32_e32 v29, v150, v29
	v_mul_f32_e32 v30, v150, v30
	v_mul_f32_e32 v31, v150, v31
	v_mul_f32_e32 v32, v150, v32
	v_mul_f32_e32 v33, v150, v33
	v_cvt_pk_bf16_f32 v182, v26, v27
	v_cvt_pk_bf16_f32 v183, v28, v29
	v_cvt_pk_bf16_f32 v184, v30, v31
	v_cvt_pk_bf16_f32 v185, v32, v33
	v_xor_b32_e32 v167, 64, v164
	ds_write_b128 v167, v[182:185]
	v_mov_b32_e32 v18, 0
	v_mov_b32_e32 v22, 0
	v_mov_b32_e32 v26, 0
	v_mov_b32_e32 v30, 0
	v_mov_b32_e32 v19, 0
	v_mov_b32_e32 v23, 0
	v_mov_b32_e32 v27, 0
	v_mov_b32_e32 v31, 0
	v_mov_b32_e32 v20, 0
	v_mov_b32_e32 v24, 0
	v_mov_b32_e32 v28, 0
	v_mov_b32_e32 v32, 0
	v_mov_b32_e32 v21, 0
	v_mov_b32_e32 v25, 0
	v_mov_b32_e32 v29, 0
	v_mov_b32_e32 v33, 0
	ds_read_b128 v[182:185], v165 offset:0
	v_cmp_lt_i32_e32 vcc, -1, v151
	v_lshlrev_b32_e32 v148, 13, v151
	v_mov_b32_e32 v149, 0
	v_lshl_add_u64 v[148:149], v[148:149], 0, v[86:87]
	v_cndmask_b32_e32 v148, v168, v148, vcc
	v_cndmask_b32_e32 v149, v169, v149, vcc
	s_waitcnt lgkmcnt(0)
	global_store_dwordx4 v[148:149], v[182:185], off
	ds_read_b128 v[182:185], v165 offset:8192
	v_cmp_lt_i32_e32 vcc, -1, v166
	v_lshlrev_b32_e32 v148, 13, v166
	v_mov_b32_e32 v149, 0
	v_lshl_add_u64 v[148:149], v[148:149], 0, v[86:87]
	v_cndmask_b32_e32 v148, v168, v148, vcc
	v_cndmask_b32_e32 v149, v169, v149, vcc
	s_waitcnt lgkmcnt(0)
	global_store_dwordx4 v[148:149], v[182:185], off
	ds_read_b32 v150, v82 offset:1024
	ds_read_b32 v151, v83 offset:1024
	ds_read_b32 v166, v83 offset:1152
	s_waitcnt lgkmcnt(2)
	v_mul_f32_e32 v2, v150, v2
	v_mul_f32_e32 v3, v150, v3
	v_mul_f32_e32 v4, v150, v4
	v_mul_f32_e32 v5, v150, v5
	v_mul_f32_e32 v6, v150, v6
	v_mul_f32_e32 v7, v150, v7
	v_mul_f32_e32 v8, v150, v8
	v_mul_f32_e32 v9, v150, v9
	v_cvt_pk_bf16_f32 v182, v2, v3
	v_cvt_pk_bf16_f32 v183, v4, v5
	v_cvt_pk_bf16_f32 v184, v6, v7
	v_cvt_pk_bf16_f32 v185, v8, v9
	ds_write_b128 v164, v[182:185]
	v_mul_f32_e32 v10, v150, v10
	v_mul_f32_e32 v11, v150, v11
	v_mul_f32_e32 v12, v150, v12
	v_mul_f32_e32 v13, v150, v13
	v_mul_f32_e32 v14, v150, v14
	v_mul_f32_e32 v15, v150, v15
	v_mul_f32_e32 v16, v150, v16
	v_mul_f32_e32 v17, v150, v17
	v_cvt_pk_bf16_f32 v182, v10, v11
	v_cvt_pk_bf16_f32 v183, v12, v13
	v_cvt_pk_bf16_f32 v184, v14, v15
	v_cvt_pk_bf16_f32 v185, v16, v17
	v_xor_b32_e32 v167, 64, v164
	ds_write_b128 v167, v[182:185]
	v_mov_b32_e32 v2, 0
	v_mov_b32_e32 v6, 0
	v_mov_b32_e32 v10, 0
	v_mov_b32_e32 v14, 0
	v_mov_b32_e32 v3, 0
	v_mov_b32_e32 v7, 0
	v_mov_b32_e32 v11, 0
	v_mov_b32_e32 v15, 0
	v_mov_b32_e32 v4, 0
	v_mov_b32_e32 v8, 0
	v_mov_b32_e32 v12, 0
	v_mov_b32_e32 v16, 0
	v_mov_b32_e32 v5, 0
	v_mov_b32_e32 v9, 0
	v_mov_b32_e32 v13, 0
	v_mov_b32_e32 v17, 0
	ds_read_b128 v[182:185], v165 offset:0
	v_cmp_lt_i32_e32 vcc, -1, v151
	v_lshlrev_b32_e32 v148, 13, v151
	v_mov_b32_e32 v149, 0
	v_lshl_add_u64 v[148:149], v[148:149], 0, v[86:87]
	v_cndmask_b32_e32 v148, v168, v148, vcc
	v_cndmask_b32_e32 v149, v169, v149, vcc
	s_waitcnt lgkmcnt(0)
	global_store_dwordx4 v[148:149], v[182:185], off
	ds_read_b128 v[182:185], v165 offset:8192
	v_cmp_lt_i32_e32 vcc, -1, v166
	v_lshlrev_b32_e32 v148, 13, v166
	v_mov_b32_e32 v149, 0
	v_lshl_add_u64 v[148:149], v[148:149], 0, v[86:87]
	v_cndmask_b32_e32 v148, v168, v148, vcc
	v_cndmask_b32_e32 v149, v169, v149, vcc
	s_waitcnt lgkmcnt(0)
	global_store_dwordx4 v[148:149], v[182:185], off
	v_add_co_u32_e32 v86, vcc, 0x800, v86
	s_nop 1
	v_addc_co_u32_e32 v87, vcc, 0, v87, vcc
	s_waitcnt lgkmcnt(0)
	v_cvt_pk_bf16_f32 v172, v114, v116
	v_cvt_pk_bf16_f32 v173, v118, v120
	v_cvt_pk_bf16_f32 v174, v122, v124
	v_cvt_pk_bf16_f32 v175, v126, v128
	v_cvt_pk_bf16_f32 v176, v115, v117
	v_cvt_pk_bf16_f32 v177, v119, v121
	v_cvt_pk_bf16_f32 v178, v123, v125
	v_cvt_pk_bf16_f32 v179, v127, v129
	ds_write_b128 v95, v[172:175] offset:19456
	ds_write_b128 v95, v[176:179] offset:19584
	v_add_u32_e32 v91, s46, v135
	v_add_u32_e32 v93, s46, v137
	ds_read_b128 v[238:241], v139 offset:0
	ds_read_b128 v[242:245], v139 offset:2048
	ds_read_b128 v[246:249], v139 offset:4096
	ds_read_b128 v[250:253], v139 offset:6144
	ds_read_b128 v[218:221], v91 offset:0
	ds_read_b128 v[222:225], v91 offset:2048
	ds_read_b128 v[226:229], v91 offset:4096
	ds_read_b128 v[230:233], v91 offset:6144
	ds_read_b128 v[234:237], v91 offset:8192
	s_add_i32 s49, s48, s74
	s_add_i32 s52, s52, 1
	s_and_b32 s54, s52, 7
	s_cmp_eq_u32 s54, 0
	s_cselect_b32 s54, s53, s32
	s_cselect_b32 s55, -1, 0
	s_add_u32 s30, s30, s54
	s_addc_u32 s31, s31, s55
	s_waitcnt lgkmcnt(0)
; #define MD_GLDS_A(buf, tau) do { _Pragma("unroll") for (int i = 0; i < 5; ++i) if (amask & (1u << i)) \
;         __builtin_amdgcn_global_load_lds((const unsigned*)((const char*)HIDp + aoff[i] + (size_t)((tau) & 7) * 128), (PG8_LAS unsigned*)(MD_SA(buf) + wid * 1024 + i * 8192), 16, 0, 0); } while (0)
; #define MD_B_ISSUE(sb, tau) do { const char* kb_ = Bb + (size_t)((tau) >> 3) * 512 + (size_t)((tau) & 7) * (64 * (size_t)RB); _Pragma("unroll") for (int j = 0; j < 8; ++j) { const char* p_ = kb_ + (size_t)j * RB; \
;         asm volatile("global_load_dwordx2 %0, %1, off" : "=&v"(sb[j]) : "v"(p_) : "memory"); } } while (0)
; #define MD_B_WAIT(sb, N) asm volatile("s_waitcnt vmcnt(%8)" : "+v"(sb[0]), "+v"(sb[1]), "+v"(sb[2]), "+v"(sb[3]), "+v"(sb[4]), "+v"(sb[5]), "+v"(sb[6]), "+v"(sb[7]) : "n"(N) : "memory")
; #define MD_END(last) do { if (last) asm volatile("s_waitcnt vmcnt(0)" ::: "memory"); else asm volatile("s_waitcnt vmcnt(8)" ::: "memory"); \
;         asm volatile("s_waitcnt lgkmcnt(0)" ::: "memory"); __builtin_amdgcn_s_barrier(); asm volatile("" ::: "memory"); } while (0)
; __device__ __forceinline__ void moe_down_stream(PG8_LAS unsigned char* lds, int e, int cb0, int slot0, int nv, const bf16_t* HIDp, const float* Wd, bf16_t* Y, const float* slot_w, const int* slot_dst) {
;     ...
;     for (int t = 0; t < NT; t += 2) {
;         if (t + 2 < NT) MD_B_WAIT(s1, 8); else MD_B_WAIT(s1, 0);
;         MD_B_WRITE(s1, 1); __builtin_amdgcn_sched_barrier(0); MD_GLDS_A(1, t + 1); __builtin_amdgcn_sched_barrier(0);
;         if (t + 3 < NT) MD_B_ISSUE(s1, t + 3);
;         MD_COMPUTE(0);
;         MD_END(t + 3 >= NT);
;         if (t + 2 < NT) { MD_B_WAIT(s0, 8); MD_B_WRITE(s0, 0); __builtin_amdgcn_sched_barrier(0); MD_GLDS_A(0, t + 2); __builtin_amdgcn_sched_barrier(0); }
;         if (t + 4 < NT) MD_B_ISSUE(s0, t + 4);
;         MD_COMPUTE(1);
;         MD_END(t + 4 >= NT);
	v_mfma_f32_16x16x32_bf16 v[78:81], v[238:241], v[218:221], v[78:81]
	v_mfma_f32_16x16x32_bf16 v[74:77], v[242:245], v[218:221], v[74:77]
	v_mfma_f32_16x16x32_bf16 v[70:73], v[246:249], v[218:221], v[70:73]
	v_mfma_f32_16x16x32_bf16 v[66:69], v[250:253], v[218:221], v[66:69]
	ds_read_b128 v[218:221], v93 offset:0
	ds_read_b128 v[142:145], v141 offset:0
	s_mov_b32 m0, s49
	s_nop 0
	global_load_lds_dwordx4 v88, s[30:31]
	v_mfma_f32_16x16x32_bf16 v[62:65], v[238:241], v[222:225], v[62:65]
	v_mfma_f32_16x16x32_bf16 v[58:61], v[242:245], v[222:225], v[58:61]
	v_mfma_f32_16x16x32_bf16 v[54:57], v[246:249], v[222:225], v[54:57]
	v_mfma_f32_16x16x32_bf16 v[50:53], v[250:253], v[222:225], v[50:53]
	ds_read_b128 v[222:225], v93 offset:2048
	ds_read_b128 v[146:149], v141 offset:2048
	s_add_i32 m0, s49, 0x2000
	s_nop 0
	global_load_lds_dwordx4 v90, s[30:31]
	v_mfma_f32_16x16x32_bf16 v[46:49], v[238:241], v[226:229], v[46:49]
	v_mfma_f32_16x16x32_bf16 v[42:45], v[242:245], v[226:229], v[42:45]
	v_mfma_f32_16x16x32_bf16 v[38:41], v[246:249], v[226:229], v[38:41]
	v_mfma_f32_16x16x32_bf16 v[34:37], v[250:253], v[226:229], v[34:37]
	ds_read_b128 v[226:229], v93 offset:4096
	ds_read_b128 v[156:159], v141 offset:4096
	s_add_i32 m0, s49, 0x4000
	s_nop 0
	global_load_lds_dwordx4 v92, s[30:31]
	v_mfma_f32_16x16x32_bf16 v[18:21], v[238:241], v[230:233], v[18:21]
	v_mfma_f32_16x16x32_bf16 v[22:25], v[242:245], v[230:233], v[22:25]
	v_mfma_f32_16x16x32_bf16 v[26:29], v[246:249], v[230:233], v[26:29]
	v_mfma_f32_16x16x32_bf16 v[30:33], v[250:253], v[230:233], v[30:33]
	ds_read_b128 v[230:233], v93 offset:6144
	ds_read_b128 v[160:163], v141 offset:6144
	s_add_i32 m0, s49, 0x6000
	s_nop 0
	global_load_lds_dwordx4 v94, s[30:31]
	v_mfma_f32_16x16x32_bf16 v[2:5], v[238:241], v[234:237], v[2:5]
	v_mfma_f32_16x16x32_bf16 v[6:9], v[242:245], v[234:237], v[6:9]
	v_mfma_f32_16x16x32_bf16 v[10:13], v[246:249], v[234:237], v[10:13]
	v_mfma_f32_16x16x32_bf16 v[14:17], v[250:253], v[234:237], v[14:17]
	ds_read_b128 v[234:237], v93 offset:8192
	s_add_i32 m0, s49, 0x8000
	s_nop 0
	global_load_lds_dwordx4 v96, s[30:31]
	s_waitcnt lgkmcnt(0)
	v_mfma_f32_16x16x32_bf16 v[78:81], v[142:145], v[218:221], v[78:81]
	v_mfma_f32_16x16x32_bf16 v[74:77], v[146:149], v[218:221], v[74:77]
	v_mfma_f32_16x16x32_bf16 v[70:73], v[156:159], v[218:221], v[70:73]
	v_mfma_f32_16x16x32_bf16 v[66:69], v[160:163], v[218:221], v[66:69]
	s_add_i32 s51, s51, 1
	s_and_b32 s54, s51, 7
	s_cmp_eq_u32 s54, 0
	s_cselect_b32 s44, s34, s35
	s_cselect_b32 s45, -1, 0
	v_lshl_add_u64 v[132:133], v[132:133], 0, s[44:45]
	global_load_dwordx2 v[114:115], v[132:133], off
	v_lshl_add_u64 v[180:181], v[132:133], 0, s[24:25]
	global_load_dwordx2 v[116:117], v[180:181], off
	v_mfma_f32_16x16x32_bf16 v[62:65], v[142:145], v[222:225], v[62:65]
	v_mfma_f32_16x16x32_bf16 v[58:61], v[146:149], v[222:225], v[58:61]
	v_mfma_f32_16x16x32_bf16 v[54:57], v[156:159], v[222:225], v[54:57]
	v_mfma_f32_16x16x32_bf16 v[50:53], v[160:163], v[222:225], v[50:53]
	v_lshl_add_u64 v[180:181], v[132:133], 0, s[26:27]
	global_load_dwordx2 v[118:119], v[180:181], off
	v_lshl_add_u64 v[180:181], v[132:133], 0, s[28:29]
	global_load_dwordx2 v[120:121], v[180:181], off
	v_mfma_f32_16x16x32_bf16 v[46:49], v[142:145], v[226:229], v[46:49]
	v_mfma_f32_16x16x32_bf16 v[42:45], v[146:149], v[226:229], v[42:45]
	v_mfma_f32_16x16x32_bf16 v[38:41], v[156:159], v[226:229], v[38:41]
	v_mfma_f32_16x16x32_bf16 v[34:37], v[160:163], v[226:229], v[34:37]
	v_lshl_add_u64 v[180:181], v[132:133], 0, s[36:37]
	global_load_dwordx2 v[122:123], v[180:181], off
	v_lshl_add_u64 v[180:181], v[132:133], 0, s[38:39]
	global_load_dwordx2 v[124:125], v[180:181], off
	v_mfma_f32_16x16x32_bf16 v[18:21], v[142:145], v[230:233], v[18:21]
	v_mfma_f32_16x16x32_bf16 v[22:25], v[146:149], v[230:233], v[22:25]
	v_mfma_f32_16x16x32_bf16 v[26:29], v[156:159], v[230:233], v[26:29]
	v_mfma_f32_16x16x32_bf16 v[30:33], v[160:163], v[230:233], v[30:33]
	v_lshl_add_u64 v[180:181], v[132:133], 0, s[40:41]
	global_load_dwordx2 v[126:127], v[180:181], off
	v_lshl_add_u64 v[180:181], v[132:133], 0, s[42:43]
	global_load_dwordx2 v[128:129], v[180:181], off
	v_mfma_f32_16x16x32_bf16 v[2:5], v[142:145], v[234:237], v[2:5]
	v_mfma_f32_16x16x32_bf16 v[6:9], v[146:149], v[234:237], v[6:9]
	v_mfma_f32_16x16x32_bf16 v[10:13], v[156:159], v[234:237], v[10:13]
	v_mfma_f32_16x16x32_bf16 v[14:17], v[160:163], v[234:237], v[14:17]
	s_waitcnt vmcnt(31)
	s_waitcnt lgkmcnt(0)
	s_barrier
; #define MD_GLDS_A(buf, tau) do { _Pragma("unroll") for (int i = 0; i < 5; ++i) if (amask & (1u << i)) \
;         __builtin_amdgcn_global_load_lds((const unsigned*)((const char*)HIDp + aoff[i] + (size_t)((tau) & 7) * 128), (PG8_LAS unsigned*)(MD_SA(buf) + wid * 1024 + i * 8192), 16, 0, 0); } while (0)
; #define MD_B_ISSUE(sb, tau) do { const char* kb_ = Bb + (size_t)((tau) >> 3) * 512 + (size_t)((tau) & 7) * (64 * (size_t)RB); _Pragma("unroll") for (int j = 0; j < 8; ++j) { const char* p_ = kb_ + (size_t)j * RB; \
;         asm volatile("global_load_dwordx2 %0, %1, off" : "=&v"(sb[j]) : "v"(p_) : "memory"); } } while (0)
; #define MD_B_WAIT(sb, N) asm volatile("s_waitcnt vmcnt(%8)" : "+v"(sb[0]), "+v"(sb[1]), "+v"(sb[2]), "+v"(sb[3]), "+v"(sb[4]), "+v"(sb[5]), "+v"(sb[6]), "+v"(sb[7]) : "n"(N) : "memory")
; #define MD_END(last) do { if (last) asm volatile("s_waitcnt vmcnt(0)" ::: "memory"); else asm volatile("s_waitcnt vmcnt(8)" ::: "memory"); \
;         asm volatile("s_waitcnt lgkmcnt(0)" ::: "memory"); __builtin_amdgcn_s_barrier(); asm volatile("" ::: "memory"); } while (0)
; __device__ __forceinline__ void moe_down_stream(PG8_LAS unsigned char* lds, int e, int cb0, int slot0, int nv, const bf16_t* HIDp, const float* Wd, bf16_t* Y, const float* slot_w, const int* slot_dst) {
;     ...
;     for (int t = 0; t < NT; t += 2) {
;         if (t + 2 < NT) MD_B_WAIT(s1, 8); else MD_B_WAIT(s1, 0);
;         MD_B_WRITE(s1, 1); __builtin_amdgcn_sched_barrier(0); MD_GLDS_A(1, t + 1); __builtin_amdgcn_sched_barrier(0);
;         if (t + 3 < NT) MD_B_ISSUE(s1, t + 3);
;         MD_COMPUTE(0);
;         MD_END(t + 3 >= NT);
;         if (t + 2 < NT) { MD_B_WAIT(s0, 8); MD_B_WRITE(s0, 0); __builtin_amdgcn_sched_barrier(0); MD_GLDS_A(0, t + 2); __builtin_amdgcn_sched_barrier(0); }
;         if (t + 4 < NT) MD_B_ISSUE(s0, t + 4);
;         MD_COMPUTE(1);
;         MD_END(t + 4 >= NT);
	s_mov_b32 s49, s46
	s_mov_b32 s46, s47
	s_mov_b32 s47, s48
	s_mov_b32 s48, s49
	v_cvt_pk_bf16_f32 v172, v186, v188
	v_cvt_pk_bf16_f32 v173, v190, v192
	v_cvt_pk_bf16_f32 v174, v194, v196
	v_cvt_pk_bf16_f32 v175, v198, v200
	v_cvt_pk_bf16_f32 v176, v187, v189
	v_cvt_pk_bf16_f32 v177, v191, v193
	v_cvt_pk_bf16_f32 v178, v195, v197
	v_cvt_pk_bf16_f32 v179, v199, v201
	ds_write_b128 v95, v[172:175] offset:0
	ds_write_b128 v95, v[176:179] offset:128
	v_add_u32_e32 v91, s46, v135
	v_add_u32_e32 v93, s46, v137
	ds_read_b128 v[238:241], v139 offset:19456
	ds_read_b128 v[242:245], v139 offset:21504
	ds_read_b128 v[246:249], v139 offset:23552
	ds_read_b128 v[250:253], v139 offset:25600
	ds_read_b128 v[218:221], v91 offset:0
	ds_read_b128 v[222:225], v91 offset:2048
	ds_read_b128 v[226:229], v91 offset:4096
	ds_read_b128 v[230:233], v91 offset:6144
	ds_read_b128 v[234:237], v91 offset:8192
	s_add_i32 s49, s48, s74
	s_add_i32 s52, s52, 1
	s_and_b32 s54, s52, 7
	s_cmp_eq_u32 s54, 0
	s_cselect_b32 s54, s53, s32
	s_cselect_b32 s55, -1, 0
	s_add_u32 s30, s30, s54
	s_addc_u32 s31, s31, s55
	s_waitcnt lgkmcnt(0)
	v_mfma_f32_16x16x32_bf16 v[78:81], v[238:241], v[218:221], v[78:81]
	v_mfma_f32_16x16x32_bf16 v[74:77], v[242:245], v[218:221], v[74:77]
	v_mfma_f32_16x16x32_bf16 v[70:73], v[246:249], v[218:221], v[70:73]
	v_mfma_f32_16x16x32_bf16 v[66:69], v[250:253], v[218:221], v[66:69]
	ds_read_b128 v[218:221], v93 offset:0
	ds_read_b128 v[142:145], v141 offset:19456
	s_mov_b32 m0, s49
	s_nop 0
	global_load_lds_dwordx4 v88, s[30:31]
	v_mfma_f32_16x16x32_bf16 v[62:65], v[238:241], v[222:225], v[62:65]
	v_mfma_f32_16x16x32_bf16 v[58:61], v[242:245], v[222:225], v[58:61]
	v_mfma_f32_16x16x32_bf16 v[54:57], v[246:249], v[222:225], v[54:57]
	v_mfma_f32_16x16x32_bf16 v[50:53], v[250:253], v[222:225], v[50:53]
	ds_read_b128 v[222:225], v93 offset:2048
	ds_read_b128 v[146:149], v141 offset:21504
	s_add_i32 m0, s49, 0x2000
	s_nop 0
	global_load_lds_dwordx4 v90, s[30:31]
	v_mfma_f32_16x16x32_bf16 v[46:49], v[238:241], v[226:229], v[46:49]
	v_mfma_f32_16x16x32_bf16 v[42:45], v[242:245], v[226:229], v[42:45]
	v_mfma_f32_16x16x32_bf16 v[38:41], v[246:249], v[226:229], v[38:41]
	v_mfma_f32_16x16x32_bf16 v[34:37], v[250:253], v[226:229], v[34:37]
	ds_read_b128 v[226:229], v93 offset:4096
	ds_read_b128 v[156:159], v141 offset:23552
	s_add_i32 m0, s49, 0x4000
	s_nop 0
	global_load_lds_dwordx4 v92, s[30:31]
	v_mfma_f32_16x16x32_bf16 v[18:21], v[238:241], v[230:233], v[18:21]
	v_mfma_f32_16x16x32_bf16 v[22:25], v[242:245], v[230:233], v[22:25]
	v_mfma_f32_16x16x32_bf16 v[26:29], v[246:249], v[230:233], v[26:29]
	v_mfma_f32_16x16x32_bf16 v[30:33], v[250:253], v[230:233], v[30:33]
	ds_read_b128 v[230:233], v93 offset:6144
	ds_read_b128 v[160:163], v141 offset:25600
	s_add_i32 m0, s49, 0x6000
	s_nop 0
	global_load_lds_dwordx4 v94, s[30:31]
	v_mfma_f32_16x16x32_bf16 v[2:5], v[238:241], v[234:237], v[2:5]
	v_mfma_f32_16x16x32_bf16 v[6:9], v[242:245], v[234:237], v[6:9]
	v_mfma_f32_16x16x32_bf16 v[10:13], v[246:249], v[234:237], v[10:13]
	v_mfma_f32_16x16x32_bf16 v[14:17], v[250:253], v[234:237], v[14:17]
	ds_read_b128 v[234:237], v93 offset:8192
	s_add_i32 m0, s49, 0x8000
	s_nop 0
	global_load_lds_dwordx4 v96, s[30:31]
	s_waitcnt lgkmcnt(0)
	v_mfma_f32_16x16x32_bf16 v[78:81], v[142:145], v[218:221], v[78:81]
	v_mfma_f32_16x16x32_bf16 v[74:77], v[146:149], v[218:221], v[74:77]
	v_mfma_f32_16x16x32_bf16 v[70:73], v[156:159], v[218:221], v[70:73]
	v_mfma_f32_16x16x32_bf16 v[66:69], v[160:163], v[218:221], v[66:69]
	s_add_i32 s51, s51, 1
	s_and_b32 s54, s51, 7
	s_cmp_eq_u32 s54, 0
	s_cselect_b32 s44, s34, s35
	s_cselect_b32 s45, -1, 0
	v_lshl_add_u64 v[132:133], v[132:133], 0, s[44:45]
	global_load_dwordx2 v[186:187], v[132:133], off
	v_lshl_add_u64 v[180:181], v[132:133], 0, s[24:25]
	global_load_dwordx2 v[188:189], v[180:181], off
	v_mfma_f32_16x16x32_bf16 v[62:65], v[142:145], v[222:225], v[62:65]
	v_mfma_f32_16x16x32_bf16 v[58:61], v[146:149], v[222:225], v[58:61]
	v_mfma_f32_16x16x32_bf16 v[54:57], v[156:159], v[222:225], v[54:57]
	v_mfma_f32_16x16x32_bf16 v[50:53], v[160:163], v[222:225], v[50:53]
	v_lshl_add_u64 v[180:181], v[132:133], 0, s[26:27]
	global_load_dwordx2 v[190:191], v[180:181], off
	v_lshl_add_u64 v[180:181], v[132:133], 0, s[28:29]
	global_load_dwordx2 v[192:193], v[180:181], off
	v_mfma_f32_16x16x32_bf16 v[46:49], v[142:145], v[226:229], v[46:49]
	v_mfma_f32_16x16x32_bf16 v[42:45], v[146:149], v[226:229], v[42:45]
	v_mfma_f32_16x16x32_bf16 v[38:41], v[156:159], v[226:229], v[38:41]
	v_mfma_f32_16x16x32_bf16 v[34:37], v[160:163], v[226:229], v[34:37]
	v_lshl_add_u64 v[180:181], v[132:133], 0, s[36:37]
	global_load_dwordx2 v[194:195], v[180:181], off
	v_lshl_add_u64 v[180:181], v[132:133], 0, s[38:39]
	global_load_dwordx2 v[196:197], v[180:181], off
	v_mfma_f32_16x16x32_bf16 v[18:21], v[142:145], v[230:233], v[18:21]
	v_mfma_f32_16x16x32_bf16 v[22:25], v[146:149], v[230:233], v[22:25]
	v_mfma_f32_16x16x32_bf16 v[26:29], v[156:159], v[230:233], v[26:29]
	v_mfma_f32_16x16x32_bf16 v[30:33], v[160:163], v[230:233], v[30:33]
	v_lshl_add_u64 v[180:181], v[132:133], 0, s[40:41]
	global_load_dwordx2 v[198:199], v[180:181], off
	v_lshl_add_u64 v[180:181], v[132:133], 0, s[42:43]
	global_load_dwordx2 v[200:201], v[180:181], off
	v_mfma_f32_16x16x32_bf16 v[2:5], v[142:145], v[234:237], v[2:5]
	v_mfma_f32_16x16x32_bf16 v[6:9], v[146:149], v[234:237], v[6:9]
	v_mfma_f32_16x16x32_bf16 v[10:13], v[156:159], v[234:237], v[10:13]
	v_mfma_f32_16x16x32_bf16 v[14:17], v[160:163], v[234:237], v[14:17]
	s_waitcnt vmcnt(21)
	s_waitcnt lgkmcnt(0)
	s_barrier
; #define MD_GLDS_A(buf, tau) do { _Pragma("unroll") for (int i = 0; i < 5; ++i) if (amask & (1u << i)) \
;         __builtin_amdgcn_global_load_lds((const unsigned*)((const char*)HIDp + aoff[i] + (size_t)((tau) & 7) * 128), (PG8_LAS unsigned*)(MD_SA(buf) + wid * 1024 + i * 8192), 16, 0, 0); } while (0)
; #define MD_B_ISSUE(sb, tau) do { const char* kb_ = Bb + (size_t)((tau) >> 3) * 512 + (size_t)((tau) & 7) * (64 * (size_t)RB); _Pragma("unroll") for (int j = 0; j < 8; ++j) { const char* p_ = kb_ + (size_t)j * RB; \
;         asm volatile("global_load_dwordx2 %0, %1, off" : "=&v"(sb[j]) : "v"(p_) : "memory"); } } while (0)
; #define MD_B_WAIT(sb, N) asm volatile("s_waitcnt vmcnt(%8)" : "+v"(sb[0]), "+v"(sb[1]), "+v"(sb[2]), "+v"(sb[3]), "+v"(sb[4]), "+v"(sb[5]), "+v"(sb[6]), "+v"(sb[7]) : "n"(N) : "memory")
; #define MD_END(last) do { if (last) asm volatile("s_waitcnt vmcnt(0)" ::: "memory"); else asm volatile("s_waitcnt vmcnt(8)" ::: "memory"); \
;         asm volatile("s_waitcnt lgkmcnt(0)" ::: "memory"); __builtin_amdgcn_s_barrier(); asm volatile("" ::: "memory"); } while (0)
; __device__ __forceinline__ void moe_down_stream(PG8_LAS unsigned char* lds, int e, int cb0, int slot0, int nv, const bf16_t* HIDp, const float* Wd, bf16_t* Y, const float* slot_w, const int* slot_dst) {
;     ...
;     for (int t = 0; t < NT; t += 2) {
;         if (t + 2 < NT) MD_B_WAIT(s1, 8); else MD_B_WAIT(s1, 0);
;         MD_B_WRITE(s1, 1); __builtin_amdgcn_sched_barrier(0); MD_GLDS_A(1, t + 1); __builtin_amdgcn_sched_barrier(0);
;         if (t + 3 < NT) MD_B_ISSUE(s1, t + 3);
;         MD_COMPUTE(0);
;         MD_END(t + 3 >= NT);
;         if (t + 2 < NT) { MD_B_WAIT(s0, 8); MD_B_WRITE(s0, 0); __builtin_amdgcn_sched_barrier(0); MD_GLDS_A(0, t + 2); __builtin_amdgcn_sched_barrier(0); }
;         if (t + 4 < NT) MD_B_ISSUE(s0, t + 4);
;         MD_COMPUTE(1);
;         MD_END(t + 4 >= NT);
	s_mov_b32 s49, s46
	s_mov_b32 s46, s47
	s_mov_b32 s47, s48
	s_mov_b32 s48, s49
	v_cvt_pk_bf16_f32 v172, v202, v204
	v_cvt_pk_bf16_f32 v173, v206, v208
	v_cvt_pk_bf16_f32 v174, v210, v212
	v_cvt_pk_bf16_f32 v175, v214, v216
	v_cvt_pk_bf16_f32 v176, v203, v205
	v_cvt_pk_bf16_f32 v177, v207, v209
	v_cvt_pk_bf16_f32 v178, v211, v213
	v_cvt_pk_bf16_f32 v179, v215, v217
	ds_write_b128 v95, v[172:175] offset:19456
	ds_write_b128 v95, v[176:179] offset:19584
	v_add_u32_e32 v91, s46, v135
	v_add_u32_e32 v93, s46, v137
	ds_read_b128 v[238:241], v139 offset:0
	ds_read_b128 v[242:245], v139 offset:2048
	ds_read_b128 v[246:249], v139 offset:4096
	ds_read_b128 v[250:253], v139 offset:6144
	ds_read_b128 v[218:221], v91 offset:0
	ds_read_b128 v[222:225], v91 offset:2048
	ds_read_b128 v[226:229], v91 offset:4096
	ds_read_b128 v[230:233], v91 offset:6144
	ds_read_b128 v[234:237], v91 offset:8192
	s_add_i32 s49, s48, s74
	s_add_i32 s52, s52, 1
	s_and_b32 s54, s52, 7
	s_cmp_eq_u32 s54, 0
	s_cselect_b32 s54, s53, s32
	s_cselect_b32 s55, -1, 0
	s_add_u32 s30, s30, s54
	s_addc_u32 s31, s31, s55
	s_waitcnt lgkmcnt(0)
	v_mfma_f32_16x16x32_bf16 v[78:81], v[238:241], v[218:221], v[78:81]
	v_mfma_f32_16x16x32_bf16 v[74:77], v[242:245], v[218:221], v[74:77]
	v_mfma_f32_16x16x32_bf16 v[70:73], v[246:249], v[218:221], v[70:73]
	v_mfma_f32_16x16x32_bf16 v[66:69], v[250:253], v[218:221], v[66:69]
	ds_read_b128 v[218:221], v93 offset:0
	ds_read_b128 v[142:145], v141 offset:0
	s_mov_b32 m0, s49
	s_nop 0
	global_load_lds_dwordx4 v88, s[30:31]
	v_mfma_f32_16x16x32_bf16 v[62:65], v[238:241], v[222:225], v[62:65]
	v_mfma_f32_16x16x32_bf16 v[58:61], v[242:245], v[222:225], v[58:61]
	v_mfma_f32_16x16x32_bf16 v[54:57], v[246:249], v[222:225], v[54:57]
	v_mfma_f32_16x16x32_bf16 v[50:53], v[250:253], v[222:225], v[50:53]
	ds_read_b128 v[222:225], v93 offset:2048
	ds_read_b128 v[146:149], v141 offset:2048
	s_add_i32 m0, s49, 0x2000
	s_nop 0
	global_load_lds_dwordx4 v90, s[30:31]
	v_mfma_f32_16x16x32_bf16 v[46:49], v[238:241], v[226:229], v[46:49]
	v_mfma_f32_16x16x32_bf16 v[42:45], v[242:245], v[226:229], v[42:45]
	v_mfma_f32_16x16x32_bf16 v[38:41], v[246:249], v[226:229], v[38:41]
	v_mfma_f32_16x16x32_bf16 v[34:37], v[250:253], v[226:229], v[34:37]
	ds_read_b128 v[226:229], v93 offset:4096
	ds_read_b128 v[156:159], v141 offset:4096
	s_add_i32 m0, s49, 0x4000
	s_nop 0
	global_load_lds_dwordx4 v92, s[30:31]
	v_mfma_f32_16x16x32_bf16 v[18:21], v[238:241], v[230:233], v[18:21]
	v_mfma_f32_16x16x32_bf16 v[22:25], v[242:245], v[230:233], v[22:25]
	v_mfma_f32_16x16x32_bf16 v[26:29], v[246:249], v[230:233], v[26:29]
	v_mfma_f32_16x16x32_bf16 v[30:33], v[250:253], v[230:233], v[30:33]
	ds_read_b128 v[230:233], v93 offset:6144
	ds_read_b128 v[160:163], v141 offset:6144
	s_add_i32 m0, s49, 0x6000
	s_nop 0
	global_load_lds_dwordx4 v94, s[30:31]
	v_mfma_f32_16x16x32_bf16 v[2:5], v[238:241], v[234:237], v[2:5]
	v_mfma_f32_16x16x32_bf16 v[6:9], v[242:245], v[234:237], v[6:9]
	v_mfma_f32_16x16x32_bf16 v[10:13], v[246:249], v[234:237], v[10:13]
	v_mfma_f32_16x16x32_bf16 v[14:17], v[250:253], v[234:237], v[14:17]
	ds_read_b128 v[234:237], v93 offset:8192
	s_add_i32 m0, s49, 0x8000
	s_nop 0
	global_load_lds_dwordx4 v96, s[30:31]
	s_waitcnt lgkmcnt(0)
	v_mfma_f32_16x16x32_bf16 v[78:81], v[142:145], v[218:221], v[78:81]
	v_mfma_f32_16x16x32_bf16 v[74:77], v[146:149], v[218:221], v[74:77]
	v_mfma_f32_16x16x32_bf16 v[70:73], v[156:159], v[218:221], v[70:73]
	v_mfma_f32_16x16x32_bf16 v[66:69], v[160:163], v[218:221], v[66:69]
	s_add_i32 s51, s51, 1
	s_and_b32 s54, s51, 7
	s_cmp_eq_u32 s54, 0
	s_cselect_b32 s44, s34, s35
	s_cselect_b32 s45, -1, 0
	v_lshl_add_u64 v[132:133], v[132:133], 0, s[44:45]
	global_load_dwordx2 v[202:203], v[132:133], off
	v_lshl_add_u64 v[180:181], v[132:133], 0, s[24:25]
	global_load_dwordx2 v[204:205], v[180:181], off
	v_mfma_f32_16x16x32_bf16 v[62:65], v[142:145], v[222:225], v[62:65]
	v_mfma_f32_16x16x32_bf16 v[58:61], v[146:149], v[222:225], v[58:61]
	v_mfma_f32_16x16x32_bf16 v[54:57], v[156:159], v[222:225], v[54:57]
	v_mfma_f32_16x16x32_bf16 v[50:53], v[160:163], v[222:225], v[50:53]
	v_lshl_add_u64 v[180:181], v[132:133], 0, s[26:27]
	global_load_dwordx2 v[206:207], v[180:181], off
	v_lshl_add_u64 v[180:181], v[132:133], 0, s[28:29]
	global_load_dwordx2 v[208:209], v[180:181], off
	v_mfma_f32_16x16x32_bf16 v[46:49], v[142:145], v[226:229], v[46:49]
	v_mfma_f32_16x16x32_bf16 v[42:45], v[146:149], v[226:229], v[42:45]
	v_mfma_f32_16x16x32_bf16 v[38:41], v[156:159], v[226:229], v[38:41]
	v_mfma_f32_16x16x32_bf16 v[34:37], v[160:163], v[226:229], v[34:37]
	v_lshl_add_u64 v[180:181], v[132:133], 0, s[36:37]
	global_load_dwordx2 v[210:211], v[180:181], off
	v_lshl_add_u64 v[180:181], v[132:133], 0, s[38:39]
	global_load_dwordx2 v[212:213], v[180:181], off
	v_mfma_f32_16x16x32_bf16 v[18:21], v[142:145], v[230:233], v[18:21]
	v_mfma_f32_16x16x32_bf16 v[22:25], v[146:149], v[230:233], v[22:25]
	v_mfma_f32_16x16x32_bf16 v[26:29], v[156:159], v[230:233], v[26:29]
	v_mfma_f32_16x16x32_bf16 v[30:33], v[160:163], v[230:233], v[30:33]
	v_lshl_add_u64 v[180:181], v[132:133], 0, s[40:41]
	global_load_dwordx2 v[214:215], v[180:181], off
	v_lshl_add_u64 v[180:181], v[132:133], 0, s[42:43]
	global_load_dwordx2 v[216:217], v[180:181], off
	v_mfma_f32_16x16x32_bf16 v[2:5], v[142:145], v[234:237], v[2:5]
	v_mfma_f32_16x16x32_bf16 v[6:9], v[146:149], v[234:237], v[6:9]
	v_mfma_f32_16x16x32_bf16 v[10:13], v[156:159], v[234:237], v[10:13]
	v_mfma_f32_16x16x32_bf16 v[14:17], v[160:163], v[234:237], v[14:17]
	s_waitcnt vmcnt(21)
	s_waitcnt lgkmcnt(0)
	s_barrier
; #define MD_GLDS_A(buf, tau) do { _Pragma("unroll") for (int i = 0; i < 5; ++i) if (amask & (1u << i)) \
;         __builtin_amdgcn_global_load_lds((const unsigned*)((const char*)HIDp + aoff[i] + (size_t)((tau) & 7) * 128), (PG8_LAS unsigned*)(MD_SA(buf) + wid * 1024 + i * 8192), 16, 0, 0); } while (0)
; #define MD_B_ISSUE(sb, tau) do { const char* kb_ = Bb + (size_t)((tau) >> 3) * 512 + (size_t)((tau) & 7) * (64 * (size_t)RB); _Pragma("unroll") for (int j = 0; j < 8; ++j) { const char* p_ = kb_ + (size_t)j * RB; \
;         asm volatile("global_load_dwordx2 %0, %1, off" : "=&v"(sb[j]) : "v"(p_) : "memory"); } } while (0)
; #define MD_B_WAIT(sb, N) asm volatile("s_waitcnt vmcnt(%8)" : "+v"(sb[0]), "+v"(sb[1]), "+v"(sb[2]), "+v"(sb[3]), "+v"(sb[4]), "+v"(sb[5]), "+v"(sb[6]), "+v"(sb[7]) : "n"(N) : "memory")
; #define MD_END(last) do { if (last) asm volatile("s_waitcnt vmcnt(0)" ::: "memory"); else asm volatile("s_waitcnt vmcnt(8)" ::: "memory"); \
;         asm volatile("s_waitcnt lgkmcnt(0)" ::: "memory"); __builtin_amdgcn_s_barrier(); asm volatile("" ::: "memory"); } while (0)
; __device__ __forceinline__ void moe_down_stream(PG8_LAS unsigned char* lds, int e, int cb0, int slot0, int nv, const bf16_t* HIDp, const float* Wd, bf16_t* Y, const float* slot_w, const int* slot_dst) {
;     ...
;     for (int t = 0; t < NT; t += 2) {
;         if (t + 2 < NT) MD_B_WAIT(s1, 8); else MD_B_WAIT(s1, 0);
;         MD_B_WRITE(s1, 1); __builtin_amdgcn_sched_barrier(0); MD_GLDS_A(1, t + 1); __builtin_amdgcn_sched_barrier(0);
;         if (t + 3 < NT) MD_B_ISSUE(s1, t + 3);
;         MD_COMPUTE(0);
;         MD_END(t + 3 >= NT);
;         if (t + 2 < NT) { MD_B_WAIT(s0, 8); MD_B_WRITE(s0, 0); __builtin_amdgcn_sched_barrier(0); MD_GLDS_A(0, t + 2); __builtin_amdgcn_sched_barrier(0); }
;         if (t + 4 < NT) MD_B_ISSUE(s0, t + 4);
;         MD_COMPUTE(1);
;         MD_END(t + 4 >= NT);
	s_mov_b32 s49, s46
	s_mov_b32 s46, s47
	s_mov_b32 s47, s48
	s_mov_b32 s48, s49
	v_cvt_pk_bf16_f32 v172, v98, v100
	v_cvt_pk_bf16_f32 v173, v102, v104
	v_cvt_pk_bf16_f32 v174, v106, v108
	v_cvt_pk_bf16_f32 v175, v110, v112
	v_cvt_pk_bf16_f32 v176, v99, v101
	v_cvt_pk_bf16_f32 v177, v103, v105
	v_cvt_pk_bf16_f32 v178, v107, v109
	v_cvt_pk_bf16_f32 v179, v111, v113
	ds_write_b128 v95, v[172:175] offset:0
	ds_write_b128 v95, v[176:179] offset:128
	v_add_u32_e32 v91, s46, v135
	v_add_u32_e32 v93, s46, v137
	ds_read_b128 v[238:241], v139 offset:19456
	ds_read_b128 v[242:245], v139 offset:21504
	ds_read_b128 v[246:249], v139 offset:23552
	ds_read_b128 v[250:253], v139 offset:25600
	ds_read_b128 v[218:221], v91 offset:0
	ds_read_b128 v[222:225], v91 offset:2048
	ds_read_b128 v[226:229], v91 offset:4096
	ds_read_b128 v[230:233], v91 offset:6144
	ds_read_b128 v[234:237], v91 offset:8192
	s_add_i32 s49, s48, s74
	s_add_i32 s52, s52, 1
	s_and_b32 s54, s52, 7
	s_cmp_eq_u32 s54, 0
	s_cselect_b32 s54, s53, s32
	s_cselect_b32 s55, -1, 0
	s_add_u32 s30, s30, s54
	s_addc_u32 s31, s31, s55
	s_waitcnt lgkmcnt(0)
	v_mfma_f32_16x16x32_bf16 v[78:81], v[238:241], v[218:221], v[78:81]
	v_mfma_f32_16x16x32_bf16 v[74:77], v[242:245], v[218:221], v[74:77]
	v_mfma_f32_16x16x32_bf16 v[70:73], v[246:249], v[218:221], v[70:73]
	v_mfma_f32_16x16x32_bf16 v[66:69], v[250:253], v[218:221], v[66:69]
	ds_read_b128 v[218:221], v93 offset:0
	ds_read_b128 v[142:145], v141 offset:19456
	s_mov_b32 m0, s49
	s_nop 0
	global_load_lds_dwordx4 v88, s[30:31]
	v_mfma_f32_16x16x32_bf16 v[62:65], v[238:241], v[222:225], v[62:65]
	v_mfma_f32_16x16x32_bf16 v[58:61], v[242:245], v[222:225], v[58:61]
	v_mfma_f32_16x16x32_bf16 v[54:57], v[246:249], v[222:225], v[54:57]
	v_mfma_f32_16x16x32_bf16 v[50:53], v[250:253], v[222:225], v[50:53]
	ds_read_b128 v[222:225], v93 offset:2048
	ds_read_b128 v[146:149], v141 offset:21504
	s_add_i32 m0, s49, 0x2000
	s_nop 0
	global_load_lds_dwordx4 v90, s[30:31]
	v_mfma_f32_16x16x32_bf16 v[46:49], v[238:241], v[226:229], v[46:49]
	v_mfma_f32_16x16x32_bf16 v[42:45], v[242:245], v[226:229], v[42:45]
	v_mfma_f32_16x16x32_bf16 v[38:41], v[246:249], v[226:229], v[38:41]
	v_mfma_f32_16x16x32_bf16 v[34:37], v[250:253], v[226:229], v[34:37]
	ds_read_b128 v[226:229], v93 offset:4096
	ds_read_b128 v[156:159], v141 offset:23552
	s_add_i32 m0, s49, 0x4000
	s_nop 0
	global_load_lds_dwordx4 v92, s[30:31]
	v_mfma_f32_16x16x32_bf16 v[18:21], v[238:241], v[230:233], v[18:21]
	v_mfma_f32_16x16x32_bf16 v[22:25], v[242:245], v[230:233], v[22:25]
	v_mfma_f32_16x16x32_bf16 v[26:29], v[246:249], v[230:233], v[26:29]
	v_mfma_f32_16x16x32_bf16 v[30:33], v[250:253], v[230:233], v[30:33]
	ds_read_b128 v[230:233], v93 offset:6144
	ds_read_b128 v[160:163], v141 offset:25600
	s_add_i32 m0, s49, 0x6000
	s_nop 0
	global_load_lds_dwordx4 v94, s[30:31]
	v_mfma_f32_16x16x32_bf16 v[2:5], v[238:241], v[234:237], v[2:5]
	v_mfma_f32_16x16x32_bf16 v[6:9], v[242:245], v[234:237], v[6:9]
	v_mfma_f32_16x16x32_bf16 v[10:13], v[246:249], v[234:237], v[10:13]
	v_mfma_f32_16x16x32_bf16 v[14:17], v[250:253], v[234:237], v[14:17]
	ds_read_b128 v[234:237], v93 offset:8192
	s_add_i32 m0, s49, 0x8000
	s_nop 0
	global_load_lds_dwordx4 v96, s[30:31]
	s_waitcnt lgkmcnt(0)
	v_mfma_f32_16x16x32_bf16 v[78:81], v[142:145], v[218:221], v[78:81]
	v_mfma_f32_16x16x32_bf16 v[74:77], v[146:149], v[218:221], v[74:77]
	v_mfma_f32_16x16x32_bf16 v[70:73], v[156:159], v[218:221], v[70:73]
	v_mfma_f32_16x16x32_bf16 v[66:69], v[160:163], v[218:221], v[66:69]
	v_mfma_f32_16x16x32_bf16 v[62:65], v[142:145], v[222:225], v[62:65]
	v_mfma_f32_16x16x32_bf16 v[58:61], v[146:149], v[222:225], v[58:61]
	v_mfma_f32_16x16x32_bf16 v[54:57], v[156:159], v[222:225], v[54:57]
	v_mfma_f32_16x16x32_bf16 v[50:53], v[160:163], v[222:225], v[50:53]
	v_mfma_f32_16x16x32_bf16 v[46:49], v[142:145], v[226:229], v[46:49]
	v_mfma_f32_16x16x32_bf16 v[42:45], v[146:149], v[226:229], v[42:45]
	v_mfma_f32_16x16x32_bf16 v[38:41], v[156:159], v[226:229], v[38:41]
	v_mfma_f32_16x16x32_bf16 v[34:37], v[160:163], v[226:229], v[34:37]
	v_mfma_f32_16x16x32_bf16 v[18:21], v[142:145], v[230:233], v[18:21]
	v_mfma_f32_16x16x32_bf16 v[22:25], v[146:149], v[230:233], v[22:25]
	v_mfma_f32_16x16x32_bf16 v[26:29], v[156:159], v[230:233], v[26:29]
	v_mfma_f32_16x16x32_bf16 v[30:33], v[160:163], v[230:233], v[30:33]
	v_mfma_f32_16x16x32_bf16 v[2:5], v[142:145], v[234:237], v[2:5]
	v_mfma_f32_16x16x32_bf16 v[6:9], v[146:149], v[234:237], v[6:9]
	v_mfma_f32_16x16x32_bf16 v[10:13], v[156:159], v[234:237], v[10:13]
	v_mfma_f32_16x16x32_bf16 v[14:17], v[160:163], v[234:237], v[14:17]
	s_waitcnt vmcnt(13)
	s_waitcnt lgkmcnt(0)
	s_barrier
; #define MD_GLDS_A(buf, tau) do { _Pragma("unroll") for (int i = 0; i < 5; ++i) if (amask & (1u << i)) \
;         __builtin_amdgcn_global_load_lds((const unsigned*)((const char*)HIDp + aoff[i] + (size_t)((tau) & 7) * 128), (PG8_LAS unsigned*)(MD_SA(buf) + wid * 1024 + i * 8192), 16, 0, 0); } while (0)
; #define MD_B_ISSUE(sb, tau) do { const char* kb_ = Bb + (size_t)((tau) >> 3) * 512 + (size_t)((tau) & 7) * (64 * (size_t)RB); _Pragma("unroll") for (int j = 0; j < 8; ++j) { const char* p_ = kb_ + (size_t)j * RB; \
;         asm volatile("global_load_dwordx2 %0, %1, off" : "=&v"(sb[j]) : "v"(p_) : "memory"); } } while (0)
; #define MD_B_WAIT(sb, N) asm volatile("s_waitcnt vmcnt(%8)" : "+v"(sb[0]), "+v"(sb[1]), "+v"(sb[2]), "+v"(sb[3]), "+v"(sb[4]), "+v"(sb[5]), "+v"(sb[6]), "+v"(sb[7]) : "n"(N) : "memory")
; #define MD_END(last) do { if (last) asm volatile("s_waitcnt vmcnt(0)" ::: "memory"); else asm volatile("s_waitcnt vmcnt(8)" ::: "memory"); \
;         asm volatile("s_waitcnt lgkmcnt(0)" ::: "memory"); __builtin_amdgcn_s_barrier(); asm volatile("" ::: "memory"); } while (0)
; __device__ __forceinline__ void moe_down_stream(PG8_LAS unsigned char* lds, int e, int cb0, int slot0, int nv, const bf16_t* HIDp, const float* Wd, bf16_t* Y, const float* slot_w, const int* slot_dst) {
;     ...
;     for (int t = 0; t < NT; t += 2) {
;         if (t + 2 < NT) MD_B_WAIT(s1, 8); else MD_B_WAIT(s1, 0);
;         MD_B_WRITE(s1, 1); __builtin_amdgcn_sched_barrier(0); MD_GLDS_A(1, t + 1); __builtin_amdgcn_sched_barrier(0);
;         if (t + 3 < NT) MD_B_ISSUE(s1, t + 3);
;         MD_COMPUTE(0);
;         MD_END(t + 3 >= NT);
;         if (t + 2 < NT) { MD_B_WAIT(s0, 8); MD_B_WRITE(s0, 0); __builtin_amdgcn_sched_barrier(0); MD_GLDS_A(0, t + 2); __builtin_amdgcn_sched_barrier(0); }
;         if (t + 4 < NT) MD_B_ISSUE(s0, t + 4);
;         MD_COMPUTE(1);
;         MD_END(t + 4 >= NT);
	s_mov_b32 s49, s46
	s_mov_b32 s46, s47
	s_mov_b32 s47, s48
	s_mov_b32 s48, s49
	v_cvt_pk_bf16_f32 v172, v114, v116
	v_cvt_pk_bf16_f32 v173, v118, v120
	v_cvt_pk_bf16_f32 v174, v122, v124
	v_cvt_pk_bf16_f32 v175, v126, v128
	v_cvt_pk_bf16_f32 v176, v115, v117
	v_cvt_pk_bf16_f32 v177, v119, v121
	v_cvt_pk_bf16_f32 v178, v123, v125
	v_cvt_pk_bf16_f32 v179, v127, v129
	ds_write_b128 v95, v[172:175] offset:19456
	ds_write_b128 v95, v[176:179] offset:19584
	v_add_u32_e32 v91, s46, v135
	v_add_u32_e32 v93, s46, v137
	ds_read_b128 v[238:241], v139 offset:0
	ds_read_b128 v[242:245], v139 offset:2048
	ds_read_b128 v[246:249], v139 offset:4096
	ds_read_b128 v[250:253], v139 offset:6144
	ds_read_b128 v[218:221], v91 offset:0
	ds_read_b128 v[222:225], v91 offset:2048
	ds_read_b128 v[226:229], v91 offset:4096
	ds_read_b128 v[230:233], v91 offset:6144
	ds_read_b128 v[234:237], v91 offset:8192
	s_add_i32 s49, s48, s74
	s_add_i32 s52, s52, 1
	s_and_b32 s54, s52, 7
	s_cmp_eq_u32 s54, 0
	s_cselect_b32 s54, s53, s32
	s_cselect_b32 s55, -1, 0
	s_add_u32 s30, s30, s54
	s_addc_u32 s31, s31, s55
	s_waitcnt lgkmcnt(0)
	v_mfma_f32_16x16x32_bf16 v[78:81], v[238:241], v[218:221], v[78:81]
	v_mfma_f32_16x16x32_bf16 v[74:77], v[242:245], v[218:221], v[74:77]
	v_mfma_f32_16x16x32_bf16 v[70:73], v[246:249], v[218:221], v[70:73]
	v_mfma_f32_16x16x32_bf16 v[66:69], v[250:253], v[218:221], v[66:69]
	ds_read_b128 v[218:221], v93 offset:0
	ds_read_b128 v[142:145], v141 offset:0
	s_mov_b32 m0, s49
	s_nop 0
	global_load_lds_dwordx4 v88, s[30:31]
	v_mfma_f32_16x16x32_bf16 v[62:65], v[238:241], v[222:225], v[62:65]
	v_mfma_f32_16x16x32_bf16 v[58:61], v[242:245], v[222:225], v[58:61]
	v_mfma_f32_16x16x32_bf16 v[54:57], v[246:249], v[222:225], v[54:57]
	v_mfma_f32_16x16x32_bf16 v[50:53], v[250:253], v[222:225], v[50:53]
	ds_read_b128 v[222:225], v93 offset:2048
	ds_read_b128 v[146:149], v141 offset:2048
	s_add_i32 m0, s49, 0x2000
	s_nop 0
	global_load_lds_dwordx4 v90, s[30:31]
	v_mfma_f32_16x16x32_bf16 v[46:49], v[238:241], v[226:229], v[46:49]
	v_mfma_f32_16x16x32_bf16 v[42:45], v[242:245], v[226:229], v[42:45]
	v_mfma_f32_16x16x32_bf16 v[38:41], v[246:249], v[226:229], v[38:41]
	v_mfma_f32_16x16x32_bf16 v[34:37], v[250:253], v[226:229], v[34:37]
	ds_read_b128 v[226:229], v93 offset:4096
	ds_read_b128 v[156:159], v141 offset:4096
	s_add_i32 m0, s49, 0x4000
	s_nop 0
	global_load_lds_dwordx4 v92, s[30:31]
	v_mfma_f32_16x16x32_bf16 v[18:21], v[238:241], v[230:233], v[18:21]
	v_mfma_f32_16x16x32_bf16 v[22:25], v[242:245], v[230:233], v[22:25]
	v_mfma_f32_16x16x32_bf16 v[26:29], v[246:249], v[230:233], v[26:29]
	v_mfma_f32_16x16x32_bf16 v[30:33], v[250:253], v[230:233], v[30:33]
	ds_read_b128 v[230:233], v93 offset:6144
	ds_read_b128 v[160:163], v141 offset:6144
	s_add_i32 m0, s49, 0x6000
	s_nop 0
	global_load_lds_dwordx4 v94, s[30:31]
	v_mfma_f32_16x16x32_bf16 v[2:5], v[238:241], v[234:237], v[2:5]
	v_mfma_f32_16x16x32_bf16 v[6:9], v[242:245], v[234:237], v[6:9]
	v_mfma_f32_16x16x32_bf16 v[10:13], v[246:249], v[234:237], v[10:13]
	v_mfma_f32_16x16x32_bf16 v[14:17], v[250:253], v[234:237], v[14:17]
	ds_read_b128 v[234:237], v93 offset:8192
	s_add_i32 m0, s49, 0x8000
	s_nop 0
	global_load_lds_dwordx4 v96, s[30:31]
	s_waitcnt lgkmcnt(0)
	v_mfma_f32_16x16x32_bf16 v[78:81], v[142:145], v[218:221], v[78:81]
	v_mfma_f32_16x16x32_bf16 v[74:77], v[146:149], v[218:221], v[74:77]
	v_mfma_f32_16x16x32_bf16 v[70:73], v[156:159], v[218:221], v[70:73]
	v_mfma_f32_16x16x32_bf16 v[66:69], v[160:163], v[218:221], v[66:69]
	v_mfma_f32_16x16x32_bf16 v[62:65], v[142:145], v[222:225], v[62:65]
	v_mfma_f32_16x16x32_bf16 v[58:61], v[146:149], v[222:225], v[58:61]
	v_mfma_f32_16x16x32_bf16 v[54:57], v[156:159], v[222:225], v[54:57]
	v_mfma_f32_16x16x32_bf16 v[50:53], v[160:163], v[222:225], v[50:53]
	v_mfma_f32_16x16x32_bf16 v[46:49], v[142:145], v[226:229], v[46:49]
	v_mfma_f32_16x16x32_bf16 v[42:45], v[146:149], v[226:229], v[42:45]
	v_mfma_f32_16x16x32_bf16 v[38:41], v[156:159], v[226:229], v[38:41]
	v_mfma_f32_16x16x32_bf16 v[34:37], v[160:163], v[226:229], v[34:37]
	v_mfma_f32_16x16x32_bf16 v[18:21], v[142:145], v[230:233], v[18:21]
	v_mfma_f32_16x16x32_bf16 v[22:25], v[146:149], v[230:233], v[22:25]
	v_mfma_f32_16x16x32_bf16 v[26:29], v[156:159], v[230:233], v[26:29]
	v_mfma_f32_16x16x32_bf16 v[30:33], v[160:163], v[230:233], v[30:33]
	v_mfma_f32_16x16x32_bf16 v[2:5], v[142:145], v[234:237], v[2:5]
	v_mfma_f32_16x16x32_bf16 v[6:9], v[146:149], v[234:237], v[6:9]
	v_mfma_f32_16x16x32_bf16 v[10:13], v[156:159], v[234:237], v[10:13]
	v_mfma_f32_16x16x32_bf16 v[14:17], v[160:163], v[234:237], v[14:17]
	s_waitcnt vmcnt(5)
	s_waitcnt lgkmcnt(0)
	s_barrier
; #define MD_GLDS_A(buf, tau) do { _Pragma("unroll") for (int i = 0; i < 5; ++i) if (amask & (1u << i)) \
;         __builtin_amdgcn_global_load_lds((const unsigned*)((const char*)HIDp + aoff[i] + (size_t)((tau) & 7) * 128), (PG8_LAS unsigned*)(MD_SA(buf) + wid * 1024 + i * 8192), 16, 0, 0); } while (0)
; #define MD_B_ISSUE(sb, tau) do { const char* kb_ = Bb + (size_t)((tau) >> 3) * 512 + (size_t)((tau) & 7) * (64 * (size_t)RB); _Pragma("unroll") for (int j = 0; j < 8; ++j) { const char* p_ = kb_ + (size_t)j * RB; \
;         asm volatile("global_load_dwordx2 %0, %1, off" : "=&v"(sb[j]) : "v"(p_) : "memory"); } } while (0)
; #define MD_B_WAIT(sb, N) asm volatile("s_waitcnt vmcnt(%8)" : "+v"(sb[0]), "+v"(sb[1]), "+v"(sb[2]), "+v"(sb[3]), "+v"(sb[4]), "+v"(sb[5]), "+v"(sb[6]), "+v"(sb[7]) : "n"(N) : "memory")
; #define MD_END(last) do { if (last) asm volatile("s_waitcnt vmcnt(0)" ::: "memory"); else asm volatile("s_waitcnt vmcnt(8)" ::: "memory"); \
;         asm volatile("s_waitcnt lgkmcnt(0)" ::: "memory"); __builtin_amdgcn_s_barrier(); asm volatile("" ::: "memory"); } while (0)
; __device__ __forceinline__ void moe_down_stream(PG8_LAS unsigned char* lds, int e, int cb0, int slot0, int nv, const bf16_t* HIDp, const float* Wd, bf16_t* Y, const float* slot_w, const int* slot_dst) {
;     ...
;     for (int t = 0; t < NT; t += 2) {
;         if (t + 2 < NT) MD_B_WAIT(s1, 8); else MD_B_WAIT(s1, 0);
;         MD_B_WRITE(s1, 1); __builtin_amdgcn_sched_barrier(0); MD_GLDS_A(1, t + 1); __builtin_amdgcn_sched_barrier(0);
;         if (t + 3 < NT) MD_B_ISSUE(s1, t + 3);
;         MD_COMPUTE(0);
;         MD_END(t + 3 >= NT);
;         if (t + 2 < NT) { MD_B_WAIT(s0, 8); MD_B_WRITE(s0, 0); __builtin_amdgcn_sched_barrier(0); MD_GLDS_A(0, t + 2); __builtin_amdgcn_sched_barrier(0); }
;         if (t + 4 < NT) MD_B_ISSUE(s0, t + 4);
;         MD_COMPUTE(1);
;         MD_END(t + 4 >= NT);
	s_mov_b32 s49, s46
	s_mov_b32 s46, s47
	s_mov_b32 s47, s48
	s_mov_b32 s48, s49
	v_cvt_pk_bf16_f32 v172, v186, v188
	v_cvt_pk_bf16_f32 v173, v190, v192
	v_cvt_pk_bf16_f32 v174, v194, v196
	v_cvt_pk_bf16_f32 v175, v198, v200
	v_cvt_pk_bf16_f32 v176, v187, v189
	v_cvt_pk_bf16_f32 v177, v191, v193
	v_cvt_pk_bf16_f32 v178, v195, v197
	v_cvt_pk_bf16_f32 v179, v199, v201
	ds_write_b128 v95, v[172:175] offset:0
	ds_write_b128 v95, v[176:179] offset:128
	v_add_u32_e32 v91, s46, v135
	v_add_u32_e32 v93, s46, v137
	ds_read_b128 v[238:241], v139 offset:19456
	ds_read_b128 v[242:245], v139 offset:21504
	ds_read_b128 v[246:249], v139 offset:23552
	ds_read_b128 v[250:253], v139 offset:25600
	ds_read_b128 v[218:221], v91 offset:0
	ds_read_b128 v[222:225], v91 offset:2048
	ds_read_b128 v[226:229], v91 offset:4096
	ds_read_b128 v[230:233], v91 offset:6144
	ds_read_b128 v[234:237], v91 offset:8192
	s_add_i32 s49, s48, s74
	s_add_i32 s52, s52, 1
	s_and_b32 s54, s52, 7
	s_cmp_eq_u32 s54, 0
	s_cselect_b32 s54, s53, s32
	s_cselect_b32 s55, -1, 0
	s_add_u32 s30, s30, s54
	s_addc_u32 s31, s31, s55
	s_waitcnt lgkmcnt(0)
	v_mfma_f32_16x16x32_bf16 v[78:81], v[238:241], v[218:221], v[78:81]
	v_mfma_f32_16x16x32_bf16 v[74:77], v[242:245], v[218:221], v[74:77]
	v_mfma_f32_16x16x32_bf16 v[70:73], v[246:249], v[218:221], v[70:73]
	v_mfma_f32_16x16x32_bf16 v[66:69], v[250:253], v[218:221], v[66:69]
	ds_read_b128 v[218:221], v93 offset:0
	ds_read_b128 v[142:145], v141 offset:19456
	s_mov_b32 m0, s49
	s_nop 0
	global_load_lds_dwordx4 v88, s[30:31]
	v_mfma_f32_16x16x32_bf16 v[62:65], v[238:241], v[222:225], v[62:65]
	v_mfma_f32_16x16x32_bf16 v[58:61], v[242:245], v[222:225], v[58:61]
	v_mfma_f32_16x16x32_bf16 v[54:57], v[246:249], v[222:225], v[54:57]
	v_mfma_f32_16x16x32_bf16 v[50:53], v[250:253], v[222:225], v[50:53]
	ds_read_b128 v[222:225], v93 offset:2048
	ds_read_b128 v[146:149], v141 offset:21504
	s_add_i32 m0, s49, 0x2000
	s_nop 0
	global_load_lds_dwordx4 v90, s[30:31]
	v_mfma_f32_16x16x32_bf16 v[46:49], v[238:241], v[226:229], v[46:49]
	v_mfma_f32_16x16x32_bf16 v[42:45], v[242:245], v[226:229], v[42:45]
	v_mfma_f32_16x16x32_bf16 v[38:41], v[246:249], v[226:229], v[38:41]
	v_mfma_f32_16x16x32_bf16 v[34:37], v[250:253], v[226:229], v[34:37]
	ds_read_b128 v[226:229], v93 offset:4096
	ds_read_b128 v[156:159], v141 offset:23552
	s_add_i32 m0, s49, 0x4000
	s_nop 0
	global_load_lds_dwordx4 v92, s[30:31]
	v_mfma_f32_16x16x32_bf16 v[18:21], v[238:241], v[230:233], v[18:21]
	v_mfma_f32_16x16x32_bf16 v[22:25], v[242:245], v[230:233], v[22:25]
	v_mfma_f32_16x16x32_bf16 v[26:29], v[246:249], v[230:233], v[26:29]
	v_mfma_f32_16x16x32_bf16 v[30:33], v[250:253], v[230:233], v[30:33]
	ds_read_b128 v[230:233], v93 offset:6144
	ds_read_b128 v[160:163], v141 offset:25600
	s_add_i32 m0, s49, 0x6000
	s_nop 0
	global_load_lds_dwordx4 v94, s[30:31]
	v_mfma_f32_16x16x32_bf16 v[2:5], v[238:241], v[234:237], v[2:5]
	v_mfma_f32_16x16x32_bf16 v[6:9], v[242:245], v[234:237], v[6:9]
	v_mfma_f32_16x16x32_bf16 v[10:13], v[246:249], v[234:237], v[10:13]
	v_mfma_f32_16x16x32_bf16 v[14:17], v[250:253], v[234:237], v[14:17]
	ds_read_b128 v[234:237], v93 offset:8192
	s_add_i32 m0, s49, 0x8000
	s_nop 0
	global_load_lds_dwordx4 v96, s[30:31]
	s_waitcnt lgkmcnt(0)
	v_mfma_f32_16x16x32_bf16 v[78:81], v[142:145], v[218:221], v[78:81]
	v_mfma_f32_16x16x32_bf16 v[74:77], v[146:149], v[218:221], v[74:77]
	v_mfma_f32_16x16x32_bf16 v[70:73], v[156:159], v[218:221], v[70:73]
	v_mfma_f32_16x16x32_bf16 v[66:69], v[160:163], v[218:221], v[66:69]
	v_mfma_f32_16x16x32_bf16 v[62:65], v[142:145], v[222:225], v[62:65]
	v_mfma_f32_16x16x32_bf16 v[58:61], v[146:149], v[222:225], v[58:61]
	v_mfma_f32_16x16x32_bf16 v[54:57], v[156:159], v[222:225], v[54:57]
	v_mfma_f32_16x16x32_bf16 v[50:53], v[160:163], v[222:225], v[50:53]
	v_mfma_f32_16x16x32_bf16 v[46:49], v[142:145], v[226:229], v[46:49]
	v_mfma_f32_16x16x32_bf16 v[42:45], v[146:149], v[226:229], v[42:45]
	v_mfma_f32_16x16x32_bf16 v[38:41], v[156:159], v[226:229], v[38:41]
	v_mfma_f32_16x16x32_bf16 v[34:37], v[160:163], v[226:229], v[34:37]
	v_mfma_f32_16x16x32_bf16 v[18:21], v[142:145], v[230:233], v[18:21]
	v_mfma_f32_16x16x32_bf16 v[22:25], v[146:149], v[230:233], v[22:25]
	v_mfma_f32_16x16x32_bf16 v[26:29], v[156:159], v[230:233], v[26:29]
	v_mfma_f32_16x16x32_bf16 v[30:33], v[160:163], v[230:233], v[30:33]
	v_mfma_f32_16x16x32_bf16 v[2:5], v[142:145], v[234:237], v[2:5]
	v_mfma_f32_16x16x32_bf16 v[6:9], v[146:149], v[234:237], v[6:9]
	v_mfma_f32_16x16x32_bf16 v[10:13], v[156:159], v[234:237], v[10:13]
	v_mfma_f32_16x16x32_bf16 v[14:17], v[160:163], v[234:237], v[14:17]
	s_waitcnt vmcnt(5)
	s_waitcnt lgkmcnt(0)
	s_barrier
; #define MD_GLDS_A(buf, tau) do { _Pragma("unroll") for (int i = 0; i < 5; ++i) if (amask & (1u << i)) \
;         __builtin_amdgcn_global_load_lds((const unsigned*)((const char*)HIDp + aoff[i] + (size_t)((tau) & 7) * 128), (PG8_LAS unsigned*)(MD_SA(buf) + wid * 1024 + i * 8192), 16, 0, 0); } while (0)
; #define MD_B_ISSUE(sb, tau) do { const char* kb_ = Bb + (size_t)((tau) >> 3) * 512 + (size_t)((tau) & 7) * (64 * (size_t)RB); _Pragma("unroll") for (int j = 0; j < 8; ++j) { const char* p_ = kb_ + (size_t)j * RB; \
;         asm volatile("global_load_dwordx2 %0, %1, off" : "=&v"(sb[j]) : "v"(p_) : "memory"); } } while (0)
; #define MD_B_WAIT(sb, N) asm volatile("s_waitcnt vmcnt(%8)" : "+v"(sb[0]), "+v"(sb[1]), "+v"(sb[2]), "+v"(sb[3]), "+v"(sb[4]), "+v"(sb[5]), "+v"(sb[6]), "+v"(sb[7]) : "n"(N) : "memory")
; #define MD_END(last) do { if (last) asm volatile("s_waitcnt vmcnt(0)" ::: "memory"); else asm volatile("s_waitcnt vmcnt(8)" ::: "memory"); \
;         asm volatile("s_waitcnt lgkmcnt(0)" ::: "memory"); __builtin_amdgcn_s_barrier(); asm volatile("" ::: "memory"); } while (0)
; __device__ __forceinline__ void moe_down_stream(PG8_LAS unsigned char* lds, int e, int cb0, int slot0, int nv, const bf16_t* HIDp, const float* Wd, bf16_t* Y, const float* slot_w, const int* slot_dst) {
;     ...
;     for (int t = 0; t < NT; t += 2) {
;         if (t + 2 < NT) MD_B_WAIT(s1, 8); else MD_B_WAIT(s1, 0);
;         MD_B_WRITE(s1, 1); __builtin_amdgcn_sched_barrier(0); MD_GLDS_A(1, t + 1); __builtin_amdgcn_sched_barrier(0);
;         if (t + 3 < NT) MD_B_ISSUE(s1, t + 3);
;         MD_COMPUTE(0);
;         MD_END(t + 3 >= NT);
;         if (t + 2 < NT) { MD_B_WAIT(s0, 8); MD_B_WRITE(s0, 0); __builtin_amdgcn_sched_barrier(0); MD_GLDS_A(0, t + 2); __builtin_amdgcn_sched_barrier(0); }
;         if (t + 4 < NT) MD_B_ISSUE(s0, t + 4);
;         MD_COMPUTE(1);
;         MD_END(t + 4 >= NT);
	s_mov_b32 s49, s46
	s_mov_b32 s46, s47
	s_mov_b32 s47, s48
	s_mov_b32 s48, s49
	v_cvt_pk_bf16_f32 v172, v202, v204
	v_cvt_pk_bf16_f32 v173, v206, v208
	v_cvt_pk_bf16_f32 v174, v210, v212
	v_cvt_pk_bf16_f32 v175, v214, v216
	v_cvt_pk_bf16_f32 v176, v203, v205
	v_cvt_pk_bf16_f32 v177, v207, v209
	v_cvt_pk_bf16_f32 v178, v211, v213
	v_cvt_pk_bf16_f32 v179, v215, v217
	ds_write_b128 v95, v[172:175] offset:19456
	ds_write_b128 v95, v[176:179] offset:19584
	v_add_u32_e32 v91, s46, v135
	v_add_u32_e32 v93, s46, v137
	ds_read_b128 v[238:241], v139 offset:0
	ds_read_b128 v[242:245], v139 offset:2048
	ds_read_b128 v[246:249], v139 offset:4096
	ds_read_b128 v[250:253], v139 offset:6144
	ds_read_b128 v[218:221], v91 offset:0
	ds_read_b128 v[222:225], v91 offset:2048
	ds_read_b128 v[226:229], v91 offset:4096
	ds_read_b128 v[230:233], v91 offset:6144
	ds_read_b128 v[234:237], v91 offset:8192
	s_waitcnt lgkmcnt(0)
	v_mfma_f32_16x16x32_bf16 v[78:81], v[238:241], v[218:221], v[78:81]
	v_mfma_f32_16x16x32_bf16 v[74:77], v[242:245], v[218:221], v[74:77]
	v_mfma_f32_16x16x32_bf16 v[70:73], v[246:249], v[218:221], v[70:73]
	v_mfma_f32_16x16x32_bf16 v[66:69], v[250:253], v[218:221], v[66:69]
	ds_read_b128 v[218:221], v93 offset:0
	ds_read_b128 v[142:145], v141 offset:0
	v_mfma_f32_16x16x32_bf16 v[62:65], v[238:241], v[222:225], v[62:65]
	v_mfma_f32_16x16x32_bf16 v[58:61], v[242:245], v[222:225], v[58:61]
	v_mfma_f32_16x16x32_bf16 v[54:57], v[246:249], v[222:225], v[54:57]
	v_mfma_f32_16x16x32_bf16 v[50:53], v[250:253], v[222:225], v[50:53]
	ds_read_b128 v[222:225], v93 offset:2048
	ds_read_b128 v[146:149], v141 offset:2048
	v_mfma_f32_16x16x32_bf16 v[46:49], v[238:241], v[226:229], v[46:49]
	v_mfma_f32_16x16x32_bf16 v[42:45], v[242:245], v[226:229], v[42:45]
	v_mfma_f32_16x16x32_bf16 v[38:41], v[246:249], v[226:229], v[38:41]
	v_mfma_f32_16x16x32_bf16 v[34:37], v[250:253], v[226:229], v[34:37]
	ds_read_b128 v[226:229], v93 offset:4096
	ds_read_b128 v[156:159], v141 offset:4096
	v_mfma_f32_16x16x32_bf16 v[18:21], v[238:241], v[230:233], v[18:21]
	v_mfma_f32_16x16x32_bf16 v[22:25], v[242:245], v[230:233], v[22:25]
	v_mfma_f32_16x16x32_bf16 v[26:29], v[246:249], v[230:233], v[26:29]
	v_mfma_f32_16x16x32_bf16 v[30:33], v[250:253], v[230:233], v[30:33]
	ds_read_b128 v[230:233], v93 offset:6144
	ds_read_b128 v[160:163], v141 offset:6144
	v_mfma_f32_16x16x32_bf16 v[2:5], v[238:241], v[234:237], v[2:5]
	v_mfma_f32_16x16x32_bf16 v[6:9], v[242:245], v[234:237], v[6:9]
	v_mfma_f32_16x16x32_bf16 v[10:13], v[246:249], v[234:237], v[10:13]
	v_mfma_f32_16x16x32_bf16 v[14:17], v[250:253], v[234:237], v[14:17]
	ds_read_b128 v[234:237], v93 offset:8192
	s_waitcnt lgkmcnt(0)
	v_mfma_f32_16x16x32_bf16 v[78:81], v[142:145], v[218:221], v[78:81]
	v_mfma_f32_16x16x32_bf16 v[74:77], v[146:149], v[218:221], v[74:77]
	v_mfma_f32_16x16x32_bf16 v[70:73], v[156:159], v[218:221], v[70:73]
	v_mfma_f32_16x16x32_bf16 v[66:69], v[160:163], v[218:221], v[66:69]
	v_mfma_f32_16x16x32_bf16 v[62:65], v[142:145], v[222:225], v[62:65]
	v_mfma_f32_16x16x32_bf16 v[58:61], v[146:149], v[222:225], v[58:61]
	v_mfma_f32_16x16x32_bf16 v[54:57], v[156:159], v[222:225], v[54:57]
	v_mfma_f32_16x16x32_bf16 v[50:53], v[160:163], v[222:225], v[50:53]
	v_mfma_f32_16x16x32_bf16 v[46:49], v[142:145], v[226:229], v[46:49]
	v_mfma_f32_16x16x32_bf16 v[42:45], v[146:149], v[226:229], v[42:45]
	v_mfma_f32_16x16x32_bf16 v[38:41], v[156:159], v[226:229], v[38:41]
	v_mfma_f32_16x16x32_bf16 v[34:37], v[160:163], v[226:229], v[34:37]
	v_mfma_f32_16x16x32_bf16 v[18:21], v[142:145], v[230:233], v[18:21]
	v_mfma_f32_16x16x32_bf16 v[22:25], v[146:149], v[230:233], v[22:25]
	v_mfma_f32_16x16x32_bf16 v[26:29], v[156:159], v[230:233], v[26:29]
	v_mfma_f32_16x16x32_bf16 v[30:33], v[160:163], v[230:233], v[30:33]
	v_mfma_f32_16x16x32_bf16 v[2:5], v[142:145], v[234:237], v[2:5]
	v_mfma_f32_16x16x32_bf16 v[6:9], v[146:149], v[234:237], v[6:9]
	v_mfma_f32_16x16x32_bf16 v[10:13], v[156:159], v[234:237], v[10:13]
	v_mfma_f32_16x16x32_bf16 v[14:17], v[160:163], v[234:237], v[14:17]
	s_waitcnt vmcnt(0)
	s_waitcnt lgkmcnt(0)
	s_barrier
	s_mov_b32 s49, s46
	s_mov_b32 s46, s47
	s_mov_b32 s47, s48
	s_mov_b32 s48, s49
	v_add_u32_e32 v91, s46, v135
	v_add_u32_e32 v93, s46, v137
	ds_read_b128 v[238:241], v139 offset:19456
	ds_read_b128 v[242:245], v139 offset:21504
	ds_read_b128 v[246:249], v139 offset:23552
	ds_read_b128 v[250:253], v139 offset:25600
	ds_read_b128 v[218:221], v91 offset:0
	ds_read_b128 v[222:225], v91 offset:2048
	ds_read_b128 v[226:229], v91 offset:4096
	ds_read_b128 v[230:233], v91 offset:6144
	ds_read_b128 v[234:237], v91 offset:8192
	s_waitcnt lgkmcnt(0)
	v_mfma_f32_16x16x32_bf16 v[78:81], v[238:241], v[218:221], v[78:81]
	v_mfma_f32_16x16x32_bf16 v[74:77], v[242:245], v[218:221], v[74:77]
	v_mfma_f32_16x16x32_bf16 v[70:73], v[246:249], v[218:221], v[70:73]
	v_mfma_f32_16x16x32_bf16 v[66:69], v[250:253], v[218:221], v[66:69]
	ds_read_b128 v[218:221], v93 offset:0
	ds_read_b128 v[142:145], v141 offset:19456
	v_mfma_f32_16x16x32_bf16 v[62:65], v[238:241], v[222:225], v[62:65]
	v_mfma_f32_16x16x32_bf16 v[58:61], v[242:245], v[222:225], v[58:61]
	v_mfma_f32_16x16x32_bf16 v[54:57], v[246:249], v[222:225], v[54:57]
	v_mfma_f32_16x16x32_bf16 v[50:53], v[250:253], v[222:225], v[50:53]
	ds_read_b128 v[222:225], v93 offset:2048
	ds_read_b128 v[146:149], v141 offset:21504
	v_mfma_f32_16x16x32_bf16 v[46:49], v[238:241], v[226:229], v[46:49]
	v_mfma_f32_16x16x32_bf16 v[42:45], v[242:245], v[226:229], v[42:45]
	v_mfma_f32_16x16x32_bf16 v[38:41], v[246:249], v[226:229], v[38:41]
	v_mfma_f32_16x16x32_bf16 v[34:37], v[250:253], v[226:229], v[34:37]
	ds_read_b128 v[226:229], v93 offset:4096
	ds_read_b128 v[156:159], v141 offset:23552
	v_mfma_f32_16x16x32_bf16 v[18:21], v[238:241], v[230:233], v[18:21]
	v_mfma_f32_16x16x32_bf16 v[22:25], v[242:245], v[230:233], v[22:25]
	v_mfma_f32_16x16x32_bf16 v[26:29], v[246:249], v[230:233], v[26:29]
	v_mfma_f32_16x16x32_bf16 v[30:33], v[250:253], v[230:233], v[30:33]
	ds_read_b128 v[230:233], v93 offset:6144
	ds_read_b128 v[160:163], v141 offset:25600
	v_mfma_f32_16x16x32_bf16 v[2:5], v[238:241], v[234:237], v[2:5]
	v_mfma_f32_16x16x32_bf16 v[6:9], v[242:245], v[234:237], v[6:9]
	v_mfma_f32_16x16x32_bf16 v[10:13], v[246:249], v[234:237], v[10:13]
	v_mfma_f32_16x16x32_bf16 v[14:17], v[250:253], v[234:237], v[14:17]
	ds_read_b128 v[234:237], v93 offset:8192
	s_waitcnt lgkmcnt(0)
; #define PG8_LAS __attribute__((address_space(3)))
; __device__ __forceinline__ unsigned cvtpk(float lo, float hi) { f32x2 v = {lo, hi}; bf16x2_t b = __builtin_convertvector(v, bf16x2_t); return __builtin_bit_cast(unsigned, b); }
; __device__ __forceinline__ void moe_down_stream(PG8_LAS unsigned char* lds, int e, int cb0, int slot0, int nv, const bf16_t* HIDp, const float* Wd, bf16_t* Y, const float* slot_w, const int* slot_dst) {
;     ...
;         if (((t + 1) & 7) == 7) {
;             const int cb = cb0 + ((t + 1) >> 3);
; #pragma unroll
;             for (int m = 0; m < DNM; ++m) {
;                 const float w_ = lw[4 * (16 * m + fr) + wr];
; #pragma unroll
;                 for (int p = 0; p < 2; ++p) { const f32x4 v0 = acc[m][2 * p] * w_, v1 = acc[m][2 * p + 1] * w_; u32x4 w; w.x = cvtpk(v0[0], v0[1]); w.y = cvtpk(v0[2], v0[3]); w.z = cvtpk(v1[0], v1[1]); w.w = cvtpk(v1[2], v1[3]);
;                     *(PG8_LAS u32x4*)(stg + fr * 128 + (((4 * p + fq) ^ (fr & 7)) * 16)) = w; }
; #pragma unroll
;                 for (int hh = 0; hh < 2; ++hh) { const int r = (lane >> 3) + 8 * hh, cc = lane & 7; const u32x4 d = *(const PG8_LAS u32x4*)(stg + r * 128 + ((cc ^ (r & 7)) * 16)); const int dst_ = ldst[4 * (16 * m + r) + wr];
;                     if (dst_ >= 0) *(u32x4*)(Y + (size_t)dst_ * D + 128 * cb + 64 * wc + 8 * cc) = d; }
; #pragma unroll
;                 for (int n = 0; n < 4; ++n) acc[m][n] = (f32x4){0.f, 0.f, 0.f, 0.f}; } }
	v_mfma_f32_16x16x32_bf16 v[78:81], v[142:145], v[218:221], v[78:81]
	v_mfma_f32_16x16x32_bf16 v[74:77], v[146:149], v[218:221], v[74:77]
	v_mfma_f32_16x16x32_bf16 v[70:73], v[156:159], v[218:221], v[70:73]
	v_mfma_f32_16x16x32_bf16 v[66:69], v[160:163], v[218:221], v[66:69]
	v_mfma_f32_16x16x32_bf16 v[62:65], v[142:145], v[222:225], v[62:65]
	v_mfma_f32_16x16x32_bf16 v[58:61], v[146:149], v[222:225], v[58:61]
	v_mfma_f32_16x16x32_bf16 v[54:57], v[156:159], v[222:225], v[54:57]
	v_mfma_f32_16x16x32_bf16 v[50:53], v[160:163], v[222:225], v[50:53]
	v_mfma_f32_16x16x32_bf16 v[46:49], v[142:145], v[226:229], v[46:49]
	v_mfma_f32_16x16x32_bf16 v[42:45], v[146:149], v[226:229], v[42:45]
	v_mfma_f32_16x16x32_bf16 v[38:41], v[156:159], v[226:229], v[38:41]
	v_mfma_f32_16x16x32_bf16 v[34:37], v[160:163], v[226:229], v[34:37]
	v_mfma_f32_16x16x32_bf16 v[18:21], v[142:145], v[230:233], v[18:21]
	v_mfma_f32_16x16x32_bf16 v[22:25], v[146:149], v[230:233], v[22:25]
	v_mfma_f32_16x16x32_bf16 v[26:29], v[156:159], v[230:233], v[26:29]
	v_mfma_f32_16x16x32_bf16 v[30:33], v[160:163], v[230:233], v[30:33]
	v_mfma_f32_16x16x32_bf16 v[2:5], v[142:145], v[234:237], v[2:5]
	v_mfma_f32_16x16x32_bf16 v[6:9], v[146:149], v[234:237], v[6:9]
	v_mfma_f32_16x16x32_bf16 v[10:13], v[156:159], v[234:237], v[10:13]
	v_mfma_f32_16x16x32_bf16 v[14:17], v[160:163], v[234:237], v[14:17]
	s_waitcnt lgkmcnt(0)
	s_barrier
	s_mov_b32 s49, s46
	s_mov_b32 s46, s47
	s_mov_b32 s47, s48
	s_mov_b32 s48, s49
	s_add_i32 s54, s48, s74
	v_add_u32_e32 v164, s54, v84
	v_add_u32_e32 v165, s54, v85
	ds_read_b32 v150, v82 offset:0
	ds_read_b32 v151, v83 offset:0
	ds_read_b32 v166, v83 offset:128
	s_waitcnt lgkmcnt(2)
	v_mul_f32_e32 v78, v150, v78
	v_mul_f32_e32 v79, v150, v79
	v_mul_f32_e32 v80, v150, v80
	v_mul_f32_e32 v81, v150, v81
	v_mul_f32_e32 v74, v150, v74
	v_mul_f32_e32 v75, v150, v75
	v_mul_f32_e32 v76, v150, v76
	v_mul_f32_e32 v77, v150, v77
	v_cvt_pk_bf16_f32 v182, v78, v79
	v_cvt_pk_bf16_f32 v183, v80, v81
	v_cvt_pk_bf16_f32 v184, v74, v75
	v_cvt_pk_bf16_f32 v185, v76, v77
	ds_write_b128 v164, v[182:185]
	v_mul_f32_e32 v70, v150, v70
	v_mul_f32_e32 v71, v150, v71
	v_mul_f32_e32 v72, v150, v72
	v_mul_f32_e32 v73, v150, v73
	v_mul_f32_e32 v66, v150, v66
	v_mul_f32_e32 v67, v150, v67
	v_mul_f32_e32 v68, v150, v68
	v_mul_f32_e32 v69, v150, v69
	v_cvt_pk_bf16_f32 v182, v70, v71
	v_cvt_pk_bf16_f32 v183, v72, v73
	v_cvt_pk_bf16_f32 v184, v66, v67
	v_cvt_pk_bf16_f32 v185, v68, v69
	v_xor_b32_e32 v167, 64, v164
	ds_write_b128 v167, v[182:185]
	v_mov_b32_e32 v78, 0
	v_mov_b32_e32 v74, 0
	v_mov_b32_e32 v70, 0
	v_mov_b32_e32 v66, 0
	v_mov_b32_e32 v79, 0
	v_mov_b32_e32 v75, 0
	v_mov_b32_e32 v71, 0
	v_mov_b32_e32 v67, 0
	v_mov_b32_e32 v80, 0
	v_mov_b32_e32 v76, 0
	v_mov_b32_e32 v72, 0
	v_mov_b32_e32 v68, 0
	v_mov_b32_e32 v81, 0
	v_mov_b32_e32 v77, 0
	v_mov_b32_e32 v73, 0
	v_mov_b32_e32 v69, 0
	ds_read_b128 v[182:185], v165 offset:0
	v_cmp_lt_i32_e32 vcc, -1, v151
	v_lshlrev_b32_e32 v148, 13, v151
	v_mov_b32_e32 v149, 0
	v_lshl_add_u64 v[148:149], v[148:149], 0, v[86:87]
	v_cndmask_b32_e32 v148, v168, v148, vcc
	v_cndmask_b32_e32 v149, v169, v149, vcc
	s_waitcnt lgkmcnt(0)
	global_store_dwordx4 v[148:149], v[182:185], off
	ds_read_b128 v[182:185], v165 offset:8192
	v_cmp_lt_i32_e32 vcc, -1, v166
	v_lshlrev_b32_e32 v148, 13, v166
	v_mov_b32_e32 v149, 0
	v_lshl_add_u64 v[148:149], v[148:149], 0, v[86:87]
	v_cndmask_b32_e32 v148, v168, v148, vcc
	v_cndmask_b32_e32 v149, v169, v149, vcc
	s_waitcnt lgkmcnt(0)
	global_store_dwordx4 v[148:149], v[182:185], off
	ds_read_b32 v150, v82 offset:256
	ds_read_b32 v151, v83 offset:256
	ds_read_b32 v166, v83 offset:384
	s_waitcnt lgkmcnt(2)
	v_mul_f32_e32 v62, v150, v62
	v_mul_f32_e32 v63, v150, v63
	v_mul_f32_e32 v64, v150, v64
	v_mul_f32_e32 v65, v150, v65
	v_mul_f32_e32 v58, v150, v58
	v_mul_f32_e32 v59, v150, v59
	v_mul_f32_e32 v60, v150, v60
	v_mul_f32_e32 v61, v150, v61
	v_cvt_pk_bf16_f32 v182, v62, v63
	v_cvt_pk_bf16_f32 v183, v64, v65
	v_cvt_pk_bf16_f32 v184, v58, v59
	v_cvt_pk_bf16_f32 v185, v60, v61
	ds_write_b128 v164, v[182:185]
	v_mul_f32_e32 v54, v150, v54
	v_mul_f32_e32 v55, v150, v55
	v_mul_f32_e32 v56, v150, v56
	v_mul_f32_e32 v57, v150, v57
	v_mul_f32_e32 v50, v150, v50
	v_mul_f32_e32 v51, v150, v51
	v_mul_f32_e32 v52, v150, v52
	v_mul_f32_e32 v53, v150, v53
	v_cvt_pk_bf16_f32 v182, v54, v55
	v_cvt_pk_bf16_f32 v183, v56, v57
	v_cvt_pk_bf16_f32 v184, v50, v51
	v_cvt_pk_bf16_f32 v185, v52, v53
	v_xor_b32_e32 v167, 64, v164
	ds_write_b128 v167, v[182:185]
	v_mov_b32_e32 v62, 0
	v_mov_b32_e32 v58, 0
	v_mov_b32_e32 v54, 0
	v_mov_b32_e32 v50, 0
	v_mov_b32_e32 v63, 0
	v_mov_b32_e32 v59, 0
	v_mov_b32_e32 v55, 0
	v_mov_b32_e32 v51, 0
	v_mov_b32_e32 v64, 0
	v_mov_b32_e32 v60, 0
	v_mov_b32_e32 v56, 0
	v_mov_b32_e32 v52, 0
	v_mov_b32_e32 v65, 0
	v_mov_b32_e32 v61, 0
	v_mov_b32_e32 v57, 0
	v_mov_b32_e32 v53, 0
	ds_read_b128 v[182:185], v165 offset:0
	v_cmp_lt_i32_e32 vcc, -1, v151
	v_lshlrev_b32_e32 v148, 13, v151
	v_mov_b32_e32 v149, 0
	v_lshl_add_u64 v[148:149], v[148:149], 0, v[86:87]
	v_cndmask_b32_e32 v148, v168, v148, vcc
	v_cndmask_b32_e32 v149, v169, v149, vcc
	s_waitcnt lgkmcnt(0)
	global_store_dwordx4 v[148:149], v[182:185], off
	ds_read_b128 v[182:185], v165 offset:8192
	v_cmp_lt_i32_e32 vcc, -1, v166
	v_lshlrev_b32_e32 v148, 13, v166
	v_mov_b32_e32 v149, 0
	v_lshl_add_u64 v[148:149], v[148:149], 0, v[86:87]
	v_cndmask_b32_e32 v148, v168, v148, vcc
	v_cndmask_b32_e32 v149, v169, v149, vcc
	s_waitcnt lgkmcnt(0)
	global_store_dwordx4 v[148:149], v[182:185], off
	ds_read_b32 v150, v82 offset:512
	ds_read_b32 v151, v83 offset:512
	ds_read_b32 v166, v83 offset:640
	s_waitcnt lgkmcnt(2)
; #define PG8_LAS __attribute__((address_space(3)))
; __device__ __forceinline__ unsigned cvtpk(float lo, float hi) { f32x2 v = {lo, hi}; bf16x2_t b = __builtin_convertvector(v, bf16x2_t); return __builtin_bit_cast(unsigned, b); }
; __device__ __forceinline__ void moe_down_stream(PG8_LAS unsigned char* lds, int e, int cb0, int slot0, int nv, const bf16_t* HIDp, const float* Wd, bf16_t* Y, const float* slot_w, const int* slot_dst) {
;     ...
;         if (((t + 1) & 7) == 7) {
;             const int cb = cb0 + ((t + 1) >> 3);
; #pragma unroll
;             for (int m = 0; m < DNM; ++m) {
;                 const float w_ = lw[4 * (16 * m + fr) + wr];
; #pragma unroll
;                 for (int p = 0; p < 2; ++p) { const f32x4 v0 = acc[m][2 * p] * w_, v1 = acc[m][2 * p + 1] * w_; u32x4 w; w.x = cvtpk(v0[0], v0[1]); w.y = cvtpk(v0[2], v0[3]); w.z = cvtpk(v1[0], v1[1]); w.w = cvtpk(v1[2], v1[3]);
;                     *(PG8_LAS u32x4*)(stg + fr * 128 + (((4 * p + fq) ^ (fr & 7)) * 16)) = w; }
; #pragma unroll
;                 for (int hh = 0; hh < 2; ++hh) { const int r = (lane >> 3) + 8 * hh, cc = lane & 7; const u32x4 d = *(const PG8_LAS u32x4*)(stg + r * 128 + ((cc ^ (r & 7)) * 16)); const int dst_ = ldst[4 * (16 * m + r) + wr];
;                     if (dst_ >= 0) *(u32x4*)(Y + (size_t)dst_ * D + 128 * cb + 64 * wc + 8 * cc) = d; }
; #pragma unroll
;                 for (int n = 0; n < 4; ++n) acc[m][n] = (f32x4){0.f, 0.f, 0.f, 0.f}; } }
	v_mul_f32_e32 v46, v150, v46
	v_mul_f32_e32 v47, v150, v47
	v_mul_f32_e32 v48, v150, v48
	v_mul_f32_e32 v49, v150, v49
	v_mul_f32_e32 v42, v150, v42
	v_mul_f32_e32 v43, v150, v43
	v_mul_f32_e32 v44, v150, v44
	v_mul_f32_e32 v45, v150, v45
	v_cvt_pk_bf16_f32 v182, v46, v47
	v_cvt_pk_bf16_f32 v183, v48, v49
	v_cvt_pk_bf16_f32 v184, v42, v43
	v_cvt_pk_bf16_f32 v185, v44, v45
	ds_write_b128 v164, v[182:185]
	v_mul_f32_e32 v38, v150, v38
	v_mul_f32_e32 v39, v150, v39
	v_mul_f32_e32 v40, v150, v40
	v_mul_f32_e32 v41, v150, v41
	v_mul_f32_e32 v34, v150, v34
	v_mul_f32_e32 v35, v150, v35
	v_mul_f32_e32 v36, v150, v36
	v_mul_f32_e32 v37, v150, v37
	v_cvt_pk_bf16_f32 v182, v38, v39
	v_cvt_pk_bf16_f32 v183, v40, v41
	v_cvt_pk_bf16_f32 v184, v34, v35
	v_cvt_pk_bf16_f32 v185, v36, v37
	v_xor_b32_e32 v167, 64, v164
	ds_write_b128 v167, v[182:185]
	v_mov_b32_e32 v46, 0
	v_mov_b32_e32 v42, 0
	v_mov_b32_e32 v38, 0
	v_mov_b32_e32 v34, 0
	v_mov_b32_e32 v47, 0
	v_mov_b32_e32 v43, 0
	v_mov_b32_e32 v39, 0
	v_mov_b32_e32 v35, 0
	v_mov_b32_e32 v48, 0
	v_mov_b32_e32 v44, 0
	v_mov_b32_e32 v40, 0
	v_mov_b32_e32 v36, 0
	v_mov_b32_e32 v49, 0
	v_mov_b32_e32 v45, 0
	v_mov_b32_e32 v41, 0
	v_mov_b32_e32 v37, 0
	ds_read_b128 v[182:185], v165 offset:0
	v_cmp_lt_i32_e32 vcc, -1, v151
	v_lshlrev_b32_e32 v148, 13, v151
	v_mov_b32_e32 v149, 0
	v_lshl_add_u64 v[148:149], v[148:149], 0, v[86:87]
	v_cndmask_b32_e32 v148, v168, v148, vcc
	v_cndmask_b32_e32 v149, v169, v149, vcc
	s_waitcnt lgkmcnt(0)
	global_store_dwordx4 v[148:149], v[182:185], off
	ds_read_b128 v[182:185], v165 offset:8192
	v_cmp_lt_i32_e32 vcc, -1, v166
	v_lshlrev_b32_e32 v148, 13, v166
	v_mov_b32_e32 v149, 0
	v_lshl_add_u64 v[148:149], v[148:149], 0, v[86:87]
	v_cndmask_b32_e32 v148, v168, v148, vcc
	v_cndmask_b32_e32 v149, v169, v149, vcc
	s_waitcnt lgkmcnt(0)
	global_store_dwordx4 v[148:149], v[182:185], off
	ds_read_b32 v150, v82 offset:768
	ds_read_b32 v151, v83 offset:768
	ds_read_b32 v166, v83 offset:896
	s_waitcnt lgkmcnt(2)
	v_mul_f32_e32 v18, v150, v18
	v_mul_f32_e32 v19, v150, v19
	v_mul_f32_e32 v20, v150, v20
	v_mul_f32_e32 v21, v150, v21
	v_mul_f32_e32 v22, v150, v22
	v_mul_f32_e32 v23, v150, v23
	v_mul_f32_e32 v24, v150, v24
	v_mul_f32_e32 v25, v150, v25
	v_cvt_pk_bf16_f32 v182, v18, v19
	v_cvt_pk_bf16_f32 v183, v20, v21
	v_cvt_pk_bf16_f32 v184, v22, v23
	v_cvt_pk_bf16_f32 v185, v24, v25
	ds_write_b128 v164, v[182:185]
	v_mul_f32_e32 v26, v150, v26
	v_mul_f32_e32 v27, v150, v27
	v_mul_f32_e32 v28, v150, v28
	v_mul_f32_e32 v29, v150, v29
	v_mul_f32_e32 v30, v150, v30
	v_mul_f32_e32 v31, v150, v31
	v_mul_f32_e32 v32, v150, v32
	v_mul_f32_e32 v33, v150, v33
	v_cvt_pk_bf16_f32 v182, v26, v27
	v_cvt_pk_bf16_f32 v183, v28, v29
	v_cvt_pk_bf16_f32 v184, v30, v31
	v_cvt_pk_bf16_f32 v185, v32, v33
	v_xor_b32_e32 v167, 64, v164
	ds_write_b128 v167, v[182:185]
	v_mov_b32_e32 v18, 0
	v_mov_b32_e32 v22, 0
	v_mov_b32_e32 v26, 0
	v_mov_b32_e32 v30, 0
	v_mov_b32_e32 v19, 0
	v_mov_b32_e32 v23, 0
	v_mov_b32_e32 v27, 0
	v_mov_b32_e32 v31, 0
	v_mov_b32_e32 v20, 0
	v_mov_b32_e32 v24, 0
	v_mov_b32_e32 v28, 0
	v_mov_b32_e32 v32, 0
	v_mov_b32_e32 v21, 0
	v_mov_b32_e32 v25, 0
	v_mov_b32_e32 v29, 0
	v_mov_b32_e32 v33, 0
	ds_read_b128 v[182:185], v165 offset:0
	v_cmp_lt_i32_e32 vcc, -1, v151
	v_lshlrev_b32_e32 v148, 13, v151
	v_mov_b32_e32 v149, 0
	v_lshl_add_u64 v[148:149], v[148:149], 0, v[86:87]
	v_cndmask_b32_e32 v148, v168, v148, vcc
	v_cndmask_b32_e32 v149, v169, v149, vcc
	s_waitcnt lgkmcnt(0)
	global_store_dwordx4 v[148:149], v[182:185], off
	ds_read_b128 v[182:185], v165 offset:8192
	v_cmp_lt_i32_e32 vcc, -1, v166
	v_lshlrev_b32_e32 v148, 13, v166
	v_mov_b32_e32 v149, 0
	v_lshl_add_u64 v[148:149], v[148:149], 0, v[86:87]
	v_cndmask_b32_e32 v148, v168, v148, vcc
	v_cndmask_b32_e32 v149, v169, v149, vcc
	s_waitcnt lgkmcnt(0)
	global_store_dwordx4 v[148:149], v[182:185], off
	ds_read_b32 v150, v82 offset:1024
	ds_read_b32 v151, v83 offset:1024
	ds_read_b32 v166, v83 offset:1152
	s_waitcnt lgkmcnt(2)
	v_mul_f32_e32 v2, v150, v2
	v_mul_f32_e32 v3, v150, v3
	v_mul_f32_e32 v4, v150, v4
	v_mul_f32_e32 v5, v150, v5
	v_mul_f32_e32 v6, v150, v6
	v_mul_f32_e32 v7, v150, v7
	v_mul_f32_e32 v8, v150, v8
	v_mul_f32_e32 v9, v150, v9
	v_cvt_pk_bf16_f32 v182, v2, v3
	v_cvt_pk_bf16_f32 v183, v4, v5
	v_cvt_pk_bf16_f32 v184, v6, v7
	v_cvt_pk_bf16_f32 v185, v8, v9
	ds_write_b128 v164, v[182:185]
	v_mul_f32_e32 v10, v150, v10
	v_mul_f32_e32 v11, v150, v11
	v_mul_f32_e32 v12, v150, v12
	v_mul_f32_e32 v13, v150, v13
	v_mul_f32_e32 v14, v150, v14
	v_mul_f32_e32 v15, v150, v15
	v_mul_f32_e32 v16, v150, v16
	v_mul_f32_e32 v17, v150, v17
	v_cvt_pk_bf16_f32 v182, v10, v11
	v_cvt_pk_bf16_f32 v183, v12, v13
	v_cvt_pk_bf16_f32 v184, v14, v15
	v_cvt_pk_bf16_f32 v185, v16, v17
	v_xor_b32_e32 v167, 64, v164
	ds_write_b128 v167, v[182:185]
	v_mov_b32_e32 v2, 0
	v_mov_b32_e32 v6, 0
	v_mov_b32_e32 v10, 0
	v_mov_b32_e32 v14, 0
	v_mov_b32_e32 v3, 0
	v_mov_b32_e32 v7, 0
	v_mov_b32_e32 v11, 0
	v_mov_b32_e32 v15, 0
	v_mov_b32_e32 v4, 0
	v_mov_b32_e32 v8, 0
	v_mov_b32_e32 v12, 0
	v_mov_b32_e32 v16, 0
	v_mov_b32_e32 v5, 0
	v_mov_b32_e32 v9, 0
	v_mov_b32_e32 v13, 0
	v_mov_b32_e32 v17, 0
	ds_read_b128 v[182:185], v165 offset:0
	v_cmp_lt_i32_e32 vcc, -1, v151
	v_lshlrev_b32_e32 v148, 13, v151
	v_mov_b32_e32 v149, 0
	v_lshl_add_u64 v[148:149], v[148:149], 0, v[86:87]
	v_cndmask_b32_e32 v148, v168, v148, vcc
	v_cndmask_b32_e32 v149, v169, v149, vcc
	s_waitcnt lgkmcnt(0)
	global_store_dwordx4 v[148:149], v[182:185], off
	ds_read_b128 v[182:185], v165 offset:8192
	v_cmp_lt_i32_e32 vcc, -1, v166
	v_lshlrev_b32_e32 v148, 13, v166
	v_mov_b32_e32 v149, 0
	v_lshl_add_u64 v[148:149], v[148:149], 0, v[86:87]
	v_cndmask_b32_e32 v148, v168, v148, vcc
	v_cndmask_b32_e32 v149, v169, v149, vcc
	s_waitcnt lgkmcnt(0)
	global_store_dwordx4 v[148:149], v[182:185], off
	v_add_co_u32_e32 v86, vcc, 0x800, v86
	s_nop 1
	v_addc_co_u32_e32 v87, vcc, 0, v87, vcc
	s_waitcnt lgkmcnt(0)
	s_branch .Lmd_done
; #define MD_GLDS_A(buf, tau) do { _Pragma("unroll") for (int i = 0; i < 5; ++i) if (amask & (1u << i)) \
;         __builtin_amdgcn_global_load_lds((const unsigned*)((const char*)HIDp + aoff[i] + (size_t)((tau) & 7) * 128), (PG8_LAS unsigned*)(MD_SA(buf) + wid * 1024 + i * 8192), 16, 0, 0); } while (0)
; #define MD_B_ISSUE(sb, tau) do { const char* kb_ = Bb + (size_t)((tau) >> 3) * 512 + (size_t)((tau) & 7) * (64 * (size_t)RB); _Pragma("unroll") for (int j = 0; j < 8; ++j) { const char* p_ = kb_ + (size_t)j * RB; \
;         asm volatile("global_load_dwordx2 %0, %1, off" : "=&v"(sb[j]) : "v"(p_) : "memory"); } } while (0)
; #define MD_B_WAIT(sb, N) asm volatile("s_waitcnt vmcnt(%8)" : "+v"(sb[0]), "+v"(sb[1]), "+v"(sb[2]), "+v"(sb[3]), "+v"(sb[4]), "+v"(sb[5]), "+v"(sb[6]), "+v"(sb[7]) : "n"(N) : "memory")
; #define MD_END(last) do { if (last) asm volatile("s_waitcnt vmcnt(0)" ::: "memory"); else asm volatile("s_waitcnt vmcnt(8)" ::: "memory"); \
;         asm volatile("s_waitcnt lgkmcnt(0)" ::: "memory"); __builtin_amdgcn_s_barrier(); asm volatile("" ::: "memory"); } while (0)
; __device__ __forceinline__ void moe_down_stream(PG8_LAS unsigned char* lds, int e, int cb0, int slot0, int nv, const bf16_t* HIDp, const float* Wd, bf16_t* Y, const float* slot_w, const int* slot_dst) {
;     ...
;     MD_GLDS_A(0, 0); MD_B_ISSUE(s0, 0); MD_B_ISSUE(s1, 1);
;     MD_B_WAIT(s0, 8); MD_B_WRITE(s0, 0); __builtin_amdgcn_sched_barrier(0); MD_B_ISSUE(s0, 2);
;     asm volatile("s_waitcnt vmcnt(16)" ::: "memory");
;     asm volatile("s_waitcnt lgkmcnt(0)" ::: "memory"); __builtin_amdgcn_s_barrier(); asm volatile("" ::: "memory");
; #pragma unroll 1
;     for (int t = 0; t < NT; t += 2) {
;         if (t + 2 < NT) MD_B_WAIT(s1, 8); else MD_B_WAIT(s1, 0);
;         MD_B_WRITE(s1, 1); __builtin_amdgcn_sched_barrier(0); MD_GLDS_A(1, t + 1); __builtin_amdgcn_sched_barrier(0);
;         if (t + 3 < NT) MD_B_ISSUE(s1, t + 3);
;         MD_COMPUTE(0);
;         MD_END(t + 3 >= NT);
;         if (t + 2 < NT) { MD_B_WAIT(s0, 8); MD_B_WRITE(s0, 0); __builtin_amdgcn_sched_barrier(0); MD_GLDS_A(0, t + 2); __builtin_amdgcn_sched_barrier(0); }
;         if (t + 4 < NT) MD_B_ISSUE(s0, t + 4);
;         MD_COMPUTE(1);
;         MD_END(t + 4 >= NT);
.Lmd_grpY:
	s_add_i32 s49, s48, s74
	s_add_i32 s52, s52, 1
	s_and_b32 s54, s52, 7
	s_cmp_eq_u32 s54, 0
	s_cselect_b32 s54, s53, s32
	s_cselect_b32 s55, -1, 0
	s_add_u32 s30, s30, s54
	s_addc_u32 s31, s31, s55
	s_mov_b32 m0, s49
	s_nop 0
	global_load_lds_dwordx4 v88, s[30:31]
	s_add_i32 m0, s49, 0x2000
	s_nop 0
	global_load_lds_dwordx4 v90, s[30:31]
	s_add_i32 m0, s49, 0x4000
	s_nop 0
	global_load_lds_dwordx4 v92, s[30:31]
	s_add_i32 m0, s49, 0x6000
	s_nop 0
	global_load_lds_dwordx4 v94, s[30:31]
	s_add_i32 m0, s49, 0x8000
	s_nop 0
	global_load_lds_dwordx4 v96, s[30:31]
	s_waitcnt vmcnt(29)
	v_cvt_pk_bf16_f32 v172, v114, v116
	v_cvt_pk_bf16_f32 v173, v118, v120
	v_cvt_pk_bf16_f32 v174, v122, v124
	v_cvt_pk_bf16_f32 v175, v126, v128
	v_cvt_pk_bf16_f32 v176, v115, v117
	v_cvt_pk_bf16_f32 v177, v119, v121
	v_cvt_pk_bf16_f32 v178, v123, v125
	v_cvt_pk_bf16_f32 v179, v127, v129
	ds_write_b128 v95, v[172:175] offset:19456
	ds_write_b128 v95, v[176:179] offset:19584
	v_add_u32_e32 v91, s46, v135
	v_add_u32_e32 v93, s46, v137
	ds_read_b128 v[238:241], v139 offset:0
	ds_read_b128 v[242:245], v139 offset:2048
	ds_read_b128 v[246:249], v139 offset:4096
	ds_read_b128 v[250:253], v139 offset:6144
	ds_read_b128 v[218:221], v91 offset:0
	ds_read_b128 v[222:225], v91 offset:2048
	ds_read_b128 v[226:229], v91 offset:4096
	ds_read_b128 v[230:233], v91 offset:6144
	ds_read_b128 v[234:237], v91 offset:8192
	s_waitcnt lgkmcnt(0)
	v_mfma_f32_16x16x32_bf16 v[78:81], v[238:241], v[218:221], v[78:81]
	v_mfma_f32_16x16x32_bf16 v[74:77], v[242:245], v[218:221], v[74:77]
	v_mfma_f32_16x16x32_bf16 v[70:73], v[246:249], v[218:221], v[70:73]
	v_mfma_f32_16x16x32_bf16 v[66:69], v[250:253], v[218:221], v[66:69]
	ds_read_b128 v[218:221], v93 offset:0
	ds_read_b128 v[142:145], v141 offset:0
	s_add_i32 s51, s51, 1
	s_and_b32 s54, s51, 7
	s_cmp_eq_u32 s54, 0
	s_cselect_b32 s44, s34, s35
	s_cselect_b32 s45, -1, 0
	v_lshl_add_u64 v[132:133], v[132:133], 0, s[44:45]
	global_load_dwordx2 v[114:115], v[132:133], off
	v_lshl_add_u64 v[180:181], v[132:133], 0, s[24:25]
	global_load_dwordx2 v[116:117], v[180:181], off
	v_mfma_f32_16x16x32_bf16 v[62:65], v[238:241], v[222:225], v[62:65]
	v_mfma_f32_16x16x32_bf16 v[58:61], v[242:245], v[222:225], v[58:61]
	v_mfma_f32_16x16x32_bf16 v[54:57], v[246:249], v[222:225], v[54:57]
	v_mfma_f32_16x16x32_bf16 v[50:53], v[250:253], v[222:225], v[50:53]
	ds_read_b128 v[222:225], v93 offset:2048
	ds_read_b128 v[146:149], v141 offset:2048
	v_lshl_add_u64 v[180:181], v[132:133], 0, s[26:27]
	global_load_dwordx2 v[118:119], v[180:181], off
	v_lshl_add_u64 v[180:181], v[132:133], 0, s[28:29]
	global_load_dwordx2 v[120:121], v[180:181], off
	v_mfma_f32_16x16x32_bf16 v[46:49], v[238:241], v[226:229], v[46:49]
	v_mfma_f32_16x16x32_bf16 v[42:45], v[242:245], v[226:229], v[42:45]
	v_mfma_f32_16x16x32_bf16 v[38:41], v[246:249], v[226:229], v[38:41]
	v_mfma_f32_16x16x32_bf16 v[34:37], v[250:253], v[226:229], v[34:37]
	ds_read_b128 v[226:229], v93 offset:4096
	ds_read_b128 v[156:159], v141 offset:4096
	v_lshl_add_u64 v[180:181], v[132:133], 0, s[36:37]
	global_load_dwordx2 v[122:123], v[180:181], off
	v_lshl_add_u64 v[180:181], v[132:133], 0, s[38:39]
	global_load_dwordx2 v[124:125], v[180:181], off
	v_mfma_f32_16x16x32_bf16 v[18:21], v[238:241], v[230:233], v[18:21]
	v_mfma_f32_16x16x32_bf16 v[22:25], v[242:245], v[230:233], v[22:25]
	v_mfma_f32_16x16x32_bf16 v[26:29], v[246:249], v[230:233], v[26:29]
	v_mfma_f32_16x16x32_bf16 v[30:33], v[250:253], v[230:233], v[30:33]
	ds_read_b128 v[230:233], v93 offset:6144
	ds_read_b128 v[160:163], v141 offset:6144
	v_lshl_add_u64 v[180:181], v[132:133], 0, s[40:41]
	global_load_dwordx2 v[126:127], v[180:181], off
	v_lshl_add_u64 v[180:181], v[132:133], 0, s[42:43]
	global_load_dwordx2 v[128:129], v[180:181], off
	v_mfma_f32_16x16x32_bf16 v[2:5], v[238:241], v[234:237], v[2:5]
	v_mfma_f32_16x16x32_bf16 v[6:9], v[242:245], v[234:237], v[6:9]
	v_mfma_f32_16x16x32_bf16 v[10:13], v[246:249], v[234:237], v[10:13]
	v_mfma_f32_16x16x32_bf16 v[14:17], v[250:253], v[234:237], v[14:17]
	ds_read_b128 v[234:237], v93 offset:8192
	s_waitcnt lgkmcnt(0)
	s_barrier
	s_mov_b32 s49, s46
	s_mov_b32 s46, s47
	s_mov_b32 s47, s48
	s_mov_b32 s48, s49
	s_add_i32 s49, s48, s74
	s_add_i32 s52, s52, 1
	s_and_b32 s54, s52, 7
	s_cmp_eq_u32 s54, 0
	s_cselect_b32 s54, s53, s32
	s_cselect_b32 s55, -1, 0
	s_add_u32 s30, s30, s54
	s_addc_u32 s31, s31, s55
	v_mfma_f32_16x16x32_bf16 v[78:81], v[142:145], v[218:221], v[78:81]
	v_mfma_f32_16x16x32_bf16 v[74:77], v[146:149], v[218:221], v[74:77]
	v_mfma_f32_16x16x32_bf16 v[70:73], v[156:159], v[218:221], v[70:73]
	v_mfma_f32_16x16x32_bf16 v[66:69], v[160:163], v[218:221], v[66:69]
	s_mov_b32 m0, s49
	s_nop 0
	global_load_lds_dwordx4 v88, s[30:31]
	v_mfma_f32_16x16x32_bf16 v[62:65], v[142:145], v[222:225], v[62:65]
	v_mfma_f32_16x16x32_bf16 v[58:61], v[146:149], v[222:225], v[58:61]
	v_mfma_f32_16x16x32_bf16 v[54:57], v[156:159], v[222:225], v[54:57]
	v_mfma_f32_16x16x32_bf16 v[50:53], v[160:163], v[222:225], v[50:53]
	s_add_i32 m0, s49, 0x2000
	s_nop 0
	global_load_lds_dwordx4 v90, s[30:31]
	v_mfma_f32_16x16x32_bf16 v[46:49], v[142:145], v[226:229], v[46:49]
	v_mfma_f32_16x16x32_bf16 v[42:45], v[146:149], v[226:229], v[42:45]
	v_mfma_f32_16x16x32_bf16 v[38:41], v[156:159], v[226:229], v[38:41]
	v_mfma_f32_16x16x32_bf16 v[34:37], v[160:163], v[226:229], v[34:37]
	s_add_i32 m0, s49, 0x4000
	s_nop 0
	global_load_lds_dwordx4 v92, s[30:31]
	v_mfma_f32_16x16x32_bf16 v[18:21], v[142:145], v[230:233], v[18:21]
	v_mfma_f32_16x16x32_bf16 v[22:25], v[146:149], v[230:233], v[22:25]
	v_mfma_f32_16x16x32_bf16 v[26:29], v[156:159], v[230:233], v[26:29]
	v_mfma_f32_16x16x32_bf16 v[30:33], v[160:163], v[230:233], v[30:33]
	s_add_i32 m0, s49, 0x6000
	s_nop 0
	global_load_lds_dwordx4 v94, s[30:31]
	v_mfma_f32_16x16x32_bf16 v[2:5], v[142:145], v[234:237], v[2:5]
	v_mfma_f32_16x16x32_bf16 v[6:9], v[146:149], v[234:237], v[6:9]
	v_mfma_f32_16x16x32_bf16 v[10:13], v[156:159], v[234:237], v[10:13]
	v_mfma_f32_16x16x32_bf16 v[14:17], v[160:163], v[234:237], v[14:17]
	s_add_i32 m0, s49, 0x8000
	s_nop 0
	global_load_lds_dwordx4 v96, s[30:31]
	s_waitcnt vmcnt(34)
; #define MD_GLDS_A(buf, tau) do { _Pragma("unroll") for (int i = 0; i < 5; ++i) if (amask & (1u << i)) \
;         __builtin_amdgcn_global_load_lds((const unsigned*)((const char*)HIDp + aoff[i] + (size_t)((tau) & 7) * 128), (PG8_LAS unsigned*)(MD_SA(buf) + wid * 1024 + i * 8192), 16, 0, 0); } while (0)
; #define MD_B_ISSUE(sb, tau) do { const char* kb_ = Bb + (size_t)((tau) >> 3) * 512 + (size_t)((tau) & 7) * (64 * (size_t)RB); _Pragma("unroll") for (int j = 0; j < 8; ++j) { const char* p_ = kb_ + (size_t)j * RB; \
;         asm volatile("global_load_dwordx2 %0, %1, off" : "=&v"(sb[j]) : "v"(p_) : "memory"); } } while (0)
; #define MD_B_WAIT(sb, N) asm volatile("s_waitcnt vmcnt(%8)" : "+v"(sb[0]), "+v"(sb[1]), "+v"(sb[2]), "+v"(sb[3]), "+v"(sb[4]), "+v"(sb[5]), "+v"(sb[6]), "+v"(sb[7]) : "n"(N) : "memory")
; #define MD_END(last) do { if (last) asm volatile("s_waitcnt vmcnt(0)" ::: "memory"); else asm volatile("s_waitcnt vmcnt(8)" ::: "memory"); \
;         asm volatile("s_waitcnt lgkmcnt(0)" ::: "memory"); __builtin_amdgcn_s_barrier(); asm volatile("" ::: "memory"); } while (0)
; __device__ __forceinline__ void moe_down_stream(PG8_LAS unsigned char* lds, int e, int cb0, int slot0, int nv, const bf16_t* HIDp, const float* Wd, bf16_t* Y, const float* slot_w, const int* slot_dst) {
;     ...
;     for (int t = 0; t < NT; t += 2) {
;         if (t + 2 < NT) MD_B_WAIT(s1, 8); else MD_B_WAIT(s1, 0);
;         MD_B_WRITE(s1, 1); __builtin_amdgcn_sched_barrier(0); MD_GLDS_A(1, t + 1); __builtin_amdgcn_sched_barrier(0);
;         if (t + 3 < NT) MD_B_ISSUE(s1, t + 3);
;         MD_COMPUTE(0);
;         MD_END(t + 3 >= NT);
;         if (t + 2 < NT) { MD_B_WAIT(s0, 8); MD_B_WRITE(s0, 0); __builtin_amdgcn_sched_barrier(0); MD_GLDS_A(0, t + 2); __builtin_amdgcn_sched_barrier(0); }
;         if (t + 4 < NT) MD_B_ISSUE(s0, t + 4);
;         MD_COMPUTE(1);
;         MD_END(t + 4 >= NT);
	v_cvt_pk_bf16_f32 v172, v186, v188
	v_cvt_pk_bf16_f32 v173, v190, v192
	v_cvt_pk_bf16_f32 v174, v194, v196
	v_cvt_pk_bf16_f32 v175, v198, v200
	v_cvt_pk_bf16_f32 v176, v187, v189
	v_cvt_pk_bf16_f32 v177, v191, v193
	v_cvt_pk_bf16_f32 v178, v195, v197
	v_cvt_pk_bf16_f32 v179, v199, v201
	ds_write_b128 v95, v[172:175] offset:0
	ds_write_b128 v95, v[176:179] offset:128
	v_add_u32_e32 v91, s46, v135
	v_add_u32_e32 v93, s46, v137
	ds_read_b128 v[238:241], v139 offset:19456
	ds_read_b128 v[242:245], v139 offset:21504
	ds_read_b128 v[246:249], v139 offset:23552
	ds_read_b128 v[250:253], v139 offset:25600
	ds_read_b128 v[218:221], v91 offset:0
	ds_read_b128 v[222:225], v91 offset:2048
	ds_read_b128 v[226:229], v91 offset:4096
	ds_read_b128 v[230:233], v91 offset:6144
	ds_read_b128 v[234:237], v91 offset:8192
	s_waitcnt lgkmcnt(0)
	v_mfma_f32_16x16x32_bf16 v[78:81], v[238:241], v[218:221], v[78:81]
	v_mfma_f32_16x16x32_bf16 v[74:77], v[242:245], v[218:221], v[74:77]
	v_mfma_f32_16x16x32_bf16 v[70:73], v[246:249], v[218:221], v[70:73]
	v_mfma_f32_16x16x32_bf16 v[66:69], v[250:253], v[218:221], v[66:69]
	ds_read_b128 v[218:221], v93 offset:0
	ds_read_b128 v[142:145], v141 offset:19456
	s_add_i32 s51, s51, 1
	s_and_b32 s54, s51, 7
	s_cmp_eq_u32 s54, 0
	s_cselect_b32 s44, s34, s35
	s_cselect_b32 s45, -1, 0
	v_lshl_add_u64 v[132:133], v[132:133], 0, s[44:45]
	global_load_dwordx2 v[186:187], v[132:133], off
	v_lshl_add_u64 v[180:181], v[132:133], 0, s[24:25]
	global_load_dwordx2 v[188:189], v[180:181], off
	v_mfma_f32_16x16x32_bf16 v[62:65], v[238:241], v[222:225], v[62:65]
	v_mfma_f32_16x16x32_bf16 v[58:61], v[242:245], v[222:225], v[58:61]
	v_mfma_f32_16x16x32_bf16 v[54:57], v[246:249], v[222:225], v[54:57]
	v_mfma_f32_16x16x32_bf16 v[50:53], v[250:253], v[222:225], v[50:53]
	ds_read_b128 v[222:225], v93 offset:2048
	ds_read_b128 v[146:149], v141 offset:21504
	v_lshl_add_u64 v[180:181], v[132:133], 0, s[26:27]
	global_load_dwordx2 v[190:191], v[180:181], off
	v_lshl_add_u64 v[180:181], v[132:133], 0, s[28:29]
	global_load_dwordx2 v[192:193], v[180:181], off
	v_mfma_f32_16x16x32_bf16 v[46:49], v[238:241], v[226:229], v[46:49]
	v_mfma_f32_16x16x32_bf16 v[42:45], v[242:245], v[226:229], v[42:45]
	v_mfma_f32_16x16x32_bf16 v[38:41], v[246:249], v[226:229], v[38:41]
	v_mfma_f32_16x16x32_bf16 v[34:37], v[250:253], v[226:229], v[34:37]
	ds_read_b128 v[226:229], v93 offset:4096
	ds_read_b128 v[156:159], v141 offset:23552
	v_lshl_add_u64 v[180:181], v[132:133], 0, s[36:37]
	global_load_dwordx2 v[194:195], v[180:181], off
	v_lshl_add_u64 v[180:181], v[132:133], 0, s[38:39]
	global_load_dwordx2 v[196:197], v[180:181], off
	v_mfma_f32_16x16x32_bf16 v[18:21], v[238:241], v[230:233], v[18:21]
	v_mfma_f32_16x16x32_bf16 v[22:25], v[242:245], v[230:233], v[22:25]
	v_mfma_f32_16x16x32_bf16 v[26:29], v[246:249], v[230:233], v[26:29]
	v_mfma_f32_16x16x32_bf16 v[30:33], v[250:253], v[230:233], v[30:33]
	ds_read_b128 v[230:233], v93 offset:6144
	ds_read_b128 v[160:163], v141 offset:25600
	v_lshl_add_u64 v[180:181], v[132:133], 0, s[40:41]
	global_load_dwordx2 v[198:199], v[180:181], off
	v_lshl_add_u64 v[180:181], v[132:133], 0, s[42:43]
	global_load_dwordx2 v[200:201], v[180:181], off
	v_mfma_f32_16x16x32_bf16 v[2:5], v[238:241], v[234:237], v[2:5]
	v_mfma_f32_16x16x32_bf16 v[6:9], v[242:245], v[234:237], v[6:9]
	v_mfma_f32_16x16x32_bf16 v[10:13], v[246:249], v[234:237], v[10:13]
	v_mfma_f32_16x16x32_bf16 v[14:17], v[250:253], v[234:237], v[14:17]
	ds_read_b128 v[234:237], v93 offset:8192
	s_waitcnt vmcnt(21)
	s_waitcnt lgkmcnt(0)
	s_barrier
	s_mov_b32 s49, s46
	s_mov_b32 s46, s47
	s_mov_b32 s47, s48
	s_mov_b32 s48, s49
	s_add_i32 s49, s48, s74
	s_add_i32 s52, s52, 1
	s_and_b32 s54, s52, 7
	s_cmp_eq_u32 s54, 0
	s_cselect_b32 s54, s53, s32
	s_cselect_b32 s55, -1, 0
	s_add_u32 s30, s30, s54
	s_addc_u32 s31, s31, s55
	v_mfma_f32_16x16x32_bf16 v[78:81], v[142:145], v[218:221], v[78:81]
	v_mfma_f32_16x16x32_bf16 v[74:77], v[146:149], v[218:221], v[74:77]
	v_mfma_f32_16x16x32_bf16 v[70:73], v[156:159], v[218:221], v[70:73]
	v_mfma_f32_16x16x32_bf16 v[66:69], v[160:163], v[218:221], v[66:69]
	s_mov_b32 m0, s49
	s_nop 0
	global_load_lds_dwordx4 v88, s[30:31]
	v_mfma_f32_16x16x32_bf16 v[62:65], v[142:145], v[222:225], v[62:65]
	v_mfma_f32_16x16x32_bf16 v[58:61], v[146:149], v[222:225], v[58:61]
	v_mfma_f32_16x16x32_bf16 v[54:57], v[156:159], v[222:225], v[54:57]
	v_mfma_f32_16x16x32_bf16 v[50:53], v[160:163], v[222:225], v[50:53]
	s_add_i32 m0, s49, 0x2000
	s_nop 0
	global_load_lds_dwordx4 v90, s[30:31]
	v_mfma_f32_16x16x32_bf16 v[46:49], v[142:145], v[226:229], v[46:49]
	v_mfma_f32_16x16x32_bf16 v[42:45], v[146:149], v[226:229], v[42:45]
	v_mfma_f32_16x16x32_bf16 v[38:41], v[156:159], v[226:229], v[38:41]
	v_mfma_f32_16x16x32_bf16 v[34:37], v[160:163], v[226:229], v[34:37]
	s_add_i32 m0, s49, 0x4000
	s_nop 0
	global_load_lds_dwordx4 v92, s[30:31]
	v_mfma_f32_16x16x32_bf16 v[18:21], v[142:145], v[230:233], v[18:21]
	v_mfma_f32_16x16x32_bf16 v[22:25], v[146:149], v[230:233], v[22:25]
	v_mfma_f32_16x16x32_bf16 v[26:29], v[156:159], v[230:233], v[26:29]
	v_mfma_f32_16x16x32_bf16 v[30:33], v[160:163], v[230:233], v[30:33]
	s_add_i32 m0, s49, 0x6000
	s_nop 0
	global_load_lds_dwordx4 v94, s[30:31]
	v_mfma_f32_16x16x32_bf16 v[2:5], v[142:145], v[234:237], v[2:5]
	v_mfma_f32_16x16x32_bf16 v[6:9], v[146:149], v[234:237], v[6:9]
	v_mfma_f32_16x16x32_bf16 v[10:13], v[156:159], v[234:237], v[10:13]
	v_mfma_f32_16x16x32_bf16 v[14:17], v[160:163], v[234:237], v[14:17]
	s_add_i32 m0, s49, 0x8000
	s_nop 0
	global_load_lds_dwordx4 v96, s[30:31]
	v_cvt_pk_bf16_f32 v172, v202, v204
	v_cvt_pk_bf16_f32 v173, v206, v208
	v_cvt_pk_bf16_f32 v174, v210, v212
	v_cvt_pk_bf16_f32 v175, v214, v216
	v_cvt_pk_bf16_f32 v176, v203, v205
	v_cvt_pk_bf16_f32 v177, v207, v209
	v_cvt_pk_bf16_f32 v178, v211, v213
	v_cvt_pk_bf16_f32 v179, v215, v217
	ds_write_b128 v95, v[172:175] offset:19456
	ds_write_b128 v95, v[176:179] offset:19584
	v_add_u32_e32 v91, s46, v135
	v_add_u32_e32 v93, s46, v137
	ds_read_b128 v[238:241], v139 offset:0
	ds_read_b128 v[242:245], v139 offset:2048
	ds_read_b128 v[246:249], v139 offset:4096
	ds_read_b128 v[250:253], v139 offset:6144
	ds_read_b128 v[218:221], v91 offset:0
	ds_read_b128 v[222:225], v91 offset:2048
	ds_read_b128 v[226:229], v91 offset:4096
	ds_read_b128 v[230:233], v91 offset:6144
	ds_read_b128 v[234:237], v91 offset:8192
	s_waitcnt lgkmcnt(0)
; #define MD_GLDS_A(buf, tau) do { _Pragma("unroll") for (int i = 0; i < 5; ++i) if (amask & (1u << i)) \
;         __builtin_amdgcn_global_load_lds((const unsigned*)((const char*)HIDp + aoff[i] + (size_t)((tau) & 7) * 128), (PG8_LAS unsigned*)(MD_SA(buf) + wid * 1024 + i * 8192), 16, 0, 0); } while (0)
; #define MD_B_ISSUE(sb, tau) do { const char* kb_ = Bb + (size_t)((tau) >> 3) * 512 + (size_t)((tau) & 7) * (64 * (size_t)RB); _Pragma("unroll") for (int j = 0; j < 8; ++j) { const char* p_ = kb_ + (size_t)j * RB; \
;         asm volatile("global_load_dwordx2 %0, %1, off" : "=&v"(sb[j]) : "v"(p_) : "memory"); } } while (0)
; #define MD_B_WAIT(sb, N) asm volatile("s_waitcnt vmcnt(%8)" : "+v"(sb[0]), "+v"(sb[1]), "+v"(sb[2]), "+v"(sb[3]), "+v"(sb[4]), "+v"(sb[5]), "+v"(sb[6]), "+v"(sb[7]) : "n"(N) : "memory")
; #define MD_END(last) do { if (last) asm volatile("s_waitcnt vmcnt(0)" ::: "memory"); else asm volatile("s_waitcnt vmcnt(8)" ::: "memory"); \
;         asm volatile("s_waitcnt lgkmcnt(0)" ::: "memory"); __builtin_amdgcn_s_barrier(); asm volatile("" ::: "memory"); } while (0)
; __device__ __forceinline__ void moe_down_stream(PG8_LAS unsigned char* lds, int e, int cb0, int slot0, int nv, const bf16_t* HIDp, const float* Wd, bf16_t* Y, const float* slot_w, const int* slot_dst) {
;     ...
;     for (int t = 0; t < NT; t += 2) {
;         if (t + 2 < NT) MD_B_WAIT(s1, 8); else MD_B_WAIT(s1, 0);
;         MD_B_WRITE(s1, 1); __builtin_amdgcn_sched_barrier(0); MD_GLDS_A(1, t + 1); __builtin_amdgcn_sched_barrier(0);
;         if (t + 3 < NT) MD_B_ISSUE(s1, t + 3);
;         MD_COMPUTE(0);
;         MD_END(t + 3 >= NT);
;         if (t + 2 < NT) { MD_B_WAIT(s0, 8); MD_B_WRITE(s0, 0); __builtin_amdgcn_sched_barrier(0); MD_GLDS_A(0, t + 2); __builtin_amdgcn_sched_barrier(0); }
;         if (t + 4 < NT) MD_B_ISSUE(s0, t + 4);
;         MD_COMPUTE(1);
;         MD_END(t + 4 >= NT);
	v_mfma_f32_16x16x32_bf16 v[78:81], v[238:241], v[218:221], v[78:81]
	v_mfma_f32_16x16x32_bf16 v[74:77], v[242:245], v[218:221], v[74:77]
	v_mfma_f32_16x16x32_bf16 v[70:73], v[246:249], v[218:221], v[70:73]
	v_mfma_f32_16x16x32_bf16 v[66:69], v[250:253], v[218:221], v[66:69]
	ds_read_b128 v[218:221], v93 offset:0
	ds_read_b128 v[142:145], v141 offset:0
	s_add_i32 s51, s51, 1
	s_and_b32 s54, s51, 7
	s_cmp_eq_u32 s54, 0
	s_cselect_b32 s44, s34, s35
	s_cselect_b32 s45, -1, 0
	v_lshl_add_u64 v[132:133], v[132:133], 0, s[44:45]
	global_load_dwordx2 v[202:203], v[132:133], off
	v_lshl_add_u64 v[180:181], v[132:133], 0, s[24:25]
	global_load_dwordx2 v[204:205], v[180:181], off
	v_mfma_f32_16x16x32_bf16 v[62:65], v[238:241], v[222:225], v[62:65]
	v_mfma_f32_16x16x32_bf16 v[58:61], v[242:245], v[222:225], v[58:61]
	v_mfma_f32_16x16x32_bf16 v[54:57], v[246:249], v[222:225], v[54:57]
	v_mfma_f32_16x16x32_bf16 v[50:53], v[250:253], v[222:225], v[50:53]
	ds_read_b128 v[222:225], v93 offset:2048
	ds_read_b128 v[146:149], v141 offset:2048
	v_lshl_add_u64 v[180:181], v[132:133], 0, s[26:27]
	global_load_dwordx2 v[206:207], v[180:181], off
	v_lshl_add_u64 v[180:181], v[132:133], 0, s[28:29]
	global_load_dwordx2 v[208:209], v[180:181], off
	v_mfma_f32_16x16x32_bf16 v[46:49], v[238:241], v[226:229], v[46:49]
	v_mfma_f32_16x16x32_bf16 v[42:45], v[242:245], v[226:229], v[42:45]
	v_mfma_f32_16x16x32_bf16 v[38:41], v[246:249], v[226:229], v[38:41]
	v_mfma_f32_16x16x32_bf16 v[34:37], v[250:253], v[226:229], v[34:37]
	ds_read_b128 v[226:229], v93 offset:4096
	ds_read_b128 v[156:159], v141 offset:4096
	v_lshl_add_u64 v[180:181], v[132:133], 0, s[36:37]
	global_load_dwordx2 v[210:211], v[180:181], off
	v_lshl_add_u64 v[180:181], v[132:133], 0, s[38:39]
	global_load_dwordx2 v[212:213], v[180:181], off
	v_mfma_f32_16x16x32_bf16 v[18:21], v[238:241], v[230:233], v[18:21]
	v_mfma_f32_16x16x32_bf16 v[22:25], v[242:245], v[230:233], v[22:25]
	v_mfma_f32_16x16x32_bf16 v[26:29], v[246:249], v[230:233], v[26:29]
	v_mfma_f32_16x16x32_bf16 v[30:33], v[250:253], v[230:233], v[30:33]
	ds_read_b128 v[230:233], v93 offset:6144
	ds_read_b128 v[160:163], v141 offset:6144
	v_lshl_add_u64 v[180:181], v[132:133], 0, s[40:41]
	global_load_dwordx2 v[214:215], v[180:181], off
	v_lshl_add_u64 v[180:181], v[132:133], 0, s[42:43]
	global_load_dwordx2 v[216:217], v[180:181], off
	v_mfma_f32_16x16x32_bf16 v[2:5], v[238:241], v[234:237], v[2:5]
	v_mfma_f32_16x16x32_bf16 v[6:9], v[242:245], v[234:237], v[6:9]
	v_mfma_f32_16x16x32_bf16 v[10:13], v[246:249], v[234:237], v[10:13]
	v_mfma_f32_16x16x32_bf16 v[14:17], v[250:253], v[234:237], v[14:17]
	ds_read_b128 v[234:237], v93 offset:8192
	s_waitcnt vmcnt(21)
	s_waitcnt lgkmcnt(0)
	s_barrier
	s_mov_b32 s49, s46
	s_mov_b32 s46, s47
	s_mov_b32 s47, s48
	s_mov_b32 s48, s49
	s_add_i32 s49, s48, s74
	s_add_i32 s52, s52, 1
	s_and_b32 s54, s52, 7
	s_cmp_eq_u32 s54, 0
	s_cselect_b32 s54, s53, s32
	s_cselect_b32 s55, -1, 0
	s_add_u32 s30, s30, s54
	s_addc_u32 s31, s31, s55
	v_mfma_f32_16x16x32_bf16 v[78:81], v[142:145], v[218:221], v[78:81]
	v_mfma_f32_16x16x32_bf16 v[74:77], v[146:149], v[218:221], v[74:77]
	v_mfma_f32_16x16x32_bf16 v[70:73], v[156:159], v[218:221], v[70:73]
	v_mfma_f32_16x16x32_bf16 v[66:69], v[160:163], v[218:221], v[66:69]
	s_mov_b32 m0, s49
	s_nop 0
	global_load_lds_dwordx4 v88, s[30:31]
	v_mfma_f32_16x16x32_bf16 v[62:65], v[142:145], v[222:225], v[62:65]
	v_mfma_f32_16x16x32_bf16 v[58:61], v[146:149], v[222:225], v[58:61]
	v_mfma_f32_16x16x32_bf16 v[54:57], v[156:159], v[222:225], v[54:57]
	v_mfma_f32_16x16x32_bf16 v[50:53], v[160:163], v[222:225], v[50:53]
	s_add_i32 m0, s49, 0x2000
	s_nop 0
	global_load_lds_dwordx4 v90, s[30:31]
	v_mfma_f32_16x16x32_bf16 v[46:49], v[142:145], v[226:229], v[46:49]
	v_mfma_f32_16x16x32_bf16 v[42:45], v[146:149], v[226:229], v[42:45]
	v_mfma_f32_16x16x32_bf16 v[38:41], v[156:159], v[226:229], v[38:41]
	v_mfma_f32_16x16x32_bf16 v[34:37], v[160:163], v[226:229], v[34:37]
	s_add_i32 m0, s49, 0x4000
	s_nop 0
	global_load_lds_dwordx4 v92, s[30:31]
	v_mfma_f32_16x16x32_bf16 v[18:21], v[142:145], v[230:233], v[18:21]
	v_mfma_f32_16x16x32_bf16 v[22:25], v[146:149], v[230:233], v[22:25]
	v_mfma_f32_16x16x32_bf16 v[26:29], v[156:159], v[230:233], v[26:29]
	v_mfma_f32_16x16x32_bf16 v[30:33], v[160:163], v[230:233], v[30:33]
	s_add_i32 m0, s49, 0x6000
	s_nop 0
	global_load_lds_dwordx4 v94, s[30:31]
	v_mfma_f32_16x16x32_bf16 v[2:5], v[142:145], v[234:237], v[2:5]
	v_mfma_f32_16x16x32_bf16 v[6:9], v[146:149], v[234:237], v[6:9]
	v_mfma_f32_16x16x32_bf16 v[10:13], v[156:159], v[234:237], v[10:13]
	v_mfma_f32_16x16x32_bf16 v[14:17], v[160:163], v[234:237], v[14:17]
	s_add_i32 m0, s49, 0x8000
	s_nop 0
	global_load_lds_dwordx4 v96, s[30:31]
	v_cvt_pk_bf16_f32 v172, v98, v100
	v_cvt_pk_bf16_f32 v173, v102, v104
	v_cvt_pk_bf16_f32 v174, v106, v108
	v_cvt_pk_bf16_f32 v175, v110, v112
	v_cvt_pk_bf16_f32 v176, v99, v101
	v_cvt_pk_bf16_f32 v177, v103, v105
	v_cvt_pk_bf16_f32 v178, v107, v109
	v_cvt_pk_bf16_f32 v179, v111, v113
	ds_write_b128 v95, v[172:175] offset:0
	ds_write_b128 v95, v[176:179] offset:128
	v_add_u32_e32 v91, s46, v135
	v_add_u32_e32 v93, s46, v137
	ds_read_b128 v[238:241], v139 offset:19456
	ds_read_b128 v[242:245], v139 offset:21504
	ds_read_b128 v[246:249], v139 offset:23552
	ds_read_b128 v[250:253], v139 offset:25600
	ds_read_b128 v[218:221], v91 offset:0
	ds_read_b128 v[222:225], v91 offset:2048
	ds_read_b128 v[226:229], v91 offset:4096
	ds_read_b128 v[230:233], v91 offset:6144
	ds_read_b128 v[234:237], v91 offset:8192
	s_waitcnt lgkmcnt(0)
; #define MD_GLDS_A(buf, tau) do { _Pragma("unroll") for (int i = 0; i < 5; ++i) if (amask & (1u << i)) \
;         __builtin_amdgcn_global_load_lds((const unsigned*)((const char*)HIDp + aoff[i] + (size_t)((tau) & 7) * 128), (PG8_LAS unsigned*)(MD_SA(buf) + wid * 1024 + i * 8192), 16, 0, 0); } while (0)
; #define MD_B_ISSUE(sb, tau) do { const char* kb_ = Bb + (size_t)((tau) >> 3) * 512 + (size_t)((tau) & 7) * (64 * (size_t)RB); _Pragma("unroll") for (int j = 0; j < 8; ++j) { const char* p_ = kb_ + (size_t)j * RB; \
;         asm volatile("global_load_dwordx2 %0, %1, off" : "=&v"(sb[j]) : "v"(p_) : "memory"); } } while (0)
; #define MD_B_WAIT(sb, N) asm volatile("s_waitcnt vmcnt(%8)" : "+v"(sb[0]), "+v"(sb[1]), "+v"(sb[2]), "+v"(sb[3]), "+v"(sb[4]), "+v"(sb[5]), "+v"(sb[6]), "+v"(sb[7]) : "n"(N) : "memory")
; #define MD_END(last) do { if (last) asm volatile("s_waitcnt vmcnt(0)" ::: "memory"); else asm volatile("s_waitcnt vmcnt(8)" ::: "memory"); \
;         asm volatile("s_waitcnt lgkmcnt(0)" ::: "memory"); __builtin_amdgcn_s_barrier(); asm volatile("" ::: "memory"); } while (0)
; __device__ __forceinline__ void moe_down_stream(PG8_LAS unsigned char* lds, int e, int cb0, int slot0, int nv, const bf16_t* HIDp, const float* Wd, bf16_t* Y, const float* slot_w, const int* slot_dst) {
;     ...
;     for (int t = 0; t < NT; t += 2) {
;         if (t + 2 < NT) MD_B_WAIT(s1, 8); else MD_B_WAIT(s1, 0);
;         MD_B_WRITE(s1, 1); __builtin_amdgcn_sched_barrier(0); MD_GLDS_A(1, t + 1); __builtin_amdgcn_sched_barrier(0);
;         if (t + 3 < NT) MD_B_ISSUE(s1, t + 3);
;         MD_COMPUTE(0);
;         MD_END(t + 3 >= NT);
;         if (t + 2 < NT) { MD_B_WAIT(s0, 8); MD_B_WRITE(s0, 0); __builtin_amdgcn_sched_barrier(0); MD_GLDS_A(0, t + 2); __builtin_amdgcn_sched_barrier(0); }
;         if (t + 4 < NT) MD_B_ISSUE(s0, t + 4);
;         MD_COMPUTE(1);
;         MD_END(t + 4 >= NT);
	v_mfma_f32_16x16x32_bf16 v[78:81], v[238:241], v[218:221], v[78:81]
	v_mfma_f32_16x16x32_bf16 v[74:77], v[242:245], v[218:221], v[74:77]
	v_mfma_f32_16x16x32_bf16 v[70:73], v[246:249], v[218:221], v[70:73]
	v_mfma_f32_16x16x32_bf16 v[66:69], v[250:253], v[218:221], v[66:69]
	ds_read_b128 v[218:221], v93 offset:0
	ds_read_b128 v[142:145], v141 offset:19456
	s_add_i32 s51, s51, 1
	s_and_b32 s54, s51, 7
	s_cmp_eq_u32 s54, 0
	s_cselect_b32 s44, s34, s35
	s_cselect_b32 s45, -1, 0
	v_lshl_add_u64 v[132:133], v[132:133], 0, s[44:45]
	global_load_dwordx2 v[98:99], v[132:133], off
	v_lshl_add_u64 v[180:181], v[132:133], 0, s[24:25]
	global_load_dwordx2 v[100:101], v[180:181], off
	v_mfma_f32_16x16x32_bf16 v[62:65], v[238:241], v[222:225], v[62:65]
	v_mfma_f32_16x16x32_bf16 v[58:61], v[242:245], v[222:225], v[58:61]
	v_mfma_f32_16x16x32_bf16 v[54:57], v[246:249], v[222:225], v[54:57]
	v_mfma_f32_16x16x32_bf16 v[50:53], v[250:253], v[222:225], v[50:53]
	ds_read_b128 v[222:225], v93 offset:2048
	ds_read_b128 v[146:149], v141 offset:21504
	v_lshl_add_u64 v[180:181], v[132:133], 0, s[26:27]
	global_load_dwordx2 v[102:103], v[180:181], off
	v_lshl_add_u64 v[180:181], v[132:133], 0, s[28:29]
	global_load_dwordx2 v[104:105], v[180:181], off
	v_mfma_f32_16x16x32_bf16 v[46:49], v[238:241], v[226:229], v[46:49]
	v_mfma_f32_16x16x32_bf16 v[42:45], v[242:245], v[226:229], v[42:45]
	v_mfma_f32_16x16x32_bf16 v[38:41], v[246:249], v[226:229], v[38:41]
	v_mfma_f32_16x16x32_bf16 v[34:37], v[250:253], v[226:229], v[34:37]
	ds_read_b128 v[226:229], v93 offset:4096
	ds_read_b128 v[156:159], v141 offset:23552
	v_lshl_add_u64 v[180:181], v[132:133], 0, s[36:37]
	global_load_dwordx2 v[106:107], v[180:181], off
	v_lshl_add_u64 v[180:181], v[132:133], 0, s[38:39]
	global_load_dwordx2 v[108:109], v[180:181], off
	v_mfma_f32_16x16x32_bf16 v[18:21], v[238:241], v[230:233], v[18:21]
	v_mfma_f32_16x16x32_bf16 v[22:25], v[242:245], v[230:233], v[22:25]
	v_mfma_f32_16x16x32_bf16 v[26:29], v[246:249], v[230:233], v[26:29]
	v_mfma_f32_16x16x32_bf16 v[30:33], v[250:253], v[230:233], v[30:33]
	ds_read_b128 v[230:233], v93 offset:6144
	ds_read_b128 v[160:163], v141 offset:25600
	v_lshl_add_u64 v[180:181], v[132:133], 0, s[40:41]
	global_load_dwordx2 v[110:111], v[180:181], off
	v_lshl_add_u64 v[180:181], v[132:133], 0, s[42:43]
	global_load_dwordx2 v[112:113], v[180:181], off
	v_mfma_f32_16x16x32_bf16 v[2:5], v[238:241], v[234:237], v[2:5]
	v_mfma_f32_16x16x32_bf16 v[6:9], v[242:245], v[234:237], v[6:9]
	v_mfma_f32_16x16x32_bf16 v[10:13], v[246:249], v[234:237], v[10:13]
	v_mfma_f32_16x16x32_bf16 v[14:17], v[250:253], v[234:237], v[14:17]
	ds_read_b128 v[234:237], v93 offset:8192
	s_waitcnt vmcnt(21)
	s_waitcnt lgkmcnt(0)
	s_barrier
	s_mov_b32 s49, s46
	s_mov_b32 s46, s47
	s_mov_b32 s47, s48
	s_mov_b32 s48, s49
	s_add_i32 s49, s48, s74
	s_add_i32 s52, s52, 1
	s_and_b32 s54, s52, 7
	s_cmp_eq_u32 s54, 0
	s_cselect_b32 s54, s53, s32
	s_cselect_b32 s55, -1, 0
	s_add_u32 s30, s30, s54
	s_addc_u32 s31, s31, s55
	v_mfma_f32_16x16x32_bf16 v[78:81], v[142:145], v[218:221], v[78:81]
	v_mfma_f32_16x16x32_bf16 v[74:77], v[146:149], v[218:221], v[74:77]
	v_mfma_f32_16x16x32_bf16 v[70:73], v[156:159], v[218:221], v[70:73]
	v_mfma_f32_16x16x32_bf16 v[66:69], v[160:163], v[218:221], v[66:69]
	s_mov_b32 m0, s49
	s_nop 0
	global_load_lds_dwordx4 v88, s[30:31]
	v_mfma_f32_16x16x32_bf16 v[62:65], v[142:145], v[222:225], v[62:65]
	v_mfma_f32_16x16x32_bf16 v[58:61], v[146:149], v[222:225], v[58:61]
	v_mfma_f32_16x16x32_bf16 v[54:57], v[156:159], v[222:225], v[54:57]
	v_mfma_f32_16x16x32_bf16 v[50:53], v[160:163], v[222:225], v[50:53]
	s_add_i32 m0, s49, 0x2000
	s_nop 0
	global_load_lds_dwordx4 v90, s[30:31]
	v_mfma_f32_16x16x32_bf16 v[46:49], v[142:145], v[226:229], v[46:49]
	v_mfma_f32_16x16x32_bf16 v[42:45], v[146:149], v[226:229], v[42:45]
	v_mfma_f32_16x16x32_bf16 v[38:41], v[156:159], v[226:229], v[38:41]
	v_mfma_f32_16x16x32_bf16 v[34:37], v[160:163], v[226:229], v[34:37]
	s_add_i32 m0, s49, 0x4000
	s_nop 0
	global_load_lds_dwordx4 v92, s[30:31]
	v_mfma_f32_16x16x32_bf16 v[18:21], v[142:145], v[230:233], v[18:21]
	v_mfma_f32_16x16x32_bf16 v[22:25], v[146:149], v[230:233], v[22:25]
	v_mfma_f32_16x16x32_bf16 v[26:29], v[156:159], v[230:233], v[26:29]
	v_mfma_f32_16x16x32_bf16 v[30:33], v[160:163], v[230:233], v[30:33]
	s_add_i32 m0, s49, 0x6000
	s_nop 0
	global_load_lds_dwordx4 v94, s[30:31]
	v_mfma_f32_16x16x32_bf16 v[2:5], v[142:145], v[234:237], v[2:5]
	v_mfma_f32_16x16x32_bf16 v[6:9], v[146:149], v[234:237], v[6:9]
	v_mfma_f32_16x16x32_bf16 v[10:13], v[156:159], v[234:237], v[10:13]
	v_mfma_f32_16x16x32_bf16 v[14:17], v[160:163], v[234:237], v[14:17]
	s_add_i32 m0, s49, 0x8000
	s_nop 0
	global_load_lds_dwordx4 v96, s[30:31]
	v_cvt_pk_bf16_f32 v172, v114, v116
	v_cvt_pk_bf16_f32 v173, v118, v120
	v_cvt_pk_bf16_f32 v174, v122, v124
	v_cvt_pk_bf16_f32 v175, v126, v128
	v_cvt_pk_bf16_f32 v176, v115, v117
	v_cvt_pk_bf16_f32 v177, v119, v121
	v_cvt_pk_bf16_f32 v178, v123, v125
	v_cvt_pk_bf16_f32 v179, v127, v129
	ds_write_b128 v95, v[172:175] offset:19456
	ds_write_b128 v95, v[176:179] offset:19584
	v_add_u32_e32 v91, s46, v135
	v_add_u32_e32 v93, s46, v137
	ds_read_b128 v[238:241], v139 offset:0
	ds_read_b128 v[242:245], v139 offset:2048
	ds_read_b128 v[246:249], v139 offset:4096
	ds_read_b128 v[250:253], v139 offset:6144
	ds_read_b128 v[218:221], v91 offset:0
	ds_read_b128 v[222:225], v91 offset:2048
	ds_read_b128 v[226:229], v91 offset:4096
	ds_read_b128 v[230:233], v91 offset:6144
	ds_read_b128 v[234:237], v91 offset:8192
	s_waitcnt lgkmcnt(0)
; #define MD_GLDS_A(buf, tau) do { _Pragma("unroll") for (int i = 0; i < 5; ++i) if (amask & (1u << i)) \
;         __builtin_amdgcn_global_load_lds((const unsigned*)((const char*)HIDp + aoff[i] + (size_t)((tau) & 7) * 128), (PG8_LAS unsigned*)(MD_SA(buf) + wid * 1024 + i * 8192), 16, 0, 0); } while (0)
; #define MD_B_ISSUE(sb, tau) do { const char* kb_ = Bb + (size_t)((tau) >> 3) * 512 + (size_t)((tau) & 7) * (64 * (size_t)RB); _Pragma("unroll") for (int j = 0; j < 8; ++j) { const char* p_ = kb_ + (size_t)j * RB; \
;         asm volatile("global_load_dwordx2 %0, %1, off" : "=&v"(sb[j]) : "v"(p_) : "memory"); } } while (0)
; #define MD_B_WAIT(sb, N) asm volatile("s_waitcnt vmcnt(%8)" : "+v"(sb[0]), "+v"(sb[1]), "+v"(sb[2]), "+v"(sb[3]), "+v"(sb[4]), "+v"(sb[5]), "+v"(sb[6]), "+v"(sb[7]) : "n"(N) : "memory")
; #define MD_END(last) do { if (last) asm volatile("s_waitcnt vmcnt(0)" ::: "memory"); else asm volatile("s_waitcnt vmcnt(8)" ::: "memory"); \
;         asm volatile("s_waitcnt lgkmcnt(0)" ::: "memory"); __builtin_amdgcn_s_barrier(); asm volatile("" ::: "memory"); } while (0)
; __device__ __forceinline__ void moe_down_stream(PG8_LAS unsigned char* lds, int e, int cb0, int slot0, int nv, const bf16_t* HIDp, const float* Wd, bf16_t* Y, const float* slot_w, const int* slot_dst) {
;     ...
;     for (int t = 0; t < NT; t += 2) {
;         if (t + 2 < NT) MD_B_WAIT(s1, 8); else MD_B_WAIT(s1, 0);
;         MD_B_WRITE(s1, 1); __builtin_amdgcn_sched_barrier(0); MD_GLDS_A(1, t + 1); __builtin_amdgcn_sched_barrier(0);
;         if (t + 3 < NT) MD_B_ISSUE(s1, t + 3);
;         MD_COMPUTE(0);
;         MD_END(t + 3 >= NT);
;         if (t + 2 < NT) { MD_B_WAIT(s0, 8); MD_B_WRITE(s0, 0); __builtin_amdgcn_sched_barrier(0); MD_GLDS_A(0, t + 2); __builtin_amdgcn_sched_barrier(0); }
;         if (t + 4 < NT) MD_B_ISSUE(s0, t + 4);
;         MD_COMPUTE(1);
;         MD_END(t + 4 >= NT);
	v_mfma_f32_16x16x32_bf16 v[78:81], v[238:241], v[218:221], v[78:81]
	v_mfma_f32_16x16x32_bf16 v[74:77], v[242:245], v[218:221], v[74:77]
	v_mfma_f32_16x16x32_bf16 v[70:73], v[246:249], v[218:221], v[70:73]
	v_mfma_f32_16x16x32_bf16 v[66:69], v[250:253], v[218:221], v[66:69]
	ds_read_b128 v[218:221], v93 offset:0
	ds_read_b128 v[142:145], v141 offset:0
	s_add_i32 s51, s51, 1
	s_and_b32 s54, s51, 7
	s_cmp_eq_u32 s54, 0
	s_cselect_b32 s44, s34, s35
	s_cselect_b32 s45, -1, 0
	v_lshl_add_u64 v[132:133], v[132:133], 0, s[44:45]
	global_load_dwordx2 v[114:115], v[132:133], off
	v_lshl_add_u64 v[180:181], v[132:133], 0, s[24:25]
	global_load_dwordx2 v[116:117], v[180:181], off
	v_mfma_f32_16x16x32_bf16 v[62:65], v[238:241], v[222:225], v[62:65]
	v_mfma_f32_16x16x32_bf16 v[58:61], v[242:245], v[222:225], v[58:61]
	v_mfma_f32_16x16x32_bf16 v[54:57], v[246:249], v[222:225], v[54:57]
	v_mfma_f32_16x16x32_bf16 v[50:53], v[250:253], v[222:225], v[50:53]
	ds_read_b128 v[222:225], v93 offset:2048
	ds_read_b128 v[146:149], v141 offset:2048
	v_lshl_add_u64 v[180:181], v[132:133], 0, s[26:27]
	global_load_dwordx2 v[118:119], v[180:181], off
	v_lshl_add_u64 v[180:181], v[132:133], 0, s[28:29]
	global_load_dwordx2 v[120:121], v[180:181], off
	v_mfma_f32_16x16x32_bf16 v[46:49], v[238:241], v[226:229], v[46:49]
	v_mfma_f32_16x16x32_bf16 v[42:45], v[242:245], v[226:229], v[42:45]
	v_mfma_f32_16x16x32_bf16 v[38:41], v[246:249], v[226:229], v[38:41]
	v_mfma_f32_16x16x32_bf16 v[34:37], v[250:253], v[226:229], v[34:37]
	ds_read_b128 v[226:229], v93 offset:4096
	ds_read_b128 v[156:159], v141 offset:4096
	v_lshl_add_u64 v[180:181], v[132:133], 0, s[36:37]
	global_load_dwordx2 v[122:123], v[180:181], off
	v_lshl_add_u64 v[180:181], v[132:133], 0, s[38:39]
	global_load_dwordx2 v[124:125], v[180:181], off
	v_mfma_f32_16x16x32_bf16 v[18:21], v[238:241], v[230:233], v[18:21]
	v_mfma_f32_16x16x32_bf16 v[22:25], v[242:245], v[230:233], v[22:25]
	v_mfma_f32_16x16x32_bf16 v[26:29], v[246:249], v[230:233], v[26:29]
	v_mfma_f32_16x16x32_bf16 v[30:33], v[250:253], v[230:233], v[30:33]
	ds_read_b128 v[230:233], v93 offset:6144
	ds_read_b128 v[160:163], v141 offset:6144
	v_lshl_add_u64 v[180:181], v[132:133], 0, s[40:41]
	global_load_dwordx2 v[126:127], v[180:181], off
	v_lshl_add_u64 v[180:181], v[132:133], 0, s[42:43]
	global_load_dwordx2 v[128:129], v[180:181], off
	v_mfma_f32_16x16x32_bf16 v[2:5], v[238:241], v[234:237], v[2:5]
	v_mfma_f32_16x16x32_bf16 v[6:9], v[242:245], v[234:237], v[6:9]
	v_mfma_f32_16x16x32_bf16 v[10:13], v[246:249], v[234:237], v[10:13]
	v_mfma_f32_16x16x32_bf16 v[14:17], v[250:253], v[234:237], v[14:17]
	ds_read_b128 v[234:237], v93 offset:8192
	s_waitcnt vmcnt(21)
	s_waitcnt lgkmcnt(0)
	s_barrier
	s_mov_b32 s49, s46
	s_mov_b32 s46, s47
	s_mov_b32 s47, s48
	s_mov_b32 s48, s49
	s_add_i32 s49, s48, s74
	s_add_i32 s52, s52, 1
	s_and_b32 s54, s52, 7
	s_cmp_eq_u32 s54, 0
	s_cselect_b32 s54, s53, s32
	s_cselect_b32 s55, -1, 0
	s_add_u32 s30, s30, s54
	s_addc_u32 s31, s31, s55
	v_mfma_f32_16x16x32_bf16 v[78:81], v[142:145], v[218:221], v[78:81]
	v_mfma_f32_16x16x32_bf16 v[74:77], v[146:149], v[218:221], v[74:77]
	v_mfma_f32_16x16x32_bf16 v[70:73], v[156:159], v[218:221], v[70:73]
	v_mfma_f32_16x16x32_bf16 v[66:69], v[160:163], v[218:221], v[66:69]
	s_mov_b32 m0, s49
	s_nop 0
	global_load_lds_dwordx4 v88, s[30:31]
	v_mfma_f32_16x16x32_bf16 v[62:65], v[142:145], v[222:225], v[62:65]
	v_mfma_f32_16x16x32_bf16 v[58:61], v[146:149], v[222:225], v[58:61]
	v_mfma_f32_16x16x32_bf16 v[54:57], v[156:159], v[222:225], v[54:57]
	v_mfma_f32_16x16x32_bf16 v[50:53], v[160:163], v[222:225], v[50:53]
	s_add_i32 m0, s49, 0x2000
	s_nop 0
	global_load_lds_dwordx4 v90, s[30:31]
	v_mfma_f32_16x16x32_bf16 v[46:49], v[142:145], v[226:229], v[46:49]
	v_mfma_f32_16x16x32_bf16 v[42:45], v[146:149], v[226:229], v[42:45]
	v_mfma_f32_16x16x32_bf16 v[38:41], v[156:159], v[226:229], v[38:41]
	v_mfma_f32_16x16x32_bf16 v[34:37], v[160:163], v[226:229], v[34:37]
	s_add_i32 m0, s49, 0x4000
	s_nop 0
	global_load_lds_dwordx4 v92, s[30:31]
	v_mfma_f32_16x16x32_bf16 v[18:21], v[142:145], v[230:233], v[18:21]
	v_mfma_f32_16x16x32_bf16 v[22:25], v[146:149], v[230:233], v[22:25]
	v_mfma_f32_16x16x32_bf16 v[26:29], v[156:159], v[230:233], v[26:29]
	v_mfma_f32_16x16x32_bf16 v[30:33], v[160:163], v[230:233], v[30:33]
	s_add_i32 m0, s49, 0x6000
	s_nop 0
	global_load_lds_dwordx4 v94, s[30:31]
	v_mfma_f32_16x16x32_bf16 v[2:5], v[142:145], v[234:237], v[2:5]
	v_mfma_f32_16x16x32_bf16 v[6:9], v[146:149], v[234:237], v[6:9]
	v_mfma_f32_16x16x32_bf16 v[10:13], v[156:159], v[234:237], v[10:13]
	v_mfma_f32_16x16x32_bf16 v[14:17], v[160:163], v[234:237], v[14:17]
	s_add_i32 m0, s49, 0x8000
	s_nop 0
	global_load_lds_dwordx4 v96, s[30:31]
	v_cvt_pk_bf16_f32 v172, v186, v188
	v_cvt_pk_bf16_f32 v173, v190, v192
	v_cvt_pk_bf16_f32 v174, v194, v196
	v_cvt_pk_bf16_f32 v175, v198, v200
	v_cvt_pk_bf16_f32 v176, v187, v189
	v_cvt_pk_bf16_f32 v177, v191, v193
	v_cvt_pk_bf16_f32 v178, v195, v197
	v_cvt_pk_bf16_f32 v179, v199, v201
	ds_write_b128 v95, v[172:175] offset:0
	ds_write_b128 v95, v[176:179] offset:128
	v_add_u32_e32 v91, s46, v135
	v_add_u32_e32 v93, s46, v137
	ds_read_b128 v[238:241], v139 offset:19456
	ds_read_b128 v[242:245], v139 offset:21504
	ds_read_b128 v[246:249], v139 offset:23552
	ds_read_b128 v[250:253], v139 offset:25600
	ds_read_b128 v[218:221], v91 offset:0
	ds_read_b128 v[222:225], v91 offset:2048
	ds_read_b128 v[226:229], v91 offset:4096
	ds_read_b128 v[230:233], v91 offset:6144
	ds_read_b128 v[234:237], v91 offset:8192
	s_waitcnt lgkmcnt(0)
; #define MD_GLDS_A(buf, tau) do { _Pragma("unroll") for (int i = 0; i < 5; ++i) if (amask & (1u << i)) \
;         __builtin_amdgcn_global_load_lds((const unsigned*)((const char*)HIDp + aoff[i] + (size_t)((tau) & 7) * 128), (PG8_LAS unsigned*)(MD_SA(buf) + wid * 1024 + i * 8192), 16, 0, 0); } while (0)
; #define MD_B_ISSUE(sb, tau) do { const char* kb_ = Bb + (size_t)((tau) >> 3) * 512 + (size_t)((tau) & 7) * (64 * (size_t)RB); _Pragma("unroll") for (int j = 0; j < 8; ++j) { const char* p_ = kb_ + (size_t)j * RB; \
;         asm volatile("global_load_dwordx2 %0, %1, off" : "=&v"(sb[j]) : "v"(p_) : "memory"); } } while (0)
; #define MD_B_WAIT(sb, N) asm volatile("s_waitcnt vmcnt(%8)" : "+v"(sb[0]), "+v"(sb[1]), "+v"(sb[2]), "+v"(sb[3]), "+v"(sb[4]), "+v"(sb[5]), "+v"(sb[6]), "+v"(sb[7]) : "n"(N) : "memory")
; #define MD_END(last) do { if (last) asm volatile("s_waitcnt vmcnt(0)" ::: "memory"); else asm volatile("s_waitcnt vmcnt(8)" ::: "memory"); \
;         asm volatile("s_waitcnt lgkmcnt(0)" ::: "memory"); __builtin_amdgcn_s_barrier(); asm volatile("" ::: "memory"); } while (0)
; __device__ __forceinline__ void moe_down_stream(PG8_LAS unsigned char* lds, int e, int cb0, int slot0, int nv, const bf16_t* HIDp, const float* Wd, bf16_t* Y, const float* slot_w, const int* slot_dst) {
;     ...
;     for (int t = 0; t < NT; t += 2) {
;         if (t + 2 < NT) MD_B_WAIT(s1, 8); else MD_B_WAIT(s1, 0);
;         MD_B_WRITE(s1, 1); __builtin_amdgcn_sched_barrier(0); MD_GLDS_A(1, t + 1); __builtin_amdgcn_sched_barrier(0);
;         if (t + 3 < NT) MD_B_ISSUE(s1, t + 3);
;         MD_COMPUTE(0);
;         MD_END(t + 3 >= NT);
;         if (t + 2 < NT) { MD_B_WAIT(s0, 8); MD_B_WRITE(s0, 0); __builtin_amdgcn_sched_barrier(0); MD_GLDS_A(0, t + 2); __builtin_amdgcn_sched_barrier(0); }
;         if (t + 4 < NT) MD_B_ISSUE(s0, t + 4);
;         MD_COMPUTE(1);
;         MD_END(t + 4 >= NT);
	v_mfma_f32_16x16x32_bf16 v[78:81], v[238:241], v[218:221], v[78:81]
	v_mfma_f32_16x16x32_bf16 v[74:77], v[242:245], v[218:221], v[74:77]
	v_mfma_f32_16x16x32_bf16 v[70:73], v[246:249], v[218:221], v[70:73]
	v_mfma_f32_16x16x32_bf16 v[66:69], v[250:253], v[218:221], v[66:69]
	ds_read_b128 v[218:221], v93 offset:0
	ds_read_b128 v[142:145], v141 offset:19456
	s_add_i32 s51, s51, 1
	s_and_b32 s54, s51, 7
	s_cmp_eq_u32 s54, 0
	s_cselect_b32 s44, s34, s35
	s_cselect_b32 s45, -1, 0
	v_lshl_add_u64 v[132:133], v[132:133], 0, s[44:45]
	global_load_dwordx2 v[186:187], v[132:133], off
	v_lshl_add_u64 v[180:181], v[132:133], 0, s[24:25]
	global_load_dwordx2 v[188:189], v[180:181], off
	v_mfma_f32_16x16x32_bf16 v[62:65], v[238:241], v[222:225], v[62:65]
	v_mfma_f32_16x16x32_bf16 v[58:61], v[242:245], v[222:225], v[58:61]
	v_mfma_f32_16x16x32_bf16 v[54:57], v[246:249], v[222:225], v[54:57]
	v_mfma_f32_16x16x32_bf16 v[50:53], v[250:253], v[222:225], v[50:53]
	ds_read_b128 v[222:225], v93 offset:2048
	ds_read_b128 v[146:149], v141 offset:21504
	v_lshl_add_u64 v[180:181], v[132:133], 0, s[26:27]
	global_load_dwordx2 v[190:191], v[180:181], off
	v_lshl_add_u64 v[180:181], v[132:133], 0, s[28:29]
	global_load_dwordx2 v[192:193], v[180:181], off
	v_mfma_f32_16x16x32_bf16 v[46:49], v[238:241], v[226:229], v[46:49]
	v_mfma_f32_16x16x32_bf16 v[42:45], v[242:245], v[226:229], v[42:45]
	v_mfma_f32_16x16x32_bf16 v[38:41], v[246:249], v[226:229], v[38:41]
	v_mfma_f32_16x16x32_bf16 v[34:37], v[250:253], v[226:229], v[34:37]
	ds_read_b128 v[226:229], v93 offset:4096
	ds_read_b128 v[156:159], v141 offset:23552
	v_lshl_add_u64 v[180:181], v[132:133], 0, s[36:37]
	global_load_dwordx2 v[194:195], v[180:181], off
	v_lshl_add_u64 v[180:181], v[132:133], 0, s[38:39]
	global_load_dwordx2 v[196:197], v[180:181], off
	v_mfma_f32_16x16x32_bf16 v[18:21], v[238:241], v[230:233], v[18:21]
	v_mfma_f32_16x16x32_bf16 v[22:25], v[242:245], v[230:233], v[22:25]
	v_mfma_f32_16x16x32_bf16 v[26:29], v[246:249], v[230:233], v[26:29]
	v_mfma_f32_16x16x32_bf16 v[30:33], v[250:253], v[230:233], v[30:33]
	ds_read_b128 v[230:233], v93 offset:6144
	ds_read_b128 v[160:163], v141 offset:25600
	v_lshl_add_u64 v[180:181], v[132:133], 0, s[40:41]
	global_load_dwordx2 v[198:199], v[180:181], off
	v_lshl_add_u64 v[180:181], v[132:133], 0, s[42:43]
	global_load_dwordx2 v[200:201], v[180:181], off
	v_mfma_f32_16x16x32_bf16 v[2:5], v[238:241], v[234:237], v[2:5]
	v_mfma_f32_16x16x32_bf16 v[6:9], v[242:245], v[234:237], v[6:9]
	v_mfma_f32_16x16x32_bf16 v[10:13], v[246:249], v[234:237], v[10:13]
	v_mfma_f32_16x16x32_bf16 v[14:17], v[250:253], v[234:237], v[14:17]
	ds_read_b128 v[234:237], v93 offset:8192
	s_waitcnt vmcnt(21)
	s_waitcnt lgkmcnt(0)
	s_barrier
	s_mov_b32 s49, s46
	s_mov_b32 s46, s47
	s_mov_b32 s47, s48
	s_mov_b32 s48, s49
	s_add_i32 s49, s48, s74
	s_add_i32 s52, s52, 1
	s_and_b32 s54, s52, 7
	s_cmp_eq_u32 s54, 0
	s_cselect_b32 s54, s53, s32
	s_cselect_b32 s55, -1, 0
	s_add_u32 s30, s30, s54
	s_addc_u32 s31, s31, s55
	v_mfma_f32_16x16x32_bf16 v[78:81], v[142:145], v[218:221], v[78:81]
	v_mfma_f32_16x16x32_bf16 v[74:77], v[146:149], v[218:221], v[74:77]
	v_mfma_f32_16x16x32_bf16 v[70:73], v[156:159], v[218:221], v[70:73]
	v_mfma_f32_16x16x32_bf16 v[66:69], v[160:163], v[218:221], v[66:69]
	s_mov_b32 m0, s49
	s_nop 0
	global_load_lds_dwordx4 v88, s[30:31]
	v_mfma_f32_16x16x32_bf16 v[62:65], v[142:145], v[222:225], v[62:65]
	v_mfma_f32_16x16x32_bf16 v[58:61], v[146:149], v[222:225], v[58:61]
	v_mfma_f32_16x16x32_bf16 v[54:57], v[156:159], v[222:225], v[54:57]
	v_mfma_f32_16x16x32_bf16 v[50:53], v[160:163], v[222:225], v[50:53]
	s_add_i32 m0, s49, 0x2000
	s_nop 0
	global_load_lds_dwordx4 v90, s[30:31]
	v_mfma_f32_16x16x32_bf16 v[46:49], v[142:145], v[226:229], v[46:49]
	v_mfma_f32_16x16x32_bf16 v[42:45], v[146:149], v[226:229], v[42:45]
	v_mfma_f32_16x16x32_bf16 v[38:41], v[156:159], v[226:229], v[38:41]
	v_mfma_f32_16x16x32_bf16 v[34:37], v[160:163], v[226:229], v[34:37]
	s_add_i32 m0, s49, 0x4000
	s_nop 0
	global_load_lds_dwordx4 v92, s[30:31]
	v_mfma_f32_16x16x32_bf16 v[18:21], v[142:145], v[230:233], v[18:21]
	v_mfma_f32_16x16x32_bf16 v[22:25], v[146:149], v[230:233], v[22:25]
	v_mfma_f32_16x16x32_bf16 v[26:29], v[156:159], v[230:233], v[26:29]
	v_mfma_f32_16x16x32_bf16 v[30:33], v[160:163], v[230:233], v[30:33]
	s_add_i32 m0, s49, 0x6000
	s_nop 0
	global_load_lds_dwordx4 v94, s[30:31]
	v_mfma_f32_16x16x32_bf16 v[2:5], v[142:145], v[234:237], v[2:5]
	v_mfma_f32_16x16x32_bf16 v[6:9], v[146:149], v[234:237], v[6:9]
	v_mfma_f32_16x16x32_bf16 v[10:13], v[156:159], v[234:237], v[10:13]
	v_mfma_f32_16x16x32_bf16 v[14:17], v[160:163], v[234:237], v[14:17]
	s_add_i32 m0, s49, 0x8000
	s_nop 0
	global_load_lds_dwordx4 v96, s[30:31]
	v_cvt_pk_bf16_f32 v172, v202, v204
	v_cvt_pk_bf16_f32 v173, v206, v208
	v_cvt_pk_bf16_f32 v174, v210, v212
	v_cvt_pk_bf16_f32 v175, v214, v216
	v_cvt_pk_bf16_f32 v176, v203, v205
	v_cvt_pk_bf16_f32 v177, v207, v209
	v_cvt_pk_bf16_f32 v178, v211, v213
	v_cvt_pk_bf16_f32 v179, v215, v217
	ds_write_b128 v95, v[172:175] offset:19456
	ds_write_b128 v95, v[176:179] offset:19584
	v_add_u32_e32 v91, s46, v135
	v_add_u32_e32 v93, s46, v137
	ds_read_b128 v[238:241], v139 offset:0
	ds_read_b128 v[242:245], v139 offset:2048
	ds_read_b128 v[246:249], v139 offset:4096
	ds_read_b128 v[250:253], v139 offset:6144
	ds_read_b128 v[218:221], v91 offset:0
	ds_read_b128 v[222:225], v91 offset:2048
	ds_read_b128 v[226:229], v91 offset:4096
	ds_read_b128 v[230:233], v91 offset:6144
	ds_read_b128 v[234:237], v91 offset:8192
	s_waitcnt lgkmcnt(0)
; #define MD_GLDS_A(buf, tau) do { _Pragma("unroll") for (int i = 0; i < 5; ++i) if (amask & (1u << i)) \
;         __builtin_amdgcn_global_load_lds((const unsigned*)((const char*)HIDp + aoff[i] + (size_t)((tau) & 7) * 128), (PG8_LAS unsigned*)(MD_SA(buf) + wid * 1024 + i * 8192), 16, 0, 0); } while (0)
; #define MD_B_ISSUE(sb, tau) do { const char* kb_ = Bb + (size_t)((tau) >> 3) * 512 + (size_t)((tau) & 7) * (64 * (size_t)RB); _Pragma("unroll") for (int j = 0; j < 8; ++j) { const char* p_ = kb_ + (size_t)j * RB; \
;         asm volatile("global_load_dwordx2 %0, %1, off" : "=&v"(sb[j]) : "v"(p_) : "memory"); } } while (0)
; #define MD_B_WAIT(sb, N) asm volatile("s_waitcnt vmcnt(%8)" : "+v"(sb[0]), "+v"(sb[1]), "+v"(sb[2]), "+v"(sb[3]), "+v"(sb[4]), "+v"(sb[5]), "+v"(sb[6]), "+v"(sb[7]) : "n"(N) : "memory")
; #define MD_END(last) do { if (last) asm volatile("s_waitcnt vmcnt(0)" ::: "memory"); else asm volatile("s_waitcnt vmcnt(8)" ::: "memory"); \
;         asm volatile("s_waitcnt lgkmcnt(0)" ::: "memory"); __builtin_amdgcn_s_barrier(); asm volatile("" ::: "memory"); } while (0)
; __device__ __forceinline__ void moe_down_stream(PG8_LAS unsigned char* lds, int e, int cb0, int slot0, int nv, const bf16_t* HIDp, const float* Wd, bf16_t* Y, const float* slot_w, const int* slot_dst) {
;     ...
;     for (int t = 0; t < NT; t += 2) {
;         if (t + 2 < NT) MD_B_WAIT(s1, 8); else MD_B_WAIT(s1, 0);
;         MD_B_WRITE(s1, 1); __builtin_amdgcn_sched_barrier(0); MD_GLDS_A(1, t + 1); __builtin_amdgcn_sched_barrier(0);
;         if (t + 3 < NT) MD_B_ISSUE(s1, t + 3);
;         MD_COMPUTE(0);
;         MD_END(t + 3 >= NT);
;         if (t + 2 < NT) { MD_B_WAIT(s0, 8); MD_B_WRITE(s0, 0); __builtin_amdgcn_sched_barrier(0); MD_GLDS_A(0, t + 2); __builtin_amdgcn_sched_barrier(0); }
;         if (t + 4 < NT) MD_B_ISSUE(s0, t + 4);
;         MD_COMPUTE(1);
;         MD_END(t + 4 >= NT);
	v_mfma_f32_16x16x32_bf16 v[78:81], v[238:241], v[218:221], v[78:81]
	v_mfma_f32_16x16x32_bf16 v[74:77], v[242:245], v[218:221], v[74:77]
	v_mfma_f32_16x16x32_bf16 v[70:73], v[246:249], v[218:221], v[70:73]
	v_mfma_f32_16x16x32_bf16 v[66:69], v[250:253], v[218:221], v[66:69]
	ds_read_b128 v[218:221], v93 offset:0
	ds_read_b128 v[142:145], v141 offset:0
	s_add_i32 s51, s51, 1
	s_and_b32 s54, s51, 7
	s_cmp_eq_u32 s54, 0
	s_cselect_b32 s44, s34, s35
	s_cselect_b32 s45, -1, 0
	v_lshl_add_u64 v[132:133], v[132:133], 0, s[44:45]
	global_load_dwordx2 v[202:203], v[132:133], off
	v_lshl_add_u64 v[180:181], v[132:133], 0, s[24:25]
	global_load_dwordx2 v[204:205], v[180:181], off
	v_mfma_f32_16x16x32_bf16 v[62:65], v[238:241], v[222:225], v[62:65]
	v_mfma_f32_16x16x32_bf16 v[58:61], v[242:245], v[222:225], v[58:61]
	v_mfma_f32_16x16x32_bf16 v[54:57], v[246:249], v[222:225], v[54:57]
	v_mfma_f32_16x16x32_bf16 v[50:53], v[250:253], v[222:225], v[50:53]
	ds_read_b128 v[222:225], v93 offset:2048
	ds_read_b128 v[146:149], v141 offset:2048
	v_lshl_add_u64 v[180:181], v[132:133], 0, s[26:27]
	global_load_dwordx2 v[206:207], v[180:181], off
	v_lshl_add_u64 v[180:181], v[132:133], 0, s[28:29]
	global_load_dwordx2 v[208:209], v[180:181], off
	v_mfma_f32_16x16x32_bf16 v[46:49], v[238:241], v[226:229], v[46:49]
	v_mfma_f32_16x16x32_bf16 v[42:45], v[242:245], v[226:229], v[42:45]
	v_mfma_f32_16x16x32_bf16 v[38:41], v[246:249], v[226:229], v[38:41]
	v_mfma_f32_16x16x32_bf16 v[34:37], v[250:253], v[226:229], v[34:37]
	ds_read_b128 v[226:229], v93 offset:4096
	ds_read_b128 v[156:159], v141 offset:4096
	v_lshl_add_u64 v[180:181], v[132:133], 0, s[36:37]
	global_load_dwordx2 v[210:211], v[180:181], off
	v_lshl_add_u64 v[180:181], v[132:133], 0, s[38:39]
	global_load_dwordx2 v[212:213], v[180:181], off
	v_mfma_f32_16x16x32_bf16 v[18:21], v[238:241], v[230:233], v[18:21]
	v_mfma_f32_16x16x32_bf16 v[22:25], v[242:245], v[230:233], v[22:25]
	v_mfma_f32_16x16x32_bf16 v[26:29], v[246:249], v[230:233], v[26:29]
	v_mfma_f32_16x16x32_bf16 v[30:33], v[250:253], v[230:233], v[30:33]
	ds_read_b128 v[230:233], v93 offset:6144
	ds_read_b128 v[160:163], v141 offset:6144
	v_lshl_add_u64 v[180:181], v[132:133], 0, s[40:41]
	global_load_dwordx2 v[214:215], v[180:181], off
	v_lshl_add_u64 v[180:181], v[132:133], 0, s[42:43]
	global_load_dwordx2 v[216:217], v[180:181], off
	v_mfma_f32_16x16x32_bf16 v[2:5], v[238:241], v[234:237], v[2:5]
	v_mfma_f32_16x16x32_bf16 v[6:9], v[242:245], v[234:237], v[6:9]
	v_mfma_f32_16x16x32_bf16 v[10:13], v[246:249], v[234:237], v[10:13]
	v_mfma_f32_16x16x32_bf16 v[14:17], v[250:253], v[234:237], v[14:17]
	ds_read_b128 v[234:237], v93 offset:8192
	s_waitcnt vmcnt(21)
	s_waitcnt lgkmcnt(0)
	s_barrier
	s_mov_b32 s49, s46
	s_mov_b32 s46, s47
	s_mov_b32 s47, s48
	s_mov_b32 s48, s49
	s_add_i32 s49, s48, s74
	s_add_i32 s52, s52, 1
	s_and_b32 s54, s52, 7
	s_cmp_eq_u32 s54, 0
	s_cselect_b32 s54, s53, s32
	s_cselect_b32 s55, -1, 0
	s_add_u32 s30, s30, s54
	s_addc_u32 s31, s31, s55
	v_mfma_f32_16x16x32_bf16 v[78:81], v[142:145], v[218:221], v[78:81]
	v_mfma_f32_16x16x32_bf16 v[74:77], v[146:149], v[218:221], v[74:77]
	v_mfma_f32_16x16x32_bf16 v[70:73], v[156:159], v[218:221], v[70:73]
	v_mfma_f32_16x16x32_bf16 v[66:69], v[160:163], v[218:221], v[66:69]
	s_mov_b32 m0, s49
	s_nop 0
	global_load_lds_dwordx4 v88, s[30:31]
	v_mfma_f32_16x16x32_bf16 v[62:65], v[142:145], v[222:225], v[62:65]
	v_mfma_f32_16x16x32_bf16 v[58:61], v[146:149], v[222:225], v[58:61]
	v_mfma_f32_16x16x32_bf16 v[54:57], v[156:159], v[222:225], v[54:57]
	v_mfma_f32_16x16x32_bf16 v[50:53], v[160:163], v[222:225], v[50:53]
	s_add_i32 m0, s49, 0x2000
	s_nop 0
	global_load_lds_dwordx4 v90, s[30:31]
	v_mfma_f32_16x16x32_bf16 v[46:49], v[142:145], v[226:229], v[46:49]
	v_mfma_f32_16x16x32_bf16 v[42:45], v[146:149], v[226:229], v[42:45]
	v_mfma_f32_16x16x32_bf16 v[38:41], v[156:159], v[226:229], v[38:41]
	v_mfma_f32_16x16x32_bf16 v[34:37], v[160:163], v[226:229], v[34:37]
	s_add_i32 m0, s49, 0x4000
	s_nop 0
	global_load_lds_dwordx4 v92, s[30:31]
	v_mfma_f32_16x16x32_bf16 v[18:21], v[142:145], v[230:233], v[18:21]
	v_mfma_f32_16x16x32_bf16 v[22:25], v[146:149], v[230:233], v[22:25]
	v_mfma_f32_16x16x32_bf16 v[26:29], v[156:159], v[230:233], v[26:29]
	v_mfma_f32_16x16x32_bf16 v[30:33], v[160:163], v[230:233], v[30:33]
	s_add_i32 m0, s49, 0x6000
	s_nop 0
	global_load_lds_dwordx4 v94, s[30:31]
	v_mfma_f32_16x16x32_bf16 v[2:5], v[142:145], v[234:237], v[2:5]
	v_mfma_f32_16x16x32_bf16 v[6:9], v[146:149], v[234:237], v[6:9]
	v_mfma_f32_16x16x32_bf16 v[10:13], v[156:159], v[234:237], v[10:13]
	v_mfma_f32_16x16x32_bf16 v[14:17], v[160:163], v[234:237], v[14:17]
	s_add_i32 m0, s49, 0x8000
	s_nop 0
	global_load_lds_dwordx4 v96, s[30:31]
	v_cvt_pk_bf16_f32 v172, v98, v100
	v_cvt_pk_bf16_f32 v173, v102, v104
	v_cvt_pk_bf16_f32 v174, v106, v108
	v_cvt_pk_bf16_f32 v175, v110, v112
	v_cvt_pk_bf16_f32 v176, v99, v101
	v_cvt_pk_bf16_f32 v177, v103, v105
	v_cvt_pk_bf16_f32 v178, v107, v109
	v_cvt_pk_bf16_f32 v179, v111, v113
	ds_write_b128 v95, v[172:175] offset:0
	ds_write_b128 v95, v[176:179] offset:128
	v_add_u32_e32 v91, s46, v135
	v_add_u32_e32 v93, s46, v137
	ds_read_b128 v[238:241], v139 offset:19456
	ds_read_b128 v[242:245], v139 offset:21504
	ds_read_b128 v[246:249], v139 offset:23552
	ds_read_b128 v[250:253], v139 offset:25600
	ds_read_b128 v[218:221], v91 offset:0
	ds_read_b128 v[222:225], v91 offset:2048
	ds_read_b128 v[226:229], v91 offset:4096
	ds_read_b128 v[230:233], v91 offset:6144
	ds_read_b128 v[234:237], v91 offset:8192
	s_waitcnt lgkmcnt(0)
; #define PG8_LAS __attribute__((address_space(3)))
; __device__ __forceinline__ unsigned cvtpk(float lo, float hi) { f32x2 v = {lo, hi}; bf16x2_t b = __builtin_convertvector(v, bf16x2_t); return __builtin_bit_cast(unsigned, b); }
; __device__ __forceinline__ void moe_down_stream(PG8_LAS unsigned char* lds, int e, int cb0, int slot0, int nv, const bf16_t* HIDp, const float* Wd, bf16_t* Y, const float* slot_w, const int* slot_dst) {
;     ...
;         if (((t + 1) & 7) == 7) {
;             const int cb = cb0 + ((t + 1) >> 3);
; #pragma unroll
;             for (int m = 0; m < DNM; ++m) {
;                 const float w_ = lw[4 * (16 * m + fr) + wr];
; #pragma unroll
;                 for (int p = 0; p < 2; ++p) { const f32x4 v0 = acc[m][2 * p] * w_, v1 = acc[m][2 * p + 1] * w_; u32x4 w; w.x = cvtpk(v0[0], v0[1]); w.y = cvtpk(v0[2], v0[3]); w.z = cvtpk(v1[0], v1[1]); w.w = cvtpk(v1[2], v1[3]);
;                     *(PG8_LAS u32x4*)(stg + fr * 128 + (((4 * p + fq) ^ (fr & 7)) * 16)) = w; }
; #pragma unroll
;                 for (int hh = 0; hh < 2; ++hh) { const int r = (lane >> 3) + 8 * hh, cc = lane & 7; const u32x4 d = *(const PG8_LAS u32x4*)(stg + r * 128 + ((cc ^ (r & 7)) * 16)); const int dst_ = ldst[4 * (16 * m + r) + wr];
;                     if (dst_ >= 0) *(u32x4*)(Y + (size_t)dst_ * D + 128 * cb + 64 * wc + 8 * cc) = d; }
; #pragma unroll
;                 for (int n = 0; n < 4; ++n) acc[m][n] = (f32x4){0.f, 0.f, 0.f, 0.f}; } }
	v_mfma_f32_16x16x32_bf16 v[78:81], v[238:241], v[218:221], v[78:81]
	v_mfma_f32_16x16x32_bf16 v[74:77], v[242:245], v[218:221], v[74:77]
	v_mfma_f32_16x16x32_bf16 v[70:73], v[246:249], v[218:221], v[70:73]
	v_mfma_f32_16x16x32_bf16 v[66:69], v[250:253], v[218:221], v[66:69]
	ds_read_b128 v[218:221], v93 offset:0
	ds_read_b128 v[142:145], v141 offset:19456
	s_add_i32 s51, s51, 1
	s_and_b32 s54, s51, 7
	s_cmp_eq_u32 s54, 0
	s_cselect_b32 s44, s34, s35
	s_cselect_b32 s45, -1, 0
	v_lshl_add_u64 v[132:133], v[132:133], 0, s[44:45]
	global_load_dwordx2 v[98:99], v[132:133], off
	v_lshl_add_u64 v[180:181], v[132:133], 0, s[24:25]
	global_load_dwordx2 v[100:101], v[180:181], off
	v_mfma_f32_16x16x32_bf16 v[62:65], v[238:241], v[222:225], v[62:65]
	v_mfma_f32_16x16x32_bf16 v[58:61], v[242:245], v[222:225], v[58:61]
	v_mfma_f32_16x16x32_bf16 v[54:57], v[246:249], v[222:225], v[54:57]
	v_mfma_f32_16x16x32_bf16 v[50:53], v[250:253], v[222:225], v[50:53]
	ds_read_b128 v[222:225], v93 offset:2048
	ds_read_b128 v[146:149], v141 offset:21504
	v_lshl_add_u64 v[180:181], v[132:133], 0, s[26:27]
	global_load_dwordx2 v[102:103], v[180:181], off
	v_lshl_add_u64 v[180:181], v[132:133], 0, s[28:29]
	global_load_dwordx2 v[104:105], v[180:181], off
	v_mfma_f32_16x16x32_bf16 v[46:49], v[238:241], v[226:229], v[46:49]
	v_mfma_f32_16x16x32_bf16 v[42:45], v[242:245], v[226:229], v[42:45]
	v_mfma_f32_16x16x32_bf16 v[38:41], v[246:249], v[226:229], v[38:41]
	v_mfma_f32_16x16x32_bf16 v[34:37], v[250:253], v[226:229], v[34:37]
	ds_read_b128 v[226:229], v93 offset:4096
	ds_read_b128 v[156:159], v141 offset:23552
	v_lshl_add_u64 v[180:181], v[132:133], 0, s[36:37]
	global_load_dwordx2 v[106:107], v[180:181], off
	v_lshl_add_u64 v[180:181], v[132:133], 0, s[38:39]
	global_load_dwordx2 v[108:109], v[180:181], off
	v_mfma_f32_16x16x32_bf16 v[18:21], v[238:241], v[230:233], v[18:21]
	v_mfma_f32_16x16x32_bf16 v[22:25], v[242:245], v[230:233], v[22:25]
	v_mfma_f32_16x16x32_bf16 v[26:29], v[246:249], v[230:233], v[26:29]
	v_mfma_f32_16x16x32_bf16 v[30:33], v[250:253], v[230:233], v[30:33]
	ds_read_b128 v[230:233], v93 offset:6144
	ds_read_b128 v[160:163], v141 offset:25600
	v_lshl_add_u64 v[180:181], v[132:133], 0, s[40:41]
	global_load_dwordx2 v[110:111], v[180:181], off
	v_lshl_add_u64 v[180:181], v[132:133], 0, s[42:43]
	global_load_dwordx2 v[112:113], v[180:181], off
	v_mfma_f32_16x16x32_bf16 v[2:5], v[238:241], v[234:237], v[2:5]
	v_mfma_f32_16x16x32_bf16 v[6:9], v[242:245], v[234:237], v[6:9]
	v_mfma_f32_16x16x32_bf16 v[10:13], v[246:249], v[234:237], v[10:13]
	v_mfma_f32_16x16x32_bf16 v[14:17], v[250:253], v[234:237], v[14:17]
	ds_read_b128 v[234:237], v93 offset:8192
	s_waitcnt vmcnt(21)
	s_waitcnt lgkmcnt(0)
	s_barrier
	s_mov_b32 s49, s46
	s_mov_b32 s46, s47
	s_mov_b32 s47, s48
	s_mov_b32 s48, s49
	v_mfma_f32_16x16x32_bf16 v[78:81], v[142:145], v[218:221], v[78:81]
	v_mfma_f32_16x16x32_bf16 v[74:77], v[146:149], v[218:221], v[74:77]
	v_mfma_f32_16x16x32_bf16 v[70:73], v[156:159], v[218:221], v[70:73]
	v_mfma_f32_16x16x32_bf16 v[66:69], v[160:163], v[218:221], v[66:69]
	v_mfma_f32_16x16x32_bf16 v[62:65], v[142:145], v[222:225], v[62:65]
	v_mfma_f32_16x16x32_bf16 v[58:61], v[146:149], v[222:225], v[58:61]
	v_mfma_f32_16x16x32_bf16 v[54:57], v[156:159], v[222:225], v[54:57]
	v_mfma_f32_16x16x32_bf16 v[50:53], v[160:163], v[222:225], v[50:53]
	v_mfma_f32_16x16x32_bf16 v[46:49], v[142:145], v[226:229], v[46:49]
	v_mfma_f32_16x16x32_bf16 v[42:45], v[146:149], v[226:229], v[42:45]
	v_mfma_f32_16x16x32_bf16 v[38:41], v[156:159], v[226:229], v[38:41]
	v_mfma_f32_16x16x32_bf16 v[34:37], v[160:163], v[226:229], v[34:37]
	v_mfma_f32_16x16x32_bf16 v[18:21], v[142:145], v[230:233], v[18:21]
	v_mfma_f32_16x16x32_bf16 v[22:25], v[146:149], v[230:233], v[22:25]
	v_mfma_f32_16x16x32_bf16 v[26:29], v[156:159], v[230:233], v[26:29]
	v_mfma_f32_16x16x32_bf16 v[30:33], v[160:163], v[230:233], v[30:33]
	v_mfma_f32_16x16x32_bf16 v[2:5], v[142:145], v[234:237], v[2:5]
	v_mfma_f32_16x16x32_bf16 v[6:9], v[146:149], v[234:237], v[6:9]
	v_mfma_f32_16x16x32_bf16 v[10:13], v[156:159], v[234:237], v[10:13]
	v_mfma_f32_16x16x32_bf16 v[14:17], v[160:163], v[234:237], v[14:17]
	s_add_i32 s54, s48, s74
	v_add_u32_e32 v164, s54, v84
	v_add_u32_e32 v165, s54, v85
	ds_read_b32 v150, v82 offset:0
	ds_read_b32 v151, v83 offset:0
	ds_read_b32 v166, v83 offset:128
	s_waitcnt lgkmcnt(2)
	v_mul_f32_e32 v78, v150, v78
	v_mul_f32_e32 v79, v150, v79
	v_mul_f32_e32 v80, v150, v80
	v_mul_f32_e32 v81, v150, v81
	v_mul_f32_e32 v74, v150, v74
	v_mul_f32_e32 v75, v150, v75
	v_mul_f32_e32 v76, v150, v76
	v_mul_f32_e32 v77, v150, v77
	v_cvt_pk_bf16_f32 v182, v78, v79
	v_cvt_pk_bf16_f32 v183, v80, v81
	v_cvt_pk_bf16_f32 v184, v74, v75
	v_cvt_pk_bf16_f32 v185, v76, v77
	ds_write_b128 v164, v[182:185]
	v_mul_f32_e32 v70, v150, v70
	v_mul_f32_e32 v71, v150, v71
	v_mul_f32_e32 v72, v150, v72
	v_mul_f32_e32 v73, v150, v73
	v_mul_f32_e32 v66, v150, v66
	v_mul_f32_e32 v67, v150, v67
	v_mul_f32_e32 v68, v150, v68
	v_mul_f32_e32 v69, v150, v69
	v_cvt_pk_bf16_f32 v182, v70, v71
	v_cvt_pk_bf16_f32 v183, v72, v73
	v_cvt_pk_bf16_f32 v184, v66, v67
	v_cvt_pk_bf16_f32 v185, v68, v69
	v_xor_b32_e32 v167, 64, v164
	ds_write_b128 v167, v[182:185]
	v_mov_b32_e32 v78, 0
	v_mov_b32_e32 v74, 0
	v_mov_b32_e32 v70, 0
	v_mov_b32_e32 v66, 0
	v_mov_b32_e32 v79, 0
	v_mov_b32_e32 v75, 0
	v_mov_b32_e32 v71, 0
	v_mov_b32_e32 v67, 0
	v_mov_b32_e32 v80, 0
	v_mov_b32_e32 v76, 0
	v_mov_b32_e32 v72, 0
	v_mov_b32_e32 v68, 0
	v_mov_b32_e32 v81, 0
	v_mov_b32_e32 v77, 0
	v_mov_b32_e32 v73, 0
	v_mov_b32_e32 v69, 0
	ds_read_b128 v[182:185], v165 offset:0
	v_cmp_lt_i32_e32 vcc, -1, v151
	v_lshlrev_b32_e32 v148, 13, v151
	v_mov_b32_e32 v149, 0
	v_lshl_add_u64 v[148:149], v[148:149], 0, v[86:87]
	v_cndmask_b32_e32 v148, v168, v148, vcc
	v_cndmask_b32_e32 v149, v169, v149, vcc
	s_waitcnt lgkmcnt(0)
; #define PG8_LAS __attribute__((address_space(3)))
; __device__ __forceinline__ unsigned cvtpk(float lo, float hi) { f32x2 v = {lo, hi}; bf16x2_t b = __builtin_convertvector(v, bf16x2_t); return __builtin_bit_cast(unsigned, b); }
; __device__ __forceinline__ void moe_down_stream(PG8_LAS unsigned char* lds, int e, int cb0, int slot0, int nv, const bf16_t* HIDp, const float* Wd, bf16_t* Y, const float* slot_w, const int* slot_dst) {
;     ...
;         if (((t + 1) & 7) == 7) {
;             const int cb = cb0 + ((t + 1) >> 3);
; #pragma unroll
;             for (int m = 0; m < DNM; ++m) {
;                 const float w_ = lw[4 * (16 * m + fr) + wr];
; #pragma unroll
;                 for (int p = 0; p < 2; ++p) { const f32x4 v0 = acc[m][2 * p] * w_, v1 = acc[m][2 * p + 1] * w_; u32x4 w; w.x = cvtpk(v0[0], v0[1]); w.y = cvtpk(v0[2], v0[3]); w.z = cvtpk(v1[0], v1[1]); w.w = cvtpk(v1[2], v1[3]);
;                     *(PG8_LAS u32x4*)(stg + fr * 128 + (((4 * p + fq) ^ (fr & 7)) * 16)) = w; }
; #pragma unroll
;                 for (int hh = 0; hh < 2; ++hh) { const int r = (lane >> 3) + 8 * hh, cc = lane & 7; const u32x4 d = *(const PG8_LAS u32x4*)(stg + r * 128 + ((cc ^ (r & 7)) * 16)); const int dst_ = ldst[4 * (16 * m + r) + wr];
;                     if (dst_ >= 0) *(u32x4*)(Y + (size_t)dst_ * D + 128 * cb + 64 * wc + 8 * cc) = d; }
; #pragma unroll
;                 for (int n = 0; n < 4; ++n) acc[m][n] = (f32x4){0.f, 0.f, 0.f, 0.f}; } }
	global_store_dwordx4 v[148:149], v[182:185], off
	ds_read_b128 v[182:185], v165 offset:8192
	v_cmp_lt_i32_e32 vcc, -1, v166
	v_lshlrev_b32_e32 v148, 13, v166
	v_mov_b32_e32 v149, 0
	v_lshl_add_u64 v[148:149], v[148:149], 0, v[86:87]
	v_cndmask_b32_e32 v148, v168, v148, vcc
	v_cndmask_b32_e32 v149, v169, v149, vcc
	s_waitcnt lgkmcnt(0)
	global_store_dwordx4 v[148:149], v[182:185], off
	ds_read_b32 v150, v82 offset:256
	ds_read_b32 v151, v83 offset:256
	ds_read_b32 v166, v83 offset:384
	s_waitcnt lgkmcnt(2)
	v_mul_f32_e32 v62, v150, v62
	v_mul_f32_e32 v63, v150, v63
	v_mul_f32_e32 v64, v150, v64
	v_mul_f32_e32 v65, v150, v65
	v_mul_f32_e32 v58, v150, v58
	v_mul_f32_e32 v59, v150, v59
	v_mul_f32_e32 v60, v150, v60
	v_mul_f32_e32 v61, v150, v61
	v_cvt_pk_bf16_f32 v182, v62, v63
	v_cvt_pk_bf16_f32 v183, v64, v65
	v_cvt_pk_bf16_f32 v184, v58, v59
	v_cvt_pk_bf16_f32 v185, v60, v61
	ds_write_b128 v164, v[182:185]
	v_mul_f32_e32 v54, v150, v54
	v_mul_f32_e32 v55, v150, v55
	v_mul_f32_e32 v56, v150, v56
	v_mul_f32_e32 v57, v150, v57
	v_mul_f32_e32 v50, v150, v50
	v_mul_f32_e32 v51, v150, v51
	v_mul_f32_e32 v52, v150, v52
	v_mul_f32_e32 v53, v150, v53
	v_cvt_pk_bf16_f32 v182, v54, v55
	v_cvt_pk_bf16_f32 v183, v56, v57
	v_cvt_pk_bf16_f32 v184, v50, v51
	v_cvt_pk_bf16_f32 v185, v52, v53
	v_xor_b32_e32 v167, 64, v164
	ds_write_b128 v167, v[182:185]
	v_mov_b32_e32 v62, 0
	v_mov_b32_e32 v58, 0
	v_mov_b32_e32 v54, 0
	v_mov_b32_e32 v50, 0
	v_mov_b32_e32 v63, 0
	v_mov_b32_e32 v59, 0
	v_mov_b32_e32 v55, 0
	v_mov_b32_e32 v51, 0
	v_mov_b32_e32 v64, 0
	v_mov_b32_e32 v60, 0
	v_mov_b32_e32 v56, 0
	v_mov_b32_e32 v52, 0
	v_mov_b32_e32 v65, 0
	v_mov_b32_e32 v61, 0
	v_mov_b32_e32 v57, 0
	v_mov_b32_e32 v53, 0
	ds_read_b128 v[182:185], v165 offset:0
	v_cmp_lt_i32_e32 vcc, -1, v151
	v_lshlrev_b32_e32 v148, 13, v151
	v_mov_b32_e32 v149, 0
	v_lshl_add_u64 v[148:149], v[148:149], 0, v[86:87]
	v_cndmask_b32_e32 v148, v168, v148, vcc
	v_cndmask_b32_e32 v149, v169, v149, vcc
	s_waitcnt lgkmcnt(0)
	global_store_dwordx4 v[148:149], v[182:185], off
	ds_read_b128 v[182:185], v165 offset:8192
	v_cmp_lt_i32_e32 vcc, -1, v166
	v_lshlrev_b32_e32 v148, 13, v166
	v_mov_b32_e32 v149, 0
	v_lshl_add_u64 v[148:149], v[148:149], 0, v[86:87]
	v_cndmask_b32_e32 v148, v168, v148, vcc
	v_cndmask_b32_e32 v149, v169, v149, vcc
	s_waitcnt lgkmcnt(0)
	global_store_dwordx4 v[148:149], v[182:185], off
	ds_read_b32 v150, v82 offset:512
	ds_read_b32 v151, v83 offset:512
	ds_read_b32 v166, v83 offset:640
	s_waitcnt lgkmcnt(2)
	v_mul_f32_e32 v46, v150, v46
	v_mul_f32_e32 v47, v150, v47
	v_mul_f32_e32 v48, v150, v48
	v_mul_f32_e32 v49, v150, v49
	v_mul_f32_e32 v42, v150, v42
	v_mul_f32_e32 v43, v150, v43
	v_mul_f32_e32 v44, v150, v44
	v_mul_f32_e32 v45, v150, v45
	v_cvt_pk_bf16_f32 v182, v46, v47
	v_cvt_pk_bf16_f32 v183, v48, v49
	v_cvt_pk_bf16_f32 v184, v42, v43
	v_cvt_pk_bf16_f32 v185, v44, v45
	ds_write_b128 v164, v[182:185]
	v_mul_f32_e32 v38, v150, v38
	v_mul_f32_e32 v39, v150, v39
	v_mul_f32_e32 v40, v150, v40
	v_mul_f32_e32 v41, v150, v41
	v_mul_f32_e32 v34, v150, v34
	v_mul_f32_e32 v35, v150, v35
	v_mul_f32_e32 v36, v150, v36
	v_mul_f32_e32 v37, v150, v37
	v_cvt_pk_bf16_f32 v182, v38, v39
	v_cvt_pk_bf16_f32 v183, v40, v41
	v_cvt_pk_bf16_f32 v184, v34, v35
	v_cvt_pk_bf16_f32 v185, v36, v37
	v_xor_b32_e32 v167, 64, v164
	ds_write_b128 v167, v[182:185]
	v_mov_b32_e32 v46, 0
	v_mov_b32_e32 v42, 0
	v_mov_b32_e32 v38, 0
	v_mov_b32_e32 v34, 0
	v_mov_b32_e32 v47, 0
	v_mov_b32_e32 v43, 0
	v_mov_b32_e32 v39, 0
	v_mov_b32_e32 v35, 0
	v_mov_b32_e32 v48, 0
	v_mov_b32_e32 v44, 0
	v_mov_b32_e32 v40, 0
	v_mov_b32_e32 v36, 0
	v_mov_b32_e32 v49, 0
	v_mov_b32_e32 v45, 0
	v_mov_b32_e32 v41, 0
	v_mov_b32_e32 v37, 0
	ds_read_b128 v[182:185], v165 offset:0
	v_cmp_lt_i32_e32 vcc, -1, v151
	v_lshlrev_b32_e32 v148, 13, v151
	v_mov_b32_e32 v149, 0
	v_lshl_add_u64 v[148:149], v[148:149], 0, v[86:87]
	v_cndmask_b32_e32 v148, v168, v148, vcc
	v_cndmask_b32_e32 v149, v169, v149, vcc
	s_waitcnt lgkmcnt(0)
	global_store_dwordx4 v[148:149], v[182:185], off
	ds_read_b128 v[182:185], v165 offset:8192
	v_cmp_lt_i32_e32 vcc, -1, v166
	v_lshlrev_b32_e32 v148, 13, v166
	v_mov_b32_e32 v149, 0
	v_lshl_add_u64 v[148:149], v[148:149], 0, v[86:87]
	v_cndmask_b32_e32 v148, v168, v148, vcc
	v_cndmask_b32_e32 v149, v169, v149, vcc
	s_waitcnt lgkmcnt(0)
	global_store_dwordx4 v[148:149], v[182:185], off
	ds_read_b32 v150, v82 offset:768
	ds_read_b32 v151, v83 offset:768
	ds_read_b32 v166, v83 offset:896
	s_waitcnt lgkmcnt(2)
	v_mul_f32_e32 v18, v150, v18
	v_mul_f32_e32 v19, v150, v19
	v_mul_f32_e32 v20, v150, v20
	v_mul_f32_e32 v21, v150, v21
	v_mul_f32_e32 v22, v150, v22
	v_mul_f32_e32 v23, v150, v23
	v_mul_f32_e32 v24, v150, v24
	v_mul_f32_e32 v25, v150, v25
	v_cvt_pk_bf16_f32 v182, v18, v19
	v_cvt_pk_bf16_f32 v183, v20, v21
	v_cvt_pk_bf16_f32 v184, v22, v23
	v_cvt_pk_bf16_f32 v185, v24, v25
	ds_write_b128 v164, v[182:185]
	v_mul_f32_e32 v26, v150, v26
	v_mul_f32_e32 v27, v150, v27
	v_mul_f32_e32 v28, v150, v28
	v_mul_f32_e32 v29, v150, v29
	v_mul_f32_e32 v30, v150, v30
	v_mul_f32_e32 v31, v150, v31
	v_mul_f32_e32 v32, v150, v32
	v_mul_f32_e32 v33, v150, v33
	v_cvt_pk_bf16_f32 v182, v26, v27
	v_cvt_pk_bf16_f32 v183, v28, v29
	v_cvt_pk_bf16_f32 v184, v30, v31
	v_cvt_pk_bf16_f32 v185, v32, v33
	v_xor_b32_e32 v167, 64, v164
	ds_write_b128 v167, v[182:185]
	v_mov_b32_e32 v18, 0
	v_mov_b32_e32 v22, 0
	v_mov_b32_e32 v26, 0
	v_mov_b32_e32 v30, 0
	v_mov_b32_e32 v19, 0
	v_mov_b32_e32 v23, 0
	v_mov_b32_e32 v27, 0
	v_mov_b32_e32 v31, 0
	v_mov_b32_e32 v20, 0
	v_mov_b32_e32 v24, 0
	v_mov_b32_e32 v28, 0
	v_mov_b32_e32 v32, 0
	v_mov_b32_e32 v21, 0
	v_mov_b32_e32 v25, 0
	v_mov_b32_e32 v29, 0
	v_mov_b32_e32 v33, 0
	ds_read_b128 v[182:185], v165 offset:0
	v_cmp_lt_i32_e32 vcc, -1, v151
	v_lshlrev_b32_e32 v148, 13, v151
	v_mov_b32_e32 v149, 0
	v_lshl_add_u64 v[148:149], v[148:149], 0, v[86:87]
	v_cndmask_b32_e32 v148, v168, v148, vcc
	v_cndmask_b32_e32 v149, v169, v149, vcc
	s_waitcnt lgkmcnt(0)
; #define PG8_LAS __attribute__((address_space(3)))
; __device__ __forceinline__ unsigned cvtpk(float lo, float hi) { f32x2 v = {lo, hi}; bf16x2_t b = __builtin_convertvector(v, bf16x2_t); return __builtin_bit_cast(unsigned, b); }
; __device__ __forceinline__ void moe_down_stream(PG8_LAS unsigned char* lds, int e, int cb0, int slot0, int nv, const bf16_t* HIDp, const float* Wd, bf16_t* Y, const float* slot_w, const int* slot_dst) {
;     ...
;         if (((t + 1) & 7) == 7) {
;             const int cb = cb0 + ((t + 1) >> 3);
; #pragma unroll
;             for (int m = 0; m < DNM; ++m) {
;                 const float w_ = lw[4 * (16 * m + fr) + wr];
; #pragma unroll
;                 for (int p = 0; p < 2; ++p) { const f32x4 v0 = acc[m][2 * p] * w_, v1 = acc[m][2 * p + 1] * w_; u32x4 w; w.x = cvtpk(v0[0], v0[1]); w.y = cvtpk(v0[2], v0[3]); w.z = cvtpk(v1[0], v1[1]); w.w = cvtpk(v1[2], v1[3]);
;                     *(PG8_LAS u32x4*)(stg + fr * 128 + (((4 * p + fq) ^ (fr & 7)) * 16)) = w; }
; #pragma unroll
;                 for (int hh = 0; hh < 2; ++hh) { const int r = (lane >> 3) + 8 * hh, cc = lane & 7; const u32x4 d = *(const PG8_LAS u32x4*)(stg + r * 128 + ((cc ^ (r & 7)) * 16)); const int dst_ = ldst[4 * (16 * m + r) + wr];
;                     if (dst_ >= 0) *(u32x4*)(Y + (size_t)dst_ * D + 128 * cb + 64 * wc + 8 * cc) = d; }
; #pragma unroll
;                 for (int n = 0; n < 4; ++n) acc[m][n] = (f32x4){0.f, 0.f, 0.f, 0.f}; } }
	global_store_dwordx4 v[148:149], v[182:185], off
	ds_read_b128 v[182:185], v165 offset:8192
	v_cmp_lt_i32_e32 vcc, -1, v166
	v_lshlrev_b32_e32 v148, 13, v166
	v_mov_b32_e32 v149, 0
	v_lshl_add_u64 v[148:149], v[148:149], 0, v[86:87]
	v_cndmask_b32_e32 v148, v168, v148, vcc
	v_cndmask_b32_e32 v149, v169, v149, vcc
	s_waitcnt lgkmcnt(0)
	global_store_dwordx4 v[148:149], v[182:185], off
	ds_read_b32 v150, v82 offset:1024
	ds_read_b32 v151, v83 offset:1024
	ds_read_b32 v166, v83 offset:1152
	s_waitcnt lgkmcnt(2)
	v_mul_f32_e32 v2, v150, v2
	v_mul_f32_e32 v3, v150, v3
	v_mul_f32_e32 v4, v150, v4
	v_mul_f32_e32 v5, v150, v5
	v_mul_f32_e32 v6, v150, v6
	v_mul_f32_e32 v7, v150, v7
	v_mul_f32_e32 v8, v150, v8
	v_mul_f32_e32 v9, v150, v9
	v_cvt_pk_bf16_f32 v182, v2, v3
	v_cvt_pk_bf16_f32 v183, v4, v5
	v_cvt_pk_bf16_f32 v184, v6, v7
	v_cvt_pk_bf16_f32 v185, v8, v9
	ds_write_b128 v164, v[182:185]
	v_mul_f32_e32 v10, v150, v10
	v_mul_f32_e32 v11, v150, v11
	v_mul_f32_e32 v12, v150, v12
	v_mul_f32_e32 v13, v150, v13
	v_mul_f32_e32 v14, v150, v14
	v_mul_f32_e32 v15, v150, v15
	v_mul_f32_e32 v16, v150, v16
	v_mul_f32_e32 v17, v150, v17
	v_cvt_pk_bf16_f32 v182, v10, v11
	v_cvt_pk_bf16_f32 v183, v12, v13
	v_cvt_pk_bf16_f32 v184, v14, v15
	v_cvt_pk_bf16_f32 v185, v16, v17
	v_xor_b32_e32 v167, 64, v164
	ds_write_b128 v167, v[182:185]
	v_mov_b32_e32 v2, 0
	v_mov_b32_e32 v6, 0
	v_mov_b32_e32 v10, 0
	v_mov_b32_e32 v14, 0
	v_mov_b32_e32 v3, 0
	v_mov_b32_e32 v7, 0
	v_mov_b32_e32 v11, 0
	v_mov_b32_e32 v15, 0
	v_mov_b32_e32 v4, 0
	v_mov_b32_e32 v8, 0
	v_mov_b32_e32 v12, 0
	v_mov_b32_e32 v16, 0
	v_mov_b32_e32 v5, 0
	v_mov_b32_e32 v9, 0
	v_mov_b32_e32 v13, 0
	v_mov_b32_e32 v17, 0
	ds_read_b128 v[182:185], v165 offset:0
	v_cmp_lt_i32_e32 vcc, -1, v151
	v_lshlrev_b32_e32 v148, 13, v151
	v_mov_b32_e32 v149, 0
	v_lshl_add_u64 v[148:149], v[148:149], 0, v[86:87]
	v_cndmask_b32_e32 v148, v168, v148, vcc
	v_cndmask_b32_e32 v149, v169, v149, vcc
	s_waitcnt lgkmcnt(0)
	global_store_dwordx4 v[148:149], v[182:185], off
	ds_read_b128 v[182:185], v165 offset:8192
	v_cmp_lt_i32_e32 vcc, -1, v166
	v_lshlrev_b32_e32 v148, 13, v166
	v_mov_b32_e32 v149, 0
	v_lshl_add_u64 v[148:149], v[148:149], 0, v[86:87]
	v_cndmask_b32_e32 v148, v168, v148, vcc
	v_cndmask_b32_e32 v149, v169, v149, vcc
	s_waitcnt lgkmcnt(0)
	global_store_dwordx4 v[148:149], v[182:185], off
	v_add_co_u32_e32 v86, vcc, 0x800, v86
	s_nop 1
	v_addc_co_u32_e32 v87, vcc, 0, v87, vcc
	s_waitcnt lgkmcnt(0)
	s_add_i32 s49, s48, s74
	s_add_i32 s52, s52, 1
	s_and_b32 s54, s52, 7
	s_cmp_eq_u32 s54, 0
	s_cselect_b32 s54, s53, s32
	s_cselect_b32 s55, -1, 0
	s_add_u32 s30, s30, s54
	s_addc_u32 s31, s31, s55
	s_mov_b32 m0, s49
	s_nop 0
	global_load_lds_dwordx4 v88, s[30:31]
	s_add_i32 m0, s49, 0x2000
	s_nop 0
	global_load_lds_dwordx4 v90, s[30:31]
	s_add_i32 m0, s49, 0x4000
	s_nop 0
	global_load_lds_dwordx4 v92, s[30:31]
	s_add_i32 m0, s49, 0x6000
	s_nop 0
	global_load_lds_dwordx4 v94, s[30:31]
	s_add_i32 m0, s49, 0x8000
	s_nop 0
	global_load_lds_dwordx4 v96, s[30:31]
	v_cvt_pk_bf16_f32 v172, v114, v116
	v_cvt_pk_bf16_f32 v173, v118, v120
	v_cvt_pk_bf16_f32 v174, v122, v124
	v_cvt_pk_bf16_f32 v175, v126, v128
	v_cvt_pk_bf16_f32 v176, v115, v117
	v_cvt_pk_bf16_f32 v177, v119, v121
	v_cvt_pk_bf16_f32 v178, v123, v125
	v_cvt_pk_bf16_f32 v179, v127, v129
	ds_write_b128 v95, v[172:175] offset:19456
	ds_write_b128 v95, v[176:179] offset:19584
	v_add_u32_e32 v91, s46, v135
	v_add_u32_e32 v93, s46, v137
	ds_read_b128 v[238:241], v139 offset:0
	ds_read_b128 v[242:245], v139 offset:2048
	ds_read_b128 v[246:249], v139 offset:4096
	ds_read_b128 v[250:253], v139 offset:6144
	ds_read_b128 v[218:221], v91 offset:0
	ds_read_b128 v[222:225], v91 offset:2048
	ds_read_b128 v[226:229], v91 offset:4096
	ds_read_b128 v[230:233], v91 offset:6144
	ds_read_b128 v[234:237], v91 offset:8192
	s_waitcnt lgkmcnt(0)
	v_mfma_f32_16x16x32_bf16 v[78:81], v[238:241], v[218:221], v[78:81]
	v_mfma_f32_16x16x32_bf16 v[74:77], v[242:245], v[218:221], v[74:77]
	v_mfma_f32_16x16x32_bf16 v[70:73], v[246:249], v[218:221], v[70:73]
	v_mfma_f32_16x16x32_bf16 v[66:69], v[250:253], v[218:221], v[66:69]
	ds_read_b128 v[218:221], v93 offset:0
	ds_read_b128 v[142:145], v141 offset:0
	s_add_i32 s51, s51, 1
	s_and_b32 s54, s51, 7
	s_cmp_eq_u32 s54, 0
	s_cselect_b32 s44, s34, s35
	s_cselect_b32 s45, -1, 0
	v_lshl_add_u64 v[132:133], v[132:133], 0, s[44:45]
	global_load_dwordx2 v[114:115], v[132:133], off
	v_lshl_add_u64 v[180:181], v[132:133], 0, s[24:25]
	global_load_dwordx2 v[116:117], v[180:181], off
	v_mfma_f32_16x16x32_bf16 v[62:65], v[238:241], v[222:225], v[62:65]
	v_mfma_f32_16x16x32_bf16 v[58:61], v[242:245], v[222:225], v[58:61]
	v_mfma_f32_16x16x32_bf16 v[54:57], v[246:249], v[222:225], v[54:57]
	v_mfma_f32_16x16x32_bf16 v[50:53], v[250:253], v[222:225], v[50:53]
	ds_read_b128 v[222:225], v93 offset:2048
	ds_read_b128 v[146:149], v141 offset:2048
	v_lshl_add_u64 v[180:181], v[132:133], 0, s[26:27]
	global_load_dwordx2 v[118:119], v[180:181], off
	v_lshl_add_u64 v[180:181], v[132:133], 0, s[28:29]
	global_load_dwordx2 v[120:121], v[180:181], off
	v_mfma_f32_16x16x32_bf16 v[46:49], v[238:241], v[226:229], v[46:49]
	v_mfma_f32_16x16x32_bf16 v[42:45], v[242:245], v[226:229], v[42:45]
	v_mfma_f32_16x16x32_bf16 v[38:41], v[246:249], v[226:229], v[38:41]
	v_mfma_f32_16x16x32_bf16 v[34:37], v[250:253], v[226:229], v[34:37]
	ds_read_b128 v[226:229], v93 offset:4096
	ds_read_b128 v[156:159], v141 offset:4096
	v_lshl_add_u64 v[180:181], v[132:133], 0, s[36:37]
	global_load_dwordx2 v[122:123], v[180:181], off
	v_lshl_add_u64 v[180:181], v[132:133], 0, s[38:39]
	global_load_dwordx2 v[124:125], v[180:181], off
	v_mfma_f32_16x16x32_bf16 v[18:21], v[238:241], v[230:233], v[18:21]
	v_mfma_f32_16x16x32_bf16 v[22:25], v[242:245], v[230:233], v[22:25]
	v_mfma_f32_16x16x32_bf16 v[26:29], v[246:249], v[230:233], v[26:29]
	v_mfma_f32_16x16x32_bf16 v[30:33], v[250:253], v[230:233], v[30:33]
	ds_read_b128 v[230:233], v93 offset:6144
	ds_read_b128 v[160:163], v141 offset:6144
	v_lshl_add_u64 v[180:181], v[132:133], 0, s[40:41]
	global_load_dwordx2 v[126:127], v[180:181], off
	v_lshl_add_u64 v[180:181], v[132:133], 0, s[42:43]
	global_load_dwordx2 v[128:129], v[180:181], off
	v_mfma_f32_16x16x32_bf16 v[2:5], v[238:241], v[234:237], v[2:5]
	v_mfma_f32_16x16x32_bf16 v[6:9], v[242:245], v[234:237], v[6:9]
	v_mfma_f32_16x16x32_bf16 v[10:13], v[246:249], v[234:237], v[10:13]
	v_mfma_f32_16x16x32_bf16 v[14:17], v[250:253], v[234:237], v[14:17]
	ds_read_b128 v[234:237], v93 offset:8192
	s_waitcnt vmcnt(31)
	s_waitcnt lgkmcnt(0)
	s_barrier
; #define MD_GLDS_A(buf, tau) do { _Pragma("unroll") for (int i = 0; i < 5; ++i) if (amask & (1u << i)) \
;         __builtin_amdgcn_global_load_lds((const unsigned*)((const char*)HIDp + aoff[i] + (size_t)((tau) & 7) * 128), (PG8_LAS unsigned*)(MD_SA(buf) + wid * 1024 + i * 8192), 16, 0, 0); } while (0)
; #define MD_B_ISSUE(sb, tau) do { const char* kb_ = Bb + (size_t)((tau) >> 3) * 512 + (size_t)((tau) & 7) * (64 * (size_t)RB); _Pragma("unroll") for (int j = 0; j < 8; ++j) { const char* p_ = kb_ + (size_t)j * RB; \
;         asm volatile("global_load_dwordx2 %0, %1, off" : "=&v"(sb[j]) : "v"(p_) : "memory"); } } while (0)
; #define MD_B_WAIT(sb, N) asm volatile("s_waitcnt vmcnt(%8)" : "+v"(sb[0]), "+v"(sb[1]), "+v"(sb[2]), "+v"(sb[3]), "+v"(sb[4]), "+v"(sb[5]), "+v"(sb[6]), "+v"(sb[7]) : "n"(N) : "memory")
; #define MD_END(last) do { if (last) asm volatile("s_waitcnt vmcnt(0)" ::: "memory"); else asm volatile("s_waitcnt vmcnt(8)" ::: "memory"); \
;         asm volatile("s_waitcnt lgkmcnt(0)" ::: "memory"); __builtin_amdgcn_s_barrier(); asm volatile("" ::: "memory"); } while (0)
; __device__ __forceinline__ void moe_down_stream(PG8_LAS unsigned char* lds, int e, int cb0, int slot0, int nv, const bf16_t* HIDp, const float* Wd, bf16_t* Y, const float* slot_w, const int* slot_dst) {
;     ...
;     for (int t = 0; t < NT; t += 2) {
;         if (t + 2 < NT) MD_B_WAIT(s1, 8); else MD_B_WAIT(s1, 0);
;         MD_B_WRITE(s1, 1); __builtin_amdgcn_sched_barrier(0); MD_GLDS_A(1, t + 1); __builtin_amdgcn_sched_barrier(0);
;         if (t + 3 < NT) MD_B_ISSUE(s1, t + 3);
;         MD_COMPUTE(0);
;         MD_END(t + 3 >= NT);
;         if (t + 2 < NT) { MD_B_WAIT(s0, 8); MD_B_WRITE(s0, 0); __builtin_amdgcn_sched_barrier(0); MD_GLDS_A(0, t + 2); __builtin_amdgcn_sched_barrier(0); }
;         if (t + 4 < NT) MD_B_ISSUE(s0, t + 4);
;         MD_COMPUTE(1);
;         MD_END(t + 4 >= NT);
	s_mov_b32 s49, s46
	s_mov_b32 s46, s47
	s_mov_b32 s47, s48
	s_mov_b32 s48, s49
	s_add_i32 s49, s48, s74
	s_add_i32 s52, s52, 1
	s_and_b32 s54, s52, 7
	s_cmp_eq_u32 s54, 0
	s_cselect_b32 s54, s53, s32
	s_cselect_b32 s55, -1, 0
	s_add_u32 s30, s30, s54
	s_addc_u32 s31, s31, s55
	v_mfma_f32_16x16x32_bf16 v[78:81], v[142:145], v[218:221], v[78:81]
	v_mfma_f32_16x16x32_bf16 v[74:77], v[146:149], v[218:221], v[74:77]
	v_mfma_f32_16x16x32_bf16 v[70:73], v[156:159], v[218:221], v[70:73]
	v_mfma_f32_16x16x32_bf16 v[66:69], v[160:163], v[218:221], v[66:69]
	s_mov_b32 m0, s49
	s_nop 0
	global_load_lds_dwordx4 v88, s[30:31]
	v_mfma_f32_16x16x32_bf16 v[62:65], v[142:145], v[222:225], v[62:65]
	v_mfma_f32_16x16x32_bf16 v[58:61], v[146:149], v[222:225], v[58:61]
	v_mfma_f32_16x16x32_bf16 v[54:57], v[156:159], v[222:225], v[54:57]
	v_mfma_f32_16x16x32_bf16 v[50:53], v[160:163], v[222:225], v[50:53]
	s_add_i32 m0, s49, 0x2000
	s_nop 0
	global_load_lds_dwordx4 v90, s[30:31]
	v_mfma_f32_16x16x32_bf16 v[46:49], v[142:145], v[226:229], v[46:49]
	v_mfma_f32_16x16x32_bf16 v[42:45], v[146:149], v[226:229], v[42:45]
	v_mfma_f32_16x16x32_bf16 v[38:41], v[156:159], v[226:229], v[38:41]
	v_mfma_f32_16x16x32_bf16 v[34:37], v[160:163], v[226:229], v[34:37]
	s_add_i32 m0, s49, 0x4000
	s_nop 0
	global_load_lds_dwordx4 v92, s[30:31]
	v_mfma_f32_16x16x32_bf16 v[18:21], v[142:145], v[230:233], v[18:21]
	v_mfma_f32_16x16x32_bf16 v[22:25], v[146:149], v[230:233], v[22:25]
	v_mfma_f32_16x16x32_bf16 v[26:29], v[156:159], v[230:233], v[26:29]
	v_mfma_f32_16x16x32_bf16 v[30:33], v[160:163], v[230:233], v[30:33]
	s_add_i32 m0, s49, 0x6000
	s_nop 0
	global_load_lds_dwordx4 v94, s[30:31]
	v_mfma_f32_16x16x32_bf16 v[2:5], v[142:145], v[234:237], v[2:5]
	v_mfma_f32_16x16x32_bf16 v[6:9], v[146:149], v[234:237], v[6:9]
	v_mfma_f32_16x16x32_bf16 v[10:13], v[156:159], v[234:237], v[10:13]
	v_mfma_f32_16x16x32_bf16 v[14:17], v[160:163], v[234:237], v[14:17]
	s_add_i32 m0, s49, 0x8000
	s_nop 0
	global_load_lds_dwordx4 v96, s[30:31]
	v_cvt_pk_bf16_f32 v172, v186, v188
	v_cvt_pk_bf16_f32 v173, v190, v192
	v_cvt_pk_bf16_f32 v174, v194, v196
	v_cvt_pk_bf16_f32 v175, v198, v200
	v_cvt_pk_bf16_f32 v176, v187, v189
	v_cvt_pk_bf16_f32 v177, v191, v193
	v_cvt_pk_bf16_f32 v178, v195, v197
	v_cvt_pk_bf16_f32 v179, v199, v201
	ds_write_b128 v95, v[172:175] offset:0
	ds_write_b128 v95, v[176:179] offset:128
	v_add_u32_e32 v91, s46, v135
	v_add_u32_e32 v93, s46, v137
	ds_read_b128 v[238:241], v139 offset:19456
	ds_read_b128 v[242:245], v139 offset:21504
	ds_read_b128 v[246:249], v139 offset:23552
	ds_read_b128 v[250:253], v139 offset:25600
	ds_read_b128 v[218:221], v91 offset:0
	ds_read_b128 v[222:225], v91 offset:2048
	ds_read_b128 v[226:229], v91 offset:4096
	ds_read_b128 v[230:233], v91 offset:6144
	ds_read_b128 v[234:237], v91 offset:8192
	s_waitcnt lgkmcnt(0)
	v_mfma_f32_16x16x32_bf16 v[78:81], v[238:241], v[218:221], v[78:81]
	v_mfma_f32_16x16x32_bf16 v[74:77], v[242:245], v[218:221], v[74:77]
	v_mfma_f32_16x16x32_bf16 v[70:73], v[246:249], v[218:221], v[70:73]
	v_mfma_f32_16x16x32_bf16 v[66:69], v[250:253], v[218:221], v[66:69]
	ds_read_b128 v[218:221], v93 offset:0
	ds_read_b128 v[142:145], v141 offset:19456
	s_add_i32 s51, s51, 1
	s_and_b32 s54, s51, 7
	s_cmp_eq_u32 s54, 0
	s_cselect_b32 s44, s34, s35
	s_cselect_b32 s45, -1, 0
	v_lshl_add_u64 v[132:133], v[132:133], 0, s[44:45]
	global_load_dwordx2 v[186:187], v[132:133], off
	v_lshl_add_u64 v[180:181], v[132:133], 0, s[24:25]
	global_load_dwordx2 v[188:189], v[180:181], off
	v_mfma_f32_16x16x32_bf16 v[62:65], v[238:241], v[222:225], v[62:65]
	v_mfma_f32_16x16x32_bf16 v[58:61], v[242:245], v[222:225], v[58:61]
	v_mfma_f32_16x16x32_bf16 v[54:57], v[246:249], v[222:225], v[54:57]
	v_mfma_f32_16x16x32_bf16 v[50:53], v[250:253], v[222:225], v[50:53]
	ds_read_b128 v[222:225], v93 offset:2048
	ds_read_b128 v[146:149], v141 offset:21504
	v_lshl_add_u64 v[180:181], v[132:133], 0, s[26:27]
	global_load_dwordx2 v[190:191], v[180:181], off
	v_lshl_add_u64 v[180:181], v[132:133], 0, s[28:29]
	global_load_dwordx2 v[192:193], v[180:181], off
	v_mfma_f32_16x16x32_bf16 v[46:49], v[238:241], v[226:229], v[46:49]
	v_mfma_f32_16x16x32_bf16 v[42:45], v[242:245], v[226:229], v[42:45]
	v_mfma_f32_16x16x32_bf16 v[38:41], v[246:249], v[226:229], v[38:41]
	v_mfma_f32_16x16x32_bf16 v[34:37], v[250:253], v[226:229], v[34:37]
	ds_read_b128 v[226:229], v93 offset:4096
	ds_read_b128 v[156:159], v141 offset:23552
	v_lshl_add_u64 v[180:181], v[132:133], 0, s[36:37]
	global_load_dwordx2 v[194:195], v[180:181], off
	v_lshl_add_u64 v[180:181], v[132:133], 0, s[38:39]
	global_load_dwordx2 v[196:197], v[180:181], off
	v_mfma_f32_16x16x32_bf16 v[18:21], v[238:241], v[230:233], v[18:21]
	v_mfma_f32_16x16x32_bf16 v[22:25], v[242:245], v[230:233], v[22:25]
	v_mfma_f32_16x16x32_bf16 v[26:29], v[246:249], v[230:233], v[26:29]
	v_mfma_f32_16x16x32_bf16 v[30:33], v[250:253], v[230:233], v[30:33]
	ds_read_b128 v[230:233], v93 offset:6144
	ds_read_b128 v[160:163], v141 offset:25600
	v_lshl_add_u64 v[180:181], v[132:133], 0, s[40:41]
	global_load_dwordx2 v[198:199], v[180:181], off
	v_lshl_add_u64 v[180:181], v[132:133], 0, s[42:43]
	global_load_dwordx2 v[200:201], v[180:181], off
	v_mfma_f32_16x16x32_bf16 v[2:5], v[238:241], v[234:237], v[2:5]
	v_mfma_f32_16x16x32_bf16 v[6:9], v[242:245], v[234:237], v[6:9]
	v_mfma_f32_16x16x32_bf16 v[10:13], v[246:249], v[234:237], v[10:13]
	v_mfma_f32_16x16x32_bf16 v[14:17], v[250:253], v[234:237], v[14:17]
	ds_read_b128 v[234:237], v93 offset:8192
	s_waitcnt vmcnt(21)
	s_waitcnt lgkmcnt(0)
	s_barrier
; #define MD_GLDS_A(buf, tau) do { _Pragma("unroll") for (int i = 0; i < 5; ++i) if (amask & (1u << i)) \
;         __builtin_amdgcn_global_load_lds((const unsigned*)((const char*)HIDp + aoff[i] + (size_t)((tau) & 7) * 128), (PG8_LAS unsigned*)(MD_SA(buf) + wid * 1024 + i * 8192), 16, 0, 0); } while (0)
; #define MD_B_ISSUE(sb, tau) do { const char* kb_ = Bb + (size_t)((tau) >> 3) * 512 + (size_t)((tau) & 7) * (64 * (size_t)RB); _Pragma("unroll") for (int j = 0; j < 8; ++j) { const char* p_ = kb_ + (size_t)j * RB; \
;         asm volatile("global_load_dwordx2 %0, %1, off" : "=&v"(sb[j]) : "v"(p_) : "memory"); } } while (0)
; #define MD_B_WAIT(sb, N) asm volatile("s_waitcnt vmcnt(%8)" : "+v"(sb[0]), "+v"(sb[1]), "+v"(sb[2]), "+v"(sb[3]), "+v"(sb[4]), "+v"(sb[5]), "+v"(sb[6]), "+v"(sb[7]) : "n"(N) : "memory")
; #define MD_END(last) do { if (last) asm volatile("s_waitcnt vmcnt(0)" ::: "memory"); else asm volatile("s_waitcnt vmcnt(8)" ::: "memory"); \
;         asm volatile("s_waitcnt lgkmcnt(0)" ::: "memory"); __builtin_amdgcn_s_barrier(); asm volatile("" ::: "memory"); } while (0)
; __device__ __forceinline__ void moe_down_stream(PG8_LAS unsigned char* lds, int e, int cb0, int slot0, int nv, const bf16_t* HIDp, const float* Wd, bf16_t* Y, const float* slot_w, const int* slot_dst) {
;     ...
;     for (int t = 0; t < NT; t += 2) {
;         if (t + 2 < NT) MD_B_WAIT(s1, 8); else MD_B_WAIT(s1, 0);
;         MD_B_WRITE(s1, 1); __builtin_amdgcn_sched_barrier(0); MD_GLDS_A(1, t + 1); __builtin_amdgcn_sched_barrier(0);
;         if (t + 3 < NT) MD_B_ISSUE(s1, t + 3);
;         MD_COMPUTE(0);
;         MD_END(t + 3 >= NT);
;         if (t + 2 < NT) { MD_B_WAIT(s0, 8); MD_B_WRITE(s0, 0); __builtin_amdgcn_sched_barrier(0); MD_GLDS_A(0, t + 2); __builtin_amdgcn_sched_barrier(0); }
;         if (t + 4 < NT) MD_B_ISSUE(s0, t + 4);
;         MD_COMPUTE(1);
;         MD_END(t + 4 >= NT);
	s_mov_b32 s49, s46
	s_mov_b32 s46, s47
	s_mov_b32 s47, s48
	s_mov_b32 s48, s49
	s_add_i32 s49, s48, s74
	s_add_i32 s52, s52, 1
	s_and_b32 s54, s52, 7
	s_cmp_eq_u32 s54, 0
	s_cselect_b32 s54, s53, s32
	s_cselect_b32 s55, -1, 0
	s_add_u32 s30, s30, s54
	s_addc_u32 s31, s31, s55
	v_mfma_f32_16x16x32_bf16 v[78:81], v[142:145], v[218:221], v[78:81]
	v_mfma_f32_16x16x32_bf16 v[74:77], v[146:149], v[218:221], v[74:77]
	v_mfma_f32_16x16x32_bf16 v[70:73], v[156:159], v[218:221], v[70:73]
	v_mfma_f32_16x16x32_bf16 v[66:69], v[160:163], v[218:221], v[66:69]
	s_mov_b32 m0, s49
	s_nop 0
	global_load_lds_dwordx4 v88, s[30:31]
	v_mfma_f32_16x16x32_bf16 v[62:65], v[142:145], v[222:225], v[62:65]
	v_mfma_f32_16x16x32_bf16 v[58:61], v[146:149], v[222:225], v[58:61]
	v_mfma_f32_16x16x32_bf16 v[54:57], v[156:159], v[222:225], v[54:57]
	v_mfma_f32_16x16x32_bf16 v[50:53], v[160:163], v[222:225], v[50:53]
	s_add_i32 m0, s49, 0x2000
	s_nop 0
	global_load_lds_dwordx4 v90, s[30:31]
	v_mfma_f32_16x16x32_bf16 v[46:49], v[142:145], v[226:229], v[46:49]
	v_mfma_f32_16x16x32_bf16 v[42:45], v[146:149], v[226:229], v[42:45]
	v_mfma_f32_16x16x32_bf16 v[38:41], v[156:159], v[226:229], v[38:41]
	v_mfma_f32_16x16x32_bf16 v[34:37], v[160:163], v[226:229], v[34:37]
	s_add_i32 m0, s49, 0x4000
	s_nop 0
	global_load_lds_dwordx4 v92, s[30:31]
	v_mfma_f32_16x16x32_bf16 v[18:21], v[142:145], v[230:233], v[18:21]
	v_mfma_f32_16x16x32_bf16 v[22:25], v[146:149], v[230:233], v[22:25]
	v_mfma_f32_16x16x32_bf16 v[26:29], v[156:159], v[230:233], v[26:29]
	v_mfma_f32_16x16x32_bf16 v[30:33], v[160:163], v[230:233], v[30:33]
	s_add_i32 m0, s49, 0x6000
	s_nop 0
	global_load_lds_dwordx4 v94, s[30:31]
	v_mfma_f32_16x16x32_bf16 v[2:5], v[142:145], v[234:237], v[2:5]
	v_mfma_f32_16x16x32_bf16 v[6:9], v[146:149], v[234:237], v[6:9]
	v_mfma_f32_16x16x32_bf16 v[10:13], v[156:159], v[234:237], v[10:13]
	v_mfma_f32_16x16x32_bf16 v[14:17], v[160:163], v[234:237], v[14:17]
	s_add_i32 m0, s49, 0x8000
	s_nop 0
	global_load_lds_dwordx4 v96, s[30:31]
	v_cvt_pk_bf16_f32 v172, v202, v204
	v_cvt_pk_bf16_f32 v173, v206, v208
	v_cvt_pk_bf16_f32 v174, v210, v212
	v_cvt_pk_bf16_f32 v175, v214, v216
	v_cvt_pk_bf16_f32 v176, v203, v205
	v_cvt_pk_bf16_f32 v177, v207, v209
	v_cvt_pk_bf16_f32 v178, v211, v213
	v_cvt_pk_bf16_f32 v179, v215, v217
	ds_write_b128 v95, v[172:175] offset:19456
	ds_write_b128 v95, v[176:179] offset:19584
	v_add_u32_e32 v91, s46, v135
	v_add_u32_e32 v93, s46, v137
	ds_read_b128 v[238:241], v139 offset:0
	ds_read_b128 v[242:245], v139 offset:2048
	ds_read_b128 v[246:249], v139 offset:4096
	ds_read_b128 v[250:253], v139 offset:6144
	ds_read_b128 v[218:221], v91 offset:0
	ds_read_b128 v[222:225], v91 offset:2048
	ds_read_b128 v[226:229], v91 offset:4096
	ds_read_b128 v[230:233], v91 offset:6144
	ds_read_b128 v[234:237], v91 offset:8192
	s_waitcnt lgkmcnt(0)
	v_mfma_f32_16x16x32_bf16 v[78:81], v[238:241], v[218:221], v[78:81]
	v_mfma_f32_16x16x32_bf16 v[74:77], v[242:245], v[218:221], v[74:77]
	v_mfma_f32_16x16x32_bf16 v[70:73], v[246:249], v[218:221], v[70:73]
	v_mfma_f32_16x16x32_bf16 v[66:69], v[250:253], v[218:221], v[66:69]
	ds_read_b128 v[218:221], v93 offset:0
	ds_read_b128 v[142:145], v141 offset:0
	s_add_i32 s51, s51, 1
	s_and_b32 s54, s51, 7
	s_cmp_eq_u32 s54, 0
	s_cselect_b32 s44, s34, s35
	s_cselect_b32 s45, -1, 0
	v_lshl_add_u64 v[132:133], v[132:133], 0, s[44:45]
	global_load_dwordx2 v[202:203], v[132:133], off
	v_lshl_add_u64 v[180:181], v[132:133], 0, s[24:25]
	global_load_dwordx2 v[204:205], v[180:181], off
	v_mfma_f32_16x16x32_bf16 v[62:65], v[238:241], v[222:225], v[62:65]
	v_mfma_f32_16x16x32_bf16 v[58:61], v[242:245], v[222:225], v[58:61]
	v_mfma_f32_16x16x32_bf16 v[54:57], v[246:249], v[222:225], v[54:57]
	v_mfma_f32_16x16x32_bf16 v[50:53], v[250:253], v[222:225], v[50:53]
	ds_read_b128 v[222:225], v93 offset:2048
	ds_read_b128 v[146:149], v141 offset:2048
	v_lshl_add_u64 v[180:181], v[132:133], 0, s[26:27]
	global_load_dwordx2 v[206:207], v[180:181], off
	v_lshl_add_u64 v[180:181], v[132:133], 0, s[28:29]
	global_load_dwordx2 v[208:209], v[180:181], off
	v_mfma_f32_16x16x32_bf16 v[46:49], v[238:241], v[226:229], v[46:49]
	v_mfma_f32_16x16x32_bf16 v[42:45], v[242:245], v[226:229], v[42:45]
	v_mfma_f32_16x16x32_bf16 v[38:41], v[246:249], v[226:229], v[38:41]
	v_mfma_f32_16x16x32_bf16 v[34:37], v[250:253], v[226:229], v[34:37]
	ds_read_b128 v[226:229], v93 offset:4096
	ds_read_b128 v[156:159], v141 offset:4096
	v_lshl_add_u64 v[180:181], v[132:133], 0, s[36:37]
	global_load_dwordx2 v[210:211], v[180:181], off
	v_lshl_add_u64 v[180:181], v[132:133], 0, s[38:39]
	global_load_dwordx2 v[212:213], v[180:181], off
	v_mfma_f32_16x16x32_bf16 v[18:21], v[238:241], v[230:233], v[18:21]
	v_mfma_f32_16x16x32_bf16 v[22:25], v[242:245], v[230:233], v[22:25]
	v_mfma_f32_16x16x32_bf16 v[26:29], v[246:249], v[230:233], v[26:29]
	v_mfma_f32_16x16x32_bf16 v[30:33], v[250:253], v[230:233], v[30:33]
	ds_read_b128 v[230:233], v93 offset:6144
	ds_read_b128 v[160:163], v141 offset:6144
	v_lshl_add_u64 v[180:181], v[132:133], 0, s[40:41]
	global_load_dwordx2 v[214:215], v[180:181], off
	v_lshl_add_u64 v[180:181], v[132:133], 0, s[42:43]
	global_load_dwordx2 v[216:217], v[180:181], off
	v_mfma_f32_16x16x32_bf16 v[2:5], v[238:241], v[234:237], v[2:5]
	v_mfma_f32_16x16x32_bf16 v[6:9], v[242:245], v[234:237], v[6:9]
	v_mfma_f32_16x16x32_bf16 v[10:13], v[246:249], v[234:237], v[10:13]
	v_mfma_f32_16x16x32_bf16 v[14:17], v[250:253], v[234:237], v[14:17]
	ds_read_b128 v[234:237], v93 offset:8192
	s_waitcnt vmcnt(21)
	s_waitcnt lgkmcnt(0)
	s_barrier
; #define MD_GLDS_A(buf, tau) do { _Pragma("unroll") for (int i = 0; i < 5; ++i) if (amask & (1u << i)) \
;         __builtin_amdgcn_global_load_lds((const unsigned*)((const char*)HIDp + aoff[i] + (size_t)((tau) & 7) * 128), (PG8_LAS unsigned*)(MD_SA(buf) + wid * 1024 + i * 8192), 16, 0, 0); } while (0)
; #define MD_B_ISSUE(sb, tau) do { const char* kb_ = Bb + (size_t)((tau) >> 3) * 512 + (size_t)((tau) & 7) * (64 * (size_t)RB); _Pragma("unroll") for (int j = 0; j < 8; ++j) { const char* p_ = kb_ + (size_t)j * RB; \
;         asm volatile("global_load_dwordx2 %0, %1, off" : "=&v"(sb[j]) : "v"(p_) : "memory"); } } while (0)
; #define MD_B_WAIT(sb, N) asm volatile("s_waitcnt vmcnt(%8)" : "+v"(sb[0]), "+v"(sb[1]), "+v"(sb[2]), "+v"(sb[3]), "+v"(sb[4]), "+v"(sb[5]), "+v"(sb[6]), "+v"(sb[7]) : "n"(N) : "memory")
; #define MD_END(last) do { if (last) asm volatile("s_waitcnt vmcnt(0)" ::: "memory"); else asm volatile("s_waitcnt vmcnt(8)" ::: "memory"); \
;         asm volatile("s_waitcnt lgkmcnt(0)" ::: "memory"); __builtin_amdgcn_s_barrier(); asm volatile("" ::: "memory"); } while (0)
; __device__ __forceinline__ void moe_down_stream(PG8_LAS unsigned char* lds, int e, int cb0, int slot0, int nv, const bf16_t* HIDp, const float* Wd, bf16_t* Y, const float* slot_w, const int* slot_dst) {
;     ...
;     for (int t = 0; t < NT; t += 2) {
;         if (t + 2 < NT) MD_B_WAIT(s1, 8); else MD_B_WAIT(s1, 0);
;         MD_B_WRITE(s1, 1); __builtin_amdgcn_sched_barrier(0); MD_GLDS_A(1, t + 1); __builtin_amdgcn_sched_barrier(0);
;         if (t + 3 < NT) MD_B_ISSUE(s1, t + 3);
;         MD_COMPUTE(0);
;         MD_END(t + 3 >= NT);
;         if (t + 2 < NT) { MD_B_WAIT(s0, 8); MD_B_WRITE(s0, 0); __builtin_amdgcn_sched_barrier(0); MD_GLDS_A(0, t + 2); __builtin_amdgcn_sched_barrier(0); }
;         if (t + 4 < NT) MD_B_ISSUE(s0, t + 4);
;         MD_COMPUTE(1);
;         MD_END(t + 4 >= NT);
	s_mov_b32 s49, s46
	s_mov_b32 s46, s47
	s_mov_b32 s47, s48
	s_mov_b32 s48, s49
	s_add_i32 s49, s48, s74
	s_add_i32 s52, s52, 1
	s_and_b32 s54, s52, 7
	s_cmp_eq_u32 s54, 0
	s_cselect_b32 s54, s53, s32
	s_cselect_b32 s55, -1, 0
	s_add_u32 s30, s30, s54
	s_addc_u32 s31, s31, s55
	v_mfma_f32_16x16x32_bf16 v[78:81], v[142:145], v[218:221], v[78:81]
	v_mfma_f32_16x16x32_bf16 v[74:77], v[146:149], v[218:221], v[74:77]
	v_mfma_f32_16x16x32_bf16 v[70:73], v[156:159], v[218:221], v[70:73]
	v_mfma_f32_16x16x32_bf16 v[66:69], v[160:163], v[218:221], v[66:69]
	s_mov_b32 m0, s49
	s_nop 0
	global_load_lds_dwordx4 v88, s[30:31]
	v_mfma_f32_16x16x32_bf16 v[62:65], v[142:145], v[222:225], v[62:65]
	v_mfma_f32_16x16x32_bf16 v[58:61], v[146:149], v[222:225], v[58:61]
	v_mfma_f32_16x16x32_bf16 v[54:57], v[156:159], v[222:225], v[54:57]
	v_mfma_f32_16x16x32_bf16 v[50:53], v[160:163], v[222:225], v[50:53]
	s_add_i32 m0, s49, 0x2000
	s_nop 0
	global_load_lds_dwordx4 v90, s[30:31]
	v_mfma_f32_16x16x32_bf16 v[46:49], v[142:145], v[226:229], v[46:49]
	v_mfma_f32_16x16x32_bf16 v[42:45], v[146:149], v[226:229], v[42:45]
	v_mfma_f32_16x16x32_bf16 v[38:41], v[156:159], v[226:229], v[38:41]
	v_mfma_f32_16x16x32_bf16 v[34:37], v[160:163], v[226:229], v[34:37]
	s_add_i32 m0, s49, 0x4000
	s_nop 0
	global_load_lds_dwordx4 v92, s[30:31]
	v_mfma_f32_16x16x32_bf16 v[18:21], v[142:145], v[230:233], v[18:21]
	v_mfma_f32_16x16x32_bf16 v[22:25], v[146:149], v[230:233], v[22:25]
	v_mfma_f32_16x16x32_bf16 v[26:29], v[156:159], v[230:233], v[26:29]
	v_mfma_f32_16x16x32_bf16 v[30:33], v[160:163], v[230:233], v[30:33]
	s_add_i32 m0, s49, 0x6000
	s_nop 0
	global_load_lds_dwordx4 v94, s[30:31]
	v_mfma_f32_16x16x32_bf16 v[2:5], v[142:145], v[234:237], v[2:5]
	v_mfma_f32_16x16x32_bf16 v[6:9], v[146:149], v[234:237], v[6:9]
	v_mfma_f32_16x16x32_bf16 v[10:13], v[156:159], v[234:237], v[10:13]
	v_mfma_f32_16x16x32_bf16 v[14:17], v[160:163], v[234:237], v[14:17]
	s_add_i32 m0, s49, 0x8000
	s_nop 0
	global_load_lds_dwordx4 v96, s[30:31]
	v_cvt_pk_bf16_f32 v172, v98, v100
	v_cvt_pk_bf16_f32 v173, v102, v104
	v_cvt_pk_bf16_f32 v174, v106, v108
	v_cvt_pk_bf16_f32 v175, v110, v112
	v_cvt_pk_bf16_f32 v176, v99, v101
	v_cvt_pk_bf16_f32 v177, v103, v105
	v_cvt_pk_bf16_f32 v178, v107, v109
	v_cvt_pk_bf16_f32 v179, v111, v113
	ds_write_b128 v95, v[172:175] offset:0
	ds_write_b128 v95, v[176:179] offset:128
	v_add_u32_e32 v91, s46, v135
	v_add_u32_e32 v93, s46, v137
	ds_read_b128 v[238:241], v139 offset:19456
	ds_read_b128 v[242:245], v139 offset:21504
	ds_read_b128 v[246:249], v139 offset:23552
	ds_read_b128 v[250:253], v139 offset:25600
	ds_read_b128 v[218:221], v91 offset:0
	ds_read_b128 v[222:225], v91 offset:2048
	ds_read_b128 v[226:229], v91 offset:4096
	ds_read_b128 v[230:233], v91 offset:6144
	ds_read_b128 v[234:237], v91 offset:8192
	s_waitcnt lgkmcnt(0)
	v_mfma_f32_16x16x32_bf16 v[78:81], v[238:241], v[218:221], v[78:81]
	v_mfma_f32_16x16x32_bf16 v[74:77], v[242:245], v[218:221], v[74:77]
	v_mfma_f32_16x16x32_bf16 v[70:73], v[246:249], v[218:221], v[70:73]
	v_mfma_f32_16x16x32_bf16 v[66:69], v[250:253], v[218:221], v[66:69]
	ds_read_b128 v[218:221], v93 offset:0
	ds_read_b128 v[142:145], v141 offset:19456
	s_add_i32 s51, s51, 1
	s_and_b32 s54, s51, 7
	s_cmp_eq_u32 s54, 0
	s_cselect_b32 s44, s34, s35
	s_cselect_b32 s45, -1, 0
	v_lshl_add_u64 v[132:133], v[132:133], 0, s[44:45]
	global_load_dwordx2 v[98:99], v[132:133], off
	v_lshl_add_u64 v[180:181], v[132:133], 0, s[24:25]
	global_load_dwordx2 v[100:101], v[180:181], off
	v_mfma_f32_16x16x32_bf16 v[62:65], v[238:241], v[222:225], v[62:65]
	v_mfma_f32_16x16x32_bf16 v[58:61], v[242:245], v[222:225], v[58:61]
	v_mfma_f32_16x16x32_bf16 v[54:57], v[246:249], v[222:225], v[54:57]
	v_mfma_f32_16x16x32_bf16 v[50:53], v[250:253], v[222:225], v[50:53]
	ds_read_b128 v[222:225], v93 offset:2048
	ds_read_b128 v[146:149], v141 offset:21504
	v_lshl_add_u64 v[180:181], v[132:133], 0, s[26:27]
	global_load_dwordx2 v[102:103], v[180:181], off
	v_lshl_add_u64 v[180:181], v[132:133], 0, s[28:29]
	global_load_dwordx2 v[104:105], v[180:181], off
	v_mfma_f32_16x16x32_bf16 v[46:49], v[238:241], v[226:229], v[46:49]
	v_mfma_f32_16x16x32_bf16 v[42:45], v[242:245], v[226:229], v[42:45]
	v_mfma_f32_16x16x32_bf16 v[38:41], v[246:249], v[226:229], v[38:41]
	v_mfma_f32_16x16x32_bf16 v[34:37], v[250:253], v[226:229], v[34:37]
	ds_read_b128 v[226:229], v93 offset:4096
	ds_read_b128 v[156:159], v141 offset:23552
	v_lshl_add_u64 v[180:181], v[132:133], 0, s[36:37]
	global_load_dwordx2 v[106:107], v[180:181], off
	v_lshl_add_u64 v[180:181], v[132:133], 0, s[38:39]
	global_load_dwordx2 v[108:109], v[180:181], off
	v_mfma_f32_16x16x32_bf16 v[18:21], v[238:241], v[230:233], v[18:21]
	v_mfma_f32_16x16x32_bf16 v[22:25], v[242:245], v[230:233], v[22:25]
	v_mfma_f32_16x16x32_bf16 v[26:29], v[246:249], v[230:233], v[26:29]
	v_mfma_f32_16x16x32_bf16 v[30:33], v[250:253], v[230:233], v[30:33]
	ds_read_b128 v[230:233], v93 offset:6144
	ds_read_b128 v[160:163], v141 offset:25600
	v_lshl_add_u64 v[180:181], v[132:133], 0, s[40:41]
	global_load_dwordx2 v[110:111], v[180:181], off
	v_lshl_add_u64 v[180:181], v[132:133], 0, s[42:43]
	global_load_dwordx2 v[112:113], v[180:181], off
	v_mfma_f32_16x16x32_bf16 v[2:5], v[238:241], v[234:237], v[2:5]
	v_mfma_f32_16x16x32_bf16 v[6:9], v[242:245], v[234:237], v[6:9]
	v_mfma_f32_16x16x32_bf16 v[10:13], v[246:249], v[234:237], v[10:13]
	v_mfma_f32_16x16x32_bf16 v[14:17], v[250:253], v[234:237], v[14:17]
	ds_read_b128 v[234:237], v93 offset:8192
	s_waitcnt vmcnt(21)
	s_waitcnt lgkmcnt(0)
	s_barrier
; #define MD_GLDS_A(buf, tau) do { _Pragma("unroll") for (int i = 0; i < 5; ++i) if (amask & (1u << i)) \
;         __builtin_amdgcn_global_load_lds((const unsigned*)((const char*)HIDp + aoff[i] + (size_t)((tau) & 7) * 128), (PG8_LAS unsigned*)(MD_SA(buf) + wid * 1024 + i * 8192), 16, 0, 0); } while (0)
; #define MD_B_ISSUE(sb, tau) do { const char* kb_ = Bb + (size_t)((tau) >> 3) * 512 + (size_t)((tau) & 7) * (64 * (size_t)RB); _Pragma("unroll") for (int j = 0; j < 8; ++j) { const char* p_ = kb_ + (size_t)j * RB; \
;         asm volatile("global_load_dwordx2 %0, %1, off" : "=&v"(sb[j]) : "v"(p_) : "memory"); } } while (0)
; #define MD_B_WAIT(sb, N) asm volatile("s_waitcnt vmcnt(%8)" : "+v"(sb[0]), "+v"(sb[1]), "+v"(sb[2]), "+v"(sb[3]), "+v"(sb[4]), "+v"(sb[5]), "+v"(sb[6]), "+v"(sb[7]) : "n"(N) : "memory")
; #define MD_END(last) do { if (last) asm volatile("s_waitcnt vmcnt(0)" ::: "memory"); else asm volatile("s_waitcnt vmcnt(8)" ::: "memory"); \
;         asm volatile("s_waitcnt lgkmcnt(0)" ::: "memory"); __builtin_amdgcn_s_barrier(); asm volatile("" ::: "memory"); } while (0)
; __device__ __forceinline__ void moe_down_stream(PG8_LAS unsigned char* lds, int e, int cb0, int slot0, int nv, const bf16_t* HIDp, const float* Wd, bf16_t* Y, const float* slot_w, const int* slot_dst) {
;     ...
;     for (int t = 0; t < NT; t += 2) {
;         if (t + 2 < NT) MD_B_WAIT(s1, 8); else MD_B_WAIT(s1, 0);
;         MD_B_WRITE(s1, 1); __builtin_amdgcn_sched_barrier(0); MD_GLDS_A(1, t + 1); __builtin_amdgcn_sched_barrier(0);
;         if (t + 3 < NT) MD_B_ISSUE(s1, t + 3);
;         MD_COMPUTE(0);
;         MD_END(t + 3 >= NT);
;         if (t + 2 < NT) { MD_B_WAIT(s0, 8); MD_B_WRITE(s0, 0); __builtin_amdgcn_sched_barrier(0); MD_GLDS_A(0, t + 2); __builtin_amdgcn_sched_barrier(0); }
;         if (t + 4 < NT) MD_B_ISSUE(s0, t + 4);
;         MD_COMPUTE(1);
;         MD_END(t + 4 >= NT);
	s_mov_b32 s49, s46
	s_mov_b32 s46, s47
	s_mov_b32 s47, s48
	s_mov_b32 s48, s49
	s_add_i32 s49, s48, s74
	s_add_i32 s52, s52, 1
	s_and_b32 s54, s52, 7
	s_cmp_eq_u32 s54, 0
	s_cselect_b32 s54, s53, s32
	s_cselect_b32 s55, -1, 0
	s_add_u32 s30, s30, s54
	s_addc_u32 s31, s31, s55
	v_mfma_f32_16x16x32_bf16 v[78:81], v[142:145], v[218:221], v[78:81]
	v_mfma_f32_16x16x32_bf16 v[74:77], v[146:149], v[218:221], v[74:77]
	v_mfma_f32_16x16x32_bf16 v[70:73], v[156:159], v[218:221], v[70:73]
	v_mfma_f32_16x16x32_bf16 v[66:69], v[160:163], v[218:221], v[66:69]
	s_mov_b32 m0, s49
	s_nop 0
	global_load_lds_dwordx4 v88, s[30:31]
	v_mfma_f32_16x16x32_bf16 v[62:65], v[142:145], v[222:225], v[62:65]
	v_mfma_f32_16x16x32_bf16 v[58:61], v[146:149], v[222:225], v[58:61]
	v_mfma_f32_16x16x32_bf16 v[54:57], v[156:159], v[222:225], v[54:57]
	v_mfma_f32_16x16x32_bf16 v[50:53], v[160:163], v[222:225], v[50:53]
	s_add_i32 m0, s49, 0x2000
	s_nop 0
	global_load_lds_dwordx4 v90, s[30:31]
	v_mfma_f32_16x16x32_bf16 v[46:49], v[142:145], v[226:229], v[46:49]
	v_mfma_f32_16x16x32_bf16 v[42:45], v[146:149], v[226:229], v[42:45]
	v_mfma_f32_16x16x32_bf16 v[38:41], v[156:159], v[226:229], v[38:41]
	v_mfma_f32_16x16x32_bf16 v[34:37], v[160:163], v[226:229], v[34:37]
	s_add_i32 m0, s49, 0x4000
	s_nop 0
	global_load_lds_dwordx4 v92, s[30:31]
	v_mfma_f32_16x16x32_bf16 v[18:21], v[142:145], v[230:233], v[18:21]
	v_mfma_f32_16x16x32_bf16 v[22:25], v[146:149], v[230:233], v[22:25]
	v_mfma_f32_16x16x32_bf16 v[26:29], v[156:159], v[230:233], v[26:29]
	v_mfma_f32_16x16x32_bf16 v[30:33], v[160:163], v[230:233], v[30:33]
	s_add_i32 m0, s49, 0x6000
	s_nop 0
	global_load_lds_dwordx4 v94, s[30:31]
	v_mfma_f32_16x16x32_bf16 v[2:5], v[142:145], v[234:237], v[2:5]
	v_mfma_f32_16x16x32_bf16 v[6:9], v[146:149], v[234:237], v[6:9]
	v_mfma_f32_16x16x32_bf16 v[10:13], v[156:159], v[234:237], v[10:13]
	v_mfma_f32_16x16x32_bf16 v[14:17], v[160:163], v[234:237], v[14:17]
	s_add_i32 m0, s49, 0x8000
	s_nop 0
	global_load_lds_dwordx4 v96, s[30:31]
	v_cvt_pk_bf16_f32 v172, v114, v116
	v_cvt_pk_bf16_f32 v173, v118, v120
	v_cvt_pk_bf16_f32 v174, v122, v124
	v_cvt_pk_bf16_f32 v175, v126, v128
	v_cvt_pk_bf16_f32 v176, v115, v117
	v_cvt_pk_bf16_f32 v177, v119, v121
	v_cvt_pk_bf16_f32 v178, v123, v125
	v_cvt_pk_bf16_f32 v179, v127, v129
	ds_write_b128 v95, v[172:175] offset:19456
	ds_write_b128 v95, v[176:179] offset:19584
	v_add_u32_e32 v91, s46, v135
	v_add_u32_e32 v93, s46, v137
	ds_read_b128 v[238:241], v139 offset:0
	ds_read_b128 v[242:245], v139 offset:2048
	ds_read_b128 v[246:249], v139 offset:4096
	ds_read_b128 v[250:253], v139 offset:6144
	ds_read_b128 v[218:221], v91 offset:0
	ds_read_b128 v[222:225], v91 offset:2048
	ds_read_b128 v[226:229], v91 offset:4096
	ds_read_b128 v[230:233], v91 offset:6144
	ds_read_b128 v[234:237], v91 offset:8192
	s_waitcnt lgkmcnt(0)
	v_mfma_f32_16x16x32_bf16 v[78:81], v[238:241], v[218:221], v[78:81]
	v_mfma_f32_16x16x32_bf16 v[74:77], v[242:245], v[218:221], v[74:77]
	v_mfma_f32_16x16x32_bf16 v[70:73], v[246:249], v[218:221], v[70:73]
	v_mfma_f32_16x16x32_bf16 v[66:69], v[250:253], v[218:221], v[66:69]
	ds_read_b128 v[218:221], v93 offset:0
	ds_read_b128 v[142:145], v141 offset:0
	s_add_i32 s51, s51, 1
	s_and_b32 s54, s51, 7
	s_cmp_eq_u32 s54, 0
	s_cselect_b32 s44, s34, s35
	s_cselect_b32 s45, -1, 0
	v_lshl_add_u64 v[132:133], v[132:133], 0, s[44:45]
	global_load_dwordx2 v[114:115], v[132:133], off
	v_lshl_add_u64 v[180:181], v[132:133], 0, s[24:25]
	global_load_dwordx2 v[116:117], v[180:181], off
	v_mfma_f32_16x16x32_bf16 v[62:65], v[238:241], v[222:225], v[62:65]
	v_mfma_f32_16x16x32_bf16 v[58:61], v[242:245], v[222:225], v[58:61]
	v_mfma_f32_16x16x32_bf16 v[54:57], v[246:249], v[222:225], v[54:57]
	v_mfma_f32_16x16x32_bf16 v[50:53], v[250:253], v[222:225], v[50:53]
	ds_read_b128 v[222:225], v93 offset:2048
	ds_read_b128 v[146:149], v141 offset:2048
	v_lshl_add_u64 v[180:181], v[132:133], 0, s[26:27]
	global_load_dwordx2 v[118:119], v[180:181], off
	v_lshl_add_u64 v[180:181], v[132:133], 0, s[28:29]
	global_load_dwordx2 v[120:121], v[180:181], off
	v_mfma_f32_16x16x32_bf16 v[46:49], v[238:241], v[226:229], v[46:49]
	v_mfma_f32_16x16x32_bf16 v[42:45], v[242:245], v[226:229], v[42:45]
	v_mfma_f32_16x16x32_bf16 v[38:41], v[246:249], v[226:229], v[38:41]
	v_mfma_f32_16x16x32_bf16 v[34:37], v[250:253], v[226:229], v[34:37]
	ds_read_b128 v[226:229], v93 offset:4096
	ds_read_b128 v[156:159], v141 offset:4096
	v_lshl_add_u64 v[180:181], v[132:133], 0, s[36:37]
	global_load_dwordx2 v[122:123], v[180:181], off
	v_lshl_add_u64 v[180:181], v[132:133], 0, s[38:39]
	global_load_dwordx2 v[124:125], v[180:181], off
	v_mfma_f32_16x16x32_bf16 v[18:21], v[238:241], v[230:233], v[18:21]
	v_mfma_f32_16x16x32_bf16 v[22:25], v[242:245], v[230:233], v[22:25]
	v_mfma_f32_16x16x32_bf16 v[26:29], v[246:249], v[230:233], v[26:29]
	v_mfma_f32_16x16x32_bf16 v[30:33], v[250:253], v[230:233], v[30:33]
	ds_read_b128 v[230:233], v93 offset:6144
	ds_read_b128 v[160:163], v141 offset:6144
	v_lshl_add_u64 v[180:181], v[132:133], 0, s[40:41]
	global_load_dwordx2 v[126:127], v[180:181], off
	v_lshl_add_u64 v[180:181], v[132:133], 0, s[42:43]
	global_load_dwordx2 v[128:129], v[180:181], off
	v_mfma_f32_16x16x32_bf16 v[2:5], v[238:241], v[234:237], v[2:5]
	v_mfma_f32_16x16x32_bf16 v[6:9], v[242:245], v[234:237], v[6:9]
	v_mfma_f32_16x16x32_bf16 v[10:13], v[246:249], v[234:237], v[10:13]
	v_mfma_f32_16x16x32_bf16 v[14:17], v[250:253], v[234:237], v[14:17]
	ds_read_b128 v[234:237], v93 offset:8192
	s_waitcnt vmcnt(21)
	s_waitcnt lgkmcnt(0)
	s_barrier
; #define MD_GLDS_A(buf, tau) do { _Pragma("unroll") for (int i = 0; i < 5; ++i) if (amask & (1u << i)) \
;         __builtin_amdgcn_global_load_lds((const unsigned*)((const char*)HIDp + aoff[i] + (size_t)((tau) & 7) * 128), (PG8_LAS unsigned*)(MD_SA(buf) + wid * 1024 + i * 8192), 16, 0, 0); } while (0)
; #define MD_B_ISSUE(sb, tau) do { const char* kb_ = Bb + (size_t)((tau) >> 3) * 512 + (size_t)((tau) & 7) * (64 * (size_t)RB); _Pragma("unroll") for (int j = 0; j < 8; ++j) { const char* p_ = kb_ + (size_t)j * RB; \
;         asm volatile("global_load_dwordx2 %0, %1, off" : "=&v"(sb[j]) : "v"(p_) : "memory"); } } while (0)
; #define MD_B_WAIT(sb, N) asm volatile("s_waitcnt vmcnt(%8)" : "+v"(sb[0]), "+v"(sb[1]), "+v"(sb[2]), "+v"(sb[3]), "+v"(sb[4]), "+v"(sb[5]), "+v"(sb[6]), "+v"(sb[7]) : "n"(N) : "memory")
; #define MD_END(last) do { if (last) asm volatile("s_waitcnt vmcnt(0)" ::: "memory"); else asm volatile("s_waitcnt vmcnt(8)" ::: "memory"); \
;         asm volatile("s_waitcnt lgkmcnt(0)" ::: "memory"); __builtin_amdgcn_s_barrier(); asm volatile("" ::: "memory"); } while (0)
; __device__ __forceinline__ void moe_down_stream(PG8_LAS unsigned char* lds, int e, int cb0, int slot0, int nv, const bf16_t* HIDp, const float* Wd, bf16_t* Y, const float* slot_w, const int* slot_dst) {
;     ...
;     for (int t = 0; t < NT; t += 2) {
;         if (t + 2 < NT) MD_B_WAIT(s1, 8); else MD_B_WAIT(s1, 0);
;         MD_B_WRITE(s1, 1); __builtin_amdgcn_sched_barrier(0); MD_GLDS_A(1, t + 1); __builtin_amdgcn_sched_barrier(0);
;         if (t + 3 < NT) MD_B_ISSUE(s1, t + 3);
;         MD_COMPUTE(0);
;         MD_END(t + 3 >= NT);
;         if (t + 2 < NT) { MD_B_WAIT(s0, 8); MD_B_WRITE(s0, 0); __builtin_amdgcn_sched_barrier(0); MD_GLDS_A(0, t + 2); __builtin_amdgcn_sched_barrier(0); }
;         if (t + 4 < NT) MD_B_ISSUE(s0, t + 4);
;         MD_COMPUTE(1);
;         MD_END(t + 4 >= NT);
	s_mov_b32 s49, s46
	s_mov_b32 s46, s47
	s_mov_b32 s47, s48
	s_mov_b32 s48, s49
	s_add_i32 s49, s48, s74
	s_add_i32 s52, s52, 1
	s_and_b32 s54, s52, 7
	s_cmp_eq_u32 s54, 0
	s_cselect_b32 s54, s53, s32
	s_cselect_b32 s55, -1, 0
	s_add_u32 s30, s30, s54
	s_addc_u32 s31, s31, s55
	v_mfma_f32_16x16x32_bf16 v[78:81], v[142:145], v[218:221], v[78:81]
	v_mfma_f32_16x16x32_bf16 v[74:77], v[146:149], v[218:221], v[74:77]
	v_mfma_f32_16x16x32_bf16 v[70:73], v[156:159], v[218:221], v[70:73]
	v_mfma_f32_16x16x32_bf16 v[66:69], v[160:163], v[218:221], v[66:69]
	s_mov_b32 m0, s49
	s_nop 0
	global_load_lds_dwordx4 v88, s[30:31]
	v_mfma_f32_16x16x32_bf16 v[62:65], v[142:145], v[222:225], v[62:65]
	v_mfma_f32_16x16x32_bf16 v[58:61], v[146:149], v[222:225], v[58:61]
	v_mfma_f32_16x16x32_bf16 v[54:57], v[156:159], v[222:225], v[54:57]
	v_mfma_f32_16x16x32_bf16 v[50:53], v[160:163], v[222:225], v[50:53]
	s_add_i32 m0, s49, 0x2000
	s_nop 0
	global_load_lds_dwordx4 v90, s[30:31]
	v_mfma_f32_16x16x32_bf16 v[46:49], v[142:145], v[226:229], v[46:49]
	v_mfma_f32_16x16x32_bf16 v[42:45], v[146:149], v[226:229], v[42:45]
	v_mfma_f32_16x16x32_bf16 v[38:41], v[156:159], v[226:229], v[38:41]
	v_mfma_f32_16x16x32_bf16 v[34:37], v[160:163], v[226:229], v[34:37]
	s_add_i32 m0, s49, 0x4000
	s_nop 0
	global_load_lds_dwordx4 v92, s[30:31]
	v_mfma_f32_16x16x32_bf16 v[18:21], v[142:145], v[230:233], v[18:21]
	v_mfma_f32_16x16x32_bf16 v[22:25], v[146:149], v[230:233], v[22:25]
	v_mfma_f32_16x16x32_bf16 v[26:29], v[156:159], v[230:233], v[26:29]
	v_mfma_f32_16x16x32_bf16 v[30:33], v[160:163], v[230:233], v[30:33]
	s_add_i32 m0, s49, 0x6000
	s_nop 0
	global_load_lds_dwordx4 v94, s[30:31]
	v_mfma_f32_16x16x32_bf16 v[2:5], v[142:145], v[234:237], v[2:5]
	v_mfma_f32_16x16x32_bf16 v[6:9], v[146:149], v[234:237], v[6:9]
	v_mfma_f32_16x16x32_bf16 v[10:13], v[156:159], v[234:237], v[10:13]
	v_mfma_f32_16x16x32_bf16 v[14:17], v[160:163], v[234:237], v[14:17]
	s_add_i32 m0, s49, 0x8000
	s_nop 0
	global_load_lds_dwordx4 v96, s[30:31]
	v_cvt_pk_bf16_f32 v172, v186, v188
	v_cvt_pk_bf16_f32 v173, v190, v192
	v_cvt_pk_bf16_f32 v174, v194, v196
	v_cvt_pk_bf16_f32 v175, v198, v200
	v_cvt_pk_bf16_f32 v176, v187, v189
	v_cvt_pk_bf16_f32 v177, v191, v193
	v_cvt_pk_bf16_f32 v178, v195, v197
	v_cvt_pk_bf16_f32 v179, v199, v201
	ds_write_b128 v95, v[172:175] offset:0
	ds_write_b128 v95, v[176:179] offset:128
	v_add_u32_e32 v91, s46, v135
	v_add_u32_e32 v93, s46, v137
	ds_read_b128 v[238:241], v139 offset:19456
	ds_read_b128 v[242:245], v139 offset:21504
	ds_read_b128 v[246:249], v139 offset:23552
	ds_read_b128 v[250:253], v139 offset:25600
	ds_read_b128 v[218:221], v91 offset:0
	ds_read_b128 v[222:225], v91 offset:2048
	ds_read_b128 v[226:229], v91 offset:4096
	ds_read_b128 v[230:233], v91 offset:6144
	ds_read_b128 v[234:237], v91 offset:8192
	s_waitcnt lgkmcnt(0)
	v_mfma_f32_16x16x32_bf16 v[78:81], v[238:241], v[218:221], v[78:81]
	v_mfma_f32_16x16x32_bf16 v[74:77], v[242:245], v[218:221], v[74:77]
	v_mfma_f32_16x16x32_bf16 v[70:73], v[246:249], v[218:221], v[70:73]
	v_mfma_f32_16x16x32_bf16 v[66:69], v[250:253], v[218:221], v[66:69]
	ds_read_b128 v[218:221], v93 offset:0
	ds_read_b128 v[142:145], v141 offset:19456
	s_add_i32 s51, s51, 1
	s_and_b32 s54, s51, 7
	s_cmp_eq_u32 s54, 0
	s_cselect_b32 s44, s34, s35
	s_cselect_b32 s45, -1, 0
	v_lshl_add_u64 v[132:133], v[132:133], 0, s[44:45]
	global_load_dwordx2 v[186:187], v[132:133], off
	v_lshl_add_u64 v[180:181], v[132:133], 0, s[24:25]
	global_load_dwordx2 v[188:189], v[180:181], off
	v_mfma_f32_16x16x32_bf16 v[62:65], v[238:241], v[222:225], v[62:65]
	v_mfma_f32_16x16x32_bf16 v[58:61], v[242:245], v[222:225], v[58:61]
	v_mfma_f32_16x16x32_bf16 v[54:57], v[246:249], v[222:225], v[54:57]
	v_mfma_f32_16x16x32_bf16 v[50:53], v[250:253], v[222:225], v[50:53]
	ds_read_b128 v[222:225], v93 offset:2048
	ds_read_b128 v[146:149], v141 offset:21504
	v_lshl_add_u64 v[180:181], v[132:133], 0, s[26:27]
	global_load_dwordx2 v[190:191], v[180:181], off
	v_lshl_add_u64 v[180:181], v[132:133], 0, s[28:29]
	global_load_dwordx2 v[192:193], v[180:181], off
	v_mfma_f32_16x16x32_bf16 v[46:49], v[238:241], v[226:229], v[46:49]
	v_mfma_f32_16x16x32_bf16 v[42:45], v[242:245], v[226:229], v[42:45]
	v_mfma_f32_16x16x32_bf16 v[38:41], v[246:249], v[226:229], v[38:41]
	v_mfma_f32_16x16x32_bf16 v[34:37], v[250:253], v[226:229], v[34:37]
	ds_read_b128 v[226:229], v93 offset:4096
	ds_read_b128 v[156:159], v141 offset:23552
	v_lshl_add_u64 v[180:181], v[132:133], 0, s[36:37]
	global_load_dwordx2 v[194:195], v[180:181], off
	v_lshl_add_u64 v[180:181], v[132:133], 0, s[38:39]
	global_load_dwordx2 v[196:197], v[180:181], off
	v_mfma_f32_16x16x32_bf16 v[18:21], v[238:241], v[230:233], v[18:21]
	v_mfma_f32_16x16x32_bf16 v[22:25], v[242:245], v[230:233], v[22:25]
	v_mfma_f32_16x16x32_bf16 v[26:29], v[246:249], v[230:233], v[26:29]
	v_mfma_f32_16x16x32_bf16 v[30:33], v[250:253], v[230:233], v[30:33]
	ds_read_b128 v[230:233], v93 offset:6144
	ds_read_b128 v[160:163], v141 offset:25600
	v_lshl_add_u64 v[180:181], v[132:133], 0, s[40:41]
	global_load_dwordx2 v[198:199], v[180:181], off
	v_lshl_add_u64 v[180:181], v[132:133], 0, s[42:43]
	global_load_dwordx2 v[200:201], v[180:181], off
	v_mfma_f32_16x16x32_bf16 v[2:5], v[238:241], v[234:237], v[2:5]
	v_mfma_f32_16x16x32_bf16 v[6:9], v[242:245], v[234:237], v[6:9]
	v_mfma_f32_16x16x32_bf16 v[10:13], v[246:249], v[234:237], v[10:13]
	v_mfma_f32_16x16x32_bf16 v[14:17], v[250:253], v[234:237], v[14:17]
	ds_read_b128 v[234:237], v93 offset:8192
	s_waitcnt vmcnt(21)
	s_waitcnt lgkmcnt(0)
	s_barrier
; #define MD_GLDS_A(buf, tau) do { _Pragma("unroll") for (int i = 0; i < 5; ++i) if (amask & (1u << i)) \
;         __builtin_amdgcn_global_load_lds((const unsigned*)((const char*)HIDp + aoff[i] + (size_t)((tau) & 7) * 128), (PG8_LAS unsigned*)(MD_SA(buf) + wid * 1024 + i * 8192), 16, 0, 0); } while (0)
; #define MD_B_ISSUE(sb, tau) do { const char* kb_ = Bb + (size_t)((tau) >> 3) * 512 + (size_t)((tau) & 7) * (64 * (size_t)RB); _Pragma("unroll") for (int j = 0; j < 8; ++j) { const char* p_ = kb_ + (size_t)j * RB; \
;         asm volatile("global_load_dwordx2 %0, %1, off" : "=&v"(sb[j]) : "v"(p_) : "memory"); } } while (0)
; #define MD_B_WAIT(sb, N) asm volatile("s_waitcnt vmcnt(%8)" : "+v"(sb[0]), "+v"(sb[1]), "+v"(sb[2]), "+v"(sb[3]), "+v"(sb[4]), "+v"(sb[5]), "+v"(sb[6]), "+v"(sb[7]) : "n"(N) : "memory")
; #define MD_END(last) do { if (last) asm volatile("s_waitcnt vmcnt(0)" ::: "memory"); else asm volatile("s_waitcnt vmcnt(8)" ::: "memory"); \
;         asm volatile("s_waitcnt lgkmcnt(0)" ::: "memory"); __builtin_amdgcn_s_barrier(); asm volatile("" ::: "memory"); } while (0)
; __device__ __forceinline__ void moe_down_stream(PG8_LAS unsigned char* lds, int e, int cb0, int slot0, int nv, const bf16_t* HIDp, const float* Wd, bf16_t* Y, const float* slot_w, const int* slot_dst) {
;     ...
;     for (int t = 0; t < NT; t += 2) {
;         if (t + 2 < NT) MD_B_WAIT(s1, 8); else MD_B_WAIT(s1, 0);
;         MD_B_WRITE(s1, 1); __builtin_amdgcn_sched_barrier(0); MD_GLDS_A(1, t + 1); __builtin_amdgcn_sched_barrier(0);
;         if (t + 3 < NT) MD_B_ISSUE(s1, t + 3);
;         MD_COMPUTE(0);
;         MD_END(t + 3 >= NT);
;         if (t + 2 < NT) { MD_B_WAIT(s0, 8); MD_B_WRITE(s0, 0); __builtin_amdgcn_sched_barrier(0); MD_GLDS_A(0, t + 2); __builtin_amdgcn_sched_barrier(0); }
;         if (t + 4 < NT) MD_B_ISSUE(s0, t + 4);
;         MD_COMPUTE(1);
;         MD_END(t + 4 >= NT);
	s_mov_b32 s49, s46
	s_mov_b32 s46, s47
	s_mov_b32 s47, s48
	s_mov_b32 s48, s49
	s_add_i32 s49, s48, s74
	s_add_i32 s52, s52, 1
	s_and_b32 s54, s52, 7
	s_cmp_eq_u32 s54, 0
	s_cselect_b32 s54, s53, s32
	s_cselect_b32 s55, -1, 0
	s_add_u32 s30, s30, s54
	s_addc_u32 s31, s31, s55
	v_mfma_f32_16x16x32_bf16 v[78:81], v[142:145], v[218:221], v[78:81]
	v_mfma_f32_16x16x32_bf16 v[74:77], v[146:149], v[218:221], v[74:77]
	v_mfma_f32_16x16x32_bf16 v[70:73], v[156:159], v[218:221], v[70:73]
	v_mfma_f32_16x16x32_bf16 v[66:69], v[160:163], v[218:221], v[66:69]
	s_mov_b32 m0, s49
	s_nop 0
	global_load_lds_dwordx4 v88, s[30:31]
	v_mfma_f32_16x16x32_bf16 v[62:65], v[142:145], v[222:225], v[62:65]
	v_mfma_f32_16x16x32_bf16 v[58:61], v[146:149], v[222:225], v[58:61]
	v_mfma_f32_16x16x32_bf16 v[54:57], v[156:159], v[222:225], v[54:57]
	v_mfma_f32_16x16x32_bf16 v[50:53], v[160:163], v[222:225], v[50:53]
	s_add_i32 m0, s49, 0x2000
	s_nop 0
	global_load_lds_dwordx4 v90, s[30:31]
	v_mfma_f32_16x16x32_bf16 v[46:49], v[142:145], v[226:229], v[46:49]
	v_mfma_f32_16x16x32_bf16 v[42:45], v[146:149], v[226:229], v[42:45]
	v_mfma_f32_16x16x32_bf16 v[38:41], v[156:159], v[226:229], v[38:41]
	v_mfma_f32_16x16x32_bf16 v[34:37], v[160:163], v[226:229], v[34:37]
	s_add_i32 m0, s49, 0x4000
	s_nop 0
	global_load_lds_dwordx4 v92, s[30:31]
	v_mfma_f32_16x16x32_bf16 v[18:21], v[142:145], v[230:233], v[18:21]
	v_mfma_f32_16x16x32_bf16 v[22:25], v[146:149], v[230:233], v[22:25]
	v_mfma_f32_16x16x32_bf16 v[26:29], v[156:159], v[230:233], v[26:29]
	v_mfma_f32_16x16x32_bf16 v[30:33], v[160:163], v[230:233], v[30:33]
	s_add_i32 m0, s49, 0x6000
	s_nop 0
	global_load_lds_dwordx4 v94, s[30:31]
	v_mfma_f32_16x16x32_bf16 v[2:5], v[142:145], v[234:237], v[2:5]
	v_mfma_f32_16x16x32_bf16 v[6:9], v[146:149], v[234:237], v[6:9]
	v_mfma_f32_16x16x32_bf16 v[10:13], v[156:159], v[234:237], v[10:13]
	v_mfma_f32_16x16x32_bf16 v[14:17], v[160:163], v[234:237], v[14:17]
	s_add_i32 m0, s49, 0x8000
	s_nop 0
	global_load_lds_dwordx4 v96, s[30:31]
	v_cvt_pk_bf16_f32 v172, v202, v204
	v_cvt_pk_bf16_f32 v173, v206, v208
	v_cvt_pk_bf16_f32 v174, v210, v212
	v_cvt_pk_bf16_f32 v175, v214, v216
	v_cvt_pk_bf16_f32 v176, v203, v205
	v_cvt_pk_bf16_f32 v177, v207, v209
	v_cvt_pk_bf16_f32 v178, v211, v213
	v_cvt_pk_bf16_f32 v179, v215, v217
	ds_write_b128 v95, v[172:175] offset:19456
	ds_write_b128 v95, v[176:179] offset:19584
	v_add_u32_e32 v91, s46, v135
	v_add_u32_e32 v93, s46, v137
	ds_read_b128 v[238:241], v139 offset:0
	ds_read_b128 v[242:245], v139 offset:2048
	ds_read_b128 v[246:249], v139 offset:4096
	ds_read_b128 v[250:253], v139 offset:6144
	ds_read_b128 v[218:221], v91 offset:0
	ds_read_b128 v[222:225], v91 offset:2048
	ds_read_b128 v[226:229], v91 offset:4096
	ds_read_b128 v[230:233], v91 offset:6144
	ds_read_b128 v[234:237], v91 offset:8192
	s_waitcnt lgkmcnt(0)
	v_mfma_f32_16x16x32_bf16 v[78:81], v[238:241], v[218:221], v[78:81]
	v_mfma_f32_16x16x32_bf16 v[74:77], v[242:245], v[218:221], v[74:77]
	v_mfma_f32_16x16x32_bf16 v[70:73], v[246:249], v[218:221], v[70:73]
	v_mfma_f32_16x16x32_bf16 v[66:69], v[250:253], v[218:221], v[66:69]
	ds_read_b128 v[218:221], v93 offset:0
	ds_read_b128 v[142:145], v141 offset:0
	s_add_i32 s51, s51, 1
	s_and_b32 s54, s51, 7
	s_cmp_eq_u32 s54, 0
	s_cselect_b32 s44, s34, s35
	s_cselect_b32 s45, -1, 0
	v_lshl_add_u64 v[132:133], v[132:133], 0, s[44:45]
	global_load_dwordx2 v[202:203], v[132:133], off
	v_lshl_add_u64 v[180:181], v[132:133], 0, s[24:25]
	global_load_dwordx2 v[204:205], v[180:181], off
	v_mfma_f32_16x16x32_bf16 v[62:65], v[238:241], v[222:225], v[62:65]
	v_mfma_f32_16x16x32_bf16 v[58:61], v[242:245], v[222:225], v[58:61]
	v_mfma_f32_16x16x32_bf16 v[54:57], v[246:249], v[222:225], v[54:57]
	v_mfma_f32_16x16x32_bf16 v[50:53], v[250:253], v[222:225], v[50:53]
	ds_read_b128 v[222:225], v93 offset:2048
	ds_read_b128 v[146:149], v141 offset:2048
	v_lshl_add_u64 v[180:181], v[132:133], 0, s[26:27]
	global_load_dwordx2 v[206:207], v[180:181], off
	v_lshl_add_u64 v[180:181], v[132:133], 0, s[28:29]
	global_load_dwordx2 v[208:209], v[180:181], off
	v_mfma_f32_16x16x32_bf16 v[46:49], v[238:241], v[226:229], v[46:49]
	v_mfma_f32_16x16x32_bf16 v[42:45], v[242:245], v[226:229], v[42:45]
	v_mfma_f32_16x16x32_bf16 v[38:41], v[246:249], v[226:229], v[38:41]
	v_mfma_f32_16x16x32_bf16 v[34:37], v[250:253], v[226:229], v[34:37]
	ds_read_b128 v[226:229], v93 offset:4096
	ds_read_b128 v[156:159], v141 offset:4096
	v_lshl_add_u64 v[180:181], v[132:133], 0, s[36:37]
	global_load_dwordx2 v[210:211], v[180:181], off
	v_lshl_add_u64 v[180:181], v[132:133], 0, s[38:39]
	global_load_dwordx2 v[212:213], v[180:181], off
	v_mfma_f32_16x16x32_bf16 v[18:21], v[238:241], v[230:233], v[18:21]
	v_mfma_f32_16x16x32_bf16 v[22:25], v[242:245], v[230:233], v[22:25]
	v_mfma_f32_16x16x32_bf16 v[26:29], v[246:249], v[230:233], v[26:29]
	v_mfma_f32_16x16x32_bf16 v[30:33], v[250:253], v[230:233], v[30:33]
	ds_read_b128 v[230:233], v93 offset:6144
	ds_read_b128 v[160:163], v141 offset:6144
	v_lshl_add_u64 v[180:181], v[132:133], 0, s[40:41]
	global_load_dwordx2 v[214:215], v[180:181], off
	v_lshl_add_u64 v[180:181], v[132:133], 0, s[42:43]
	global_load_dwordx2 v[216:217], v[180:181], off
	v_mfma_f32_16x16x32_bf16 v[2:5], v[238:241], v[234:237], v[2:5]
	v_mfma_f32_16x16x32_bf16 v[6:9], v[242:245], v[234:237], v[6:9]
	v_mfma_f32_16x16x32_bf16 v[10:13], v[246:249], v[234:237], v[10:13]
	v_mfma_f32_16x16x32_bf16 v[14:17], v[250:253], v[234:237], v[14:17]
	ds_read_b128 v[234:237], v93 offset:8192
	s_waitcnt vmcnt(21)
	s_waitcnt lgkmcnt(0)
	s_barrier
; #define MD_GLDS_A(buf, tau) do { _Pragma("unroll") for (int i = 0; i < 5; ++i) if (amask & (1u << i)) \
;         __builtin_amdgcn_global_load_lds((const unsigned*)((const char*)HIDp + aoff[i] + (size_t)((tau) & 7) * 128), (PG8_LAS unsigned*)(MD_SA(buf) + wid * 1024 + i * 8192), 16, 0, 0); } while (0)
; #define MD_B_ISSUE(sb, tau) do { const char* kb_ = Bb + (size_t)((tau) >> 3) * 512 + (size_t)((tau) & 7) * (64 * (size_t)RB); _Pragma("unroll") for (int j = 0; j < 8; ++j) { const char* p_ = kb_ + (size_t)j * RB; \
;         asm volatile("global_load_dwordx2 %0, %1, off" : "=&v"(sb[j]) : "v"(p_) : "memory"); } } while (0)
; #define MD_B_WAIT(sb, N) asm volatile("s_waitcnt vmcnt(%8)" : "+v"(sb[0]), "+v"(sb[1]), "+v"(sb[2]), "+v"(sb[3]), "+v"(sb[4]), "+v"(sb[5]), "+v"(sb[6]), "+v"(sb[7]) : "n"(N) : "memory")
; #define MD_END(last) do { if (last) asm volatile("s_waitcnt vmcnt(0)" ::: "memory"); else asm volatile("s_waitcnt vmcnt(8)" ::: "memory"); \
;         asm volatile("s_waitcnt lgkmcnt(0)" ::: "memory"); __builtin_amdgcn_s_barrier(); asm volatile("" ::: "memory"); } while (0)
; __device__ __forceinline__ void moe_down_stream(PG8_LAS unsigned char* lds, int e, int cb0, int slot0, int nv, const bf16_t* HIDp, const float* Wd, bf16_t* Y, const float* slot_w, const int* slot_dst) {
;     ...
;     for (int t = 0; t < NT; t += 2) {
;         if (t + 2 < NT) MD_B_WAIT(s1, 8); else MD_B_WAIT(s1, 0);
;         MD_B_WRITE(s1, 1); __builtin_amdgcn_sched_barrier(0); MD_GLDS_A(1, t + 1); __builtin_amdgcn_sched_barrier(0);
;         if (t + 3 < NT) MD_B_ISSUE(s1, t + 3);
;         MD_COMPUTE(0);
;         MD_END(t + 3 >= NT);
;         if (t + 2 < NT) { MD_B_WAIT(s0, 8); MD_B_WRITE(s0, 0); __builtin_amdgcn_sched_barrier(0); MD_GLDS_A(0, t + 2); __builtin_amdgcn_sched_barrier(0); }
;         if (t + 4 < NT) MD_B_ISSUE(s0, t + 4);
;         MD_COMPUTE(1);
;         MD_END(t + 4 >= NT);
	s_mov_b32 s49, s46
	s_mov_b32 s46, s47
	s_mov_b32 s47, s48
	s_mov_b32 s48, s49
	s_add_i32 s49, s48, s74
	s_add_i32 s52, s52, 1
	s_and_b32 s54, s52, 7
	s_cmp_eq_u32 s54, 0
	s_cselect_b32 s54, s53, s32
	s_cselect_b32 s55, -1, 0
	s_add_u32 s30, s30, s54
	s_addc_u32 s31, s31, s55
	v_mfma_f32_16x16x32_bf16 v[78:81], v[142:145], v[218:221], v[78:81]
	v_mfma_f32_16x16x32_bf16 v[74:77], v[146:149], v[218:221], v[74:77]
	v_mfma_f32_16x16x32_bf16 v[70:73], v[156:159], v[218:221], v[70:73]
	v_mfma_f32_16x16x32_bf16 v[66:69], v[160:163], v[218:221], v[66:69]
	s_mov_b32 m0, s49
	s_nop 0
	global_load_lds_dwordx4 v88, s[30:31]
	v_mfma_f32_16x16x32_bf16 v[62:65], v[142:145], v[222:225], v[62:65]
	v_mfma_f32_16x16x32_bf16 v[58:61], v[146:149], v[222:225], v[58:61]
	v_mfma_f32_16x16x32_bf16 v[54:57], v[156:159], v[222:225], v[54:57]
	v_mfma_f32_16x16x32_bf16 v[50:53], v[160:163], v[222:225], v[50:53]
	s_add_i32 m0, s49, 0x2000
	s_nop 0
	global_load_lds_dwordx4 v90, s[30:31]
	v_mfma_f32_16x16x32_bf16 v[46:49], v[142:145], v[226:229], v[46:49]
	v_mfma_f32_16x16x32_bf16 v[42:45], v[146:149], v[226:229], v[42:45]
	v_mfma_f32_16x16x32_bf16 v[38:41], v[156:159], v[226:229], v[38:41]
	v_mfma_f32_16x16x32_bf16 v[34:37], v[160:163], v[226:229], v[34:37]
	s_add_i32 m0, s49, 0x4000
	s_nop 0
	global_load_lds_dwordx4 v92, s[30:31]
	v_mfma_f32_16x16x32_bf16 v[18:21], v[142:145], v[230:233], v[18:21]
	v_mfma_f32_16x16x32_bf16 v[22:25], v[146:149], v[230:233], v[22:25]
	v_mfma_f32_16x16x32_bf16 v[26:29], v[156:159], v[230:233], v[26:29]
	v_mfma_f32_16x16x32_bf16 v[30:33], v[160:163], v[230:233], v[30:33]
	s_add_i32 m0, s49, 0x6000
	s_nop 0
	global_load_lds_dwordx4 v94, s[30:31]
	v_mfma_f32_16x16x32_bf16 v[2:5], v[142:145], v[234:237], v[2:5]
	v_mfma_f32_16x16x32_bf16 v[6:9], v[146:149], v[234:237], v[6:9]
	v_mfma_f32_16x16x32_bf16 v[10:13], v[156:159], v[234:237], v[10:13]
	v_mfma_f32_16x16x32_bf16 v[14:17], v[160:163], v[234:237], v[14:17]
	s_add_i32 m0, s49, 0x8000
	s_nop 0
	global_load_lds_dwordx4 v96, s[30:31]
	v_cvt_pk_bf16_f32 v172, v98, v100
	v_cvt_pk_bf16_f32 v173, v102, v104
	v_cvt_pk_bf16_f32 v174, v106, v108
	v_cvt_pk_bf16_f32 v175, v110, v112
	v_cvt_pk_bf16_f32 v176, v99, v101
	v_cvt_pk_bf16_f32 v177, v103, v105
	v_cvt_pk_bf16_f32 v178, v107, v109
	v_cvt_pk_bf16_f32 v179, v111, v113
	ds_write_b128 v95, v[172:175] offset:0
	ds_write_b128 v95, v[176:179] offset:128
	v_add_u32_e32 v91, s46, v135
	v_add_u32_e32 v93, s46, v137
	ds_read_b128 v[238:241], v139 offset:19456
	ds_read_b128 v[242:245], v139 offset:21504
	ds_read_b128 v[246:249], v139 offset:23552
	ds_read_b128 v[250:253], v139 offset:25600
	ds_read_b128 v[218:221], v91 offset:0
	ds_read_b128 v[222:225], v91 offset:2048
	ds_read_b128 v[226:229], v91 offset:4096
	ds_read_b128 v[230:233], v91 offset:6144
	ds_read_b128 v[234:237], v91 offset:8192
	s_waitcnt lgkmcnt(0)
	v_mfma_f32_16x16x32_bf16 v[78:81], v[238:241], v[218:221], v[78:81]
	v_mfma_f32_16x16x32_bf16 v[74:77], v[242:245], v[218:221], v[74:77]
	v_mfma_f32_16x16x32_bf16 v[70:73], v[246:249], v[218:221], v[70:73]
	v_mfma_f32_16x16x32_bf16 v[66:69], v[250:253], v[218:221], v[66:69]
	ds_read_b128 v[218:221], v93 offset:0
	ds_read_b128 v[142:145], v141 offset:19456
	s_add_i32 s51, s51, 1
	s_and_b32 s54, s51, 7
	s_cmp_eq_u32 s54, 0
	s_cselect_b32 s44, s34, s35
	s_cselect_b32 s45, -1, 0
	v_lshl_add_u64 v[132:133], v[132:133], 0, s[44:45]
	global_load_dwordx2 v[98:99], v[132:133], off
	v_lshl_add_u64 v[180:181], v[132:133], 0, s[24:25]
	global_load_dwordx2 v[100:101], v[180:181], off
	v_mfma_f32_16x16x32_bf16 v[62:65], v[238:241], v[222:225], v[62:65]
	v_mfma_f32_16x16x32_bf16 v[58:61], v[242:245], v[222:225], v[58:61]
	v_mfma_f32_16x16x32_bf16 v[54:57], v[246:249], v[222:225], v[54:57]
	v_mfma_f32_16x16x32_bf16 v[50:53], v[250:253], v[222:225], v[50:53]
	ds_read_b128 v[222:225], v93 offset:2048
	ds_read_b128 v[146:149], v141 offset:21504
	v_lshl_add_u64 v[180:181], v[132:133], 0, s[26:27]
	global_load_dwordx2 v[102:103], v[180:181], off
	v_lshl_add_u64 v[180:181], v[132:133], 0, s[28:29]
	global_load_dwordx2 v[104:105], v[180:181], off
	v_mfma_f32_16x16x32_bf16 v[46:49], v[238:241], v[226:229], v[46:49]
	v_mfma_f32_16x16x32_bf16 v[42:45], v[242:245], v[226:229], v[42:45]
	v_mfma_f32_16x16x32_bf16 v[38:41], v[246:249], v[226:229], v[38:41]
	v_mfma_f32_16x16x32_bf16 v[34:37], v[250:253], v[226:229], v[34:37]
	ds_read_b128 v[226:229], v93 offset:4096
	ds_read_b128 v[156:159], v141 offset:23552
	v_lshl_add_u64 v[180:181], v[132:133], 0, s[36:37]
	global_load_dwordx2 v[106:107], v[180:181], off
	v_lshl_add_u64 v[180:181], v[132:133], 0, s[38:39]
	global_load_dwordx2 v[108:109], v[180:181], off
	v_mfma_f32_16x16x32_bf16 v[18:21], v[238:241], v[230:233], v[18:21]
	v_mfma_f32_16x16x32_bf16 v[22:25], v[242:245], v[230:233], v[22:25]
	v_mfma_f32_16x16x32_bf16 v[26:29], v[246:249], v[230:233], v[26:29]
	v_mfma_f32_16x16x32_bf16 v[30:33], v[250:253], v[230:233], v[30:33]
	ds_read_b128 v[230:233], v93 offset:6144
	ds_read_b128 v[160:163], v141 offset:25600
	v_lshl_add_u64 v[180:181], v[132:133], 0, s[40:41]
	global_load_dwordx2 v[110:111], v[180:181], off
	v_lshl_add_u64 v[180:181], v[132:133], 0, s[42:43]
	global_load_dwordx2 v[112:113], v[180:181], off
	v_mfma_f32_16x16x32_bf16 v[2:5], v[238:241], v[234:237], v[2:5]
	v_mfma_f32_16x16x32_bf16 v[6:9], v[242:245], v[234:237], v[6:9]
	v_mfma_f32_16x16x32_bf16 v[10:13], v[246:249], v[234:237], v[10:13]
	v_mfma_f32_16x16x32_bf16 v[14:17], v[250:253], v[234:237], v[14:17]
	ds_read_b128 v[234:237], v93 offset:8192
	s_waitcnt vmcnt(21)
	s_waitcnt lgkmcnt(0)
	s_barrier
; #define PG8_LAS __attribute__((address_space(3)))
; __device__ __forceinline__ unsigned cvtpk(float lo, float hi) { f32x2 v = {lo, hi}; bf16x2_t b = __builtin_convertvector(v, bf16x2_t); return __builtin_bit_cast(unsigned, b); }
; __device__ __forceinline__ void moe_down_stream(PG8_LAS unsigned char* lds, int e, int cb0, int slot0, int nv, const bf16_t* HIDp, const float* Wd, bf16_t* Y, const float* slot_w, const int* slot_dst) {
;     ...
;         if (((t + 1) & 7) == 7) {
;             const int cb = cb0 + ((t + 1) >> 3);
; #pragma unroll
;             for (int m = 0; m < DNM; ++m) {
;                 const float w_ = lw[4 * (16 * m + fr) + wr];
; #pragma unroll
;                 for (int p = 0; p < 2; ++p) { const f32x4 v0 = acc[m][2 * p] * w_, v1 = acc[m][2 * p + 1] * w_; u32x4 w; w.x = cvtpk(v0[0], v0[1]); w.y = cvtpk(v0[2], v0[3]); w.z = cvtpk(v1[0], v1[1]); w.w = cvtpk(v1[2], v1[3]);
;                     *(PG8_LAS u32x4*)(stg + fr * 128 + (((4 * p + fq) ^ (fr & 7)) * 16)) = w; }
; #pragma unroll
;                 for (int hh = 0; hh < 2; ++hh) { const int r = (lane >> 3) + 8 * hh, cc = lane & 7; const u32x4 d = *(const PG8_LAS u32x4*)(stg + r * 128 + ((cc ^ (r & 7)) * 16)); const int dst_ = ldst[4 * (16 * m + r) + wr];
;                     if (dst_ >= 0) *(u32x4*)(Y + (size_t)dst_ * D + 128 * cb + 64 * wc + 8 * cc) = d; }
; #pragma unroll
;                 for (int n = 0; n < 4; ++n) acc[m][n] = (f32x4){0.f, 0.f, 0.f, 0.f}; } }
	s_mov_b32 s49, s46
	s_mov_b32 s46, s47
	s_mov_b32 s47, s48
	s_mov_b32 s48, s49
	v_mfma_f32_16x16x32_bf16 v[78:81], v[142:145], v[218:221], v[78:81]
	v_mfma_f32_16x16x32_bf16 v[74:77], v[146:149], v[218:221], v[74:77]
	v_mfma_f32_16x16x32_bf16 v[70:73], v[156:159], v[218:221], v[70:73]
	v_mfma_f32_16x16x32_bf16 v[66:69], v[160:163], v[218:221], v[66:69]
	v_mfma_f32_16x16x32_bf16 v[62:65], v[142:145], v[222:225], v[62:65]
	v_mfma_f32_16x16x32_bf16 v[58:61], v[146:149], v[222:225], v[58:61]
	v_mfma_f32_16x16x32_bf16 v[54:57], v[156:159], v[222:225], v[54:57]
	v_mfma_f32_16x16x32_bf16 v[50:53], v[160:163], v[222:225], v[50:53]
	v_mfma_f32_16x16x32_bf16 v[46:49], v[142:145], v[226:229], v[46:49]
	v_mfma_f32_16x16x32_bf16 v[42:45], v[146:149], v[226:229], v[42:45]
	v_mfma_f32_16x16x32_bf16 v[38:41], v[156:159], v[226:229], v[38:41]
	v_mfma_f32_16x16x32_bf16 v[34:37], v[160:163], v[226:229], v[34:37]
	v_mfma_f32_16x16x32_bf16 v[18:21], v[142:145], v[230:233], v[18:21]
	v_mfma_f32_16x16x32_bf16 v[22:25], v[146:149], v[230:233], v[22:25]
	v_mfma_f32_16x16x32_bf16 v[26:29], v[156:159], v[230:233], v[26:29]
	v_mfma_f32_16x16x32_bf16 v[30:33], v[160:163], v[230:233], v[30:33]
	v_mfma_f32_16x16x32_bf16 v[2:5], v[142:145], v[234:237], v[2:5]
	v_mfma_f32_16x16x32_bf16 v[6:9], v[146:149], v[234:237], v[6:9]
	v_mfma_f32_16x16x32_bf16 v[10:13], v[156:159], v[234:237], v[10:13]
	v_mfma_f32_16x16x32_bf16 v[14:17], v[160:163], v[234:237], v[14:17]
	s_add_i32 s54, s48, s74
	v_add_u32_e32 v164, s54, v84
	v_add_u32_e32 v165, s54, v85
	ds_read_b32 v150, v82 offset:0
	ds_read_b32 v151, v83 offset:0
	ds_read_b32 v166, v83 offset:128
	s_waitcnt lgkmcnt(2)
	v_mul_f32_e32 v78, v150, v78
	v_mul_f32_e32 v79, v150, v79
	v_mul_f32_e32 v80, v150, v80
	v_mul_f32_e32 v81, v150, v81
	v_mul_f32_e32 v74, v150, v74
	v_mul_f32_e32 v75, v150, v75
	v_mul_f32_e32 v76, v150, v76
	v_mul_f32_e32 v77, v150, v77
	v_cvt_pk_bf16_f32 v182, v78, v79
	v_cvt_pk_bf16_f32 v183, v80, v81
	v_cvt_pk_bf16_f32 v184, v74, v75
	v_cvt_pk_bf16_f32 v185, v76, v77
	ds_write_b128 v164, v[182:185]
	v_mul_f32_e32 v70, v150, v70
	v_mul_f32_e32 v71, v150, v71
	v_mul_f32_e32 v72, v150, v72
	v_mul_f32_e32 v73, v150, v73
	v_mul_f32_e32 v66, v150, v66
	v_mul_f32_e32 v67, v150, v67
	v_mul_f32_e32 v68, v150, v68
	v_mul_f32_e32 v69, v150, v69
	v_cvt_pk_bf16_f32 v182, v70, v71
	v_cvt_pk_bf16_f32 v183, v72, v73
	v_cvt_pk_bf16_f32 v184, v66, v67
	v_cvt_pk_bf16_f32 v185, v68, v69
	v_xor_b32_e32 v167, 64, v164
	ds_write_b128 v167, v[182:185]
	v_mov_b32_e32 v78, 0
	v_mov_b32_e32 v74, 0
	v_mov_b32_e32 v70, 0
	v_mov_b32_e32 v66, 0
	v_mov_b32_e32 v79, 0
	v_mov_b32_e32 v75, 0
	v_mov_b32_e32 v71, 0
	v_mov_b32_e32 v67, 0
	v_mov_b32_e32 v80, 0
	v_mov_b32_e32 v76, 0
	v_mov_b32_e32 v72, 0
	v_mov_b32_e32 v68, 0
	v_mov_b32_e32 v81, 0
	v_mov_b32_e32 v77, 0
	v_mov_b32_e32 v73, 0
	v_mov_b32_e32 v69, 0
	ds_read_b128 v[182:185], v165 offset:0
	v_cmp_lt_i32_e32 vcc, -1, v151
	v_lshlrev_b32_e32 v148, 13, v151
	v_mov_b32_e32 v149, 0
	v_lshl_add_u64 v[148:149], v[148:149], 0, v[86:87]
	v_cndmask_b32_e32 v148, v168, v148, vcc
	v_cndmask_b32_e32 v149, v169, v149, vcc
	s_waitcnt lgkmcnt(0)
	global_store_dwordx4 v[148:149], v[182:185], off
	ds_read_b128 v[182:185], v165 offset:8192
	v_cmp_lt_i32_e32 vcc, -1, v166
	v_lshlrev_b32_e32 v148, 13, v166
	v_mov_b32_e32 v149, 0
	v_lshl_add_u64 v[148:149], v[148:149], 0, v[86:87]
	v_cndmask_b32_e32 v148, v168, v148, vcc
	v_cndmask_b32_e32 v149, v169, v149, vcc
	s_waitcnt lgkmcnt(0)
	global_store_dwordx4 v[148:149], v[182:185], off
	ds_read_b32 v150, v82 offset:256
	ds_read_b32 v151, v83 offset:256
	ds_read_b32 v166, v83 offset:384
	s_waitcnt lgkmcnt(2)
	v_mul_f32_e32 v62, v150, v62
	v_mul_f32_e32 v63, v150, v63
	v_mul_f32_e32 v64, v150, v64
	v_mul_f32_e32 v65, v150, v65
	v_mul_f32_e32 v58, v150, v58
	v_mul_f32_e32 v59, v150, v59
	v_mul_f32_e32 v60, v150, v60
	v_mul_f32_e32 v61, v150, v61
	v_cvt_pk_bf16_f32 v182, v62, v63
	v_cvt_pk_bf16_f32 v183, v64, v65
	v_cvt_pk_bf16_f32 v184, v58, v59
	v_cvt_pk_bf16_f32 v185, v60, v61
	ds_write_b128 v164, v[182:185]
	v_mul_f32_e32 v54, v150, v54
	v_mul_f32_e32 v55, v150, v55
	v_mul_f32_e32 v56, v150, v56
	v_mul_f32_e32 v57, v150, v57
	v_mul_f32_e32 v50, v150, v50
	v_mul_f32_e32 v51, v150, v51
	v_mul_f32_e32 v52, v150, v52
	v_mul_f32_e32 v53, v150, v53
	v_cvt_pk_bf16_f32 v182, v54, v55
	v_cvt_pk_bf16_f32 v183, v56, v57
	v_cvt_pk_bf16_f32 v184, v50, v51
	v_cvt_pk_bf16_f32 v185, v52, v53
	v_xor_b32_e32 v167, 64, v164
	ds_write_b128 v167, v[182:185]
	v_mov_b32_e32 v62, 0
	v_mov_b32_e32 v58, 0
	v_mov_b32_e32 v54, 0
	v_mov_b32_e32 v50, 0
	v_mov_b32_e32 v63, 0
	v_mov_b32_e32 v59, 0
	v_mov_b32_e32 v55, 0
	v_mov_b32_e32 v51, 0
	v_mov_b32_e32 v64, 0
	v_mov_b32_e32 v60, 0
	v_mov_b32_e32 v56, 0
	v_mov_b32_e32 v52, 0
	v_mov_b32_e32 v65, 0
	v_mov_b32_e32 v61, 0
	v_mov_b32_e32 v57, 0
	v_mov_b32_e32 v53, 0
	ds_read_b128 v[182:185], v165 offset:0
	v_cmp_lt_i32_e32 vcc, -1, v151
	v_lshlrev_b32_e32 v148, 13, v151
	v_mov_b32_e32 v149, 0
	v_lshl_add_u64 v[148:149], v[148:149], 0, v[86:87]
	v_cndmask_b32_e32 v148, v168, v148, vcc
	v_cndmask_b32_e32 v149, v169, v149, vcc
	s_waitcnt lgkmcnt(0)
	global_store_dwordx4 v[148:149], v[182:185], off
	ds_read_b128 v[182:185], v165 offset:8192
	v_cmp_lt_i32_e32 vcc, -1, v166
	v_lshlrev_b32_e32 v148, 13, v166
	v_mov_b32_e32 v149, 0
	v_lshl_add_u64 v[148:149], v[148:149], 0, v[86:87]
	v_cndmask_b32_e32 v148, v168, v148, vcc
	v_cndmask_b32_e32 v149, v169, v149, vcc
	s_waitcnt lgkmcnt(0)
	global_store_dwordx4 v[148:149], v[182:185], off
	ds_read_b32 v150, v82 offset:512
	ds_read_b32 v151, v83 offset:512
	ds_read_b32 v166, v83 offset:640
	s_waitcnt lgkmcnt(2)
; #define PG8_LAS __attribute__((address_space(3)))
; __device__ __forceinline__ unsigned cvtpk(float lo, float hi) { f32x2 v = {lo, hi}; bf16x2_t b = __builtin_convertvector(v, bf16x2_t); return __builtin_bit_cast(unsigned, b); }
; __device__ __forceinline__ void moe_down_stream(PG8_LAS unsigned char* lds, int e, int cb0, int slot0, int nv, const bf16_t* HIDp, const float* Wd, bf16_t* Y, const float* slot_w, const int* slot_dst) {
;     ...
;         if (((t + 1) & 7) == 7) {
;             const int cb = cb0 + ((t + 1) >> 3);
; #pragma unroll
;             for (int m = 0; m < DNM; ++m) {
;                 const float w_ = lw[4 * (16 * m + fr) + wr];
; #pragma unroll
;                 for (int p = 0; p < 2; ++p) { const f32x4 v0 = acc[m][2 * p] * w_, v1 = acc[m][2 * p + 1] * w_; u32x4 w; w.x = cvtpk(v0[0], v0[1]); w.y = cvtpk(v0[2], v0[3]); w.z = cvtpk(v1[0], v1[1]); w.w = cvtpk(v1[2], v1[3]);
;                     *(PG8_LAS u32x4*)(stg + fr * 128 + (((4 * p + fq) ^ (fr & 7)) * 16)) = w; }
; #pragma unroll
;                 for (int hh = 0; hh < 2; ++hh) { const int r = (lane >> 3) + 8 * hh, cc = lane & 7; const u32x4 d = *(const PG8_LAS u32x4*)(stg + r * 128 + ((cc ^ (r & 7)) * 16)); const int dst_ = ldst[4 * (16 * m + r) + wr];
;                     if (dst_ >= 0) *(u32x4*)(Y + (size_t)dst_ * D + 128 * cb + 64 * wc + 8 * cc) = d; }
; #pragma unroll
;                 for (int n = 0; n < 4; ++n) acc[m][n] = (f32x4){0.f, 0.f, 0.f, 0.f}; } }
	v_mul_f32_e32 v46, v150, v46
	v_mul_f32_e32 v47, v150, v47
	v_mul_f32_e32 v48, v150, v48
	v_mul_f32_e32 v49, v150, v49
	v_mul_f32_e32 v42, v150, v42
	v_mul_f32_e32 v43, v150, v43
	v_mul_f32_e32 v44, v150, v44
	v_mul_f32_e32 v45, v150, v45
	v_cvt_pk_bf16_f32 v182, v46, v47
	v_cvt_pk_bf16_f32 v183, v48, v49
	v_cvt_pk_bf16_f32 v184, v42, v43
	v_cvt_pk_bf16_f32 v185, v44, v45
	ds_write_b128 v164, v[182:185]
	v_mul_f32_e32 v38, v150, v38
	v_mul_f32_e32 v39, v150, v39
	v_mul_f32_e32 v40, v150, v40
	v_mul_f32_e32 v41, v150, v41
	v_mul_f32_e32 v34, v150, v34
	v_mul_f32_e32 v35, v150, v35
	v_mul_f32_e32 v36, v150, v36
	v_mul_f32_e32 v37, v150, v37
	v_cvt_pk_bf16_f32 v182, v38, v39
	v_cvt_pk_bf16_f32 v183, v40, v41
	v_cvt_pk_bf16_f32 v184, v34, v35
	v_cvt_pk_bf16_f32 v185, v36, v37
	v_xor_b32_e32 v167, 64, v164
	ds_write_b128 v167, v[182:185]
	v_mov_b32_e32 v46, 0
	v_mov_b32_e32 v42, 0
	v_mov_b32_e32 v38, 0
	v_mov_b32_e32 v34, 0
	v_mov_b32_e32 v47, 0
	v_mov_b32_e32 v43, 0
	v_mov_b32_e32 v39, 0
	v_mov_b32_e32 v35, 0
	v_mov_b32_e32 v48, 0
	v_mov_b32_e32 v44, 0
	v_mov_b32_e32 v40, 0
	v_mov_b32_e32 v36, 0
	v_mov_b32_e32 v49, 0
	v_mov_b32_e32 v45, 0
	v_mov_b32_e32 v41, 0
	v_mov_b32_e32 v37, 0
	ds_read_b128 v[182:185], v165 offset:0
	v_cmp_lt_i32_e32 vcc, -1, v151
	v_lshlrev_b32_e32 v148, 13, v151
	v_mov_b32_e32 v149, 0
	v_lshl_add_u64 v[148:149], v[148:149], 0, v[86:87]
	v_cndmask_b32_e32 v148, v168, v148, vcc
	v_cndmask_b32_e32 v149, v169, v149, vcc
	s_waitcnt lgkmcnt(0)
	global_store_dwordx4 v[148:149], v[182:185], off
	ds_read_b128 v[182:185], v165 offset:8192
	v_cmp_lt_i32_e32 vcc, -1, v166
	v_lshlrev_b32_e32 v148, 13, v166
	v_mov_b32_e32 v149, 0
	v_lshl_add_u64 v[148:149], v[148:149], 0, v[86:87]
	v_cndmask_b32_e32 v148, v168, v148, vcc
	v_cndmask_b32_e32 v149, v169, v149, vcc
	s_waitcnt lgkmcnt(0)
	global_store_dwordx4 v[148:149], v[182:185], off
	ds_read_b32 v150, v82 offset:768
	ds_read_b32 v151, v83 offset:768
	ds_read_b32 v166, v83 offset:896
	s_waitcnt lgkmcnt(2)
	v_mul_f32_e32 v18, v150, v18
	v_mul_f32_e32 v19, v150, v19
	v_mul_f32_e32 v20, v150, v20
	v_mul_f32_e32 v21, v150, v21
	v_mul_f32_e32 v22, v150, v22
	v_mul_f32_e32 v23, v150, v23
	v_mul_f32_e32 v24, v150, v24
	v_mul_f32_e32 v25, v150, v25
	v_cvt_pk_bf16_f32 v182, v18, v19
	v_cvt_pk_bf16_f32 v183, v20, v21
	v_cvt_pk_bf16_f32 v184, v22, v23
	v_cvt_pk_bf16_f32 v185, v24, v25
	ds_write_b128 v164, v[182:185]
	v_mul_f32_e32 v26, v150, v26
	v_mul_f32_e32 v27, v150, v27
	v_mul_f32_e32 v28, v150, v28
	v_mul_f32_e32 v29, v150, v29
	v_mul_f32_e32 v30, v150, v30
	v_mul_f32_e32 v31, v150, v31
	v_mul_f32_e32 v32, v150, v32
	v_mul_f32_e32 v33, v150, v33
	v_cvt_pk_bf16_f32 v182, v26, v27
	v_cvt_pk_bf16_f32 v183, v28, v29
	v_cvt_pk_bf16_f32 v184, v30, v31
	v_cvt_pk_bf16_f32 v185, v32, v33
	v_xor_b32_e32 v167, 64, v164
	ds_write_b128 v167, v[182:185]
	v_mov_b32_e32 v18, 0
	v_mov_b32_e32 v22, 0
	v_mov_b32_e32 v26, 0
	v_mov_b32_e32 v30, 0
	v_mov_b32_e32 v19, 0
	v_mov_b32_e32 v23, 0
	v_mov_b32_e32 v27, 0
	v_mov_b32_e32 v31, 0
	v_mov_b32_e32 v20, 0
	v_mov_b32_e32 v24, 0
	v_mov_b32_e32 v28, 0
	v_mov_b32_e32 v32, 0
	v_mov_b32_e32 v21, 0
	v_mov_b32_e32 v25, 0
	v_mov_b32_e32 v29, 0
	v_mov_b32_e32 v33, 0
	ds_read_b128 v[182:185], v165 offset:0
	v_cmp_lt_i32_e32 vcc, -1, v151
	v_lshlrev_b32_e32 v148, 13, v151
	v_mov_b32_e32 v149, 0
	v_lshl_add_u64 v[148:149], v[148:149], 0, v[86:87]
	v_cndmask_b32_e32 v148, v168, v148, vcc
	v_cndmask_b32_e32 v149, v169, v149, vcc
	s_waitcnt lgkmcnt(0)
	global_store_dwordx4 v[148:149], v[182:185], off
	ds_read_b128 v[182:185], v165 offset:8192
	v_cmp_lt_i32_e32 vcc, -1, v166
	v_lshlrev_b32_e32 v148, 13, v166
	v_mov_b32_e32 v149, 0
	v_lshl_add_u64 v[148:149], v[148:149], 0, v[86:87]
	v_cndmask_b32_e32 v148, v168, v148, vcc
	v_cndmask_b32_e32 v149, v169, v149, vcc
	s_waitcnt lgkmcnt(0)
	global_store_dwordx4 v[148:149], v[182:185], off
	ds_read_b32 v150, v82 offset:1024
	ds_read_b32 v151, v83 offset:1024
	ds_read_b32 v166, v83 offset:1152
	s_waitcnt lgkmcnt(2)
	v_mul_f32_e32 v2, v150, v2
	v_mul_f32_e32 v3, v150, v3
	v_mul_f32_e32 v4, v150, v4
	v_mul_f32_e32 v5, v150, v5
	v_mul_f32_e32 v6, v150, v6
	v_mul_f32_e32 v7, v150, v7
	v_mul_f32_e32 v8, v150, v8
	v_mul_f32_e32 v9, v150, v9
	v_cvt_pk_bf16_f32 v182, v2, v3
	v_cvt_pk_bf16_f32 v183, v4, v5
	v_cvt_pk_bf16_f32 v184, v6, v7
	v_cvt_pk_bf16_f32 v185, v8, v9
	ds_write_b128 v164, v[182:185]
	v_mul_f32_e32 v10, v150, v10
	v_mul_f32_e32 v11, v150, v11
	v_mul_f32_e32 v12, v150, v12
	v_mul_f32_e32 v13, v150, v13
	v_mul_f32_e32 v14, v150, v14
	v_mul_f32_e32 v15, v150, v15
	v_mul_f32_e32 v16, v150, v16
	v_mul_f32_e32 v17, v150, v17
	v_cvt_pk_bf16_f32 v182, v10, v11
	v_cvt_pk_bf16_f32 v183, v12, v13
	v_cvt_pk_bf16_f32 v184, v14, v15
	v_cvt_pk_bf16_f32 v185, v16, v17
	v_xor_b32_e32 v167, 64, v164
	ds_write_b128 v167, v[182:185]
	v_mov_b32_e32 v2, 0
	v_mov_b32_e32 v6, 0
	v_mov_b32_e32 v10, 0
	v_mov_b32_e32 v14, 0
	v_mov_b32_e32 v3, 0
	v_mov_b32_e32 v7, 0
	v_mov_b32_e32 v11, 0
	v_mov_b32_e32 v15, 0
	v_mov_b32_e32 v4, 0
	v_mov_b32_e32 v8, 0
	v_mov_b32_e32 v12, 0
	v_mov_b32_e32 v16, 0
	v_mov_b32_e32 v5, 0
	v_mov_b32_e32 v9, 0
	v_mov_b32_e32 v13, 0
	v_mov_b32_e32 v17, 0
	ds_read_b128 v[182:185], v165 offset:0
	v_cmp_lt_i32_e32 vcc, -1, v151
	v_lshlrev_b32_e32 v148, 13, v151
	v_mov_b32_e32 v149, 0
	v_lshl_add_u64 v[148:149], v[148:149], 0, v[86:87]
	v_cndmask_b32_e32 v148, v168, v148, vcc
	v_cndmask_b32_e32 v149, v169, v149, vcc
	s_waitcnt lgkmcnt(0)
	global_store_dwordx4 v[148:149], v[182:185], off
	ds_read_b128 v[182:185], v165 offset:8192
	v_cmp_lt_i32_e32 vcc, -1, v166
	v_lshlrev_b32_e32 v148, 13, v166
	v_mov_b32_e32 v149, 0
	v_lshl_add_u64 v[148:149], v[148:149], 0, v[86:87]
	v_cndmask_b32_e32 v148, v168, v148, vcc
	v_cndmask_b32_e32 v149, v169, v149, vcc
	s_waitcnt lgkmcnt(0)
; #define PG8_LAS __attribute__((address_space(3)))
; __device__ __forceinline__ unsigned cvtpk(float lo, float hi) { f32x2 v = {lo, hi}; bf16x2_t b = __builtin_convertvector(v, bf16x2_t); return __builtin_bit_cast(unsigned, b); }
; __device__ __forceinline__ void moe_down_stream(PG8_LAS unsigned char* lds, int e, int cb0, int slot0, int nv, const bf16_t* HIDp, const float* Wd, bf16_t* Y, const float* slot_w, const int* slot_dst) {
;     ...
;         if (((t + 1) & 7) == 7) {
;             const int cb = cb0 + ((t + 1) >> 3);
; #pragma unroll
;             for (int m = 0; m < DNM; ++m) {
;                 const float w_ = lw[4 * (16 * m + fr) + wr];
; #pragma unroll
;                 for (int p = 0; p < 2; ++p) { const f32x4 v0 = acc[m][2 * p] * w_, v1 = acc[m][2 * p + 1] * w_; u32x4 w; w.x = cvtpk(v0[0], v0[1]); w.y = cvtpk(v0[2], v0[3]); w.z = cvtpk(v1[0], v1[1]); w.w = cvtpk(v1[2], v1[3]);
;                     *(PG8_LAS u32x4*)(stg + fr * 128 + (((4 * p + fq) ^ (fr & 7)) * 16)) = w; }
; #pragma unroll
;                 for (int hh = 0; hh < 2; ++hh) { const int r = (lane >> 3) + 8 * hh, cc = lane & 7; const u32x4 d = *(const PG8_LAS u32x4*)(stg + r * 128 + ((cc ^ (r & 7)) * 16)); const int dst_ = ldst[4 * (16 * m + r) + wr];
;                     if (dst_ >= 0) *(u32x4*)(Y + (size_t)dst_ * D + 128 * cb + 64 * wc + 8 * cc) = d; }
; #pragma unroll
;                 for (int n = 0; n < 4; ++n) acc[m][n] = (f32x4){0.f, 0.f, 0.f, 0.f}; } }
	global_store_dwordx4 v[148:149], v[182:185], off
	v_add_co_u32_e32 v86, vcc, 0x800, v86
	s_nop 1
	v_addc_co_u32_e32 v87, vcc, 0, v87, vcc
	s_waitcnt lgkmcnt(0)
	s_add_i32 s49, s48, s74
	s_add_i32 s52, s52, 1
	s_and_b32 s54, s52, 7
	s_cmp_eq_u32 s54, 0
	s_cselect_b32 s54, s53, s32
	s_cselect_b32 s55, -1, 0
	s_add_u32 s30, s30, s54
	s_addc_u32 s31, s31, s55
	s_mov_b32 m0, s49
	s_nop 0
	global_load_lds_dwordx4 v88, s[30:31]
	s_add_i32 m0, s49, 0x2000
	s_nop 0
	global_load_lds_dwordx4 v90, s[30:31]
	s_add_i32 m0, s49, 0x4000
	s_nop 0
	global_load_lds_dwordx4 v92, s[30:31]
	s_add_i32 m0, s49, 0x6000
	s_nop 0
	global_load_lds_dwordx4 v94, s[30:31]
	s_add_i32 m0, s49, 0x8000
	s_nop 0
	global_load_lds_dwordx4 v96, s[30:31]
	v_cvt_pk_bf16_f32 v172, v114, v116
	v_cvt_pk_bf16_f32 v173, v118, v120
	v_cvt_pk_bf16_f32 v174, v122, v124
	v_cvt_pk_bf16_f32 v175, v126, v128
	v_cvt_pk_bf16_f32 v176, v115, v117
	v_cvt_pk_bf16_f32 v177, v119, v121
	v_cvt_pk_bf16_f32 v178, v123, v125
	v_cvt_pk_bf16_f32 v179, v127, v129
	ds_write_b128 v95, v[172:175] offset:19456
	ds_write_b128 v95, v[176:179] offset:19584
	v_add_u32_e32 v91, s46, v135
	v_add_u32_e32 v93, s46, v137
	ds_read_b128 v[238:241], v139 offset:0
	ds_read_b128 v[242:245], v139 offset:2048
	ds_read_b128 v[246:249], v139 offset:4096
	ds_read_b128 v[250:253], v139 offset:6144
	ds_read_b128 v[218:221], v91 offset:0
	ds_read_b128 v[222:225], v91 offset:2048
	ds_read_b128 v[226:229], v91 offset:4096
	ds_read_b128 v[230:233], v91 offset:6144
	ds_read_b128 v[234:237], v91 offset:8192
	s_waitcnt lgkmcnt(0)
	v_mfma_f32_16x16x32_bf16 v[78:81], v[238:241], v[218:221], v[78:81]
	v_mfma_f32_16x16x32_bf16 v[74:77], v[242:245], v[218:221], v[74:77]
	v_mfma_f32_16x16x32_bf16 v[70:73], v[246:249], v[218:221], v[70:73]
	v_mfma_f32_16x16x32_bf16 v[66:69], v[250:253], v[218:221], v[66:69]
	ds_read_b128 v[218:221], v93 offset:0
	ds_read_b128 v[142:145], v141 offset:0
	s_add_i32 s51, s51, 1
	s_and_b32 s54, s51, 7
	s_cmp_eq_u32 s54, 0
	s_cselect_b32 s44, s34, s35
	s_cselect_b32 s45, -1, 0
	v_lshl_add_u64 v[132:133], v[132:133], 0, s[44:45]
	global_load_dwordx2 v[114:115], v[132:133], off
	v_lshl_add_u64 v[180:181], v[132:133], 0, s[24:25]
	global_load_dwordx2 v[116:117], v[180:181], off
	v_mfma_f32_16x16x32_bf16 v[62:65], v[238:241], v[222:225], v[62:65]
	v_mfma_f32_16x16x32_bf16 v[58:61], v[242:245], v[222:225], v[58:61]
	v_mfma_f32_16x16x32_bf16 v[54:57], v[246:249], v[222:225], v[54:57]
	v_mfma_f32_16x16x32_bf16 v[50:53], v[250:253], v[222:225], v[50:53]
	ds_read_b128 v[222:225], v93 offset:2048
	ds_read_b128 v[146:149], v141 offset:2048
	v_lshl_add_u64 v[180:181], v[132:133], 0, s[26:27]
	global_load_dwordx2 v[118:119], v[180:181], off
	v_lshl_add_u64 v[180:181], v[132:133], 0, s[28:29]
	global_load_dwordx2 v[120:121], v[180:181], off
	v_mfma_f32_16x16x32_bf16 v[46:49], v[238:241], v[226:229], v[46:49]
	v_mfma_f32_16x16x32_bf16 v[42:45], v[242:245], v[226:229], v[42:45]
	v_mfma_f32_16x16x32_bf16 v[38:41], v[246:249], v[226:229], v[38:41]
	v_mfma_f32_16x16x32_bf16 v[34:37], v[250:253], v[226:229], v[34:37]
	ds_read_b128 v[226:229], v93 offset:4096
	ds_read_b128 v[156:159], v141 offset:4096
	v_lshl_add_u64 v[180:181], v[132:133], 0, s[36:37]
	global_load_dwordx2 v[122:123], v[180:181], off
	v_lshl_add_u64 v[180:181], v[132:133], 0, s[38:39]
	global_load_dwordx2 v[124:125], v[180:181], off
	v_mfma_f32_16x16x32_bf16 v[18:21], v[238:241], v[230:233], v[18:21]
	v_mfma_f32_16x16x32_bf16 v[22:25], v[242:245], v[230:233], v[22:25]
	v_mfma_f32_16x16x32_bf16 v[26:29], v[246:249], v[230:233], v[26:29]
	v_mfma_f32_16x16x32_bf16 v[30:33], v[250:253], v[230:233], v[30:33]
	ds_read_b128 v[230:233], v93 offset:6144
	ds_read_b128 v[160:163], v141 offset:6144
	v_lshl_add_u64 v[180:181], v[132:133], 0, s[40:41]
	global_load_dwordx2 v[126:127], v[180:181], off
	v_lshl_add_u64 v[180:181], v[132:133], 0, s[42:43]
	global_load_dwordx2 v[128:129], v[180:181], off
	v_mfma_f32_16x16x32_bf16 v[2:5], v[238:241], v[234:237], v[2:5]
	v_mfma_f32_16x16x32_bf16 v[6:9], v[242:245], v[234:237], v[6:9]
	v_mfma_f32_16x16x32_bf16 v[10:13], v[246:249], v[234:237], v[10:13]
	v_mfma_f32_16x16x32_bf16 v[14:17], v[250:253], v[234:237], v[14:17]
	ds_read_b128 v[234:237], v93 offset:8192
	s_waitcnt vmcnt(31)
	s_waitcnt lgkmcnt(0)
	s_barrier
; #define MD_GLDS_A(buf, tau) do { _Pragma("unroll") for (int i = 0; i < 5; ++i) if (amask & (1u << i)) \
;         __builtin_amdgcn_global_load_lds((const unsigned*)((const char*)HIDp + aoff[i] + (size_t)((tau) & 7) * 128), (PG8_LAS unsigned*)(MD_SA(buf) + wid * 1024 + i * 8192), 16, 0, 0); } while (0)
; #define MD_B_ISSUE(sb, tau) do { const char* kb_ = Bb + (size_t)((tau) >> 3) * 512 + (size_t)((tau) & 7) * (64 * (size_t)RB); _Pragma("unroll") for (int j = 0; j < 8; ++j) { const char* p_ = kb_ + (size_t)j * RB; \
;         asm volatile("global_load_dwordx2 %0, %1, off" : "=&v"(sb[j]) : "v"(p_) : "memory"); } } while (0)
; #define MD_B_WAIT(sb, N) asm volatile("s_waitcnt vmcnt(%8)" : "+v"(sb[0]), "+v"(sb[1]), "+v"(sb[2]), "+v"(sb[3]), "+v"(sb[4]), "+v"(sb[5]), "+v"(sb[6]), "+v"(sb[7]) : "n"(N) : "memory")
; #define MD_END(last) do { if (last) asm volatile("s_waitcnt vmcnt(0)" ::: "memory"); else asm volatile("s_waitcnt vmcnt(8)" ::: "memory"); \
;         asm volatile("s_waitcnt lgkmcnt(0)" ::: "memory"); __builtin_amdgcn_s_barrier(); asm volatile("" ::: "memory"); } while (0)
; __device__ __forceinline__ void moe_down_stream(PG8_LAS unsigned char* lds, int e, int cb0, int slot0, int nv, const bf16_t* HIDp, const float* Wd, bf16_t* Y, const float* slot_w, const int* slot_dst) {
;     ...
;     for (int t = 0; t < NT; t += 2) {
;         if (t + 2 < NT) MD_B_WAIT(s1, 8); else MD_B_WAIT(s1, 0);
;         MD_B_WRITE(s1, 1); __builtin_amdgcn_sched_barrier(0); MD_GLDS_A(1, t + 1); __builtin_amdgcn_sched_barrier(0);
;         if (t + 3 < NT) MD_B_ISSUE(s1, t + 3);
;         MD_COMPUTE(0);
;         MD_END(t + 3 >= NT);
;         if (t + 2 < NT) { MD_B_WAIT(s0, 8); MD_B_WRITE(s0, 0); __builtin_amdgcn_sched_barrier(0); MD_GLDS_A(0, t + 2); __builtin_amdgcn_sched_barrier(0); }
;         if (t + 4 < NT) MD_B_ISSUE(s0, t + 4);
;         MD_COMPUTE(1);
;         MD_END(t + 4 >= NT);
	s_mov_b32 s49, s46
	s_mov_b32 s46, s47
	s_mov_b32 s47, s48
	s_mov_b32 s48, s49
	s_add_i32 s49, s48, s74
	s_add_i32 s52, s52, 1
	s_and_b32 s54, s52, 7
	s_cmp_eq_u32 s54, 0
	s_cselect_b32 s54, s53, s32
	s_cselect_b32 s55, -1, 0
	s_add_u32 s30, s30, s54
	s_addc_u32 s31, s31, s55
	v_mfma_f32_16x16x32_bf16 v[78:81], v[142:145], v[218:221], v[78:81]
	v_mfma_f32_16x16x32_bf16 v[74:77], v[146:149], v[218:221], v[74:77]
	v_mfma_f32_16x16x32_bf16 v[70:73], v[156:159], v[218:221], v[70:73]
	v_mfma_f32_16x16x32_bf16 v[66:69], v[160:163], v[218:221], v[66:69]
	s_mov_b32 m0, s49
	s_nop 0
	global_load_lds_dwordx4 v88, s[30:31]
	v_mfma_f32_16x16x32_bf16 v[62:65], v[142:145], v[222:225], v[62:65]
	v_mfma_f32_16x16x32_bf16 v[58:61], v[146:149], v[222:225], v[58:61]
	v_mfma_f32_16x16x32_bf16 v[54:57], v[156:159], v[222:225], v[54:57]
	v_mfma_f32_16x16x32_bf16 v[50:53], v[160:163], v[222:225], v[50:53]
	s_add_i32 m0, s49, 0x2000
	s_nop 0
	global_load_lds_dwordx4 v90, s[30:31]
	v_mfma_f32_16x16x32_bf16 v[46:49], v[142:145], v[226:229], v[46:49]
	v_mfma_f32_16x16x32_bf16 v[42:45], v[146:149], v[226:229], v[42:45]
	v_mfma_f32_16x16x32_bf16 v[38:41], v[156:159], v[226:229], v[38:41]
	v_mfma_f32_16x16x32_bf16 v[34:37], v[160:163], v[226:229], v[34:37]
	s_add_i32 m0, s49, 0x4000
	s_nop 0
	global_load_lds_dwordx4 v92, s[30:31]
	v_mfma_f32_16x16x32_bf16 v[18:21], v[142:145], v[230:233], v[18:21]
	v_mfma_f32_16x16x32_bf16 v[22:25], v[146:149], v[230:233], v[22:25]
	v_mfma_f32_16x16x32_bf16 v[26:29], v[156:159], v[230:233], v[26:29]
	v_mfma_f32_16x16x32_bf16 v[30:33], v[160:163], v[230:233], v[30:33]
	s_add_i32 m0, s49, 0x6000
	s_nop 0
	global_load_lds_dwordx4 v94, s[30:31]
	v_mfma_f32_16x16x32_bf16 v[2:5], v[142:145], v[234:237], v[2:5]
	v_mfma_f32_16x16x32_bf16 v[6:9], v[146:149], v[234:237], v[6:9]
	v_mfma_f32_16x16x32_bf16 v[10:13], v[156:159], v[234:237], v[10:13]
	v_mfma_f32_16x16x32_bf16 v[14:17], v[160:163], v[234:237], v[14:17]
	s_add_i32 m0, s49, 0x8000
	s_nop 0
	global_load_lds_dwordx4 v96, s[30:31]
	v_cvt_pk_bf16_f32 v172, v186, v188
	v_cvt_pk_bf16_f32 v173, v190, v192
	v_cvt_pk_bf16_f32 v174, v194, v196
	v_cvt_pk_bf16_f32 v175, v198, v200
	v_cvt_pk_bf16_f32 v176, v187, v189
	v_cvt_pk_bf16_f32 v177, v191, v193
	v_cvt_pk_bf16_f32 v178, v195, v197
	v_cvt_pk_bf16_f32 v179, v199, v201
	ds_write_b128 v95, v[172:175] offset:0
	ds_write_b128 v95, v[176:179] offset:128
	v_add_u32_e32 v91, s46, v135
	v_add_u32_e32 v93, s46, v137
	ds_read_b128 v[238:241], v139 offset:19456
	ds_read_b128 v[242:245], v139 offset:21504
	ds_read_b128 v[246:249], v139 offset:23552
	ds_read_b128 v[250:253], v139 offset:25600
	ds_read_b128 v[218:221], v91 offset:0
	ds_read_b128 v[222:225], v91 offset:2048
	ds_read_b128 v[226:229], v91 offset:4096
	ds_read_b128 v[230:233], v91 offset:6144
	ds_read_b128 v[234:237], v91 offset:8192
	s_waitcnt lgkmcnt(0)
	v_mfma_f32_16x16x32_bf16 v[78:81], v[238:241], v[218:221], v[78:81]
	v_mfma_f32_16x16x32_bf16 v[74:77], v[242:245], v[218:221], v[74:77]
	v_mfma_f32_16x16x32_bf16 v[70:73], v[246:249], v[218:221], v[70:73]
	v_mfma_f32_16x16x32_bf16 v[66:69], v[250:253], v[218:221], v[66:69]
	ds_read_b128 v[218:221], v93 offset:0
	ds_read_b128 v[142:145], v141 offset:19456
	s_add_i32 s51, s51, 1
	s_and_b32 s54, s51, 7
	s_cmp_eq_u32 s54, 0
	s_cselect_b32 s44, s34, s35
	s_cselect_b32 s45, -1, 0
	v_lshl_add_u64 v[132:133], v[132:133], 0, s[44:45]
	global_load_dwordx2 v[186:187], v[132:133], off
	v_lshl_add_u64 v[180:181], v[132:133], 0, s[24:25]
	global_load_dwordx2 v[188:189], v[180:181], off
	v_mfma_f32_16x16x32_bf16 v[62:65], v[238:241], v[222:225], v[62:65]
	v_mfma_f32_16x16x32_bf16 v[58:61], v[242:245], v[222:225], v[58:61]
	v_mfma_f32_16x16x32_bf16 v[54:57], v[246:249], v[222:225], v[54:57]
	v_mfma_f32_16x16x32_bf16 v[50:53], v[250:253], v[222:225], v[50:53]
	ds_read_b128 v[222:225], v93 offset:2048
	ds_read_b128 v[146:149], v141 offset:21504
	v_lshl_add_u64 v[180:181], v[132:133], 0, s[26:27]
	global_load_dwordx2 v[190:191], v[180:181], off
	v_lshl_add_u64 v[180:181], v[132:133], 0, s[28:29]
	global_load_dwordx2 v[192:193], v[180:181], off
	v_mfma_f32_16x16x32_bf16 v[46:49], v[238:241], v[226:229], v[46:49]
	v_mfma_f32_16x16x32_bf16 v[42:45], v[242:245], v[226:229], v[42:45]
	v_mfma_f32_16x16x32_bf16 v[38:41], v[246:249], v[226:229], v[38:41]
	v_mfma_f32_16x16x32_bf16 v[34:37], v[250:253], v[226:229], v[34:37]
	ds_read_b128 v[226:229], v93 offset:4096
	ds_read_b128 v[156:159], v141 offset:23552
	v_lshl_add_u64 v[180:181], v[132:133], 0, s[36:37]
	global_load_dwordx2 v[194:195], v[180:181], off
	v_lshl_add_u64 v[180:181], v[132:133], 0, s[38:39]
	global_load_dwordx2 v[196:197], v[180:181], off
	v_mfma_f32_16x16x32_bf16 v[18:21], v[238:241], v[230:233], v[18:21]
	v_mfma_f32_16x16x32_bf16 v[22:25], v[242:245], v[230:233], v[22:25]
	v_mfma_f32_16x16x32_bf16 v[26:29], v[246:249], v[230:233], v[26:29]
	v_mfma_f32_16x16x32_bf16 v[30:33], v[250:253], v[230:233], v[30:33]
	ds_read_b128 v[230:233], v93 offset:6144
	ds_read_b128 v[160:163], v141 offset:25600
	v_lshl_add_u64 v[180:181], v[132:133], 0, s[40:41]
	global_load_dwordx2 v[198:199], v[180:181], off
	v_lshl_add_u64 v[180:181], v[132:133], 0, s[42:43]
	global_load_dwordx2 v[200:201], v[180:181], off
	v_mfma_f32_16x16x32_bf16 v[2:5], v[238:241], v[234:237], v[2:5]
	v_mfma_f32_16x16x32_bf16 v[6:9], v[242:245], v[234:237], v[6:9]
	v_mfma_f32_16x16x32_bf16 v[10:13], v[246:249], v[234:237], v[10:13]
	v_mfma_f32_16x16x32_bf16 v[14:17], v[250:253], v[234:237], v[14:17]
	ds_read_b128 v[234:237], v93 offset:8192
	s_waitcnt vmcnt(21)
	s_waitcnt lgkmcnt(0)
	s_barrier
; #define MD_GLDS_A(buf, tau) do { _Pragma("unroll") for (int i = 0; i < 5; ++i) if (amask & (1u << i)) \
;         __builtin_amdgcn_global_load_lds((const unsigned*)((const char*)HIDp + aoff[i] + (size_t)((tau) & 7) * 128), (PG8_LAS unsigned*)(MD_SA(buf) + wid * 1024 + i * 8192), 16, 0, 0); } while (0)
; #define MD_B_ISSUE(sb, tau) do { const char* kb_ = Bb + (size_t)((tau) >> 3) * 512 + (size_t)((tau) & 7) * (64 * (size_t)RB); _Pragma("unroll") for (int j = 0; j < 8; ++j) { const char* p_ = kb_ + (size_t)j * RB; \
;         asm volatile("global_load_dwordx2 %0, %1, off" : "=&v"(sb[j]) : "v"(p_) : "memory"); } } while (0)
; #define MD_B_WAIT(sb, N) asm volatile("s_waitcnt vmcnt(%8)" : "+v"(sb[0]), "+v"(sb[1]), "+v"(sb[2]), "+v"(sb[3]), "+v"(sb[4]), "+v"(sb[5]), "+v"(sb[6]), "+v"(sb[7]) : "n"(N) : "memory")
; #define MD_END(last) do { if (last) asm volatile("s_waitcnt vmcnt(0)" ::: "memory"); else asm volatile("s_waitcnt vmcnt(8)" ::: "memory"); \
;         asm volatile("s_waitcnt lgkmcnt(0)" ::: "memory"); __builtin_amdgcn_s_barrier(); asm volatile("" ::: "memory"); } while (0)
; __device__ __forceinline__ void moe_down_stream(PG8_LAS unsigned char* lds, int e, int cb0, int slot0, int nv, const bf16_t* HIDp, const float* Wd, bf16_t* Y, const float* slot_w, const int* slot_dst) {
;     ...
;     for (int t = 0; t < NT; t += 2) {
;         if (t + 2 < NT) MD_B_WAIT(s1, 8); else MD_B_WAIT(s1, 0);
;         MD_B_WRITE(s1, 1); __builtin_amdgcn_sched_barrier(0); MD_GLDS_A(1, t + 1); __builtin_amdgcn_sched_barrier(0);
;         if (t + 3 < NT) MD_B_ISSUE(s1, t + 3);
;         MD_COMPUTE(0);
;         MD_END(t + 3 >= NT);
;         if (t + 2 < NT) { MD_B_WAIT(s0, 8); MD_B_WRITE(s0, 0); __builtin_amdgcn_sched_barrier(0); MD_GLDS_A(0, t + 2); __builtin_amdgcn_sched_barrier(0); }
;         if (t + 4 < NT) MD_B_ISSUE(s0, t + 4);
;         MD_COMPUTE(1);
;         MD_END(t + 4 >= NT);
	s_mov_b32 s49, s46
	s_mov_b32 s46, s47
	s_mov_b32 s47, s48
	s_mov_b32 s48, s49
	s_add_i32 s49, s48, s74
	s_add_i32 s52, s52, 1
	s_and_b32 s54, s52, 7
	s_cmp_eq_u32 s54, 0
	s_cselect_b32 s54, s53, s32
	s_cselect_b32 s55, -1, 0
	s_add_u32 s30, s30, s54
	s_addc_u32 s31, s31, s55
	v_mfma_f32_16x16x32_bf16 v[78:81], v[142:145], v[218:221], v[78:81]
	v_mfma_f32_16x16x32_bf16 v[74:77], v[146:149], v[218:221], v[74:77]
	v_mfma_f32_16x16x32_bf16 v[70:73], v[156:159], v[218:221], v[70:73]
	v_mfma_f32_16x16x32_bf16 v[66:69], v[160:163], v[218:221], v[66:69]
	s_mov_b32 m0, s49
	s_nop 0
	global_load_lds_dwordx4 v88, s[30:31]
	v_mfma_f32_16x16x32_bf16 v[62:65], v[142:145], v[222:225], v[62:65]
	v_mfma_f32_16x16x32_bf16 v[58:61], v[146:149], v[222:225], v[58:61]
	v_mfma_f32_16x16x32_bf16 v[54:57], v[156:159], v[222:225], v[54:57]
	v_mfma_f32_16x16x32_bf16 v[50:53], v[160:163], v[222:225], v[50:53]
	s_add_i32 m0, s49, 0x2000
	s_nop 0
	global_load_lds_dwordx4 v90, s[30:31]
	v_mfma_f32_16x16x32_bf16 v[46:49], v[142:145], v[226:229], v[46:49]
	v_mfma_f32_16x16x32_bf16 v[42:45], v[146:149], v[226:229], v[42:45]
	v_mfma_f32_16x16x32_bf16 v[38:41], v[156:159], v[226:229], v[38:41]
	v_mfma_f32_16x16x32_bf16 v[34:37], v[160:163], v[226:229], v[34:37]
	s_add_i32 m0, s49, 0x4000
	s_nop 0
	global_load_lds_dwordx4 v92, s[30:31]
	v_mfma_f32_16x16x32_bf16 v[18:21], v[142:145], v[230:233], v[18:21]
	v_mfma_f32_16x16x32_bf16 v[22:25], v[146:149], v[230:233], v[22:25]
	v_mfma_f32_16x16x32_bf16 v[26:29], v[156:159], v[230:233], v[26:29]
	v_mfma_f32_16x16x32_bf16 v[30:33], v[160:163], v[230:233], v[30:33]
	s_add_i32 m0, s49, 0x6000
	s_nop 0
	global_load_lds_dwordx4 v94, s[30:31]
	v_mfma_f32_16x16x32_bf16 v[2:5], v[142:145], v[234:237], v[2:5]
	v_mfma_f32_16x16x32_bf16 v[6:9], v[146:149], v[234:237], v[6:9]
	v_mfma_f32_16x16x32_bf16 v[10:13], v[156:159], v[234:237], v[10:13]
	v_mfma_f32_16x16x32_bf16 v[14:17], v[160:163], v[234:237], v[14:17]
	s_add_i32 m0, s49, 0x8000
	s_nop 0
	global_load_lds_dwordx4 v96, s[30:31]
	v_cvt_pk_bf16_f32 v172, v202, v204
	v_cvt_pk_bf16_f32 v173, v206, v208
	v_cvt_pk_bf16_f32 v174, v210, v212
	v_cvt_pk_bf16_f32 v175, v214, v216
	v_cvt_pk_bf16_f32 v176, v203, v205
	v_cvt_pk_bf16_f32 v177, v207, v209
	v_cvt_pk_bf16_f32 v178, v211, v213
	v_cvt_pk_bf16_f32 v179, v215, v217
	ds_write_b128 v95, v[172:175] offset:19456
	ds_write_b128 v95, v[176:179] offset:19584
	v_add_u32_e32 v91, s46, v135
	v_add_u32_e32 v93, s46, v137
	ds_read_b128 v[238:241], v139 offset:0
	ds_read_b128 v[242:245], v139 offset:2048
	ds_read_b128 v[246:249], v139 offset:4096
	ds_read_b128 v[250:253], v139 offset:6144
	ds_read_b128 v[218:221], v91 offset:0
	ds_read_b128 v[222:225], v91 offset:2048
	ds_read_b128 v[226:229], v91 offset:4096
	ds_read_b128 v[230:233], v91 offset:6144
	ds_read_b128 v[234:237], v91 offset:8192
	s_waitcnt lgkmcnt(0)
	v_mfma_f32_16x16x32_bf16 v[78:81], v[238:241], v[218:221], v[78:81]
	v_mfma_f32_16x16x32_bf16 v[74:77], v[242:245], v[218:221], v[74:77]
	v_mfma_f32_16x16x32_bf16 v[70:73], v[246:249], v[218:221], v[70:73]
	v_mfma_f32_16x16x32_bf16 v[66:69], v[250:253], v[218:221], v[66:69]
	ds_read_b128 v[218:221], v93 offset:0
	ds_read_b128 v[142:145], v141 offset:0
	s_add_i32 s51, s51, 1
	s_and_b32 s54, s51, 7
	s_cmp_eq_u32 s54, 0
	s_cselect_b32 s44, s34, s35
	s_cselect_b32 s45, -1, 0
	v_lshl_add_u64 v[132:133], v[132:133], 0, s[44:45]
	global_load_dwordx2 v[202:203], v[132:133], off
	v_lshl_add_u64 v[180:181], v[132:133], 0, s[24:25]
	global_load_dwordx2 v[204:205], v[180:181], off
	v_mfma_f32_16x16x32_bf16 v[62:65], v[238:241], v[222:225], v[62:65]
	v_mfma_f32_16x16x32_bf16 v[58:61], v[242:245], v[222:225], v[58:61]
	v_mfma_f32_16x16x32_bf16 v[54:57], v[246:249], v[222:225], v[54:57]
	v_mfma_f32_16x16x32_bf16 v[50:53], v[250:253], v[222:225], v[50:53]
	ds_read_b128 v[222:225], v93 offset:2048
	ds_read_b128 v[146:149], v141 offset:2048
	v_lshl_add_u64 v[180:181], v[132:133], 0, s[26:27]
	global_load_dwordx2 v[206:207], v[180:181], off
	v_lshl_add_u64 v[180:181], v[132:133], 0, s[28:29]
	global_load_dwordx2 v[208:209], v[180:181], off
	v_mfma_f32_16x16x32_bf16 v[46:49], v[238:241], v[226:229], v[46:49]
	v_mfma_f32_16x16x32_bf16 v[42:45], v[242:245], v[226:229], v[42:45]
	v_mfma_f32_16x16x32_bf16 v[38:41], v[246:249], v[226:229], v[38:41]
	v_mfma_f32_16x16x32_bf16 v[34:37], v[250:253], v[226:229], v[34:37]
	ds_read_b128 v[226:229], v93 offset:4096
	ds_read_b128 v[156:159], v141 offset:4096
	v_lshl_add_u64 v[180:181], v[132:133], 0, s[36:37]
	global_load_dwordx2 v[210:211], v[180:181], off
	v_lshl_add_u64 v[180:181], v[132:133], 0, s[38:39]
	global_load_dwordx2 v[212:213], v[180:181], off
	v_mfma_f32_16x16x32_bf16 v[18:21], v[238:241], v[230:233], v[18:21]
	v_mfma_f32_16x16x32_bf16 v[22:25], v[242:245], v[230:233], v[22:25]
	v_mfma_f32_16x16x32_bf16 v[26:29], v[246:249], v[230:233], v[26:29]
	v_mfma_f32_16x16x32_bf16 v[30:33], v[250:253], v[230:233], v[30:33]
	ds_read_b128 v[230:233], v93 offset:6144
	ds_read_b128 v[160:163], v141 offset:6144
	v_lshl_add_u64 v[180:181], v[132:133], 0, s[40:41]
	global_load_dwordx2 v[214:215], v[180:181], off
	v_lshl_add_u64 v[180:181], v[132:133], 0, s[42:43]
	global_load_dwordx2 v[216:217], v[180:181], off
	v_mfma_f32_16x16x32_bf16 v[2:5], v[238:241], v[234:237], v[2:5]
	v_mfma_f32_16x16x32_bf16 v[6:9], v[242:245], v[234:237], v[6:9]
	v_mfma_f32_16x16x32_bf16 v[10:13], v[246:249], v[234:237], v[10:13]
	v_mfma_f32_16x16x32_bf16 v[14:17], v[250:253], v[234:237], v[14:17]
	ds_read_b128 v[234:237], v93 offset:8192
	s_waitcnt vmcnt(21)
	s_waitcnt lgkmcnt(0)
	s_barrier
; #define MD_GLDS_A(buf, tau) do { _Pragma("unroll") for (int i = 0; i < 5; ++i) if (amask & (1u << i)) \
;         __builtin_amdgcn_global_load_lds((const unsigned*)((const char*)HIDp + aoff[i] + (size_t)((tau) & 7) * 128), (PG8_LAS unsigned*)(MD_SA(buf) + wid * 1024 + i * 8192), 16, 0, 0); } while (0)
; #define MD_B_ISSUE(sb, tau) do { const char* kb_ = Bb + (size_t)((tau) >> 3) * 512 + (size_t)((tau) & 7) * (64 * (size_t)RB); _Pragma("unroll") for (int j = 0; j < 8; ++j) { const char* p_ = kb_ + (size_t)j * RB; \
;         asm volatile("global_load_dwordx2 %0, %1, off" : "=&v"(sb[j]) : "v"(p_) : "memory"); } } while (0)
; #define MD_B_WAIT(sb, N) asm volatile("s_waitcnt vmcnt(%8)" : "+v"(sb[0]), "+v"(sb[1]), "+v"(sb[2]), "+v"(sb[3]), "+v"(sb[4]), "+v"(sb[5]), "+v"(sb[6]), "+v"(sb[7]) : "n"(N) : "memory")
; #define MD_END(last) do { if (last) asm volatile("s_waitcnt vmcnt(0)" ::: "memory"); else asm volatile("s_waitcnt vmcnt(8)" ::: "memory"); \
;         asm volatile("s_waitcnt lgkmcnt(0)" ::: "memory"); __builtin_amdgcn_s_barrier(); asm volatile("" ::: "memory"); } while (0)
; __device__ __forceinline__ void moe_down_stream(PG8_LAS unsigned char* lds, int e, int cb0, int slot0, int nv, const bf16_t* HIDp, const float* Wd, bf16_t* Y, const float* slot_w, const int* slot_dst) {
;     ...
;     for (int t = 0; t < NT; t += 2) {
;         if (t + 2 < NT) MD_B_WAIT(s1, 8); else MD_B_WAIT(s1, 0);
;         MD_B_WRITE(s1, 1); __builtin_amdgcn_sched_barrier(0); MD_GLDS_A(1, t + 1); __builtin_amdgcn_sched_barrier(0);
;         if (t + 3 < NT) MD_B_ISSUE(s1, t + 3);
;         MD_COMPUTE(0);
;         MD_END(t + 3 >= NT);
;         if (t + 2 < NT) { MD_B_WAIT(s0, 8); MD_B_WRITE(s0, 0); __builtin_amdgcn_sched_barrier(0); MD_GLDS_A(0, t + 2); __builtin_amdgcn_sched_barrier(0); }
;         if (t + 4 < NT) MD_B_ISSUE(s0, t + 4);
;         MD_COMPUTE(1);
;         MD_END(t + 4 >= NT);
	s_mov_b32 s49, s46
	s_mov_b32 s46, s47
	s_mov_b32 s47, s48
	s_mov_b32 s48, s49
	s_add_i32 s49, s48, s74
	s_add_i32 s52, s52, 1
	s_and_b32 s54, s52, 7
	s_cmp_eq_u32 s54, 0
	s_cselect_b32 s54, s53, s32
	s_cselect_b32 s55, -1, 0
	s_add_u32 s30, s30, s54
	s_addc_u32 s31, s31, s55
	v_mfma_f32_16x16x32_bf16 v[78:81], v[142:145], v[218:221], v[78:81]
	v_mfma_f32_16x16x32_bf16 v[74:77], v[146:149], v[218:221], v[74:77]
	v_mfma_f32_16x16x32_bf16 v[70:73], v[156:159], v[218:221], v[70:73]
	v_mfma_f32_16x16x32_bf16 v[66:69], v[160:163], v[218:221], v[66:69]
	s_mov_b32 m0, s49
	s_nop 0
	global_load_lds_dwordx4 v88, s[30:31]
	v_mfma_f32_16x16x32_bf16 v[62:65], v[142:145], v[222:225], v[62:65]
	v_mfma_f32_16x16x32_bf16 v[58:61], v[146:149], v[222:225], v[58:61]
	v_mfma_f32_16x16x32_bf16 v[54:57], v[156:159], v[222:225], v[54:57]
	v_mfma_f32_16x16x32_bf16 v[50:53], v[160:163], v[222:225], v[50:53]
	s_add_i32 m0, s49, 0x2000
	s_nop 0
	global_load_lds_dwordx4 v90, s[30:31]
	v_mfma_f32_16x16x32_bf16 v[46:49], v[142:145], v[226:229], v[46:49]
	v_mfma_f32_16x16x32_bf16 v[42:45], v[146:149], v[226:229], v[42:45]
	v_mfma_f32_16x16x32_bf16 v[38:41], v[156:159], v[226:229], v[38:41]
	v_mfma_f32_16x16x32_bf16 v[34:37], v[160:163], v[226:229], v[34:37]
	s_add_i32 m0, s49, 0x4000
	s_nop 0
	global_load_lds_dwordx4 v92, s[30:31]
	v_mfma_f32_16x16x32_bf16 v[18:21], v[142:145], v[230:233], v[18:21]
	v_mfma_f32_16x16x32_bf16 v[22:25], v[146:149], v[230:233], v[22:25]
	v_mfma_f32_16x16x32_bf16 v[26:29], v[156:159], v[230:233], v[26:29]
	v_mfma_f32_16x16x32_bf16 v[30:33], v[160:163], v[230:233], v[30:33]
	s_add_i32 m0, s49, 0x6000
	s_nop 0
	global_load_lds_dwordx4 v94, s[30:31]
	v_mfma_f32_16x16x32_bf16 v[2:5], v[142:145], v[234:237], v[2:5]
	v_mfma_f32_16x16x32_bf16 v[6:9], v[146:149], v[234:237], v[6:9]
	v_mfma_f32_16x16x32_bf16 v[10:13], v[156:159], v[234:237], v[10:13]
	v_mfma_f32_16x16x32_bf16 v[14:17], v[160:163], v[234:237], v[14:17]
	s_add_i32 m0, s49, 0x8000
	s_nop 0
	global_load_lds_dwordx4 v96, s[30:31]
	v_cvt_pk_bf16_f32 v172, v98, v100
	v_cvt_pk_bf16_f32 v173, v102, v104
	v_cvt_pk_bf16_f32 v174, v106, v108
	v_cvt_pk_bf16_f32 v175, v110, v112
	v_cvt_pk_bf16_f32 v176, v99, v101
	v_cvt_pk_bf16_f32 v177, v103, v105
	v_cvt_pk_bf16_f32 v178, v107, v109
	v_cvt_pk_bf16_f32 v179, v111, v113
	ds_write_b128 v95, v[172:175] offset:0
	ds_write_b128 v95, v[176:179] offset:128
	v_add_u32_e32 v91, s46, v135
	v_add_u32_e32 v93, s46, v137
	ds_read_b128 v[238:241], v139 offset:19456
	ds_read_b128 v[242:245], v139 offset:21504
	ds_read_b128 v[246:249], v139 offset:23552
	ds_read_b128 v[250:253], v139 offset:25600
	ds_read_b128 v[218:221], v91 offset:0
	ds_read_b128 v[222:225], v91 offset:2048
	ds_read_b128 v[226:229], v91 offset:4096
	ds_read_b128 v[230:233], v91 offset:6144
	ds_read_b128 v[234:237], v91 offset:8192
	s_waitcnt lgkmcnt(0)
	v_mfma_f32_16x16x32_bf16 v[78:81], v[238:241], v[218:221], v[78:81]
	v_mfma_f32_16x16x32_bf16 v[74:77], v[242:245], v[218:221], v[74:77]
	v_mfma_f32_16x16x32_bf16 v[70:73], v[246:249], v[218:221], v[70:73]
	v_mfma_f32_16x16x32_bf16 v[66:69], v[250:253], v[218:221], v[66:69]
	ds_read_b128 v[218:221], v93 offset:0
	ds_read_b128 v[142:145], v141 offset:19456
	s_add_i32 s51, s51, 1
	s_and_b32 s54, s51, 7
	s_cmp_eq_u32 s54, 0
	s_cselect_b32 s44, s34, s35
	s_cselect_b32 s45, -1, 0
	v_lshl_add_u64 v[132:133], v[132:133], 0, s[44:45]
	global_load_dwordx2 v[98:99], v[132:133], off
	v_lshl_add_u64 v[180:181], v[132:133], 0, s[24:25]
	global_load_dwordx2 v[100:101], v[180:181], off
	v_mfma_f32_16x16x32_bf16 v[62:65], v[238:241], v[222:225], v[62:65]
	v_mfma_f32_16x16x32_bf16 v[58:61], v[242:245], v[222:225], v[58:61]
	v_mfma_f32_16x16x32_bf16 v[54:57], v[246:249], v[222:225], v[54:57]
	v_mfma_f32_16x16x32_bf16 v[50:53], v[250:253], v[222:225], v[50:53]
	ds_read_b128 v[222:225], v93 offset:2048
	ds_read_b128 v[146:149], v141 offset:21504
	v_lshl_add_u64 v[180:181], v[132:133], 0, s[26:27]
	global_load_dwordx2 v[102:103], v[180:181], off
	v_lshl_add_u64 v[180:181], v[132:133], 0, s[28:29]
	global_load_dwordx2 v[104:105], v[180:181], off
	v_mfma_f32_16x16x32_bf16 v[46:49], v[238:241], v[226:229], v[46:49]
	v_mfma_f32_16x16x32_bf16 v[42:45], v[242:245], v[226:229], v[42:45]
	v_mfma_f32_16x16x32_bf16 v[38:41], v[246:249], v[226:229], v[38:41]
	v_mfma_f32_16x16x32_bf16 v[34:37], v[250:253], v[226:229], v[34:37]
	ds_read_b128 v[226:229], v93 offset:4096
	ds_read_b128 v[156:159], v141 offset:23552
	v_lshl_add_u64 v[180:181], v[132:133], 0, s[36:37]
	global_load_dwordx2 v[106:107], v[180:181], off
	v_lshl_add_u64 v[180:181], v[132:133], 0, s[38:39]
	global_load_dwordx2 v[108:109], v[180:181], off
	v_mfma_f32_16x16x32_bf16 v[18:21], v[238:241], v[230:233], v[18:21]
	v_mfma_f32_16x16x32_bf16 v[22:25], v[242:245], v[230:233], v[22:25]
	v_mfma_f32_16x16x32_bf16 v[26:29], v[246:249], v[230:233], v[26:29]
	v_mfma_f32_16x16x32_bf16 v[30:33], v[250:253], v[230:233], v[30:33]
	ds_read_b128 v[230:233], v93 offset:6144
	ds_read_b128 v[160:163], v141 offset:25600
	v_lshl_add_u64 v[180:181], v[132:133], 0, s[40:41]
	global_load_dwordx2 v[110:111], v[180:181], off
	v_lshl_add_u64 v[180:181], v[132:133], 0, s[42:43]
	global_load_dwordx2 v[112:113], v[180:181], off
	v_mfma_f32_16x16x32_bf16 v[2:5], v[238:241], v[234:237], v[2:5]
	v_mfma_f32_16x16x32_bf16 v[6:9], v[242:245], v[234:237], v[6:9]
	v_mfma_f32_16x16x32_bf16 v[10:13], v[246:249], v[234:237], v[10:13]
	v_mfma_f32_16x16x32_bf16 v[14:17], v[250:253], v[234:237], v[14:17]
	ds_read_b128 v[234:237], v93 offset:8192
	s_waitcnt vmcnt(21)
	s_waitcnt lgkmcnt(0)
	s_barrier
; #define MD_GLDS_A(buf, tau) do { _Pragma("unroll") for (int i = 0; i < 5; ++i) if (amask & (1u << i)) \
;         __builtin_amdgcn_global_load_lds((const unsigned*)((const char*)HIDp + aoff[i] + (size_t)((tau) & 7) * 128), (PG8_LAS unsigned*)(MD_SA(buf) + wid * 1024 + i * 8192), 16, 0, 0); } while (0)
; #define MD_B_ISSUE(sb, tau) do { const char* kb_ = Bb + (size_t)((tau) >> 3) * 512 + (size_t)((tau) & 7) * (64 * (size_t)RB); _Pragma("unroll") for (int j = 0; j < 8; ++j) { const char* p_ = kb_ + (size_t)j * RB; \
;         asm volatile("global_load_dwordx2 %0, %1, off" : "=&v"(sb[j]) : "v"(p_) : "memory"); } } while (0)
; #define MD_B_WAIT(sb, N) asm volatile("s_waitcnt vmcnt(%8)" : "+v"(sb[0]), "+v"(sb[1]), "+v"(sb[2]), "+v"(sb[3]), "+v"(sb[4]), "+v"(sb[5]), "+v"(sb[6]), "+v"(sb[7]) : "n"(N) : "memory")
; #define MD_END(last) do { if (last) asm volatile("s_waitcnt vmcnt(0)" ::: "memory"); else asm volatile("s_waitcnt vmcnt(8)" ::: "memory"); \
;         asm volatile("s_waitcnt lgkmcnt(0)" ::: "memory"); __builtin_amdgcn_s_barrier(); asm volatile("" ::: "memory"); } while (0)
; __device__ __forceinline__ void moe_down_stream(PG8_LAS unsigned char* lds, int e, int cb0, int slot0, int nv, const bf16_t* HIDp, const float* Wd, bf16_t* Y, const float* slot_w, const int* slot_dst) {
;     ...
;     for (int t = 0; t < NT; t += 2) {
;         if (t + 2 < NT) MD_B_WAIT(s1, 8); else MD_B_WAIT(s1, 0);
;         MD_B_WRITE(s1, 1); __builtin_amdgcn_sched_barrier(0); MD_GLDS_A(1, t + 1); __builtin_amdgcn_sched_barrier(0);
;         if (t + 3 < NT) MD_B_ISSUE(s1, t + 3);
;         MD_COMPUTE(0);
;         MD_END(t + 3 >= NT);
;         if (t + 2 < NT) { MD_B_WAIT(s0, 8); MD_B_WRITE(s0, 0); __builtin_amdgcn_sched_barrier(0); MD_GLDS_A(0, t + 2); __builtin_amdgcn_sched_barrier(0); }
;         if (t + 4 < NT) MD_B_ISSUE(s0, t + 4);
;         MD_COMPUTE(1);
;         MD_END(t + 4 >= NT);
	s_mov_b32 s49, s46
	s_mov_b32 s46, s47
	s_mov_b32 s47, s48
	s_mov_b32 s48, s49
	s_add_i32 s49, s48, s74
	s_add_i32 s52, s52, 1
	s_and_b32 s54, s52, 7
	s_cmp_eq_u32 s54, 0
	s_cselect_b32 s54, s53, s32
	s_cselect_b32 s55, -1, 0
	s_add_u32 s30, s30, s54
	s_addc_u32 s31, s31, s55
	v_mfma_f32_16x16x32_bf16 v[78:81], v[142:145], v[218:221], v[78:81]
	v_mfma_f32_16x16x32_bf16 v[74:77], v[146:149], v[218:221], v[74:77]
	v_mfma_f32_16x16x32_bf16 v[70:73], v[156:159], v[218:221], v[70:73]
	v_mfma_f32_16x16x32_bf16 v[66:69], v[160:163], v[218:221], v[66:69]
	s_mov_b32 m0, s49
	s_nop 0
	global_load_lds_dwordx4 v88, s[30:31]
	v_mfma_f32_16x16x32_bf16 v[62:65], v[142:145], v[222:225], v[62:65]
	v_mfma_f32_16x16x32_bf16 v[58:61], v[146:149], v[222:225], v[58:61]
	v_mfma_f32_16x16x32_bf16 v[54:57], v[156:159], v[222:225], v[54:57]
	v_mfma_f32_16x16x32_bf16 v[50:53], v[160:163], v[222:225], v[50:53]
	s_add_i32 m0, s49, 0x2000
	s_nop 0
	global_load_lds_dwordx4 v90, s[30:31]
	v_mfma_f32_16x16x32_bf16 v[46:49], v[142:145], v[226:229], v[46:49]
	v_mfma_f32_16x16x32_bf16 v[42:45], v[146:149], v[226:229], v[42:45]
	v_mfma_f32_16x16x32_bf16 v[38:41], v[156:159], v[226:229], v[38:41]
	v_mfma_f32_16x16x32_bf16 v[34:37], v[160:163], v[226:229], v[34:37]
	s_add_i32 m0, s49, 0x4000
	s_nop 0
	global_load_lds_dwordx4 v92, s[30:31]
	v_mfma_f32_16x16x32_bf16 v[18:21], v[142:145], v[230:233], v[18:21]
	v_mfma_f32_16x16x32_bf16 v[22:25], v[146:149], v[230:233], v[22:25]
	v_mfma_f32_16x16x32_bf16 v[26:29], v[156:159], v[230:233], v[26:29]
	v_mfma_f32_16x16x32_bf16 v[30:33], v[160:163], v[230:233], v[30:33]
	s_add_i32 m0, s49, 0x6000
	s_nop 0
	global_load_lds_dwordx4 v94, s[30:31]
	v_mfma_f32_16x16x32_bf16 v[2:5], v[142:145], v[234:237], v[2:5]
	v_mfma_f32_16x16x32_bf16 v[6:9], v[146:149], v[234:237], v[6:9]
	v_mfma_f32_16x16x32_bf16 v[10:13], v[156:159], v[234:237], v[10:13]
	v_mfma_f32_16x16x32_bf16 v[14:17], v[160:163], v[234:237], v[14:17]
	s_add_i32 m0, s49, 0x8000
	s_nop 0
	global_load_lds_dwordx4 v96, s[30:31]
	v_cvt_pk_bf16_f32 v172, v114, v116
	v_cvt_pk_bf16_f32 v173, v118, v120
	v_cvt_pk_bf16_f32 v174, v122, v124
	v_cvt_pk_bf16_f32 v175, v126, v128
	v_cvt_pk_bf16_f32 v176, v115, v117
	v_cvt_pk_bf16_f32 v177, v119, v121
	v_cvt_pk_bf16_f32 v178, v123, v125
	v_cvt_pk_bf16_f32 v179, v127, v129
	ds_write_b128 v95, v[172:175] offset:19456
	ds_write_b128 v95, v[176:179] offset:19584
	v_add_u32_e32 v91, s46, v135
	v_add_u32_e32 v93, s46, v137
	ds_read_b128 v[238:241], v139 offset:0
	ds_read_b128 v[242:245], v139 offset:2048
	ds_read_b128 v[246:249], v139 offset:4096
	ds_read_b128 v[250:253], v139 offset:6144
	ds_read_b128 v[218:221], v91 offset:0
	ds_read_b128 v[222:225], v91 offset:2048
	ds_read_b128 v[226:229], v91 offset:4096
	ds_read_b128 v[230:233], v91 offset:6144
	ds_read_b128 v[234:237], v91 offset:8192
	s_waitcnt lgkmcnt(0)
	v_mfma_f32_16x16x32_bf16 v[78:81], v[238:241], v[218:221], v[78:81]
	v_mfma_f32_16x16x32_bf16 v[74:77], v[242:245], v[218:221], v[74:77]
	v_mfma_f32_16x16x32_bf16 v[70:73], v[246:249], v[218:221], v[70:73]
	v_mfma_f32_16x16x32_bf16 v[66:69], v[250:253], v[218:221], v[66:69]
	ds_read_b128 v[218:221], v93 offset:0
	ds_read_b128 v[142:145], v141 offset:0
	s_add_i32 s51, s51, 1
	s_and_b32 s54, s51, 7
	s_cmp_eq_u32 s54, 0
	s_cselect_b32 s44, s34, s35
	s_cselect_b32 s45, -1, 0
	v_lshl_add_u64 v[132:133], v[132:133], 0, s[44:45]
	global_load_dwordx2 v[114:115], v[132:133], off
	v_lshl_add_u64 v[180:181], v[132:133], 0, s[24:25]
	global_load_dwordx2 v[116:117], v[180:181], off
	v_mfma_f32_16x16x32_bf16 v[62:65], v[238:241], v[222:225], v[62:65]
	v_mfma_f32_16x16x32_bf16 v[58:61], v[242:245], v[222:225], v[58:61]
	v_mfma_f32_16x16x32_bf16 v[54:57], v[246:249], v[222:225], v[54:57]
	v_mfma_f32_16x16x32_bf16 v[50:53], v[250:253], v[222:225], v[50:53]
	ds_read_b128 v[222:225], v93 offset:2048
	ds_read_b128 v[146:149], v141 offset:2048
	v_lshl_add_u64 v[180:181], v[132:133], 0, s[26:27]
	global_load_dwordx2 v[118:119], v[180:181], off
	v_lshl_add_u64 v[180:181], v[132:133], 0, s[28:29]
	global_load_dwordx2 v[120:121], v[180:181], off
	v_mfma_f32_16x16x32_bf16 v[46:49], v[238:241], v[226:229], v[46:49]
	v_mfma_f32_16x16x32_bf16 v[42:45], v[242:245], v[226:229], v[42:45]
	v_mfma_f32_16x16x32_bf16 v[38:41], v[246:249], v[226:229], v[38:41]
	v_mfma_f32_16x16x32_bf16 v[34:37], v[250:253], v[226:229], v[34:37]
	ds_read_b128 v[226:229], v93 offset:4096
	ds_read_b128 v[156:159], v141 offset:4096
	v_lshl_add_u64 v[180:181], v[132:133], 0, s[36:37]
	global_load_dwordx2 v[122:123], v[180:181], off
	v_lshl_add_u64 v[180:181], v[132:133], 0, s[38:39]
	global_load_dwordx2 v[124:125], v[180:181], off
	v_mfma_f32_16x16x32_bf16 v[18:21], v[238:241], v[230:233], v[18:21]
	v_mfma_f32_16x16x32_bf16 v[22:25], v[242:245], v[230:233], v[22:25]
	v_mfma_f32_16x16x32_bf16 v[26:29], v[246:249], v[230:233], v[26:29]
	v_mfma_f32_16x16x32_bf16 v[30:33], v[250:253], v[230:233], v[30:33]
	ds_read_b128 v[230:233], v93 offset:6144
	ds_read_b128 v[160:163], v141 offset:6144
	v_lshl_add_u64 v[180:181], v[132:133], 0, s[40:41]
	global_load_dwordx2 v[126:127], v[180:181], off
	v_lshl_add_u64 v[180:181], v[132:133], 0, s[42:43]
	global_load_dwordx2 v[128:129], v[180:181], off
	v_mfma_f32_16x16x32_bf16 v[2:5], v[238:241], v[234:237], v[2:5]
	v_mfma_f32_16x16x32_bf16 v[6:9], v[242:245], v[234:237], v[6:9]
	v_mfma_f32_16x16x32_bf16 v[10:13], v[246:249], v[234:237], v[10:13]
	v_mfma_f32_16x16x32_bf16 v[14:17], v[250:253], v[234:237], v[14:17]
	ds_read_b128 v[234:237], v93 offset:8192
	s_waitcnt vmcnt(21)
	s_waitcnt lgkmcnt(0)
	s_barrier
; #define MD_GLDS_A(buf, tau) do { _Pragma("unroll") for (int i = 0; i < 5; ++i) if (amask & (1u << i)) \
;         __builtin_amdgcn_global_load_lds((const unsigned*)((const char*)HIDp + aoff[i] + (size_t)((tau) & 7) * 128), (PG8_LAS unsigned*)(MD_SA(buf) + wid * 1024 + i * 8192), 16, 0, 0); } while (0)
; #define MD_B_ISSUE(sb, tau) do { const char* kb_ = Bb + (size_t)((tau) >> 3) * 512 + (size_t)((tau) & 7) * (64 * (size_t)RB); _Pragma("unroll") for (int j = 0; j < 8; ++j) { const char* p_ = kb_ + (size_t)j * RB; \
;         asm volatile("global_load_dwordx2 %0, %1, off" : "=&v"(sb[j]) : "v"(p_) : "memory"); } } while (0)
; #define MD_B_WAIT(sb, N) asm volatile("s_waitcnt vmcnt(%8)" : "+v"(sb[0]), "+v"(sb[1]), "+v"(sb[2]), "+v"(sb[3]), "+v"(sb[4]), "+v"(sb[5]), "+v"(sb[6]), "+v"(sb[7]) : "n"(N) : "memory")
; #define MD_END(last) do { if (last) asm volatile("s_waitcnt vmcnt(0)" ::: "memory"); else asm volatile("s_waitcnt vmcnt(8)" ::: "memory"); \
;         asm volatile("s_waitcnt lgkmcnt(0)" ::: "memory"); __builtin_amdgcn_s_barrier(); asm volatile("" ::: "memory"); } while (0)
; __device__ __forceinline__ void moe_down_stream(PG8_LAS unsigned char* lds, int e, int cb0, int slot0, int nv, const bf16_t* HIDp, const float* Wd, bf16_t* Y, const float* slot_w, const int* slot_dst) {
;     ...
;     for (int t = 0; t < NT; t += 2) {
;         if (t + 2 < NT) MD_B_WAIT(s1, 8); else MD_B_WAIT(s1, 0);
;         MD_B_WRITE(s1, 1); __builtin_amdgcn_sched_barrier(0); MD_GLDS_A(1, t + 1); __builtin_amdgcn_sched_barrier(0);
;         if (t + 3 < NT) MD_B_ISSUE(s1, t + 3);
;         MD_COMPUTE(0);
;         MD_END(t + 3 >= NT);
;         if (t + 2 < NT) { MD_B_WAIT(s0, 8); MD_B_WRITE(s0, 0); __builtin_amdgcn_sched_barrier(0); MD_GLDS_A(0, t + 2); __builtin_amdgcn_sched_barrier(0); }
;         if (t + 4 < NT) MD_B_ISSUE(s0, t + 4);
;         MD_COMPUTE(1);
;         MD_END(t + 4 >= NT);
	s_mov_b32 s49, s46
	s_mov_b32 s46, s47
	s_mov_b32 s47, s48
	s_mov_b32 s48, s49
	s_add_i32 s49, s48, s74
	s_add_i32 s52, s52, 1
	s_and_b32 s54, s52, 7
	s_cmp_eq_u32 s54, 0
	s_cselect_b32 s54, s53, s32
	s_cselect_b32 s55, -1, 0
	s_add_u32 s30, s30, s54
	s_addc_u32 s31, s31, s55
	v_mfma_f32_16x16x32_bf16 v[78:81], v[142:145], v[218:221], v[78:81]
	v_mfma_f32_16x16x32_bf16 v[74:77], v[146:149], v[218:221], v[74:77]
	v_mfma_f32_16x16x32_bf16 v[70:73], v[156:159], v[218:221], v[70:73]
	v_mfma_f32_16x16x32_bf16 v[66:69], v[160:163], v[218:221], v[66:69]
	s_mov_b32 m0, s49
	s_nop 0
	global_load_lds_dwordx4 v88, s[30:31]
	v_mfma_f32_16x16x32_bf16 v[62:65], v[142:145], v[222:225], v[62:65]
	v_mfma_f32_16x16x32_bf16 v[58:61], v[146:149], v[222:225], v[58:61]
	v_mfma_f32_16x16x32_bf16 v[54:57], v[156:159], v[222:225], v[54:57]
	v_mfma_f32_16x16x32_bf16 v[50:53], v[160:163], v[222:225], v[50:53]
	s_add_i32 m0, s49, 0x2000
	s_nop 0
	global_load_lds_dwordx4 v90, s[30:31]
	v_mfma_f32_16x16x32_bf16 v[46:49], v[142:145], v[226:229], v[46:49]
	v_mfma_f32_16x16x32_bf16 v[42:45], v[146:149], v[226:229], v[42:45]
	v_mfma_f32_16x16x32_bf16 v[38:41], v[156:159], v[226:229], v[38:41]
	v_mfma_f32_16x16x32_bf16 v[34:37], v[160:163], v[226:229], v[34:37]
	s_add_i32 m0, s49, 0x4000
	s_nop 0
	global_load_lds_dwordx4 v92, s[30:31]
	v_mfma_f32_16x16x32_bf16 v[18:21], v[142:145], v[230:233], v[18:21]
	v_mfma_f32_16x16x32_bf16 v[22:25], v[146:149], v[230:233], v[22:25]
	v_mfma_f32_16x16x32_bf16 v[26:29], v[156:159], v[230:233], v[26:29]
	v_mfma_f32_16x16x32_bf16 v[30:33], v[160:163], v[230:233], v[30:33]
	s_add_i32 m0, s49, 0x6000
	s_nop 0
	global_load_lds_dwordx4 v94, s[30:31]
	v_mfma_f32_16x16x32_bf16 v[2:5], v[142:145], v[234:237], v[2:5]
	v_mfma_f32_16x16x32_bf16 v[6:9], v[146:149], v[234:237], v[6:9]
	v_mfma_f32_16x16x32_bf16 v[10:13], v[156:159], v[234:237], v[10:13]
	v_mfma_f32_16x16x32_bf16 v[14:17], v[160:163], v[234:237], v[14:17]
	s_add_i32 m0, s49, 0x8000
	s_nop 0
	global_load_lds_dwordx4 v96, s[30:31]
	v_cvt_pk_bf16_f32 v172, v186, v188
	v_cvt_pk_bf16_f32 v173, v190, v192
	v_cvt_pk_bf16_f32 v174, v194, v196
	v_cvt_pk_bf16_f32 v175, v198, v200
	v_cvt_pk_bf16_f32 v176, v187, v189
	v_cvt_pk_bf16_f32 v177, v191, v193
	v_cvt_pk_bf16_f32 v178, v195, v197
	v_cvt_pk_bf16_f32 v179, v199, v201
	ds_write_b128 v95, v[172:175] offset:0
	ds_write_b128 v95, v[176:179] offset:128
	v_add_u32_e32 v91, s46, v135
	v_add_u32_e32 v93, s46, v137
	ds_read_b128 v[238:241], v139 offset:19456
	ds_read_b128 v[242:245], v139 offset:21504
	ds_read_b128 v[246:249], v139 offset:23552
	ds_read_b128 v[250:253], v139 offset:25600
	ds_read_b128 v[218:221], v91 offset:0
	ds_read_b128 v[222:225], v91 offset:2048
	ds_read_b128 v[226:229], v91 offset:4096
	ds_read_b128 v[230:233], v91 offset:6144
	ds_read_b128 v[234:237], v91 offset:8192
	s_waitcnt lgkmcnt(0)
	v_mfma_f32_16x16x32_bf16 v[78:81], v[238:241], v[218:221], v[78:81]
	v_mfma_f32_16x16x32_bf16 v[74:77], v[242:245], v[218:221], v[74:77]
	v_mfma_f32_16x16x32_bf16 v[70:73], v[246:249], v[218:221], v[70:73]
	v_mfma_f32_16x16x32_bf16 v[66:69], v[250:253], v[218:221], v[66:69]
	ds_read_b128 v[218:221], v93 offset:0
	ds_read_b128 v[142:145], v141 offset:19456
	s_add_i32 s51, s51, 1
	s_and_b32 s54, s51, 7
	s_cmp_eq_u32 s54, 0
	s_cselect_b32 s44, s34, s35
	s_cselect_b32 s45, -1, 0
	v_lshl_add_u64 v[132:133], v[132:133], 0, s[44:45]
	global_load_dwordx2 v[186:187], v[132:133], off
	v_lshl_add_u64 v[180:181], v[132:133], 0, s[24:25]
	global_load_dwordx2 v[188:189], v[180:181], off
	v_mfma_f32_16x16x32_bf16 v[62:65], v[238:241], v[222:225], v[62:65]
	v_mfma_f32_16x16x32_bf16 v[58:61], v[242:245], v[222:225], v[58:61]
	v_mfma_f32_16x16x32_bf16 v[54:57], v[246:249], v[222:225], v[54:57]
	v_mfma_f32_16x16x32_bf16 v[50:53], v[250:253], v[222:225], v[50:53]
	ds_read_b128 v[222:225], v93 offset:2048
	ds_read_b128 v[146:149], v141 offset:21504
	v_lshl_add_u64 v[180:181], v[132:133], 0, s[26:27]
	global_load_dwordx2 v[190:191], v[180:181], off
	v_lshl_add_u64 v[180:181], v[132:133], 0, s[28:29]
	global_load_dwordx2 v[192:193], v[180:181], off
	v_mfma_f32_16x16x32_bf16 v[46:49], v[238:241], v[226:229], v[46:49]
	v_mfma_f32_16x16x32_bf16 v[42:45], v[242:245], v[226:229], v[42:45]
	v_mfma_f32_16x16x32_bf16 v[38:41], v[246:249], v[226:229], v[38:41]
	v_mfma_f32_16x16x32_bf16 v[34:37], v[250:253], v[226:229], v[34:37]
	ds_read_b128 v[226:229], v93 offset:4096
	ds_read_b128 v[156:159], v141 offset:23552
	v_lshl_add_u64 v[180:181], v[132:133], 0, s[36:37]
	global_load_dwordx2 v[194:195], v[180:181], off
	v_lshl_add_u64 v[180:181], v[132:133], 0, s[38:39]
	global_load_dwordx2 v[196:197], v[180:181], off
	v_mfma_f32_16x16x32_bf16 v[18:21], v[238:241], v[230:233], v[18:21]
	v_mfma_f32_16x16x32_bf16 v[22:25], v[242:245], v[230:233], v[22:25]
	v_mfma_f32_16x16x32_bf16 v[26:29], v[246:249], v[230:233], v[26:29]
	v_mfma_f32_16x16x32_bf16 v[30:33], v[250:253], v[230:233], v[30:33]
	ds_read_b128 v[230:233], v93 offset:6144
	ds_read_b128 v[160:163], v141 offset:25600
	v_lshl_add_u64 v[180:181], v[132:133], 0, s[40:41]
	global_load_dwordx2 v[198:199], v[180:181], off
	v_lshl_add_u64 v[180:181], v[132:133], 0, s[42:43]
	global_load_dwordx2 v[200:201], v[180:181], off
	v_mfma_f32_16x16x32_bf16 v[2:5], v[238:241], v[234:237], v[2:5]
	v_mfma_f32_16x16x32_bf16 v[6:9], v[242:245], v[234:237], v[6:9]
	v_mfma_f32_16x16x32_bf16 v[10:13], v[246:249], v[234:237], v[10:13]
	v_mfma_f32_16x16x32_bf16 v[14:17], v[250:253], v[234:237], v[14:17]
	ds_read_b128 v[234:237], v93 offset:8192
	s_waitcnt vmcnt(21)
	s_waitcnt lgkmcnt(0)
	s_barrier
; #define MD_GLDS_A(buf, tau) do { _Pragma("unroll") for (int i = 0; i < 5; ++i) if (amask & (1u << i)) \
;         __builtin_amdgcn_global_load_lds((const unsigned*)((const char*)HIDp + aoff[i] + (size_t)((tau) & 7) * 128), (PG8_LAS unsigned*)(MD_SA(buf) + wid * 1024 + i * 8192), 16, 0, 0); } while (0)
; #define MD_B_ISSUE(sb, tau) do { const char* kb_ = Bb + (size_t)((tau) >> 3) * 512 + (size_t)((tau) & 7) * (64 * (size_t)RB); _Pragma("unroll") for (int j = 0; j < 8; ++j) { const char* p_ = kb_ + (size_t)j * RB; \
;         asm volatile("global_load_dwordx2 %0, %1, off" : "=&v"(sb[j]) : "v"(p_) : "memory"); } } while (0)
; #define MD_B_WAIT(sb, N) asm volatile("s_waitcnt vmcnt(%8)" : "+v"(sb[0]), "+v"(sb[1]), "+v"(sb[2]), "+v"(sb[3]), "+v"(sb[4]), "+v"(sb[5]), "+v"(sb[6]), "+v"(sb[7]) : "n"(N) : "memory")
; #define MD_END(last) do { if (last) asm volatile("s_waitcnt vmcnt(0)" ::: "memory"); else asm volatile("s_waitcnt vmcnt(8)" ::: "memory"); \
;         asm volatile("s_waitcnt lgkmcnt(0)" ::: "memory"); __builtin_amdgcn_s_barrier(); asm volatile("" ::: "memory"); } while (0)
; __device__ __forceinline__ void moe_down_stream(PG8_LAS unsigned char* lds, int e, int cb0, int slot0, int nv, const bf16_t* HIDp, const float* Wd, bf16_t* Y, const float* slot_w, const int* slot_dst) {
;     ...
;     for (int t = 0; t < NT; t += 2) {
;         if (t + 2 < NT) MD_B_WAIT(s1, 8); else MD_B_WAIT(s1, 0);
;         MD_B_WRITE(s1, 1); __builtin_amdgcn_sched_barrier(0); MD_GLDS_A(1, t + 1); __builtin_amdgcn_sched_barrier(0);
;         if (t + 3 < NT) MD_B_ISSUE(s1, t + 3);
;         MD_COMPUTE(0);
;         MD_END(t + 3 >= NT);
;         if (t + 2 < NT) { MD_B_WAIT(s0, 8); MD_B_WRITE(s0, 0); __builtin_amdgcn_sched_barrier(0); MD_GLDS_A(0, t + 2); __builtin_amdgcn_sched_barrier(0); }
;         if (t + 4 < NT) MD_B_ISSUE(s0, t + 4);
;         MD_COMPUTE(1);
;         MD_END(t + 4 >= NT);
	s_mov_b32 s49, s46
	s_mov_b32 s46, s47
	s_mov_b32 s47, s48
	s_mov_b32 s48, s49
	s_add_i32 s49, s48, s74
	s_add_i32 s52, s52, 1
	s_and_b32 s54, s52, 7
	s_cmp_eq_u32 s54, 0
	s_cselect_b32 s54, s53, s32
	s_cselect_b32 s55, -1, 0
	s_add_u32 s30, s30, s54
	s_addc_u32 s31, s31, s55
	v_mfma_f32_16x16x32_bf16 v[78:81], v[142:145], v[218:221], v[78:81]
	v_mfma_f32_16x16x32_bf16 v[74:77], v[146:149], v[218:221], v[74:77]
	v_mfma_f32_16x16x32_bf16 v[70:73], v[156:159], v[218:221], v[70:73]
	v_mfma_f32_16x16x32_bf16 v[66:69], v[160:163], v[218:221], v[66:69]
	s_mov_b32 m0, s49
	s_nop 0
	global_load_lds_dwordx4 v88, s[30:31]
	v_mfma_f32_16x16x32_bf16 v[62:65], v[142:145], v[222:225], v[62:65]
	v_mfma_f32_16x16x32_bf16 v[58:61], v[146:149], v[222:225], v[58:61]
	v_mfma_f32_16x16x32_bf16 v[54:57], v[156:159], v[222:225], v[54:57]
	v_mfma_f32_16x16x32_bf16 v[50:53], v[160:163], v[222:225], v[50:53]
	s_add_i32 m0, s49, 0x2000
	s_nop 0
	global_load_lds_dwordx4 v90, s[30:31]
	v_mfma_f32_16x16x32_bf16 v[46:49], v[142:145], v[226:229], v[46:49]
	v_mfma_f32_16x16x32_bf16 v[42:45], v[146:149], v[226:229], v[42:45]
	v_mfma_f32_16x16x32_bf16 v[38:41], v[156:159], v[226:229], v[38:41]
	v_mfma_f32_16x16x32_bf16 v[34:37], v[160:163], v[226:229], v[34:37]
	s_add_i32 m0, s49, 0x4000
	s_nop 0
	global_load_lds_dwordx4 v92, s[30:31]
	v_mfma_f32_16x16x32_bf16 v[18:21], v[142:145], v[230:233], v[18:21]
	v_mfma_f32_16x16x32_bf16 v[22:25], v[146:149], v[230:233], v[22:25]
	v_mfma_f32_16x16x32_bf16 v[26:29], v[156:159], v[230:233], v[26:29]
	v_mfma_f32_16x16x32_bf16 v[30:33], v[160:163], v[230:233], v[30:33]
	s_add_i32 m0, s49, 0x6000
	s_nop 0
	global_load_lds_dwordx4 v94, s[30:31]
	v_mfma_f32_16x16x32_bf16 v[2:5], v[142:145], v[234:237], v[2:5]
	v_mfma_f32_16x16x32_bf16 v[6:9], v[146:149], v[234:237], v[6:9]
	v_mfma_f32_16x16x32_bf16 v[10:13], v[156:159], v[234:237], v[10:13]
	v_mfma_f32_16x16x32_bf16 v[14:17], v[160:163], v[234:237], v[14:17]
	s_add_i32 m0, s49, 0x8000
	s_nop 0
	global_load_lds_dwordx4 v96, s[30:31]
	v_cvt_pk_bf16_f32 v172, v202, v204
	v_cvt_pk_bf16_f32 v173, v206, v208
	v_cvt_pk_bf16_f32 v174, v210, v212
	v_cvt_pk_bf16_f32 v175, v214, v216
	v_cvt_pk_bf16_f32 v176, v203, v205
	v_cvt_pk_bf16_f32 v177, v207, v209
	v_cvt_pk_bf16_f32 v178, v211, v213
	v_cvt_pk_bf16_f32 v179, v215, v217
	ds_write_b128 v95, v[172:175] offset:19456
	ds_write_b128 v95, v[176:179] offset:19584
	v_add_u32_e32 v91, s46, v135
	v_add_u32_e32 v93, s46, v137
	ds_read_b128 v[238:241], v139 offset:0
	ds_read_b128 v[242:245], v139 offset:2048
	ds_read_b128 v[246:249], v139 offset:4096
	ds_read_b128 v[250:253], v139 offset:6144
	ds_read_b128 v[218:221], v91 offset:0
	ds_read_b128 v[222:225], v91 offset:2048
	ds_read_b128 v[226:229], v91 offset:4096
	ds_read_b128 v[230:233], v91 offset:6144
	ds_read_b128 v[234:237], v91 offset:8192
	s_waitcnt lgkmcnt(0)
	v_mfma_f32_16x16x32_bf16 v[78:81], v[238:241], v[218:221], v[78:81]
	v_mfma_f32_16x16x32_bf16 v[74:77], v[242:245], v[218:221], v[74:77]
	v_mfma_f32_16x16x32_bf16 v[70:73], v[246:249], v[218:221], v[70:73]
	v_mfma_f32_16x16x32_bf16 v[66:69], v[250:253], v[218:221], v[66:69]
	ds_read_b128 v[218:221], v93 offset:0
	ds_read_b128 v[142:145], v141 offset:0
	s_add_i32 s51, s51, 1
	s_and_b32 s54, s51, 7
	s_cmp_eq_u32 s54, 0
	s_cselect_b32 s44, s34, s35
	s_cselect_b32 s45, -1, 0
	v_lshl_add_u64 v[132:133], v[132:133], 0, s[44:45]
	global_load_dwordx2 v[202:203], v[132:133], off
	v_lshl_add_u64 v[180:181], v[132:133], 0, s[24:25]
	global_load_dwordx2 v[204:205], v[180:181], off
	v_mfma_f32_16x16x32_bf16 v[62:65], v[238:241], v[222:225], v[62:65]
	v_mfma_f32_16x16x32_bf16 v[58:61], v[242:245], v[222:225], v[58:61]
	v_mfma_f32_16x16x32_bf16 v[54:57], v[246:249], v[222:225], v[54:57]
	v_mfma_f32_16x16x32_bf16 v[50:53], v[250:253], v[222:225], v[50:53]
	ds_read_b128 v[222:225], v93 offset:2048
	ds_read_b128 v[146:149], v141 offset:2048
	v_lshl_add_u64 v[180:181], v[132:133], 0, s[26:27]
	global_load_dwordx2 v[206:207], v[180:181], off
	v_lshl_add_u64 v[180:181], v[132:133], 0, s[28:29]
	global_load_dwordx2 v[208:209], v[180:181], off
	v_mfma_f32_16x16x32_bf16 v[46:49], v[238:241], v[226:229], v[46:49]
	v_mfma_f32_16x16x32_bf16 v[42:45], v[242:245], v[226:229], v[42:45]
	v_mfma_f32_16x16x32_bf16 v[38:41], v[246:249], v[226:229], v[38:41]
	v_mfma_f32_16x16x32_bf16 v[34:37], v[250:253], v[226:229], v[34:37]
	ds_read_b128 v[226:229], v93 offset:4096
	ds_read_b128 v[156:159], v141 offset:4096
	v_lshl_add_u64 v[180:181], v[132:133], 0, s[36:37]
	global_load_dwordx2 v[210:211], v[180:181], off
	v_lshl_add_u64 v[180:181], v[132:133], 0, s[38:39]
	global_load_dwordx2 v[212:213], v[180:181], off
	v_mfma_f32_16x16x32_bf16 v[18:21], v[238:241], v[230:233], v[18:21]
	v_mfma_f32_16x16x32_bf16 v[22:25], v[242:245], v[230:233], v[22:25]
	v_mfma_f32_16x16x32_bf16 v[26:29], v[246:249], v[230:233], v[26:29]
	v_mfma_f32_16x16x32_bf16 v[30:33], v[250:253], v[230:233], v[30:33]
	ds_read_b128 v[230:233], v93 offset:6144
	ds_read_b128 v[160:163], v141 offset:6144
	v_lshl_add_u64 v[180:181], v[132:133], 0, s[40:41]
	global_load_dwordx2 v[214:215], v[180:181], off
	v_lshl_add_u64 v[180:181], v[132:133], 0, s[42:43]
	global_load_dwordx2 v[216:217], v[180:181], off
	v_mfma_f32_16x16x32_bf16 v[2:5], v[238:241], v[234:237], v[2:5]
	v_mfma_f32_16x16x32_bf16 v[6:9], v[242:245], v[234:237], v[6:9]
	v_mfma_f32_16x16x32_bf16 v[10:13], v[246:249], v[234:237], v[10:13]
	v_mfma_f32_16x16x32_bf16 v[14:17], v[250:253], v[234:237], v[14:17]
	ds_read_b128 v[234:237], v93 offset:8192
	s_waitcnt vmcnt(21)
	s_waitcnt lgkmcnt(0)
	s_barrier
; #define MD_GLDS_A(buf, tau) do { _Pragma("unroll") for (int i = 0; i < 5; ++i) if (amask & (1u << i)) \
;         __builtin_amdgcn_global_load_lds((const unsigned*)((const char*)HIDp + aoff[i] + (size_t)((tau) & 7) * 128), (PG8_LAS unsigned*)(MD_SA(buf) + wid * 1024 + i * 8192), 16, 0, 0); } while (0)
; #define MD_B_ISSUE(sb, tau) do { const char* kb_ = Bb + (size_t)((tau) >> 3) * 512 + (size_t)((tau) & 7) * (64 * (size_t)RB); _Pragma("unroll") for (int j = 0; j < 8; ++j) { const char* p_ = kb_ + (size_t)j * RB; \
;         asm volatile("global_load_dwordx2 %0, %1, off" : "=&v"(sb[j]) : "v"(p_) : "memory"); } } while (0)
; #define MD_B_WAIT(sb, N) asm volatile("s_waitcnt vmcnt(%8)" : "+v"(sb[0]), "+v"(sb[1]), "+v"(sb[2]), "+v"(sb[3]), "+v"(sb[4]), "+v"(sb[5]), "+v"(sb[6]), "+v"(sb[7]) : "n"(N) : "memory")
; #define MD_END(last) do { if (last) asm volatile("s_waitcnt vmcnt(0)" ::: "memory"); else asm volatile("s_waitcnt vmcnt(8)" ::: "memory"); \
;         asm volatile("s_waitcnt lgkmcnt(0)" ::: "memory"); __builtin_amdgcn_s_barrier(); asm volatile("" ::: "memory"); } while (0)
; __device__ __forceinline__ void moe_down_stream(PG8_LAS unsigned char* lds, int e, int cb0, int slot0, int nv, const bf16_t* HIDp, const float* Wd, bf16_t* Y, const float* slot_w, const int* slot_dst) {
;     ...
;     for (int t = 0; t < NT; t += 2) {
;         if (t + 2 < NT) MD_B_WAIT(s1, 8); else MD_B_WAIT(s1, 0);
;         MD_B_WRITE(s1, 1); __builtin_amdgcn_sched_barrier(0); MD_GLDS_A(1, t + 1); __builtin_amdgcn_sched_barrier(0);
;         if (t + 3 < NT) MD_B_ISSUE(s1, t + 3);
;         MD_COMPUTE(0);
;         MD_END(t + 3 >= NT);
;         if (t + 2 < NT) { MD_B_WAIT(s0, 8); MD_B_WRITE(s0, 0); __builtin_amdgcn_sched_barrier(0); MD_GLDS_A(0, t + 2); __builtin_amdgcn_sched_barrier(0); }
;         if (t + 4 < NT) MD_B_ISSUE(s0, t + 4);
;         MD_COMPUTE(1);
;         MD_END(t + 4 >= NT);
	s_mov_b32 s49, s46
	s_mov_b32 s46, s47
	s_mov_b32 s47, s48
	s_mov_b32 s48, s49
	s_add_i32 s49, s48, s74
	s_add_i32 s52, s52, 1
	s_and_b32 s54, s52, 7
	s_cmp_eq_u32 s54, 0
	s_cselect_b32 s54, s53, s32
	s_cselect_b32 s55, -1, 0
	s_add_u32 s30, s30, s54
	s_addc_u32 s31, s31, s55
	v_mfma_f32_16x16x32_bf16 v[78:81], v[142:145], v[218:221], v[78:81]
	v_mfma_f32_16x16x32_bf16 v[74:77], v[146:149], v[218:221], v[74:77]
	v_mfma_f32_16x16x32_bf16 v[70:73], v[156:159], v[218:221], v[70:73]
	v_mfma_f32_16x16x32_bf16 v[66:69], v[160:163], v[218:221], v[66:69]
	s_mov_b32 m0, s49
	s_nop 0
	global_load_lds_dwordx4 v88, s[30:31]
	v_mfma_f32_16x16x32_bf16 v[62:65], v[142:145], v[222:225], v[62:65]
	v_mfma_f32_16x16x32_bf16 v[58:61], v[146:149], v[222:225], v[58:61]
	v_mfma_f32_16x16x32_bf16 v[54:57], v[156:159], v[222:225], v[54:57]
	v_mfma_f32_16x16x32_bf16 v[50:53], v[160:163], v[222:225], v[50:53]
	s_add_i32 m0, s49, 0x2000
	s_nop 0
	global_load_lds_dwordx4 v90, s[30:31]
	v_mfma_f32_16x16x32_bf16 v[46:49], v[142:145], v[226:229], v[46:49]
	v_mfma_f32_16x16x32_bf16 v[42:45], v[146:149], v[226:229], v[42:45]
	v_mfma_f32_16x16x32_bf16 v[38:41], v[156:159], v[226:229], v[38:41]
	v_mfma_f32_16x16x32_bf16 v[34:37], v[160:163], v[226:229], v[34:37]
	s_add_i32 m0, s49, 0x4000
	s_nop 0
	global_load_lds_dwordx4 v92, s[30:31]
	v_mfma_f32_16x16x32_bf16 v[18:21], v[142:145], v[230:233], v[18:21]
	v_mfma_f32_16x16x32_bf16 v[22:25], v[146:149], v[230:233], v[22:25]
	v_mfma_f32_16x16x32_bf16 v[26:29], v[156:159], v[230:233], v[26:29]
	v_mfma_f32_16x16x32_bf16 v[30:33], v[160:163], v[230:233], v[30:33]
	s_add_i32 m0, s49, 0x6000
	s_nop 0
	global_load_lds_dwordx4 v94, s[30:31]
	v_mfma_f32_16x16x32_bf16 v[2:5], v[142:145], v[234:237], v[2:5]
	v_mfma_f32_16x16x32_bf16 v[6:9], v[146:149], v[234:237], v[6:9]
	v_mfma_f32_16x16x32_bf16 v[10:13], v[156:159], v[234:237], v[10:13]
	v_mfma_f32_16x16x32_bf16 v[14:17], v[160:163], v[234:237], v[14:17]
	s_add_i32 m0, s49, 0x8000
	s_nop 0
	global_load_lds_dwordx4 v96, s[30:31]
	v_cvt_pk_bf16_f32 v172, v98, v100
	v_cvt_pk_bf16_f32 v173, v102, v104
	v_cvt_pk_bf16_f32 v174, v106, v108
	v_cvt_pk_bf16_f32 v175, v110, v112
	v_cvt_pk_bf16_f32 v176, v99, v101
	v_cvt_pk_bf16_f32 v177, v103, v105
	v_cvt_pk_bf16_f32 v178, v107, v109
	v_cvt_pk_bf16_f32 v179, v111, v113
	ds_write_b128 v95, v[172:175] offset:0
	ds_write_b128 v95, v[176:179] offset:128
	v_add_u32_e32 v91, s46, v135
	v_add_u32_e32 v93, s46, v137
	ds_read_b128 v[238:241], v139 offset:19456
	ds_read_b128 v[242:245], v139 offset:21504
	ds_read_b128 v[246:249], v139 offset:23552
	ds_read_b128 v[250:253], v139 offset:25600
	ds_read_b128 v[218:221], v91 offset:0
	ds_read_b128 v[222:225], v91 offset:2048
	ds_read_b128 v[226:229], v91 offset:4096
	ds_read_b128 v[230:233], v91 offset:6144
	ds_read_b128 v[234:237], v91 offset:8192
	s_waitcnt lgkmcnt(0)
	v_mfma_f32_16x16x32_bf16 v[78:81], v[238:241], v[218:221], v[78:81]
	v_mfma_f32_16x16x32_bf16 v[74:77], v[242:245], v[218:221], v[74:77]
	v_mfma_f32_16x16x32_bf16 v[70:73], v[246:249], v[218:221], v[70:73]
	v_mfma_f32_16x16x32_bf16 v[66:69], v[250:253], v[218:221], v[66:69]
	ds_read_b128 v[218:221], v93 offset:0
	ds_read_b128 v[142:145], v141 offset:19456
	s_add_i32 s51, s51, 1
	s_and_b32 s54, s51, 7
	s_cmp_eq_u32 s54, 0
	s_cselect_b32 s44, s34, s35
	s_cselect_b32 s45, -1, 0
	v_lshl_add_u64 v[132:133], v[132:133], 0, s[44:45]
	global_load_dwordx2 v[98:99], v[132:133], off
	v_lshl_add_u64 v[180:181], v[132:133], 0, s[24:25]
	global_load_dwordx2 v[100:101], v[180:181], off
	v_mfma_f32_16x16x32_bf16 v[62:65], v[238:241], v[222:225], v[62:65]
	v_mfma_f32_16x16x32_bf16 v[58:61], v[242:245], v[222:225], v[58:61]
	v_mfma_f32_16x16x32_bf16 v[54:57], v[246:249], v[222:225], v[54:57]
	v_mfma_f32_16x16x32_bf16 v[50:53], v[250:253], v[222:225], v[50:53]
	ds_read_b128 v[222:225], v93 offset:2048
	ds_read_b128 v[146:149], v141 offset:21504
	v_lshl_add_u64 v[180:181], v[132:133], 0, s[26:27]
	global_load_dwordx2 v[102:103], v[180:181], off
	v_lshl_add_u64 v[180:181], v[132:133], 0, s[28:29]
	global_load_dwordx2 v[104:105], v[180:181], off
	v_mfma_f32_16x16x32_bf16 v[46:49], v[238:241], v[226:229], v[46:49]
	v_mfma_f32_16x16x32_bf16 v[42:45], v[242:245], v[226:229], v[42:45]
	v_mfma_f32_16x16x32_bf16 v[38:41], v[246:249], v[226:229], v[38:41]
	v_mfma_f32_16x16x32_bf16 v[34:37], v[250:253], v[226:229], v[34:37]
	ds_read_b128 v[226:229], v93 offset:4096
	ds_read_b128 v[156:159], v141 offset:23552
	v_lshl_add_u64 v[180:181], v[132:133], 0, s[36:37]
	global_load_dwordx2 v[106:107], v[180:181], off
	v_lshl_add_u64 v[180:181], v[132:133], 0, s[38:39]
	global_load_dwordx2 v[108:109], v[180:181], off
	v_mfma_f32_16x16x32_bf16 v[18:21], v[238:241], v[230:233], v[18:21]
	v_mfma_f32_16x16x32_bf16 v[22:25], v[242:245], v[230:233], v[22:25]
	v_mfma_f32_16x16x32_bf16 v[26:29], v[246:249], v[230:233], v[26:29]
	v_mfma_f32_16x16x32_bf16 v[30:33], v[250:253], v[230:233], v[30:33]
	ds_read_b128 v[230:233], v93 offset:6144
	ds_read_b128 v[160:163], v141 offset:25600
	v_lshl_add_u64 v[180:181], v[132:133], 0, s[40:41]
	global_load_dwordx2 v[110:111], v[180:181], off
	v_lshl_add_u64 v[180:181], v[132:133], 0, s[42:43]
	global_load_dwordx2 v[112:113], v[180:181], off
	v_mfma_f32_16x16x32_bf16 v[2:5], v[238:241], v[234:237], v[2:5]
	v_mfma_f32_16x16x32_bf16 v[6:9], v[242:245], v[234:237], v[6:9]
	v_mfma_f32_16x16x32_bf16 v[10:13], v[246:249], v[234:237], v[10:13]
	v_mfma_f32_16x16x32_bf16 v[14:17], v[250:253], v[234:237], v[14:17]
	ds_read_b128 v[234:237], v93 offset:8192
	s_waitcnt vmcnt(21)
	s_waitcnt lgkmcnt(0)
	s_barrier
; #define PG8_LAS __attribute__((address_space(3)))
; __device__ __forceinline__ unsigned cvtpk(float lo, float hi) { f32x2 v = {lo, hi}; bf16x2_t b = __builtin_convertvector(v, bf16x2_t); return __builtin_bit_cast(unsigned, b); }
; __device__ __forceinline__ void moe_down_stream(PG8_LAS unsigned char* lds, int e, int cb0, int slot0, int nv, const bf16_t* HIDp, const float* Wd, bf16_t* Y, const float* slot_w, const int* slot_dst) {
;     ...
;         if (((t + 1) & 7) == 7) {
;             const int cb = cb0 + ((t + 1) >> 3);
; #pragma unroll
;             for (int m = 0; m < DNM; ++m) {
;                 const float w_ = lw[4 * (16 * m + fr) + wr];
; #pragma unroll
;                 for (int p = 0; p < 2; ++p) { const f32x4 v0 = acc[m][2 * p] * w_, v1 = acc[m][2 * p + 1] * w_; u32x4 w; w.x = cvtpk(v0[0], v0[1]); w.y = cvtpk(v0[2], v0[3]); w.z = cvtpk(v1[0], v1[1]); w.w = cvtpk(v1[2], v1[3]);
;                     *(PG8_LAS u32x4*)(stg + fr * 128 + (((4 * p + fq) ^ (fr & 7)) * 16)) = w; }
; #pragma unroll
;                 for (int hh = 0; hh < 2; ++hh) { const int r = (lane >> 3) + 8 * hh, cc = lane & 7; const u32x4 d = *(const PG8_LAS u32x4*)(stg + r * 128 + ((cc ^ (r & 7)) * 16)); const int dst_ = ldst[4 * (16 * m + r) + wr];
;                     if (dst_ >= 0) *(u32x4*)(Y + (size_t)dst_ * D + 128 * cb + 64 * wc + 8 * cc) = d; }
; #pragma unroll
;                 for (int n = 0; n < 4; ++n) acc[m][n] = (f32x4){0.f, 0.f, 0.f, 0.f}; } }
	s_mov_b32 s49, s46
	s_mov_b32 s46, s47
	s_mov_b32 s47, s48
	s_mov_b32 s48, s49
	v_mfma_f32_16x16x32_bf16 v[78:81], v[142:145], v[218:221], v[78:81]
	v_mfma_f32_16x16x32_bf16 v[74:77], v[146:149], v[218:221], v[74:77]
	v_mfma_f32_16x16x32_bf16 v[70:73], v[156:159], v[218:221], v[70:73]
	v_mfma_f32_16x16x32_bf16 v[66:69], v[160:163], v[218:221], v[66:69]
	v_mfma_f32_16x16x32_bf16 v[62:65], v[142:145], v[222:225], v[62:65]
	v_mfma_f32_16x16x32_bf16 v[58:61], v[146:149], v[222:225], v[58:61]
	v_mfma_f32_16x16x32_bf16 v[54:57], v[156:159], v[222:225], v[54:57]
	v_mfma_f32_16x16x32_bf16 v[50:53], v[160:163], v[222:225], v[50:53]
	v_mfma_f32_16x16x32_bf16 v[46:49], v[142:145], v[226:229], v[46:49]
	v_mfma_f32_16x16x32_bf16 v[42:45], v[146:149], v[226:229], v[42:45]
	v_mfma_f32_16x16x32_bf16 v[38:41], v[156:159], v[226:229], v[38:41]
	v_mfma_f32_16x16x32_bf16 v[34:37], v[160:163], v[226:229], v[34:37]
	v_mfma_f32_16x16x32_bf16 v[18:21], v[142:145], v[230:233], v[18:21]
	v_mfma_f32_16x16x32_bf16 v[22:25], v[146:149], v[230:233], v[22:25]
	v_mfma_f32_16x16x32_bf16 v[26:29], v[156:159], v[230:233], v[26:29]
	v_mfma_f32_16x16x32_bf16 v[30:33], v[160:163], v[230:233], v[30:33]
	v_mfma_f32_16x16x32_bf16 v[2:5], v[142:145], v[234:237], v[2:5]
	v_mfma_f32_16x16x32_bf16 v[6:9], v[146:149], v[234:237], v[6:9]
	v_mfma_f32_16x16x32_bf16 v[10:13], v[156:159], v[234:237], v[10:13]
	v_mfma_f32_16x16x32_bf16 v[14:17], v[160:163], v[234:237], v[14:17]
	s_add_i32 s54, s48, s74
	v_add_u32_e32 v164, s54, v84
	v_add_u32_e32 v165, s54, v85
	ds_read_b32 v150, v82 offset:0
	ds_read_b32 v151, v83 offset:0
	ds_read_b32 v166, v83 offset:128
	s_waitcnt lgkmcnt(2)
	v_mul_f32_e32 v78, v150, v78
	v_mul_f32_e32 v79, v150, v79
	v_mul_f32_e32 v80, v150, v80
	v_mul_f32_e32 v81, v150, v81
	v_mul_f32_e32 v74, v150, v74
	v_mul_f32_e32 v75, v150, v75
	v_mul_f32_e32 v76, v150, v76
	v_mul_f32_e32 v77, v150, v77
	v_cvt_pk_bf16_f32 v182, v78, v79
	v_cvt_pk_bf16_f32 v183, v80, v81
	v_cvt_pk_bf16_f32 v184, v74, v75
	v_cvt_pk_bf16_f32 v185, v76, v77
	ds_write_b128 v164, v[182:185]
	v_mul_f32_e32 v70, v150, v70
	v_mul_f32_e32 v71, v150, v71
	v_mul_f32_e32 v72, v150, v72
	v_mul_f32_e32 v73, v150, v73
	v_mul_f32_e32 v66, v150, v66
	v_mul_f32_e32 v67, v150, v67
	v_mul_f32_e32 v68, v150, v68
	v_mul_f32_e32 v69, v150, v69
	v_cvt_pk_bf16_f32 v182, v70, v71
	v_cvt_pk_bf16_f32 v183, v72, v73
	v_cvt_pk_bf16_f32 v184, v66, v67
	v_cvt_pk_bf16_f32 v185, v68, v69
	v_xor_b32_e32 v167, 64, v164
	ds_write_b128 v167, v[182:185]
	v_mov_b32_e32 v78, 0
	v_mov_b32_e32 v74, 0
	v_mov_b32_e32 v70, 0
	v_mov_b32_e32 v66, 0
	v_mov_b32_e32 v79, 0
	v_mov_b32_e32 v75, 0
	v_mov_b32_e32 v71, 0
	v_mov_b32_e32 v67, 0
	v_mov_b32_e32 v80, 0
	v_mov_b32_e32 v76, 0
	v_mov_b32_e32 v72, 0
	v_mov_b32_e32 v68, 0
	v_mov_b32_e32 v81, 0
	v_mov_b32_e32 v77, 0
	v_mov_b32_e32 v73, 0
	v_mov_b32_e32 v69, 0
	ds_read_b128 v[182:185], v165 offset:0
	v_cmp_lt_i32_e32 vcc, -1, v151
	v_lshlrev_b32_e32 v148, 13, v151
	v_mov_b32_e32 v149, 0
	v_lshl_add_u64 v[148:149], v[148:149], 0, v[86:87]
	v_cndmask_b32_e32 v148, v168, v148, vcc
	v_cndmask_b32_e32 v149, v169, v149, vcc
	s_waitcnt lgkmcnt(0)
	global_store_dwordx4 v[148:149], v[182:185], off
	ds_read_b128 v[182:185], v165 offset:8192
	v_cmp_lt_i32_e32 vcc, -1, v166
	v_lshlrev_b32_e32 v148, 13, v166
	v_mov_b32_e32 v149, 0
	v_lshl_add_u64 v[148:149], v[148:149], 0, v[86:87]
	v_cndmask_b32_e32 v148, v168, v148, vcc
	v_cndmask_b32_e32 v149, v169, v149, vcc
	s_waitcnt lgkmcnt(0)
	global_store_dwordx4 v[148:149], v[182:185], off
	ds_read_b32 v150, v82 offset:256
	ds_read_b32 v151, v83 offset:256
	ds_read_b32 v166, v83 offset:384
	s_waitcnt lgkmcnt(2)
	v_mul_f32_e32 v62, v150, v62
	v_mul_f32_e32 v63, v150, v63
	v_mul_f32_e32 v64, v150, v64
	v_mul_f32_e32 v65, v150, v65
	v_mul_f32_e32 v58, v150, v58
	v_mul_f32_e32 v59, v150, v59
	v_mul_f32_e32 v60, v150, v60
	v_mul_f32_e32 v61, v150, v61
	v_cvt_pk_bf16_f32 v182, v62, v63
	v_cvt_pk_bf16_f32 v183, v64, v65
	v_cvt_pk_bf16_f32 v184, v58, v59
	v_cvt_pk_bf16_f32 v185, v60, v61
	ds_write_b128 v164, v[182:185]
	v_mul_f32_e32 v54, v150, v54
	v_mul_f32_e32 v55, v150, v55
	v_mul_f32_e32 v56, v150, v56
	v_mul_f32_e32 v57, v150, v57
	v_mul_f32_e32 v50, v150, v50
	v_mul_f32_e32 v51, v150, v51
	v_mul_f32_e32 v52, v150, v52
	v_mul_f32_e32 v53, v150, v53
	v_cvt_pk_bf16_f32 v182, v54, v55
	v_cvt_pk_bf16_f32 v183, v56, v57
	v_cvt_pk_bf16_f32 v184, v50, v51
	v_cvt_pk_bf16_f32 v185, v52, v53
	v_xor_b32_e32 v167, 64, v164
	ds_write_b128 v167, v[182:185]
	v_mov_b32_e32 v62, 0
	v_mov_b32_e32 v58, 0
	v_mov_b32_e32 v54, 0
	v_mov_b32_e32 v50, 0
	v_mov_b32_e32 v63, 0
	v_mov_b32_e32 v59, 0
	v_mov_b32_e32 v55, 0
	v_mov_b32_e32 v51, 0
	v_mov_b32_e32 v64, 0
	v_mov_b32_e32 v60, 0
	v_mov_b32_e32 v56, 0
	v_mov_b32_e32 v52, 0
	v_mov_b32_e32 v65, 0
	v_mov_b32_e32 v61, 0
	v_mov_b32_e32 v57, 0
	v_mov_b32_e32 v53, 0
	ds_read_b128 v[182:185], v165 offset:0
	v_cmp_lt_i32_e32 vcc, -1, v151
	v_lshlrev_b32_e32 v148, 13, v151
	v_mov_b32_e32 v149, 0
	v_lshl_add_u64 v[148:149], v[148:149], 0, v[86:87]
	v_cndmask_b32_e32 v148, v168, v148, vcc
	v_cndmask_b32_e32 v149, v169, v149, vcc
	s_waitcnt lgkmcnt(0)
	global_store_dwordx4 v[148:149], v[182:185], off
	ds_read_b128 v[182:185], v165 offset:8192
	v_cmp_lt_i32_e32 vcc, -1, v166
	v_lshlrev_b32_e32 v148, 13, v166
	v_mov_b32_e32 v149, 0
	v_lshl_add_u64 v[148:149], v[148:149], 0, v[86:87]
	v_cndmask_b32_e32 v148, v168, v148, vcc
	v_cndmask_b32_e32 v149, v169, v149, vcc
	s_waitcnt lgkmcnt(0)
	global_store_dwordx4 v[148:149], v[182:185], off
	ds_read_b32 v150, v82 offset:512
	ds_read_b32 v151, v83 offset:512
	ds_read_b32 v166, v83 offset:640
	s_waitcnt lgkmcnt(2)
; #define PG8_LAS __attribute__((address_space(3)))
; __device__ __forceinline__ unsigned cvtpk(float lo, float hi) { f32x2 v = {lo, hi}; bf16x2_t b = __builtin_convertvector(v, bf16x2_t); return __builtin_bit_cast(unsigned, b); }
; __device__ __forceinline__ void moe_down_stream(PG8_LAS unsigned char* lds, int e, int cb0, int slot0, int nv, const bf16_t* HIDp, const float* Wd, bf16_t* Y, const float* slot_w, const int* slot_dst) {
;     ...
;         if (((t + 1) & 7) == 7) {
;             const int cb = cb0 + ((t + 1) >> 3);
; #pragma unroll
;             for (int m = 0; m < DNM; ++m) {
;                 const float w_ = lw[4 * (16 * m + fr) + wr];
; #pragma unroll
;                 for (int p = 0; p < 2; ++p) { const f32x4 v0 = acc[m][2 * p] * w_, v1 = acc[m][2 * p + 1] * w_; u32x4 w; w.x = cvtpk(v0[0], v0[1]); w.y = cvtpk(v0[2], v0[3]); w.z = cvtpk(v1[0], v1[1]); w.w = cvtpk(v1[2], v1[3]);
;                     *(PG8_LAS u32x4*)(stg + fr * 128 + (((4 * p + fq) ^ (fr & 7)) * 16)) = w; }
; #pragma unroll
;                 for (int hh = 0; hh < 2; ++hh) { const int r = (lane >> 3) + 8 * hh, cc = lane & 7; const u32x4 d = *(const PG8_LAS u32x4*)(stg + r * 128 + ((cc ^ (r & 7)) * 16)); const int dst_ = ldst[4 * (16 * m + r) + wr];
;                     if (dst_ >= 0) *(u32x4*)(Y + (size_t)dst_ * D + 128 * cb + 64 * wc + 8 * cc) = d; }
; #pragma unroll
;                 for (int n = 0; n < 4; ++n) acc[m][n] = (f32x4){0.f, 0.f, 0.f, 0.f}; } }
	v_mul_f32_e32 v46, v150, v46
	v_mul_f32_e32 v47, v150, v47
	v_mul_f32_e32 v48, v150, v48
	v_mul_f32_e32 v49, v150, v49
	v_mul_f32_e32 v42, v150, v42
	v_mul_f32_e32 v43, v150, v43
	v_mul_f32_e32 v44, v150, v44
	v_mul_f32_e32 v45, v150, v45
	v_cvt_pk_bf16_f32 v182, v46, v47
	v_cvt_pk_bf16_f32 v183, v48, v49
	v_cvt_pk_bf16_f32 v184, v42, v43
	v_cvt_pk_bf16_f32 v185, v44, v45
	ds_write_b128 v164, v[182:185]
	v_mul_f32_e32 v38, v150, v38
	v_mul_f32_e32 v39, v150, v39
	v_mul_f32_e32 v40, v150, v40
	v_mul_f32_e32 v41, v150, v41
	v_mul_f32_e32 v34, v150, v34
	v_mul_f32_e32 v35, v150, v35
	v_mul_f32_e32 v36, v150, v36
	v_mul_f32_e32 v37, v150, v37
	v_cvt_pk_bf16_f32 v182, v38, v39
	v_cvt_pk_bf16_f32 v183, v40, v41
	v_cvt_pk_bf16_f32 v184, v34, v35
	v_cvt_pk_bf16_f32 v185, v36, v37
	v_xor_b32_e32 v167, 64, v164
	ds_write_b128 v167, v[182:185]
	v_mov_b32_e32 v46, 0
	v_mov_b32_e32 v42, 0
	v_mov_b32_e32 v38, 0
	v_mov_b32_e32 v34, 0
	v_mov_b32_e32 v47, 0
	v_mov_b32_e32 v43, 0
	v_mov_b32_e32 v39, 0
	v_mov_b32_e32 v35, 0
	v_mov_b32_e32 v48, 0
	v_mov_b32_e32 v44, 0
	v_mov_b32_e32 v40, 0
	v_mov_b32_e32 v36, 0
	v_mov_b32_e32 v49, 0
	v_mov_b32_e32 v45, 0
	v_mov_b32_e32 v41, 0
	v_mov_b32_e32 v37, 0
	ds_read_b128 v[182:185], v165 offset:0
	v_cmp_lt_i32_e32 vcc, -1, v151
	v_lshlrev_b32_e32 v148, 13, v151
	v_mov_b32_e32 v149, 0
	v_lshl_add_u64 v[148:149], v[148:149], 0, v[86:87]
	v_cndmask_b32_e32 v148, v168, v148, vcc
	v_cndmask_b32_e32 v149, v169, v149, vcc
	s_waitcnt lgkmcnt(0)
	global_store_dwordx4 v[148:149], v[182:185], off
	ds_read_b128 v[182:185], v165 offset:8192
	v_cmp_lt_i32_e32 vcc, -1, v166
	v_lshlrev_b32_e32 v148, 13, v166
	v_mov_b32_e32 v149, 0
	v_lshl_add_u64 v[148:149], v[148:149], 0, v[86:87]
	v_cndmask_b32_e32 v148, v168, v148, vcc
	v_cndmask_b32_e32 v149, v169, v149, vcc
	s_waitcnt lgkmcnt(0)
	global_store_dwordx4 v[148:149], v[182:185], off
	ds_read_b32 v150, v82 offset:768
	ds_read_b32 v151, v83 offset:768
	ds_read_b32 v166, v83 offset:896
	s_waitcnt lgkmcnt(2)
	v_mul_f32_e32 v18, v150, v18
	v_mul_f32_e32 v19, v150, v19
	v_mul_f32_e32 v20, v150, v20
	v_mul_f32_e32 v21, v150, v21
	v_mul_f32_e32 v22, v150, v22
	v_mul_f32_e32 v23, v150, v23
	v_mul_f32_e32 v24, v150, v24
	v_mul_f32_e32 v25, v150, v25
	v_cvt_pk_bf16_f32 v182, v18, v19
	v_cvt_pk_bf16_f32 v183, v20, v21
	v_cvt_pk_bf16_f32 v184, v22, v23
	v_cvt_pk_bf16_f32 v185, v24, v25
	ds_write_b128 v164, v[182:185]
	v_mul_f32_e32 v26, v150, v26
	v_mul_f32_e32 v27, v150, v27
	v_mul_f32_e32 v28, v150, v28
	v_mul_f32_e32 v29, v150, v29
	v_mul_f32_e32 v30, v150, v30
	v_mul_f32_e32 v31, v150, v31
	v_mul_f32_e32 v32, v150, v32
	v_mul_f32_e32 v33, v150, v33
	v_cvt_pk_bf16_f32 v182, v26, v27
	v_cvt_pk_bf16_f32 v183, v28, v29
	v_cvt_pk_bf16_f32 v184, v30, v31
	v_cvt_pk_bf16_f32 v185, v32, v33
	v_xor_b32_e32 v167, 64, v164
	ds_write_b128 v167, v[182:185]
	v_mov_b32_e32 v18, 0
	v_mov_b32_e32 v22, 0
	v_mov_b32_e32 v26, 0
	v_mov_b32_e32 v30, 0
	v_mov_b32_e32 v19, 0
	v_mov_b32_e32 v23, 0
	v_mov_b32_e32 v27, 0
	v_mov_b32_e32 v31, 0
	v_mov_b32_e32 v20, 0
	v_mov_b32_e32 v24, 0
	v_mov_b32_e32 v28, 0
	v_mov_b32_e32 v32, 0
	v_mov_b32_e32 v21, 0
	v_mov_b32_e32 v25, 0
	v_mov_b32_e32 v29, 0
	v_mov_b32_e32 v33, 0
	ds_read_b128 v[182:185], v165 offset:0
	v_cmp_lt_i32_e32 vcc, -1, v151
	v_lshlrev_b32_e32 v148, 13, v151
	v_mov_b32_e32 v149, 0
	v_lshl_add_u64 v[148:149], v[148:149], 0, v[86:87]
	v_cndmask_b32_e32 v148, v168, v148, vcc
	v_cndmask_b32_e32 v149, v169, v149, vcc
	s_waitcnt lgkmcnt(0)
	global_store_dwordx4 v[148:149], v[182:185], off
	ds_read_b128 v[182:185], v165 offset:8192
	v_cmp_lt_i32_e32 vcc, -1, v166
	v_lshlrev_b32_e32 v148, 13, v166
	v_mov_b32_e32 v149, 0
	v_lshl_add_u64 v[148:149], v[148:149], 0, v[86:87]
	v_cndmask_b32_e32 v148, v168, v148, vcc
	v_cndmask_b32_e32 v149, v169, v149, vcc
	s_waitcnt lgkmcnt(0)
	global_store_dwordx4 v[148:149], v[182:185], off
	ds_read_b32 v150, v82 offset:1024
	ds_read_b32 v151, v83 offset:1024
	ds_read_b32 v166, v83 offset:1152
	s_waitcnt lgkmcnt(2)
	v_mul_f32_e32 v2, v150, v2
	v_mul_f32_e32 v3, v150, v3
	v_mul_f32_e32 v4, v150, v4
	v_mul_f32_e32 v5, v150, v5
	v_mul_f32_e32 v6, v150, v6
	v_mul_f32_e32 v7, v150, v7
	v_mul_f32_e32 v8, v150, v8
	v_mul_f32_e32 v9, v150, v9
	v_cvt_pk_bf16_f32 v182, v2, v3
	v_cvt_pk_bf16_f32 v183, v4, v5
	v_cvt_pk_bf16_f32 v184, v6, v7
	v_cvt_pk_bf16_f32 v185, v8, v9
	ds_write_b128 v164, v[182:185]
	v_mul_f32_e32 v10, v150, v10
	v_mul_f32_e32 v11, v150, v11
	v_mul_f32_e32 v12, v150, v12
	v_mul_f32_e32 v13, v150, v13
	v_mul_f32_e32 v14, v150, v14
	v_mul_f32_e32 v15, v150, v15
	v_mul_f32_e32 v16, v150, v16
	v_mul_f32_e32 v17, v150, v17
	v_cvt_pk_bf16_f32 v182, v10, v11
	v_cvt_pk_bf16_f32 v183, v12, v13
	v_cvt_pk_bf16_f32 v184, v14, v15
	v_cvt_pk_bf16_f32 v185, v16, v17
	v_xor_b32_e32 v167, 64, v164
	ds_write_b128 v167, v[182:185]
	v_mov_b32_e32 v2, 0
	v_mov_b32_e32 v6, 0
	v_mov_b32_e32 v10, 0
	v_mov_b32_e32 v14, 0
	v_mov_b32_e32 v3, 0
	v_mov_b32_e32 v7, 0
	v_mov_b32_e32 v11, 0
	v_mov_b32_e32 v15, 0
	v_mov_b32_e32 v4, 0
	v_mov_b32_e32 v8, 0
	v_mov_b32_e32 v12, 0
	v_mov_b32_e32 v16, 0
	v_mov_b32_e32 v5, 0
	v_mov_b32_e32 v9, 0
	v_mov_b32_e32 v13, 0
	v_mov_b32_e32 v17, 0
	ds_read_b128 v[182:185], v165 offset:0
	v_cmp_lt_i32_e32 vcc, -1, v151
	v_lshlrev_b32_e32 v148, 13, v151
	v_mov_b32_e32 v149, 0
	v_lshl_add_u64 v[148:149], v[148:149], 0, v[86:87]
	v_cndmask_b32_e32 v148, v168, v148, vcc
	v_cndmask_b32_e32 v149, v169, v149, vcc
	s_waitcnt lgkmcnt(0)
	global_store_dwordx4 v[148:149], v[182:185], off
	ds_read_b128 v[182:185], v165 offset:8192
	v_cmp_lt_i32_e32 vcc, -1, v166
	v_lshlrev_b32_e32 v148, 13, v166
	v_mov_b32_e32 v149, 0
	v_lshl_add_u64 v[148:149], v[148:149], 0, v[86:87]
	v_cndmask_b32_e32 v148, v168, v148, vcc
	v_cndmask_b32_e32 v149, v169, v149, vcc
	s_waitcnt lgkmcnt(0)
; #define MD_GLDS_A(buf, tau) do { _Pragma("unroll") for (int i = 0; i < 5; ++i) if (amask & (1u << i)) \
;         __builtin_amdgcn_global_load_lds((const unsigned*)((const char*)HIDp + aoff[i] + (size_t)((tau) & 7) * 128), (PG8_LAS unsigned*)(MD_SA(buf) + wid * 1024 + i * 8192), 16, 0, 0); } while (0)
; #define MD_B_ISSUE(sb, tau) do { const char* kb_ = Bb + (size_t)((tau) >> 3) * 512 + (size_t)((tau) & 7) * (64 * (size_t)RB); _Pragma("unroll") for (int j = 0; j < 8; ++j) { const char* p_ = kb_ + (size_t)j * RB; \
;         asm volatile("global_load_dwordx2 %0, %1, off" : "=&v"(sb[j]) : "v"(p_) : "memory"); } } while (0)
; #define MD_B_WAIT(sb, N) asm volatile("s_waitcnt vmcnt(%8)" : "+v"(sb[0]), "+v"(sb[1]), "+v"(sb[2]), "+v"(sb[3]), "+v"(sb[4]), "+v"(sb[5]), "+v"(sb[6]), "+v"(sb[7]) : "n"(N) : "memory")
; #define MD_END(last) do { if (last) asm volatile("s_waitcnt vmcnt(0)" ::: "memory"); else asm volatile("s_waitcnt vmcnt(8)" ::: "memory"); \
;         asm volatile("s_waitcnt lgkmcnt(0)" ::: "memory"); __builtin_amdgcn_s_barrier(); asm volatile("" ::: "memory"); } while (0)
; __device__ __forceinline__ void moe_down_stream(PG8_LAS unsigned char* lds, int e, int cb0, int slot0, int nv, const bf16_t* HIDp, const float* Wd, bf16_t* Y, const float* slot_w, const int* slot_dst) {
;     ...
;         MD_B_WRITE(s1, 1); __builtin_amdgcn_sched_barrier(0); MD_GLDS_A(1, t + 1); __builtin_amdgcn_sched_barrier(0);
;         if (t + 3 < NT) MD_B_ISSUE(s1, t + 3);
;         MD_COMPUTE(0);
;         MD_END(t + 3 >= NT);
;         if (t + 2 < NT) { MD_B_WAIT(s0, 8); MD_B_WRITE(s0, 0); __builtin_amdgcn_sched_barrier(0); MD_GLDS_A(0, t + 2); __builtin_amdgcn_sched_barrier(0); }
;         if (t + 4 < NT) MD_B_ISSUE(s0, t + 4);
;         MD_COMPUTE(1);
;         MD_END(t + 4 >= NT);
;     ...
;                     if (dst_ >= 0) *(u32x4*)(Y + (size_t)dst_ * D + 128 * cb + 64 * wc + 8 * cc) = d; }
	global_store_dwordx4 v[148:149], v[182:185], off
	v_add_co_u32_e32 v86, vcc, 0x800, v86
	s_nop 1
	v_addc_co_u32_e32 v87, vcc, 0, v87, vcc
	s_waitcnt lgkmcnt(0)
	s_add_i32 s49, s48, s74
	s_add_i32 s52, s52, 1
	s_and_b32 s54, s52, 7
	s_cmp_eq_u32 s54, 0
	s_cselect_b32 s54, s53, s32
	s_cselect_b32 s55, -1, 0
	s_add_u32 s30, s30, s54
	s_addc_u32 s31, s31, s55
	s_mov_b32 m0, s49
	s_nop 0
	global_load_lds_dwordx4 v88, s[30:31]
	s_add_i32 m0, s49, 0x2000
	s_nop 0
	global_load_lds_dwordx4 v90, s[30:31]
	s_add_i32 m0, s49, 0x4000
	s_nop 0
	global_load_lds_dwordx4 v92, s[30:31]
	s_add_i32 m0, s49, 0x6000
	s_nop 0
	global_load_lds_dwordx4 v94, s[30:31]
	s_add_i32 m0, s49, 0x8000
	s_nop 0
	global_load_lds_dwordx4 v96, s[30:31]
	v_cvt_pk_bf16_f32 v172, v114, v116
	v_cvt_pk_bf16_f32 v173, v118, v120
	v_cvt_pk_bf16_f32 v174, v122, v124
	v_cvt_pk_bf16_f32 v175, v126, v128
	v_cvt_pk_bf16_f32 v176, v115, v117
	v_cvt_pk_bf16_f32 v177, v119, v121
	v_cvt_pk_bf16_f32 v178, v123, v125
	v_cvt_pk_bf16_f32 v179, v127, v129
	ds_write_b128 v95, v[172:175] offset:19456
	ds_write_b128 v95, v[176:179] offset:19584
	v_add_u32_e32 v91, s46, v135
	v_add_u32_e32 v93, s46, v137
	ds_read_b128 v[238:241], v139 offset:0
	ds_read_b128 v[242:245], v139 offset:2048
	ds_read_b128 v[246:249], v139 offset:4096
	ds_read_b128 v[250:253], v139 offset:6144
	ds_read_b128 v[218:221], v91 offset:0
	ds_read_b128 v[222:225], v91 offset:2048
	ds_read_b128 v[226:229], v91 offset:4096
	ds_read_b128 v[230:233], v91 offset:6144
	ds_read_b128 v[234:237], v91 offset:8192
	s_waitcnt lgkmcnt(0)
	v_mfma_f32_16x16x32_bf16 v[78:81], v[238:241], v[218:221], v[78:81]
	v_mfma_f32_16x16x32_bf16 v[74:77], v[242:245], v[218:221], v[74:77]
	v_mfma_f32_16x16x32_bf16 v[70:73], v[246:249], v[218:221], v[70:73]
	v_mfma_f32_16x16x32_bf16 v[66:69], v[250:253], v[218:221], v[66:69]
	ds_read_b128 v[218:221], v93 offset:0
	ds_read_b128 v[142:145], v141 offset:0
	s_add_i32 s51, s51, 1
	s_and_b32 s54, s51, 7
	s_cmp_eq_u32 s54, 0
	s_cselect_b32 s44, s34, s35
	s_cselect_b32 s45, -1, 0
	v_lshl_add_u64 v[132:133], v[132:133], 0, s[44:45]
	global_load_dwordx2 v[114:115], v[132:133], off
	v_lshl_add_u64 v[180:181], v[132:133], 0, s[24:25]
	global_load_dwordx2 v[116:117], v[180:181], off
	v_mfma_f32_16x16x32_bf16 v[62:65], v[238:241], v[222:225], v[62:65]
	v_mfma_f32_16x16x32_bf16 v[58:61], v[242:245], v[222:225], v[58:61]
	v_mfma_f32_16x16x32_bf16 v[54:57], v[246:249], v[222:225], v[54:57]
	v_mfma_f32_16x16x32_bf16 v[50:53], v[250:253], v[222:225], v[50:53]
	ds_read_b128 v[222:225], v93 offset:2048
	ds_read_b128 v[146:149], v141 offset:2048
	v_lshl_add_u64 v[180:181], v[132:133], 0, s[26:27]
	global_load_dwordx2 v[118:119], v[180:181], off
	v_lshl_add_u64 v[180:181], v[132:133], 0, s[28:29]
	global_load_dwordx2 v[120:121], v[180:181], off
	v_mfma_f32_16x16x32_bf16 v[46:49], v[238:241], v[226:229], v[46:49]
	v_mfma_f32_16x16x32_bf16 v[42:45], v[242:245], v[226:229], v[42:45]
	v_mfma_f32_16x16x32_bf16 v[38:41], v[246:249], v[226:229], v[38:41]
	v_mfma_f32_16x16x32_bf16 v[34:37], v[250:253], v[226:229], v[34:37]
	ds_read_b128 v[226:229], v93 offset:4096
	ds_read_b128 v[156:159], v141 offset:4096
	v_lshl_add_u64 v[180:181], v[132:133], 0, s[36:37]
	global_load_dwordx2 v[122:123], v[180:181], off
	v_lshl_add_u64 v[180:181], v[132:133], 0, s[38:39]
	global_load_dwordx2 v[124:125], v[180:181], off
	v_mfma_f32_16x16x32_bf16 v[18:21], v[238:241], v[230:233], v[18:21]
	v_mfma_f32_16x16x32_bf16 v[22:25], v[242:245], v[230:233], v[22:25]
	v_mfma_f32_16x16x32_bf16 v[26:29], v[246:249], v[230:233], v[26:29]
	v_mfma_f32_16x16x32_bf16 v[30:33], v[250:253], v[230:233], v[30:33]
	ds_read_b128 v[230:233], v93 offset:6144
	ds_read_b128 v[160:163], v141 offset:6144
	v_lshl_add_u64 v[180:181], v[132:133], 0, s[40:41]
	global_load_dwordx2 v[126:127], v[180:181], off
	v_lshl_add_u64 v[180:181], v[132:133], 0, s[42:43]
	global_load_dwordx2 v[128:129], v[180:181], off
	v_mfma_f32_16x16x32_bf16 v[2:5], v[238:241], v[234:237], v[2:5]
	v_mfma_f32_16x16x32_bf16 v[6:9], v[242:245], v[234:237], v[6:9]
	v_mfma_f32_16x16x32_bf16 v[10:13], v[246:249], v[234:237], v[10:13]
	v_mfma_f32_16x16x32_bf16 v[14:17], v[250:253], v[234:237], v[14:17]
	ds_read_b128 v[234:237], v93 offset:8192
	s_waitcnt vmcnt(31)
	s_waitcnt lgkmcnt(0)
	s_barrier
; #define MD_GLDS_A(buf, tau) do { _Pragma("unroll") for (int i = 0; i < 5; ++i) if (amask & (1u << i)) \
;         __builtin_amdgcn_global_load_lds((const unsigned*)((const char*)HIDp + aoff[i] + (size_t)((tau) & 7) * 128), (PG8_LAS unsigned*)(MD_SA(buf) + wid * 1024 + i * 8192), 16, 0, 0); } while (0)
; #define MD_B_ISSUE(sb, tau) do { const char* kb_ = Bb + (size_t)((tau) >> 3) * 512 + (size_t)((tau) & 7) * (64 * (size_t)RB); _Pragma("unroll") for (int j = 0; j < 8; ++j) { const char* p_ = kb_ + (size_t)j * RB; \
;         asm volatile("global_load_dwordx2 %0, %1, off" : "=&v"(sb[j]) : "v"(p_) : "memory"); } } while (0)
; #define MD_B_WAIT(sb, N) asm volatile("s_waitcnt vmcnt(%8)" : "+v"(sb[0]), "+v"(sb[1]), "+v"(sb[2]), "+v"(sb[3]), "+v"(sb[4]), "+v"(sb[5]), "+v"(sb[6]), "+v"(sb[7]) : "n"(N) : "memory")
; #define MD_END(last) do { if (last) asm volatile("s_waitcnt vmcnt(0)" ::: "memory"); else asm volatile("s_waitcnt vmcnt(8)" ::: "memory"); \
;         asm volatile("s_waitcnt lgkmcnt(0)" ::: "memory"); __builtin_amdgcn_s_barrier(); asm volatile("" ::: "memory"); } while (0)
; __device__ __forceinline__ void moe_down_stream(PG8_LAS unsigned char* lds, int e, int cb0, int slot0, int nv, const bf16_t* HIDp, const float* Wd, bf16_t* Y, const float* slot_w, const int* slot_dst) {
;     ...
;     for (int t = 0; t < NT; t += 2) {
;         if (t + 2 < NT) MD_B_WAIT(s1, 8); else MD_B_WAIT(s1, 0);
;         MD_B_WRITE(s1, 1); __builtin_amdgcn_sched_barrier(0); MD_GLDS_A(1, t + 1); __builtin_amdgcn_sched_barrier(0);
;         if (t + 3 < NT) MD_B_ISSUE(s1, t + 3);
;         MD_COMPUTE(0);
;         MD_END(t + 3 >= NT);
;         if (t + 2 < NT) { MD_B_WAIT(s0, 8); MD_B_WRITE(s0, 0); __builtin_amdgcn_sched_barrier(0); MD_GLDS_A(0, t + 2); __builtin_amdgcn_sched_barrier(0); }
;         if (t + 4 < NT) MD_B_ISSUE(s0, t + 4);
;         MD_COMPUTE(1);
;         MD_END(t + 4 >= NT);
	s_mov_b32 s49, s46
	s_mov_b32 s46, s47
	s_mov_b32 s47, s48
	s_mov_b32 s48, s49
	s_add_i32 s49, s48, s74
	s_add_i32 s52, s52, 1
	s_and_b32 s54, s52, 7
	s_cmp_eq_u32 s54, 0
	s_cselect_b32 s54, s53, s32
	s_cselect_b32 s55, -1, 0
	s_add_u32 s30, s30, s54
	s_addc_u32 s31, s31, s55
	v_mfma_f32_16x16x32_bf16 v[78:81], v[142:145], v[218:221], v[78:81]
	v_mfma_f32_16x16x32_bf16 v[74:77], v[146:149], v[218:221], v[74:77]
	v_mfma_f32_16x16x32_bf16 v[70:73], v[156:159], v[218:221], v[70:73]
	v_mfma_f32_16x16x32_bf16 v[66:69], v[160:163], v[218:221], v[66:69]
	s_mov_b32 m0, s49
	s_nop 0
	global_load_lds_dwordx4 v88, s[30:31]
	v_mfma_f32_16x16x32_bf16 v[62:65], v[142:145], v[222:225], v[62:65]
	v_mfma_f32_16x16x32_bf16 v[58:61], v[146:149], v[222:225], v[58:61]
	v_mfma_f32_16x16x32_bf16 v[54:57], v[156:159], v[222:225], v[54:57]
	v_mfma_f32_16x16x32_bf16 v[50:53], v[160:163], v[222:225], v[50:53]
	s_add_i32 m0, s49, 0x2000
	s_nop 0
	global_load_lds_dwordx4 v90, s[30:31]
	v_mfma_f32_16x16x32_bf16 v[46:49], v[142:145], v[226:229], v[46:49]
	v_mfma_f32_16x16x32_bf16 v[42:45], v[146:149], v[226:229], v[42:45]
	v_mfma_f32_16x16x32_bf16 v[38:41], v[156:159], v[226:229], v[38:41]
	v_mfma_f32_16x16x32_bf16 v[34:37], v[160:163], v[226:229], v[34:37]
	s_add_i32 m0, s49, 0x4000
	s_nop 0
	global_load_lds_dwordx4 v92, s[30:31]
	v_mfma_f32_16x16x32_bf16 v[18:21], v[142:145], v[230:233], v[18:21]
	v_mfma_f32_16x16x32_bf16 v[22:25], v[146:149], v[230:233], v[22:25]
	v_mfma_f32_16x16x32_bf16 v[26:29], v[156:159], v[230:233], v[26:29]
	v_mfma_f32_16x16x32_bf16 v[30:33], v[160:163], v[230:233], v[30:33]
	s_add_i32 m0, s49, 0x6000
	s_nop 0
	global_load_lds_dwordx4 v94, s[30:31]
	v_mfma_f32_16x16x32_bf16 v[2:5], v[142:145], v[234:237], v[2:5]
	v_mfma_f32_16x16x32_bf16 v[6:9], v[146:149], v[234:237], v[6:9]
	v_mfma_f32_16x16x32_bf16 v[10:13], v[156:159], v[234:237], v[10:13]
	v_mfma_f32_16x16x32_bf16 v[14:17], v[160:163], v[234:237], v[14:17]
	s_add_i32 m0, s49, 0x8000
	s_nop 0
	global_load_lds_dwordx4 v96, s[30:31]
	v_cvt_pk_bf16_f32 v172, v186, v188
	v_cvt_pk_bf16_f32 v173, v190, v192
	v_cvt_pk_bf16_f32 v174, v194, v196
	v_cvt_pk_bf16_f32 v175, v198, v200
	v_cvt_pk_bf16_f32 v176, v187, v189
	v_cvt_pk_bf16_f32 v177, v191, v193
	v_cvt_pk_bf16_f32 v178, v195, v197
	v_cvt_pk_bf16_f32 v179, v199, v201
	ds_write_b128 v95, v[172:175] offset:0
	ds_write_b128 v95, v[176:179] offset:128
	v_add_u32_e32 v91, s46, v135
	v_add_u32_e32 v93, s46, v137
	ds_read_b128 v[238:241], v139 offset:19456
	ds_read_b128 v[242:245], v139 offset:21504
	ds_read_b128 v[246:249], v139 offset:23552
	ds_read_b128 v[250:253], v139 offset:25600
	ds_read_b128 v[218:221], v91 offset:0
	ds_read_b128 v[222:225], v91 offset:2048
	ds_read_b128 v[226:229], v91 offset:4096
	ds_read_b128 v[230:233], v91 offset:6144
	ds_read_b128 v[234:237], v91 offset:8192
	s_waitcnt lgkmcnt(0)
	v_mfma_f32_16x16x32_bf16 v[78:81], v[238:241], v[218:221], v[78:81]
	v_mfma_f32_16x16x32_bf16 v[74:77], v[242:245], v[218:221], v[74:77]
	v_mfma_f32_16x16x32_bf16 v[70:73], v[246:249], v[218:221], v[70:73]
	v_mfma_f32_16x16x32_bf16 v[66:69], v[250:253], v[218:221], v[66:69]
	ds_read_b128 v[218:221], v93 offset:0
	ds_read_b128 v[142:145], v141 offset:19456
	s_add_i32 s51, s51, 1
	s_and_b32 s54, s51, 7
	s_cmp_eq_u32 s54, 0
	s_cselect_b32 s44, s34, s35
	s_cselect_b32 s45, -1, 0
	v_lshl_add_u64 v[132:133], v[132:133], 0, s[44:45]
	global_load_dwordx2 v[186:187], v[132:133], off
	v_lshl_add_u64 v[180:181], v[132:133], 0, s[24:25]
	global_load_dwordx2 v[188:189], v[180:181], off
	v_mfma_f32_16x16x32_bf16 v[62:65], v[238:241], v[222:225], v[62:65]
	v_mfma_f32_16x16x32_bf16 v[58:61], v[242:245], v[222:225], v[58:61]
	v_mfma_f32_16x16x32_bf16 v[54:57], v[246:249], v[222:225], v[54:57]
	v_mfma_f32_16x16x32_bf16 v[50:53], v[250:253], v[222:225], v[50:53]
	ds_read_b128 v[222:225], v93 offset:2048
	ds_read_b128 v[146:149], v141 offset:21504
	v_lshl_add_u64 v[180:181], v[132:133], 0, s[26:27]
	global_load_dwordx2 v[190:191], v[180:181], off
	v_lshl_add_u64 v[180:181], v[132:133], 0, s[28:29]
	global_load_dwordx2 v[192:193], v[180:181], off
	v_mfma_f32_16x16x32_bf16 v[46:49], v[238:241], v[226:229], v[46:49]
	v_mfma_f32_16x16x32_bf16 v[42:45], v[242:245], v[226:229], v[42:45]
	v_mfma_f32_16x16x32_bf16 v[38:41], v[246:249], v[226:229], v[38:41]
	v_mfma_f32_16x16x32_bf16 v[34:37], v[250:253], v[226:229], v[34:37]
	ds_read_b128 v[226:229], v93 offset:4096
	ds_read_b128 v[156:159], v141 offset:23552
	v_lshl_add_u64 v[180:181], v[132:133], 0, s[36:37]
	global_load_dwordx2 v[194:195], v[180:181], off
	v_lshl_add_u64 v[180:181], v[132:133], 0, s[38:39]
	global_load_dwordx2 v[196:197], v[180:181], off
	v_mfma_f32_16x16x32_bf16 v[18:21], v[238:241], v[230:233], v[18:21]
	v_mfma_f32_16x16x32_bf16 v[22:25], v[242:245], v[230:233], v[22:25]
	v_mfma_f32_16x16x32_bf16 v[26:29], v[246:249], v[230:233], v[26:29]
	v_mfma_f32_16x16x32_bf16 v[30:33], v[250:253], v[230:233], v[30:33]
	ds_read_b128 v[230:233], v93 offset:6144
	ds_read_b128 v[160:163], v141 offset:25600
	v_lshl_add_u64 v[180:181], v[132:133], 0, s[40:41]
	global_load_dwordx2 v[198:199], v[180:181], off
	v_lshl_add_u64 v[180:181], v[132:133], 0, s[42:43]
	global_load_dwordx2 v[200:201], v[180:181], off
	v_mfma_f32_16x16x32_bf16 v[2:5], v[238:241], v[234:237], v[2:5]
	v_mfma_f32_16x16x32_bf16 v[6:9], v[242:245], v[234:237], v[6:9]
	v_mfma_f32_16x16x32_bf16 v[10:13], v[246:249], v[234:237], v[10:13]
	v_mfma_f32_16x16x32_bf16 v[14:17], v[250:253], v[234:237], v[14:17]
	ds_read_b128 v[234:237], v93 offset:8192
	s_waitcnt vmcnt(21)
	s_waitcnt lgkmcnt(0)
	s_barrier
; #define MD_GLDS_A(buf, tau) do { _Pragma("unroll") for (int i = 0; i < 5; ++i) if (amask & (1u << i)) \
;         __builtin_amdgcn_global_load_lds((const unsigned*)((const char*)HIDp + aoff[i] + (size_t)((tau) & 7) * 128), (PG8_LAS unsigned*)(MD_SA(buf) + wid * 1024 + i * 8192), 16, 0, 0); } while (0)
; #define MD_B_ISSUE(sb, tau) do { const char* kb_ = Bb + (size_t)((tau) >> 3) * 512 + (size_t)((tau) & 7) * (64 * (size_t)RB); _Pragma("unroll") for (int j = 0; j < 8; ++j) { const char* p_ = kb_ + (size_t)j * RB; \
;         asm volatile("global_load_dwordx2 %0, %1, off" : "=&v"(sb[j]) : "v"(p_) : "memory"); } } while (0)
; #define MD_B_WAIT(sb, N) asm volatile("s_waitcnt vmcnt(%8)" : "+v"(sb[0]), "+v"(sb[1]), "+v"(sb[2]), "+v"(sb[3]), "+v"(sb[4]), "+v"(sb[5]), "+v"(sb[6]), "+v"(sb[7]) : "n"(N) : "memory")
; #define MD_END(last) do { if (last) asm volatile("s_waitcnt vmcnt(0)" ::: "memory"); else asm volatile("s_waitcnt vmcnt(8)" ::: "memory"); \
;         asm volatile("s_waitcnt lgkmcnt(0)" ::: "memory"); __builtin_amdgcn_s_barrier(); asm volatile("" ::: "memory"); } while (0)
; __device__ __forceinline__ void moe_down_stream(PG8_LAS unsigned char* lds, int e, int cb0, int slot0, int nv, const bf16_t* HIDp, const float* Wd, bf16_t* Y, const float* slot_w, const int* slot_dst) {
;     ...
;     for (int t = 0; t < NT; t += 2) {
;         if (t + 2 < NT) MD_B_WAIT(s1, 8); else MD_B_WAIT(s1, 0);
;         MD_B_WRITE(s1, 1); __builtin_amdgcn_sched_barrier(0); MD_GLDS_A(1, t + 1); __builtin_amdgcn_sched_barrier(0);
;         if (t + 3 < NT) MD_B_ISSUE(s1, t + 3);
;         MD_COMPUTE(0);
;         MD_END(t + 3 >= NT);
;         if (t + 2 < NT) { MD_B_WAIT(s0, 8); MD_B_WRITE(s0, 0); __builtin_amdgcn_sched_barrier(0); MD_GLDS_A(0, t + 2); __builtin_amdgcn_sched_barrier(0); }
;         if (t + 4 < NT) MD_B_ISSUE(s0, t + 4);
;         MD_COMPUTE(1);
;         MD_END(t + 4 >= NT);
	s_mov_b32 s49, s46
	s_mov_b32 s46, s47
	s_mov_b32 s47, s48
	s_mov_b32 s48, s49
	s_add_i32 s49, s48, s74
	s_add_i32 s52, s52, 1
	s_and_b32 s54, s52, 7
	s_cmp_eq_u32 s54, 0
	s_cselect_b32 s54, s53, s32
	s_cselect_b32 s55, -1, 0
	s_add_u32 s30, s30, s54
	s_addc_u32 s31, s31, s55
	v_mfma_f32_16x16x32_bf16 v[78:81], v[142:145], v[218:221], v[78:81]
	v_mfma_f32_16x16x32_bf16 v[74:77], v[146:149], v[218:221], v[74:77]
	v_mfma_f32_16x16x32_bf16 v[70:73], v[156:159], v[218:221], v[70:73]
	v_mfma_f32_16x16x32_bf16 v[66:69], v[160:163], v[218:221], v[66:69]
	s_mov_b32 m0, s49
	s_nop 0
	global_load_lds_dwordx4 v88, s[30:31]
	v_mfma_f32_16x16x32_bf16 v[62:65], v[142:145], v[222:225], v[62:65]
	v_mfma_f32_16x16x32_bf16 v[58:61], v[146:149], v[222:225], v[58:61]
	v_mfma_f32_16x16x32_bf16 v[54:57], v[156:159], v[222:225], v[54:57]
	v_mfma_f32_16x16x32_bf16 v[50:53], v[160:163], v[222:225], v[50:53]
	s_add_i32 m0, s49, 0x2000
	s_nop 0
	global_load_lds_dwordx4 v90, s[30:31]
	v_mfma_f32_16x16x32_bf16 v[46:49], v[142:145], v[226:229], v[46:49]
	v_mfma_f32_16x16x32_bf16 v[42:45], v[146:149], v[226:229], v[42:45]
	v_mfma_f32_16x16x32_bf16 v[38:41], v[156:159], v[226:229], v[38:41]
	v_mfma_f32_16x16x32_bf16 v[34:37], v[160:163], v[226:229], v[34:37]
	s_add_i32 m0, s49, 0x4000
	s_nop 0
	global_load_lds_dwordx4 v92, s[30:31]
	v_mfma_f32_16x16x32_bf16 v[18:21], v[142:145], v[230:233], v[18:21]
	v_mfma_f32_16x16x32_bf16 v[22:25], v[146:149], v[230:233], v[22:25]
	v_mfma_f32_16x16x32_bf16 v[26:29], v[156:159], v[230:233], v[26:29]
	v_mfma_f32_16x16x32_bf16 v[30:33], v[160:163], v[230:233], v[30:33]
	s_add_i32 m0, s49, 0x6000
	s_nop 0
	global_load_lds_dwordx4 v94, s[30:31]
	v_mfma_f32_16x16x32_bf16 v[2:5], v[142:145], v[234:237], v[2:5]
	v_mfma_f32_16x16x32_bf16 v[6:9], v[146:149], v[234:237], v[6:9]
	v_mfma_f32_16x16x32_bf16 v[10:13], v[156:159], v[234:237], v[10:13]
	v_mfma_f32_16x16x32_bf16 v[14:17], v[160:163], v[234:237], v[14:17]
	s_add_i32 m0, s49, 0x8000
	s_nop 0
	global_load_lds_dwordx4 v96, s[30:31]
	v_cvt_pk_bf16_f32 v172, v202, v204
	v_cvt_pk_bf16_f32 v173, v206, v208
	v_cvt_pk_bf16_f32 v174, v210, v212
	v_cvt_pk_bf16_f32 v175, v214, v216
	v_cvt_pk_bf16_f32 v176, v203, v205
	v_cvt_pk_bf16_f32 v177, v207, v209
	v_cvt_pk_bf16_f32 v178, v211, v213
	v_cvt_pk_bf16_f32 v179, v215, v217
	ds_write_b128 v95, v[172:175] offset:19456
	ds_write_b128 v95, v[176:179] offset:19584
	v_add_u32_e32 v91, s46, v135
	v_add_u32_e32 v93, s46, v137
	ds_read_b128 v[238:241], v139 offset:0
	ds_read_b128 v[242:245], v139 offset:2048
	ds_read_b128 v[246:249], v139 offset:4096
	ds_read_b128 v[250:253], v139 offset:6144
	ds_read_b128 v[218:221], v91 offset:0
	ds_read_b128 v[222:225], v91 offset:2048
	ds_read_b128 v[226:229], v91 offset:4096
	ds_read_b128 v[230:233], v91 offset:6144
	ds_read_b128 v[234:237], v91 offset:8192
	s_waitcnt lgkmcnt(0)
	v_mfma_f32_16x16x32_bf16 v[78:81], v[238:241], v[218:221], v[78:81]
	v_mfma_f32_16x16x32_bf16 v[74:77], v[242:245], v[218:221], v[74:77]
	v_mfma_f32_16x16x32_bf16 v[70:73], v[246:249], v[218:221], v[70:73]
	v_mfma_f32_16x16x32_bf16 v[66:69], v[250:253], v[218:221], v[66:69]
	ds_read_b128 v[218:221], v93 offset:0
	ds_read_b128 v[142:145], v141 offset:0
	s_add_i32 s51, s51, 1
	s_and_b32 s54, s51, 7
	s_cmp_eq_u32 s54, 0
	s_cselect_b32 s44, s34, s35
	s_cselect_b32 s45, -1, 0
	v_lshl_add_u64 v[132:133], v[132:133], 0, s[44:45]
	global_load_dwordx2 v[202:203], v[132:133], off
	v_lshl_add_u64 v[180:181], v[132:133], 0, s[24:25]
	global_load_dwordx2 v[204:205], v[180:181], off
	v_mfma_f32_16x16x32_bf16 v[62:65], v[238:241], v[222:225], v[62:65]
	v_mfma_f32_16x16x32_bf16 v[58:61], v[242:245], v[222:225], v[58:61]
	v_mfma_f32_16x16x32_bf16 v[54:57], v[246:249], v[222:225], v[54:57]
	v_mfma_f32_16x16x32_bf16 v[50:53], v[250:253], v[222:225], v[50:53]
	ds_read_b128 v[222:225], v93 offset:2048
	ds_read_b128 v[146:149], v141 offset:2048
	v_lshl_add_u64 v[180:181], v[132:133], 0, s[26:27]
	global_load_dwordx2 v[206:207], v[180:181], off
	v_lshl_add_u64 v[180:181], v[132:133], 0, s[28:29]
	global_load_dwordx2 v[208:209], v[180:181], off
	v_mfma_f32_16x16x32_bf16 v[46:49], v[238:241], v[226:229], v[46:49]
	v_mfma_f32_16x16x32_bf16 v[42:45], v[242:245], v[226:229], v[42:45]
	v_mfma_f32_16x16x32_bf16 v[38:41], v[246:249], v[226:229], v[38:41]
	v_mfma_f32_16x16x32_bf16 v[34:37], v[250:253], v[226:229], v[34:37]
	ds_read_b128 v[226:229], v93 offset:4096
	ds_read_b128 v[156:159], v141 offset:4096
	v_lshl_add_u64 v[180:181], v[132:133], 0, s[36:37]
	global_load_dwordx2 v[210:211], v[180:181], off
	v_lshl_add_u64 v[180:181], v[132:133], 0, s[38:39]
	global_load_dwordx2 v[212:213], v[180:181], off
	v_mfma_f32_16x16x32_bf16 v[18:21], v[238:241], v[230:233], v[18:21]
	v_mfma_f32_16x16x32_bf16 v[22:25], v[242:245], v[230:233], v[22:25]
	v_mfma_f32_16x16x32_bf16 v[26:29], v[246:249], v[230:233], v[26:29]
	v_mfma_f32_16x16x32_bf16 v[30:33], v[250:253], v[230:233], v[30:33]
	ds_read_b128 v[230:233], v93 offset:6144
	ds_read_b128 v[160:163], v141 offset:6144
	v_lshl_add_u64 v[180:181], v[132:133], 0, s[40:41]
	global_load_dwordx2 v[214:215], v[180:181], off
	v_lshl_add_u64 v[180:181], v[132:133], 0, s[42:43]
	global_load_dwordx2 v[216:217], v[180:181], off
	v_mfma_f32_16x16x32_bf16 v[2:5], v[238:241], v[234:237], v[2:5]
	v_mfma_f32_16x16x32_bf16 v[6:9], v[242:245], v[234:237], v[6:9]
	v_mfma_f32_16x16x32_bf16 v[10:13], v[246:249], v[234:237], v[10:13]
	v_mfma_f32_16x16x32_bf16 v[14:17], v[250:253], v[234:237], v[14:17]
	ds_read_b128 v[234:237], v93 offset:8192
	s_waitcnt vmcnt(21)
	s_waitcnt lgkmcnt(0)
	s_barrier
; #define MD_GLDS_A(buf, tau) do { _Pragma("unroll") for (int i = 0; i < 5; ++i) if (amask & (1u << i)) \
;         __builtin_amdgcn_global_load_lds((const unsigned*)((const char*)HIDp + aoff[i] + (size_t)((tau) & 7) * 128), (PG8_LAS unsigned*)(MD_SA(buf) + wid * 1024 + i * 8192), 16, 0, 0); } while (0)
; #define MD_B_ISSUE(sb, tau) do { const char* kb_ = Bb + (size_t)((tau) >> 3) * 512 + (size_t)((tau) & 7) * (64 * (size_t)RB); _Pragma("unroll") for (int j = 0; j < 8; ++j) { const char* p_ = kb_ + (size_t)j * RB; \
;         asm volatile("global_load_dwordx2 %0, %1, off" : "=&v"(sb[j]) : "v"(p_) : "memory"); } } while (0)
; #define MD_B_WAIT(sb, N) asm volatile("s_waitcnt vmcnt(%8)" : "+v"(sb[0]), "+v"(sb[1]), "+v"(sb[2]), "+v"(sb[3]), "+v"(sb[4]), "+v"(sb[5]), "+v"(sb[6]), "+v"(sb[7]) : "n"(N) : "memory")
; #define MD_END(last) do { if (last) asm volatile("s_waitcnt vmcnt(0)" ::: "memory"); else asm volatile("s_waitcnt vmcnt(8)" ::: "memory"); \
;         asm volatile("s_waitcnt lgkmcnt(0)" ::: "memory"); __builtin_amdgcn_s_barrier(); asm volatile("" ::: "memory"); } while (0)
; __device__ __forceinline__ void moe_down_stream(PG8_LAS unsigned char* lds, int e, int cb0, int slot0, int nv, const bf16_t* HIDp, const float* Wd, bf16_t* Y, const float* slot_w, const int* slot_dst) {
;     ...
;     for (int t = 0; t < NT; t += 2) {
;         if (t + 2 < NT) MD_B_WAIT(s1, 8); else MD_B_WAIT(s1, 0);
;         MD_B_WRITE(s1, 1); __builtin_amdgcn_sched_barrier(0); MD_GLDS_A(1, t + 1); __builtin_amdgcn_sched_barrier(0);
;         if (t + 3 < NT) MD_B_ISSUE(s1, t + 3);
;         MD_COMPUTE(0);
;         MD_END(t + 3 >= NT);
;         if (t + 2 < NT) { MD_B_WAIT(s0, 8); MD_B_WRITE(s0, 0); __builtin_amdgcn_sched_barrier(0); MD_GLDS_A(0, t + 2); __builtin_amdgcn_sched_barrier(0); }
;         if (t + 4 < NT) MD_B_ISSUE(s0, t + 4);
;         MD_COMPUTE(1);
;         MD_END(t + 4 >= NT);
	s_mov_b32 s49, s46
	s_mov_b32 s46, s47
	s_mov_b32 s47, s48
	s_mov_b32 s48, s49
	s_add_i32 s49, s48, s74
	s_add_i32 s52, s52, 1
	s_and_b32 s54, s52, 7
	s_cmp_eq_u32 s54, 0
	s_cselect_b32 s54, s53, s32
	s_cselect_b32 s55, -1, 0
	s_add_u32 s30, s30, s54
	s_addc_u32 s31, s31, s55
	v_mfma_f32_16x16x32_bf16 v[78:81], v[142:145], v[218:221], v[78:81]
	v_mfma_f32_16x16x32_bf16 v[74:77], v[146:149], v[218:221], v[74:77]
	v_mfma_f32_16x16x32_bf16 v[70:73], v[156:159], v[218:221], v[70:73]
	v_mfma_f32_16x16x32_bf16 v[66:69], v[160:163], v[218:221], v[66:69]
	s_mov_b32 m0, s49
	s_nop 0
	global_load_lds_dwordx4 v88, s[30:31]
	v_mfma_f32_16x16x32_bf16 v[62:65], v[142:145], v[222:225], v[62:65]
	v_mfma_f32_16x16x32_bf16 v[58:61], v[146:149], v[222:225], v[58:61]
	v_mfma_f32_16x16x32_bf16 v[54:57], v[156:159], v[222:225], v[54:57]
	v_mfma_f32_16x16x32_bf16 v[50:53], v[160:163], v[222:225], v[50:53]
	s_add_i32 m0, s49, 0x2000
	s_nop 0
	global_load_lds_dwordx4 v90, s[30:31]
	v_mfma_f32_16x16x32_bf16 v[46:49], v[142:145], v[226:229], v[46:49]
	v_mfma_f32_16x16x32_bf16 v[42:45], v[146:149], v[226:229], v[42:45]
	v_mfma_f32_16x16x32_bf16 v[38:41], v[156:159], v[226:229], v[38:41]
	v_mfma_f32_16x16x32_bf16 v[34:37], v[160:163], v[226:229], v[34:37]
	s_add_i32 m0, s49, 0x4000
	s_nop 0
	global_load_lds_dwordx4 v92, s[30:31]
	v_mfma_f32_16x16x32_bf16 v[18:21], v[142:145], v[230:233], v[18:21]
	v_mfma_f32_16x16x32_bf16 v[22:25], v[146:149], v[230:233], v[22:25]
	v_mfma_f32_16x16x32_bf16 v[26:29], v[156:159], v[230:233], v[26:29]
	v_mfma_f32_16x16x32_bf16 v[30:33], v[160:163], v[230:233], v[30:33]
	s_add_i32 m0, s49, 0x6000
	s_nop 0
	global_load_lds_dwordx4 v94, s[30:31]
	v_mfma_f32_16x16x32_bf16 v[2:5], v[142:145], v[234:237], v[2:5]
	v_mfma_f32_16x16x32_bf16 v[6:9], v[146:149], v[234:237], v[6:9]
	v_mfma_f32_16x16x32_bf16 v[10:13], v[156:159], v[234:237], v[10:13]
	v_mfma_f32_16x16x32_bf16 v[14:17], v[160:163], v[234:237], v[14:17]
	s_add_i32 m0, s49, 0x8000
	s_nop 0
	global_load_lds_dwordx4 v96, s[30:31]
	v_cvt_pk_bf16_f32 v172, v98, v100
	v_cvt_pk_bf16_f32 v173, v102, v104
	v_cvt_pk_bf16_f32 v174, v106, v108
	v_cvt_pk_bf16_f32 v175, v110, v112
	v_cvt_pk_bf16_f32 v176, v99, v101
	v_cvt_pk_bf16_f32 v177, v103, v105
	v_cvt_pk_bf16_f32 v178, v107, v109
	v_cvt_pk_bf16_f32 v179, v111, v113
	ds_write_b128 v95, v[172:175] offset:0
	ds_write_b128 v95, v[176:179] offset:128
	v_add_u32_e32 v91, s46, v135
	v_add_u32_e32 v93, s46, v137
	ds_read_b128 v[238:241], v139 offset:19456
	ds_read_b128 v[242:245], v139 offset:21504
	ds_read_b128 v[246:249], v139 offset:23552
	ds_read_b128 v[250:253], v139 offset:25600
	ds_read_b128 v[218:221], v91 offset:0
	ds_read_b128 v[222:225], v91 offset:2048
	ds_read_b128 v[226:229], v91 offset:4096
	ds_read_b128 v[230:233], v91 offset:6144
	ds_read_b128 v[234:237], v91 offset:8192
	s_waitcnt lgkmcnt(0)
	v_mfma_f32_16x16x32_bf16 v[78:81], v[238:241], v[218:221], v[78:81]
	v_mfma_f32_16x16x32_bf16 v[74:77], v[242:245], v[218:221], v[74:77]
	v_mfma_f32_16x16x32_bf16 v[70:73], v[246:249], v[218:221], v[70:73]
	v_mfma_f32_16x16x32_bf16 v[66:69], v[250:253], v[218:221], v[66:69]
	ds_read_b128 v[218:221], v93 offset:0
	ds_read_b128 v[142:145], v141 offset:19456
	v_mfma_f32_16x16x32_bf16 v[62:65], v[238:241], v[222:225], v[62:65]
	v_mfma_f32_16x16x32_bf16 v[58:61], v[242:245], v[222:225], v[58:61]
	v_mfma_f32_16x16x32_bf16 v[54:57], v[246:249], v[222:225], v[54:57]
	v_mfma_f32_16x16x32_bf16 v[50:53], v[250:253], v[222:225], v[50:53]
	ds_read_b128 v[222:225], v93 offset:2048
	ds_read_b128 v[146:149], v141 offset:21504
	v_mfma_f32_16x16x32_bf16 v[46:49], v[238:241], v[226:229], v[46:49]
	v_mfma_f32_16x16x32_bf16 v[42:45], v[242:245], v[226:229], v[42:45]
	v_mfma_f32_16x16x32_bf16 v[38:41], v[246:249], v[226:229], v[38:41]
	v_mfma_f32_16x16x32_bf16 v[34:37], v[250:253], v[226:229], v[34:37]
	ds_read_b128 v[226:229], v93 offset:4096
	ds_read_b128 v[156:159], v141 offset:23552
	v_mfma_f32_16x16x32_bf16 v[18:21], v[238:241], v[230:233], v[18:21]
	v_mfma_f32_16x16x32_bf16 v[22:25], v[242:245], v[230:233], v[22:25]
	v_mfma_f32_16x16x32_bf16 v[26:29], v[246:249], v[230:233], v[26:29]
	v_mfma_f32_16x16x32_bf16 v[30:33], v[250:253], v[230:233], v[30:33]
	ds_read_b128 v[230:233], v93 offset:6144
	ds_read_b128 v[160:163], v141 offset:25600
	v_mfma_f32_16x16x32_bf16 v[2:5], v[238:241], v[234:237], v[2:5]
	v_mfma_f32_16x16x32_bf16 v[6:9], v[242:245], v[234:237], v[6:9]
	v_mfma_f32_16x16x32_bf16 v[10:13], v[246:249], v[234:237], v[10:13]
	v_mfma_f32_16x16x32_bf16 v[14:17], v[250:253], v[234:237], v[14:17]
	ds_read_b128 v[234:237], v93 offset:8192
	s_waitcnt vmcnt(13)
	s_waitcnt lgkmcnt(0)
	s_barrier
; #define MD_GLDS_A(buf, tau) do { _Pragma("unroll") for (int i = 0; i < 5; ++i) if (amask & (1u << i)) \
;         __builtin_amdgcn_global_load_lds((const unsigned*)((const char*)HIDp + aoff[i] + (size_t)((tau) & 7) * 128), (PG8_LAS unsigned*)(MD_SA(buf) + wid * 1024 + i * 8192), 16, 0, 0); } while (0)
; #define MD_B_ISSUE(sb, tau) do { const char* kb_ = Bb + (size_t)((tau) >> 3) * 512 + (size_t)((tau) & 7) * (64 * (size_t)RB); _Pragma("unroll") for (int j = 0; j < 8; ++j) { const char* p_ = kb_ + (size_t)j * RB; \
;         asm volatile("global_load_dwordx2 %0, %1, off" : "=&v"(sb[j]) : "v"(p_) : "memory"); } } while (0)
; #define MD_B_WAIT(sb, N) asm volatile("s_waitcnt vmcnt(%8)" : "+v"(sb[0]), "+v"(sb[1]), "+v"(sb[2]), "+v"(sb[3]), "+v"(sb[4]), "+v"(sb[5]), "+v"(sb[6]), "+v"(sb[7]) : "n"(N) : "memory")
; #define MD_END(last) do { if (last) asm volatile("s_waitcnt vmcnt(0)" ::: "memory"); else asm volatile("s_waitcnt vmcnt(8)" ::: "memory"); \
;         asm volatile("s_waitcnt lgkmcnt(0)" ::: "memory"); __builtin_amdgcn_s_barrier(); asm volatile("" ::: "memory"); } while (0)
; __device__ __forceinline__ void moe_down_stream(PG8_LAS unsigned char* lds, int e, int cb0, int slot0, int nv, const bf16_t* HIDp, const float* Wd, bf16_t* Y, const float* slot_w, const int* slot_dst) {
;     ...
;     for (int t = 0; t < NT; t += 2) {
;         if (t + 2 < NT) MD_B_WAIT(s1, 8); else MD_B_WAIT(s1, 0);
;         MD_B_WRITE(s1, 1); __builtin_amdgcn_sched_barrier(0); MD_GLDS_A(1, t + 1); __builtin_amdgcn_sched_barrier(0);
;         if (t + 3 < NT) MD_B_ISSUE(s1, t + 3);
;         MD_COMPUTE(0);
;         MD_END(t + 3 >= NT);
;         if (t + 2 < NT) { MD_B_WAIT(s0, 8); MD_B_WRITE(s0, 0); __builtin_amdgcn_sched_barrier(0); MD_GLDS_A(0, t + 2); __builtin_amdgcn_sched_barrier(0); }
;         if (t + 4 < NT) MD_B_ISSUE(s0, t + 4);
;         MD_COMPUTE(1);
;         MD_END(t + 4 >= NT);
	s_mov_b32 s49, s46
	s_mov_b32 s46, s47
	s_mov_b32 s47, s48
	s_mov_b32 s48, s49
	s_add_i32 s49, s48, s74
	s_add_i32 s52, s52, 1
	s_and_b32 s54, s52, 7
	s_cmp_eq_u32 s54, 0
	s_cselect_b32 s54, s53, s32
	s_cselect_b32 s55, -1, 0
	s_add_u32 s30, s30, s54
	s_addc_u32 s31, s31, s55
	v_mfma_f32_16x16x32_bf16 v[78:81], v[142:145], v[218:221], v[78:81]
	v_mfma_f32_16x16x32_bf16 v[74:77], v[146:149], v[218:221], v[74:77]
	v_mfma_f32_16x16x32_bf16 v[70:73], v[156:159], v[218:221], v[70:73]
	v_mfma_f32_16x16x32_bf16 v[66:69], v[160:163], v[218:221], v[66:69]
	s_mov_b32 m0, s49
	s_nop 0
	global_load_lds_dwordx4 v88, s[30:31]
	v_mfma_f32_16x16x32_bf16 v[62:65], v[142:145], v[222:225], v[62:65]
	v_mfma_f32_16x16x32_bf16 v[58:61], v[146:149], v[222:225], v[58:61]
	v_mfma_f32_16x16x32_bf16 v[54:57], v[156:159], v[222:225], v[54:57]
	v_mfma_f32_16x16x32_bf16 v[50:53], v[160:163], v[222:225], v[50:53]
	s_add_i32 m0, s49, 0x2000
	s_nop 0
	global_load_lds_dwordx4 v90, s[30:31]
	v_mfma_f32_16x16x32_bf16 v[46:49], v[142:145], v[226:229], v[46:49]
	v_mfma_f32_16x16x32_bf16 v[42:45], v[146:149], v[226:229], v[42:45]
	v_mfma_f32_16x16x32_bf16 v[38:41], v[156:159], v[226:229], v[38:41]
	v_mfma_f32_16x16x32_bf16 v[34:37], v[160:163], v[226:229], v[34:37]
	s_add_i32 m0, s49, 0x4000
	s_nop 0
	global_load_lds_dwordx4 v92, s[30:31]
	v_mfma_f32_16x16x32_bf16 v[18:21], v[142:145], v[230:233], v[18:21]
	v_mfma_f32_16x16x32_bf16 v[22:25], v[146:149], v[230:233], v[22:25]
	v_mfma_f32_16x16x32_bf16 v[26:29], v[156:159], v[230:233], v[26:29]
	v_mfma_f32_16x16x32_bf16 v[30:33], v[160:163], v[230:233], v[30:33]
	s_add_i32 m0, s49, 0x6000
	s_nop 0
	global_load_lds_dwordx4 v94, s[30:31]
	v_mfma_f32_16x16x32_bf16 v[2:5], v[142:145], v[234:237], v[2:5]
	v_mfma_f32_16x16x32_bf16 v[6:9], v[146:149], v[234:237], v[6:9]
	v_mfma_f32_16x16x32_bf16 v[10:13], v[156:159], v[234:237], v[10:13]
	v_mfma_f32_16x16x32_bf16 v[14:17], v[160:163], v[234:237], v[14:17]
	s_add_i32 m0, s49, 0x8000
	s_nop 0
	global_load_lds_dwordx4 v96, s[30:31]
	v_cvt_pk_bf16_f32 v172, v114, v116
	v_cvt_pk_bf16_f32 v173, v118, v120
	v_cvt_pk_bf16_f32 v174, v122, v124
	v_cvt_pk_bf16_f32 v175, v126, v128
	v_cvt_pk_bf16_f32 v176, v115, v117
	v_cvt_pk_bf16_f32 v177, v119, v121
	v_cvt_pk_bf16_f32 v178, v123, v125
	v_cvt_pk_bf16_f32 v179, v127, v129
	ds_write_b128 v95, v[172:175] offset:19456
	ds_write_b128 v95, v[176:179] offset:19584
	v_add_u32_e32 v91, s46, v135
	v_add_u32_e32 v93, s46, v137
	ds_read_b128 v[238:241], v139 offset:0
	ds_read_b128 v[242:245], v139 offset:2048
	ds_read_b128 v[246:249], v139 offset:4096
	ds_read_b128 v[250:253], v139 offset:6144
	ds_read_b128 v[218:221], v91 offset:0
	ds_read_b128 v[222:225], v91 offset:2048
	ds_read_b128 v[226:229], v91 offset:4096
	ds_read_b128 v[230:233], v91 offset:6144
	ds_read_b128 v[234:237], v91 offset:8192
	s_waitcnt lgkmcnt(0)
	v_mfma_f32_16x16x32_bf16 v[78:81], v[238:241], v[218:221], v[78:81]
	v_mfma_f32_16x16x32_bf16 v[74:77], v[242:245], v[218:221], v[74:77]
	v_mfma_f32_16x16x32_bf16 v[70:73], v[246:249], v[218:221], v[70:73]
	v_mfma_f32_16x16x32_bf16 v[66:69], v[250:253], v[218:221], v[66:69]
	ds_read_b128 v[218:221], v93 offset:0
	ds_read_b128 v[142:145], v141 offset:0
	v_mfma_f32_16x16x32_bf16 v[62:65], v[238:241], v[222:225], v[62:65]
	v_mfma_f32_16x16x32_bf16 v[58:61], v[242:245], v[222:225], v[58:61]
	v_mfma_f32_16x16x32_bf16 v[54:57], v[246:249], v[222:225], v[54:57]
	v_mfma_f32_16x16x32_bf16 v[50:53], v[250:253], v[222:225], v[50:53]
	ds_read_b128 v[222:225], v93 offset:2048
	ds_read_b128 v[146:149], v141 offset:2048
	v_mfma_f32_16x16x32_bf16 v[46:49], v[238:241], v[226:229], v[46:49]
	v_mfma_f32_16x16x32_bf16 v[42:45], v[242:245], v[226:229], v[42:45]
	v_mfma_f32_16x16x32_bf16 v[38:41], v[246:249], v[226:229], v[38:41]
	v_mfma_f32_16x16x32_bf16 v[34:37], v[250:253], v[226:229], v[34:37]
	ds_read_b128 v[226:229], v93 offset:4096
	ds_read_b128 v[156:159], v141 offset:4096
	v_mfma_f32_16x16x32_bf16 v[18:21], v[238:241], v[230:233], v[18:21]
	v_mfma_f32_16x16x32_bf16 v[22:25], v[242:245], v[230:233], v[22:25]
	v_mfma_f32_16x16x32_bf16 v[26:29], v[246:249], v[230:233], v[26:29]
	v_mfma_f32_16x16x32_bf16 v[30:33], v[250:253], v[230:233], v[30:33]
	ds_read_b128 v[230:233], v93 offset:6144
	ds_read_b128 v[160:163], v141 offset:6144
	v_mfma_f32_16x16x32_bf16 v[2:5], v[238:241], v[234:237], v[2:5]
	v_mfma_f32_16x16x32_bf16 v[6:9], v[242:245], v[234:237], v[6:9]
	v_mfma_f32_16x16x32_bf16 v[10:13], v[246:249], v[234:237], v[10:13]
	v_mfma_f32_16x16x32_bf16 v[14:17], v[250:253], v[234:237], v[14:17]
	ds_read_b128 v[234:237], v93 offset:8192
	s_waitcnt vmcnt(5)
	s_waitcnt lgkmcnt(0)
	s_barrier
; #define MD_GLDS_A(buf, tau) do { _Pragma("unroll") for (int i = 0; i < 5; ++i) if (amask & (1u << i)) \
;         __builtin_amdgcn_global_load_lds((const unsigned*)((const char*)HIDp + aoff[i] + (size_t)((tau) & 7) * 128), (PG8_LAS unsigned*)(MD_SA(buf) + wid * 1024 + i * 8192), 16, 0, 0); } while (0)
; #define MD_B_ISSUE(sb, tau) do { const char* kb_ = Bb + (size_t)((tau) >> 3) * 512 + (size_t)((tau) & 7) * (64 * (size_t)RB); _Pragma("unroll") for (int j = 0; j < 8; ++j) { const char* p_ = kb_ + (size_t)j * RB; \
;         asm volatile("global_load_dwordx2 %0, %1, off" : "=&v"(sb[j]) : "v"(p_) : "memory"); } } while (0)
; #define MD_B_WAIT(sb, N) asm volatile("s_waitcnt vmcnt(%8)" : "+v"(sb[0]), "+v"(sb[1]), "+v"(sb[2]), "+v"(sb[3]), "+v"(sb[4]), "+v"(sb[5]), "+v"(sb[6]), "+v"(sb[7]) : "n"(N) : "memory")
; #define MD_END(last) do { if (last) asm volatile("s_waitcnt vmcnt(0)" ::: "memory"); else asm volatile("s_waitcnt vmcnt(8)" ::: "memory"); \
;         asm volatile("s_waitcnt lgkmcnt(0)" ::: "memory"); __builtin_amdgcn_s_barrier(); asm volatile("" ::: "memory"); } while (0)
; __device__ __forceinline__ void moe_down_stream(PG8_LAS unsigned char* lds, int e, int cb0, int slot0, int nv, const bf16_t* HIDp, const float* Wd, bf16_t* Y, const float* slot_w, const int* slot_dst) {
;     ...
;     for (int t = 0; t < NT; t += 2) {
;         if (t + 2 < NT) MD_B_WAIT(s1, 8); else MD_B_WAIT(s1, 0);
;         MD_B_WRITE(s1, 1); __builtin_amdgcn_sched_barrier(0); MD_GLDS_A(1, t + 1); __builtin_amdgcn_sched_barrier(0);
;         if (t + 3 < NT) MD_B_ISSUE(s1, t + 3);
;         MD_COMPUTE(0);
;         MD_END(t + 3 >= NT);
;         if (t + 2 < NT) { MD_B_WAIT(s0, 8); MD_B_WRITE(s0, 0); __builtin_amdgcn_sched_barrier(0); MD_GLDS_A(0, t + 2); __builtin_amdgcn_sched_barrier(0); }
;         if (t + 4 < NT) MD_B_ISSUE(s0, t + 4);
;         MD_COMPUTE(1);
;         MD_END(t + 4 >= NT);
	s_mov_b32 s49, s46
	s_mov_b32 s46, s47
	s_mov_b32 s47, s48
	s_mov_b32 s48, s49
	s_add_i32 s49, s48, s74
	s_add_i32 s52, s52, 1
	s_and_b32 s54, s52, 7
	s_cmp_eq_u32 s54, 0
	s_cselect_b32 s54, s53, s32
	s_cselect_b32 s55, -1, 0
	s_add_u32 s30, s30, s54
	s_addc_u32 s31, s31, s55
	v_mfma_f32_16x16x32_bf16 v[78:81], v[142:145], v[218:221], v[78:81]
	v_mfma_f32_16x16x32_bf16 v[74:77], v[146:149], v[218:221], v[74:77]
	v_mfma_f32_16x16x32_bf16 v[70:73], v[156:159], v[218:221], v[70:73]
	v_mfma_f32_16x16x32_bf16 v[66:69], v[160:163], v[218:221], v[66:69]
	s_mov_b32 m0, s49
	s_nop 0
	global_load_lds_dwordx4 v88, s[30:31]
	v_mfma_f32_16x16x32_bf16 v[62:65], v[142:145], v[222:225], v[62:65]
	v_mfma_f32_16x16x32_bf16 v[58:61], v[146:149], v[222:225], v[58:61]
	v_mfma_f32_16x16x32_bf16 v[54:57], v[156:159], v[222:225], v[54:57]
	v_mfma_f32_16x16x32_bf16 v[50:53], v[160:163], v[222:225], v[50:53]
	s_add_i32 m0, s49, 0x2000
	s_nop 0
	global_load_lds_dwordx4 v90, s[30:31]
	v_mfma_f32_16x16x32_bf16 v[46:49], v[142:145], v[226:229], v[46:49]
	v_mfma_f32_16x16x32_bf16 v[42:45], v[146:149], v[226:229], v[42:45]
	v_mfma_f32_16x16x32_bf16 v[38:41], v[156:159], v[226:229], v[38:41]
	v_mfma_f32_16x16x32_bf16 v[34:37], v[160:163], v[226:229], v[34:37]
	s_add_i32 m0, s49, 0x4000
	s_nop 0
	global_load_lds_dwordx4 v92, s[30:31]
	v_mfma_f32_16x16x32_bf16 v[18:21], v[142:145], v[230:233], v[18:21]
	v_mfma_f32_16x16x32_bf16 v[22:25], v[146:149], v[230:233], v[22:25]
	v_mfma_f32_16x16x32_bf16 v[26:29], v[156:159], v[230:233], v[26:29]
	v_mfma_f32_16x16x32_bf16 v[30:33], v[160:163], v[230:233], v[30:33]
	s_add_i32 m0, s49, 0x6000
	s_nop 0
	global_load_lds_dwordx4 v94, s[30:31]
	v_mfma_f32_16x16x32_bf16 v[2:5], v[142:145], v[234:237], v[2:5]
	v_mfma_f32_16x16x32_bf16 v[6:9], v[146:149], v[234:237], v[6:9]
	v_mfma_f32_16x16x32_bf16 v[10:13], v[156:159], v[234:237], v[10:13]
	v_mfma_f32_16x16x32_bf16 v[14:17], v[160:163], v[234:237], v[14:17]
	s_add_i32 m0, s49, 0x8000
	s_nop 0
	global_load_lds_dwordx4 v96, s[30:31]
	v_cvt_pk_bf16_f32 v172, v186, v188
	v_cvt_pk_bf16_f32 v173, v190, v192
	v_cvt_pk_bf16_f32 v174, v194, v196
	v_cvt_pk_bf16_f32 v175, v198, v200
	v_cvt_pk_bf16_f32 v176, v187, v189
	v_cvt_pk_bf16_f32 v177, v191, v193
	v_cvt_pk_bf16_f32 v178, v195, v197
	v_cvt_pk_bf16_f32 v179, v199, v201
	ds_write_b128 v95, v[172:175] offset:0
	ds_write_b128 v95, v[176:179] offset:128
	v_add_u32_e32 v91, s46, v135
	v_add_u32_e32 v93, s46, v137
	ds_read_b128 v[238:241], v139 offset:19456
	ds_read_b128 v[242:245], v139 offset:21504
	ds_read_b128 v[246:249], v139 offset:23552
	ds_read_b128 v[250:253], v139 offset:25600
	ds_read_b128 v[218:221], v91 offset:0
	ds_read_b128 v[222:225], v91 offset:2048
	ds_read_b128 v[226:229], v91 offset:4096
	ds_read_b128 v[230:233], v91 offset:6144
	ds_read_b128 v[234:237], v91 offset:8192
	s_waitcnt lgkmcnt(0)
	v_mfma_f32_16x16x32_bf16 v[78:81], v[238:241], v[218:221], v[78:81]
	v_mfma_f32_16x16x32_bf16 v[74:77], v[242:245], v[218:221], v[74:77]
	v_mfma_f32_16x16x32_bf16 v[70:73], v[246:249], v[218:221], v[70:73]
	v_mfma_f32_16x16x32_bf16 v[66:69], v[250:253], v[218:221], v[66:69]
	ds_read_b128 v[218:221], v93 offset:0
	ds_read_b128 v[142:145], v141 offset:19456
	v_mfma_f32_16x16x32_bf16 v[62:65], v[238:241], v[222:225], v[62:65]
	v_mfma_f32_16x16x32_bf16 v[58:61], v[242:245], v[222:225], v[58:61]
	v_mfma_f32_16x16x32_bf16 v[54:57], v[246:249], v[222:225], v[54:57]
	v_mfma_f32_16x16x32_bf16 v[50:53], v[250:253], v[222:225], v[50:53]
	ds_read_b128 v[222:225], v93 offset:2048
	ds_read_b128 v[146:149], v141 offset:21504
	v_mfma_f32_16x16x32_bf16 v[46:49], v[238:241], v[226:229], v[46:49]
	v_mfma_f32_16x16x32_bf16 v[42:45], v[242:245], v[226:229], v[42:45]
	v_mfma_f32_16x16x32_bf16 v[38:41], v[246:249], v[226:229], v[38:41]
	v_mfma_f32_16x16x32_bf16 v[34:37], v[250:253], v[226:229], v[34:37]
	ds_read_b128 v[226:229], v93 offset:4096
	ds_read_b128 v[156:159], v141 offset:23552
	v_mfma_f32_16x16x32_bf16 v[18:21], v[238:241], v[230:233], v[18:21]
	v_mfma_f32_16x16x32_bf16 v[22:25], v[242:245], v[230:233], v[22:25]
	v_mfma_f32_16x16x32_bf16 v[26:29], v[246:249], v[230:233], v[26:29]
	v_mfma_f32_16x16x32_bf16 v[30:33], v[250:253], v[230:233], v[30:33]
	ds_read_b128 v[230:233], v93 offset:6144
	ds_read_b128 v[160:163], v141 offset:25600
	v_mfma_f32_16x16x32_bf16 v[2:5], v[238:241], v[234:237], v[2:5]
	v_mfma_f32_16x16x32_bf16 v[6:9], v[242:245], v[234:237], v[6:9]
	v_mfma_f32_16x16x32_bf16 v[10:13], v[246:249], v[234:237], v[10:13]
	v_mfma_f32_16x16x32_bf16 v[14:17], v[250:253], v[234:237], v[14:17]
	ds_read_b128 v[234:237], v93 offset:8192
	s_waitcnt vmcnt(5)
	s_waitcnt lgkmcnt(0)
	s_barrier
; #define MD_GLDS_A(buf, tau) do { _Pragma("unroll") for (int i = 0; i < 5; ++i) if (amask & (1u << i)) \
;         __builtin_amdgcn_global_load_lds((const unsigned*)((const char*)HIDp + aoff[i] + (size_t)((tau) & 7) * 128), (PG8_LAS unsigned*)(MD_SA(buf) + wid * 1024 + i * 8192), 16, 0, 0); } while (0)
; #define MD_B_ISSUE(sb, tau) do { const char* kb_ = Bb + (size_t)((tau) >> 3) * 512 + (size_t)((tau) & 7) * (64 * (size_t)RB); _Pragma("unroll") for (int j = 0; j < 8; ++j) { const char* p_ = kb_ + (size_t)j * RB; \
;         asm volatile("global_load_dwordx2 %0, %1, off" : "=&v"(sb[j]) : "v"(p_) : "memory"); } } while (0)
; #define MD_B_WAIT(sb, N) asm volatile("s_waitcnt vmcnt(%8)" : "+v"(sb[0]), "+v"(sb[1]), "+v"(sb[2]), "+v"(sb[3]), "+v"(sb[4]), "+v"(sb[5]), "+v"(sb[6]), "+v"(sb[7]) : "n"(N) : "memory")
; #define MD_END(last) do { if (last) asm volatile("s_waitcnt vmcnt(0)" ::: "memory"); else asm volatile("s_waitcnt vmcnt(8)" ::: "memory"); \
;         asm volatile("s_waitcnt lgkmcnt(0)" ::: "memory"); __builtin_amdgcn_s_barrier(); asm volatile("" ::: "memory"); } while (0)
; __device__ __forceinline__ void moe_down_stream(PG8_LAS unsigned char* lds, int e, int cb0, int slot0, int nv, const bf16_t* HIDp, const float* Wd, bf16_t* Y, const float* slot_w, const int* slot_dst) {
;     ...
;     for (int t = 0; t < NT; t += 2) {
;         if (t + 2 < NT) MD_B_WAIT(s1, 8); else MD_B_WAIT(s1, 0);
;         MD_B_WRITE(s1, 1); __builtin_amdgcn_sched_barrier(0); MD_GLDS_A(1, t + 1); __builtin_amdgcn_sched_barrier(0);
;         if (t + 3 < NT) MD_B_ISSUE(s1, t + 3);
;         MD_COMPUTE(0);
;         MD_END(t + 3 >= NT);
;         if (t + 2 < NT) { MD_B_WAIT(s0, 8); MD_B_WRITE(s0, 0); __builtin_amdgcn_sched_barrier(0); MD_GLDS_A(0, t + 2); __builtin_amdgcn_sched_barrier(0); }
;         if (t + 4 < NT) MD_B_ISSUE(s0, t + 4);
;         MD_COMPUTE(1);
;         MD_END(t + 4 >= NT);
	s_mov_b32 s49, s46
	s_mov_b32 s46, s47
	s_mov_b32 s47, s48
	s_mov_b32 s48, s49
	v_mfma_f32_16x16x32_bf16 v[78:81], v[142:145], v[218:221], v[78:81]
	v_mfma_f32_16x16x32_bf16 v[74:77], v[146:149], v[218:221], v[74:77]
	v_mfma_f32_16x16x32_bf16 v[70:73], v[156:159], v[218:221], v[70:73]
	v_mfma_f32_16x16x32_bf16 v[66:69], v[160:163], v[218:221], v[66:69]
	v_mfma_f32_16x16x32_bf16 v[62:65], v[142:145], v[222:225], v[62:65]
	v_mfma_f32_16x16x32_bf16 v[58:61], v[146:149], v[222:225], v[58:61]
	v_mfma_f32_16x16x32_bf16 v[54:57], v[156:159], v[222:225], v[54:57]
	v_mfma_f32_16x16x32_bf16 v[50:53], v[160:163], v[222:225], v[50:53]
	v_mfma_f32_16x16x32_bf16 v[46:49], v[142:145], v[226:229], v[46:49]
	v_mfma_f32_16x16x32_bf16 v[42:45], v[146:149], v[226:229], v[42:45]
	v_mfma_f32_16x16x32_bf16 v[38:41], v[156:159], v[226:229], v[38:41]
	v_mfma_f32_16x16x32_bf16 v[34:37], v[160:163], v[226:229], v[34:37]
	v_mfma_f32_16x16x32_bf16 v[18:21], v[142:145], v[230:233], v[18:21]
	v_mfma_f32_16x16x32_bf16 v[22:25], v[146:149], v[230:233], v[22:25]
	v_mfma_f32_16x16x32_bf16 v[26:29], v[156:159], v[230:233], v[26:29]
	v_mfma_f32_16x16x32_bf16 v[30:33], v[160:163], v[230:233], v[30:33]
	v_mfma_f32_16x16x32_bf16 v[2:5], v[142:145], v[234:237], v[2:5]
	v_mfma_f32_16x16x32_bf16 v[6:9], v[146:149], v[234:237], v[6:9]
	v_mfma_f32_16x16x32_bf16 v[10:13], v[156:159], v[234:237], v[10:13]
	v_mfma_f32_16x16x32_bf16 v[14:17], v[160:163], v[234:237], v[14:17]
	v_cvt_pk_bf16_f32 v172, v202, v204
	v_cvt_pk_bf16_f32 v173, v206, v208
	v_cvt_pk_bf16_f32 v174, v210, v212
	v_cvt_pk_bf16_f32 v175, v214, v216
	v_cvt_pk_bf16_f32 v176, v203, v205
	v_cvt_pk_bf16_f32 v177, v207, v209
	v_cvt_pk_bf16_f32 v178, v211, v213
	v_cvt_pk_bf16_f32 v179, v215, v217
	ds_write_b128 v95, v[172:175] offset:19456
	ds_write_b128 v95, v[176:179] offset:19584
	v_add_u32_e32 v91, s46, v135
	v_add_u32_e32 v93, s46, v137
	ds_read_b128 v[238:241], v139 offset:0
	ds_read_b128 v[242:245], v139 offset:2048
	ds_read_b128 v[246:249], v139 offset:4096
	ds_read_b128 v[250:253], v139 offset:6144
	ds_read_b128 v[218:221], v91 offset:0
	ds_read_b128 v[222:225], v91 offset:2048
	ds_read_b128 v[226:229], v91 offset:4096
	ds_read_b128 v[230:233], v91 offset:6144
	ds_read_b128 v[234:237], v91 offset:8192
	s_waitcnt lgkmcnt(0)
	v_mfma_f32_16x16x32_bf16 v[78:81], v[238:241], v[218:221], v[78:81]
	v_mfma_f32_16x16x32_bf16 v[74:77], v[242:245], v[218:221], v[74:77]
	v_mfma_f32_16x16x32_bf16 v[70:73], v[246:249], v[218:221], v[70:73]
	v_mfma_f32_16x16x32_bf16 v[66:69], v[250:253], v[218:221], v[66:69]
	ds_read_b128 v[218:221], v93 offset:0
	ds_read_b128 v[142:145], v141 offset:0
	v_mfma_f32_16x16x32_bf16 v[62:65], v[238:241], v[222:225], v[62:65]
	v_mfma_f32_16x16x32_bf16 v[58:61], v[242:245], v[222:225], v[58:61]
	v_mfma_f32_16x16x32_bf16 v[54:57], v[246:249], v[222:225], v[54:57]
	v_mfma_f32_16x16x32_bf16 v[50:53], v[250:253], v[222:225], v[50:53]
	ds_read_b128 v[222:225], v93 offset:2048
	ds_read_b128 v[146:149], v141 offset:2048
	v_mfma_f32_16x16x32_bf16 v[46:49], v[238:241], v[226:229], v[46:49]
	v_mfma_f32_16x16x32_bf16 v[42:45], v[242:245], v[226:229], v[42:45]
	v_mfma_f32_16x16x32_bf16 v[38:41], v[246:249], v[226:229], v[38:41]
	v_mfma_f32_16x16x32_bf16 v[34:37], v[250:253], v[226:229], v[34:37]
	ds_read_b128 v[226:229], v93 offset:4096
	ds_read_b128 v[156:159], v141 offset:4096
	v_mfma_f32_16x16x32_bf16 v[18:21], v[238:241], v[230:233], v[18:21]
	v_mfma_f32_16x16x32_bf16 v[22:25], v[242:245], v[230:233], v[22:25]
	v_mfma_f32_16x16x32_bf16 v[26:29], v[246:249], v[230:233], v[26:29]
	v_mfma_f32_16x16x32_bf16 v[30:33], v[250:253], v[230:233], v[30:33]
	ds_read_b128 v[230:233], v93 offset:6144
	ds_read_b128 v[160:163], v141 offset:6144
	v_mfma_f32_16x16x32_bf16 v[2:5], v[238:241], v[234:237], v[2:5]
	v_mfma_f32_16x16x32_bf16 v[6:9], v[242:245], v[234:237], v[6:9]
	v_mfma_f32_16x16x32_bf16 v[10:13], v[246:249], v[234:237], v[10:13]
	v_mfma_f32_16x16x32_bf16 v[14:17], v[250:253], v[234:237], v[14:17]
	ds_read_b128 v[234:237], v93 offset:8192
	s_waitcnt vmcnt(0)
	s_waitcnt lgkmcnt(0)
	s_barrier
	s_mov_b32 s49, s46
	s_mov_b32 s46, s47
	s_mov_b32 s47, s48
	s_mov_b32 s48, s49
	v_mfma_f32_16x16x32_bf16 v[78:81], v[142:145], v[218:221], v[78:81]
	v_mfma_f32_16x16x32_bf16 v[74:77], v[146:149], v[218:221], v[74:77]
	v_mfma_f32_16x16x32_bf16 v[70:73], v[156:159], v[218:221], v[70:73]
	v_mfma_f32_16x16x32_bf16 v[66:69], v[160:163], v[218:221], v[66:69]
	v_mfma_f32_16x16x32_bf16 v[62:65], v[142:145], v[222:225], v[62:65]
	v_mfma_f32_16x16x32_bf16 v[58:61], v[146:149], v[222:225], v[58:61]
	v_mfma_f32_16x16x32_bf16 v[54:57], v[156:159], v[222:225], v[54:57]
	v_mfma_f32_16x16x32_bf16 v[50:53], v[160:163], v[222:225], v[50:53]
	v_mfma_f32_16x16x32_bf16 v[46:49], v[142:145], v[226:229], v[46:49]
	v_mfma_f32_16x16x32_bf16 v[42:45], v[146:149], v[226:229], v[42:45]
	v_mfma_f32_16x16x32_bf16 v[38:41], v[156:159], v[226:229], v[38:41]
	v_mfma_f32_16x16x32_bf16 v[34:37], v[160:163], v[226:229], v[34:37]
	v_mfma_f32_16x16x32_bf16 v[18:21], v[142:145], v[230:233], v[18:21]
	v_mfma_f32_16x16x32_bf16 v[22:25], v[146:149], v[230:233], v[22:25]
	v_mfma_f32_16x16x32_bf16 v[26:29], v[156:159], v[230:233], v[26:29]
	v_mfma_f32_16x16x32_bf16 v[30:33], v[160:163], v[230:233], v[30:33]
	v_mfma_f32_16x16x32_bf16 v[2:5], v[142:145], v[234:237], v[2:5]
	v_mfma_f32_16x16x32_bf16 v[6:9], v[146:149], v[234:237], v[6:9]
	v_mfma_f32_16x16x32_bf16 v[10:13], v[156:159], v[234:237], v[10:13]
	v_mfma_f32_16x16x32_bf16 v[14:17], v[160:163], v[234:237], v[14:17]
	v_add_u32_e32 v91, s46, v135
	v_add_u32_e32 v93, s46, v137
	ds_read_b128 v[238:241], v139 offset:19456
	ds_read_b128 v[242:245], v139 offset:21504
	ds_read_b128 v[246:249], v139 offset:23552
	ds_read_b128 v[250:253], v139 offset:25600
	ds_read_b128 v[218:221], v91 offset:0
	ds_read_b128 v[222:225], v91 offset:2048
	ds_read_b128 v[226:229], v91 offset:4096
	ds_read_b128 v[230:233], v91 offset:6144
	ds_read_b128 v[234:237], v91 offset:8192
	s_waitcnt lgkmcnt(0)
; #define PG8_LAS __attribute__((address_space(3)))
; __device__ __forceinline__ unsigned cvtpk(float lo, float hi) { f32x2 v = {lo, hi}; bf16x2_t b = __builtin_convertvector(v, bf16x2_t); return __builtin_bit_cast(unsigned, b); }
; #define MD_END(last) do { if (last) asm volatile("s_waitcnt vmcnt(0)" ::: "memory"); else asm volatile("s_waitcnt vmcnt(8)" ::: "memory"); \
;         asm volatile("s_waitcnt lgkmcnt(0)" ::: "memory"); __builtin_amdgcn_s_barrier(); asm volatile("" ::: "memory"); } while (0)
; __device__ __forceinline__ void moe_down_stream(PG8_LAS unsigned char* lds, int e, int cb0, int slot0, int nv, const bf16_t* HIDp, const float* Wd, bf16_t* Y, const float* slot_w, const int* slot_dst) {
;     ...
;         MD_COMPUTE(1);
;         MD_END(t + 4 >= NT);
;         if (((t + 1) & 7) == 7) {
;             const int cb = cb0 + ((t + 1) >> 3);
; #pragma unroll
;             for (int m = 0; m < DNM; ++m) {
;                 const float w_ = lw[4 * (16 * m + fr) + wr];
; #pragma unroll
;                 for (int p = 0; p < 2; ++p) { const f32x4 v0 = acc[m][2 * p] * w_, v1 = acc[m][2 * p + 1] * w_; u32x4 w; w.x = cvtpk(v0[0], v0[1]); w.y = cvtpk(v0[2], v0[3]); w.z = cvtpk(v1[0], v1[1]); w.w = cvtpk(v1[2], v1[3]);
;                     *(PG8_LAS u32x4*)(stg + fr * 128 + (((4 * p + fq) ^ (fr & 7)) * 16)) = w; }
; #pragma unroll
;                 for (int hh = 0; hh < 2; ++hh) { const int r = (lane >> 3) + 8 * hh, cc = lane & 7; const u32x4 d = *(const PG8_LAS u32x4*)(stg + r * 128 + ((cc ^ (r & 7)) * 16)); const int dst_ = ldst[4 * (16 * m + r) + wr];
;                     if (dst_ >= 0) *(u32x4*)(Y + (size_t)dst_ * D + 128 * cb + 64 * wc + 8 * cc) = d; }
; #pragma unroll
;                 for (int n = 0; n < 4; ++n) acc[m][n] = (f32x4){0.f, 0.f, 0.f, 0.f}; } }
	v_mfma_f32_16x16x32_bf16 v[78:81], v[238:241], v[218:221], v[78:81]
	v_mfma_f32_16x16x32_bf16 v[74:77], v[242:245], v[218:221], v[74:77]
	v_mfma_f32_16x16x32_bf16 v[70:73], v[246:249], v[218:221], v[70:73]
	v_mfma_f32_16x16x32_bf16 v[66:69], v[250:253], v[218:221], v[66:69]
	ds_read_b128 v[218:221], v93 offset:0
	ds_read_b128 v[142:145], v141 offset:19456
	v_mfma_f32_16x16x32_bf16 v[62:65], v[238:241], v[222:225], v[62:65]
	v_mfma_f32_16x16x32_bf16 v[58:61], v[242:245], v[222:225], v[58:61]
	v_mfma_f32_16x16x32_bf16 v[54:57], v[246:249], v[222:225], v[54:57]
	v_mfma_f32_16x16x32_bf16 v[50:53], v[250:253], v[222:225], v[50:53]
	ds_read_b128 v[222:225], v93 offset:2048
	ds_read_b128 v[146:149], v141 offset:21504
	v_mfma_f32_16x16x32_bf16 v[46:49], v[238:241], v[226:229], v[46:49]
	v_mfma_f32_16x16x32_bf16 v[42:45], v[242:245], v[226:229], v[42:45]
	v_mfma_f32_16x16x32_bf16 v[38:41], v[246:249], v[226:229], v[38:41]
	v_mfma_f32_16x16x32_bf16 v[34:37], v[250:253], v[226:229], v[34:37]
	ds_read_b128 v[226:229], v93 offset:4096
	ds_read_b128 v[156:159], v141 offset:23552
	v_mfma_f32_16x16x32_bf16 v[18:21], v[238:241], v[230:233], v[18:21]
	v_mfma_f32_16x16x32_bf16 v[22:25], v[242:245], v[230:233], v[22:25]
	v_mfma_f32_16x16x32_bf16 v[26:29], v[246:249], v[230:233], v[26:29]
	v_mfma_f32_16x16x32_bf16 v[30:33], v[250:253], v[230:233], v[30:33]
	ds_read_b128 v[230:233], v93 offset:6144
	ds_read_b128 v[160:163], v141 offset:25600
	v_mfma_f32_16x16x32_bf16 v[2:5], v[238:241], v[234:237], v[2:5]
	v_mfma_f32_16x16x32_bf16 v[6:9], v[242:245], v[234:237], v[6:9]
	v_mfma_f32_16x16x32_bf16 v[10:13], v[246:249], v[234:237], v[10:13]
	v_mfma_f32_16x16x32_bf16 v[14:17], v[250:253], v[234:237], v[14:17]
	ds_read_b128 v[234:237], v93 offset:8192
	s_waitcnt lgkmcnt(0)
	s_barrier
	s_mov_b32 s49, s46
	s_mov_b32 s46, s47
	s_mov_b32 s47, s48
	s_mov_b32 s48, s49
	v_mfma_f32_16x16x32_bf16 v[78:81], v[142:145], v[218:221], v[78:81]
	v_mfma_f32_16x16x32_bf16 v[74:77], v[146:149], v[218:221], v[74:77]
	v_mfma_f32_16x16x32_bf16 v[70:73], v[156:159], v[218:221], v[70:73]
	v_mfma_f32_16x16x32_bf16 v[66:69], v[160:163], v[218:221], v[66:69]
	v_mfma_f32_16x16x32_bf16 v[62:65], v[142:145], v[222:225], v[62:65]
	v_mfma_f32_16x16x32_bf16 v[58:61], v[146:149], v[222:225], v[58:61]
	v_mfma_f32_16x16x32_bf16 v[54:57], v[156:159], v[222:225], v[54:57]
	v_mfma_f32_16x16x32_bf16 v[50:53], v[160:163], v[222:225], v[50:53]
	v_mfma_f32_16x16x32_bf16 v[46:49], v[142:145], v[226:229], v[46:49]
	v_mfma_f32_16x16x32_bf16 v[42:45], v[146:149], v[226:229], v[42:45]
	v_mfma_f32_16x16x32_bf16 v[38:41], v[156:159], v[226:229], v[38:41]
	v_mfma_f32_16x16x32_bf16 v[34:37], v[160:163], v[226:229], v[34:37]
	v_mfma_f32_16x16x32_bf16 v[18:21], v[142:145], v[230:233], v[18:21]
	v_mfma_f32_16x16x32_bf16 v[22:25], v[146:149], v[230:233], v[22:25]
	v_mfma_f32_16x16x32_bf16 v[26:29], v[156:159], v[230:233], v[26:29]
	v_mfma_f32_16x16x32_bf16 v[30:33], v[160:163], v[230:233], v[30:33]
	v_mfma_f32_16x16x32_bf16 v[2:5], v[142:145], v[234:237], v[2:5]
	v_mfma_f32_16x16x32_bf16 v[6:9], v[146:149], v[234:237], v[6:9]
	v_mfma_f32_16x16x32_bf16 v[10:13], v[156:159], v[234:237], v[10:13]
	v_mfma_f32_16x16x32_bf16 v[14:17], v[160:163], v[234:237], v[14:17]
	s_add_i32 s54, s48, s74
	v_add_u32_e32 v164, s54, v84
	v_add_u32_e32 v165, s54, v85
	ds_read_b32 v150, v82 offset:0
	ds_read_b32 v151, v83 offset:0
	ds_read_b32 v166, v83 offset:128
	s_waitcnt lgkmcnt(2)
	v_mul_f32_e32 v78, v150, v78
	v_mul_f32_e32 v79, v150, v79
	v_mul_f32_e32 v80, v150, v80
	v_mul_f32_e32 v81, v150, v81
	v_mul_f32_e32 v74, v150, v74
	v_mul_f32_e32 v75, v150, v75
	v_mul_f32_e32 v76, v150, v76
	v_mul_f32_e32 v77, v150, v77
	v_cvt_pk_bf16_f32 v182, v78, v79
	v_cvt_pk_bf16_f32 v183, v80, v81
	v_cvt_pk_bf16_f32 v184, v74, v75
	v_cvt_pk_bf16_f32 v185, v76, v77
	ds_write_b128 v164, v[182:185]
	v_mul_f32_e32 v70, v150, v70
	v_mul_f32_e32 v71, v150, v71
	v_mul_f32_e32 v72, v150, v72
	v_mul_f32_e32 v73, v150, v73
	v_mul_f32_e32 v66, v150, v66
	v_mul_f32_e32 v67, v150, v67
	v_mul_f32_e32 v68, v150, v68
	v_mul_f32_e32 v69, v150, v69
	v_cvt_pk_bf16_f32 v182, v70, v71
	v_cvt_pk_bf16_f32 v183, v72, v73
	v_cvt_pk_bf16_f32 v184, v66, v67
	v_cvt_pk_bf16_f32 v185, v68, v69
	v_xor_b32_e32 v167, 64, v164
	ds_write_b128 v167, v[182:185]
	v_mov_b32_e32 v78, 0
	v_mov_b32_e32 v74, 0
	v_mov_b32_e32 v70, 0
	v_mov_b32_e32 v66, 0
	v_mov_b32_e32 v79, 0
	v_mov_b32_e32 v75, 0
	v_mov_b32_e32 v71, 0
	v_mov_b32_e32 v67, 0
	v_mov_b32_e32 v80, 0
	v_mov_b32_e32 v76, 0
	v_mov_b32_e32 v72, 0
	v_mov_b32_e32 v68, 0
	v_mov_b32_e32 v81, 0
	v_mov_b32_e32 v77, 0
	v_mov_b32_e32 v73, 0
	v_mov_b32_e32 v69, 0
	ds_read_b128 v[182:185], v165 offset:0
	v_cmp_lt_i32_e32 vcc, -1, v151
	v_lshlrev_b32_e32 v148, 13, v151
	v_mov_b32_e32 v149, 0
	v_lshl_add_u64 v[148:149], v[148:149], 0, v[86:87]
	v_cndmask_b32_e32 v148, v168, v148, vcc
	v_cndmask_b32_e32 v149, v169, v149, vcc
	s_waitcnt lgkmcnt(0)
	global_store_dwordx4 v[148:149], v[182:185], off
	ds_read_b128 v[182:185], v165 offset:8192
	v_cmp_lt_i32_e32 vcc, -1, v166
	v_lshlrev_b32_e32 v148, 13, v166
	v_mov_b32_e32 v149, 0
	v_lshl_add_u64 v[148:149], v[148:149], 0, v[86:87]
	v_cndmask_b32_e32 v148, v168, v148, vcc
	v_cndmask_b32_e32 v149, v169, v149, vcc
	s_waitcnt lgkmcnt(0)
	global_store_dwordx4 v[148:149], v[182:185], off
	ds_read_b32 v150, v82 offset:256
	ds_read_b32 v151, v83 offset:256
	ds_read_b32 v166, v83 offset:384
	s_waitcnt lgkmcnt(2)
; #define PG8_LAS __attribute__((address_space(3)))
; __device__ __forceinline__ unsigned cvtpk(float lo, float hi) { f32x2 v = {lo, hi}; bf16x2_t b = __builtin_convertvector(v, bf16x2_t); return __builtin_bit_cast(unsigned, b); }
; __device__ __forceinline__ void moe_down_stream(PG8_LAS unsigned char* lds, int e, int cb0, int slot0, int nv, const bf16_t* HIDp, const float* Wd, bf16_t* Y, const float* slot_w, const int* slot_dst) {
;     ...
;         if (((t + 1) & 7) == 7) {
;             const int cb = cb0 + ((t + 1) >> 3);
; #pragma unroll
;             for (int m = 0; m < DNM; ++m) {
;                 const float w_ = lw[4 * (16 * m + fr) + wr];
; #pragma unroll
;                 for (int p = 0; p < 2; ++p) { const f32x4 v0 = acc[m][2 * p] * w_, v1 = acc[m][2 * p + 1] * w_; u32x4 w; w.x = cvtpk(v0[0], v0[1]); w.y = cvtpk(v0[2], v0[3]); w.z = cvtpk(v1[0], v1[1]); w.w = cvtpk(v1[2], v1[3]);
;                     *(PG8_LAS u32x4*)(stg + fr * 128 + (((4 * p + fq) ^ (fr & 7)) * 16)) = w; }
; #pragma unroll
;                 for (int hh = 0; hh < 2; ++hh) { const int r = (lane >> 3) + 8 * hh, cc = lane & 7; const u32x4 d = *(const PG8_LAS u32x4*)(stg + r * 128 + ((cc ^ (r & 7)) * 16)); const int dst_ = ldst[4 * (16 * m + r) + wr];
;                     if (dst_ >= 0) *(u32x4*)(Y + (size_t)dst_ * D + 128 * cb + 64 * wc + 8 * cc) = d; }
; #pragma unroll
;                 for (int n = 0; n < 4; ++n) acc[m][n] = (f32x4){0.f, 0.f, 0.f, 0.f}; } }
	v_mul_f32_e32 v62, v150, v62
	v_mul_f32_e32 v63, v150, v63
	v_mul_f32_e32 v64, v150, v64
	v_mul_f32_e32 v65, v150, v65
	v_mul_f32_e32 v58, v150, v58
	v_mul_f32_e32 v59, v150, v59
	v_mul_f32_e32 v60, v150, v60
	v_mul_f32_e32 v61, v150, v61
	v_cvt_pk_bf16_f32 v182, v62, v63
	v_cvt_pk_bf16_f32 v183, v64, v65
	v_cvt_pk_bf16_f32 v184, v58, v59
	v_cvt_pk_bf16_f32 v185, v60, v61
	ds_write_b128 v164, v[182:185]
	v_mul_f32_e32 v54, v150, v54
	v_mul_f32_e32 v55, v150, v55
	v_mul_f32_e32 v56, v150, v56
	v_mul_f32_e32 v57, v150, v57
	v_mul_f32_e32 v50, v150, v50
	v_mul_f32_e32 v51, v150, v51
	v_mul_f32_e32 v52, v150, v52
	v_mul_f32_e32 v53, v150, v53
	v_cvt_pk_bf16_f32 v182, v54, v55
	v_cvt_pk_bf16_f32 v183, v56, v57
	v_cvt_pk_bf16_f32 v184, v50, v51
	v_cvt_pk_bf16_f32 v185, v52, v53
	v_xor_b32_e32 v167, 64, v164
	ds_write_b128 v167, v[182:185]
	v_mov_b32_e32 v62, 0
	v_mov_b32_e32 v58, 0
	v_mov_b32_e32 v54, 0
	v_mov_b32_e32 v50, 0
	v_mov_b32_e32 v63, 0
	v_mov_b32_e32 v59, 0
	v_mov_b32_e32 v55, 0
	v_mov_b32_e32 v51, 0
	v_mov_b32_e32 v64, 0
	v_mov_b32_e32 v60, 0
	v_mov_b32_e32 v56, 0
	v_mov_b32_e32 v52, 0
	v_mov_b32_e32 v65, 0
	v_mov_b32_e32 v61, 0
	v_mov_b32_e32 v57, 0
	v_mov_b32_e32 v53, 0
	ds_read_b128 v[182:185], v165 offset:0
	v_cmp_lt_i32_e32 vcc, -1, v151
	v_lshlrev_b32_e32 v148, 13, v151
	v_mov_b32_e32 v149, 0
	v_lshl_add_u64 v[148:149], v[148:149], 0, v[86:87]
	v_cndmask_b32_e32 v148, v168, v148, vcc
	v_cndmask_b32_e32 v149, v169, v149, vcc
	s_waitcnt lgkmcnt(0)
	global_store_dwordx4 v[148:149], v[182:185], off
	ds_read_b128 v[182:185], v165 offset:8192
	v_cmp_lt_i32_e32 vcc, -1, v166
	v_lshlrev_b32_e32 v148, 13, v166
	v_mov_b32_e32 v149, 0
	v_lshl_add_u64 v[148:149], v[148:149], 0, v[86:87]
	v_cndmask_b32_e32 v148, v168, v148, vcc
	v_cndmask_b32_e32 v149, v169, v149, vcc
	s_waitcnt lgkmcnt(0)
	global_store_dwordx4 v[148:149], v[182:185], off
	ds_read_b32 v150, v82 offset:512
	ds_read_b32 v151, v83 offset:512
	ds_read_b32 v166, v83 offset:640
	s_waitcnt lgkmcnt(2)
	v_mul_f32_e32 v46, v150, v46
	v_mul_f32_e32 v47, v150, v47
	v_mul_f32_e32 v48, v150, v48
	v_mul_f32_e32 v49, v150, v49
	v_mul_f32_e32 v42, v150, v42
	v_mul_f32_e32 v43, v150, v43
	v_mul_f32_e32 v44, v150, v44
	v_mul_f32_e32 v45, v150, v45
	v_cvt_pk_bf16_f32 v182, v46, v47
	v_cvt_pk_bf16_f32 v183, v48, v49
	v_cvt_pk_bf16_f32 v184, v42, v43
	v_cvt_pk_bf16_f32 v185, v44, v45
	ds_write_b128 v164, v[182:185]
	v_mul_f32_e32 v38, v150, v38
	v_mul_f32_e32 v39, v150, v39
	v_mul_f32_e32 v40, v150, v40
	v_mul_f32_e32 v41, v150, v41
	v_mul_f32_e32 v34, v150, v34
	v_mul_f32_e32 v35, v150, v35
	v_mul_f32_e32 v36, v150, v36
	v_mul_f32_e32 v37, v150, v37
	v_cvt_pk_bf16_f32 v182, v38, v39
	v_cvt_pk_bf16_f32 v183, v40, v41
	v_cvt_pk_bf16_f32 v184, v34, v35
	v_cvt_pk_bf16_f32 v185, v36, v37
	v_xor_b32_e32 v167, 64, v164
	ds_write_b128 v167, v[182:185]
	v_mov_b32_e32 v46, 0
	v_mov_b32_e32 v42, 0
	v_mov_b32_e32 v38, 0
	v_mov_b32_e32 v34, 0
	v_mov_b32_e32 v47, 0
	v_mov_b32_e32 v43, 0
	v_mov_b32_e32 v39, 0
	v_mov_b32_e32 v35, 0
	v_mov_b32_e32 v48, 0
	v_mov_b32_e32 v44, 0
	v_mov_b32_e32 v40, 0
	v_mov_b32_e32 v36, 0
	v_mov_b32_e32 v49, 0
	v_mov_b32_e32 v45, 0
	v_mov_b32_e32 v41, 0
	v_mov_b32_e32 v37, 0
	ds_read_b128 v[182:185], v165 offset:0
	v_cmp_lt_i32_e32 vcc, -1, v151
	v_lshlrev_b32_e32 v148, 13, v151
	v_mov_b32_e32 v149, 0
	v_lshl_add_u64 v[148:149], v[148:149], 0, v[86:87]
	v_cndmask_b32_e32 v148, v168, v148, vcc
	v_cndmask_b32_e32 v149, v169, v149, vcc
	s_waitcnt lgkmcnt(0)
	global_store_dwordx4 v[148:149], v[182:185], off
	ds_read_b128 v[182:185], v165 offset:8192
	v_cmp_lt_i32_e32 vcc, -1, v166
	v_lshlrev_b32_e32 v148, 13, v166
	v_mov_b32_e32 v149, 0
	v_lshl_add_u64 v[148:149], v[148:149], 0, v[86:87]
	v_cndmask_b32_e32 v148, v168, v148, vcc
	v_cndmask_b32_e32 v149, v169, v149, vcc
	s_waitcnt lgkmcnt(0)
	global_store_dwordx4 v[148:149], v[182:185], off
	ds_read_b32 v150, v82 offset:768
	ds_read_b32 v151, v83 offset:768
	ds_read_b32 v166, v83 offset:896
	s_waitcnt lgkmcnt(2)
; #define PG8_LAS __attribute__((address_space(3)))
; __device__ __forceinline__ unsigned cvtpk(float lo, float hi) { f32x2 v = {lo, hi}; bf16x2_t b = __builtin_convertvector(v, bf16x2_t); return __builtin_bit_cast(unsigned, b); }
; __device__ __forceinline__ void moe_down_stream(PG8_LAS unsigned char* lds, int e, int cb0, int slot0, int nv, const bf16_t* HIDp, const float* Wd, bf16_t* Y, const float* slot_w, const int* slot_dst) {
;     ...
;         if (((t + 1) & 7) == 7) {
;             const int cb = cb0 + ((t + 1) >> 3);
; #pragma unroll
;             for (int m = 0; m < DNM; ++m) {
;                 const float w_ = lw[4 * (16 * m + fr) + wr];
; #pragma unroll
;                 for (int p = 0; p < 2; ++p) { const f32x4 v0 = acc[m][2 * p] * w_, v1 = acc[m][2 * p + 1] * w_; u32x4 w; w.x = cvtpk(v0[0], v0[1]); w.y = cvtpk(v0[2], v0[3]); w.z = cvtpk(v1[0], v1[1]); w.w = cvtpk(v1[2], v1[3]);
;                     *(PG8_LAS u32x4*)(stg + fr * 128 + (((4 * p + fq) ^ (fr & 7)) * 16)) = w; }
; #pragma unroll
;                 for (int hh = 0; hh < 2; ++hh) { const int r = (lane >> 3) + 8 * hh, cc = lane & 7; const u32x4 d = *(const PG8_LAS u32x4*)(stg + r * 128 + ((cc ^ (r & 7)) * 16)); const int dst_ = ldst[4 * (16 * m + r) + wr];
;                     if (dst_ >= 0) *(u32x4*)(Y + (size_t)dst_ * D + 128 * cb + 64 * wc + 8 * cc) = d; }
; #pragma unroll
;                 for (int n = 0; n < 4; ++n) acc[m][n] = (f32x4){0.f, 0.f, 0.f, 0.f}; } }
	v_mul_f32_e32 v18, v150, v18
	v_mul_f32_e32 v19, v150, v19
	v_mul_f32_e32 v20, v150, v20
	v_mul_f32_e32 v21, v150, v21
	v_mul_f32_e32 v22, v150, v22
	v_mul_f32_e32 v23, v150, v23
	v_mul_f32_e32 v24, v150, v24
	v_mul_f32_e32 v25, v150, v25
	v_cvt_pk_bf16_f32 v182, v18, v19
	v_cvt_pk_bf16_f32 v183, v20, v21
	v_cvt_pk_bf16_f32 v184, v22, v23
	v_cvt_pk_bf16_f32 v185, v24, v25
	ds_write_b128 v164, v[182:185]
	v_mul_f32_e32 v26, v150, v26
	v_mul_f32_e32 v27, v150, v27
	v_mul_f32_e32 v28, v150, v28
	v_mul_f32_e32 v29, v150, v29
	v_mul_f32_e32 v30, v150, v30
	v_mul_f32_e32 v31, v150, v31
	v_mul_f32_e32 v32, v150, v32
	v_mul_f32_e32 v33, v150, v33
	v_cvt_pk_bf16_f32 v182, v26, v27
	v_cvt_pk_bf16_f32 v183, v28, v29
	v_cvt_pk_bf16_f32 v184, v30, v31
	v_cvt_pk_bf16_f32 v185, v32, v33
	v_xor_b32_e32 v167, 64, v164
	ds_write_b128 v167, v[182:185]
	v_mov_b32_e32 v18, 0
	v_mov_b32_e32 v22, 0
	v_mov_b32_e32 v26, 0
	v_mov_b32_e32 v30, 0
	v_mov_b32_e32 v19, 0
	v_mov_b32_e32 v23, 0
	v_mov_b32_e32 v27, 0
	v_mov_b32_e32 v31, 0
	v_mov_b32_e32 v20, 0
	v_mov_b32_e32 v24, 0
	v_mov_b32_e32 v28, 0
	v_mov_b32_e32 v32, 0
	v_mov_b32_e32 v21, 0
	v_mov_b32_e32 v25, 0
	v_mov_b32_e32 v29, 0
	v_mov_b32_e32 v33, 0
	ds_read_b128 v[182:185], v165 offset:0
	v_cmp_lt_i32_e32 vcc, -1, v151
	v_lshlrev_b32_e32 v148, 13, v151
	v_mov_b32_e32 v149, 0
	v_lshl_add_u64 v[148:149], v[148:149], 0, v[86:87]
	v_cndmask_b32_e32 v148, v168, v148, vcc
	v_cndmask_b32_e32 v149, v169, v149, vcc
	s_waitcnt lgkmcnt(0)
	global_store_dwordx4 v[148:149], v[182:185], off
	ds_read_b128 v[182:185], v165 offset:8192
	v_cmp_lt_i32_e32 vcc, -1, v166
	v_lshlrev_b32_e32 v148, 13, v166
	v_mov_b32_e32 v149, 0
	v_lshl_add_u64 v[148:149], v[148:149], 0, v[86:87]
	v_cndmask_b32_e32 v148, v168, v148, vcc
	v_cndmask_b32_e32 v149, v169, v149, vcc
	s_waitcnt lgkmcnt(0)
	global_store_dwordx4 v[148:149], v[182:185], off
	ds_read_b32 v150, v82 offset:1024
	ds_read_b32 v151, v83 offset:1024
	ds_read_b32 v166, v83 offset:1152
	s_waitcnt lgkmcnt(2)
	v_mul_f32_e32 v2, v150, v2
	v_mul_f32_e32 v3, v150, v3
	v_mul_f32_e32 v4, v150, v4
	v_mul_f32_e32 v5, v150, v5
	v_mul_f32_e32 v6, v150, v6
	v_mul_f32_e32 v7, v150, v7
	v_mul_f32_e32 v8, v150, v8
	v_mul_f32_e32 v9, v150, v9
	v_cvt_pk_bf16_f32 v182, v2, v3
	v_cvt_pk_bf16_f32 v183, v4, v5
	v_cvt_pk_bf16_f32 v184, v6, v7
	v_cvt_pk_bf16_f32 v185, v8, v9
	ds_write_b128 v164, v[182:185]
	v_mul_f32_e32 v10, v150, v10
	v_mul_f32_e32 v11, v150, v11
	v_mul_f32_e32 v12, v150, v12
	v_mul_f32_e32 v13, v150, v13
	v_mul_f32_e32 v14, v150, v14
	v_mul_f32_e32 v15, v150, v15
	v_mul_f32_e32 v16, v150, v16
	v_mul_f32_e32 v17, v150, v17
	v_cvt_pk_bf16_f32 v182, v10, v11
	v_cvt_pk_bf16_f32 v183, v12, v13
	v_cvt_pk_bf16_f32 v184, v14, v15
	v_cvt_pk_bf16_f32 v185, v16, v17
	v_xor_b32_e32 v167, 64, v164
	ds_write_b128 v167, v[182:185]
	v_mov_b32_e32 v2, 0
	v_mov_b32_e32 v6, 0
	v_mov_b32_e32 v10, 0
	v_mov_b32_e32 v14, 0
	v_mov_b32_e32 v3, 0
	v_mov_b32_e32 v7, 0
	v_mov_b32_e32 v11, 0
	v_mov_b32_e32 v15, 0
	v_mov_b32_e32 v4, 0
	v_mov_b32_e32 v8, 0
	v_mov_b32_e32 v12, 0
	v_mov_b32_e32 v16, 0
	v_mov_b32_e32 v5, 0
	v_mov_b32_e32 v9, 0
	v_mov_b32_e32 v13, 0
	v_mov_b32_e32 v17, 0
	ds_read_b128 v[182:185], v165 offset:0
	v_cmp_lt_i32_e32 vcc, -1, v151
	v_lshlrev_b32_e32 v148, 13, v151
	v_mov_b32_e32 v149, 0
	v_lshl_add_u64 v[148:149], v[148:149], 0, v[86:87]
	v_cndmask_b32_e32 v148, v168, v148, vcc
	v_cndmask_b32_e32 v149, v169, v149, vcc
	s_waitcnt lgkmcnt(0)
	global_store_dwordx4 v[148:149], v[182:185], off
	ds_read_b128 v[182:185], v165 offset:8192
	v_cmp_lt_i32_e32 vcc, -1, v166
	v_lshlrev_b32_e32 v148, 13, v166
	v_mov_b32_e32 v149, 0
	v_lshl_add_u64 v[148:149], v[148:149], 0, v[86:87]
	v_cndmask_b32_e32 v148, v168, v148, vcc
	v_cndmask_b32_e32 v149, v169, v149, vcc
	s_waitcnt lgkmcnt(0)
	global_store_dwordx4 v[148:149], v[182:185], off
	v_add_co_u32_e32 v86, vcc, 0x800, v86
	s_nop 1
	v_addc_co_u32_e32 v87, vcc, 0, v87, vcc
	s_waitcnt lgkmcnt(0)
.Lmd_done:
	s_branch .LBB0_789


; __global__ void __launch_bounds__(NTHREADS, 2) hymba_fwd(Args args) {
;     extern __shared__ __attribute__((aligned(16))) unsigned char lds[];
	.amdhsa_kernel _Z9hymba_fwd4Args
		.amdhsa_group_segment_fixed_size 19520
		.amdhsa_private_segment_fixed_size 0
		.amdhsa_kernarg_size 424
		.amdhsa_user_sgpr_count 2
		.amdhsa_user_sgpr_dispatch_ptr 0
		.amdhsa_user_sgpr_queue_ptr 0
		.amdhsa_user_sgpr_kernarg_segment_ptr 1
		.amdhsa_user_sgpr_dispatch_id 0
		.amdhsa_user_sgpr_kernarg_preload_length 0
		.amdhsa_user_sgpr_kernarg_preload_offset 0
		.amdhsa_user_sgpr_private_segment_size 0
		.amdhsa_uses_dynamic_stack 0
		.amdhsa_enable_private_segment 0
		.amdhsa_system_sgpr_workgroup_id_x 1
		.amdhsa_system_sgpr_workgroup_id_y 0
		.amdhsa_system_sgpr_workgroup_id_z 0
		.amdhsa_system_sgpr_workgroup_info 0
		.amdhsa_system_vgpr_workitem_id 0
		.amdhsa_next_free_vgpr 255
		.amdhsa_next_free_sgpr 98
		.amdhsa_accum_offset 256
		.amdhsa_reserve_vcc 1
		.amdhsa_float_round_mode_32 0
		.amdhsa_float_round_mode_16_64 0
		.amdhsa_float_denorm_mode_32 3
		.amdhsa_float_denorm_mode_16_64 3
		.amdhsa_dx10_clamp 1
		.amdhsa_ieee_mode 1
		.amdhsa_fp16_overflow 0
		.amdhsa_tg_split 0
		.amdhsa_exception_fp_ieee_invalid_op 0
		.amdhsa_exception_fp_denorm_src 0
		.amdhsa_exception_fp_ieee_div_zero 0
		.amdhsa_exception_fp_ieee_overflow 0
		.amdhsa_exception_fp_ieee_underflow 0
		.amdhsa_exception_fp_ieee_inexact 0
		.amdhsa_exception_int_div_zero 0
	.end_amdhsa_kernel

; __global__ void __launch_bounds__(NTHREADS, 2) hymba_fwd(Args args) {
;     extern __shared__ __attribute__((aligned(16))) unsigned char lds[];
amdhsa.kernels:
  - .agpr_count:     0
    .args:
      - .offset:         0
        .size:           168
        .value_kind:     by_value
      - .offset:         168
        .size:           4
        .value_kind:     hidden_block_count_x
      - .offset:         172
        .size:           4
        .value_kind:     hidden_block_count_y
      - .offset:         176
        .size:           4
        .value_kind:     hidden_block_count_z
      - .offset:         180
        .size:           2
        .value_kind:     hidden_group_size_x
      - .offset:         182
        .size:           2
        .value_kind:     hidden_group_size_y
      - .offset:         184
        .size:           2
        .value_kind:     hidden_group_size_z
      - .offset:         186
        .size:           2
        .value_kind:     hidden_remainder_x
      - .offset:         188
        .size:           2
        .value_kind:     hidden_remainder_y
      - .offset:         190
        .size:           2
        .value_kind:     hidden_remainder_z
      - .offset:         208
        .size:           8
        .value_kind:     hidden_global_offset_x
      - .offset:         216
        .size:           8
        .value_kind:     hidden_global_offset_y
      - .offset:         224
        .size:           8
        .value_kind:     hidden_global_offset_z
      - .offset:         232
        .size:           2
        .value_kind:     hidden_grid_dims
      - .offset:         288
        .size:           4
        .value_kind:     hidden_dynamic_lds_size
    .group_segment_fixed_size: 19520
    .kernarg_segment_align: 8
    .kernarg_segment_size: 424
    .language:       OpenCL C
    .language_version:
      - 2
      - 0
    .max_flat_workgroup_size: 512
    .name:           _Z9hymba_fwd4Args
    .private_segment_fixed_size: 0
    .sgpr_count:     104
    .sgpr_spill_count: 62
    .symbol:         _Z9hymba_fwd4Args.kd
    .uniform_work_group_size: 1
    .uses_dynamic_stack: false
    .vgpr_count:     255
    .vgpr_spill_count: 0
    .wavefront_size: 64
